# baseline (speedup 1.0000x reference)
.LBB0_22:
	s_or_b64 exec, exec, s[8:9]
	v_cmp_lt_i32_e32 vcc, -1, v4
	s_and_saveexec_b64 s[8:9], vcc
	s_cbranch_execz .LBB0_2
	v_ashrrev_i32_e32 v1, 31, v0
	v_lshlrev_b64 v[0:1], 11, v[0:1]
	v_lshl_add_u64 v[40:41], v[10:11], 0, v[0:1]
	v_lshl_add_u64 v[38:39], v[8:9], 0, v[0:1]
	global_load_dwordx4 v[0:3], v[40:41], off
	global_load_dwordx4 v[24:27], v[38:39], off
	global_load_dwordx4 v[28:31], v[38:39], off offset:16
	global_load_dwordx4 v[34:37], v[40:41], off offset:16
	v_lshlrev_b64 v[38:39], 10, v[4:5]
	v_lshl_add_u64 v[38:39], v[12:13], 0, v[38:39]
	s_andn2_b64 vcc, exec, s[4:5]
	s_waitcnt vmcnt(2)
	v_pk_fma_f32 v[0:1], v[16:17], v[24:25], v[0:1]
	v_pk_fma_f32 v[2:3], v[18:19], v[26:27], v[2:3]
	s_waitcnt vmcnt(0)
	v_pk_fma_f32 v[24:25], v[20:21], v[28:29], v[34:35]
	v_pk_fma_f32 v[34:35], v[22:23], v[30:31], v[36:37]
	v_pk_mul_f32 v[30:31], v[0:1], s[6:7] op_sel_hi:[1,0]
	v_pk_mul_f32 v[28:29], v[2:3], s[6:7] op_sel_hi:[1,0]
	v_pk_mul_f32 v[26:27], v[24:25], s[6:7] op_sel_hi:[1,0]
	v_pk_mul_f32 v[24:25], v[34:35], s[6:7] op_sel_hi:[1,0]
	v_cvt_pk_f16_f32 v0, v30, v31
	v_cvt_pk_f16_f32 v1, v28, v29
	v_cvt_pk_f16_f32 v2, v26, v27
	v_cvt_pk_f16_f32 v3, v24, v25
	global_store_dwordx4 v[38:39], v[0:3], off sc1
	s_cbranch_vccnz .LBB0_2
	v_cvt_f32_f16_sdwa v37, v0 dst_sel:DWORD dst_unused:UNUSED_PAD src0_sel:WORD_1
	v_cvt_f32_f16_e32 v36, v0
	v_cvt_f32_f16_sdwa v39, v1 dst_sel:DWORD dst_unused:UNUSED_PAD src0_sel:WORD_1
	v_cvt_f32_f16_e32 v38, v1
	v_lshlrev_b64 v[34:35], 9, v[4:5]
	v_pk_add_f32 v[0:1], v[30:31], v[36:37] neg_lo:[0,1] neg_hi:[0,1]
	v_cvt_f32_f16_sdwa v31, v2 dst_sel:DWORD dst_unused:UNUSED_PAD src0_sel:WORD_1
	v_cvt_f32_f16_e32 v30, v2
	v_cvt_f32_f16_sdwa v37, v3 dst_sel:DWORD dst_unused:UNUSED_PAD src0_sel:WORD_1
	v_cvt_f32_f16_e32 v36, v3
	v_pk_add_f32 v[28:29], v[28:29], v[38:39] neg_lo:[0,1] neg_hi:[0,1]
	v_pk_add_f32 v[2:3], v[26:27], v[30:31] neg_lo:[0,1] neg_hi:[0,1]
	v_lshl_add_u64 v[34:35], v[34:35], 1, v[14:15]
	v_pk_add_f32 v[24:25], v[24:25], v[36:37] neg_lo:[0,1] neg_hi:[0,1]
	v_cvt_pk_f16_f32 v0, v0, v1
	v_cvt_pk_f16_f32 v1, v28, v29
	v_cvt_pk_f16_f32 v2, v2, v3
	v_cvt_pk_f16_f32 v3, v24, v25
	global_store_dwordx4 v[34:35], v[0:3], off sc1
	s_branch .LBB0_2

.LBB1_1:
	v_accvgpr_read_b32 v0, a130
	v_accvgpr_read_b32 v1, a131
	v_lshl_add_u64 v[0:1], v[0:1], 0, s[0:1]
	s_barrier
	global_load_ushort v0, v[0:1], off
	s_waitcnt vmcnt(0)
	v_cvt_f32_f16_e32 v2, v0
	v_accvgpr_read_b32 v0, a132
	v_accvgpr_read_b32 v1, a133
	v_lshl_add_u64 v[0:1], v[0:1], 0, s[0:1]
	global_load_ushort v0, v[0:1], off
	v_accvgpr_read_b32 v1, a2
	s_waitcnt vmcnt(0)
	v_cvt_f32_f16_e32 v0, v0
	v_add_f32_e32 v0, v2, v0
	ds_write_b32 v1, v0
	v_accvgpr_read_b32 v0, a94
	v_accvgpr_read_b32 v1, a95
	v_lshl_add_u64 v[0:1], v[0:1], 0, s[2:3]
	global_load_ushort v0, v[0:1], off
	s_waitcnt vmcnt(0)
	v_cvt_f32_f16_e32 v2, v0
	v_accvgpr_read_b32 v0, a96
	v_accvgpr_read_b32 v1, a97
	v_lshl_add_u64 v[0:1], v[0:1], 0, s[2:3]
	global_load_ushort v0, v[0:1], off
	v_accvgpr_read_b32 v1, a3
	s_waitcnt vmcnt(0)
	v_cvt_f32_f16_e32 v0, v0
	v_add_f32_e32 v0, v2, v0
	ds_write_b32 v1, v0
	v_accvgpr_read_b32 v0, a128
	v_accvgpr_read_b32 v1, a129
	v_lshl_add_u64 v[0:1], v[0:1], 0, s[0:1]
	global_load_ushort v0, v[0:1], off
	s_waitcnt vmcnt(0)
	v_cvt_f32_f16_e32 v2, v0
	v_accvgpr_read_b32 v0, a126
	v_accvgpr_read_b32 v1, a127
	v_lshl_add_u64 v[0:1], v[0:1], 0, s[0:1]
	global_load_ushort v0, v[0:1], off
	v_accvgpr_read_b32 v1, a4
	s_waitcnt vmcnt(0)
	v_cvt_f32_f16_e32 v0, v0
	v_add_f32_e32 v0, v2, v0
	ds_write_b32 v1, v0
	v_accvgpr_read_b32 v0, a92
	v_accvgpr_read_b32 v1, a93
	v_lshl_add_u64 v[0:1], v[0:1], 0, s[2:3]
	global_load_ushort v0, v[0:1], off
	s_waitcnt vmcnt(0)
	v_cvt_f32_f16_e32 v2, v0
	v_accvgpr_read_b32 v0, a90
	v_accvgpr_read_b32 v1, a91
	v_lshl_add_u64 v[0:1], v[0:1], 0, s[2:3]
	global_load_ushort v0, v[0:1], off
	v_accvgpr_read_b32 v1, a5
	s_waitcnt vmcnt(0)
	v_cvt_f32_f16_e32 v0, v0
	v_add_f32_e32 v0, v2, v0
	ds_write_b32 v1, v0
	v_accvgpr_read_b32 v0, a124
	v_accvgpr_read_b32 v1, a125
	v_lshl_add_u64 v[0:1], v[0:1], 0, s[0:1]
	global_load_ushort v0, v[0:1], off
	s_waitcnt vmcnt(0)
	v_cvt_f32_f16_e32 v2, v0
	v_accvgpr_read_b32 v0, a122
	v_accvgpr_read_b32 v1, a123
	v_lshl_add_u64 v[0:1], v[0:1], 0, s[0:1]
	global_load_ushort v0, v[0:1], off
	v_accvgpr_read_b32 v1, a6
	s_waitcnt vmcnt(0)
	v_cvt_f32_f16_e32 v0, v0
	v_add_f32_e32 v0, v2, v0
	ds_write_b32 v1, v0
	v_accvgpr_read_b32 v0, a88
	v_accvgpr_read_b32 v1, a89
	v_lshl_add_u64 v[0:1], v[0:1], 0, s[2:3]
	global_load_ushort v0, v[0:1], off
	s_waitcnt vmcnt(0)
	v_cvt_f32_f16_e32 v2, v0
	v_accvgpr_read_b32 v0, a86
	v_accvgpr_read_b32 v1, a87
	v_lshl_add_u64 v[0:1], v[0:1], 0, s[2:3]
	global_load_ushort v0, v[0:1], off
	v_accvgpr_read_b32 v1, a7
	s_waitcnt vmcnt(0)
	v_cvt_f32_f16_e32 v0, v0
	v_add_f32_e32 v0, v2, v0
	ds_write_b32 v1, v0
	v_accvgpr_read_b32 v0, a120
	v_accvgpr_read_b32 v1, a121
	v_lshl_add_u64 v[0:1], v[0:1], 0, s[0:1]
	global_load_ushort v0, v[0:1], off
	s_waitcnt vmcnt(0)
	v_cvt_f32_f16_e32 v2, v0
	v_accvgpr_read_b32 v0, a118
	v_accvgpr_read_b32 v1, a119
	v_lshl_add_u64 v[0:1], v[0:1], 0, s[0:1]
	global_load_ushort v0, v[0:1], off
	v_accvgpr_read_b32 v1, a8
	s_waitcnt vmcnt(0)
	v_cvt_f32_f16_e32 v0, v0
	v_add_f32_e32 v0, v2, v0
	ds_write_b32 v1, v0
	v_accvgpr_read_b32 v0, a84
	v_accvgpr_read_b32 v1, a85
	v_lshl_add_u64 v[0:1], v[0:1], 0, s[2:3]
	global_load_ushort v0, v[0:1], off
	s_waitcnt vmcnt(0)
	v_cvt_f32_f16_e32 v2, v0
	v_accvgpr_read_b32 v0, a82
	v_accvgpr_read_b32 v1, a83
	v_lshl_add_u64 v[0:1], v[0:1], 0, s[2:3]
	global_load_ushort v0, v[0:1], off
	v_accvgpr_read_b32 v1, a9
	s_waitcnt vmcnt(0)
	v_cvt_f32_f16_e32 v0, v0
	v_add_f32_e32 v0, v2, v0
	ds_write_b32 v1, v0
	v_accvgpr_read_b32 v0, a116
	v_accvgpr_read_b32 v1, a117
	v_lshl_add_u64 v[0:1], v[0:1], 0, s[0:1]
	global_load_ushort v0, v[0:1], off
	s_waitcnt vmcnt(0)
	v_cvt_f32_f16_e32 v2, v0
	v_accvgpr_read_b32 v0, a114
	v_accvgpr_read_b32 v1, a115
	v_lshl_add_u64 v[0:1], v[0:1], 0, s[0:1]
	global_load_ushort v0, v[0:1], off
	v_accvgpr_read_b32 v1, a10
	s_waitcnt vmcnt(0)
	v_cvt_f32_f16_e32 v0, v0
	v_add_f32_e32 v0, v2, v0
	ds_write_b32 v1, v0
	v_accvgpr_read_b32 v0, a80
	v_accvgpr_read_b32 v1, a81
	v_lshl_add_u64 v[0:1], v[0:1], 0, s[2:3]
	global_load_ushort v0, v[0:1], off
	s_waitcnt vmcnt(0)
	v_cvt_f32_f16_e32 v2, v0
	v_accvgpr_read_b32 v0, a78
	v_accvgpr_read_b32 v1, a79
	v_lshl_add_u64 v[0:1], v[0:1], 0, s[2:3]
	global_load_ushort v0, v[0:1], off
	v_accvgpr_read_b32 v1, a11
	s_waitcnt vmcnt(0)
	v_cvt_f32_f16_e32 v0, v0
	v_add_f32_e32 v0, v2, v0
	ds_write_b32 v1, v0
	v_accvgpr_read_b32 v0, a112
	v_accvgpr_read_b32 v1, a113
	v_lshl_add_u64 v[0:1], v[0:1], 0, s[0:1]
	global_load_ushort v0, v[0:1], off
	s_waitcnt vmcnt(0)
	v_cvt_f32_f16_e32 v2, v0
	v_accvgpr_read_b32 v0, a110
	v_accvgpr_read_b32 v1, a111
	v_lshl_add_u64 v[0:1], v[0:1], 0, s[0:1]
	global_load_ushort v0, v[0:1], off
	v_accvgpr_read_b32 v1, a12
	s_waitcnt vmcnt(0)
	v_cvt_f32_f16_e32 v0, v0
	v_add_f32_e32 v0, v2, v0
	ds_write_b32 v1, v0
	v_accvgpr_read_b32 v0, a76
	v_accvgpr_read_b32 v1, a77
	v_lshl_add_u64 v[0:1], v[0:1], 0, s[2:3]
	global_load_ushort v0, v[0:1], off
	s_waitcnt vmcnt(0)
	v_cvt_f32_f16_e32 v2, v0
	v_accvgpr_read_b32 v0, a74
	v_accvgpr_read_b32 v1, a75
	v_lshl_add_u64 v[0:1], v[0:1], 0, s[2:3]
	global_load_ushort v0, v[0:1], off
	v_accvgpr_read_b32 v1, a13
	s_waitcnt vmcnt(0)
	v_cvt_f32_f16_e32 v0, v0
	v_add_f32_e32 v0, v2, v0
	ds_write_b32 v1, v0
	v_accvgpr_read_b32 v0, a108
	v_accvgpr_read_b32 v1, a109
	v_lshl_add_u64 v[0:1], v[0:1], 0, s[0:1]
	global_load_ushort v0, v[0:1], off
	s_waitcnt vmcnt(0)
	v_cvt_f32_f16_e32 v2, v0
	v_accvgpr_read_b32 v0, a106
	v_accvgpr_read_b32 v1, a107
	v_lshl_add_u64 v[0:1], v[0:1], 0, s[0:1]
	global_load_ushort v0, v[0:1], off
	v_accvgpr_read_b32 v1, a14
	s_waitcnt vmcnt(0)
	v_cvt_f32_f16_e32 v0, v0
	v_add_f32_e32 v0, v2, v0
	ds_write_b32 v1, v0
	v_accvgpr_read_b32 v0, a72
	v_accvgpr_read_b32 v1, a73
	v_lshl_add_u64 v[0:1], v[0:1], 0, s[2:3]
	global_load_ushort v0, v[0:1], off
	s_waitcnt vmcnt(0)
	v_cvt_f32_f16_e32 v2, v0
	v_accvgpr_read_b32 v0, a70
	v_accvgpr_read_b32 v1, a71
	v_lshl_add_u64 v[0:1], v[0:1], 0, s[2:3]
	global_load_ushort v0, v[0:1], off
	v_accvgpr_read_b32 v1, a15
	s_waitcnt vmcnt(0)
	v_cvt_f32_f16_e32 v0, v0
	v_add_f32_e32 v0, v2, v0
	ds_write_b32 v1, v0
	v_accvgpr_read_b32 v0, a104
	v_accvgpr_read_b32 v1, a105
	v_lshl_add_u64 v[0:1], v[0:1], 0, s[0:1]
	global_load_ushort v0, v[0:1], off
	s_waitcnt vmcnt(0)
	v_cvt_f32_f16_e32 v2, v0
	v_accvgpr_read_b32 v0, a102
	v_accvgpr_read_b32 v1, a103
	v_lshl_add_u64 v[0:1], v[0:1], 0, s[0:1]
	global_load_ushort v0, v[0:1], off
	v_accvgpr_read_b32 v1, a16
	s_waitcnt vmcnt(0)
	v_cvt_f32_f16_e32 v0, v0
	v_add_f32_e32 v0, v2, v0
	ds_write_b32 v1, v0
	v_accvgpr_read_b32 v0, a68
	v_accvgpr_read_b32 v1, a69
	v_lshl_add_u64 v[0:1], v[0:1], 0, s[2:3]
	global_load_ushort v0, v[0:1], off
	s_waitcnt vmcnt(0)
	v_cvt_f32_f16_e32 v2, v0
	v_accvgpr_read_b32 v0, a66
	v_accvgpr_read_b32 v1, a67
	v_lshl_add_u64 v[0:1], v[0:1], 0, s[2:3]
	global_load_ushort v0, v[0:1], off
	v_accvgpr_read_b32 v1, a17
	s_waitcnt vmcnt(0)
	v_cvt_f32_f16_e32 v0, v0
	v_add_f32_e32 v0, v2, v0
	ds_write_b32 v1, v0
	v_accvgpr_read_b32 v0, a100
	v_accvgpr_read_b32 v1, a101
	v_lshl_add_u64 v[0:1], v[0:1], 0, s[0:1]
	global_load_ushort v0, v[0:1], off
	s_waitcnt vmcnt(0)
	v_cvt_f32_f16_e32 v2, v0
	v_accvgpr_read_b32 v0, a98
	v_accvgpr_read_b32 v1, a99
	v_lshl_add_u64 v[0:1], v[0:1], 0, s[0:1]
	global_load_ushort v0, v[0:1], off
	v_accvgpr_read_b32 v1, a18
	s_waitcnt vmcnt(0)
	v_cvt_f32_f16_e32 v0, v0
	v_add_f32_e32 v0, v2, v0
	ds_write_b32 v1, v0
	v_accvgpr_read_b32 v0, a64
	v_accvgpr_read_b32 v1, a65
	v_lshl_add_u64 v[0:1], v[0:1], 0, s[2:3]
	global_load_ushort v0, v[0:1], off
	s_waitcnt vmcnt(0)
	v_cvt_f32_f16_e32 v2, v0
	v_accvgpr_read_b32 v0, a62
	v_accvgpr_read_b32 v1, a63
	v_lshl_add_u64 v[0:1], v[0:1], 0, s[2:3]
	global_load_ushort v0, v[0:1], off
	v_accvgpr_read_b32 v1, a19
	s_waitcnt vmcnt(0)
	v_cvt_f32_f16_e32 v0, v0
	v_add_f32_e32 v0, v2, v0
	ds_write_b32 v1, v0
	v_lshl_add_u64 v[0:1], v[142:143], 0, s[0:1]
	global_load_ushort v0, v[0:1], off
	s_waitcnt vmcnt(0)
	v_cvt_f32_f16_e32 v2, v0
	v_lshl_add_u64 v[0:1], v[140:141], 0, s[0:1]
	global_load_ushort v0, v[0:1], off
	v_accvgpr_read_b32 v1, a20
	s_waitcnt vmcnt(0)
	v_cvt_f32_f16_e32 v0, v0
	v_add_f32_e32 v0, v2, v0
	ds_write_b32 v1, v0
	v_accvgpr_read_b32 v0, a60
	v_accvgpr_read_b32 v1, a61
	v_lshl_add_u64 v[0:1], v[0:1], 0, s[2:3]
	global_load_ushort v0, v[0:1], off
	s_waitcnt vmcnt(0)
	v_cvt_f32_f16_e32 v2, v0
	v_accvgpr_read_b32 v0, a58
	v_accvgpr_read_b32 v1, a59
	v_lshl_add_u64 v[0:1], v[0:1], 0, s[2:3]
	global_load_ushort v0, v[0:1], off
	v_accvgpr_read_b32 v1, a21
	s_waitcnt vmcnt(0)
	v_cvt_f32_f16_e32 v0, v0
	v_add_f32_e32 v0, v2, v0
	ds_write_b32 v1, v0
	v_lshl_add_u64 v[0:1], v[138:139], 0, s[0:1]
	global_load_ushort v0, v[0:1], off
	s_waitcnt vmcnt(0)
	v_cvt_f32_f16_e32 v2, v0
	v_lshl_add_u64 v[0:1], v[136:137], 0, s[0:1]
	global_load_ushort v0, v[0:1], off
	v_accvgpr_read_b32 v1, a22
	s_waitcnt vmcnt(0)
	v_cvt_f32_f16_e32 v0, v0
	v_add_f32_e32 v0, v2, v0
	ds_write_b32 v1, v0
	v_accvgpr_read_b32 v0, a56
	v_accvgpr_read_b32 v1, a57
	v_lshl_add_u64 v[0:1], v[0:1], 0, s[2:3]
	global_load_ushort v0, v[0:1], off
	s_waitcnt vmcnt(0)
	v_cvt_f32_f16_e32 v2, v0
	v_accvgpr_read_b32 v0, a54
	v_accvgpr_read_b32 v1, a55
	v_lshl_add_u64 v[0:1], v[0:1], 0, s[2:3]
	global_load_ushort v0, v[0:1], off
	v_accvgpr_read_b32 v1, a23
	s_waitcnt vmcnt(0)
	v_cvt_f32_f16_e32 v0, v0
	v_add_f32_e32 v0, v2, v0
	ds_write_b32 v1, v0
	v_lshl_add_u64 v[0:1], v[134:135], 0, s[0:1]
	global_load_ushort v0, v[0:1], off
	s_waitcnt vmcnt(0)
	v_cvt_f32_f16_e32 v2, v0
	v_lshl_add_u64 v[0:1], v[132:133], 0, s[0:1]
	global_load_ushort v0, v[0:1], off
	v_accvgpr_read_b32 v1, a24
	s_waitcnt vmcnt(0)
	v_cvt_f32_f16_e32 v0, v0
	v_add_f32_e32 v0, v2, v0
	ds_write_b32 v1, v0
	v_accvgpr_read_b32 v0, a52
	v_accvgpr_read_b32 v1, a53
	v_lshl_add_u64 v[0:1], v[0:1], 0, s[2:3]
	global_load_ushort v0, v[0:1], off
	s_waitcnt vmcnt(0)
	v_cvt_f32_f16_e32 v2, v0
	v_accvgpr_read_b32 v0, a50
	v_accvgpr_read_b32 v1, a51
	v_lshl_add_u64 v[0:1], v[0:1], 0, s[2:3]
	global_load_ushort v0, v[0:1], off
	v_accvgpr_read_b32 v1, a25
	s_waitcnt vmcnt(0)
	v_cvt_f32_f16_e32 v0, v0
	v_add_f32_e32 v0, v2, v0
	ds_write_b32 v1, v0
	v_lshl_add_u64 v[0:1], v[130:131], 0, s[0:1]
	global_load_ushort v0, v[0:1], off
	s_waitcnt vmcnt(0)
	v_cvt_f32_f16_e32 v2, v0
	v_lshl_add_u64 v[0:1], v[128:129], 0, s[0:1]
	global_load_ushort v0, v[0:1], off
	v_accvgpr_read_b32 v1, a26
	s_waitcnt vmcnt(0)
	v_cvt_f32_f16_e32 v0, v0
	v_add_f32_e32 v0, v2, v0
	ds_write_b32 v1, v0
	v_accvgpr_read_b32 v0, a48
	v_accvgpr_read_b32 v1, a49
	v_lshl_add_u64 v[0:1], v[0:1], 0, s[2:3]
	global_load_ushort v0, v[0:1], off
	s_waitcnt vmcnt(0)
	v_cvt_f32_f16_e32 v2, v0
	v_accvgpr_read_b32 v0, a46
	v_accvgpr_read_b32 v1, a47
	v_lshl_add_u64 v[0:1], v[0:1], 0, s[2:3]
	global_load_ushort v0, v[0:1], off
	v_accvgpr_read_b32 v1, a27
	s_waitcnt vmcnt(0)
	v_cvt_f32_f16_e32 v0, v0
	v_add_f32_e32 v0, v2, v0
	ds_write_b32 v1, v0
	v_lshl_add_u64 v[0:1], v[126:127], 0, s[0:1]
	global_load_ushort v0, v[0:1], off
	s_waitcnt vmcnt(0)
	v_cvt_f32_f16_e32 v2, v0
	v_accvgpr_read_b32 v0, a142
	v_accvgpr_read_b32 v1, a143
	v_lshl_add_u64 v[0:1], v[0:1], 0, s[0:1]
	global_load_ushort v0, v[0:1], off
	v_accvgpr_read_b32 v1, a28
	s_waitcnt vmcnt(0)
	v_cvt_f32_f16_e32 v0, v0
	v_add_f32_e32 v0, v2, v0
	ds_write_b32 v1, v0
	v_accvgpr_read_b32 v0, a44
	v_accvgpr_read_b32 v1, a45
	v_lshl_add_u64 v[0:1], v[0:1], 0, s[2:3]
	global_load_ushort v0, v[0:1], off
	s_waitcnt vmcnt(0)
	v_cvt_f32_f16_e32 v2, v0
	v_accvgpr_read_b32 v0, a42
	v_accvgpr_read_b32 v1, a43
	v_lshl_add_u64 v[0:1], v[0:1], 0, s[2:3]
	global_load_ushort v0, v[0:1], off
	v_accvgpr_read_b32 v1, a29
	s_waitcnt vmcnt(0)
	v_cvt_f32_f16_e32 v0, v0
	v_add_f32_e32 v0, v2, v0
	ds_write_b32 v1, v0
	v_accvgpr_read_b32 v0, a140
	v_accvgpr_read_b32 v1, a141
	v_lshl_add_u64 v[0:1], v[0:1], 0, s[0:1]
	global_load_ushort v0, v[0:1], off
	s_waitcnt vmcnt(0)
	v_cvt_f32_f16_e32 v2, v0
	v_accvgpr_read_b32 v0, a138
	v_accvgpr_read_b32 v1, a139
	v_lshl_add_u64 v[0:1], v[0:1], 0, s[0:1]
	global_load_ushort v0, v[0:1], off
	v_accvgpr_read_b32 v1, a30
	s_waitcnt vmcnt(0)
	v_cvt_f32_f16_e32 v0, v0
	v_add_f32_e32 v0, v2, v0
	ds_write_b32 v1, v0
	v_accvgpr_read_b32 v0, a40
	v_accvgpr_read_b32 v1, a41
	v_lshl_add_u64 v[0:1], v[0:1], 0, s[2:3]
	global_load_ushort v0, v[0:1], off
	s_waitcnt vmcnt(0)
	v_cvt_f32_f16_e32 v2, v0
	v_accvgpr_read_b32 v0, a38
	v_accvgpr_read_b32 v1, a39
	v_lshl_add_u64 v[0:1], v[0:1], 0, s[2:3]
	global_load_ushort v0, v[0:1], off
	v_accvgpr_read_b32 v1, a31
	s_waitcnt vmcnt(0)
	v_cvt_f32_f16_e32 v0, v0
	v_add_f32_e32 v0, v2, v0
	ds_write_b32 v1, v0
	v_accvgpr_read_b32 v0, a136
	v_accvgpr_read_b32 v1, a137
	v_lshl_add_u64 v[0:1], v[0:1], 0, s[0:1]
	global_load_ushort v0, v[0:1], off
	s_waitcnt vmcnt(0)
	v_cvt_f32_f16_e32 v2, v0
	v_accvgpr_read_b32 v0, a134
	v_accvgpr_read_b32 v1, a135
	v_lshl_add_u64 v[0:1], v[0:1], 0, s[0:1]
	global_load_ushort v0, v[0:1], off
	v_accvgpr_read_b32 v1, a32
	s_waitcnt vmcnt(0)
	v_cvt_f32_f16_e32 v0, v0
	v_add_f32_e32 v0, v2, v0
	ds_write_b32 v1, v0
	v_accvgpr_read_b32 v0, a36
	v_accvgpr_read_b32 v1, a37
	v_lshl_add_u64 v[0:1], v[0:1], 0, s[2:3]
	global_load_ushort v0, v[0:1], off
	s_waitcnt vmcnt(0)
	v_cvt_f32_f16_e32 v2, v0
	v_accvgpr_read_b32 v0, a34
	v_accvgpr_read_b32 v1, a35
	v_lshl_add_u64 v[0:1], v[0:1], 0, s[2:3]
	global_load_ushort v0, v[0:1], off
	v_accvgpr_read_b32 v1, a33
	s_add_u32 s2, s2, 64
	s_addc_u32 s3, s3, 0
	s_add_u32 s0, s0, 0x1000
	s_addc_u32 s1, s1, 0
	s_cmpk_eq_i32 s2, 0x800
	s_waitcnt vmcnt(0)
	v_cvt_f32_f16_e32 v0, v0
	v_add_f32_e32 v0, v2, v0
	ds_write_b32 v1, v0
	s_waitcnt lgkmcnt(0)
	s_barrier
	ds_read_b128 v[0:3], v102
	ds_read_b128 v[18:21], v102 offset:512
	s_waitcnt lgkmcnt(1)
	v_fma_f32 v9, v48, v0, 0
	v_fmac_f32_e32 v9, v49, v1
	v_fmac_f32_e32 v9, v50, v2
	v_fmac_f32_e32 v9, v51, v3
	ds_read_b128 v[0:3], v102 offset:16
	s_waitcnt lgkmcnt(0)
	v_fmac_f32_e32 v9, v52, v0
	v_fmac_f32_e32 v9, v53, v1
	v_fmac_f32_e32 v9, v54, v2
	v_fmac_f32_e32 v9, v55, v3
	ds_read_b128 v[0:3], v102 offset:32
	s_waitcnt lgkmcnt(0)
	v_fmac_f32_e32 v9, v56, v0
	v_fmac_f32_e32 v9, v57, v1
	v_fmac_f32_e32 v9, v58, v2
	v_fmac_f32_e32 v9, v59, v3
	ds_read_b128 v[0:3], v102 offset:48
	s_waitcnt lgkmcnt(0)
	v_fmac_f32_e32 v9, v60, v0
	v_fmac_f32_e32 v9, v61, v1
	v_fmac_f32_e32 v9, v62, v2
	v_fmac_f32_e32 v9, v63, v3
	ds_read_b128 v[0:3], v102 offset:64
	s_waitcnt lgkmcnt(0)
	v_fmac_f32_e32 v9, v64, v0
	v_fmac_f32_e32 v9, v65, v1
	v_fmac_f32_e32 v9, v66, v2
	v_fmac_f32_e32 v9, v67, v3
	ds_read_b128 v[0:3], v102 offset:80
	s_waitcnt lgkmcnt(0)
	v_fmac_f32_e32 v9, v68, v0
	v_fmac_f32_e32 v9, v69, v1
	v_fmac_f32_e32 v9, v70, v2
	v_fmac_f32_e32 v9, v71, v3
	ds_read_b128 v[0:3], v102 offset:96
	s_waitcnt lgkmcnt(0)
	v_fmac_f32_e32 v9, v72, v0
	v_fmac_f32_e32 v9, v73, v1
	v_fmac_f32_e32 v9, v74, v2
	v_fmac_f32_e32 v9, v75, v3
	ds_read_b128 v[0:3], v102 offset:112
	s_waitcnt lgkmcnt(0)
	v_fmac_f32_e32 v9, v76, v0
	v_fmac_f32_e32 v9, v77, v1
	v_fmac_f32_e32 v9, v78, v2
	v_fmac_f32_e32 v9, v79, v3
	ds_read_b128 v[0:3], v102 offset:128
	s_waitcnt lgkmcnt(0)
	v_fmac_f32_e32 v9, v80, v0
	v_fmac_f32_e32 v9, v81, v1
	v_fmac_f32_e32 v9, v82, v2
	v_fmac_f32_e32 v9, v83, v3
	ds_read_b128 v[0:3], v102 offset:144
	s_waitcnt lgkmcnt(0)
	v_fmac_f32_e32 v9, v84, v0
	v_fmac_f32_e32 v9, v85, v1
	v_fmac_f32_e32 v9, v86, v2
	v_fmac_f32_e32 v9, v87, v3
	ds_read_b128 v[0:3], v102 offset:160
	s_waitcnt lgkmcnt(0)
	v_fmac_f32_e32 v9, v88, v0
	v_fmac_f32_e32 v9, v89, v1
	v_fmac_f32_e32 v9, v90, v2
	v_fmac_f32_e32 v9, v91, v3
	ds_read_b128 v[0:3], v102 offset:176
	s_waitcnt lgkmcnt(0)
	v_fmac_f32_e32 v9, v92, v0
	v_fmac_f32_e32 v9, v93, v1
	v_fmac_f32_e32 v9, v94, v2
	v_fmac_f32_e32 v9, v95, v3
	ds_read_b128 v[0:3], v102 offset:192
	s_waitcnt lgkmcnt(0)
	v_fmac_f32_e32 v9, v96, v0
	v_fmac_f32_e32 v9, v97, v1
	v_fmac_f32_e32 v9, v98, v2
	v_fmac_f32_e32 v9, v99, v3
	ds_read_b128 v[0:3], v102 offset:208
	s_waitcnt lgkmcnt(0)
	v_fmac_f32_e32 v9, v100, v0
	v_fmac_f32_e32 v9, v101, v1
	v_fmac_f32_e32 v9, v12, v2
	v_fmac_f32_e32 v9, v13, v3
	ds_read_b128 v[0:3], v102 offset:224
	s_waitcnt lgkmcnt(0)
	v_pk_mul_f32 v[0:1], v[14:15], v[0:1]
	s_nop 0
	v_add_f32_e32 v0, v9, v0
	v_add_f32_e32 v9, v0, v1
	v_pk_mul_f32 v[0:1], v[6:7], v[2:3]
	s_nop 0
	v_add_f32_e32 v0, v9, v0
	v_add_f32_e32 v9, v0, v1
	ds_read_b128 v[0:3], v102 offset:240
	s_waitcnt lgkmcnt(0)
	v_pk_mul_f32 v[0:1], v[16:17], v[0:1]
	s_nop 0
	v_add_f32_e32 v0, v9, v0
	v_add_f32_e32 v9, v0, v1
	v_pk_mul_f32 v[0:1], v[4:5], v[2:3]
	s_nop 0
	v_add_f32_e32 v0, v9, v0
	v_add_f32_e32 v9, v0, v1
	ds_read_b128 v[0:3], v102 offset:256
	v_mul_f32_e32 v10, 0x39800000, v9
	s_waitcnt lgkmcnt(0)
	v_fma_f32 v11, v48, v0, 0
	v_fmac_f32_e32 v11, v49, v1
	v_fmac_f32_e32 v11, v50, v2
	v_fmac_f32_e32 v11, v51, v3
	ds_read_b128 v[0:3], v102 offset:272
	s_waitcnt lgkmcnt(0)
	v_fmac_f32_e32 v11, v52, v0
	v_fmac_f32_e32 v11, v53, v1
	v_fmac_f32_e32 v11, v54, v2
	v_fmac_f32_e32 v11, v55, v3
	ds_read_b128 v[0:3], v102 offset:288
	s_waitcnt lgkmcnt(0)
	v_fmac_f32_e32 v11, v56, v0
	v_fmac_f32_e32 v11, v57, v1
	v_fmac_f32_e32 v11, v58, v2
	v_fmac_f32_e32 v11, v59, v3
	ds_read_b128 v[0:3], v102 offset:304
	s_waitcnt lgkmcnt(0)
	v_fmac_f32_e32 v11, v60, v0
	v_fmac_f32_e32 v11, v61, v1
	v_fmac_f32_e32 v11, v62, v2
	v_fmac_f32_e32 v11, v63, v3
	ds_read_b128 v[0:3], v102 offset:320
	s_waitcnt lgkmcnt(0)
	v_fmac_f32_e32 v11, v64, v0
	v_fmac_f32_e32 v11, v65, v1
	v_fmac_f32_e32 v11, v66, v2
	v_fmac_f32_e32 v11, v67, v3
	ds_read_b128 v[0:3], v102 offset:336
	s_waitcnt lgkmcnt(0)
	v_fmac_f32_e32 v11, v68, v0
	v_fmac_f32_e32 v11, v69, v1
	v_fmac_f32_e32 v11, v70, v2
	v_fmac_f32_e32 v11, v71, v3
	ds_read_b128 v[0:3], v102 offset:352
	s_waitcnt lgkmcnt(0)
	v_fmac_f32_e32 v11, v72, v0
	v_fmac_f32_e32 v11, v73, v1
	v_fmac_f32_e32 v11, v74, v2
	v_fmac_f32_e32 v11, v75, v3
	ds_read_b128 v[0:3], v102 offset:368
	s_waitcnt lgkmcnt(0)
	v_fmac_f32_e32 v11, v76, v0
	v_fmac_f32_e32 v11, v77, v1
	v_fmac_f32_e32 v11, v78, v2
	v_fmac_f32_e32 v11, v79, v3
	ds_read_b128 v[0:3], v102 offset:384
	s_waitcnt lgkmcnt(0)
	v_fmac_f32_e32 v11, v80, v0
	v_fmac_f32_e32 v11, v81, v1
	v_fmac_f32_e32 v11, v82, v2
	v_fmac_f32_e32 v11, v83, v3
	ds_read_b128 v[0:3], v102 offset:400
	s_waitcnt lgkmcnt(0)
	v_fmac_f32_e32 v11, v84, v0
	v_fmac_f32_e32 v11, v85, v1
	v_fmac_f32_e32 v11, v86, v2
	v_fmac_f32_e32 v11, v87, v3
	ds_read_b128 v[0:3], v102 offset:416
	s_waitcnt lgkmcnt(0)
	v_fmac_f32_e32 v11, v88, v0
	v_fmac_f32_e32 v11, v89, v1
	v_fmac_f32_e32 v11, v90, v2
	v_fmac_f32_e32 v11, v91, v3
	ds_read_b128 v[0:3], v102 offset:432
	s_waitcnt lgkmcnt(0)
	v_fmac_f32_e32 v11, v92, v0
	v_fmac_f32_e32 v11, v93, v1
	v_fmac_f32_e32 v11, v94, v2
	v_fmac_f32_e32 v11, v95, v3
	ds_read_b128 v[0:3], v102 offset:448
	s_waitcnt lgkmcnt(0)
	v_fmac_f32_e32 v11, v96, v0
	v_fmac_f32_e32 v11, v97, v1
	v_fmac_f32_e32 v11, v98, v2
	v_fmac_f32_e32 v11, v99, v3
	ds_read_b128 v[0:3], v102 offset:464
	s_waitcnt lgkmcnt(0)
	v_fmac_f32_e32 v11, v100, v0
	v_fmac_f32_e32 v11, v101, v1
	v_fmac_f32_e32 v11, v12, v2
	v_fmac_f32_e32 v11, v13, v3
	ds_read_b128 v[0:3], v102 offset:480
	s_waitcnt lgkmcnt(0)
	v_pk_mul_f32 v[0:1], v[14:15], v[0:1]
	s_nop 0
	v_add_f32_e32 v0, v11, v0
	v_add_f32_e32 v11, v0, v1
	v_pk_mul_f32 v[0:1], v[6:7], v[2:3]
	s_nop 0
	v_add_f32_e32 v0, v11, v0
	v_add_f32_e32 v11, v0, v1
	ds_read_b128 v[0:3], v102 offset:496
	s_waitcnt lgkmcnt(0)
	v_pk_mul_f32 v[0:1], v[16:17], v[0:1]
	s_nop 0
	v_add_f32_e32 v0, v11, v0
	v_add_f32_e32 v11, v0, v1
	v_pk_mul_f32 v[0:1], v[4:5], v[2:3]
	s_nop 0
	v_add_f32_e32 v0, v11, v0
	v_add_f32_e32 v214, v0, v1
	v_fma_f32 v1, v48, v18, 0
	v_fmac_f32_e32 v1, v49, v19
	v_fmac_f32_e32 v1, v50, v20
	v_fmac_f32_e32 v1, v51, v21
	ds_read_b128 v[18:21], v102 offset:528
	v_mul_f32_e32 v0, 0x39800000, v214
	v_max3_f32 v0, v8, v10, v0
	s_waitcnt lgkmcnt(0)
	v_fmac_f32_e32 v1, v52, v18
	v_fmac_f32_e32 v1, v53, v19
	v_fmac_f32_e32 v1, v54, v20
	v_fmac_f32_e32 v1, v55, v21
	ds_read_b128 v[18:21], v102 offset:544
	s_waitcnt lgkmcnt(0)
	v_fmac_f32_e32 v1, v56, v18
	v_fmac_f32_e32 v1, v57, v19
	v_fmac_f32_e32 v1, v58, v20
	v_fmac_f32_e32 v1, v59, v21
	ds_read_b128 v[18:21], v102 offset:560
	s_waitcnt lgkmcnt(0)
	v_fmac_f32_e32 v1, v60, v18
	v_fmac_f32_e32 v1, v61, v19
	v_fmac_f32_e32 v1, v62, v20
	v_fmac_f32_e32 v1, v63, v21
	ds_read_b128 v[18:21], v102 offset:576
	s_waitcnt lgkmcnt(0)
	v_fmac_f32_e32 v1, v64, v18
	v_fmac_f32_e32 v1, v65, v19
	v_fmac_f32_e32 v1, v66, v20
	v_fmac_f32_e32 v1, v67, v21
	ds_read_b128 v[18:21], v102 offset:592
	s_waitcnt lgkmcnt(0)
	v_fmac_f32_e32 v1, v68, v18
	v_fmac_f32_e32 v1, v69, v19
	v_fmac_f32_e32 v1, v70, v20
	v_fmac_f32_e32 v1, v71, v21
	ds_read_b128 v[18:21], v102 offset:608
	s_waitcnt lgkmcnt(0)
	v_fmac_f32_e32 v1, v72, v18
	v_fmac_f32_e32 v1, v73, v19
	v_fmac_f32_e32 v1, v74, v20
	v_fmac_f32_e32 v1, v75, v21
	ds_read_b128 v[18:21], v102 offset:624
	s_waitcnt lgkmcnt(0)
	v_fmac_f32_e32 v1, v76, v18
	v_fmac_f32_e32 v1, v77, v19
	v_fmac_f32_e32 v1, v78, v20
	v_fmac_f32_e32 v1, v79, v21
	ds_read_b128 v[18:21], v102 offset:640
	s_waitcnt lgkmcnt(0)
	v_fmac_f32_e32 v1, v80, v18
	v_fmac_f32_e32 v1, v81, v19
	v_fmac_f32_e32 v1, v82, v20
	v_fmac_f32_e32 v1, v83, v21
	ds_read_b128 v[18:21], v102 offset:656
	s_waitcnt lgkmcnt(0)
	v_fmac_f32_e32 v1, v84, v18
	v_fmac_f32_e32 v1, v85, v19
	v_fmac_f32_e32 v1, v86, v20
	v_fmac_f32_e32 v1, v87, v21
	ds_read_b128 v[18:21], v102 offset:672
	s_waitcnt lgkmcnt(0)
	v_fmac_f32_e32 v1, v88, v18
	v_fmac_f32_e32 v1, v89, v19
	v_fmac_f32_e32 v1, v90, v20
	v_fmac_f32_e32 v1, v91, v21
	ds_read_b128 v[18:21], v102 offset:688
	s_waitcnt lgkmcnt(0)
	v_fmac_f32_e32 v1, v92, v18
	v_fmac_f32_e32 v1, v93, v19
	v_fmac_f32_e32 v1, v94, v20
	v_fmac_f32_e32 v1, v95, v21
	ds_read_b128 v[18:21], v102 offset:704
	s_waitcnt lgkmcnt(0)
	v_fmac_f32_e32 v1, v96, v18
	v_fmac_f32_e32 v1, v97, v19
	v_fmac_f32_e32 v1, v98, v20
	v_fmac_f32_e32 v1, v99, v21
	ds_read_b128 v[18:21], v102 offset:720
	s_waitcnt lgkmcnt(0)
	v_fmac_f32_e32 v1, v100, v18
	v_fmac_f32_e32 v1, v101, v19
	v_fmac_f32_e32 v1, v12, v20
	v_fmac_f32_e32 v1, v13, v21
	ds_read_b128 v[18:21], v102 offset:736
	s_waitcnt lgkmcnt(0)
	v_pk_mul_f32 v[2:3], v[14:15], v[18:19]
	s_nop 0
	v_add_f32_e32 v1, v1, v2
	v_add_f32_e32 v1, v1, v3
	v_pk_mul_f32 v[2:3], v[6:7], v[20:21]
	ds_read_b128 v[18:21], v102 offset:752
	v_add_f32_e32 v1, v1, v2
	v_add_f32_e32 v1, v1, v3
	s_waitcnt lgkmcnt(0)
	v_pk_mul_f32 v[2:3], v[16:17], v[18:19]
	s_nop 0
	v_add_f32_e32 v1, v1, v2
	v_add_f32_e32 v1, v1, v3
	v_pk_mul_f32 v[2:3], v[4:5], v[20:21]
	ds_read_b128 v[18:21], v102 offset:768
	v_add_f32_e32 v1, v1, v2
	v_add_f32_e32 v228, v1, v3
	v_mul_f32_e32 v1, 0x39800000, v228
	s_waitcnt lgkmcnt(0)
	v_fma_f32 v10, v48, v18, 0
	v_fmac_f32_e32 v10, v49, v19
	v_fmac_f32_e32 v10, v50, v20
	v_fmac_f32_e32 v10, v51, v21
	ds_read_b128 v[18:21], v102 offset:784
	s_waitcnt lgkmcnt(0)
	v_fmac_f32_e32 v10, v52, v18
	v_fmac_f32_e32 v10, v53, v19
	v_fmac_f32_e32 v10, v54, v20
	v_fmac_f32_e32 v10, v55, v21
	ds_read_b128 v[18:21], v102 offset:800
	s_waitcnt lgkmcnt(0)
	v_fmac_f32_e32 v10, v56, v18
	v_fmac_f32_e32 v10, v57, v19
	v_fmac_f32_e32 v10, v58, v20
	v_fmac_f32_e32 v10, v59, v21
	ds_read_b128 v[18:21], v102 offset:816
	s_waitcnt lgkmcnt(0)
	v_fmac_f32_e32 v10, v60, v18
	v_fmac_f32_e32 v10, v61, v19
	v_fmac_f32_e32 v10, v62, v20
	v_fmac_f32_e32 v10, v63, v21
	ds_read_b128 v[18:21], v102 offset:832
	s_waitcnt lgkmcnt(0)
	v_fmac_f32_e32 v10, v64, v18
	v_fmac_f32_e32 v10, v65, v19
	v_fmac_f32_e32 v10, v66, v20
	v_fmac_f32_e32 v10, v67, v21
	ds_read_b128 v[18:21], v102 offset:848
	s_waitcnt lgkmcnt(0)
	v_fmac_f32_e32 v10, v68, v18
	v_fmac_f32_e32 v10, v69, v19
	v_fmac_f32_e32 v10, v70, v20
	v_fmac_f32_e32 v10, v71, v21
	ds_read_b128 v[18:21], v102 offset:864
	s_waitcnt lgkmcnt(0)
	v_fmac_f32_e32 v10, v72, v18
	v_fmac_f32_e32 v10, v73, v19
	v_fmac_f32_e32 v10, v74, v20
	v_fmac_f32_e32 v10, v75, v21
	ds_read_b128 v[18:21], v102 offset:880
	s_waitcnt lgkmcnt(0)
	v_fmac_f32_e32 v10, v76, v18
	v_fmac_f32_e32 v10, v77, v19
	v_fmac_f32_e32 v10, v78, v20
	v_fmac_f32_e32 v10, v79, v21
	ds_read_b128 v[18:21], v102 offset:896
	s_waitcnt lgkmcnt(0)
	v_fmac_f32_e32 v10, v80, v18
	v_fmac_f32_e32 v10, v81, v19
	v_fmac_f32_e32 v10, v82, v20
	v_fmac_f32_e32 v10, v83, v21
	ds_read_b128 v[18:21], v102 offset:912
	s_waitcnt lgkmcnt(0)
	v_fmac_f32_e32 v10, v84, v18
	v_fmac_f32_e32 v10, v85, v19
	v_fmac_f32_e32 v10, v86, v20
	v_fmac_f32_e32 v10, v87, v21
	ds_read_b128 v[18:21], v102 offset:928
	s_waitcnt lgkmcnt(0)
	v_fmac_f32_e32 v10, v88, v18
	v_fmac_f32_e32 v10, v89, v19
	v_fmac_f32_e32 v10, v90, v20
	v_fmac_f32_e32 v10, v91, v21
	ds_read_b128 v[18:21], v102 offset:944
	s_waitcnt lgkmcnt(0)
	v_fmac_f32_e32 v10, v92, v18
	v_fmac_f32_e32 v10, v93, v19
	v_fmac_f32_e32 v10, v94, v20
	v_fmac_f32_e32 v10, v95, v21
	ds_read_b128 v[18:21], v102 offset:960
	s_waitcnt lgkmcnt(0)
	v_fmac_f32_e32 v10, v96, v18
	v_fmac_f32_e32 v10, v97, v19
	v_fmac_f32_e32 v10, v98, v20
	v_fmac_f32_e32 v10, v99, v21
	ds_read_b128 v[18:21], v102 offset:976
	s_waitcnt lgkmcnt(0)
	v_fmac_f32_e32 v10, v100, v18
	v_fmac_f32_e32 v10, v101, v19
	v_fmac_f32_e32 v10, v12, v20
	v_fmac_f32_e32 v10, v13, v21
	ds_read_b128 v[18:21], v102 offset:992
	s_waitcnt lgkmcnt(0)
	v_pk_mul_f32 v[2:3], v[14:15], v[18:19]
	s_nop 0
	v_add_f32_e32 v2, v10, v2
	v_add_f32_e32 v10, v2, v3
	v_pk_mul_f32 v[2:3], v[6:7], v[20:21]
	ds_read_b128 v[18:21], v102 offset:1008
	v_add_f32_e32 v2, v10, v2
	v_add_f32_e32 v10, v2, v3
	s_waitcnt lgkmcnt(0)
	v_pk_mul_f32 v[2:3], v[16:17], v[18:19]
	s_nop 0
	v_add_f32_e32 v2, v10, v2
	v_add_f32_e32 v10, v2, v3
	v_pk_mul_f32 v[2:3], v[4:5], v[20:21]
	ds_read_b128 v[18:21], v102 offset:1024
	v_add_f32_e32 v2, v10, v2
	v_add_f32_e32 v230, v2, v3
	v_mul_f32_e32 v2, 0x39800000, v230
	v_max3_f32 v0, v0, v1, v2
	s_waitcnt lgkmcnt(0)
	v_fma_f32 v1, v48, v18, 0
	v_fmac_f32_e32 v1, v49, v19
	v_fmac_f32_e32 v1, v50, v20
	v_fmac_f32_e32 v1, v51, v21
	ds_read_b128 v[18:21], v102 offset:1040
	s_waitcnt lgkmcnt(0)
	v_fmac_f32_e32 v1, v52, v18
	v_fmac_f32_e32 v1, v53, v19
	v_fmac_f32_e32 v1, v54, v20
	v_fmac_f32_e32 v1, v55, v21
	ds_read_b128 v[18:21], v102 offset:1056
	s_waitcnt lgkmcnt(0)
	v_fmac_f32_e32 v1, v56, v18
	v_fmac_f32_e32 v1, v57, v19
	v_fmac_f32_e32 v1, v58, v20
	v_fmac_f32_e32 v1, v59, v21
	ds_read_b128 v[18:21], v102 offset:1072
	s_waitcnt lgkmcnt(0)
	v_fmac_f32_e32 v1, v60, v18
	v_fmac_f32_e32 v1, v61, v19
	v_fmac_f32_e32 v1, v62, v20
	v_fmac_f32_e32 v1, v63, v21
	ds_read_b128 v[18:21], v102 offset:1088
	s_waitcnt lgkmcnt(0)
	v_fmac_f32_e32 v1, v64, v18
	v_fmac_f32_e32 v1, v65, v19
	v_fmac_f32_e32 v1, v66, v20
	v_fmac_f32_e32 v1, v67, v21
	ds_read_b128 v[18:21], v102 offset:1104
	s_waitcnt lgkmcnt(0)
	v_fmac_f32_e32 v1, v68, v18
	v_fmac_f32_e32 v1, v69, v19
	v_fmac_f32_e32 v1, v70, v20
	v_fmac_f32_e32 v1, v71, v21
	ds_read_b128 v[18:21], v102 offset:1120
	s_waitcnt lgkmcnt(0)
	v_fmac_f32_e32 v1, v72, v18
	v_fmac_f32_e32 v1, v73, v19
	v_fmac_f32_e32 v1, v74, v20
	v_fmac_f32_e32 v1, v75, v21
	ds_read_b128 v[18:21], v102 offset:1136
	s_waitcnt lgkmcnt(0)
	v_fmac_f32_e32 v1, v76, v18
	v_fmac_f32_e32 v1, v77, v19
	v_fmac_f32_e32 v1, v78, v20
	v_fmac_f32_e32 v1, v79, v21
	ds_read_b128 v[18:21], v102 offset:1152
	s_waitcnt lgkmcnt(0)
	v_fmac_f32_e32 v1, v80, v18
	v_fmac_f32_e32 v1, v81, v19
	v_fmac_f32_e32 v1, v82, v20
	v_fmac_f32_e32 v1, v83, v21
	ds_read_b128 v[18:21], v102 offset:1168
	s_waitcnt lgkmcnt(0)
	v_fmac_f32_e32 v1, v84, v18
	v_fmac_f32_e32 v1, v85, v19
	v_fmac_f32_e32 v1, v86, v20
	v_fmac_f32_e32 v1, v87, v21
	ds_read_b128 v[18:21], v102 offset:1184
	s_waitcnt lgkmcnt(0)
	v_fmac_f32_e32 v1, v88, v18
	v_fmac_f32_e32 v1, v89, v19
	v_fmac_f32_e32 v1, v90, v20
	v_fmac_f32_e32 v1, v91, v21
	ds_read_b128 v[18:21], v102 offset:1200
	s_waitcnt lgkmcnt(0)
	v_fmac_f32_e32 v1, v92, v18
	v_fmac_f32_e32 v1, v93, v19
	v_fmac_f32_e32 v1, v94, v20
	v_fmac_f32_e32 v1, v95, v21
	ds_read_b128 v[18:21], v102 offset:1216
	s_waitcnt lgkmcnt(0)
	v_fmac_f32_e32 v1, v96, v18
	v_fmac_f32_e32 v1, v97, v19
	v_fmac_f32_e32 v1, v98, v20
	v_fmac_f32_e32 v1, v99, v21
	ds_read_b128 v[18:21], v102 offset:1232
	s_waitcnt lgkmcnt(0)
	v_fmac_f32_e32 v1, v100, v18
	v_fmac_f32_e32 v1, v101, v19
	v_fmac_f32_e32 v1, v12, v20
	v_fmac_f32_e32 v1, v13, v21
	ds_read_b128 v[18:21], v102 offset:1248
	s_waitcnt lgkmcnt(0)
	v_pk_mul_f32 v[2:3], v[14:15], v[18:19]
	s_nop 0
	v_add_f32_e32 v1, v1, v2
	v_add_f32_e32 v1, v1, v3
	v_pk_mul_f32 v[2:3], v[6:7], v[20:21]
	ds_read_b128 v[18:21], v102 offset:1264
	v_add_f32_e32 v1, v1, v2
	v_add_f32_e32 v1, v1, v3
	s_waitcnt lgkmcnt(0)
	v_pk_mul_f32 v[2:3], v[16:17], v[18:19]
	s_nop 0
	v_add_f32_e32 v1, v1, v2
	v_add_f32_e32 v1, v1, v3
	v_pk_mul_f32 v[2:3], v[4:5], v[20:21]
	ds_read_b128 v[18:21], v102 offset:1280
	v_add_f32_e32 v1, v1, v2
	v_add_f32_e32 v231, v1, v3
	v_mul_f32_e32 v1, 0x39800000, v231
	s_waitcnt lgkmcnt(0)
	v_fma_f32 v10, v48, v18, 0
	v_fmac_f32_e32 v10, v49, v19
	v_fmac_f32_e32 v10, v50, v20
	v_fmac_f32_e32 v10, v51, v21
	ds_read_b128 v[18:21], v102 offset:1296
	s_waitcnt lgkmcnt(0)
	v_fmac_f32_e32 v10, v52, v18
	v_fmac_f32_e32 v10, v53, v19
	v_fmac_f32_e32 v10, v54, v20
	v_fmac_f32_e32 v10, v55, v21
	ds_read_b128 v[18:21], v102 offset:1312
	s_waitcnt lgkmcnt(0)
	v_fmac_f32_e32 v10, v56, v18
	v_fmac_f32_e32 v10, v57, v19
	v_fmac_f32_e32 v10, v58, v20
	v_fmac_f32_e32 v10, v59, v21
	ds_read_b128 v[18:21], v102 offset:1328
	s_waitcnt lgkmcnt(0)
	v_fmac_f32_e32 v10, v60, v18
	v_fmac_f32_e32 v10, v61, v19
	v_fmac_f32_e32 v10, v62, v20
	v_fmac_f32_e32 v10, v63, v21
	ds_read_b128 v[18:21], v102 offset:1344
	s_waitcnt lgkmcnt(0)
	v_fmac_f32_e32 v10, v64, v18
	v_fmac_f32_e32 v10, v65, v19
	v_fmac_f32_e32 v10, v66, v20
	v_fmac_f32_e32 v10, v67, v21
	ds_read_b128 v[18:21], v102 offset:1360
	s_waitcnt lgkmcnt(0)
	v_fmac_f32_e32 v10, v68, v18
	v_fmac_f32_e32 v10, v69, v19
	v_fmac_f32_e32 v10, v70, v20
	v_fmac_f32_e32 v10, v71, v21
	ds_read_b128 v[18:21], v102 offset:1376
	s_waitcnt lgkmcnt(0)
	v_fmac_f32_e32 v10, v72, v18
	v_fmac_f32_e32 v10, v73, v19
	v_fmac_f32_e32 v10, v74, v20
	v_fmac_f32_e32 v10, v75, v21
	ds_read_b128 v[18:21], v102 offset:1392
	s_waitcnt lgkmcnt(0)
	v_fmac_f32_e32 v10, v76, v18
	v_fmac_f32_e32 v10, v77, v19
	v_fmac_f32_e32 v10, v78, v20
	v_fmac_f32_e32 v10, v79, v21
	ds_read_b128 v[18:21], v102 offset:1408
	s_waitcnt lgkmcnt(0)
	v_fmac_f32_e32 v10, v80, v18
	v_fmac_f32_e32 v10, v81, v19
	v_fmac_f32_e32 v10, v82, v20
	v_fmac_f32_e32 v10, v83, v21
	ds_read_b128 v[18:21], v102 offset:1424
	s_waitcnt lgkmcnt(0)
	v_fmac_f32_e32 v10, v84, v18
	v_fmac_f32_e32 v10, v85, v19
	v_fmac_f32_e32 v10, v86, v20
	v_fmac_f32_e32 v10, v87, v21
	ds_read_b128 v[18:21], v102 offset:1440
	s_waitcnt lgkmcnt(0)
	v_fmac_f32_e32 v10, v88, v18
	v_fmac_f32_e32 v10, v89, v19
	v_fmac_f32_e32 v10, v90, v20
	v_fmac_f32_e32 v10, v91, v21
	ds_read_b128 v[18:21], v102 offset:1456
	s_waitcnt lgkmcnt(0)
	v_fmac_f32_e32 v10, v92, v18
	v_fmac_f32_e32 v10, v93, v19
	v_fmac_f32_e32 v10, v94, v20
	v_fmac_f32_e32 v10, v95, v21
	ds_read_b128 v[18:21], v102 offset:1472
	s_waitcnt lgkmcnt(0)
	v_fmac_f32_e32 v10, v96, v18
	v_fmac_f32_e32 v10, v97, v19
	v_fmac_f32_e32 v10, v98, v20
	v_fmac_f32_e32 v10, v99, v21
	ds_read_b128 v[18:21], v102 offset:1488
	s_waitcnt lgkmcnt(0)
	v_fmac_f32_e32 v10, v100, v18
	v_fmac_f32_e32 v10, v101, v19
	v_fmac_f32_e32 v10, v12, v20
	v_fmac_f32_e32 v10, v13, v21
	ds_read_b128 v[18:21], v102 offset:1504
	s_waitcnt lgkmcnt(0)
	v_pk_mul_f32 v[2:3], v[14:15], v[18:19]
	s_nop 0
	v_add_f32_e32 v2, v10, v2
	v_add_f32_e32 v10, v2, v3
	v_pk_mul_f32 v[2:3], v[6:7], v[20:21]
	ds_read_b128 v[18:21], v102 offset:1520
	v_add_f32_e32 v2, v10, v2
	v_add_f32_e32 v10, v2, v3
	s_waitcnt lgkmcnt(0)
	v_pk_mul_f32 v[2:3], v[16:17], v[18:19]
	s_nop 0
	v_add_f32_e32 v2, v10, v2
	v_add_f32_e32 v10, v2, v3
	v_pk_mul_f32 v[2:3], v[4:5], v[20:21]
	ds_read_b128 v[18:21], v102 offset:1536
	v_add_f32_e32 v2, v10, v2
	v_add_f32_e32 v232, v2, v3
	v_mul_f32_e32 v2, 0x39800000, v232
	v_max3_f32 v0, v0, v1, v2
	s_waitcnt lgkmcnt(0)
	v_fma_f32 v1, v48, v18, 0
	v_fmac_f32_e32 v1, v49, v19
	v_fmac_f32_e32 v1, v50, v20
	v_fmac_f32_e32 v1, v51, v21
	ds_read_b128 v[18:21], v102 offset:1552
	s_waitcnt lgkmcnt(0)
	v_fmac_f32_e32 v1, v52, v18
	v_fmac_f32_e32 v1, v53, v19
	v_fmac_f32_e32 v1, v54, v20
	v_fmac_f32_e32 v1, v55, v21
	ds_read_b128 v[18:21], v102 offset:1568
	s_waitcnt lgkmcnt(0)
	v_fmac_f32_e32 v1, v56, v18
	v_fmac_f32_e32 v1, v57, v19
	v_fmac_f32_e32 v1, v58, v20
	v_fmac_f32_e32 v1, v59, v21
	ds_read_b128 v[18:21], v102 offset:1584
	s_waitcnt lgkmcnt(0)
	v_fmac_f32_e32 v1, v60, v18
	v_fmac_f32_e32 v1, v61, v19
	v_fmac_f32_e32 v1, v62, v20
	v_fmac_f32_e32 v1, v63, v21
	ds_read_b128 v[18:21], v102 offset:1600
	s_waitcnt lgkmcnt(0)
	v_fmac_f32_e32 v1, v64, v18
	v_fmac_f32_e32 v1, v65, v19
	v_fmac_f32_e32 v1, v66, v20
	v_fmac_f32_e32 v1, v67, v21
	ds_read_b128 v[18:21], v102 offset:1616
	s_waitcnt lgkmcnt(0)
	v_fmac_f32_e32 v1, v68, v18
	v_fmac_f32_e32 v1, v69, v19
	v_fmac_f32_e32 v1, v70, v20
	v_fmac_f32_e32 v1, v71, v21
	ds_read_b128 v[18:21], v102 offset:1632
	s_waitcnt lgkmcnt(0)
	v_fmac_f32_e32 v1, v72, v18
	v_fmac_f32_e32 v1, v73, v19
	v_fmac_f32_e32 v1, v74, v20
	v_fmac_f32_e32 v1, v75, v21
	ds_read_b128 v[18:21], v102 offset:1648
	s_waitcnt lgkmcnt(0)
	v_fmac_f32_e32 v1, v76, v18
	v_fmac_f32_e32 v1, v77, v19
	v_fmac_f32_e32 v1, v78, v20
	v_fmac_f32_e32 v1, v79, v21
	ds_read_b128 v[18:21], v102 offset:1664
	s_waitcnt lgkmcnt(0)
	v_fmac_f32_e32 v1, v80, v18
	v_fmac_f32_e32 v1, v81, v19
	v_fmac_f32_e32 v1, v82, v20
	v_fmac_f32_e32 v1, v83, v21
	ds_read_b128 v[18:21], v102 offset:1680
	s_waitcnt lgkmcnt(0)
	v_fmac_f32_e32 v1, v84, v18
	v_fmac_f32_e32 v1, v85, v19
	v_fmac_f32_e32 v1, v86, v20
	v_fmac_f32_e32 v1, v87, v21
	ds_read_b128 v[18:21], v102 offset:1696
	s_waitcnt lgkmcnt(0)
	v_fmac_f32_e32 v1, v88, v18
	v_fmac_f32_e32 v1, v89, v19
	v_fmac_f32_e32 v1, v90, v20
	v_fmac_f32_e32 v1, v91, v21
	ds_read_b128 v[18:21], v102 offset:1712
	s_waitcnt lgkmcnt(0)
	v_fmac_f32_e32 v1, v92, v18
	v_fmac_f32_e32 v1, v93, v19
	v_fmac_f32_e32 v1, v94, v20
	v_fmac_f32_e32 v1, v95, v21
	ds_read_b128 v[18:21], v102 offset:1728
	s_waitcnt lgkmcnt(0)
	v_fmac_f32_e32 v1, v96, v18
	v_fmac_f32_e32 v1, v97, v19
	v_fmac_f32_e32 v1, v98, v20
	v_fmac_f32_e32 v1, v99, v21
	ds_read_b128 v[18:21], v102 offset:1744
	s_waitcnt lgkmcnt(0)
	v_fmac_f32_e32 v1, v100, v18
	v_fmac_f32_e32 v1, v101, v19
	v_fmac_f32_e32 v1, v12, v20
	v_fmac_f32_e32 v1, v13, v21
	ds_read_b128 v[18:21], v102 offset:1760
	s_waitcnt lgkmcnt(0)
	v_pk_mul_f32 v[2:3], v[14:15], v[18:19]
	s_nop 0
	v_add_f32_e32 v1, v1, v2
	v_add_f32_e32 v1, v1, v3
	v_pk_mul_f32 v[2:3], v[6:7], v[20:21]
	ds_read_b128 v[18:21], v102 offset:1776
	v_add_f32_e32 v1, v1, v2
	v_add_f32_e32 v1, v1, v3
	s_waitcnt lgkmcnt(0)
	v_pk_mul_f32 v[2:3], v[16:17], v[18:19]
	s_nop 0
	v_add_f32_e32 v1, v1, v2
	v_add_f32_e32 v1, v1, v3
	v_pk_mul_f32 v[2:3], v[4:5], v[20:21]
	ds_read_b128 v[18:21], v102 offset:1792
	v_add_f32_e32 v1, v1, v2
	v_add_f32_e32 v117, v1, v3
	v_mul_f32_e32 v1, 0x39800000, v117
	s_waitcnt lgkmcnt(0)
	v_fma_f32 v10, v48, v18, 0
	v_fmac_f32_e32 v10, v49, v19
	v_fmac_f32_e32 v10, v50, v20
	v_fmac_f32_e32 v10, v51, v21
	ds_read_b128 v[18:21], v102 offset:1808
	s_waitcnt lgkmcnt(0)
	v_fmac_f32_e32 v10, v52, v18
	v_fmac_f32_e32 v10, v53, v19
	v_fmac_f32_e32 v10, v54, v20
	v_fmac_f32_e32 v10, v55, v21
	ds_read_b128 v[18:21], v102 offset:1824
	s_waitcnt lgkmcnt(0)
	v_fmac_f32_e32 v10, v56, v18
	v_fmac_f32_e32 v10, v57, v19
	v_fmac_f32_e32 v10, v58, v20
	v_fmac_f32_e32 v10, v59, v21
	ds_read_b128 v[18:21], v102 offset:1840
	s_waitcnt lgkmcnt(0)
	v_fmac_f32_e32 v10, v60, v18
	v_fmac_f32_e32 v10, v61, v19
	v_fmac_f32_e32 v10, v62, v20
	v_fmac_f32_e32 v10, v63, v21
	ds_read_b128 v[18:21], v102 offset:1856
	s_waitcnt lgkmcnt(0)
	v_fmac_f32_e32 v10, v64, v18
	v_fmac_f32_e32 v10, v65, v19
	v_fmac_f32_e32 v10, v66, v20
	v_fmac_f32_e32 v10, v67, v21
	ds_read_b128 v[18:21], v102 offset:1872
	s_waitcnt lgkmcnt(0)
	v_fmac_f32_e32 v10, v68, v18
	v_fmac_f32_e32 v10, v69, v19
	v_fmac_f32_e32 v10, v70, v20
	v_fmac_f32_e32 v10, v71, v21
	ds_read_b128 v[18:21], v102 offset:1888
	s_waitcnt lgkmcnt(0)
	v_fmac_f32_e32 v10, v72, v18
	v_fmac_f32_e32 v10, v73, v19
	v_fmac_f32_e32 v10, v74, v20
	v_fmac_f32_e32 v10, v75, v21
	ds_read_b128 v[18:21], v102 offset:1904
	s_waitcnt lgkmcnt(0)
	v_fmac_f32_e32 v10, v76, v18
	v_fmac_f32_e32 v10, v77, v19
	v_fmac_f32_e32 v10, v78, v20
	v_fmac_f32_e32 v10, v79, v21
	ds_read_b128 v[18:21], v102 offset:1920
	s_waitcnt lgkmcnt(0)
	v_fmac_f32_e32 v10, v80, v18
	v_fmac_f32_e32 v10, v81, v19
	v_fmac_f32_e32 v10, v82, v20
	v_fmac_f32_e32 v10, v83, v21
	ds_read_b128 v[18:21], v102 offset:1936
	s_waitcnt lgkmcnt(0)
	v_fmac_f32_e32 v10, v84, v18
	v_fmac_f32_e32 v10, v85, v19
	v_fmac_f32_e32 v10, v86, v20
	v_fmac_f32_e32 v10, v87, v21
	ds_read_b128 v[18:21], v102 offset:1952
	s_waitcnt lgkmcnt(0)
	v_fmac_f32_e32 v10, v88, v18
	v_fmac_f32_e32 v10, v89, v19
	v_fmac_f32_e32 v10, v90, v20
	v_fmac_f32_e32 v10, v91, v21
	ds_read_b128 v[18:21], v102 offset:1968
	s_waitcnt lgkmcnt(0)
	v_fmac_f32_e32 v10, v92, v18
	v_fmac_f32_e32 v10, v93, v19
	v_fmac_f32_e32 v10, v94, v20
	v_fmac_f32_e32 v10, v95, v21
	ds_read_b128 v[18:21], v102 offset:1984
	s_waitcnt lgkmcnt(0)
	v_fmac_f32_e32 v10, v96, v18
	v_fmac_f32_e32 v10, v97, v19
	v_fmac_f32_e32 v10, v98, v20
	v_fmac_f32_e32 v10, v99, v21
	ds_read_b128 v[18:21], v102 offset:2000
	s_waitcnt lgkmcnt(0)
	v_fmac_f32_e32 v10, v100, v18
	v_fmac_f32_e32 v10, v101, v19
	v_fmac_f32_e32 v10, v12, v20
	v_fmac_f32_e32 v10, v13, v21
	ds_read_b128 v[18:21], v102 offset:2016
	s_waitcnt lgkmcnt(0)
	v_pk_mul_f32 v[2:3], v[14:15], v[18:19]
	s_nop 0
	v_add_f32_e32 v2, v10, v2
	v_add_f32_e32 v10, v2, v3
	v_pk_mul_f32 v[2:3], v[6:7], v[20:21]
	ds_read_b128 v[18:21], v102 offset:2032
	v_add_f32_e32 v2, v10, v2
	v_add_f32_e32 v10, v2, v3
	s_waitcnt lgkmcnt(0)
	v_pk_mul_f32 v[2:3], v[16:17], v[18:19]
	s_nop 0
	v_add_f32_e32 v2, v10, v2
	v_add_f32_e32 v10, v2, v3
	v_pk_mul_f32 v[2:3], v[4:5], v[20:21]
	ds_read_b128 v[18:21], v102 offset:2048
	v_add_f32_e32 v2, v10, v2
	v_add_f32_e32 v119, v2, v3
	v_mul_f32_e32 v2, 0x39800000, v119
	v_max3_f32 v0, v0, v1, v2
	s_waitcnt lgkmcnt(0)
	v_fma_f32 v1, v48, v18, 0
	v_fmac_f32_e32 v1, v49, v19
	v_fmac_f32_e32 v1, v50, v20
	v_fmac_f32_e32 v1, v51, v21
	ds_read_b128 v[18:21], v102 offset:2064
	s_waitcnt lgkmcnt(0)
	v_fmac_f32_e32 v1, v52, v18
	v_fmac_f32_e32 v1, v53, v19
	v_fmac_f32_e32 v1, v54, v20
	v_fmac_f32_e32 v1, v55, v21
	ds_read_b128 v[18:21], v102 offset:2080
	s_waitcnt lgkmcnt(0)
	v_fmac_f32_e32 v1, v56, v18
	v_fmac_f32_e32 v1, v57, v19
	v_fmac_f32_e32 v1, v58, v20
	v_fmac_f32_e32 v1, v59, v21
	ds_read_b128 v[18:21], v102 offset:2096
	s_waitcnt lgkmcnt(0)
	v_fmac_f32_e32 v1, v60, v18
	v_fmac_f32_e32 v1, v61, v19
	v_fmac_f32_e32 v1, v62, v20
	v_fmac_f32_e32 v1, v63, v21
	ds_read_b128 v[18:21], v102 offset:2112
	s_waitcnt lgkmcnt(0)
	v_fmac_f32_e32 v1, v64, v18
	v_fmac_f32_e32 v1, v65, v19
	v_fmac_f32_e32 v1, v66, v20
	v_fmac_f32_e32 v1, v67, v21
	ds_read_b128 v[18:21], v102 offset:2128
	s_waitcnt lgkmcnt(0)
	v_fmac_f32_e32 v1, v68, v18
	v_fmac_f32_e32 v1, v69, v19
	v_fmac_f32_e32 v1, v70, v20
	v_fmac_f32_e32 v1, v71, v21
	ds_read_b128 v[18:21], v102 offset:2144
	s_waitcnt lgkmcnt(0)
	v_fmac_f32_e32 v1, v72, v18
	v_fmac_f32_e32 v1, v73, v19
	v_fmac_f32_e32 v1, v74, v20
	v_fmac_f32_e32 v1, v75, v21
	ds_read_b128 v[18:21], v102 offset:2160
	s_waitcnt lgkmcnt(0)
	v_fmac_f32_e32 v1, v76, v18
	v_fmac_f32_e32 v1, v77, v19
	v_fmac_f32_e32 v1, v78, v20
	v_fmac_f32_e32 v1, v79, v21
	ds_read_b128 v[18:21], v102 offset:2176
	s_waitcnt lgkmcnt(0)
	v_fmac_f32_e32 v1, v80, v18
	v_fmac_f32_e32 v1, v81, v19
	v_fmac_f32_e32 v1, v82, v20
	v_fmac_f32_e32 v1, v83, v21
	ds_read_b128 v[18:21], v102 offset:2192
	s_waitcnt lgkmcnt(0)
	v_fmac_f32_e32 v1, v84, v18
	v_fmac_f32_e32 v1, v85, v19
	v_fmac_f32_e32 v1, v86, v20
	v_fmac_f32_e32 v1, v87, v21
	ds_read_b128 v[18:21], v102 offset:2208
	s_waitcnt lgkmcnt(0)
	v_fmac_f32_e32 v1, v88, v18
	v_fmac_f32_e32 v1, v89, v19
	v_fmac_f32_e32 v1, v90, v20
	v_fmac_f32_e32 v1, v91, v21
	ds_read_b128 v[18:21], v102 offset:2224
	s_waitcnt lgkmcnt(0)
	v_fmac_f32_e32 v1, v92, v18
	v_fmac_f32_e32 v1, v93, v19
	v_fmac_f32_e32 v1, v94, v20
	v_fmac_f32_e32 v1, v95, v21
	ds_read_b128 v[18:21], v102 offset:2240
	s_waitcnt lgkmcnt(0)
	v_fmac_f32_e32 v1, v96, v18
	v_fmac_f32_e32 v1, v97, v19
	v_fmac_f32_e32 v1, v98, v20
	v_fmac_f32_e32 v1, v99, v21
	ds_read_b128 v[18:21], v102 offset:2256
	s_waitcnt lgkmcnt(0)
	v_fmac_f32_e32 v1, v100, v18
	v_fmac_f32_e32 v1, v101, v19
	v_fmac_f32_e32 v1, v12, v20
	v_fmac_f32_e32 v1, v13, v21
	ds_read_b128 v[18:21], v102 offset:2272
	s_waitcnt lgkmcnt(0)
	v_pk_mul_f32 v[2:3], v[14:15], v[18:19]
	s_nop 0
	v_add_f32_e32 v1, v1, v2
	v_add_f32_e32 v1, v1, v3
	v_pk_mul_f32 v[2:3], v[6:7], v[20:21]
	ds_read_b128 v[18:21], v102 offset:2288
	v_add_f32_e32 v1, v1, v2
	v_add_f32_e32 v1, v1, v3
	s_waitcnt lgkmcnt(0)
	v_pk_mul_f32 v[2:3], v[16:17], v[18:19]
	s_nop 0
	v_add_f32_e32 v1, v1, v2
	v_add_f32_e32 v1, v1, v3
	v_pk_mul_f32 v[2:3], v[4:5], v[20:21]
	ds_read_b128 v[18:21], v102 offset:2304
	v_add_f32_e32 v1, v1, v2
	v_add_f32_e32 v233, v1, v3
	v_mul_f32_e32 v1, 0x39800000, v233
	s_waitcnt lgkmcnt(0)
	v_fma_f32 v10, v48, v18, 0
	v_fmac_f32_e32 v10, v49, v19
	v_fmac_f32_e32 v10, v50, v20
	v_fmac_f32_e32 v10, v51, v21
	ds_read_b128 v[18:21], v102 offset:2320
	s_waitcnt lgkmcnt(0)
	v_fmac_f32_e32 v10, v52, v18
	v_fmac_f32_e32 v10, v53, v19
	v_fmac_f32_e32 v10, v54, v20
	v_fmac_f32_e32 v10, v55, v21
	ds_read_b128 v[18:21], v102 offset:2336
	s_waitcnt lgkmcnt(0)
	v_fmac_f32_e32 v10, v56, v18
	v_fmac_f32_e32 v10, v57, v19
	v_fmac_f32_e32 v10, v58, v20
	v_fmac_f32_e32 v10, v59, v21
	ds_read_b128 v[18:21], v102 offset:2352
	s_waitcnt lgkmcnt(0)
	v_fmac_f32_e32 v10, v60, v18
	v_fmac_f32_e32 v10, v61, v19
	v_fmac_f32_e32 v10, v62, v20
	v_fmac_f32_e32 v10, v63, v21
	ds_read_b128 v[18:21], v102 offset:2368
	s_waitcnt lgkmcnt(0)
	v_fmac_f32_e32 v10, v64, v18
	v_fmac_f32_e32 v10, v65, v19
	v_fmac_f32_e32 v10, v66, v20
	v_fmac_f32_e32 v10, v67, v21
	ds_read_b128 v[18:21], v102 offset:2384
	s_waitcnt lgkmcnt(0)
	v_fmac_f32_e32 v10, v68, v18
	v_fmac_f32_e32 v10, v69, v19
	v_fmac_f32_e32 v10, v70, v20
	v_fmac_f32_e32 v10, v71, v21
	ds_read_b128 v[18:21], v102 offset:2400
	s_waitcnt lgkmcnt(0)
	v_fmac_f32_e32 v10, v72, v18
	v_fmac_f32_e32 v10, v73, v19
	v_fmac_f32_e32 v10, v74, v20
	v_fmac_f32_e32 v10, v75, v21
	ds_read_b128 v[18:21], v102 offset:2416
	s_waitcnt lgkmcnt(0)
	v_fmac_f32_e32 v10, v76, v18
	v_fmac_f32_e32 v10, v77, v19
	v_fmac_f32_e32 v10, v78, v20
	v_fmac_f32_e32 v10, v79, v21
	ds_read_b128 v[18:21], v102 offset:2432
	s_waitcnt lgkmcnt(0)
	v_fmac_f32_e32 v10, v80, v18
	v_fmac_f32_e32 v10, v81, v19
	v_fmac_f32_e32 v10, v82, v20
	v_fmac_f32_e32 v10, v83, v21
	ds_read_b128 v[18:21], v102 offset:2448
	s_waitcnt lgkmcnt(0)
	v_fmac_f32_e32 v10, v84, v18
	v_fmac_f32_e32 v10, v85, v19
	v_fmac_f32_e32 v10, v86, v20
	v_fmac_f32_e32 v10, v87, v21
	ds_read_b128 v[18:21], v102 offset:2464
	s_waitcnt lgkmcnt(0)
	v_fmac_f32_e32 v10, v88, v18
	v_fmac_f32_e32 v10, v89, v19
	v_fmac_f32_e32 v10, v90, v20
	v_fmac_f32_e32 v10, v91, v21
	ds_read_b128 v[18:21], v102 offset:2480
	s_waitcnt lgkmcnt(0)
	v_fmac_f32_e32 v10, v92, v18
	v_fmac_f32_e32 v10, v93, v19
	v_fmac_f32_e32 v10, v94, v20
	v_fmac_f32_e32 v10, v95, v21
	ds_read_b128 v[18:21], v102 offset:2496
	s_waitcnt lgkmcnt(0)
	v_fmac_f32_e32 v10, v96, v18
	v_fmac_f32_e32 v10, v97, v19
	v_fmac_f32_e32 v10, v98, v20
	v_fmac_f32_e32 v10, v99, v21
	ds_read_b128 v[18:21], v102 offset:2512
	s_waitcnt lgkmcnt(0)
	v_fmac_f32_e32 v10, v100, v18
	v_fmac_f32_e32 v10, v101, v19
	v_fmac_f32_e32 v10, v12, v20
	v_fmac_f32_e32 v10, v13, v21
	ds_read_b128 v[18:21], v102 offset:2528
	s_waitcnt lgkmcnt(0)
	v_pk_mul_f32 v[2:3], v[14:15], v[18:19]
	s_nop 0
	v_add_f32_e32 v2, v10, v2
	v_add_f32_e32 v10, v2, v3
	v_pk_mul_f32 v[2:3], v[6:7], v[20:21]
	ds_read_b128 v[18:21], v102 offset:2544
	v_add_f32_e32 v2, v10, v2
	v_add_f32_e32 v10, v2, v3
	s_waitcnt lgkmcnt(0)
	v_pk_mul_f32 v[2:3], v[16:17], v[18:19]
	s_nop 0
	v_add_f32_e32 v2, v10, v2
	v_add_f32_e32 v10, v2, v3
	v_pk_mul_f32 v[2:3], v[4:5], v[20:21]
	ds_read_b128 v[18:21], v102 offset:2560
	v_add_f32_e32 v2, v10, v2
	v_add_f32_e32 v234, v2, v3
	v_mul_f32_e32 v2, 0x39800000, v234
	v_max3_f32 v0, v0, v1, v2
	s_waitcnt lgkmcnt(0)
	v_fma_f32 v1, v48, v18, 0
	v_fmac_f32_e32 v1, v49, v19
	v_fmac_f32_e32 v1, v50, v20
	v_fmac_f32_e32 v1, v51, v21
	ds_read_b128 v[18:21], v102 offset:2576
	s_waitcnt lgkmcnt(0)
	v_fmac_f32_e32 v1, v52, v18
	v_fmac_f32_e32 v1, v53, v19
	v_fmac_f32_e32 v1, v54, v20
	v_fmac_f32_e32 v1, v55, v21
	ds_read_b128 v[18:21], v102 offset:2592
	s_waitcnt lgkmcnt(0)
	v_fmac_f32_e32 v1, v56, v18
	v_fmac_f32_e32 v1, v57, v19
	v_fmac_f32_e32 v1, v58, v20
	v_fmac_f32_e32 v1, v59, v21
	ds_read_b128 v[18:21], v102 offset:2608
	s_waitcnt lgkmcnt(0)
	v_fmac_f32_e32 v1, v60, v18
	v_fmac_f32_e32 v1, v61, v19
	v_fmac_f32_e32 v1, v62, v20
	v_fmac_f32_e32 v1, v63, v21
	ds_read_b128 v[18:21], v102 offset:2624
	s_waitcnt lgkmcnt(0)
	v_fmac_f32_e32 v1, v64, v18
	v_fmac_f32_e32 v1, v65, v19
	v_fmac_f32_e32 v1, v66, v20
	v_fmac_f32_e32 v1, v67, v21
	ds_read_b128 v[18:21], v102 offset:2640
	s_waitcnt lgkmcnt(0)
	v_fmac_f32_e32 v1, v68, v18
	v_fmac_f32_e32 v1, v69, v19
	v_fmac_f32_e32 v1, v70, v20
	v_fmac_f32_e32 v1, v71, v21
	ds_read_b128 v[18:21], v102 offset:2656
	s_waitcnt lgkmcnt(0)
	v_fmac_f32_e32 v1, v72, v18
	v_fmac_f32_e32 v1, v73, v19
	v_fmac_f32_e32 v1, v74, v20
	v_fmac_f32_e32 v1, v75, v21
	ds_read_b128 v[18:21], v102 offset:2672
	s_waitcnt lgkmcnt(0)
	v_fmac_f32_e32 v1, v76, v18
	v_fmac_f32_e32 v1, v77, v19
	v_fmac_f32_e32 v1, v78, v20
	v_fmac_f32_e32 v1, v79, v21
	ds_read_b128 v[18:21], v102 offset:2688
	s_waitcnt lgkmcnt(0)
	v_fmac_f32_e32 v1, v80, v18
	v_fmac_f32_e32 v1, v81, v19
	v_fmac_f32_e32 v1, v82, v20
	v_fmac_f32_e32 v1, v83, v21
	ds_read_b128 v[18:21], v102 offset:2704
	s_waitcnt lgkmcnt(0)
	v_fmac_f32_e32 v1, v84, v18
	v_fmac_f32_e32 v1, v85, v19
	v_fmac_f32_e32 v1, v86, v20
	v_fmac_f32_e32 v1, v87, v21
	ds_read_b128 v[18:21], v102 offset:2720
	s_waitcnt lgkmcnt(0)
	v_fmac_f32_e32 v1, v88, v18
	v_fmac_f32_e32 v1, v89, v19
	v_fmac_f32_e32 v1, v90, v20
	v_fmac_f32_e32 v1, v91, v21
	ds_read_b128 v[18:21], v102 offset:2736
	s_waitcnt lgkmcnt(0)
	v_fmac_f32_e32 v1, v92, v18
	v_fmac_f32_e32 v1, v93, v19
	v_fmac_f32_e32 v1, v94, v20
	v_fmac_f32_e32 v1, v95, v21
	ds_read_b128 v[18:21], v102 offset:2752
	s_waitcnt lgkmcnt(0)
	v_fmac_f32_e32 v1, v96, v18
	v_fmac_f32_e32 v1, v97, v19
	v_fmac_f32_e32 v1, v98, v20
	v_fmac_f32_e32 v1, v99, v21
	ds_read_b128 v[18:21], v102 offset:2768
	s_waitcnt lgkmcnt(0)
	v_fmac_f32_e32 v1, v100, v18
	v_fmac_f32_e32 v1, v101, v19
	v_fmac_f32_e32 v1, v12, v20
	v_fmac_f32_e32 v1, v13, v21
	ds_read_b128 v[18:21], v102 offset:2784
	s_waitcnt lgkmcnt(0)
	v_pk_mul_f32 v[2:3], v[14:15], v[18:19]
	s_nop 0
	v_add_f32_e32 v1, v1, v2
	v_add_f32_e32 v1, v1, v3
	v_pk_mul_f32 v[2:3], v[6:7], v[20:21]
	ds_read_b128 v[18:21], v102 offset:2800
	v_add_f32_e32 v1, v1, v2
	v_add_f32_e32 v1, v1, v3
	s_waitcnt lgkmcnt(0)
	v_pk_mul_f32 v[2:3], v[16:17], v[18:19]
	s_nop 0
	v_add_f32_e32 v1, v1, v2
	v_add_f32_e32 v1, v1, v3
	v_pk_mul_f32 v[2:3], v[4:5], v[20:21]
	ds_read_b128 v[18:21], v102 offset:2816
	v_add_f32_e32 v1, v1, v2
	v_add_f32_e32 v235, v1, v3
	v_mul_f32_e32 v1, 0x39800000, v235
	s_waitcnt lgkmcnt(0)
	v_fma_f32 v10, v48, v18, 0
	v_fmac_f32_e32 v10, v49, v19
	v_fmac_f32_e32 v10, v50, v20
	v_fmac_f32_e32 v10, v51, v21
	ds_read_b128 v[18:21], v102 offset:2832
	s_waitcnt lgkmcnt(0)
	v_fmac_f32_e32 v10, v52, v18
	v_fmac_f32_e32 v10, v53, v19
	v_fmac_f32_e32 v10, v54, v20
	v_fmac_f32_e32 v10, v55, v21
	ds_read_b128 v[18:21], v102 offset:2848
	s_waitcnt lgkmcnt(0)
	v_fmac_f32_e32 v10, v56, v18
	v_fmac_f32_e32 v10, v57, v19
	v_fmac_f32_e32 v10, v58, v20
	v_fmac_f32_e32 v10, v59, v21
	ds_read_b128 v[18:21], v102 offset:2864
	s_waitcnt lgkmcnt(0)
	v_fmac_f32_e32 v10, v60, v18
	v_fmac_f32_e32 v10, v61, v19
	v_fmac_f32_e32 v10, v62, v20
	v_fmac_f32_e32 v10, v63, v21
	ds_read_b128 v[18:21], v102 offset:2880
	s_waitcnt lgkmcnt(0)
	v_fmac_f32_e32 v10, v64, v18
	v_fmac_f32_e32 v10, v65, v19
	v_fmac_f32_e32 v10, v66, v20
	v_fmac_f32_e32 v10, v67, v21
	ds_read_b128 v[18:21], v102 offset:2896
	s_waitcnt lgkmcnt(0)
	v_fmac_f32_e32 v10, v68, v18
	v_fmac_f32_e32 v10, v69, v19
	v_fmac_f32_e32 v10, v70, v20
	v_fmac_f32_e32 v10, v71, v21
	ds_read_b128 v[18:21], v102 offset:2912
	s_waitcnt lgkmcnt(0)
	v_fmac_f32_e32 v10, v72, v18
	v_fmac_f32_e32 v10, v73, v19
	v_fmac_f32_e32 v10, v74, v20
	v_fmac_f32_e32 v10, v75, v21
	ds_read_b128 v[18:21], v102 offset:2928
	s_waitcnt lgkmcnt(0)
	v_fmac_f32_e32 v10, v76, v18
	v_fmac_f32_e32 v10, v77, v19
	v_fmac_f32_e32 v10, v78, v20
	v_fmac_f32_e32 v10, v79, v21
	ds_read_b128 v[18:21], v102 offset:2944
	s_waitcnt lgkmcnt(0)
	v_fmac_f32_e32 v10, v80, v18
	v_fmac_f32_e32 v10, v81, v19
	v_fmac_f32_e32 v10, v82, v20
	v_fmac_f32_e32 v10, v83, v21
	ds_read_b128 v[18:21], v102 offset:2960
	s_waitcnt lgkmcnt(0)
	v_fmac_f32_e32 v10, v84, v18
	v_fmac_f32_e32 v10, v85, v19
	v_fmac_f32_e32 v10, v86, v20
	v_fmac_f32_e32 v10, v87, v21
	ds_read_b128 v[18:21], v102 offset:2976
	s_waitcnt lgkmcnt(0)
	v_fmac_f32_e32 v10, v88, v18
	v_fmac_f32_e32 v10, v89, v19
	v_fmac_f32_e32 v10, v90, v20
	v_fmac_f32_e32 v10, v91, v21
	ds_read_b128 v[18:21], v102 offset:2992
	s_waitcnt lgkmcnt(0)
	v_fmac_f32_e32 v10, v92, v18
	v_fmac_f32_e32 v10, v93, v19
	v_fmac_f32_e32 v10, v94, v20
	v_fmac_f32_e32 v10, v95, v21
	ds_read_b128 v[18:21], v102 offset:3008
	s_waitcnt lgkmcnt(0)
	v_fmac_f32_e32 v10, v96, v18
	v_fmac_f32_e32 v10, v97, v19
	v_fmac_f32_e32 v10, v98, v20
	v_fmac_f32_e32 v10, v99, v21
	ds_read_b128 v[18:21], v102 offset:3024
	s_waitcnt lgkmcnt(0)
	v_fmac_f32_e32 v10, v100, v18
	v_fmac_f32_e32 v10, v101, v19
	v_fmac_f32_e32 v10, v12, v20
	v_fmac_f32_e32 v10, v13, v21
	ds_read_b128 v[18:21], v102 offset:3040
	s_waitcnt lgkmcnt(0)
	v_pk_mul_f32 v[2:3], v[14:15], v[18:19]
	s_nop 0
	v_add_f32_e32 v2, v10, v2
	v_add_f32_e32 v10, v2, v3
	v_pk_mul_f32 v[2:3], v[6:7], v[20:21]
	ds_read_b128 v[18:21], v102 offset:3056
	v_add_f32_e32 v2, v10, v2
	v_add_f32_e32 v10, v2, v3
	s_waitcnt lgkmcnt(0)
	v_pk_mul_f32 v[2:3], v[16:17], v[18:19]
	s_nop 0
	v_add_f32_e32 v2, v10, v2
	v_add_f32_e32 v10, v2, v3
	v_pk_mul_f32 v[2:3], v[4:5], v[20:21]
	ds_read_b128 v[18:21], v102 offset:3072
	v_add_f32_e32 v2, v10, v2
	v_add_f32_e32 v125, v2, v3
	v_mul_f32_e32 v2, 0x39800000, v125
	v_max3_f32 v0, v0, v1, v2
	s_waitcnt lgkmcnt(0)
	v_fma_f32 v1, v48, v18, 0
	v_fmac_f32_e32 v1, v49, v19
	v_fmac_f32_e32 v1, v50, v20
	v_fmac_f32_e32 v1, v51, v21
	ds_read_b128 v[18:21], v102 offset:3088
	s_waitcnt lgkmcnt(0)
	v_fmac_f32_e32 v1, v52, v18
	v_fmac_f32_e32 v1, v53, v19
	v_fmac_f32_e32 v1, v54, v20
	v_fmac_f32_e32 v1, v55, v21
	ds_read_b128 v[18:21], v102 offset:3104
	s_waitcnt lgkmcnt(0)
	v_fmac_f32_e32 v1, v56, v18
	v_fmac_f32_e32 v1, v57, v19
	v_fmac_f32_e32 v1, v58, v20
	v_fmac_f32_e32 v1, v59, v21
	ds_read_b128 v[18:21], v102 offset:3120
	s_waitcnt lgkmcnt(0)
	v_fmac_f32_e32 v1, v60, v18
	v_fmac_f32_e32 v1, v61, v19
	v_fmac_f32_e32 v1, v62, v20
	v_fmac_f32_e32 v1, v63, v21
	ds_read_b128 v[18:21], v102 offset:3136
	s_waitcnt lgkmcnt(0)
	v_fmac_f32_e32 v1, v64, v18
	v_fmac_f32_e32 v1, v65, v19
	v_fmac_f32_e32 v1, v66, v20
	v_fmac_f32_e32 v1, v67, v21
	ds_read_b128 v[18:21], v102 offset:3152
	s_waitcnt lgkmcnt(0)
	v_fmac_f32_e32 v1, v68, v18
	v_fmac_f32_e32 v1, v69, v19
	v_fmac_f32_e32 v1, v70, v20
	v_fmac_f32_e32 v1, v71, v21
	ds_read_b128 v[18:21], v102 offset:3168
	s_waitcnt lgkmcnt(0)
	v_fmac_f32_e32 v1, v72, v18
	v_fmac_f32_e32 v1, v73, v19
	v_fmac_f32_e32 v1, v74, v20
	v_fmac_f32_e32 v1, v75, v21
	ds_read_b128 v[18:21], v102 offset:3184
	s_waitcnt lgkmcnt(0)
	v_fmac_f32_e32 v1, v76, v18
	v_fmac_f32_e32 v1, v77, v19
	v_fmac_f32_e32 v1, v78, v20
	v_fmac_f32_e32 v1, v79, v21
	ds_read_b128 v[18:21], v102 offset:3200
	s_waitcnt lgkmcnt(0)
	v_fmac_f32_e32 v1, v80, v18
	v_fmac_f32_e32 v1, v81, v19
	v_fmac_f32_e32 v1, v82, v20
	v_fmac_f32_e32 v1, v83, v21
	ds_read_b128 v[18:21], v102 offset:3216
	s_waitcnt lgkmcnt(0)
	v_fmac_f32_e32 v1, v84, v18
	v_fmac_f32_e32 v1, v85, v19
	v_fmac_f32_e32 v1, v86, v20
	v_fmac_f32_e32 v1, v87, v21
	ds_read_b128 v[18:21], v102 offset:3232
	s_waitcnt lgkmcnt(0)
	v_fmac_f32_e32 v1, v88, v18
	v_fmac_f32_e32 v1, v89, v19
	v_fmac_f32_e32 v1, v90, v20
	v_fmac_f32_e32 v1, v91, v21
	ds_read_b128 v[18:21], v102 offset:3248
	s_waitcnt lgkmcnt(0)
	v_fmac_f32_e32 v1, v92, v18
	v_fmac_f32_e32 v1, v93, v19
	v_fmac_f32_e32 v1, v94, v20
	v_fmac_f32_e32 v1, v95, v21
	ds_read_b128 v[18:21], v102 offset:3264
	s_waitcnt lgkmcnt(0)
	v_fmac_f32_e32 v1, v96, v18
	v_fmac_f32_e32 v1, v97, v19
	v_fmac_f32_e32 v1, v98, v20
	v_fmac_f32_e32 v1, v99, v21
	ds_read_b128 v[18:21], v102 offset:3280
	s_waitcnt lgkmcnt(0)
	v_fmac_f32_e32 v1, v100, v18
	v_fmac_f32_e32 v1, v101, v19
	v_fmac_f32_e32 v1, v12, v20
	v_fmac_f32_e32 v1, v13, v21
	ds_read_b128 v[18:21], v102 offset:3296
	s_waitcnt lgkmcnt(0)
	v_pk_mul_f32 v[2:3], v[14:15], v[18:19]
	s_nop 0
	v_add_f32_e32 v1, v1, v2
	v_add_f32_e32 v1, v1, v3
	v_pk_mul_f32 v[2:3], v[6:7], v[20:21]
	ds_read_b128 v[18:21], v102 offset:3312
	v_add_f32_e32 v1, v1, v2
	v_add_f32_e32 v1, v1, v3
	s_waitcnt lgkmcnt(0)
	v_pk_mul_f32 v[2:3], v[16:17], v[18:19]
	s_nop 0
	v_add_f32_e32 v1, v1, v2
	v_add_f32_e32 v1, v1, v3
	v_pk_mul_f32 v[2:3], v[4:5], v[20:21]
	ds_read_b128 v[18:21], v102 offset:3328
	v_add_f32_e32 v1, v1, v2
	v_add_f32_e32 v229, v1, v3
	v_mul_f32_e32 v1, 0x39800000, v229
	s_waitcnt lgkmcnt(0)
	v_fma_f32 v10, v48, v18, 0
	v_fmac_f32_e32 v10, v49, v19
	v_fmac_f32_e32 v10, v50, v20
	v_fmac_f32_e32 v10, v51, v21
	ds_read_b128 v[18:21], v102 offset:3344
	s_waitcnt lgkmcnt(0)
	v_fmac_f32_e32 v10, v52, v18
	v_fmac_f32_e32 v10, v53, v19
	v_fmac_f32_e32 v10, v54, v20
	v_fmac_f32_e32 v10, v55, v21
	ds_read_b128 v[18:21], v102 offset:3360
	s_waitcnt lgkmcnt(0)
	v_fmac_f32_e32 v10, v56, v18
	v_fmac_f32_e32 v10, v57, v19
	v_fmac_f32_e32 v10, v58, v20
	v_fmac_f32_e32 v10, v59, v21
	ds_read_b128 v[18:21], v102 offset:3376
	s_waitcnt lgkmcnt(0)
	v_fmac_f32_e32 v10, v60, v18
	v_fmac_f32_e32 v10, v61, v19
	v_fmac_f32_e32 v10, v62, v20
	v_fmac_f32_e32 v10, v63, v21
	ds_read_b128 v[18:21], v102 offset:3392
	s_waitcnt lgkmcnt(0)
	v_fmac_f32_e32 v10, v64, v18
	v_fmac_f32_e32 v10, v65, v19
	v_fmac_f32_e32 v10, v66, v20
	v_fmac_f32_e32 v10, v67, v21
	ds_read_b128 v[18:21], v102 offset:3408
	s_waitcnt lgkmcnt(0)
	v_fmac_f32_e32 v10, v68, v18
	v_fmac_f32_e32 v10, v69, v19
	v_fmac_f32_e32 v10, v70, v20
	v_fmac_f32_e32 v10, v71, v21
	ds_read_b128 v[18:21], v102 offset:3424
	s_waitcnt lgkmcnt(0)
	v_fmac_f32_e32 v10, v72, v18
	v_fmac_f32_e32 v10, v73, v19
	v_fmac_f32_e32 v10, v74, v20
	v_fmac_f32_e32 v10, v75, v21
	ds_read_b128 v[18:21], v102 offset:3440
	s_waitcnt lgkmcnt(0)
	v_fmac_f32_e32 v10, v76, v18
	v_fmac_f32_e32 v10, v77, v19
	v_fmac_f32_e32 v10, v78, v20
	v_fmac_f32_e32 v10, v79, v21
	ds_read_b128 v[18:21], v102 offset:3456
	s_waitcnt lgkmcnt(0)
	v_fmac_f32_e32 v10, v80, v18
	v_fmac_f32_e32 v10, v81, v19
	v_fmac_f32_e32 v10, v82, v20
	v_fmac_f32_e32 v10, v83, v21
	ds_read_b128 v[18:21], v102 offset:3472
	s_waitcnt lgkmcnt(0)
	v_fmac_f32_e32 v10, v84, v18
	v_fmac_f32_e32 v10, v85, v19
	v_fmac_f32_e32 v10, v86, v20
	v_fmac_f32_e32 v10, v87, v21
	ds_read_b128 v[18:21], v102 offset:3488
	s_waitcnt lgkmcnt(0)
	v_fmac_f32_e32 v10, v88, v18
	v_fmac_f32_e32 v10, v89, v19
	v_fmac_f32_e32 v10, v90, v20
	v_fmac_f32_e32 v10, v91, v21
	ds_read_b128 v[18:21], v102 offset:3504
	s_waitcnt lgkmcnt(0)
	v_fmac_f32_e32 v10, v92, v18
	v_fmac_f32_e32 v10, v93, v19
	v_fmac_f32_e32 v10, v94, v20
	v_fmac_f32_e32 v10, v95, v21
	ds_read_b128 v[18:21], v102 offset:3520
	s_waitcnt lgkmcnt(0)
	v_fmac_f32_e32 v10, v96, v18
	v_fmac_f32_e32 v10, v97, v19
	v_fmac_f32_e32 v10, v98, v20
	v_fmac_f32_e32 v10, v99, v21
	ds_read_b128 v[18:21], v102 offset:3536
	s_waitcnt lgkmcnt(0)
	v_fmac_f32_e32 v10, v100, v18
	v_fmac_f32_e32 v10, v101, v19
	v_fmac_f32_e32 v10, v12, v20
	v_fmac_f32_e32 v10, v13, v21
	ds_read_b128 v[18:21], v102 offset:3552
	s_waitcnt lgkmcnt(0)
	v_pk_mul_f32 v[2:3], v[14:15], v[18:19]
	s_nop 0
	v_add_f32_e32 v2, v10, v2
	v_add_f32_e32 v10, v2, v3
	v_pk_mul_f32 v[2:3], v[6:7], v[20:21]
	ds_read_b128 v[18:21], v102 offset:3568
	v_add_f32_e32 v2, v10, v2
	v_add_f32_e32 v10, v2, v3
	s_waitcnt lgkmcnt(0)
	v_pk_mul_f32 v[2:3], v[16:17], v[18:19]
	s_nop 0
	v_add_f32_e32 v2, v10, v2
	v_add_f32_e32 v10, v2, v3
	v_pk_mul_f32 v[2:3], v[4:5], v[20:21]
	ds_read_b128 v[18:21], v102 offset:3584
	v_add_f32_e32 v2, v10, v2
	v_add_f32_e32 v109, v2, v3
	v_mul_f32_e32 v2, 0x39800000, v109
	v_max3_f32 v0, v0, v1, v2
	s_waitcnt lgkmcnt(0)
	v_fma_f32 v1, v48, v18, 0
	v_fmac_f32_e32 v1, v49, v19
	v_fmac_f32_e32 v1, v50, v20
	v_fmac_f32_e32 v1, v51, v21
	ds_read_b128 v[18:21], v102 offset:3600
	s_waitcnt lgkmcnt(0)
	v_fmac_f32_e32 v1, v52, v18
	v_fmac_f32_e32 v1, v53, v19
	v_fmac_f32_e32 v1, v54, v20
	v_fmac_f32_e32 v1, v55, v21
	ds_read_b128 v[18:21], v102 offset:3616
	s_waitcnt lgkmcnt(0)
	v_fmac_f32_e32 v1, v56, v18
	v_fmac_f32_e32 v1, v57, v19
	v_fmac_f32_e32 v1, v58, v20
	v_fmac_f32_e32 v1, v59, v21
	ds_read_b128 v[18:21], v102 offset:3632
	s_waitcnt lgkmcnt(0)
	v_fmac_f32_e32 v1, v60, v18
	v_fmac_f32_e32 v1, v61, v19
	v_fmac_f32_e32 v1, v62, v20
	v_fmac_f32_e32 v1, v63, v21
	ds_read_b128 v[18:21], v102 offset:3648
	s_waitcnt lgkmcnt(0)
	v_fmac_f32_e32 v1, v64, v18
	v_fmac_f32_e32 v1, v65, v19
	v_fmac_f32_e32 v1, v66, v20
	v_fmac_f32_e32 v1, v67, v21
	ds_read_b128 v[18:21], v102 offset:3664
	s_waitcnt lgkmcnt(0)
	v_fmac_f32_e32 v1, v68, v18
	v_fmac_f32_e32 v1, v69, v19
	v_fmac_f32_e32 v1, v70, v20
	v_fmac_f32_e32 v1, v71, v21
	ds_read_b128 v[18:21], v102 offset:3680
	s_waitcnt lgkmcnt(0)
	v_fmac_f32_e32 v1, v72, v18
	v_fmac_f32_e32 v1, v73, v19
	v_fmac_f32_e32 v1, v74, v20
	v_fmac_f32_e32 v1, v75, v21
	ds_read_b128 v[18:21], v102 offset:3696
	s_waitcnt lgkmcnt(0)
	v_fmac_f32_e32 v1, v76, v18
	v_fmac_f32_e32 v1, v77, v19
	v_fmac_f32_e32 v1, v78, v20
	v_fmac_f32_e32 v1, v79, v21
	ds_read_b128 v[18:21], v102 offset:3712
	s_waitcnt lgkmcnt(0)
	v_fmac_f32_e32 v1, v80, v18
	v_fmac_f32_e32 v1, v81, v19
	v_fmac_f32_e32 v1, v82, v20
	v_fmac_f32_e32 v1, v83, v21
	ds_read_b128 v[18:21], v102 offset:3728
	s_waitcnt lgkmcnt(0)
	v_fmac_f32_e32 v1, v84, v18
	v_fmac_f32_e32 v1, v85, v19
	v_fmac_f32_e32 v1, v86, v20
	v_fmac_f32_e32 v1, v87, v21
	ds_read_b128 v[18:21], v102 offset:3744
	s_waitcnt lgkmcnt(0)
	v_fmac_f32_e32 v1, v88, v18
	v_fmac_f32_e32 v1, v89, v19
	v_fmac_f32_e32 v1, v90, v20
	v_fmac_f32_e32 v1, v91, v21
	ds_read_b128 v[18:21], v102 offset:3760
	s_waitcnt lgkmcnt(0)
	v_fmac_f32_e32 v1, v92, v18
	v_fmac_f32_e32 v1, v93, v19
	v_fmac_f32_e32 v1, v94, v20
	v_fmac_f32_e32 v1, v95, v21
	ds_read_b128 v[18:21], v102 offset:3776
	s_waitcnt lgkmcnt(0)
	v_fmac_f32_e32 v1, v96, v18
	v_fmac_f32_e32 v1, v97, v19
	v_fmac_f32_e32 v1, v98, v20
	v_fmac_f32_e32 v1, v99, v21
	ds_read_b128 v[18:21], v102 offset:3792
	s_waitcnt lgkmcnt(0)
	v_fmac_f32_e32 v1, v100, v18
	v_fmac_f32_e32 v1, v101, v19
	v_fmac_f32_e32 v1, v12, v20
	v_fmac_f32_e32 v1, v13, v21
	ds_read_b128 v[18:21], v102 offset:3808
	s_waitcnt lgkmcnt(0)
	v_pk_mul_f32 v[2:3], v[14:15], v[18:19]
	s_nop 0
	v_add_f32_e32 v1, v1, v2
	v_add_f32_e32 v1, v1, v3
	v_pk_mul_f32 v[2:3], v[6:7], v[20:21]
	ds_read_b128 v[18:21], v102 offset:3824
	v_add_f32_e32 v1, v1, v2
	v_add_f32_e32 v1, v1, v3
	s_waitcnt lgkmcnt(0)
	v_pk_mul_f32 v[2:3], v[16:17], v[18:19]
	s_nop 0
	v_add_f32_e32 v1, v1, v2
	v_add_f32_e32 v1, v1, v3
	v_pk_mul_f32 v[2:3], v[4:5], v[20:21]
	ds_read_b128 v[18:21], v102 offset:3840
	v_add_f32_e32 v1, v1, v2
	v_add_f32_e32 v111, v1, v3
	v_mul_f32_e32 v1, 0x39800000, v111
	s_waitcnt lgkmcnt(0)
	v_fma_f32 v10, v48, v18, 0
	v_fmac_f32_e32 v10, v49, v19
	v_fmac_f32_e32 v10, v50, v20
	v_fmac_f32_e32 v10, v51, v21
	ds_read_b128 v[18:21], v102 offset:3856
	s_waitcnt lgkmcnt(0)
	v_fmac_f32_e32 v10, v52, v18
	v_fmac_f32_e32 v10, v53, v19
	v_fmac_f32_e32 v10, v54, v20
	v_fmac_f32_e32 v10, v55, v21
	ds_read_b128 v[18:21], v102 offset:3872
	s_waitcnt lgkmcnt(0)
	v_fmac_f32_e32 v10, v56, v18
	v_fmac_f32_e32 v10, v57, v19
	v_fmac_f32_e32 v10, v58, v20
	v_fmac_f32_e32 v10, v59, v21
	ds_read_b128 v[18:21], v102 offset:3888
	s_waitcnt lgkmcnt(0)
	v_fmac_f32_e32 v10, v60, v18
	v_fmac_f32_e32 v10, v61, v19
	v_fmac_f32_e32 v10, v62, v20
	v_fmac_f32_e32 v10, v63, v21
	ds_read_b128 v[18:21], v102 offset:3904
	s_waitcnt lgkmcnt(0)
	v_fmac_f32_e32 v10, v64, v18
	v_fmac_f32_e32 v10, v65, v19
	v_fmac_f32_e32 v10, v66, v20
	v_fmac_f32_e32 v10, v67, v21
	ds_read_b128 v[18:21], v102 offset:3920
	s_waitcnt lgkmcnt(0)
	v_fmac_f32_e32 v10, v68, v18
	v_fmac_f32_e32 v10, v69, v19
	v_fmac_f32_e32 v10, v70, v20
	v_fmac_f32_e32 v10, v71, v21
	ds_read_b128 v[18:21], v102 offset:3936
	s_waitcnt lgkmcnt(0)
	v_fmac_f32_e32 v10, v72, v18
	v_fmac_f32_e32 v10, v73, v19
	v_fmac_f32_e32 v10, v74, v20
	v_fmac_f32_e32 v10, v75, v21
	ds_read_b128 v[18:21], v102 offset:3952
	s_waitcnt lgkmcnt(0)
	v_fmac_f32_e32 v10, v76, v18
	v_fmac_f32_e32 v10, v77, v19
	v_fmac_f32_e32 v10, v78, v20
	v_fmac_f32_e32 v10, v79, v21
	ds_read_b128 v[18:21], v102 offset:3968
	s_waitcnt lgkmcnt(0)
	v_fmac_f32_e32 v10, v80, v18
	v_fmac_f32_e32 v10, v81, v19
	v_fmac_f32_e32 v10, v82, v20
	v_fmac_f32_e32 v10, v83, v21
	ds_read_b128 v[18:21], v102 offset:3984
	s_waitcnt lgkmcnt(0)
	v_fmac_f32_e32 v10, v84, v18
	v_fmac_f32_e32 v10, v85, v19
	v_fmac_f32_e32 v10, v86, v20
	v_fmac_f32_e32 v10, v87, v21
	ds_read_b128 v[18:21], v102 offset:4000
	s_waitcnt lgkmcnt(0)
	v_fmac_f32_e32 v10, v88, v18
	v_fmac_f32_e32 v10, v89, v19
	v_fmac_f32_e32 v10, v90, v20
	v_fmac_f32_e32 v10, v91, v21
	ds_read_b128 v[18:21], v102 offset:4016
	s_waitcnt lgkmcnt(0)
	v_fmac_f32_e32 v10, v92, v18
	v_fmac_f32_e32 v10, v93, v19
	v_fmac_f32_e32 v10, v94, v20
	v_fmac_f32_e32 v10, v95, v21
	ds_read_b128 v[18:21], v102 offset:4032
	s_waitcnt lgkmcnt(0)
	v_fmac_f32_e32 v10, v96, v18
	v_fmac_f32_e32 v10, v97, v19
	v_fmac_f32_e32 v10, v98, v20
	v_fmac_f32_e32 v10, v99, v21
	ds_read_b128 v[18:21], v102 offset:4048
	s_waitcnt lgkmcnt(0)
	v_fmac_f32_e32 v10, v100, v18
	v_fmac_f32_e32 v10, v101, v19
	v_fmac_f32_e32 v10, v12, v20
	v_fmac_f32_e32 v10, v13, v21
	ds_read_b128 v[18:21], v102 offset:4064
	s_waitcnt lgkmcnt(0)
	v_pk_mul_f32 v[2:3], v[14:15], v[18:19]
	s_nop 0
	v_add_f32_e32 v2, v10, v2
	v_add_f32_e32 v10, v2, v3
	v_pk_mul_f32 v[2:3], v[6:7], v[20:21]
	ds_read_b128 v[18:21], v102 offset:4080
	v_add_f32_e32 v2, v10, v2
	v_add_f32_e32 v10, v2, v3
	s_waitcnt lgkmcnt(0)
	v_pk_mul_f32 v[2:3], v[16:17], v[18:19]
	s_nop 0
	v_add_f32_e32 v2, v10, v2
	v_add_f32_e32 v10, v2, v3
	v_pk_mul_f32 v[2:3], v[4:5], v[20:21]
	ds_read_b128 v[18:21], v102 offset:4096
	v_add_f32_e32 v2, v10, v2
	v_add_f32_e32 v113, v2, v3
	v_mul_f32_e32 v2, 0x39800000, v113
	v_max3_f32 v0, v0, v1, v2
	s_waitcnt lgkmcnt(0)
	v_fma_f32 v1, v48, v18, 0
	v_fmac_f32_e32 v1, v49, v19
	v_fmac_f32_e32 v1, v50, v20
	v_fmac_f32_e32 v1, v51, v21
	ds_read_b128 v[18:21], v102 offset:4112
	s_waitcnt lgkmcnt(0)
	v_fmac_f32_e32 v1, v52, v18
	v_fmac_f32_e32 v1, v53, v19
	v_fmac_f32_e32 v1, v54, v20
	v_fmac_f32_e32 v1, v55, v21
	ds_read_b128 v[18:21], v102 offset:4128
	s_waitcnt lgkmcnt(0)
	v_fmac_f32_e32 v1, v56, v18
	v_fmac_f32_e32 v1, v57, v19
	v_fmac_f32_e32 v1, v58, v20
	v_fmac_f32_e32 v1, v59, v21
	ds_read_b128 v[18:21], v102 offset:4144
	s_waitcnt lgkmcnt(0)
	v_fmac_f32_e32 v1, v60, v18
	v_fmac_f32_e32 v1, v61, v19
	v_fmac_f32_e32 v1, v62, v20
	v_fmac_f32_e32 v1, v63, v21
	ds_read_b128 v[18:21], v102 offset:4160
	s_waitcnt lgkmcnt(0)
	v_fmac_f32_e32 v1, v64, v18
	v_fmac_f32_e32 v1, v65, v19
	v_fmac_f32_e32 v1, v66, v20
	v_fmac_f32_e32 v1, v67, v21
	ds_read_b128 v[18:21], v102 offset:4176
	s_waitcnt lgkmcnt(0)
	v_fmac_f32_e32 v1, v68, v18
	v_fmac_f32_e32 v1, v69, v19
	v_fmac_f32_e32 v1, v70, v20
	v_fmac_f32_e32 v1, v71, v21
	ds_read_b128 v[18:21], v102 offset:4192
	s_waitcnt lgkmcnt(0)
	v_fmac_f32_e32 v1, v72, v18
	v_fmac_f32_e32 v1, v73, v19
	v_fmac_f32_e32 v1, v74, v20
	v_fmac_f32_e32 v1, v75, v21
	ds_read_b128 v[18:21], v102 offset:4208
	s_waitcnt lgkmcnt(0)
	v_fmac_f32_e32 v1, v76, v18
	v_fmac_f32_e32 v1, v77, v19
	v_fmac_f32_e32 v1, v78, v20
	v_fmac_f32_e32 v1, v79, v21
	ds_read_b128 v[18:21], v102 offset:4224
	s_waitcnt lgkmcnt(0)
	v_fmac_f32_e32 v1, v80, v18
	v_fmac_f32_e32 v1, v81, v19
	v_fmac_f32_e32 v1, v82, v20
	v_fmac_f32_e32 v1, v83, v21
	ds_read_b128 v[18:21], v102 offset:4240
	s_waitcnt lgkmcnt(0)
	v_fmac_f32_e32 v1, v84, v18
	v_fmac_f32_e32 v1, v85, v19
	v_fmac_f32_e32 v1, v86, v20
	v_fmac_f32_e32 v1, v87, v21
	ds_read_b128 v[18:21], v102 offset:4256
	s_waitcnt lgkmcnt(0)
	v_fmac_f32_e32 v1, v88, v18
	v_fmac_f32_e32 v1, v89, v19
	v_fmac_f32_e32 v1, v90, v20
	v_fmac_f32_e32 v1, v91, v21
	ds_read_b128 v[18:21], v102 offset:4272
	s_waitcnt lgkmcnt(0)
	v_fmac_f32_e32 v1, v92, v18
	v_fmac_f32_e32 v1, v93, v19
	v_fmac_f32_e32 v1, v94, v20
	v_fmac_f32_e32 v1, v95, v21
	ds_read_b128 v[18:21], v102 offset:4288
	s_waitcnt lgkmcnt(0)
	v_fmac_f32_e32 v1, v96, v18
	v_fmac_f32_e32 v1, v97, v19
	v_fmac_f32_e32 v1, v98, v20
	v_fmac_f32_e32 v1, v99, v21
	ds_read_b128 v[18:21], v102 offset:4304
	s_waitcnt lgkmcnt(0)
	v_fmac_f32_e32 v1, v100, v18
	v_fmac_f32_e32 v1, v101, v19
	v_fmac_f32_e32 v1, v12, v20
	v_fmac_f32_e32 v1, v13, v21
	ds_read_b128 v[18:21], v102 offset:4320
	s_waitcnt lgkmcnt(0)
	v_pk_mul_f32 v[2:3], v[14:15], v[18:19]
	s_nop 0
	v_add_f32_e32 v1, v1, v2
	v_add_f32_e32 v1, v1, v3
	v_pk_mul_f32 v[2:3], v[6:7], v[20:21]
	ds_read_b128 v[18:21], v102 offset:4336
	v_add_f32_e32 v1, v1, v2
	v_add_f32_e32 v1, v1, v3
	s_waitcnt lgkmcnt(0)
	v_pk_mul_f32 v[2:3], v[16:17], v[18:19]
	s_nop 0
	v_add_f32_e32 v1, v1, v2
	v_add_f32_e32 v1, v1, v3
	v_pk_mul_f32 v[2:3], v[4:5], v[20:21]
	ds_read_b128 v[18:21], v102 offset:4352
	v_add_f32_e32 v1, v1, v2
	v_add_f32_e32 v115, v1, v3
	v_mul_f32_e32 v1, 0x39800000, v115
	s_waitcnt lgkmcnt(0)
	v_fma_f32 v10, v48, v18, 0
	v_fmac_f32_e32 v10, v49, v19
	v_fmac_f32_e32 v10, v50, v20
	v_fmac_f32_e32 v10, v51, v21
	ds_read_b128 v[18:21], v102 offset:4368
	s_waitcnt lgkmcnt(0)
	v_fmac_f32_e32 v10, v52, v18
	v_fmac_f32_e32 v10, v53, v19
	v_fmac_f32_e32 v10, v54, v20
	v_fmac_f32_e32 v10, v55, v21
	ds_read_b128 v[18:21], v102 offset:4384
	s_waitcnt lgkmcnt(0)
	v_fmac_f32_e32 v10, v56, v18
	v_fmac_f32_e32 v10, v57, v19
	v_fmac_f32_e32 v10, v58, v20
	v_fmac_f32_e32 v10, v59, v21
	ds_read_b128 v[18:21], v102 offset:4400
	s_waitcnt lgkmcnt(0)
	v_fmac_f32_e32 v10, v60, v18
	v_fmac_f32_e32 v10, v61, v19
	v_fmac_f32_e32 v10, v62, v20
	v_fmac_f32_e32 v10, v63, v21
	ds_read_b128 v[18:21], v102 offset:4416
	s_waitcnt lgkmcnt(0)
	v_fmac_f32_e32 v10, v64, v18
	v_fmac_f32_e32 v10, v65, v19
	v_fmac_f32_e32 v10, v66, v20
	v_fmac_f32_e32 v10, v67, v21
	ds_read_b128 v[18:21], v102 offset:4432
	s_waitcnt lgkmcnt(0)
	v_fmac_f32_e32 v10, v68, v18
	v_fmac_f32_e32 v10, v69, v19
	v_fmac_f32_e32 v10, v70, v20
	v_fmac_f32_e32 v10, v71, v21
	ds_read_b128 v[18:21], v102 offset:4448
	s_waitcnt lgkmcnt(0)
	v_fmac_f32_e32 v10, v72, v18
	v_fmac_f32_e32 v10, v73, v19
	v_fmac_f32_e32 v10, v74, v20
	v_fmac_f32_e32 v10, v75, v21
	ds_read_b128 v[18:21], v102 offset:4464
	s_waitcnt lgkmcnt(0)
	v_fmac_f32_e32 v10, v76, v18
	v_fmac_f32_e32 v10, v77, v19
	v_fmac_f32_e32 v10, v78, v20
	v_fmac_f32_e32 v10, v79, v21
	ds_read_b128 v[18:21], v102 offset:4480
	s_waitcnt lgkmcnt(0)
	v_fmac_f32_e32 v10, v80, v18
	v_fmac_f32_e32 v10, v81, v19
	v_fmac_f32_e32 v10, v82, v20
	v_fmac_f32_e32 v10, v83, v21
	ds_read_b128 v[18:21], v102 offset:4496
	s_waitcnt lgkmcnt(0)
	v_fmac_f32_e32 v10, v84, v18
	v_fmac_f32_e32 v10, v85, v19
	v_fmac_f32_e32 v10, v86, v20
	v_fmac_f32_e32 v10, v87, v21
	ds_read_b128 v[18:21], v102 offset:4512
	s_waitcnt lgkmcnt(0)
	v_fmac_f32_e32 v10, v88, v18
	v_fmac_f32_e32 v10, v89, v19
	v_fmac_f32_e32 v10, v90, v20
	v_fmac_f32_e32 v10, v91, v21
	ds_read_b128 v[18:21], v102 offset:4528
	s_waitcnt lgkmcnt(0)
	v_fmac_f32_e32 v10, v92, v18
	v_fmac_f32_e32 v10, v93, v19
	v_fmac_f32_e32 v10, v94, v20
	v_fmac_f32_e32 v10, v95, v21
	ds_read_b128 v[18:21], v102 offset:4544
	s_waitcnt lgkmcnt(0)
	v_fmac_f32_e32 v10, v96, v18
	v_fmac_f32_e32 v10, v97, v19
	v_fmac_f32_e32 v10, v98, v20
	v_fmac_f32_e32 v10, v99, v21
	ds_read_b128 v[18:21], v102 offset:4560
	s_waitcnt lgkmcnt(0)
	v_fmac_f32_e32 v10, v100, v18
	v_fmac_f32_e32 v10, v101, v19
	v_fmac_f32_e32 v10, v12, v20
	v_fmac_f32_e32 v10, v13, v21
	ds_read_b128 v[18:21], v102 offset:4576
	s_waitcnt lgkmcnt(0)
	v_pk_mul_f32 v[2:3], v[14:15], v[18:19]
	s_nop 0
	v_add_f32_e32 v2, v10, v2
	v_add_f32_e32 v10, v2, v3
	v_pk_mul_f32 v[2:3], v[6:7], v[20:21]
	ds_read_b128 v[18:21], v102 offset:4592
	v_add_f32_e32 v2, v10, v2
	v_add_f32_e32 v10, v2, v3
	s_waitcnt lgkmcnt(0)
	v_pk_mul_f32 v[2:3], v[16:17], v[18:19]
	s_nop 0
	v_add_f32_e32 v2, v10, v2
	v_add_f32_e32 v10, v2, v3
	v_pk_mul_f32 v[2:3], v[4:5], v[20:21]
	ds_read_b128 v[18:21], v102 offset:4608
	v_add_f32_e32 v2, v10, v2
	v_add_f32_e32 v116, v2, v3
	v_mul_f32_e32 v2, 0x39800000, v116
	v_max3_f32 v0, v0, v1, v2
	s_waitcnt lgkmcnt(0)
	v_fma_f32 v1, v48, v18, 0
	v_fmac_f32_e32 v1, v49, v19
	v_fmac_f32_e32 v1, v50, v20
	v_fmac_f32_e32 v1, v51, v21
	ds_read_b128 v[18:21], v102 offset:4624
	s_waitcnt lgkmcnt(0)
	v_fmac_f32_e32 v1, v52, v18
	v_fmac_f32_e32 v1, v53, v19
	v_fmac_f32_e32 v1, v54, v20
	v_fmac_f32_e32 v1, v55, v21
	ds_read_b128 v[18:21], v102 offset:4640
	s_waitcnt lgkmcnt(0)
	v_fmac_f32_e32 v1, v56, v18
	v_fmac_f32_e32 v1, v57, v19
	v_fmac_f32_e32 v1, v58, v20
	v_fmac_f32_e32 v1, v59, v21
	ds_read_b128 v[18:21], v102 offset:4656
	s_waitcnt lgkmcnt(0)
	v_fmac_f32_e32 v1, v60, v18
	v_fmac_f32_e32 v1, v61, v19
	v_fmac_f32_e32 v1, v62, v20
	v_fmac_f32_e32 v1, v63, v21
	ds_read_b128 v[18:21], v102 offset:4672
	s_waitcnt lgkmcnt(0)
	v_fmac_f32_e32 v1, v64, v18
	v_fmac_f32_e32 v1, v65, v19
	v_fmac_f32_e32 v1, v66, v20
	v_fmac_f32_e32 v1, v67, v21
	ds_read_b128 v[18:21], v102 offset:4688
	s_waitcnt lgkmcnt(0)
	v_fmac_f32_e32 v1, v68, v18
	v_fmac_f32_e32 v1, v69, v19
	v_fmac_f32_e32 v1, v70, v20
	v_fmac_f32_e32 v1, v71, v21
	ds_read_b128 v[18:21], v102 offset:4704
	s_waitcnt lgkmcnt(0)
	v_fmac_f32_e32 v1, v72, v18
	v_fmac_f32_e32 v1, v73, v19
	v_fmac_f32_e32 v1, v74, v20
	v_fmac_f32_e32 v1, v75, v21
	ds_read_b128 v[18:21], v102 offset:4720
	s_waitcnt lgkmcnt(0)
	v_fmac_f32_e32 v1, v76, v18
	v_fmac_f32_e32 v1, v77, v19
	v_fmac_f32_e32 v1, v78, v20
	v_fmac_f32_e32 v1, v79, v21
	ds_read_b128 v[18:21], v102 offset:4736
	s_waitcnt lgkmcnt(0)
	v_fmac_f32_e32 v1, v80, v18
	v_fmac_f32_e32 v1, v81, v19
	v_fmac_f32_e32 v1, v82, v20
	v_fmac_f32_e32 v1, v83, v21
	ds_read_b128 v[18:21], v102 offset:4752
	s_waitcnt lgkmcnt(0)
	v_fmac_f32_e32 v1, v84, v18
	v_fmac_f32_e32 v1, v85, v19
	v_fmac_f32_e32 v1, v86, v20
	v_fmac_f32_e32 v1, v87, v21
	ds_read_b128 v[18:21], v102 offset:4768
	s_waitcnt lgkmcnt(0)
	v_fmac_f32_e32 v1, v88, v18
	v_fmac_f32_e32 v1, v89, v19
	v_fmac_f32_e32 v1, v90, v20
	v_fmac_f32_e32 v1, v91, v21
	ds_read_b128 v[18:21], v102 offset:4784
	s_waitcnt lgkmcnt(0)
	v_fmac_f32_e32 v1, v92, v18
	v_fmac_f32_e32 v1, v93, v19
	v_fmac_f32_e32 v1, v94, v20
	v_fmac_f32_e32 v1, v95, v21
	ds_read_b128 v[18:21], v102 offset:4800
	s_waitcnt lgkmcnt(0)
	v_fmac_f32_e32 v1, v96, v18
	v_fmac_f32_e32 v1, v97, v19
	v_fmac_f32_e32 v1, v98, v20
	v_fmac_f32_e32 v1, v99, v21
	ds_read_b128 v[18:21], v102 offset:4816
	s_waitcnt lgkmcnt(0)
	v_fmac_f32_e32 v1, v100, v18
	v_fmac_f32_e32 v1, v101, v19
	v_fmac_f32_e32 v1, v12, v20
	v_fmac_f32_e32 v1, v13, v21
	ds_read_b128 v[18:21], v102 offset:4832
	s_waitcnt lgkmcnt(0)
	v_pk_mul_f32 v[2:3], v[14:15], v[18:19]
	s_nop 0
	v_add_f32_e32 v1, v1, v2
	v_add_f32_e32 v1, v1, v3
	v_pk_mul_f32 v[2:3], v[6:7], v[20:21]
	ds_read_b128 v[18:21], v102 offset:4848
	v_add_f32_e32 v1, v1, v2
	v_add_f32_e32 v1, v1, v3
	s_waitcnt lgkmcnt(0)
	v_pk_mul_f32 v[2:3], v[16:17], v[18:19]
	s_nop 0
	v_add_f32_e32 v1, v1, v2
	v_add_f32_e32 v1, v1, v3
	v_pk_mul_f32 v[2:3], v[4:5], v[20:21]
	ds_read_b128 v[18:21], v102 offset:4864
	v_add_f32_e32 v1, v1, v2
	v_add_f32_e32 v118, v1, v3
	v_mul_f32_e32 v1, 0x39800000, v118
	s_waitcnt lgkmcnt(0)
	v_fma_f32 v10, v48, v18, 0
	v_fmac_f32_e32 v10, v49, v19
	v_fmac_f32_e32 v10, v50, v20
	v_fmac_f32_e32 v10, v51, v21
	ds_read_b128 v[18:21], v102 offset:4880
	s_waitcnt lgkmcnt(0)
	v_fmac_f32_e32 v10, v52, v18
	v_fmac_f32_e32 v10, v53, v19
	v_fmac_f32_e32 v10, v54, v20
	v_fmac_f32_e32 v10, v55, v21
	ds_read_b128 v[18:21], v102 offset:4896
	s_waitcnt lgkmcnt(0)
	v_fmac_f32_e32 v10, v56, v18
	v_fmac_f32_e32 v10, v57, v19
	v_fmac_f32_e32 v10, v58, v20
	v_fmac_f32_e32 v10, v59, v21
	ds_read_b128 v[18:21], v102 offset:4912
	s_waitcnt lgkmcnt(0)
	v_fmac_f32_e32 v10, v60, v18
	v_fmac_f32_e32 v10, v61, v19
	v_fmac_f32_e32 v10, v62, v20
	v_fmac_f32_e32 v10, v63, v21
	ds_read_b128 v[18:21], v102 offset:4928
	s_waitcnt lgkmcnt(0)
	v_fmac_f32_e32 v10, v64, v18
	v_fmac_f32_e32 v10, v65, v19
	v_fmac_f32_e32 v10, v66, v20
	v_fmac_f32_e32 v10, v67, v21
	ds_read_b128 v[18:21], v102 offset:4944
	s_waitcnt lgkmcnt(0)
	v_fmac_f32_e32 v10, v68, v18
	v_fmac_f32_e32 v10, v69, v19
	v_fmac_f32_e32 v10, v70, v20
	v_fmac_f32_e32 v10, v71, v21
	ds_read_b128 v[18:21], v102 offset:4960
	s_waitcnt lgkmcnt(0)
	v_fmac_f32_e32 v10, v72, v18
	v_fmac_f32_e32 v10, v73, v19
	v_fmac_f32_e32 v10, v74, v20
	v_fmac_f32_e32 v10, v75, v21
	ds_read_b128 v[18:21], v102 offset:4976
	s_waitcnt lgkmcnt(0)
	v_fmac_f32_e32 v10, v76, v18
	v_fmac_f32_e32 v10, v77, v19
	v_fmac_f32_e32 v10, v78, v20
	v_fmac_f32_e32 v10, v79, v21
	ds_read_b128 v[18:21], v102 offset:4992
	s_waitcnt lgkmcnt(0)
	v_fmac_f32_e32 v10, v80, v18
	v_fmac_f32_e32 v10, v81, v19
	v_fmac_f32_e32 v10, v82, v20
	v_fmac_f32_e32 v10, v83, v21
	ds_read_b128 v[18:21], v102 offset:5008
	s_waitcnt lgkmcnt(0)
	v_fmac_f32_e32 v10, v84, v18
	v_fmac_f32_e32 v10, v85, v19
	v_fmac_f32_e32 v10, v86, v20
	v_fmac_f32_e32 v10, v87, v21
	ds_read_b128 v[18:21], v102 offset:5024
	s_waitcnt lgkmcnt(0)
	v_fmac_f32_e32 v10, v88, v18
	v_fmac_f32_e32 v10, v89, v19
	v_fmac_f32_e32 v10, v90, v20
	v_fmac_f32_e32 v10, v91, v21
	ds_read_b128 v[18:21], v102 offset:5040
	s_waitcnt lgkmcnt(0)
	v_fmac_f32_e32 v10, v92, v18
	v_fmac_f32_e32 v10, v93, v19
	v_fmac_f32_e32 v10, v94, v20
	v_fmac_f32_e32 v10, v95, v21
	ds_read_b128 v[18:21], v102 offset:5056
	s_waitcnt lgkmcnt(0)
	v_fmac_f32_e32 v10, v96, v18
	v_fmac_f32_e32 v10, v97, v19
	v_fmac_f32_e32 v10, v98, v20
	v_fmac_f32_e32 v10, v99, v21
	ds_read_b128 v[18:21], v102 offset:5072
	s_waitcnt lgkmcnt(0)
	v_fmac_f32_e32 v10, v100, v18
	v_fmac_f32_e32 v10, v101, v19
	v_fmac_f32_e32 v10, v12, v20
	v_fmac_f32_e32 v10, v13, v21
	ds_read_b128 v[18:21], v102 offset:5088
	s_waitcnt lgkmcnt(0)
	v_pk_mul_f32 v[2:3], v[14:15], v[18:19]
	s_nop 0
	v_add_f32_e32 v2, v10, v2
	v_add_f32_e32 v10, v2, v3
	v_pk_mul_f32 v[2:3], v[6:7], v[20:21]
	ds_read_b128 v[18:21], v102 offset:5104
	v_add_f32_e32 v2, v10, v2
	v_add_f32_e32 v10, v2, v3
	s_waitcnt lgkmcnt(0)
	v_pk_mul_f32 v[2:3], v[16:17], v[18:19]
	s_nop 0
	v_add_f32_e32 v2, v10, v2
	v_add_f32_e32 v10, v2, v3
	v_pk_mul_f32 v[2:3], v[4:5], v[20:21]
	ds_read_b128 v[18:21], v102 offset:5120
	v_add_f32_e32 v2, v10, v2
	v_add_f32_e32 v121, v2, v3
	v_mul_f32_e32 v2, 0x39800000, v121
	v_max3_f32 v0, v0, v1, v2
	s_waitcnt lgkmcnt(0)
	v_fma_f32 v1, v48, v18, 0
	v_fmac_f32_e32 v1, v49, v19
	v_fmac_f32_e32 v1, v50, v20
	v_fmac_f32_e32 v1, v51, v21
	ds_read_b128 v[18:21], v102 offset:5136
	s_waitcnt lgkmcnt(0)
	v_fmac_f32_e32 v1, v52, v18
	v_fmac_f32_e32 v1, v53, v19
	v_fmac_f32_e32 v1, v54, v20
	v_fmac_f32_e32 v1, v55, v21
	ds_read_b128 v[18:21], v102 offset:5152
	s_waitcnt lgkmcnt(0)
	v_fmac_f32_e32 v1, v56, v18
	v_fmac_f32_e32 v1, v57, v19
	v_fmac_f32_e32 v1, v58, v20
	v_fmac_f32_e32 v1, v59, v21
	ds_read_b128 v[18:21], v102 offset:5168
	s_waitcnt lgkmcnt(0)
	v_fmac_f32_e32 v1, v60, v18
	v_fmac_f32_e32 v1, v61, v19
	v_fmac_f32_e32 v1, v62, v20
	v_fmac_f32_e32 v1, v63, v21
	ds_read_b128 v[18:21], v102 offset:5184
	s_waitcnt lgkmcnt(0)
	v_fmac_f32_e32 v1, v64, v18
	v_fmac_f32_e32 v1, v65, v19
	v_fmac_f32_e32 v1, v66, v20
	v_fmac_f32_e32 v1, v67, v21
	ds_read_b128 v[18:21], v102 offset:5200
	s_waitcnt lgkmcnt(0)
	v_fmac_f32_e32 v1, v68, v18
	v_fmac_f32_e32 v1, v69, v19
	v_fmac_f32_e32 v1, v70, v20
	v_fmac_f32_e32 v1, v71, v21
	ds_read_b128 v[18:21], v102 offset:5216
	s_waitcnt lgkmcnt(0)
	v_fmac_f32_e32 v1, v72, v18
	v_fmac_f32_e32 v1, v73, v19
	v_fmac_f32_e32 v1, v74, v20
	v_fmac_f32_e32 v1, v75, v21
	ds_read_b128 v[18:21], v102 offset:5232
	s_waitcnt lgkmcnt(0)
	v_fmac_f32_e32 v1, v76, v18
	v_fmac_f32_e32 v1, v77, v19
	v_fmac_f32_e32 v1, v78, v20
	v_fmac_f32_e32 v1, v79, v21
	ds_read_b128 v[18:21], v102 offset:5248
	s_waitcnt lgkmcnt(0)
	v_fmac_f32_e32 v1, v80, v18
	v_fmac_f32_e32 v1, v81, v19
	v_fmac_f32_e32 v1, v82, v20
	v_fmac_f32_e32 v1, v83, v21
	ds_read_b128 v[18:21], v102 offset:5264
	s_waitcnt lgkmcnt(0)
	v_fmac_f32_e32 v1, v84, v18
	v_fmac_f32_e32 v1, v85, v19
	v_fmac_f32_e32 v1, v86, v20
	v_fmac_f32_e32 v1, v87, v21
	ds_read_b128 v[18:21], v102 offset:5280
	s_waitcnt lgkmcnt(0)
	v_fmac_f32_e32 v1, v88, v18
	v_fmac_f32_e32 v1, v89, v19
	v_fmac_f32_e32 v1, v90, v20
	v_fmac_f32_e32 v1, v91, v21
	ds_read_b128 v[18:21], v102 offset:5296
	s_waitcnt lgkmcnt(0)
	v_fmac_f32_e32 v1, v92, v18
	v_fmac_f32_e32 v1, v93, v19
	v_fmac_f32_e32 v1, v94, v20
	v_fmac_f32_e32 v1, v95, v21
	ds_read_b128 v[18:21], v102 offset:5312
	s_waitcnt lgkmcnt(0)
	v_fmac_f32_e32 v1, v96, v18
	v_fmac_f32_e32 v1, v97, v19
	v_fmac_f32_e32 v1, v98, v20
	v_fmac_f32_e32 v1, v99, v21
	ds_read_b128 v[18:21], v102 offset:5328
	s_waitcnt lgkmcnt(0)
	v_fmac_f32_e32 v1, v100, v18
	v_fmac_f32_e32 v1, v101, v19
	v_fmac_f32_e32 v1, v12, v20
	v_fmac_f32_e32 v1, v13, v21
	ds_read_b128 v[18:21], v102 offset:5344
	s_waitcnt lgkmcnt(0)
	v_pk_mul_f32 v[2:3], v[14:15], v[18:19]
	s_nop 0
	v_add_f32_e32 v1, v1, v2
	v_add_f32_e32 v1, v1, v3
	v_pk_mul_f32 v[2:3], v[6:7], v[20:21]
	ds_read_b128 v[18:21], v102 offset:5360
	v_add_f32_e32 v1, v1, v2
	v_add_f32_e32 v1, v1, v3
	s_waitcnt lgkmcnt(0)
	v_pk_mul_f32 v[2:3], v[16:17], v[18:19]
	s_nop 0
	v_add_f32_e32 v1, v1, v2
	v_add_f32_e32 v1, v1, v3
	v_pk_mul_f32 v[2:3], v[4:5], v[20:21]
	ds_read_b128 v[18:21], v102 offset:5376
	v_add_f32_e32 v1, v1, v2
	v_add_f32_e32 v123, v1, v3
	v_mul_f32_e32 v1, 0x39800000, v123
	s_waitcnt lgkmcnt(0)
	v_fma_f32 v10, v48, v18, 0
	v_fmac_f32_e32 v10, v49, v19
	v_fmac_f32_e32 v10, v50, v20
	v_fmac_f32_e32 v10, v51, v21
	ds_read_b128 v[18:21], v102 offset:5392
	s_waitcnt lgkmcnt(0)
	v_fmac_f32_e32 v10, v52, v18
	v_fmac_f32_e32 v10, v53, v19
	v_fmac_f32_e32 v10, v54, v20
	v_fmac_f32_e32 v10, v55, v21
	ds_read_b128 v[18:21], v102 offset:5408
	s_waitcnt lgkmcnt(0)
	v_fmac_f32_e32 v10, v56, v18
	v_fmac_f32_e32 v10, v57, v19
	v_fmac_f32_e32 v10, v58, v20
	v_fmac_f32_e32 v10, v59, v21
	ds_read_b128 v[18:21], v102 offset:5424
	s_waitcnt lgkmcnt(0)
	v_fmac_f32_e32 v10, v60, v18
	v_fmac_f32_e32 v10, v61, v19
	v_fmac_f32_e32 v10, v62, v20
	v_fmac_f32_e32 v10, v63, v21
	ds_read_b128 v[18:21], v102 offset:5440
	s_waitcnt lgkmcnt(0)
	v_fmac_f32_e32 v10, v64, v18
	v_fmac_f32_e32 v10, v65, v19
	v_fmac_f32_e32 v10, v66, v20
	v_fmac_f32_e32 v10, v67, v21
	ds_read_b128 v[18:21], v102 offset:5456
	s_waitcnt lgkmcnt(0)
	v_fmac_f32_e32 v10, v68, v18
	v_fmac_f32_e32 v10, v69, v19
	v_fmac_f32_e32 v10, v70, v20
	v_fmac_f32_e32 v10, v71, v21
	ds_read_b128 v[18:21], v102 offset:5472
	s_waitcnt lgkmcnt(0)
	v_fmac_f32_e32 v10, v72, v18
	v_fmac_f32_e32 v10, v73, v19
	v_fmac_f32_e32 v10, v74, v20
	v_fmac_f32_e32 v10, v75, v21
	ds_read_b128 v[18:21], v102 offset:5488
	s_waitcnt lgkmcnt(0)
	v_fmac_f32_e32 v10, v76, v18
	v_fmac_f32_e32 v10, v77, v19
	v_fmac_f32_e32 v10, v78, v20
	v_fmac_f32_e32 v10, v79, v21
	ds_read_b128 v[18:21], v102 offset:5504
	s_waitcnt lgkmcnt(0)
	v_fmac_f32_e32 v10, v80, v18
	v_fmac_f32_e32 v10, v81, v19
	v_fmac_f32_e32 v10, v82, v20
	v_fmac_f32_e32 v10, v83, v21
	ds_read_b128 v[18:21], v102 offset:5520
	s_waitcnt lgkmcnt(0)
	v_fmac_f32_e32 v10, v84, v18
	v_fmac_f32_e32 v10, v85, v19
	v_fmac_f32_e32 v10, v86, v20
	v_fmac_f32_e32 v10, v87, v21
	ds_read_b128 v[18:21], v102 offset:5536
	s_waitcnt lgkmcnt(0)
	v_fmac_f32_e32 v10, v88, v18
	v_fmac_f32_e32 v10, v89, v19
	v_fmac_f32_e32 v10, v90, v20
	v_fmac_f32_e32 v10, v91, v21
	ds_read_b128 v[18:21], v102 offset:5552
	s_waitcnt lgkmcnt(0)
	v_fmac_f32_e32 v10, v92, v18
	v_fmac_f32_e32 v10, v93, v19
	v_fmac_f32_e32 v10, v94, v20
	v_fmac_f32_e32 v10, v95, v21
	ds_read_b128 v[18:21], v102 offset:5568
	s_waitcnt lgkmcnt(0)
	v_fmac_f32_e32 v10, v96, v18
	v_fmac_f32_e32 v10, v97, v19
	v_fmac_f32_e32 v10, v98, v20
	v_fmac_f32_e32 v10, v99, v21
	ds_read_b128 v[18:21], v102 offset:5584
	s_waitcnt lgkmcnt(0)
	v_fmac_f32_e32 v10, v100, v18
	v_fmac_f32_e32 v10, v101, v19
	v_fmac_f32_e32 v10, v12, v20
	v_fmac_f32_e32 v10, v13, v21
	ds_read_b128 v[18:21], v102 offset:5600
	s_waitcnt lgkmcnt(0)
	v_pk_mul_f32 v[2:3], v[14:15], v[18:19]
	s_nop 0
	v_add_f32_e32 v2, v10, v2
	v_add_f32_e32 v10, v2, v3
	v_pk_mul_f32 v[2:3], v[6:7], v[20:21]
	ds_read_b128 v[18:21], v102 offset:5616
	v_add_f32_e32 v2, v10, v2
	v_add_f32_e32 v10, v2, v3
	s_waitcnt lgkmcnt(0)
	v_pk_mul_f32 v[2:3], v[16:17], v[18:19]
	s_nop 0
	v_add_f32_e32 v2, v10, v2
	v_add_f32_e32 v10, v2, v3
	v_pk_mul_f32 v[2:3], v[4:5], v[20:21]
	ds_read_b128 v[18:21], v102 offset:5632
	v_add_f32_e32 v2, v10, v2
	v_add_f32_e32 v120, v2, v3
	v_mul_f32_e32 v2, 0x39800000, v120
	v_max3_f32 v0, v0, v1, v2
	s_waitcnt lgkmcnt(0)
	v_fma_f32 v1, v48, v18, 0
	v_fmac_f32_e32 v1, v49, v19
	v_fmac_f32_e32 v1, v50, v20
	v_fmac_f32_e32 v1, v51, v21
	ds_read_b128 v[18:21], v102 offset:5648
	s_waitcnt lgkmcnt(0)
	v_fmac_f32_e32 v1, v52, v18
	v_fmac_f32_e32 v1, v53, v19
	v_fmac_f32_e32 v1, v54, v20
	v_fmac_f32_e32 v1, v55, v21
	ds_read_b128 v[18:21], v102 offset:5664
	s_waitcnt lgkmcnt(0)
	v_fmac_f32_e32 v1, v56, v18
	v_fmac_f32_e32 v1, v57, v19
	v_fmac_f32_e32 v1, v58, v20
	v_fmac_f32_e32 v1, v59, v21
	ds_read_b128 v[18:21], v102 offset:5680
	s_waitcnt lgkmcnt(0)
	v_fmac_f32_e32 v1, v60, v18
	v_fmac_f32_e32 v1, v61, v19
	v_fmac_f32_e32 v1, v62, v20
	v_fmac_f32_e32 v1, v63, v21
	ds_read_b128 v[18:21], v102 offset:5696
	s_waitcnt lgkmcnt(0)
	v_fmac_f32_e32 v1, v64, v18
	v_fmac_f32_e32 v1, v65, v19
	v_fmac_f32_e32 v1, v66, v20
	v_fmac_f32_e32 v1, v67, v21
	ds_read_b128 v[18:21], v102 offset:5712
	s_waitcnt lgkmcnt(0)
	v_fmac_f32_e32 v1, v68, v18
	v_fmac_f32_e32 v1, v69, v19
	v_fmac_f32_e32 v1, v70, v20
	v_fmac_f32_e32 v1, v71, v21
	ds_read_b128 v[18:21], v102 offset:5728
	s_waitcnt lgkmcnt(0)
	v_fmac_f32_e32 v1, v72, v18
	v_fmac_f32_e32 v1, v73, v19
	v_fmac_f32_e32 v1, v74, v20
	v_fmac_f32_e32 v1, v75, v21
	ds_read_b128 v[18:21], v102 offset:5744
	s_waitcnt lgkmcnt(0)
	v_fmac_f32_e32 v1, v76, v18
	v_fmac_f32_e32 v1, v77, v19
	v_fmac_f32_e32 v1, v78, v20
	v_fmac_f32_e32 v1, v79, v21
	ds_read_b128 v[18:21], v102 offset:5760
	s_waitcnt lgkmcnt(0)
	v_fmac_f32_e32 v1, v80, v18
	v_fmac_f32_e32 v1, v81, v19
	v_fmac_f32_e32 v1, v82, v20
	v_fmac_f32_e32 v1, v83, v21
	ds_read_b128 v[18:21], v102 offset:5776
	s_waitcnt lgkmcnt(0)
	v_fmac_f32_e32 v1, v84, v18
	v_fmac_f32_e32 v1, v85, v19
	v_fmac_f32_e32 v1, v86, v20
	v_fmac_f32_e32 v1, v87, v21
	ds_read_b128 v[18:21], v102 offset:5792
	s_waitcnt lgkmcnt(0)
	v_fmac_f32_e32 v1, v88, v18
	v_fmac_f32_e32 v1, v89, v19
	v_fmac_f32_e32 v1, v90, v20
	v_fmac_f32_e32 v1, v91, v21
	ds_read_b128 v[18:21], v102 offset:5808
	s_waitcnt lgkmcnt(0)
	v_fmac_f32_e32 v1, v92, v18
	v_fmac_f32_e32 v1, v93, v19
	v_fmac_f32_e32 v1, v94, v20
	v_fmac_f32_e32 v1, v95, v21
	ds_read_b128 v[18:21], v102 offset:5824
	s_waitcnt lgkmcnt(0)
	v_fmac_f32_e32 v1, v96, v18
	v_fmac_f32_e32 v1, v97, v19
	v_fmac_f32_e32 v1, v98, v20
	v_fmac_f32_e32 v1, v99, v21
	ds_read_b128 v[18:21], v102 offset:5840
	s_waitcnt lgkmcnt(0)
	v_fmac_f32_e32 v1, v100, v18
	v_fmac_f32_e32 v1, v101, v19
	v_fmac_f32_e32 v1, v12, v20
	v_fmac_f32_e32 v1, v13, v21
	ds_read_b128 v[18:21], v102 offset:5856
	s_waitcnt lgkmcnt(0)
	v_pk_mul_f32 v[2:3], v[14:15], v[18:19]
	s_nop 0
	v_add_f32_e32 v1, v1, v2
	v_add_f32_e32 v1, v1, v3
	v_pk_mul_f32 v[2:3], v[6:7], v[20:21]
	ds_read_b128 v[18:21], v102 offset:5872
	v_add_f32_e32 v1, v1, v2
	v_add_f32_e32 v1, v1, v3
	s_waitcnt lgkmcnt(0)
	v_pk_mul_f32 v[2:3], v[16:17], v[18:19]
	s_nop 0
	v_add_f32_e32 v1, v1, v2
	v_add_f32_e32 v1, v1, v3
	v_pk_mul_f32 v[2:3], v[4:5], v[20:21]
	ds_read_b128 v[18:21], v102 offset:5888
	v_add_f32_e32 v1, v1, v2
	v_add_f32_e32 v122, v1, v3
	v_mul_f32_e32 v1, 0x39800000, v122
	s_waitcnt lgkmcnt(0)
	v_fma_f32 v10, v48, v18, 0
	v_fmac_f32_e32 v10, v49, v19
	v_fmac_f32_e32 v10, v50, v20
	v_fmac_f32_e32 v10, v51, v21
	ds_read_b128 v[18:21], v102 offset:5904
	s_waitcnt lgkmcnt(0)
	v_fmac_f32_e32 v10, v52, v18
	v_fmac_f32_e32 v10, v53, v19
	v_fmac_f32_e32 v10, v54, v20
	v_fmac_f32_e32 v10, v55, v21
	ds_read_b128 v[18:21], v102 offset:5920
	s_waitcnt lgkmcnt(0)
	v_fmac_f32_e32 v10, v56, v18
	v_fmac_f32_e32 v10, v57, v19
	v_fmac_f32_e32 v10, v58, v20
	v_fmac_f32_e32 v10, v59, v21
	ds_read_b128 v[18:21], v102 offset:5936
	s_waitcnt lgkmcnt(0)
	v_fmac_f32_e32 v10, v60, v18
	v_fmac_f32_e32 v10, v61, v19
	v_fmac_f32_e32 v10, v62, v20
	v_fmac_f32_e32 v10, v63, v21
	ds_read_b128 v[18:21], v102 offset:5952
	s_waitcnt lgkmcnt(0)
	v_fmac_f32_e32 v10, v64, v18
	v_fmac_f32_e32 v10, v65, v19
	v_fmac_f32_e32 v10, v66, v20
	v_fmac_f32_e32 v10, v67, v21
	ds_read_b128 v[18:21], v102 offset:5968
	s_waitcnt lgkmcnt(0)
	v_fmac_f32_e32 v10, v68, v18
	v_fmac_f32_e32 v10, v69, v19
	v_fmac_f32_e32 v10, v70, v20
	v_fmac_f32_e32 v10, v71, v21
	ds_read_b128 v[18:21], v102 offset:5984
	s_waitcnt lgkmcnt(0)
	v_fmac_f32_e32 v10, v72, v18
	v_fmac_f32_e32 v10, v73, v19
	v_fmac_f32_e32 v10, v74, v20
	v_fmac_f32_e32 v10, v75, v21
	ds_read_b128 v[18:21], v102 offset:6000
	s_waitcnt lgkmcnt(0)
	v_fmac_f32_e32 v10, v76, v18
	v_fmac_f32_e32 v10, v77, v19
	v_fmac_f32_e32 v10, v78, v20
	v_fmac_f32_e32 v10, v79, v21
	ds_read_b128 v[18:21], v102 offset:6016
	s_waitcnt lgkmcnt(0)
	v_fmac_f32_e32 v10, v80, v18
	v_fmac_f32_e32 v10, v81, v19
	v_fmac_f32_e32 v10, v82, v20
	v_fmac_f32_e32 v10, v83, v21
	ds_read_b128 v[18:21], v102 offset:6032
	s_waitcnt lgkmcnt(0)
	v_fmac_f32_e32 v10, v84, v18
	v_fmac_f32_e32 v10, v85, v19
	v_fmac_f32_e32 v10, v86, v20
	v_fmac_f32_e32 v10, v87, v21
	ds_read_b128 v[18:21], v102 offset:6048
	s_waitcnt lgkmcnt(0)
	v_fmac_f32_e32 v10, v88, v18
	v_fmac_f32_e32 v10, v89, v19
	v_fmac_f32_e32 v10, v90, v20
	v_fmac_f32_e32 v10, v91, v21
	ds_read_b128 v[18:21], v102 offset:6064
	s_waitcnt lgkmcnt(0)
	v_fmac_f32_e32 v10, v92, v18
	v_fmac_f32_e32 v10, v93, v19
	v_fmac_f32_e32 v10, v94, v20
	v_fmac_f32_e32 v10, v95, v21
	ds_read_b128 v[18:21], v102 offset:6080
	s_waitcnt lgkmcnt(0)
	v_fmac_f32_e32 v10, v96, v18
	v_fmac_f32_e32 v10, v97, v19
	v_fmac_f32_e32 v10, v98, v20
	v_fmac_f32_e32 v10, v99, v21
	ds_read_b128 v[18:21], v102 offset:6096
	s_waitcnt lgkmcnt(0)
	v_fmac_f32_e32 v10, v100, v18
	v_fmac_f32_e32 v10, v101, v19
	v_fmac_f32_e32 v10, v12, v20
	v_fmac_f32_e32 v10, v13, v21
	ds_read_b128 v[18:21], v102 offset:6112
	s_waitcnt lgkmcnt(0)
	v_pk_mul_f32 v[2:3], v[14:15], v[18:19]
	s_nop 0
	v_add_f32_e32 v2, v10, v2
	v_add_f32_e32 v10, v2, v3
	v_pk_mul_f32 v[2:3], v[6:7], v[20:21]
	ds_read_b128 v[18:21], v102 offset:6128
	v_add_f32_e32 v2, v10, v2
	v_add_f32_e32 v10, v2, v3
	s_waitcnt lgkmcnt(0)
	v_pk_mul_f32 v[2:3], v[16:17], v[18:19]
	s_nop 0
	v_add_f32_e32 v2, v10, v2
	v_add_f32_e32 v10, v2, v3
	v_pk_mul_f32 v[2:3], v[4:5], v[20:21]
	ds_read_b128 v[18:21], v102 offset:6144
	v_add_f32_e32 v2, v10, v2
	v_add_f32_e32 v104, v2, v3
	v_mul_f32_e32 v2, 0x39800000, v104
	v_max3_f32 v0, v0, v1, v2
	s_waitcnt lgkmcnt(0)
	v_fma_f32 v1, v48, v18, 0
	v_fmac_f32_e32 v1, v49, v19
	v_fmac_f32_e32 v1, v50, v20
	v_fmac_f32_e32 v1, v51, v21
	ds_read_b128 v[18:21], v102 offset:6160
	s_waitcnt lgkmcnt(0)
	v_fmac_f32_e32 v1, v52, v18
	v_fmac_f32_e32 v1, v53, v19
	v_fmac_f32_e32 v1, v54, v20
	v_fmac_f32_e32 v1, v55, v21
	ds_read_b128 v[18:21], v102 offset:6176
	s_waitcnt lgkmcnt(0)
	v_fmac_f32_e32 v1, v56, v18
	v_fmac_f32_e32 v1, v57, v19
	v_fmac_f32_e32 v1, v58, v20
	v_fmac_f32_e32 v1, v59, v21
	ds_read_b128 v[18:21], v102 offset:6192
	s_waitcnt lgkmcnt(0)
	v_fmac_f32_e32 v1, v60, v18
	v_fmac_f32_e32 v1, v61, v19
	v_fmac_f32_e32 v1, v62, v20
	v_fmac_f32_e32 v1, v63, v21
	ds_read_b128 v[18:21], v102 offset:6208
	s_waitcnt lgkmcnt(0)
	v_fmac_f32_e32 v1, v64, v18
	v_fmac_f32_e32 v1, v65, v19
	v_fmac_f32_e32 v1, v66, v20
	v_fmac_f32_e32 v1, v67, v21
	ds_read_b128 v[18:21], v102 offset:6224
	s_waitcnt lgkmcnt(0)
	v_fmac_f32_e32 v1, v68, v18
	v_fmac_f32_e32 v1, v69, v19
	v_fmac_f32_e32 v1, v70, v20
	v_fmac_f32_e32 v1, v71, v21
	ds_read_b128 v[18:21], v102 offset:6240
	s_waitcnt lgkmcnt(0)
	v_fmac_f32_e32 v1, v72, v18
	v_fmac_f32_e32 v1, v73, v19
	v_fmac_f32_e32 v1, v74, v20
	v_fmac_f32_e32 v1, v75, v21
	ds_read_b128 v[18:21], v102 offset:6256
	s_waitcnt lgkmcnt(0)
	v_fmac_f32_e32 v1, v76, v18
	v_fmac_f32_e32 v1, v77, v19
	v_fmac_f32_e32 v1, v78, v20
	v_fmac_f32_e32 v1, v79, v21
	ds_read_b128 v[18:21], v102 offset:6272
	s_waitcnt lgkmcnt(0)
	v_fmac_f32_e32 v1, v80, v18
	v_fmac_f32_e32 v1, v81, v19
	v_fmac_f32_e32 v1, v82, v20
	v_fmac_f32_e32 v1, v83, v21
	ds_read_b128 v[18:21], v102 offset:6288
	s_waitcnt lgkmcnt(0)
	v_fmac_f32_e32 v1, v84, v18
	v_fmac_f32_e32 v1, v85, v19
	v_fmac_f32_e32 v1, v86, v20
	v_fmac_f32_e32 v1, v87, v21
	ds_read_b128 v[18:21], v102 offset:6304
	s_waitcnt lgkmcnt(0)
	v_fmac_f32_e32 v1, v88, v18
	v_fmac_f32_e32 v1, v89, v19
	v_fmac_f32_e32 v1, v90, v20
	v_fmac_f32_e32 v1, v91, v21
	ds_read_b128 v[18:21], v102 offset:6320
	s_waitcnt lgkmcnt(0)
	v_fmac_f32_e32 v1, v92, v18
	v_fmac_f32_e32 v1, v93, v19
	v_fmac_f32_e32 v1, v94, v20
	v_fmac_f32_e32 v1, v95, v21
	ds_read_b128 v[18:21], v102 offset:6336
	s_waitcnt lgkmcnt(0)
	v_fmac_f32_e32 v1, v96, v18
	v_fmac_f32_e32 v1, v97, v19
	v_fmac_f32_e32 v1, v98, v20
	v_fmac_f32_e32 v1, v99, v21
	ds_read_b128 v[18:21], v102 offset:6352
	s_waitcnt lgkmcnt(0)
	v_fmac_f32_e32 v1, v100, v18
	v_fmac_f32_e32 v1, v101, v19
	v_fmac_f32_e32 v1, v12, v20
	v_fmac_f32_e32 v1, v13, v21
	ds_read_b128 v[18:21], v102 offset:6368
	s_waitcnt lgkmcnt(0)
	v_pk_mul_f32 v[2:3], v[14:15], v[18:19]
	s_nop 0
	v_add_f32_e32 v1, v1, v2
	v_add_f32_e32 v1, v1, v3
	v_pk_mul_f32 v[2:3], v[6:7], v[20:21]
	ds_read_b128 v[18:21], v102 offset:6384
	v_add_f32_e32 v1, v1, v2
	v_add_f32_e32 v1, v1, v3
	s_waitcnt lgkmcnt(0)
	v_pk_mul_f32 v[2:3], v[16:17], v[18:19]
	s_nop 0
	v_add_f32_e32 v1, v1, v2
	v_add_f32_e32 v1, v1, v3
	v_pk_mul_f32 v[2:3], v[4:5], v[20:21]
	ds_read_b128 v[18:21], v102 offset:6400
	v_add_f32_e32 v1, v1, v2
	v_add_f32_e32 v105, v1, v3
	v_mul_f32_e32 v1, 0x39800000, v105
	s_waitcnt lgkmcnt(0)
	v_fma_f32 v10, v48, v18, 0
	v_fmac_f32_e32 v10, v49, v19
	v_fmac_f32_e32 v10, v50, v20
	v_fmac_f32_e32 v10, v51, v21
	ds_read_b128 v[18:21], v102 offset:6416
	s_waitcnt lgkmcnt(0)
	v_fmac_f32_e32 v10, v52, v18
	v_fmac_f32_e32 v10, v53, v19
	v_fmac_f32_e32 v10, v54, v20
	v_fmac_f32_e32 v10, v55, v21
	ds_read_b128 v[18:21], v102 offset:6432
	s_waitcnt lgkmcnt(0)
	v_fmac_f32_e32 v10, v56, v18
	v_fmac_f32_e32 v10, v57, v19
	v_fmac_f32_e32 v10, v58, v20
	v_fmac_f32_e32 v10, v59, v21
	ds_read_b128 v[18:21], v102 offset:6448
	s_waitcnt lgkmcnt(0)
	v_fmac_f32_e32 v10, v60, v18
	v_fmac_f32_e32 v10, v61, v19
	v_fmac_f32_e32 v10, v62, v20
	v_fmac_f32_e32 v10, v63, v21
	ds_read_b128 v[18:21], v102 offset:6464
	s_waitcnt lgkmcnt(0)
	v_fmac_f32_e32 v10, v64, v18
	v_fmac_f32_e32 v10, v65, v19
	v_fmac_f32_e32 v10, v66, v20
	v_fmac_f32_e32 v10, v67, v21
	ds_read_b128 v[18:21], v102 offset:6480
	s_waitcnt lgkmcnt(0)
	v_fmac_f32_e32 v10, v68, v18
	v_fmac_f32_e32 v10, v69, v19
	v_fmac_f32_e32 v10, v70, v20
	v_fmac_f32_e32 v10, v71, v21
	ds_read_b128 v[18:21], v102 offset:6496
	s_waitcnt lgkmcnt(0)
	v_fmac_f32_e32 v10, v72, v18
	v_fmac_f32_e32 v10, v73, v19
	v_fmac_f32_e32 v10, v74, v20
	v_fmac_f32_e32 v10, v75, v21
	ds_read_b128 v[18:21], v102 offset:6512
	s_waitcnt lgkmcnt(0)
	v_fmac_f32_e32 v10, v76, v18
	v_fmac_f32_e32 v10, v77, v19
	v_fmac_f32_e32 v10, v78, v20
	v_fmac_f32_e32 v10, v79, v21
	ds_read_b128 v[18:21], v102 offset:6528
	s_waitcnt lgkmcnt(0)
	v_fmac_f32_e32 v10, v80, v18
	v_fmac_f32_e32 v10, v81, v19
	v_fmac_f32_e32 v10, v82, v20
	v_fmac_f32_e32 v10, v83, v21
	ds_read_b128 v[18:21], v102 offset:6544
	s_waitcnt lgkmcnt(0)
	v_fmac_f32_e32 v10, v84, v18
	v_fmac_f32_e32 v10, v85, v19
	v_fmac_f32_e32 v10, v86, v20
	v_fmac_f32_e32 v10, v87, v21
	ds_read_b128 v[18:21], v102 offset:6560
	s_waitcnt lgkmcnt(0)
	v_fmac_f32_e32 v10, v88, v18
	v_fmac_f32_e32 v10, v89, v19
	v_fmac_f32_e32 v10, v90, v20
	v_fmac_f32_e32 v10, v91, v21
	ds_read_b128 v[18:21], v102 offset:6576
	s_waitcnt lgkmcnt(0)
	v_fmac_f32_e32 v10, v92, v18
	v_fmac_f32_e32 v10, v93, v19
	v_fmac_f32_e32 v10, v94, v20
	v_fmac_f32_e32 v10, v95, v21
	ds_read_b128 v[18:21], v102 offset:6592
	s_waitcnt lgkmcnt(0)
	v_fmac_f32_e32 v10, v96, v18
	v_fmac_f32_e32 v10, v97, v19
	v_fmac_f32_e32 v10, v98, v20
	v_fmac_f32_e32 v10, v99, v21
	ds_read_b128 v[18:21], v102 offset:6608
	s_waitcnt lgkmcnt(0)
	v_fmac_f32_e32 v10, v100, v18
	v_fmac_f32_e32 v10, v101, v19
	v_fmac_f32_e32 v10, v12, v20
	v_fmac_f32_e32 v10, v13, v21
	ds_read_b128 v[18:21], v102 offset:6624
	s_waitcnt lgkmcnt(0)
	v_pk_mul_f32 v[2:3], v[14:15], v[18:19]
	s_nop 0
	v_add_f32_e32 v2, v10, v2
	v_add_f32_e32 v10, v2, v3
	v_pk_mul_f32 v[2:3], v[6:7], v[20:21]
	ds_read_b128 v[18:21], v102 offset:6640
	v_add_f32_e32 v2, v10, v2
	v_add_f32_e32 v10, v2, v3
	s_waitcnt lgkmcnt(0)
	v_pk_mul_f32 v[2:3], v[16:17], v[18:19]
	s_nop 0
	v_add_f32_e32 v2, v10, v2
	v_add_f32_e32 v10, v2, v3
	v_pk_mul_f32 v[2:3], v[4:5], v[20:21]
	ds_read_b128 v[18:21], v102 offset:6656
	v_add_f32_e32 v2, v10, v2
	v_add_f32_e32 v106, v2, v3
	v_mul_f32_e32 v2, 0x39800000, v106
	v_max3_f32 v0, v0, v1, v2
	s_waitcnt lgkmcnt(0)
	v_fma_f32 v1, v48, v18, 0
	v_fmac_f32_e32 v1, v49, v19
	v_fmac_f32_e32 v1, v50, v20
	v_fmac_f32_e32 v1, v51, v21
	ds_read_b128 v[18:21], v102 offset:6672
	s_waitcnt lgkmcnt(0)
	v_fmac_f32_e32 v1, v52, v18
	v_fmac_f32_e32 v1, v53, v19
	v_fmac_f32_e32 v1, v54, v20
	v_fmac_f32_e32 v1, v55, v21
	ds_read_b128 v[18:21], v102 offset:6688
	s_waitcnt lgkmcnt(0)
	v_fmac_f32_e32 v1, v56, v18
	v_fmac_f32_e32 v1, v57, v19
	v_fmac_f32_e32 v1, v58, v20
	v_fmac_f32_e32 v1, v59, v21
	ds_read_b128 v[18:21], v102 offset:6704
	s_waitcnt lgkmcnt(0)
	v_fmac_f32_e32 v1, v60, v18
	v_fmac_f32_e32 v1, v61, v19
	v_fmac_f32_e32 v1, v62, v20
	v_fmac_f32_e32 v1, v63, v21
	ds_read_b128 v[18:21], v102 offset:6720
	s_waitcnt lgkmcnt(0)
	v_fmac_f32_e32 v1, v64, v18
	v_fmac_f32_e32 v1, v65, v19
	v_fmac_f32_e32 v1, v66, v20
	v_fmac_f32_e32 v1, v67, v21
	ds_read_b128 v[18:21], v102 offset:6736
	s_waitcnt lgkmcnt(0)
	v_fmac_f32_e32 v1, v68, v18
	v_fmac_f32_e32 v1, v69, v19
	v_fmac_f32_e32 v1, v70, v20
	v_fmac_f32_e32 v1, v71, v21
	ds_read_b128 v[18:21], v102 offset:6752
	s_waitcnt lgkmcnt(0)
	v_fmac_f32_e32 v1, v72, v18
	v_fmac_f32_e32 v1, v73, v19
	v_fmac_f32_e32 v1, v74, v20
	v_fmac_f32_e32 v1, v75, v21
	ds_read_b128 v[18:21], v102 offset:6768
	s_waitcnt lgkmcnt(0)
	v_fmac_f32_e32 v1, v76, v18
	v_fmac_f32_e32 v1, v77, v19
	v_fmac_f32_e32 v1, v78, v20
	v_fmac_f32_e32 v1, v79, v21
	ds_read_b128 v[18:21], v102 offset:6784
	s_waitcnt lgkmcnt(0)
	v_fmac_f32_e32 v1, v80, v18
	v_fmac_f32_e32 v1, v81, v19
	v_fmac_f32_e32 v1, v82, v20
	v_fmac_f32_e32 v1, v83, v21
	ds_read_b128 v[18:21], v102 offset:6800
	s_waitcnt lgkmcnt(0)
	v_fmac_f32_e32 v1, v84, v18
	v_fmac_f32_e32 v1, v85, v19
	v_fmac_f32_e32 v1, v86, v20
	v_fmac_f32_e32 v1, v87, v21
	ds_read_b128 v[18:21], v102 offset:6816
	s_waitcnt lgkmcnt(0)
	v_fmac_f32_e32 v1, v88, v18
	v_fmac_f32_e32 v1, v89, v19
	v_fmac_f32_e32 v1, v90, v20
	v_fmac_f32_e32 v1, v91, v21
	ds_read_b128 v[18:21], v102 offset:6832
	s_waitcnt lgkmcnt(0)
	v_fmac_f32_e32 v1, v92, v18
	v_fmac_f32_e32 v1, v93, v19
	v_fmac_f32_e32 v1, v94, v20
	v_fmac_f32_e32 v1, v95, v21
	ds_read_b128 v[18:21], v102 offset:6848
	s_waitcnt lgkmcnt(0)
	v_fmac_f32_e32 v1, v96, v18
	v_fmac_f32_e32 v1, v97, v19
	v_fmac_f32_e32 v1, v98, v20
	v_fmac_f32_e32 v1, v99, v21
	ds_read_b128 v[18:21], v102 offset:6864
	s_waitcnt lgkmcnt(0)
	v_fmac_f32_e32 v1, v100, v18
	v_fmac_f32_e32 v1, v101, v19
	v_fmac_f32_e32 v1, v12, v20
	v_fmac_f32_e32 v1, v13, v21
	ds_read_b128 v[18:21], v102 offset:6880
	s_waitcnt lgkmcnt(0)
	v_pk_mul_f32 v[2:3], v[14:15], v[18:19]
	s_nop 0
	v_add_f32_e32 v1, v1, v2
	v_add_f32_e32 v1, v1, v3
	v_pk_mul_f32 v[2:3], v[6:7], v[20:21]
	ds_read_b128 v[18:21], v102 offset:6896
	v_add_f32_e32 v1, v1, v2
	v_add_f32_e32 v1, v1, v3
	s_waitcnt lgkmcnt(0)
	v_pk_mul_f32 v[2:3], v[16:17], v[18:19]
	s_nop 0
	v_add_f32_e32 v1, v1, v2
	v_add_f32_e32 v1, v1, v3
	v_pk_mul_f32 v[2:3], v[4:5], v[20:21]
	ds_read_b128 v[18:21], v102 offset:6912
	v_add_f32_e32 v1, v1, v2
	v_add_f32_e32 v107, v1, v3
	v_mul_f32_e32 v1, 0x39800000, v107
	s_waitcnt lgkmcnt(0)
	v_fma_f32 v10, v48, v18, 0
	v_fmac_f32_e32 v10, v49, v19
	v_fmac_f32_e32 v10, v50, v20
	v_fmac_f32_e32 v10, v51, v21
	ds_read_b128 v[18:21], v102 offset:6928
	s_waitcnt lgkmcnt(0)
	v_fmac_f32_e32 v10, v52, v18
	v_fmac_f32_e32 v10, v53, v19
	v_fmac_f32_e32 v10, v54, v20
	v_fmac_f32_e32 v10, v55, v21
	ds_read_b128 v[18:21], v102 offset:6944
	s_waitcnt lgkmcnt(0)
	v_fmac_f32_e32 v10, v56, v18
	v_fmac_f32_e32 v10, v57, v19
	v_fmac_f32_e32 v10, v58, v20
	v_fmac_f32_e32 v10, v59, v21
	ds_read_b128 v[18:21], v102 offset:6960
	s_waitcnt lgkmcnt(0)
	v_fmac_f32_e32 v10, v60, v18
	v_fmac_f32_e32 v10, v61, v19
	v_fmac_f32_e32 v10, v62, v20
	v_fmac_f32_e32 v10, v63, v21
	ds_read_b128 v[18:21], v102 offset:6976
	s_waitcnt lgkmcnt(0)
	v_fmac_f32_e32 v10, v64, v18
	v_fmac_f32_e32 v10, v65, v19
	v_fmac_f32_e32 v10, v66, v20
	v_fmac_f32_e32 v10, v67, v21
	ds_read_b128 v[18:21], v102 offset:6992
	s_waitcnt lgkmcnt(0)
	v_fmac_f32_e32 v10, v68, v18
	v_fmac_f32_e32 v10, v69, v19
	v_fmac_f32_e32 v10, v70, v20
	v_fmac_f32_e32 v10, v71, v21
	ds_read_b128 v[18:21], v102 offset:7008
	s_waitcnt lgkmcnt(0)
	v_fmac_f32_e32 v10, v72, v18
	v_fmac_f32_e32 v10, v73, v19
	v_fmac_f32_e32 v10, v74, v20
	v_fmac_f32_e32 v10, v75, v21
	ds_read_b128 v[18:21], v102 offset:7024
	s_waitcnt lgkmcnt(0)
	v_fmac_f32_e32 v10, v76, v18
	v_fmac_f32_e32 v10, v77, v19
	v_fmac_f32_e32 v10, v78, v20
	v_fmac_f32_e32 v10, v79, v21
	ds_read_b128 v[18:21], v102 offset:7040
	s_waitcnt lgkmcnt(0)
	v_fmac_f32_e32 v10, v80, v18
	v_fmac_f32_e32 v10, v81, v19
	v_fmac_f32_e32 v10, v82, v20
	v_fmac_f32_e32 v10, v83, v21
	ds_read_b128 v[18:21], v102 offset:7056
	s_waitcnt lgkmcnt(0)
	v_fmac_f32_e32 v10, v84, v18
	v_fmac_f32_e32 v10, v85, v19
	v_fmac_f32_e32 v10, v86, v20
	v_fmac_f32_e32 v10, v87, v21
	ds_read_b128 v[18:21], v102 offset:7072
	s_waitcnt lgkmcnt(0)
	v_fmac_f32_e32 v10, v88, v18
	v_fmac_f32_e32 v10, v89, v19
	v_fmac_f32_e32 v10, v90, v20
	v_fmac_f32_e32 v10, v91, v21
	ds_read_b128 v[18:21], v102 offset:7088
	s_waitcnt lgkmcnt(0)
	v_fmac_f32_e32 v10, v92, v18
	v_fmac_f32_e32 v10, v93, v19
	v_fmac_f32_e32 v10, v94, v20
	v_fmac_f32_e32 v10, v95, v21
	ds_read_b128 v[18:21], v102 offset:7104
	s_waitcnt lgkmcnt(0)
	v_fmac_f32_e32 v10, v96, v18
	v_fmac_f32_e32 v10, v97, v19
	v_fmac_f32_e32 v10, v98, v20
	v_fmac_f32_e32 v10, v99, v21
	ds_read_b128 v[18:21], v102 offset:7120
	s_waitcnt lgkmcnt(0)
	v_fmac_f32_e32 v10, v100, v18
	v_fmac_f32_e32 v10, v101, v19
	v_fmac_f32_e32 v10, v12, v20
	v_fmac_f32_e32 v10, v13, v21
	ds_read_b128 v[18:21], v102 offset:7136
	s_waitcnt lgkmcnt(0)
	v_pk_mul_f32 v[2:3], v[14:15], v[18:19]
	s_nop 0
	v_add_f32_e32 v2, v10, v2
	v_add_f32_e32 v10, v2, v3
	v_pk_mul_f32 v[2:3], v[6:7], v[20:21]
	ds_read_b128 v[18:21], v102 offset:7152
	v_add_f32_e32 v2, v10, v2
	v_add_f32_e32 v10, v2, v3
	s_waitcnt lgkmcnt(0)
	v_pk_mul_f32 v[2:3], v[16:17], v[18:19]
	s_nop 0
	v_add_f32_e32 v2, v10, v2
	v_add_f32_e32 v10, v2, v3
	v_pk_mul_f32 v[2:3], v[4:5], v[20:21]
	ds_read_b128 v[18:21], v102 offset:7168
	v_add_f32_e32 v2, v10, v2
	v_add_f32_e32 v108, v2, v3
	v_mul_f32_e32 v2, 0x39800000, v108
	v_max3_f32 v0, v0, v1, v2
	s_waitcnt lgkmcnt(0)
	v_fma_f32 v1, v48, v18, 0
	v_fmac_f32_e32 v1, v49, v19
	v_fmac_f32_e32 v1, v50, v20
	v_fmac_f32_e32 v1, v51, v21
	ds_read_b128 v[18:21], v102 offset:7184
	s_waitcnt lgkmcnt(0)
	v_fmac_f32_e32 v1, v52, v18
	v_fmac_f32_e32 v1, v53, v19
	v_fmac_f32_e32 v1, v54, v20
	v_fmac_f32_e32 v1, v55, v21
	ds_read_b128 v[18:21], v102 offset:7200
	s_waitcnt lgkmcnt(0)
	v_fmac_f32_e32 v1, v56, v18
	v_fmac_f32_e32 v1, v57, v19
	v_fmac_f32_e32 v1, v58, v20
	v_fmac_f32_e32 v1, v59, v21
	ds_read_b128 v[18:21], v102 offset:7216
	s_waitcnt lgkmcnt(0)
	v_fmac_f32_e32 v1, v60, v18
	v_fmac_f32_e32 v1, v61, v19
	v_fmac_f32_e32 v1, v62, v20
	v_fmac_f32_e32 v1, v63, v21
	ds_read_b128 v[18:21], v102 offset:7232
	s_waitcnt lgkmcnt(0)
	v_fmac_f32_e32 v1, v64, v18
	v_fmac_f32_e32 v1, v65, v19
	v_fmac_f32_e32 v1, v66, v20
	v_fmac_f32_e32 v1, v67, v21
	ds_read_b128 v[18:21], v102 offset:7248
	s_waitcnt lgkmcnt(0)
	v_fmac_f32_e32 v1, v68, v18
	v_fmac_f32_e32 v1, v69, v19
	v_fmac_f32_e32 v1, v70, v20
	v_fmac_f32_e32 v1, v71, v21
	ds_read_b128 v[18:21], v102 offset:7264
	s_waitcnt lgkmcnt(0)
	v_fmac_f32_e32 v1, v72, v18
	v_fmac_f32_e32 v1, v73, v19
	v_fmac_f32_e32 v1, v74, v20
	v_fmac_f32_e32 v1, v75, v21
	ds_read_b128 v[18:21], v102 offset:7280
	s_waitcnt lgkmcnt(0)
	v_fmac_f32_e32 v1, v76, v18
	v_fmac_f32_e32 v1, v77, v19
	v_fmac_f32_e32 v1, v78, v20
	v_fmac_f32_e32 v1, v79, v21
	ds_read_b128 v[18:21], v102 offset:7296
	s_waitcnt lgkmcnt(0)
	v_fmac_f32_e32 v1, v80, v18
	v_fmac_f32_e32 v1, v81, v19
	v_fmac_f32_e32 v1, v82, v20
	v_fmac_f32_e32 v1, v83, v21
	ds_read_b128 v[18:21], v102 offset:7312
	s_waitcnt lgkmcnt(0)
	v_fmac_f32_e32 v1, v84, v18
	v_fmac_f32_e32 v1, v85, v19
	v_fmac_f32_e32 v1, v86, v20
	v_fmac_f32_e32 v1, v87, v21
	ds_read_b128 v[18:21], v102 offset:7328
	s_waitcnt lgkmcnt(0)
	v_fmac_f32_e32 v1, v88, v18
	v_fmac_f32_e32 v1, v89, v19
	v_fmac_f32_e32 v1, v90, v20
	v_fmac_f32_e32 v1, v91, v21
	ds_read_b128 v[18:21], v102 offset:7344
	s_waitcnt lgkmcnt(0)
	v_fmac_f32_e32 v1, v92, v18
	v_fmac_f32_e32 v1, v93, v19
	v_fmac_f32_e32 v1, v94, v20
	v_fmac_f32_e32 v1, v95, v21
	ds_read_b128 v[18:21], v102 offset:7360
	s_waitcnt lgkmcnt(0)
	v_fmac_f32_e32 v1, v96, v18
	v_fmac_f32_e32 v1, v97, v19
	v_fmac_f32_e32 v1, v98, v20
	v_fmac_f32_e32 v1, v99, v21
	ds_read_b128 v[18:21], v102 offset:7376
	s_waitcnt lgkmcnt(0)
	v_fmac_f32_e32 v1, v100, v18
	v_fmac_f32_e32 v1, v101, v19
	v_fmac_f32_e32 v1, v12, v20
	v_fmac_f32_e32 v1, v13, v21
	ds_read_b128 v[18:21], v102 offset:7392
	s_waitcnt lgkmcnt(0)
	v_pk_mul_f32 v[2:3], v[14:15], v[18:19]
	s_nop 0
	v_add_f32_e32 v1, v1, v2
	v_add_f32_e32 v1, v1, v3
	v_pk_mul_f32 v[2:3], v[6:7], v[20:21]
	ds_read_b128 v[18:21], v102 offset:7408
	v_add_f32_e32 v1, v1, v2
	v_add_f32_e32 v1, v1, v3
	s_waitcnt lgkmcnt(0)
	v_pk_mul_f32 v[2:3], v[16:17], v[18:19]
	s_nop 0
	v_add_f32_e32 v1, v1, v2
	v_add_f32_e32 v1, v1, v3
	v_pk_mul_f32 v[2:3], v[4:5], v[20:21]
	ds_read_b128 v[18:21], v102 offset:7424
	v_add_f32_e32 v1, v1, v2
	v_add_f32_e32 v110, v1, v3
	v_mul_f32_e32 v1, 0x39800000, v110
	s_waitcnt lgkmcnt(0)
	v_fma_f32 v10, v48, v18, 0
	v_fmac_f32_e32 v10, v49, v19
	v_fmac_f32_e32 v10, v50, v20
	v_fmac_f32_e32 v10, v51, v21
	ds_read_b128 v[18:21], v102 offset:7440
	s_waitcnt lgkmcnt(0)
	v_fmac_f32_e32 v10, v52, v18
	v_fmac_f32_e32 v10, v53, v19
	v_fmac_f32_e32 v10, v54, v20
	v_fmac_f32_e32 v10, v55, v21
	ds_read_b128 v[18:21], v102 offset:7456
	s_waitcnt lgkmcnt(0)
	v_fmac_f32_e32 v10, v56, v18
	v_fmac_f32_e32 v10, v57, v19
	v_fmac_f32_e32 v10, v58, v20
	v_fmac_f32_e32 v10, v59, v21
	ds_read_b128 v[18:21], v102 offset:7472
	s_waitcnt lgkmcnt(0)
	v_fmac_f32_e32 v10, v60, v18
	v_fmac_f32_e32 v10, v61, v19
	v_fmac_f32_e32 v10, v62, v20
	v_fmac_f32_e32 v10, v63, v21
	ds_read_b128 v[18:21], v102 offset:7488
	s_waitcnt lgkmcnt(0)
	v_fmac_f32_e32 v10, v64, v18
	v_fmac_f32_e32 v10, v65, v19
	v_fmac_f32_e32 v10, v66, v20
	v_fmac_f32_e32 v10, v67, v21
	ds_read_b128 v[18:21], v102 offset:7504
	s_waitcnt lgkmcnt(0)
	v_fmac_f32_e32 v10, v68, v18
	v_fmac_f32_e32 v10, v69, v19
	v_fmac_f32_e32 v10, v70, v20
	v_fmac_f32_e32 v10, v71, v21
	ds_read_b128 v[18:21], v102 offset:7520
	s_waitcnt lgkmcnt(0)
	v_fmac_f32_e32 v10, v72, v18
	v_fmac_f32_e32 v10, v73, v19
	v_fmac_f32_e32 v10, v74, v20
	v_fmac_f32_e32 v10, v75, v21
	ds_read_b128 v[18:21], v102 offset:7536
	s_waitcnt lgkmcnt(0)
	v_fmac_f32_e32 v10, v76, v18
	v_fmac_f32_e32 v10, v77, v19
	v_fmac_f32_e32 v10, v78, v20
	v_fmac_f32_e32 v10, v79, v21
	ds_read_b128 v[18:21], v102 offset:7552
	s_waitcnt lgkmcnt(0)
	v_fmac_f32_e32 v10, v80, v18
	v_fmac_f32_e32 v10, v81, v19
	v_fmac_f32_e32 v10, v82, v20
	v_fmac_f32_e32 v10, v83, v21
	ds_read_b128 v[18:21], v102 offset:7568
	s_waitcnt lgkmcnt(0)
	v_fmac_f32_e32 v10, v84, v18
	v_fmac_f32_e32 v10, v85, v19
	v_fmac_f32_e32 v10, v86, v20
	v_fmac_f32_e32 v10, v87, v21
	ds_read_b128 v[18:21], v102 offset:7584
	s_waitcnt lgkmcnt(0)
	v_fmac_f32_e32 v10, v88, v18
	v_fmac_f32_e32 v10, v89, v19
	v_fmac_f32_e32 v10, v90, v20
	v_fmac_f32_e32 v10, v91, v21
	ds_read_b128 v[18:21], v102 offset:7600
	s_waitcnt lgkmcnt(0)
	v_fmac_f32_e32 v10, v92, v18
	v_fmac_f32_e32 v10, v93, v19
	v_fmac_f32_e32 v10, v94, v20
	v_fmac_f32_e32 v10, v95, v21
	ds_read_b128 v[18:21], v102 offset:7616
	s_waitcnt lgkmcnt(0)
	v_fmac_f32_e32 v10, v96, v18
	v_fmac_f32_e32 v10, v97, v19
	v_fmac_f32_e32 v10, v98, v20
	v_fmac_f32_e32 v10, v99, v21
	ds_read_b128 v[18:21], v102 offset:7632
	s_waitcnt lgkmcnt(0)
	v_fmac_f32_e32 v10, v100, v18
	v_fmac_f32_e32 v10, v101, v19
	v_fmac_f32_e32 v10, v12, v20
	v_fmac_f32_e32 v10, v13, v21
	ds_read_b128 v[18:21], v102 offset:7648
	s_waitcnt lgkmcnt(0)
	v_pk_mul_f32 v[2:3], v[14:15], v[18:19]
	s_nop 0
	v_add_f32_e32 v2, v10, v2
	v_add_f32_e32 v10, v2, v3
	v_pk_mul_f32 v[2:3], v[6:7], v[20:21]
	ds_read_b128 v[18:21], v102 offset:7664
	v_add_f32_e32 v2, v10, v2
	v_add_f32_e32 v10, v2, v3
	s_waitcnt lgkmcnt(0)
	v_pk_mul_f32 v[2:3], v[16:17], v[18:19]
	s_nop 0
	v_add_f32_e32 v2, v10, v2
	v_add_f32_e32 v10, v2, v3
	v_pk_mul_f32 v[2:3], v[4:5], v[20:21]
	s_nop 0
	v_add_f32_e32 v2, v10, v2
	v_add_f32_e32 v112, v2, v3
	v_mul_f32_e32 v2, 0x39800000, v112
	v_max3_f32 v10, v0, v1, v2
	ds_read_b128 v[0:3], v102 offset:7680
	s_waitcnt lgkmcnt(0)
	v_fma_f32 v11, v48, v0, 0
	v_fmac_f32_e32 v11, v49, v1
	v_fmac_f32_e32 v11, v50, v2
	v_fmac_f32_e32 v11, v51, v3
	ds_read_b128 v[0:3], v102 offset:7696
	s_waitcnt lgkmcnt(0)
	v_fmac_f32_e32 v11, v52, v0
	v_fmac_f32_e32 v11, v53, v1
	v_fmac_f32_e32 v11, v54, v2
	v_fmac_f32_e32 v11, v55, v3
	ds_read_b128 v[0:3], v102 offset:7712
	s_waitcnt lgkmcnt(0)
	v_fmac_f32_e32 v11, v56, v0
	v_fmac_f32_e32 v11, v57, v1
	v_fmac_f32_e32 v11, v58, v2
	v_fmac_f32_e32 v11, v59, v3
	ds_read_b128 v[0:3], v102 offset:7728
	s_waitcnt lgkmcnt(0)
	v_fmac_f32_e32 v11, v60, v0
	v_fmac_f32_e32 v11, v61, v1
	v_fmac_f32_e32 v11, v62, v2
	v_fmac_f32_e32 v11, v63, v3
	ds_read_b128 v[0:3], v102 offset:7744
	s_waitcnt lgkmcnt(0)
	v_fmac_f32_e32 v11, v64, v0
	v_fmac_f32_e32 v11, v65, v1
	v_fmac_f32_e32 v11, v66, v2
	v_fmac_f32_e32 v11, v67, v3
	ds_read_b128 v[0:3], v102 offset:7760
	s_waitcnt lgkmcnt(0)
	v_fmac_f32_e32 v11, v68, v0
	v_fmac_f32_e32 v11, v69, v1
	v_fmac_f32_e32 v11, v70, v2
	v_fmac_f32_e32 v11, v71, v3
	ds_read_b128 v[0:3], v102 offset:7776
	s_waitcnt lgkmcnt(0)
	v_fmac_f32_e32 v11, v72, v0
	v_fmac_f32_e32 v11, v73, v1
	v_fmac_f32_e32 v11, v74, v2
	v_fmac_f32_e32 v11, v75, v3
	ds_read_b128 v[0:3], v102 offset:7792
	s_waitcnt lgkmcnt(0)
	v_fmac_f32_e32 v11, v76, v0
	v_fmac_f32_e32 v11, v77, v1
	v_fmac_f32_e32 v11, v78, v2
	v_fmac_f32_e32 v11, v79, v3
	ds_read_b128 v[0:3], v102 offset:7808
	s_waitcnt lgkmcnt(0)
	v_fmac_f32_e32 v11, v80, v0
	v_fmac_f32_e32 v11, v81, v1
	v_fmac_f32_e32 v11, v82, v2
	v_fmac_f32_e32 v11, v83, v3
	ds_read_b128 v[0:3], v102 offset:7824
	s_waitcnt lgkmcnt(0)
	v_fmac_f32_e32 v11, v84, v0
	v_fmac_f32_e32 v11, v85, v1
	v_fmac_f32_e32 v11, v86, v2
	v_fmac_f32_e32 v11, v87, v3
	ds_read_b128 v[0:3], v102 offset:7840
	s_waitcnt lgkmcnt(0)
	v_fmac_f32_e32 v11, v88, v0
	v_fmac_f32_e32 v11, v89, v1
	v_fmac_f32_e32 v11, v90, v2
	v_fmac_f32_e32 v11, v91, v3
	ds_read_b128 v[0:3], v102 offset:7856
	s_waitcnt lgkmcnt(0)
	v_fmac_f32_e32 v11, v92, v0
	v_fmac_f32_e32 v11, v93, v1
	v_fmac_f32_e32 v11, v94, v2
	v_fmac_f32_e32 v11, v95, v3
	ds_read_b128 v[0:3], v102 offset:7872
	s_waitcnt lgkmcnt(0)
	v_fmac_f32_e32 v11, v96, v0
	v_fmac_f32_e32 v11, v97, v1
	v_fmac_f32_e32 v11, v98, v2
	v_fmac_f32_e32 v11, v99, v3
	ds_read_b128 v[0:3], v102 offset:7888
	s_waitcnt lgkmcnt(0)
	v_fmac_f32_e32 v11, v100, v0
	v_fmac_f32_e32 v11, v101, v1
	v_pk_mul_f32 v[0:1], v[12:13], v[2:3]
	s_nop 0
	v_add_f32_e32 v0, v11, v0
	v_add_f32_e32 v11, v0, v1
	ds_read_b128 v[0:3], v102 offset:7904
	s_waitcnt lgkmcnt(0)
	v_pk_mul_f32 v[0:1], v[14:15], v[0:1]
	s_nop 0
	v_add_f32_e32 v0, v11, v0
	v_add_f32_e32 v11, v0, v1
	v_pk_mul_f32 v[0:1], v[6:7], v[2:3]
	s_nop 0
	v_add_f32_e32 v0, v11, v0
	v_add_f32_e32 v11, v0, v1
	ds_read_b128 v[0:3], v102 offset:7920
	s_waitcnt lgkmcnt(0)
	v_pk_mul_f32 v[0:1], v[16:17], v[0:1]
	s_nop 0
	v_add_f32_e32 v0, v11, v0
	v_add_f32_e32 v11, v0, v1
	v_pk_mul_f32 v[0:1], v[4:5], v[2:3]
	s_nop 0
	v_add_f32_e32 v0, v11, v0
	v_add_f32_e32 v114, v0, v1
	ds_read_b128 v[0:3], v102 offset:7936
	v_mul_f32_e32 v11, 0x39800000, v114
	s_waitcnt lgkmcnt(0)
	v_fma_f32 v18, v48, v0, 0
	v_fmac_f32_e32 v18, v49, v1
	v_fmac_f32_e32 v18, v50, v2
	v_fmac_f32_e32 v18, v51, v3
	ds_read_b128 v[0:3], v102 offset:7952
	s_waitcnt lgkmcnt(0)
	v_fmac_f32_e32 v18, v52, v0
	v_fmac_f32_e32 v18, v53, v1
	v_fmac_f32_e32 v18, v54, v2
	v_fmac_f32_e32 v18, v55, v3
	ds_read_b128 v[0:3], v102 offset:7968
	s_waitcnt lgkmcnt(0)
	v_fmac_f32_e32 v18, v56, v0
	v_fmac_f32_e32 v18, v57, v1
	v_fmac_f32_e32 v18, v58, v2
	v_fmac_f32_e32 v18, v59, v3
	ds_read_b128 v[0:3], v102 offset:7984
	s_waitcnt lgkmcnt(0)
	v_fmac_f32_e32 v18, v60, v0
	v_fmac_f32_e32 v18, v61, v1
	v_fmac_f32_e32 v18, v62, v2
	v_fmac_f32_e32 v18, v63, v3
	ds_read_b128 v[0:3], v102 offset:8000
	s_waitcnt lgkmcnt(0)
	v_fmac_f32_e32 v18, v64, v0
	v_fmac_f32_e32 v18, v65, v1
	v_fmac_f32_e32 v18, v66, v2
	v_fmac_f32_e32 v18, v67, v3
	ds_read_b128 v[0:3], v102 offset:8016
	s_waitcnt lgkmcnt(0)
	v_fmac_f32_e32 v18, v68, v0
	v_fmac_f32_e32 v18, v69, v1
	v_fmac_f32_e32 v18, v70, v2
	v_fmac_f32_e32 v18, v71, v3
	ds_read_b128 v[0:3], v102 offset:8032
	s_waitcnt lgkmcnt(0)
	v_fmac_f32_e32 v18, v72, v0
	v_fmac_f32_e32 v18, v73, v1
	v_fmac_f32_e32 v18, v74, v2
	v_fmac_f32_e32 v18, v75, v3
	ds_read_b128 v[0:3], v102 offset:8048
	s_waitcnt lgkmcnt(0)
	v_fmac_f32_e32 v18, v76, v0
	v_fmac_f32_e32 v18, v77, v1
	v_fmac_f32_e32 v18, v78, v2
	v_fmac_f32_e32 v18, v79, v3
	ds_read_b128 v[0:3], v102 offset:8064
	s_waitcnt lgkmcnt(0)
	v_fmac_f32_e32 v18, v80, v0
	v_fmac_f32_e32 v18, v81, v1
	v_fmac_f32_e32 v18, v82, v2
	v_fmac_f32_e32 v18, v83, v3
	ds_read_b128 v[0:3], v102 offset:8080
	s_waitcnt lgkmcnt(0)
	v_fmac_f32_e32 v18, v84, v0
	v_fmac_f32_e32 v18, v85, v1
	v_fmac_f32_e32 v18, v86, v2
	v_fmac_f32_e32 v18, v87, v3
	ds_read_b128 v[0:3], v102 offset:8096
	s_waitcnt lgkmcnt(0)
	v_fmac_f32_e32 v18, v88, v0
	v_fmac_f32_e32 v18, v89, v1
	v_fmac_f32_e32 v18, v90, v2
	v_fmac_f32_e32 v18, v91, v3
	ds_read_b128 v[0:3], v102 offset:8112
	s_waitcnt lgkmcnt(0)
	v_fmac_f32_e32 v18, v92, v0
	v_fmac_f32_e32 v18, v93, v1
	v_fmac_f32_e32 v18, v94, v2
	v_fmac_f32_e32 v18, v95, v3
	ds_read_b128 v[0:3], v102 offset:8128
	s_waitcnt lgkmcnt(0)
	v_fmac_f32_e32 v18, v96, v0
	v_fmac_f32_e32 v18, v97, v1
	v_fmac_f32_e32 v18, v98, v2
	v_fmac_f32_e32 v18, v99, v3
	ds_read_b128 v[0:3], v102 offset:8144
	s_waitcnt lgkmcnt(0)
	v_fmac_f32_e32 v18, v100, v0
	v_fmac_f32_e32 v18, v101, v1
	v_pk_mul_f32 v[0:1], v[12:13], v[2:3]
	s_nop 0
	v_add_f32_e32 v0, v18, v0
	v_add_f32_e32 v18, v0, v1
	ds_read_b128 v[0:3], v102 offset:8160
	s_waitcnt lgkmcnt(0)
	v_pk_mul_f32 v[0:1], v[14:15], v[0:1]
	s_nop 0
	v_add_f32_e32 v0, v18, v0
	v_add_f32_e32 v18, v0, v1
	v_pk_mul_f32 v[0:1], v[6:7], v[2:3]
	s_nop 0
	v_add_f32_e32 v0, v18, v0
	ds_read_b128 v[18:21], v102 offset:8176
	v_add_f32_e32 v2, v0, v1
	s_waitcnt lgkmcnt(0)
	v_pk_mul_f32 v[0:1], v[16:17], v[18:19]
	s_nop 0
	v_add_f32_e32 v0, v2, v0
	v_add_f32_e32 v2, v0, v1
	v_pk_mul_f32 v[0:1], v[4:5], v[20:21]
	s_nop 0
	v_add_f32_e32 v0, v2, v0
	v_add_f32_e32 v3, v0, v1
	v_mul_f32_e32 v0, 0x39800000, v3
	v_max3_f32 v124, v10, v11, v0
	v_sub_f32_e32 v0, v8, v124
	v_mul_f32_e32 v1, 0x3fb8aa3b, v0
	v_fma_f32 v2, v0, s5, -v1
	v_rndne_f32_e32 v8, v1
	v_fmac_f32_e32 v2, 0x32a5705f, v0
	v_sub_f32_e32 v1, v1, v8
	v_add_f32_e32 v1, v1, v2
	v_exp_f32_e32 v1, v1
	v_cvt_i32_f32_e32 v2, v8
	v_cmp_ngt_f32_e32 vcc, s6, v0
	v_fma_f32 v109, v109, s4, -v124
	v_ldexp_f32 v1, v1, v2
	v_cndmask_b32_e32 v1, 0, v1, vcc
	v_cmp_nlt_f32_e32 vcc, s7, v0
	v_fma_f32 v0, v9, s4, -v124
	s_nop 0
	v_cndmask_b32_e32 v46, v103, v1, vcc
	v_mul_f32_e32 v1, 0x3fb8aa3b, v0
	v_fma_f32 v2, v0, s5, -v1
	v_rndne_f32_e32 v8, v1
	v_fmac_f32_e32 v2, 0x32a5705f, v0
	v_sub_f32_e32 v1, v1, v8
	v_add_f32_e32 v1, v1, v2
	v_exp_f32_e32 v1, v1
	v_cvt_i32_f32_e32 v2, v8
	ds_read_b96 v[8:10], v102 offset:8192
	v_cmp_ngt_f32_e32 vcc, s6, v0
	v_ldexp_f32 v1, v1, v2
	s_nop 0
	v_cndmask_b32_e32 v1, 0, v1, vcc
	v_cmp_nlt_f32_e32 vcc, s7, v0
	s_waitcnt lgkmcnt(0)
	v_mov_b32_e32 v18, v9
	v_mov_b32_e32 v19, v10
	v_cndmask_b32_e32 v2, v103, v1, vcc
	v_mul_f32_e32 v1, v2, v8
	v_pk_mul_f32 v[8:9], v[2:3], v[18:19] op_sel_hi:[0,1]
	v_mov_b32_e32 v0, 0x200c
	v_pk_fma_f32 v[210:211], v[46:47], v[192:193], v[8:9] op_sel_hi:[0,1,1]
	ds_read2_b32 v[8:9], v0 offset1:1
	v_mov_b32_e32 v0, 0x2014
	v_fmac_f32_e32 v1, v46, v205
	s_waitcnt lgkmcnt(0)
	v_pk_mul_f32 v[8:9], v[2:3], v[8:9] op_sel_hi:[0,1]
	v_pk_fma_f32 v[212:213], v[46:47], v[190:191], v[8:9] op_sel_hi:[0,1,1]
	ds_read2_b32 v[8:9], v0 offset1:1
	v_mov_b32_e32 v0, 0x201c
	s_waitcnt lgkmcnt(0)
	v_pk_mul_f32 v[8:9], v[2:3], v[8:9] op_sel_hi:[0,1]
	v_pk_fma_f32 v[188:189], v[46:47], v[188:189], v[8:9] op_sel_hi:[0,1,1]
	ds_read2_b32 v[8:9], v0 offset1:1
	v_mov_b32_e32 v0, 0x2024
	s_waitcnt lgkmcnt(0)
	v_pk_mul_f32 v[8:9], v[2:3], v[8:9] op_sel_hi:[0,1]
	v_pk_fma_f32 v[208:209], v[46:47], v[186:187], v[8:9] op_sel_hi:[0,1,1]
	ds_read2_b32 v[8:9], v0 offset1:1
	v_mov_b32_e32 v0, 0x202c
	s_waitcnt lgkmcnt(0)
	v_pk_mul_f32 v[8:9], v[2:3], v[8:9] op_sel_hi:[0,1]
	v_pk_fma_f32 v[184:185], v[46:47], v[184:185], v[8:9] op_sel_hi:[0,1,1]
	ds_read2_b32 v[8:9], v0 offset1:1
	v_mov_b32_e32 v0, 0x2034
	s_waitcnt lgkmcnt(0)
	v_pk_mul_f32 v[8:9], v[2:3], v[8:9] op_sel_hi:[0,1]
	v_pk_fma_f32 v[182:183], v[46:47], v[182:183], v[8:9] op_sel_hi:[0,1,1]
	ds_read2_b32 v[8:9], v0 offset1:1
	v_mov_b32_e32 v0, 0x203c
	s_waitcnt lgkmcnt(0)
	v_pk_mul_f32 v[8:9], v[2:3], v[8:9] op_sel_hi:[0,1]
	v_pk_fma_f32 v[180:181], v[46:47], v[180:181], v[8:9] op_sel_hi:[0,1,1]
	ds_read2_b32 v[8:9], v0 offset1:1
	v_mov_b32_e32 v0, 0x2044
	s_waitcnt lgkmcnt(0)
	v_pk_mul_f32 v[8:9], v[2:3], v[8:9] op_sel_hi:[0,1]
	v_pk_fma_f32 v[178:179], v[46:47], v[178:179], v[8:9] op_sel_hi:[0,1,1]
	ds_read2_b32 v[8:9], v0 offset1:1
	v_mov_b32_e32 v0, 0x204c
	s_waitcnt lgkmcnt(0)
	v_pk_mul_f32 v[8:9], v[2:3], v[8:9] op_sel_hi:[0,1]
	v_pk_fma_f32 v[170:171], v[46:47], v[170:171], v[8:9] op_sel_hi:[0,1,1]
	ds_read2_b32 v[8:9], v0 offset1:1
	v_mov_b32_e32 v0, 0x2054
	s_waitcnt lgkmcnt(0)
	v_pk_mul_f32 v[8:9], v[2:3], v[8:9] op_sel_hi:[0,1]
	v_pk_fma_f32 v[168:169], v[46:47], v[168:169], v[8:9] op_sel_hi:[0,1,1]
	ds_read2_b32 v[8:9], v0 offset1:1
	v_mov_b32_e32 v0, 0x205c
	s_waitcnt lgkmcnt(0)
	v_pk_mul_f32 v[8:9], v[2:3], v[8:9] op_sel_hi:[0,1]
	v_pk_fma_f32 v[42:43], v[46:47], v[176:177], v[8:9] op_sel_hi:[0,1,1]
	ds_read2_b32 v[8:9], v0 offset1:1
	v_mov_b32_e32 v0, 0x2064
	s_waitcnt lgkmcnt(0)
	v_pk_mul_f32 v[8:9], v[2:3], v[8:9] op_sel_hi:[0,1]
	v_pk_fma_f32 v[24:25], v[46:47], v[166:167], v[8:9] op_sel_hi:[0,1,1]
	ds_read2_b32 v[8:9], v0 offset1:1
	v_mov_b32_e32 v0, 0x206c
	s_waitcnt lgkmcnt(0)
	v_pk_mul_f32 v[8:9], v[2:3], v[8:9] op_sel_hi:[0,1]
	v_pk_fma_f32 v[18:19], v[46:47], v[202:203], v[8:9] op_sel_hi:[0,1,1]
	ds_read2_b32 v[8:9], v0 offset1:1
	v_mov_b32_e32 v0, 0x2074
	s_waitcnt lgkmcnt(0)
	v_pk_mul_f32 v[8:9], v[2:3], v[8:9] op_sel_hi:[0,1]
	v_pk_fma_f32 v[22:23], v[46:47], v[200:201], v[8:9] op_sel_hi:[0,1,1]
	ds_read2_b32 v[8:9], v0 offset1:1
	v_mov_b32_e32 v0, 0x207c
	s_waitcnt lgkmcnt(0)
	v_pk_mul_f32 v[8:9], v[2:3], v[8:9] op_sel_hi:[0,1]
	v_pk_fma_f32 v[20:21], v[46:47], v[198:199], v[8:9] op_sel_hi:[0,1,1]
	ds_read2_b32 v[8:9], v0 offset1:1
	v_mov_b32_e32 v0, 0x2084
	s_waitcnt lgkmcnt(0)
	v_pk_mul_f32 v[8:9], v[2:3], v[8:9] op_sel_hi:[0,1]
	v_pk_fma_f32 v[10:11], v[46:47], v[196:197], v[8:9] op_sel_hi:[0,1,1]
	ds_read2_b32 v[8:9], v0 offset1:1
	v_mov_b32_e32 v0, 0x208c
	ds_read2_b32 v[26:27], v0 offset1:1
	v_mov_b32_e32 v0, 0x2094
	s_waitcnt lgkmcnt(1)
	v_pk_mul_f32 v[8:9], v[2:3], v[8:9] op_sel_hi:[0,1]
	v_pk_fma_f32 v[8:9], v[46:47], v[194:195], v[8:9] op_sel_hi:[0,1,1]
	s_waitcnt lgkmcnt(0)
	v_mul_f32_e32 v166, v2, v26
	v_mul_f32_e32 v167, v2, v27
	ds_read2_b32 v[26:27], v0 offset1:1
	v_mov_b32_e32 v0, 0x209c
	v_fmac_f32_e32 v166, v46, v164
	v_fmac_f32_e32 v167, v46, v165
	s_waitcnt lgkmcnt(0)
	v_pk_mul_f32 v[26:27], v[2:3], v[26:27] op_sel_hi:[0,1]
	v_pk_fma_f32 v[28:29], v[46:47], v[174:175], v[26:27] op_sel_hi:[0,1,1]
	ds_read2_b32 v[26:27], v0 offset1:1
	v_mov_b32_e32 v0, 0x20a4
	ds_read2_b32 v[30:31], v0 offset1:1
	v_mov_b32_e32 v0, 0x20ac
	s_waitcnt lgkmcnt(1)
	v_pk_mul_f32 v[26:27], v[2:3], v[26:27] op_sel_hi:[0,1]
	v_pk_fma_f32 v[26:27], v[46:47], v[172:173], v[26:27] op_sel_hi:[0,1,1]
	s_waitcnt lgkmcnt(0)
	v_mul_f32_e32 v164, v2, v30
	v_mul_f32_e32 v165, v2, v31
	ds_read2_b32 v[30:31], v0 offset1:1
	v_mov_b32_e32 v0, 0x20b4
	v_fmac_f32_e32 v164, v46, v160
	v_fmac_f32_e32 v165, v46, v161
	s_waitcnt lgkmcnt(0)
	v_pk_mul_f32 v[30:31], v[2:3], v[30:31] op_sel_hi:[0,1]
	v_pk_fma_f32 v[32:33], v[46:47], v[162:163], v[30:31] op_sel_hi:[0,1,1]
	ds_read2_b32 v[30:31], v0 offset1:1
	v_mov_b32_e32 v0, 0x20bc
	ds_read2_b32 v[34:35], v0 offset1:1
	v_mov_b32_e32 v0, 0x20c4
	s_waitcnt lgkmcnt(1)
	v_pk_mul_f32 v[30:31], v[2:3], v[30:31] op_sel_hi:[0,1]
	v_pk_fma_f32 v[30:31], v[46:47], v[158:159], v[30:31] op_sel_hi:[0,1,1]
	s_waitcnt lgkmcnt(0)
	v_mul_f32_e32 v158, v2, v34
	v_mul_f32_e32 v159, v2, v35
	ds_read2_b32 v[34:35], v0 offset1:1
	v_mov_b32_e32 v0, 0x20cc
	ds_read2_b32 v[36:37], v0 offset1:1
	v_mov_b32_e32 v0, 0x20d4
	ds_read2_b32 v[38:39], v0 offset1:1
	v_mov_b32_e32 v0, 0x20dc
	v_fmac_f32_e32 v158, v46, v152
	v_fmac_f32_e32 v159, v46, v153
	s_waitcnt lgkmcnt(2)
	v_pk_mul_f32 v[34:35], v[2:3], v[34:35] op_sel_hi:[0,1]
	s_waitcnt lgkmcnt(0)
	v_mul_f32_e32 v152, v2, v38
	v_mul_f32_e32 v153, v2, v39
	ds_read2_b32 v[38:39], v0 offset1:1
	v_mov_b32_e32 v0, 0x20e4
	v_fmac_f32_e32 v152, v46, v148
	v_fmac_f32_e32 v153, v46, v149
	v_pk_fma_f32 v[34:35], v[46:47], v[156:157], v[34:35] op_sel_hi:[0,1,1]
	s_waitcnt lgkmcnt(0)
	v_pk_mul_f32 v[38:39], v[2:3], v[38:39] op_sel_hi:[0,1]
	v_pk_fma_f32 v[40:41], v[46:47], v[150:151], v[38:39] op_sel_hi:[0,1,1]
	ds_read2_b32 v[38:39], v0 offset1:1
	v_mov_b32_e32 v0, 0x20ec
	ds_read2_b32 v[44:45], v0 offset1:1
	v_mov_b32_e32 v0, 0x20f4
	v_pk_mul_f32 v[36:37], v[2:3], v[36:37] op_sel_hi:[0,1]
	s_waitcnt lgkmcnt(1)
	v_pk_mul_f32 v[38:39], v[2:3], v[38:39] op_sel_hi:[0,1]
	v_pk_fma_f32 v[36:37], v[46:47], v[154:155], v[36:37] op_sel_hi:[0,1,1]
	s_waitcnt lgkmcnt(0)
	v_mul_f32_e32 v148, v2, v44
	v_mul_f32_e32 v149, v2, v45
	ds_read2_b32 v[44:45], v0 offset1:1
	v_mov_b32_e32 v0, 0x20fc
	v_fmac_f32_e32 v148, v46, v144
	v_fmac_f32_e32 v149, v46, v145
	ds_read2_b32 v[144:145], v0 offset1:1
	s_waitcnt lgkmcnt(1)
	v_pk_mul_f32 v[44:45], v[2:3], v[44:45] op_sel_hi:[0,1]
	v_pk_fma_f32 v[38:39], v[46:47], v[146:147], v[38:39] op_sel_hi:[0,1,1]
	v_pk_fma_f32 v[44:45], v[46:47], v[206:207], v[44:45] op_sel_hi:[0,1,1]
	s_waitcnt lgkmcnt(0)
	v_mul_f32_e32 v0, v2, v144
	v_fmac_f32_e32 v0, v46, v204
	v_fmac_f32_e32 v2, v47, v46
	v_fma_f32 v46, v214, s4, -v124
	v_mul_f32_e32 v47, 0x3fb8aa3b, v46
	v_fma_f32 v144, v46, s5, -v47
	v_rndne_f32_e32 v146, v47
	v_fmac_f32_e32 v144, 0x32a5705f, v46
	v_sub_f32_e32 v47, v47, v146
	v_add_f32_e32 v47, v47, v144
	v_exp_f32_e32 v47, v47
	v_cvt_i32_f32_e32 v144, v146
	v_cmp_ngt_f32_e32 vcc, s6, v46
	v_ldexp_f32 v47, v47, v144
	s_nop 0
	v_cndmask_b32_e32 v47, 0, v47, vcc
	v_cmp_nlt_f32_e32 vcc, s7, v46
	v_mov_b32_e32 v46, 0x2104
	ds_read2_b32 v[224:225], v46 offset1:1
	v_mov_b32_e32 v46, 0x210c
	ds_read2_b32 v[226:227], v46 offset1:1
	v_mov_b32_e32 v46, 0x2114
	ds_read2_b32 v[220:221], v46 offset1:1
	v_mov_b32_e32 v46, 0x211c
	ds_read2_b32 v[222:223], v46 offset1:1
	v_mov_b32_e32 v46, 0x2124
	ds_read2_b32 v[216:217], v46 offset1:1
	v_mov_b32_e32 v46, 0x212c
	ds_read2_b32 v[218:219], v46 offset1:1
	v_mov_b32_e32 v46, 0x2134
	ds_read2_b32 v[206:207], v46 offset1:1
	v_mov_b32_e32 v46, 0x213c
	ds_read2_b32 v[214:215], v46 offset1:1
	v_mov_b32_e32 v46, 0x2144
	ds_read2_b32 v[200:201], v46 offset1:1
	v_mov_b32_e32 v46, 0x214c
	ds_read2_b32 v[204:205], v46 offset1:1
	v_mov_b32_e32 v46, 0x2154
	v_cndmask_b32_e32 v198, v103, v47, vcc
	ds_read2_b32 v[46:47], v46 offset1:1
	v_fmac_f32_e32 v1, v198, v145
	v_add_f32_e32 v2, v2, v198
	s_waitcnt lgkmcnt(2)
	v_pk_fma_f32 v[170:171], v[198:199], v[200:201], v[170:171] op_sel_hi:[0,1,1]
	s_waitcnt lgkmcnt(0)
	v_pk_fma_f32 v[42:43], v[198:199], v[46:47], v[42:43] op_sel_hi:[0,1,1]
	v_mov_b32_e32 v46, 0x215c
	ds_read2_b32 v[46:47], v46 offset1:1
	s_waitcnt lgkmcnt(0)
	v_pk_fma_f32 v[24:25], v[198:199], v[46:47], v[24:25] op_sel_hi:[0,1,1]
	v_mov_b32_e32 v46, 0x2164
	ds_read2_b32 v[46:47], v46 offset1:1
	s_waitcnt lgkmcnt(0)
	v_pk_fma_f32 v[18:19], v[198:199], v[46:47], v[18:19] op_sel_hi:[0,1,1]
	v_mov_b32_e32 v46, 0x216c
	ds_read2_b32 v[46:47], v46 offset1:1
	s_waitcnt lgkmcnt(0)
	v_pk_fma_f32 v[22:23], v[198:199], v[46:47], v[22:23] op_sel_hi:[0,1,1]
	v_mov_b32_e32 v46, 0x2174
	ds_read2_b32 v[46:47], v46 offset1:1
	s_waitcnt lgkmcnt(0)
	v_pk_fma_f32 v[20:21], v[198:199], v[46:47], v[20:21] op_sel_hi:[0,1,1]
	v_mov_b32_e32 v46, 0x217c
	ds_read2_b32 v[46:47], v46 offset1:1
	s_waitcnt lgkmcnt(0)
	v_pk_fma_f32 v[10:11], v[198:199], v[46:47], v[10:11] op_sel_hi:[0,1,1]
	v_mov_b32_e32 v46, 0x2184
	ds_read2_b32 v[46:47], v46 offset1:1
	s_waitcnt lgkmcnt(0)
	v_pk_fma_f32 v[8:9], v[198:199], v[46:47], v[8:9] op_sel_hi:[0,1,1]
	v_mov_b32_e32 v46, 0x218c
	ds_read2_b32 v[46:47], v46 offset1:1
	s_waitcnt lgkmcnt(0)
	v_fmac_f32_e32 v166, v198, v46
	v_mov_b32_e32 v46, 0x2194
	v_fmac_f32_e32 v167, v198, v47
	ds_read2_b32 v[46:47], v46 offset1:1
	s_waitcnt lgkmcnt(0)
	v_pk_fma_f32 v[28:29], v[198:199], v[46:47], v[28:29] op_sel_hi:[0,1,1]
	v_mov_b32_e32 v46, 0x219c
	ds_read2_b32 v[46:47], v46 offset1:1
	s_waitcnt lgkmcnt(0)
	v_pk_fma_f32 v[26:27], v[198:199], v[46:47], v[26:27] op_sel_hi:[0,1,1]
	v_mov_b32_e32 v46, 0x21a4
	ds_read2_b32 v[46:47], v46 offset1:1
	s_waitcnt lgkmcnt(0)
	v_fmac_f32_e32 v164, v198, v46
	v_mov_b32_e32 v46, 0x21ac
	v_fmac_f32_e32 v165, v198, v47
	ds_read2_b32 v[46:47], v46 offset1:1
	s_waitcnt lgkmcnt(0)
	v_pk_fma_f32 v[32:33], v[198:199], v[46:47], v[32:33] op_sel_hi:[0,1,1]
	v_mov_b32_e32 v46, 0x21b4
	ds_read2_b32 v[46:47], v46 offset1:1
	s_waitcnt lgkmcnt(0)
	v_pk_fma_f32 v[30:31], v[198:199], v[46:47], v[30:31] op_sel_hi:[0,1,1]
	v_mov_b32_e32 v46, 0x21bc
	ds_read2_b32 v[46:47], v46 offset1:1
	s_waitcnt lgkmcnt(0)
	v_fmac_f32_e32 v158, v198, v46
	v_mov_b32_e32 v46, 0x21c4
	v_fmac_f32_e32 v159, v198, v47
	ds_read2_b32 v[46:47], v46 offset1:1
	s_waitcnt lgkmcnt(0)
	v_pk_fma_f32 v[34:35], v[198:199], v[46:47], v[34:35] op_sel_hi:[0,1,1]
	v_mov_b32_e32 v46, 0x21cc
	ds_read2_b32 v[46:47], v46 offset1:1
	s_waitcnt lgkmcnt(0)
	v_pk_fma_f32 v[36:37], v[198:199], v[46:47], v[36:37] op_sel_hi:[0,1,1]
	v_mov_b32_e32 v46, 0x21d4
	ds_read2_b32 v[46:47], v46 offset1:1
	s_waitcnt lgkmcnt(0)
	v_fmac_f32_e32 v152, v198, v46
	v_mov_b32_e32 v46, 0x21dc
	v_fmac_f32_e32 v153, v198, v47
	ds_read2_b32 v[46:47], v46 offset1:1
	s_waitcnt lgkmcnt(0)
	v_pk_fma_f32 v[40:41], v[198:199], v[46:47], v[40:41] op_sel_hi:[0,1,1]
	v_mov_b32_e32 v46, 0x21e4
	ds_read2_b32 v[46:47], v46 offset1:1
	s_waitcnt lgkmcnt(0)
	v_pk_fma_f32 v[38:39], v[198:199], v[46:47], v[38:39] op_sel_hi:[0,1,1]
	v_mov_b32_e32 v46, 0x21ec
	ds_read2_b32 v[46:47], v46 offset1:1
	s_waitcnt lgkmcnt(0)
	v_fmac_f32_e32 v148, v198, v46
	v_mov_b32_e32 v46, 0x21f4
	v_fmac_f32_e32 v149, v198, v47
	ds_read2_b32 v[46:47], v46 offset1:1
	s_waitcnt lgkmcnt(0)
	v_pk_fma_f32 v[44:45], v[198:199], v[46:47], v[44:45] op_sel_hi:[0,1,1]
	v_mov_b32_e32 v46, 0x21fc
	ds_read2_b32 v[46:47], v46 offset1:1
	s_waitcnt lgkmcnt(0)
	v_fmac_f32_e32 v0, v198, v46
	v_fma_f32 v46, v228, s4, -v124
	v_mul_f32_e32 v144, 0x3fb8aa3b, v46
	v_fma_f32 v145, v46, s5, -v144
	v_rndne_f32_e32 v146, v144
	v_fmac_f32_e32 v145, 0x32a5705f, v46
	v_sub_f32_e32 v144, v144, v146
	v_add_f32_e32 v144, v144, v145
	v_exp_f32_e32 v144, v144
	v_cvt_i32_f32_e32 v145, v146
	v_cmp_ngt_f32_e32 vcc, s6, v46
	v_ldexp_f32 v144, v144, v145
	s_nop 0
	v_cndmask_b32_e32 v144, 0, v144, vcc
	v_cmp_nlt_f32_e32 vcc, s7, v46
	v_mov_b32_e32 v46, 0x2254
	s_nop 0
	v_cndmask_b32_e32 v228, v103, v144, vcc
	v_fmac_f32_e32 v1, v228, v47
	ds_read2_b32 v[46:47], v46 offset1:1
	v_add_f32_e32 v2, v2, v228
	s_waitcnt lgkmcnt(0)
	v_pk_fma_f32 v[42:43], v[228:229], v[46:47], v[42:43] op_sel_hi:[0,1,1]
	v_mov_b32_e32 v46, 0x225c
	ds_read2_b32 v[46:47], v46 offset1:1
	s_waitcnt lgkmcnt(0)
	v_pk_fma_f32 v[24:25], v[228:229], v[46:47], v[24:25] op_sel_hi:[0,1,1]
	v_mov_b32_e32 v46, 0x2264
	ds_read2_b32 v[46:47], v46 offset1:1
	s_waitcnt lgkmcnt(0)
	v_pk_fma_f32 v[18:19], v[228:229], v[46:47], v[18:19] op_sel_hi:[0,1,1]
	v_mov_b32_e32 v46, 0x226c
	ds_read2_b32 v[46:47], v46 offset1:1
	s_waitcnt lgkmcnt(0)
	v_pk_fma_f32 v[22:23], v[228:229], v[46:47], v[22:23] op_sel_hi:[0,1,1]
	v_mov_b32_e32 v46, 0x2274
	ds_read2_b32 v[46:47], v46 offset1:1
	s_waitcnt lgkmcnt(0)
	v_pk_fma_f32 v[20:21], v[228:229], v[46:47], v[20:21] op_sel_hi:[0,1,1]
	v_mov_b32_e32 v46, 0x227c
	ds_read2_b32 v[46:47], v46 offset1:1
	s_waitcnt lgkmcnt(0)
	v_pk_fma_f32 v[10:11], v[228:229], v[46:47], v[10:11] op_sel_hi:[0,1,1]
	v_mov_b32_e32 v46, 0x2284
	ds_read2_b32 v[46:47], v46 offset1:1
	s_waitcnt lgkmcnt(0)
	v_pk_fma_f32 v[8:9], v[228:229], v[46:47], v[8:9] op_sel_hi:[0,1,1]
	v_mov_b32_e32 v46, 0x228c
	ds_read2_b32 v[46:47], v46 offset1:1
	s_waitcnt lgkmcnt(0)
	v_fmac_f32_e32 v166, v228, v46
	v_mov_b32_e32 v46, 0x2294
	v_fmac_f32_e32 v167, v228, v47
	ds_read2_b32 v[46:47], v46 offset1:1
	s_waitcnt lgkmcnt(0)
	v_pk_fma_f32 v[28:29], v[228:229], v[46:47], v[28:29] op_sel_hi:[0,1,1]
	v_mov_b32_e32 v46, 0x229c
	ds_read2_b32 v[46:47], v46 offset1:1
	s_waitcnt lgkmcnt(0)
	v_pk_fma_f32 v[26:27], v[228:229], v[46:47], v[26:27] op_sel_hi:[0,1,1]
	v_mov_b32_e32 v46, 0x22a4
	ds_read2_b32 v[46:47], v46 offset1:1
	s_waitcnt lgkmcnt(0)
	v_fmac_f32_e32 v164, v228, v46
	v_mov_b32_e32 v46, 0x22ac
	v_fmac_f32_e32 v165, v228, v47
	ds_read2_b32 v[46:47], v46 offset1:1
	s_waitcnt lgkmcnt(0)
	v_pk_fma_f32 v[32:33], v[228:229], v[46:47], v[32:33] op_sel_hi:[0,1,1]
	v_mov_b32_e32 v46, 0x22b4
	ds_read2_b32 v[46:47], v46 offset1:1
	s_waitcnt lgkmcnt(0)
	v_pk_fma_f32 v[30:31], v[228:229], v[46:47], v[30:31] op_sel_hi:[0,1,1]
	v_mov_b32_e32 v46, 0x22bc
	ds_read2_b32 v[46:47], v46 offset1:1
	s_waitcnt lgkmcnt(0)
	v_fmac_f32_e32 v158, v228, v46
	v_mov_b32_e32 v46, 0x22c4
	v_fmac_f32_e32 v159, v228, v47
	ds_read2_b32 v[46:47], v46 offset1:1
	s_waitcnt lgkmcnt(0)
	v_pk_fma_f32 v[34:35], v[228:229], v[46:47], v[34:35] op_sel_hi:[0,1,1]
	v_mov_b32_e32 v46, 0x22cc
	ds_read2_b32 v[46:47], v46 offset1:1
	s_waitcnt lgkmcnt(0)
	v_pk_fma_f32 v[36:37], v[228:229], v[46:47], v[36:37] op_sel_hi:[0,1,1]
	v_mov_b32_e32 v46, 0x22d4
	ds_read2_b32 v[46:47], v46 offset1:1
	s_waitcnt lgkmcnt(0)
	v_fmac_f32_e32 v152, v228, v46
	v_mov_b32_e32 v46, 0x22dc
	v_fmac_f32_e32 v153, v228, v47
	ds_read2_b32 v[46:47], v46 offset1:1
	s_waitcnt lgkmcnt(0)
	v_pk_fma_f32 v[40:41], v[228:229], v[46:47], v[40:41] op_sel_hi:[0,1,1]
	v_mov_b32_e32 v46, 0x22e4
	ds_read2_b32 v[46:47], v46 offset1:1
	s_waitcnt lgkmcnt(0)
	v_pk_fma_f32 v[46:47], v[228:229], v[46:47], v[38:39] op_sel_hi:[0,1,1]
	v_mov_b32_e32 v38, 0x22ec
	ds_read2_b32 v[38:39], v38 offset1:1
	s_waitcnt lgkmcnt(0)
	v_fmac_f32_e32 v148, v228, v38
	v_mov_b32_e32 v38, 0x22f4
	v_fmac_f32_e32 v149, v228, v39
	ds_read2_b32 v[38:39], v38 offset1:1
	s_waitcnt lgkmcnt(0)
	v_pk_fma_f32 v[44:45], v[228:229], v[38:39], v[44:45] op_sel_hi:[0,1,1]
	v_mov_b32_e32 v38, 0x22fc
	ds_read2_b32 v[38:39], v38 offset1:1
	s_waitcnt lgkmcnt(0)
	v_fmac_f32_e32 v0, v228, v38
	v_fma_f32 v38, v230, s4, -v124
	v_mul_f32_e32 v144, 0x3fb8aa3b, v38
	v_fma_f32 v145, v38, s5, -v144
	v_rndne_f32_e32 v146, v144
	v_fmac_f32_e32 v145, 0x32a5705f, v38
	v_sub_f32_e32 v144, v144, v146
	v_add_f32_e32 v144, v144, v145
	v_exp_f32_e32 v144, v144
	v_cvt_i32_f32_e32 v145, v146
	v_cmp_ngt_f32_e32 vcc, s6, v38
	v_ldexp_f32 v144, v144, v145
	s_nop 0
	v_cndmask_b32_e32 v144, 0, v144, vcc
	v_cmp_nlt_f32_e32 vcc, s7, v38
	v_mov_b32_e32 v38, 0x2354
	s_nop 0
	v_cndmask_b32_e32 v202, v103, v144, vcc
	v_fmac_f32_e32 v1, v202, v39
	ds_read2_b32 v[38:39], v38 offset1:1
	v_add_f32_e32 v2, v2, v202
	s_waitcnt lgkmcnt(0)
	v_pk_fma_f32 v[42:43], v[202:203], v[38:39], v[42:43] op_sel_hi:[0,1,1]
	v_mov_b32_e32 v38, 0x235c
	ds_read2_b32 v[38:39], v38 offset1:1
	s_waitcnt lgkmcnt(0)
	v_pk_fma_f32 v[144:145], v[202:203], v[38:39], v[24:25] op_sel_hi:[0,1,1]
	v_mov_b32_e32 v24, 0x2364
	ds_read2_b32 v[24:25], v24 offset1:1
	s_waitcnt lgkmcnt(0)
	v_pk_fma_f32 v[146:147], v[202:203], v[24:25], v[18:19] op_sel_hi:[0,1,1]
	v_mov_b32_e32 v18, 0x236c
	ds_read2_b32 v[18:19], v18 offset1:1
	v_mov_b32_e32 v24, 0x23e4
	ds_read2_b32 v[24:25], v24 offset1:1
	s_waitcnt lgkmcnt(1)
	v_pk_fma_f32 v[150:151], v[202:203], v[18:19], v[22:23] op_sel_hi:[0,1,1]
	v_mov_b32_e32 v18, 0x2374
	ds_read2_b32 v[18:19], v18 offset1:1
	v_mov_b32_e32 v22, 0x23b4
	ds_read2_b32 v[22:23], v22 offset1:1
	s_waitcnt lgkmcnt(2)
	v_pk_fma_f32 v[24:25], v[202:203], v[24:25], v[46:47] op_sel_hi:[0,1,1]
	v_pk_fma_f32 v[46:47], v[198:199], v[206:207], v[180:181] op_sel_hi:[0,1,1]
	s_waitcnt lgkmcnt(1)
	v_pk_fma_f32 v[154:155], v[202:203], v[18:19], v[20:21] op_sel_hi:[0,1,1]
	v_mov_b32_e32 v18, 0x237c
	ds_read2_b32 v[18:19], v18 offset1:1
	s_waitcnt lgkmcnt(1)
	v_pk_fma_f32 v[38:39], v[202:203], v[22:23], v[30:31] op_sel_hi:[0,1,1]
	v_mov_b32_e32 v22, 0x23bc
	ds_read2_b32 v[22:23], v22 offset1:1
	s_waitcnt lgkmcnt(1)
	v_pk_fma_f32 v[10:11], v[202:203], v[18:19], v[10:11] op_sel_hi:[0,1,1]
	v_mov_b32_e32 v18, 0x2384
	ds_read2_b32 v[18:19], v18 offset1:1
	s_waitcnt lgkmcnt(1)
	v_fmac_f32_e32 v158, v202, v22
	v_mov_b32_e32 v22, 0x23c4
	v_fmac_f32_e32 v159, v202, v23
	ds_read2_b32 v[22:23], v22 offset1:1
	s_waitcnt lgkmcnt(1)
	v_pk_fma_f32 v[156:157], v[202:203], v[18:19], v[8:9] op_sel_hi:[0,1,1]
	v_mov_b32_e32 v18, 0x239c
	ds_read2_b32 v[18:19], v18 offset1:1
	v_mov_b32_e32 v8, 0x238c
	ds_read2_b32 v[8:9], v8 offset1:1
	s_waitcnt lgkmcnt(2)
	v_pk_fma_f32 v[30:31], v[202:203], v[22:23], v[34:35] op_sel_hi:[0,1,1]
	v_mov_b32_e32 v22, 0x23cc
	s_waitcnt lgkmcnt(1)
	v_pk_fma_f32 v[20:21], v[202:203], v[18:19], v[26:27] op_sel_hi:[0,1,1]
	v_mov_b32_e32 v26, 0x23ec
	ds_read2_b32 v[26:27], v26 offset1:1
	s_waitcnt lgkmcnt(1)
	v_fmac_f32_e32 v166, v202, v8
	v_mov_b32_e32 v8, 0x2394
	v_fmac_f32_e32 v167, v202, v9
	ds_read2_b32 v[8:9], v8 offset1:1
	s_waitcnt lgkmcnt(1)
	v_fmac_f32_e32 v148, v202, v26
	v_mov_b32_e32 v26, 0x23f4
	v_fmac_f32_e32 v149, v202, v27
	ds_read2_b32 v[26:27], v26 offset1:1
	s_waitcnt lgkmcnt(1)
	v_pk_fma_f32 v[8:9], v[202:203], v[8:9], v[28:29] op_sel_hi:[0,1,1]
	v_mov_b32_e32 v18, 0x23a4
	ds_read2_b32 v[18:19], v18 offset1:1
	ds_read2_b32 v[22:23], v22 offset1:1
	s_waitcnt lgkmcnt(2)
	v_pk_fma_f32 v[194:195], v[202:203], v[26:27], v[44:45] op_sel_hi:[0,1,1]
	v_mov_b32_e32 v26, 0x23fc
	ds_read2_b32 v[26:27], v26 offset1:1
	s_waitcnt lgkmcnt(2)
	v_fmac_f32_e32 v164, v202, v18
	v_mov_b32_e32 v18, 0x23ac
	v_fmac_f32_e32 v165, v202, v19
	ds_read2_b32 v[18:19], v18 offset1:1
	s_waitcnt lgkmcnt(1)
	v_fmac_f32_e32 v0, v202, v26
	v_fma_f32 v26, v231, s4, -v124
	v_mul_f32_e32 v28, 0x3fb8aa3b, v26
	v_fma_f32 v29, v26, s5, -v28
	v_rndne_f32_e32 v34, v28
	v_fmac_f32_e32 v29, 0x32a5705f, v26
	v_sub_f32_e32 v28, v28, v34
	v_add_f32_e32 v28, v28, v29
	v_exp_f32_e32 v28, v28
	v_cvt_i32_f32_e32 v29, v34
	v_cmp_ngt_f32_e32 vcc, s6, v26
	s_waitcnt lgkmcnt(0)
	v_pk_fma_f32 v[18:19], v[202:203], v[18:19], v[32:33] op_sel_hi:[0,1,1]
	v_pk_fma_f32 v[32:33], v[202:203], v[22:23], v[36:37] op_sel_hi:[0,1,1]
	v_ldexp_f32 v28, v28, v29
	v_cndmask_b32_e32 v28, 0, v28, vcc
	v_cmp_nlt_f32_e32 vcc, s7, v26
	v_mov_b32_e32 v26, 0x2454
	v_mov_b32_e32 v22, 0x23d4
	v_cndmask_b32_e32 v196, v103, v28, vcc
	v_fmac_f32_e32 v1, v196, v27
	ds_read2_b32 v[26:27], v26 offset1:1
	v_add_f32_e32 v2, v2, v196
	v_pk_fma_f32 v[28:29], v[198:199], v[224:225], v[210:211] op_sel_hi:[0,1,1]
	ds_read2_b32 v[22:23], v22 offset1:1
	v_pk_fma_f32 v[36:37], v[198:199], v[220:221], v[188:189] op_sel_hi:[0,1,1]
	s_waitcnt lgkmcnt(1)
	v_pk_fma_f32 v[192:193], v[196:197], v[26:27], v[42:43] op_sel_hi:[0,1,1]
	v_mov_b32_e32 v26, 0x245c
	ds_read2_b32 v[26:27], v26 offset1:1
	s_waitcnt lgkmcnt(1)
	v_fmac_f32_e32 v152, v202, v22
	v_mov_b32_e32 v22, 0x23dc
	v_fmac_f32_e32 v153, v202, v23
	ds_read2_b32 v[22:23], v22 offset1:1
	s_waitcnt lgkmcnt(1)
	v_pk_fma_f32 v[190:191], v[196:197], v[26:27], v[144:145] op_sel_hi:[0,1,1]
	v_mov_b32_e32 v26, 0x2464
	ds_read2_b32 v[26:27], v26 offset1:1
	v_pk_fma_f32 v[42:43], v[198:199], v[216:217], v[184:185] op_sel_hi:[0,1,1]
	s_waitcnt lgkmcnt(1)
	v_pk_fma_f32 v[22:23], v[202:203], v[22:23], v[40:41] op_sel_hi:[0,1,1]
	s_waitcnt lgkmcnt(0)
	v_pk_fma_f32 v[176:177], v[196:197], v[26:27], v[146:147] op_sel_hi:[0,1,1]
	v_mov_b32_e32 v26, 0x246c
	ds_read2_b32 v[26:27], v26 offset1:1
	s_waitcnt lgkmcnt(0)
	v_pk_fma_f32 v[186:187], v[196:197], v[26:27], v[150:151] op_sel_hi:[0,1,1]
	v_mov_b32_e32 v26, 0x2474
	ds_read2_b32 v[26:27], v26 offset1:1
	s_waitcnt lgkmcnt(0)
	v_pk_fma_f32 v[174:175], v[196:197], v[26:27], v[154:155] op_sel_hi:[0,1,1]
	v_mov_b32_e32 v26, 0x247c
	ds_read2_b32 v[26:27], v26 offset1:1
	s_waitcnt lgkmcnt(0)
	v_pk_fma_f32 v[172:173], v[196:197], v[26:27], v[10:11] op_sel_hi:[0,1,1]
	v_mov_b32_e32 v10, 0x2484
	ds_read2_b32 v[10:11], v10 offset1:1
	s_waitcnt lgkmcnt(0)
	v_pk_fma_f32 v[162:163], v[196:197], v[10:11], v[156:157] op_sel_hi:[0,1,1]
	v_fma_f32 v10, v232, s4, -v124
	v_mul_f32_e32 v11, 0x3fb8aa3b, v10
	v_fma_f32 v26, v10, s5, -v11
	v_rndne_f32_e32 v27, v11
	v_fmac_f32_e32 v26, 0x32a5705f, v10
	v_sub_f32_e32 v11, v11, v27
	v_add_f32_e32 v11, v11, v26
	v_exp_f32_e32 v11, v11
	v_cvt_i32_f32_e32 v26, v27
	v_cmp_ngt_f32_e32 vcc, s6, v10
	v_ldexp_f32 v11, v11, v26
	s_nop 0
	v_cndmask_b32_e32 v11, 0, v11, vcc
	v_cmp_nlt_f32_e32 vcc, s7, v10
	v_fma_f32 v10, v117, s4, -v124
	s_nop 0
	v_cndmask_b32_e32 v160, v103, v11, vcc
	v_mul_f32_e32 v11, 0x3fb8aa3b, v10
	v_fma_f32 v26, v10, s5, -v11
	v_rndne_f32_e32 v27, v11
	v_fmac_f32_e32 v26, 0x32a5705f, v10
	v_sub_f32_e32 v11, v11, v27
	v_add_f32_e32 v11, v11, v26
	v_exp_f32_e32 v11, v11
	v_cvt_i32_f32_e32 v26, v27
	v_cmp_ngt_f32_e32 vcc, s6, v10
	v_add_f32_e32 v2, v2, v160
	v_ldexp_f32 v11, v11, v26
	v_cndmask_b32_e32 v11, 0, v11, vcc
	v_cmp_nlt_f32_e32 vcc, s7, v10
	v_fma_f32 v10, v119, s4, -v124
	v_mov_b32_e32 v119, 0x224c
	v_cndmask_b32_e32 v156, v103, v11, vcc
	v_mul_f32_e32 v11, 0x3fb8aa3b, v10
	v_fma_f32 v26, v10, s5, -v11
	v_rndne_f32_e32 v27, v11
	v_fmac_f32_e32 v26, 0x32a5705f, v10
	v_sub_f32_e32 v11, v11, v27
	v_add_f32_e32 v11, v11, v26
	v_exp_f32_e32 v11, v11
	v_cvt_i32_f32_e32 v26, v27
	v_cmp_ngt_f32_e32 vcc, s6, v10
	v_add_f32_e32 v2, v2, v156
	v_ldexp_f32 v11, v11, v26
	v_cndmask_b32_e32 v11, 0, v11, vcc
	v_cmp_nlt_f32_e32 vcc, s7, v10
	v_fma_f32 v10, v233, s4, -v124
	s_nop 0
	v_cndmask_b32_e32 v154, v103, v11, vcc
	v_mul_f32_e32 v11, 0x3fb8aa3b, v10
	v_fma_f32 v26, v10, s5, -v11
	v_rndne_f32_e32 v27, v11
	v_fmac_f32_e32 v26, 0x32a5705f, v10
	v_sub_f32_e32 v11, v11, v27
	v_add_f32_e32 v11, v11, v26
	v_exp_f32_e32 v11, v11
	v_cvt_i32_f32_e32 v26, v27
	v_cmp_ngt_f32_e32 vcc, s6, v10
	v_add_f32_e32 v2, v2, v154
	v_ldexp_f32 v11, v11, v26
	v_cndmask_b32_e32 v11, 0, v11, vcc
	v_cmp_nlt_f32_e32 vcc, s7, v10
	v_fma_f32 v10, v234, s4, -v124
	s_nop 0
	v_cndmask_b32_e32 v150, v103, v11, vcc
	v_mul_f32_e32 v11, 0x3fb8aa3b, v10
	v_fma_f32 v26, v10, s5, -v11
	v_rndne_f32_e32 v27, v11
	v_fmac_f32_e32 v26, 0x32a5705f, v10
	v_sub_f32_e32 v11, v11, v27
	v_add_f32_e32 v11, v11, v26
	v_exp_f32_e32 v11, v11
	v_cvt_i32_f32_e32 v26, v27
	v_cmp_ngt_f32_e32 vcc, s6, v10
	v_add_f32_e32 v2, v2, v150
	v_ldexp_f32 v11, v11, v26
	v_cndmask_b32_e32 v11, 0, v11, vcc
	v_cmp_nlt_f32_e32 vcc, s7, v10
	v_fma_f32 v10, v235, s4, -v124
	s_nop 0
	v_cndmask_b32_e32 v146, v103, v11, vcc
	v_mul_f32_e32 v11, 0x3fb8aa3b, v10
	v_fma_f32 v26, v10, s5, -v11
	v_rndne_f32_e32 v27, v11
	v_fmac_f32_e32 v26, 0x32a5705f, v10
	v_sub_f32_e32 v11, v11, v27
	v_add_f32_e32 v11, v11, v26
	v_exp_f32_e32 v11, v11
	v_cvt_i32_f32_e32 v26, v27
	v_cmp_ngt_f32_e32 vcc, s6, v10
	v_add_f32_e32 v2, v2, v146
	v_ldexp_f32 v11, v11, v26
	v_cndmask_b32_e32 v11, 0, v11, vcc
	v_cmp_nlt_f32_e32 vcc, s7, v10
	s_nop 1
	v_cndmask_b32_e32 v144, v103, v11, vcc
	v_add_f32_e32 v117, v2, v144
	v_fma_f32 v2, v125, s4, -v124
	v_mul_f32_e32 v10, 0x3fb8aa3b, v2
	v_fma_f32 v11, v2, s5, -v10
	v_rndne_f32_e32 v26, v10
	v_fmac_f32_e32 v11, 0x32a5705f, v2
	v_sub_f32_e32 v10, v10, v26
	v_add_f32_e32 v10, v10, v11
	v_exp_f32_e32 v10, v10
	v_cvt_i32_f32_e32 v11, v26
	v_mov_b32_e32 v26, 0x220c
	ds_read2_b32 v[26:27], v26 offset1:1
	v_cmp_ngt_f32_e32 vcc, s6, v2
	v_ldexp_f32 v10, v10, v11
	s_nop 0
	v_cndmask_b32_e32 v10, 0, v10, vcc
	v_cmp_nlt_f32_e32 vcc, s7, v2
	s_nop 1
	v_cndmask_b32_e32 v2, v103, v10, vcc
	v_pk_fma_f32 v[10:11], v[198:199], v[226:227], v[212:213] op_sel_hi:[0,1,1]
	s_waitcnt lgkmcnt(0)
	v_pk_fma_f32 v[10:11], v[228:229], v[26:27], v[10:11] op_sel_hi:[0,1,1]
	v_mov_b32_e32 v26, 0x230c
	ds_read2_b32 v[26:27], v26 offset1:1
	s_waitcnt lgkmcnt(0)
	v_pk_fma_f32 v[10:11], v[202:203], v[26:27], v[10:11] op_sel_hi:[0,1,1]
	v_mov_b32_e32 v26, 0x240c
	ds_read2_b32 v[26:27], v26 offset1:1
	s_waitcnt lgkmcnt(0)
	v_pk_fma_f32 v[26:27], v[196:197], v[26:27], v[10:11] op_sel_hi:[0,1,1]
	v_mov_b32_e32 v10, 0x248c
	ds_read2_b32 v[10:11], v10 offset1:1
	s_waitcnt lgkmcnt(0)
	v_fmac_f32_e32 v166, v196, v10
	v_mov_b32_e32 v10, 0x2204
	ds_read2_b32 v[34:35], v10 offset1:1
	v_mov_b32_e32 v10, 0x2304
	v_fmac_f32_e32 v167, v196, v11
	s_waitcnt lgkmcnt(0)
	v_pk_fma_f32 v[28:29], v[228:229], v[34:35], v[28:29] op_sel_hi:[0,1,1]
	ds_read2_b32 v[34:35], v10 offset1:1
	v_mov_b32_e32 v10, 0x2404
	s_waitcnt lgkmcnt(0)
	v_pk_fma_f32 v[28:29], v[202:203], v[34:35], v[28:29] op_sel_hi:[0,1,1]
	ds_read2_b32 v[34:35], v10 offset1:1
	v_mov_b32_e32 v10, 0x2494
	ds_read2_b32 v[10:11], v10 offset1:1
	s_waitcnt lgkmcnt(1)
	v_pk_fma_f32 v[28:29], v[196:197], v[34:35], v[28:29] op_sel_hi:[0,1,1]
	v_mov_b32_e32 v34, 0x221c
	s_waitcnt lgkmcnt(0)
	v_pk_fma_f32 v[10:11], v[196:197], v[10:11], v[8:9] op_sel_hi:[0,1,1]
	v_mov_b32_e32 v8, 0x249c
	ds_read2_b32 v[8:9], v8 offset1:1
	ds_read2_b32 v[34:35], v34 offset1:1
	s_waitcnt lgkmcnt(1)
	v_pk_fma_f32 v[8:9], v[196:197], v[8:9], v[20:21] op_sel_hi:[0,1,1]
	v_pk_fma_f32 v[20:21], v[198:199], v[222:223], v[208:209] op_sel_hi:[0,1,1]
	s_waitcnt lgkmcnt(0)
	v_pk_fma_f32 v[20:21], v[228:229], v[34:35], v[20:21] op_sel_hi:[0,1,1]
	v_mov_b32_e32 v34, 0x231c
	ds_read2_b32 v[34:35], v34 offset1:1
	s_waitcnt lgkmcnt(0)
	v_pk_fma_f32 v[20:21], v[202:203], v[34:35], v[20:21] op_sel_hi:[0,1,1]
	v_mov_b32_e32 v34, 0x241c
	ds_read2_b32 v[34:35], v34 offset1:1
	s_waitcnt lgkmcnt(0)
	v_pk_fma_f32 v[34:35], v[196:197], v[34:35], v[20:21] op_sel_hi:[0,1,1]
	v_mov_b32_e32 v20, 0x24a4
	ds_read2_b32 v[20:21], v20 offset1:1
	s_waitcnt lgkmcnt(0)
	v_fmac_f32_e32 v164, v196, v20
	v_mov_b32_e32 v20, 0x2214
	ds_read2_b32 v[40:41], v20 offset1:1
	v_mov_b32_e32 v20, 0x2314
	v_fmac_f32_e32 v165, v196, v21
	s_waitcnt lgkmcnt(0)
	v_pk_fma_f32 v[36:37], v[228:229], v[40:41], v[36:37] op_sel_hi:[0,1,1]
	ds_read2_b32 v[40:41], v20 offset1:1
	v_mov_b32_e32 v20, 0x2414
	s_waitcnt lgkmcnt(0)
	v_pk_fma_f32 v[36:37], v[202:203], v[40:41], v[36:37] op_sel_hi:[0,1,1]
	ds_read2_b32 v[40:41], v20 offset1:1
	v_mov_b32_e32 v20, 0x24ac
	ds_read2_b32 v[20:21], v20 offset1:1
	s_waitcnt lgkmcnt(1)
	v_pk_fma_f32 v[36:37], v[196:197], v[40:41], v[36:37] op_sel_hi:[0,1,1]
	v_mov_b32_e32 v40, 0x222c
	s_waitcnt lgkmcnt(0)
	v_pk_fma_f32 v[20:21], v[196:197], v[20:21], v[18:19] op_sel_hi:[0,1,1]
	v_mov_b32_e32 v18, 0x24b4
	ds_read2_b32 v[18:19], v18 offset1:1
	ds_read2_b32 v[40:41], v40 offset1:1
	s_waitcnt lgkmcnt(1)
	v_pk_fma_f32 v[18:19], v[196:197], v[18:19], v[38:39] op_sel_hi:[0,1,1]
	v_pk_fma_f32 v[38:39], v[198:199], v[218:219], v[182:183] op_sel_hi:[0,1,1]
	s_waitcnt lgkmcnt(0)
	v_pk_fma_f32 v[38:39], v[228:229], v[40:41], v[38:39] op_sel_hi:[0,1,1]
	v_mov_b32_e32 v40, 0x232c
	ds_read2_b32 v[40:41], v40 offset1:1
	s_waitcnt lgkmcnt(0)
	v_pk_fma_f32 v[38:39], v[202:203], v[40:41], v[38:39] op_sel_hi:[0,1,1]
	v_mov_b32_e32 v40, 0x242c
	ds_read2_b32 v[40:41], v40 offset1:1
	s_waitcnt lgkmcnt(0)
	v_pk_fma_f32 v[40:41], v[196:197], v[40:41], v[38:39] op_sel_hi:[0,1,1]
	v_mov_b32_e32 v38, 0x24bc
	ds_read2_b32 v[38:39], v38 offset1:1
	s_waitcnt lgkmcnt(0)
	v_fmac_f32_e32 v158, v196, v38
	v_mov_b32_e32 v38, 0x2224
	ds_read2_b32 v[44:45], v38 offset1:1
	v_mov_b32_e32 v38, 0x2324
	v_fmac_f32_e32 v159, v196, v39
	s_waitcnt lgkmcnt(0)
	v_pk_fma_f32 v[42:43], v[228:229], v[44:45], v[42:43] op_sel_hi:[0,1,1]
	ds_read2_b32 v[44:45], v38 offset1:1
	v_mov_b32_e32 v38, 0x2424
	s_waitcnt lgkmcnt(0)
	v_pk_fma_f32 v[42:43], v[202:203], v[44:45], v[42:43] op_sel_hi:[0,1,1]
	ds_read2_b32 v[44:45], v38 offset1:1
	v_mov_b32_e32 v38, 0x24c4
	ds_read2_b32 v[38:39], v38 offset1:1
	s_waitcnt lgkmcnt(1)
	v_pk_fma_f32 v[42:43], v[196:197], v[44:45], v[42:43] op_sel_hi:[0,1,1]
	v_mov_b32_e32 v44, 0x223c
	s_waitcnt lgkmcnt(0)
	v_pk_fma_f32 v[30:31], v[196:197], v[38:39], v[30:31] op_sel_hi:[0,1,1]
	v_mov_b32_e32 v38, 0x24cc
	ds_read2_b32 v[38:39], v38 offset1:1
	ds_read2_b32 v[44:45], v44 offset1:1
	s_waitcnt lgkmcnt(1)
	v_pk_fma_f32 v[32:33], v[196:197], v[38:39], v[32:33] op_sel_hi:[0,1,1]
	v_pk_fma_f32 v[38:39], v[198:199], v[214:215], v[178:179] op_sel_hi:[0,1,1]
	s_waitcnt lgkmcnt(0)
	v_pk_fma_f32 v[38:39], v[228:229], v[44:45], v[38:39] op_sel_hi:[0,1,1]
	v_mov_b32_e32 v44, 0x233c
	ds_read2_b32 v[44:45], v44 offset1:1
	s_waitcnt lgkmcnt(0)
	v_pk_fma_f32 v[38:39], v[202:203], v[44:45], v[38:39] op_sel_hi:[0,1,1]
	v_mov_b32_e32 v44, 0x243c
	ds_read2_b32 v[44:45], v44 offset1:1
	s_waitcnt lgkmcnt(0)
	v_pk_fma_f32 v[44:45], v[196:197], v[44:45], v[38:39] op_sel_hi:[0,1,1]
	v_mov_b32_e32 v38, 0x24d4
	ds_read2_b32 v[38:39], v38 offset1:1
	s_waitcnt lgkmcnt(0)
	v_fmac_f32_e32 v152, v196, v38
	v_mov_b32_e32 v38, 0x2234
	ds_read2_b32 v[178:179], v38 offset1:1
	v_mov_b32_e32 v38, 0x2334
	v_fmac_f32_e32 v153, v196, v39
	s_waitcnt lgkmcnt(0)
	v_pk_fma_f32 v[46:47], v[228:229], v[178:179], v[46:47] op_sel_hi:[0,1,1]
	ds_read2_b32 v[178:179], v38 offset1:1
	v_mov_b32_e32 v38, 0x2434
	s_waitcnt lgkmcnt(0)
	v_pk_fma_f32 v[46:47], v[202:203], v[178:179], v[46:47] op_sel_hi:[0,1,1]
	ds_read2_b32 v[178:179], v38 offset1:1
	v_mov_b32_e32 v38, 0x24dc
	ds_read2_b32 v[38:39], v38 offset1:1
	s_waitcnt lgkmcnt(1)
	v_pk_fma_f32 v[46:47], v[196:197], v[178:179], v[46:47] op_sel_hi:[0,1,1]
	s_waitcnt lgkmcnt(0)
	v_pk_fma_f32 v[38:39], v[196:197], v[38:39], v[22:23] op_sel_hi:[0,1,1]
	v_mov_b32_e32 v22, 0x24e4
	ds_read2_b32 v[22:23], v22 offset1:1
	s_waitcnt lgkmcnt(0)
	v_pk_fma_f32 v[22:23], v[196:197], v[22:23], v[24:25] op_sel_hi:[0,1,1]
	v_pk_fma_f32 v[24:25], v[198:199], v[204:205], v[168:169] op_sel_hi:[0,1,1]
	ds_read2_b32 v[168:169], v119 offset1:1
	v_mov_b32_e32 v119, 0x234c
	s_waitcnt lgkmcnt(0)
	v_pk_fma_f32 v[24:25], v[228:229], v[168:169], v[24:25] op_sel_hi:[0,1,1]
	ds_read2_b32 v[168:169], v119 offset1:1
	v_mov_b32_e32 v119, 0x244c
	s_waitcnt lgkmcnt(0)
	v_pk_fma_f32 v[24:25], v[202:203], v[168:169], v[24:25] op_sel_hi:[0,1,1]
	ds_read2_b32 v[168:169], v119 offset1:1
	v_mov_b32_e32 v119, 0x24ec
	s_waitcnt lgkmcnt(0)
	v_pk_fma_f32 v[24:25], v[196:197], v[168:169], v[24:25] op_sel_hi:[0,1,1]
	ds_read2_b32 v[168:169], v119 offset1:1
	v_mov_b32_e32 v119, 0x2244
	ds_read2_b32 v[178:179], v119 offset1:1
	v_mov_b32_e32 v119, 0x2344
	s_waitcnt lgkmcnt(1)
	v_fmac_f32_e32 v148, v196, v168
	v_fmac_f32_e32 v149, v196, v169
	s_waitcnt lgkmcnt(0)
	v_pk_fma_f32 v[170:171], v[228:229], v[178:179], v[170:171] op_sel_hi:[0,1,1]
	ds_read2_b32 v[178:179], v119 offset1:1
	v_mov_b32_e32 v119, 0x2444
	s_waitcnt lgkmcnt(0)
	v_pk_fma_f32 v[170:171], v[202:203], v[178:179], v[170:171] op_sel_hi:[0,1,1]
	ds_read2_b32 v[178:179], v119 offset1:1
	v_mov_b32_e32 v119, 0x24f4
	ds_read2_b32 v[168:169], v119 offset1:1
	v_mov_b32_e32 v119, 0x24fc
	s_waitcnt lgkmcnt(1)
	v_pk_fma_f32 v[170:171], v[196:197], v[178:179], v[170:171] op_sel_hi:[0,1,1]
	ds_read2_b32 v[178:179], v119 offset1:1
	v_mov_b32_e32 v119, 0x2504
	s_waitcnt lgkmcnt(1)
	v_pk_fma_f32 v[168:169], v[196:197], v[168:169], v[194:195] op_sel_hi:[0,1,1]
	s_waitcnt lgkmcnt(0)
	v_fmac_f32_e32 v0, v196, v178
	v_fmac_f32_e32 v1, v160, v179
	ds_read2_b32 v[178:179], v119 offset1:1
	v_mov_b32_e32 v119, 0x250c
	s_waitcnt lgkmcnt(0)
	v_pk_fma_f32 v[28:29], v[160:161], v[178:179], v[28:29] op_sel_hi:[0,1,1]
	ds_read2_b32 v[178:179], v119 offset1:1
	v_mov_b32_e32 v119, 0x2514
	s_waitcnt lgkmcnt(0)
	v_pk_fma_f32 v[26:27], v[160:161], v[178:179], v[26:27] op_sel_hi:[0,1,1]
	ds_read2_b32 v[178:179], v119 offset1:1
	v_mov_b32_e32 v119, 0x251c
	s_waitcnt lgkmcnt(0)
	v_pk_fma_f32 v[36:37], v[160:161], v[178:179], v[36:37] op_sel_hi:[0,1,1]
	ds_read2_b32 v[178:179], v119 offset1:1
	v_mov_b32_e32 v119, 0x2524
	s_waitcnt lgkmcnt(0)
	v_pk_fma_f32 v[34:35], v[160:161], v[178:179], v[34:35] op_sel_hi:[0,1,1]
	ds_read2_b32 v[178:179], v119 offset1:1
	v_mov_b32_e32 v119, 0x252c
	s_waitcnt lgkmcnt(0)
	v_pk_fma_f32 v[42:43], v[160:161], v[178:179], v[42:43] op_sel_hi:[0,1,1]
	ds_read2_b32 v[178:179], v119 offset1:1
	v_mov_b32_e32 v119, 0x2534
	s_waitcnt lgkmcnt(0)
	v_pk_fma_f32 v[40:41], v[160:161], v[178:179], v[40:41] op_sel_hi:[0,1,1]
	ds_read2_b32 v[178:179], v119 offset1:1
	v_mov_b32_e32 v119, 0x253c
	s_waitcnt lgkmcnt(0)
	v_pk_fma_f32 v[46:47], v[160:161], v[178:179], v[46:47] op_sel_hi:[0,1,1]
	ds_read2_b32 v[178:179], v119 offset1:1
	v_mov_b32_e32 v119, 0x2544
	s_waitcnt lgkmcnt(0)
	v_pk_fma_f32 v[44:45], v[160:161], v[178:179], v[44:45] op_sel_hi:[0,1,1]
	ds_read2_b32 v[178:179], v119 offset1:1
	v_mov_b32_e32 v119, 0x254c
	s_waitcnt lgkmcnt(0)
	v_pk_fma_f32 v[170:171], v[160:161], v[178:179], v[170:171] op_sel_hi:[0,1,1]
	ds_read2_b32 v[178:179], v119 offset1:1
	v_mov_b32_e32 v119, 0x2554
	s_waitcnt lgkmcnt(0)
	v_pk_fma_f32 v[24:25], v[160:161], v[178:179], v[24:25] op_sel_hi:[0,1,1]
	ds_read2_b32 v[178:179], v119 offset1:1
	v_mov_b32_e32 v119, 0x255c
	ds_read2_b32 v[180:181], v119 offset1:1
	v_mov_b32_e32 v119, 0x2564
	ds_read2_b32 v[182:183], v119 offset1:1
	v_mov_b32_e32 v119, 0x256c
	s_waitcnt lgkmcnt(2)
	v_pk_fma_f32 v[178:179], v[160:161], v[178:179], v[192:193] op_sel_hi:[0,1,1]
	s_waitcnt lgkmcnt(1)
	v_pk_fma_f32 v[180:181], v[160:161], v[180:181], v[190:191] op_sel_hi:[0,1,1]
	s_waitcnt lgkmcnt(0)
	v_pk_fma_f32 v[176:177], v[160:161], v[182:183], v[176:177] op_sel_hi:[0,1,1]
	ds_read2_b32 v[182:183], v119 offset1:1
	v_mov_b32_e32 v119, 0x2574
	ds_read2_b32 v[184:185], v119 offset1:1
	v_mov_b32_e32 v119, 0x257c
	s_waitcnt lgkmcnt(1)
	v_pk_fma_f32 v[182:183], v[160:161], v[182:183], v[186:187] op_sel_hi:[0,1,1]
	s_waitcnt lgkmcnt(0)
	v_pk_fma_f32 v[174:175], v[160:161], v[184:185], v[174:175] op_sel_hi:[0,1,1]
	ds_read2_b32 v[184:185], v119 offset1:1
	v_mov_b32_e32 v119, 0x2584
	s_waitcnt lgkmcnt(0)
	v_pk_fma_f32 v[172:173], v[160:161], v[184:185], v[172:173] op_sel_hi:[0,1,1]
	ds_read2_b32 v[184:185], v119 offset1:1
	v_mov_b32_e32 v119, 0x258c
	s_waitcnt lgkmcnt(0)
	v_pk_fma_f32 v[162:163], v[160:161], v[184:185], v[162:163] op_sel_hi:[0,1,1]
	ds_read2_b32 v[184:185], v119 offset1:1
	v_mov_b32_e32 v119, 0x2594
	s_waitcnt lgkmcnt(0)
	v_pk_fma_f32 v[166:167], v[160:161], v[184:185], v[166:167] op_sel_hi:[0,1,1]
	ds_read2_b32 v[184:185], v119 offset1:1
	v_mov_b32_e32 v119, 0x259c
	s_waitcnt lgkmcnt(0)
	v_pk_fma_f32 v[10:11], v[160:161], v[184:185], v[10:11] op_sel_hi:[0,1,1]
	ds_read2_b32 v[184:185], v119 offset1:1
	v_mov_b32_e32 v119, 0x25a4
	s_waitcnt lgkmcnt(0)
	v_pk_fma_f32 v[8:9], v[160:161], v[184:185], v[8:9] op_sel_hi:[0,1,1]
	ds_read2_b32 v[184:185], v119 offset1:1
	v_mov_b32_e32 v119, 0x25ac
	s_waitcnt lgkmcnt(0)
	v_pk_fma_f32 v[164:165], v[160:161], v[184:185], v[164:165] op_sel_hi:[0,1,1]
	ds_read2_b32 v[184:185], v119 offset1:1
	v_mov_b32_e32 v119, 0x25b4
	s_waitcnt lgkmcnt(0)
	v_pk_fma_f32 v[20:21], v[160:161], v[184:185], v[20:21] op_sel_hi:[0,1,1]
	ds_read2_b32 v[184:185], v119 offset1:1
	v_mov_b32_e32 v119, 0x25bc
	s_waitcnt lgkmcnt(0)
	v_pk_fma_f32 v[18:19], v[160:161], v[184:185], v[18:19] op_sel_hi:[0,1,1]
	ds_read2_b32 v[184:185], v119 offset1:1
	v_mov_b32_e32 v119, 0x25c4
	s_waitcnt lgkmcnt(0)
	v_pk_fma_f32 v[158:159], v[160:161], v[184:185], v[158:159] op_sel_hi:[0,1,1]
	ds_read2_b32 v[184:185], v119 offset1:1
	v_mov_b32_e32 v119, 0x25cc
	s_waitcnt lgkmcnt(0)
	v_pk_fma_f32 v[30:31], v[160:161], v[184:185], v[30:31] op_sel_hi:[0,1,1]
	ds_read2_b32 v[184:185], v119 offset1:1
	v_mov_b32_e32 v119, 0x25d4
	s_waitcnt lgkmcnt(0)
	v_pk_fma_f32 v[32:33], v[160:161], v[184:185], v[32:33] op_sel_hi:[0,1,1]
	ds_read2_b32 v[184:185], v119 offset1:1
	v_mov_b32_e32 v119, 0x25dc
	s_waitcnt lgkmcnt(0)
	v_pk_fma_f32 v[152:153], v[160:161], v[184:185], v[152:153] op_sel_hi:[0,1,1]
	ds_read2_b32 v[184:185], v119 offset1:1
	v_mov_b32_e32 v119, 0x25e4
	s_waitcnt lgkmcnt(0)
	v_pk_fma_f32 v[38:39], v[160:161], v[184:185], v[38:39] op_sel_hi:[0,1,1]
	ds_read2_b32 v[184:185], v119 offset1:1
	v_mov_b32_e32 v119, 0x25ec
	s_waitcnt lgkmcnt(0)
	v_pk_fma_f32 v[22:23], v[160:161], v[184:185], v[22:23] op_sel_hi:[0,1,1]
	ds_read2_b32 v[184:185], v119 offset1:1
	v_mov_b32_e32 v119, 0x25f4
	s_waitcnt lgkmcnt(0)
	v_pk_fma_f32 v[148:149], v[160:161], v[184:185], v[148:149] op_sel_hi:[0,1,1]
	ds_read2_b32 v[184:185], v119 offset1:1
	v_mov_b32_e32 v119, 0x25fc
	s_waitcnt lgkmcnt(0)
	v_pk_fma_f32 v[168:169], v[160:161], v[184:185], v[168:169] op_sel_hi:[0,1,1]
	ds_read2_b32 v[184:185], v119 offset1:1
	v_mov_b32_e32 v119, 0x2604
	s_waitcnt lgkmcnt(0)
	v_fmac_f32_e32 v0, v160, v184
	ds_read2_b32 v[160:161], v119 offset1:1
	v_mov_b32_e32 v119, 0x260c
	v_fmac_f32_e32 v1, v156, v185
	s_waitcnt lgkmcnt(0)
	v_pk_fma_f32 v[28:29], v[156:157], v[160:161], v[28:29] op_sel_hi:[0,1,1]
	ds_read2_b32 v[160:161], v119 offset1:1
	v_mov_b32_e32 v119, 0x2614
	s_waitcnt lgkmcnt(0)
	v_pk_fma_f32 v[26:27], v[156:157], v[160:161], v[26:27] op_sel_hi:[0,1,1]
	ds_read2_b32 v[160:161], v119 offset1:1
	v_mov_b32_e32 v119, 0x261c
	s_waitcnt lgkmcnt(0)
	v_pk_fma_f32 v[36:37], v[156:157], v[160:161], v[36:37] op_sel_hi:[0,1,1]
	ds_read2_b32 v[160:161], v119 offset1:1
	v_mov_b32_e32 v119, 0x2624
	s_waitcnt lgkmcnt(0)
	v_pk_fma_f32 v[34:35], v[156:157], v[160:161], v[34:35] op_sel_hi:[0,1,1]
	ds_read2_b32 v[160:161], v119 offset1:1
	v_mov_b32_e32 v119, 0x262c
	s_waitcnt lgkmcnt(0)
	v_pk_fma_f32 v[42:43], v[156:157], v[160:161], v[42:43] op_sel_hi:[0,1,1]
	ds_read2_b32 v[160:161], v119 offset1:1
	v_mov_b32_e32 v119, 0x2634
	s_waitcnt lgkmcnt(0)
	v_pk_fma_f32 v[40:41], v[156:157], v[160:161], v[40:41] op_sel_hi:[0,1,1]
	ds_read2_b32 v[160:161], v119 offset1:1
	v_mov_b32_e32 v119, 0x263c
	s_waitcnt lgkmcnt(0)
	v_pk_fma_f32 v[46:47], v[156:157], v[160:161], v[46:47] op_sel_hi:[0,1,1]
	ds_read2_b32 v[160:161], v119 offset1:1
	v_mov_b32_e32 v119, 0x2644
	s_waitcnt lgkmcnt(0)
	v_pk_fma_f32 v[44:45], v[156:157], v[160:161], v[44:45] op_sel_hi:[0,1,1]
	ds_read2_b32 v[160:161], v119 offset1:1
	v_mov_b32_e32 v119, 0x264c
	s_waitcnt lgkmcnt(0)
	v_pk_fma_f32 v[160:161], v[156:157], v[160:161], v[170:171] op_sel_hi:[0,1,1]
	ds_read2_b32 v[170:171], v119 offset1:1
	v_mov_b32_e32 v119, 0x2654
	s_waitcnt lgkmcnt(0)
	v_pk_fma_f32 v[24:25], v[156:157], v[170:171], v[24:25] op_sel_hi:[0,1,1]
	ds_read2_b32 v[170:171], v119 offset1:1
	v_mov_b32_e32 v119, 0x265c
	s_waitcnt lgkmcnt(0)
	v_pk_fma_f32 v[170:171], v[156:157], v[170:171], v[178:179] op_sel_hi:[0,1,1]
	ds_read2_b32 v[178:179], v119 offset1:1
	v_mov_b32_e32 v119, 0x2664
	s_waitcnt lgkmcnt(0)
	v_pk_fma_f32 v[178:179], v[156:157], v[178:179], v[180:181] op_sel_hi:[0,1,1]
	ds_read2_b32 v[180:181], v119 offset1:1
	v_mov_b32_e32 v119, 0x266c
	s_waitcnt lgkmcnt(0)
	v_pk_fma_f32 v[176:177], v[156:157], v[180:181], v[176:177] op_sel_hi:[0,1,1]
	ds_read2_b32 v[180:181], v119 offset1:1
	v_mov_b32_e32 v119, 0x2674
	s_waitcnt lgkmcnt(0)
	v_pk_fma_f32 v[180:181], v[156:157], v[180:181], v[182:183] op_sel_hi:[0,1,1]
	ds_read2_b32 v[182:183], v119 offset1:1
	v_mov_b32_e32 v119, 0x267c
	s_waitcnt lgkmcnt(0)
	v_pk_fma_f32 v[174:175], v[156:157], v[182:183], v[174:175] op_sel_hi:[0,1,1]
	ds_read2_b32 v[182:183], v119 offset1:1
	v_mov_b32_e32 v119, 0x2684
	s_waitcnt lgkmcnt(0)
	v_pk_fma_f32 v[172:173], v[156:157], v[182:183], v[172:173] op_sel_hi:[0,1,1]
	ds_read2_b32 v[182:183], v119 offset1:1
	v_mov_b32_e32 v119, 0x268c
	s_waitcnt lgkmcnt(0)
	v_pk_fma_f32 v[162:163], v[156:157], v[182:183], v[162:163] op_sel_hi:[0,1,1]
	ds_read2_b32 v[182:183], v119 offset1:1
	v_mov_b32_e32 v119, 0x2694
	s_waitcnt lgkmcnt(0)
	v_pk_fma_f32 v[166:167], v[156:157], v[182:183], v[166:167] op_sel_hi:[0,1,1]
	ds_read2_b32 v[182:183], v119 offset1:1
	v_mov_b32_e32 v119, 0x269c
	s_waitcnt lgkmcnt(0)
	v_pk_fma_f32 v[10:11], v[156:157], v[182:183], v[10:11] op_sel_hi:[0,1,1]
	ds_read2_b32 v[182:183], v119 offset1:1
	v_mov_b32_e32 v119, 0x26a4
	s_waitcnt lgkmcnt(0)
	v_pk_fma_f32 v[8:9], v[156:157], v[182:183], v[8:9] op_sel_hi:[0,1,1]
	ds_read2_b32 v[182:183], v119 offset1:1
	v_mov_b32_e32 v119, 0x26ac
	s_waitcnt lgkmcnt(0)
	v_pk_fma_f32 v[164:165], v[156:157], v[182:183], v[164:165] op_sel_hi:[0,1,1]
	ds_read2_b32 v[182:183], v119 offset1:1
	v_mov_b32_e32 v119, 0x26b4
	s_waitcnt lgkmcnt(0)
	v_pk_fma_f32 v[20:21], v[156:157], v[182:183], v[20:21] op_sel_hi:[0,1,1]
	ds_read2_b32 v[182:183], v119 offset1:1
	v_mov_b32_e32 v119, 0x26bc
	s_waitcnt lgkmcnt(0)
	v_pk_fma_f32 v[18:19], v[156:157], v[182:183], v[18:19] op_sel_hi:[0,1,1]
	ds_read2_b32 v[182:183], v119 offset1:1
	v_mov_b32_e32 v119, 0x26c4
	s_waitcnt lgkmcnt(0)
	v_pk_fma_f32 v[158:159], v[156:157], v[182:183], v[158:159] op_sel_hi:[0,1,1]
	ds_read2_b32 v[182:183], v119 offset1:1
	v_mov_b32_e32 v119, 0x26cc
	s_waitcnt lgkmcnt(0)
	v_pk_fma_f32 v[30:31], v[156:157], v[182:183], v[30:31] op_sel_hi:[0,1,1]
	ds_read2_b32 v[182:183], v119 offset1:1
	v_mov_b32_e32 v119, 0x26d4
	s_waitcnt lgkmcnt(0)
	v_pk_fma_f32 v[32:33], v[156:157], v[182:183], v[32:33] op_sel_hi:[0,1,1]
	ds_read2_b32 v[182:183], v119 offset1:1
	v_mov_b32_e32 v119, 0x26dc
	s_waitcnt lgkmcnt(0)
	v_pk_fma_f32 v[152:153], v[156:157], v[182:183], v[152:153] op_sel_hi:[0,1,1]
	ds_read2_b32 v[182:183], v119 offset1:1
	v_mov_b32_e32 v119, 0x26e4
	s_waitcnt lgkmcnt(0)
	v_pk_fma_f32 v[38:39], v[156:157], v[182:183], v[38:39] op_sel_hi:[0,1,1]
	ds_read2_b32 v[182:183], v119 offset1:1
	v_mov_b32_e32 v119, 0x26ec
	s_waitcnt lgkmcnt(0)
	v_pk_fma_f32 v[22:23], v[156:157], v[182:183], v[22:23] op_sel_hi:[0,1,1]
	ds_read2_b32 v[182:183], v119 offset1:1
	v_mov_b32_e32 v119, 0x26f4
	s_waitcnt lgkmcnt(0)
	v_pk_fma_f32 v[148:149], v[156:157], v[182:183], v[148:149] op_sel_hi:[0,1,1]
	ds_read2_b32 v[182:183], v119 offset1:1
	v_mov_b32_e32 v119, 0x26fc
	s_waitcnt lgkmcnt(0)
	v_pk_fma_f32 v[168:169], v[156:157], v[182:183], v[168:169] op_sel_hi:[0,1,1]
	ds_read2_b32 v[182:183], v119 offset1:1
	v_mov_b32_e32 v119, 0x2704
	s_waitcnt lgkmcnt(0)
	v_fmac_f32_e32 v0, v156, v182
	ds_read2_b32 v[156:157], v119 offset1:1
	v_mov_b32_e32 v119, 0x270c
	v_fmac_f32_e32 v1, v154, v183
	s_waitcnt lgkmcnt(0)
	v_pk_fma_f32 v[28:29], v[154:155], v[156:157], v[28:29] op_sel_hi:[0,1,1]
	ds_read2_b32 v[156:157], v119 offset1:1
	v_mov_b32_e32 v119, 0x2714
	s_waitcnt lgkmcnt(0)
	v_pk_fma_f32 v[26:27], v[154:155], v[156:157], v[26:27] op_sel_hi:[0,1,1]
	ds_read2_b32 v[156:157], v119 offset1:1
	v_mov_b32_e32 v119, 0x271c
	s_waitcnt lgkmcnt(0)
	v_pk_fma_f32 v[36:37], v[154:155], v[156:157], v[36:37] op_sel_hi:[0,1,1]
	ds_read2_b32 v[156:157], v119 offset1:1
	v_mov_b32_e32 v119, 0x2724
	s_waitcnt lgkmcnt(0)
	v_pk_fma_f32 v[34:35], v[154:155], v[156:157], v[34:35] op_sel_hi:[0,1,1]
	ds_read2_b32 v[156:157], v119 offset1:1
	v_mov_b32_e32 v119, 0x272c
	s_waitcnt lgkmcnt(0)
	v_pk_fma_f32 v[42:43], v[154:155], v[156:157], v[42:43] op_sel_hi:[0,1,1]
	ds_read2_b32 v[156:157], v119 offset1:1
	v_mov_b32_e32 v119, 0x2734
	s_waitcnt lgkmcnt(0)
	v_pk_fma_f32 v[40:41], v[154:155], v[156:157], v[40:41] op_sel_hi:[0,1,1]
	ds_read2_b32 v[156:157], v119 offset1:1
	v_mov_b32_e32 v119, 0x273c
	s_waitcnt lgkmcnt(0)
	v_pk_fma_f32 v[46:47], v[154:155], v[156:157], v[46:47] op_sel_hi:[0,1,1]
	ds_read2_b32 v[156:157], v119 offset1:1
	v_mov_b32_e32 v119, 0x2744
	s_waitcnt lgkmcnt(0)
	v_pk_fma_f32 v[44:45], v[154:155], v[156:157], v[44:45] op_sel_hi:[0,1,1]
	ds_read2_b32 v[156:157], v119 offset1:1
	v_mov_b32_e32 v119, 0x274c
	s_waitcnt lgkmcnt(0)
	v_pk_fma_f32 v[156:157], v[154:155], v[156:157], v[160:161] op_sel_hi:[0,1,1]
	ds_read2_b32 v[160:161], v119 offset1:1
	v_mov_b32_e32 v119, 0x2754
	s_waitcnt lgkmcnt(0)
	v_pk_fma_f32 v[24:25], v[154:155], v[160:161], v[24:25] op_sel_hi:[0,1,1]
	ds_read2_b32 v[160:161], v119 offset1:1
	v_mov_b32_e32 v119, 0x275c
	s_waitcnt lgkmcnt(0)
	v_pk_fma_f32 v[160:161], v[154:155], v[160:161], v[170:171] op_sel_hi:[0,1,1]
	ds_read2_b32 v[170:171], v119 offset1:1
	v_mov_b32_e32 v119, 0x2764
	s_waitcnt lgkmcnt(0)
	v_pk_fma_f32 v[170:171], v[154:155], v[170:171], v[178:179] op_sel_hi:[0,1,1]
	ds_read2_b32 v[178:179], v119 offset1:1
	v_mov_b32_e32 v119, 0x276c
	s_waitcnt lgkmcnt(0)
	v_pk_fma_f32 v[176:177], v[154:155], v[178:179], v[176:177] op_sel_hi:[0,1,1]
	ds_read2_b32 v[178:179], v119 offset1:1
	v_mov_b32_e32 v119, 0x2774
	s_waitcnt lgkmcnt(0)
	v_pk_fma_f32 v[178:179], v[154:155], v[178:179], v[180:181] op_sel_hi:[0,1,1]
	ds_read2_b32 v[180:181], v119 offset1:1
	v_mov_b32_e32 v119, 0x277c
	s_waitcnt lgkmcnt(0)
	v_pk_fma_f32 v[174:175], v[154:155], v[180:181], v[174:175] op_sel_hi:[0,1,1]
	ds_read2_b32 v[180:181], v119 offset1:1
	v_mov_b32_e32 v119, 0x2784
	s_waitcnt lgkmcnt(0)
	v_pk_fma_f32 v[172:173], v[154:155], v[180:181], v[172:173] op_sel_hi:[0,1,1]
	ds_read2_b32 v[180:181], v119 offset1:1
	v_mov_b32_e32 v119, 0x278c
	s_waitcnt lgkmcnt(0)
	v_pk_fma_f32 v[162:163], v[154:155], v[180:181], v[162:163] op_sel_hi:[0,1,1]
	ds_read2_b32 v[180:181], v119 offset1:1
	v_mov_b32_e32 v119, 0x2794
	s_waitcnt lgkmcnt(0)
	v_pk_fma_f32 v[166:167], v[154:155], v[180:181], v[166:167] op_sel_hi:[0,1,1]
	ds_read2_b32 v[180:181], v119 offset1:1
	v_mov_b32_e32 v119, 0x279c
	s_waitcnt lgkmcnt(0)
	v_pk_fma_f32 v[10:11], v[154:155], v[180:181], v[10:11] op_sel_hi:[0,1,1]
	ds_read2_b32 v[180:181], v119 offset1:1
	v_mov_b32_e32 v119, 0x27a4
	s_waitcnt lgkmcnt(0)
	v_pk_fma_f32 v[8:9], v[154:155], v[180:181], v[8:9] op_sel_hi:[0,1,1]
	ds_read2_b32 v[180:181], v119 offset1:1
	v_mov_b32_e32 v119, 0x27ac
	s_waitcnt lgkmcnt(0)
	v_pk_fma_f32 v[164:165], v[154:155], v[180:181], v[164:165] op_sel_hi:[0,1,1]
	ds_read2_b32 v[180:181], v119 offset1:1
	v_mov_b32_e32 v119, 0x27b4
	s_waitcnt lgkmcnt(0)
	v_pk_fma_f32 v[20:21], v[154:155], v[180:181], v[20:21] op_sel_hi:[0,1,1]
	ds_read2_b32 v[180:181], v119 offset1:1
	v_mov_b32_e32 v119, 0x27bc
	s_waitcnt lgkmcnt(0)
	v_pk_fma_f32 v[18:19], v[154:155], v[180:181], v[18:19] op_sel_hi:[0,1,1]
	ds_read2_b32 v[180:181], v119 offset1:1
	v_mov_b32_e32 v119, 0x27c4
	s_waitcnt lgkmcnt(0)
	v_pk_fma_f32 v[158:159], v[154:155], v[180:181], v[158:159] op_sel_hi:[0,1,1]
	ds_read2_b32 v[180:181], v119 offset1:1
	v_mov_b32_e32 v119, 0x27cc
	s_waitcnt lgkmcnt(0)
	v_pk_fma_f32 v[30:31], v[154:155], v[180:181], v[30:31] op_sel_hi:[0,1,1]
	ds_read2_b32 v[180:181], v119 offset1:1
	v_mov_b32_e32 v119, 0x27d4
	s_waitcnt lgkmcnt(0)
	v_pk_fma_f32 v[32:33], v[154:155], v[180:181], v[32:33] op_sel_hi:[0,1,1]
	ds_read2_b32 v[180:181], v119 offset1:1
	v_mov_b32_e32 v119, 0x27dc
	s_waitcnt lgkmcnt(0)
	v_pk_fma_f32 v[152:153], v[154:155], v[180:181], v[152:153] op_sel_hi:[0,1,1]
	ds_read2_b32 v[180:181], v119 offset1:1
	v_mov_b32_e32 v119, 0x27e4
	s_waitcnt lgkmcnt(0)
	v_pk_fma_f32 v[38:39], v[154:155], v[180:181], v[38:39] op_sel_hi:[0,1,1]
	ds_read2_b32 v[180:181], v119 offset1:1
	v_mov_b32_e32 v119, 0x27ec
	s_waitcnt lgkmcnt(0)
	v_pk_fma_f32 v[22:23], v[154:155], v[180:181], v[22:23] op_sel_hi:[0,1,1]
	ds_read2_b32 v[180:181], v119 offset1:1
	v_mov_b32_e32 v119, 0x27f4
	s_waitcnt lgkmcnt(0)
	v_pk_fma_f32 v[148:149], v[154:155], v[180:181], v[148:149] op_sel_hi:[0,1,1]
	ds_read2_b32 v[180:181], v119 offset1:1
	v_mov_b32_e32 v119, 0x27fc
	s_waitcnt lgkmcnt(0)
	v_pk_fma_f32 v[168:169], v[154:155], v[180:181], v[168:169] op_sel_hi:[0,1,1]
	ds_read2_b32 v[180:181], v119 offset1:1
	v_mov_b32_e32 v119, 0x2804
	s_waitcnt lgkmcnt(0)
	v_fmac_f32_e32 v0, v154, v180
	ds_read2_b32 v[154:155], v119 offset1:1
	v_mov_b32_e32 v119, 0x280c
	v_fmac_f32_e32 v1, v150, v181
	s_waitcnt lgkmcnt(0)
	v_pk_fma_f32 v[28:29], v[150:151], v[154:155], v[28:29] op_sel_hi:[0,1,1]
	ds_read2_b32 v[154:155], v119 offset1:1
	v_mov_b32_e32 v119, 0x2814
	s_waitcnt lgkmcnt(0)
	v_pk_fma_f32 v[26:27], v[150:151], v[154:155], v[26:27] op_sel_hi:[0,1,1]
	ds_read2_b32 v[154:155], v119 offset1:1
	v_mov_b32_e32 v119, 0x281c
	s_waitcnt lgkmcnt(0)
	v_pk_fma_f32 v[36:37], v[150:151], v[154:155], v[36:37] op_sel_hi:[0,1,1]
	ds_read2_b32 v[154:155], v119 offset1:1
	v_mov_b32_e32 v119, 0x2824
	s_waitcnt lgkmcnt(0)
	v_pk_fma_f32 v[34:35], v[150:151], v[154:155], v[34:35] op_sel_hi:[0,1,1]
	ds_read2_b32 v[154:155], v119 offset1:1
	v_mov_b32_e32 v119, 0x282c
	s_waitcnt lgkmcnt(0)
	v_pk_fma_f32 v[42:43], v[150:151], v[154:155], v[42:43] op_sel_hi:[0,1,1]
	ds_read2_b32 v[154:155], v119 offset1:1
	v_mov_b32_e32 v119, 0x2834
	s_waitcnt lgkmcnt(0)
	v_pk_fma_f32 v[40:41], v[150:151], v[154:155], v[40:41] op_sel_hi:[0,1,1]
	ds_read2_b32 v[154:155], v119 offset1:1
	v_mov_b32_e32 v119, 0x283c
	s_waitcnt lgkmcnt(0)
	v_pk_fma_f32 v[46:47], v[150:151], v[154:155], v[46:47] op_sel_hi:[0,1,1]
	ds_read2_b32 v[154:155], v119 offset1:1
	v_mov_b32_e32 v119, 0x2844
	s_waitcnt lgkmcnt(0)
	v_pk_fma_f32 v[44:45], v[150:151], v[154:155], v[44:45] op_sel_hi:[0,1,1]
	ds_read2_b32 v[154:155], v119 offset1:1
	v_mov_b32_e32 v119, 0x284c
	s_waitcnt lgkmcnt(0)
	v_pk_fma_f32 v[154:155], v[150:151], v[154:155], v[156:157] op_sel_hi:[0,1,1]
	ds_read2_b32 v[156:157], v119 offset1:1
	v_mov_b32_e32 v119, 0x2854
	s_waitcnt lgkmcnt(0)
	v_pk_fma_f32 v[24:25], v[150:151], v[156:157], v[24:25] op_sel_hi:[0,1,1]
	ds_read2_b32 v[156:157], v119 offset1:1
	v_mov_b32_e32 v119, 0x285c
	s_waitcnt lgkmcnt(0)
	v_pk_fma_f32 v[156:157], v[150:151], v[156:157], v[160:161] op_sel_hi:[0,1,1]
	ds_read2_b32 v[160:161], v119 offset1:1
	v_mov_b32_e32 v119, 0x2864
	s_waitcnt lgkmcnt(0)
	v_pk_fma_f32 v[160:161], v[150:151], v[160:161], v[170:171] op_sel_hi:[0,1,1]
	ds_read2_b32 v[170:171], v119 offset1:1
	v_mov_b32_e32 v119, 0x286c
	s_waitcnt lgkmcnt(0)
	v_pk_fma_f32 v[170:171], v[150:151], v[170:171], v[176:177] op_sel_hi:[0,1,1]
	ds_read2_b32 v[176:177], v119 offset1:1
	v_mov_b32_e32 v119, 0x2874
	s_waitcnt lgkmcnt(0)
	v_pk_fma_f32 v[176:177], v[150:151], v[176:177], v[178:179] op_sel_hi:[0,1,1]
	ds_read2_b32 v[178:179], v119 offset1:1
	v_mov_b32_e32 v119, 0x287c
	s_waitcnt lgkmcnt(0)
	v_pk_fma_f32 v[174:175], v[150:151], v[178:179], v[174:175] op_sel_hi:[0,1,1]
	ds_read2_b32 v[178:179], v119 offset1:1
	v_mov_b32_e32 v119, 0x2884
	s_waitcnt lgkmcnt(0)
	v_pk_fma_f32 v[172:173], v[150:151], v[178:179], v[172:173] op_sel_hi:[0,1,1]
	ds_read2_b32 v[178:179], v119 offset1:1
	v_mov_b32_e32 v119, 0x288c
	s_waitcnt lgkmcnt(0)
	v_pk_fma_f32 v[162:163], v[150:151], v[178:179], v[162:163] op_sel_hi:[0,1,1]
	ds_read2_b32 v[178:179], v119 offset1:1
	v_mov_b32_e32 v119, 0x2894
	s_waitcnt lgkmcnt(0)
	v_pk_fma_f32 v[166:167], v[150:151], v[178:179], v[166:167] op_sel_hi:[0,1,1]
	ds_read2_b32 v[178:179], v119 offset1:1
	v_mov_b32_e32 v119, 0x289c
	s_waitcnt lgkmcnt(0)
	v_pk_fma_f32 v[10:11], v[150:151], v[178:179], v[10:11] op_sel_hi:[0,1,1]
	ds_read2_b32 v[178:179], v119 offset1:1
	s_waitcnt lgkmcnt(0)
	v_pk_fma_f32 v[178:179], v[150:151], v[178:179], v[8:9] op_sel_hi:[0,1,1]
	v_mov_b32_e32 v8, 0x28a4
	ds_read2_b32 v[8:9], v8 offset1:1
	s_waitcnt lgkmcnt(0)
	v_pk_fma_f32 v[164:165], v[150:151], v[8:9], v[164:165] op_sel_hi:[0,1,1]
	v_mov_b32_e32 v8, 0x28ac
	ds_read2_b32 v[8:9], v8 offset1:1
	s_waitcnt lgkmcnt(0)
	v_pk_fma_f32 v[20:21], v[150:151], v[8:9], v[20:21] op_sel_hi:[0,1,1]
	v_mov_b32_e32 v8, 0x28b4
	ds_read2_b32 v[8:9], v8 offset1:1
	s_waitcnt lgkmcnt(0)
	v_pk_fma_f32 v[18:19], v[150:151], v[8:9], v[18:19] op_sel_hi:[0,1,1]
	v_mov_b32_e32 v8, 0x28bc
	ds_read2_b32 v[8:9], v8 offset1:1
	s_waitcnt lgkmcnt(0)
	v_pk_fma_f32 v[158:159], v[150:151], v[8:9], v[158:159] op_sel_hi:[0,1,1]
	v_mov_b32_e32 v8, 0x28c4
	ds_read2_b32 v[8:9], v8 offset1:1
	s_waitcnt lgkmcnt(0)
	v_pk_fma_f32 v[30:31], v[150:151], v[8:9], v[30:31] op_sel_hi:[0,1,1]
	v_mov_b32_e32 v8, 0x28cc
	ds_read2_b32 v[8:9], v8 offset1:1
	s_waitcnt lgkmcnt(0)
	v_pk_fma_f32 v[32:33], v[150:151], v[8:9], v[32:33] op_sel_hi:[0,1,1]
	v_mov_b32_e32 v8, 0x28d4
	ds_read2_b32 v[8:9], v8 offset1:1
	s_waitcnt lgkmcnt(0)
	v_pk_fma_f32 v[152:153], v[150:151], v[8:9], v[152:153] op_sel_hi:[0,1,1]
	v_mov_b32_e32 v8, 0x28dc
	ds_read2_b32 v[8:9], v8 offset1:1
	s_waitcnt lgkmcnt(0)
	v_pk_fma_f32 v[38:39], v[150:151], v[8:9], v[38:39] op_sel_hi:[0,1,1]
	v_mov_b32_e32 v8, 0x28e4
	ds_read2_b32 v[8:9], v8 offset1:1
	s_waitcnt lgkmcnt(0)
	v_pk_fma_f32 v[22:23], v[150:151], v[8:9], v[22:23] op_sel_hi:[0,1,1]
	v_mov_b32_e32 v8, 0x28ec
	ds_read2_b32 v[8:9], v8 offset1:1
	s_waitcnt lgkmcnt(0)
	v_pk_fma_f32 v[148:149], v[150:151], v[8:9], v[148:149] op_sel_hi:[0,1,1]
	v_mov_b32_e32 v8, 0x28f4
	ds_read2_b32 v[8:9], v8 offset1:1
	s_waitcnt lgkmcnt(0)
	v_pk_fma_f32 v[168:169], v[150:151], v[8:9], v[168:169] op_sel_hi:[0,1,1]
	v_mov_b32_e32 v8, 0x28fc
	ds_read2_b32 v[8:9], v8 offset1:1
	s_waitcnt lgkmcnt(0)
	v_fmac_f32_e32 v0, v150, v8
	v_mov_b32_e32 v8, 0x2904
	v_fmac_f32_e32 v1, v146, v9
	ds_read2_b32 v[8:9], v8 offset1:1
	s_waitcnt lgkmcnt(0)
	v_pk_fma_f32 v[28:29], v[146:147], v[8:9], v[28:29] op_sel_hi:[0,1,1]
	v_mov_b32_e32 v8, 0x290c
	ds_read2_b32 v[8:9], v8 offset1:1
	s_waitcnt lgkmcnt(0)
	v_pk_fma_f32 v[26:27], v[146:147], v[8:9], v[26:27] op_sel_hi:[0,1,1]
	v_mov_b32_e32 v8, 0x2914
	ds_read2_b32 v[8:9], v8 offset1:1
	s_waitcnt lgkmcnt(0)
	v_pk_fma_f32 v[36:37], v[146:147], v[8:9], v[36:37] op_sel_hi:[0,1,1]
	v_mov_b32_e32 v8, 0x291c
	ds_read2_b32 v[8:9], v8 offset1:1
	s_waitcnt lgkmcnt(0)
	v_pk_fma_f32 v[34:35], v[146:147], v[8:9], v[34:35] op_sel_hi:[0,1,1]
	v_mov_b32_e32 v8, 0x2924
	ds_read2_b32 v[8:9], v8 offset1:1
	s_waitcnt lgkmcnt(0)
	v_pk_fma_f32 v[42:43], v[146:147], v[8:9], v[42:43] op_sel_hi:[0,1,1]
	v_mov_b32_e32 v8, 0x292c
	ds_read2_b32 v[8:9], v8 offset1:1
	s_waitcnt lgkmcnt(0)
	v_pk_fma_f32 v[40:41], v[146:147], v[8:9], v[40:41] op_sel_hi:[0,1,1]
	v_mov_b32_e32 v8, 0x2934
	ds_read2_b32 v[8:9], v8 offset1:1
	s_waitcnt lgkmcnt(0)
	v_pk_fma_f32 v[46:47], v[146:147], v[8:9], v[46:47] op_sel_hi:[0,1,1]
	v_mov_b32_e32 v8, 0x293c
	ds_read2_b32 v[8:9], v8 offset1:1
	s_waitcnt lgkmcnt(0)
	v_pk_fma_f32 v[150:151], v[146:147], v[8:9], v[44:45] op_sel_hi:[0,1,1]
	v_mov_b32_e32 v8, 0x2944
	ds_read2_b32 v[8:9], v8 offset1:1
	v_mov_b32_e32 v44, 0x2964
	ds_read2_b32 v[44:45], v44 offset1:1
	s_waitcnt lgkmcnt(1)
	v_pk_fma_f32 v[154:155], v[146:147], v[8:9], v[154:155] op_sel_hi:[0,1,1]
	v_mov_b32_e32 v8, 0x294c
	ds_read2_b32 v[8:9], v8 offset1:1
	s_waitcnt lgkmcnt(1)
	v_pk_fma_f32 v[180:181], v[146:147], v[44:45], v[170:171] op_sel_hi:[0,1,1]
	v_mov_b32_e32 v44, 0x296c
	ds_read2_b32 v[44:45], v44 offset1:1
	s_waitcnt lgkmcnt(1)
	v_pk_fma_f32 v[24:25], v[146:147], v[8:9], v[24:25] op_sel_hi:[0,1,1]
	v_mov_b32_e32 v8, 0x2954
	ds_read2_b32 v[8:9], v8 offset1:1
	s_waitcnt lgkmcnt(0)
	v_pk_fma_f32 v[156:157], v[146:147], v[8:9], v[156:157] op_sel_hi:[0,1,1]
	v_mov_b32_e32 v8, 0x295c
	ds_read2_b32 v[8:9], v8 offset1:1
	s_waitcnt lgkmcnt(0)
	v_pk_fma_f32 v[8:9], v[146:147], v[8:9], v[160:161] op_sel_hi:[0,1,1]
	v_pk_fma_f32 v[160:161], v[146:147], v[44:45], v[176:177] op_sel_hi:[0,1,1]
	v_mov_b32_e32 v44, 0x2974
	ds_read2_b32 v[44:45], v44 offset1:1
	s_waitcnt lgkmcnt(0)
	v_pk_fma_f32 v[170:171], v[146:147], v[44:45], v[174:175] op_sel_hi:[0,1,1]
	v_mov_b32_e32 v44, 0x297c
	ds_read2_b32 v[44:45], v44 offset1:1
	s_waitcnt lgkmcnt(0)
	v_pk_fma_f32 v[172:173], v[146:147], v[44:45], v[172:173] op_sel_hi:[0,1,1]
	v_mov_b32_e32 v44, 0x2984
	ds_read2_b32 v[44:45], v44 offset1:1
	s_waitcnt lgkmcnt(0)
	v_pk_fma_f32 v[176:177], v[146:147], v[44:45], v[162:163] op_sel_hi:[0,1,1]
	v_mov_b32_e32 v44, 0x298c
	ds_read2_b32 v[44:45], v44 offset1:1
	s_waitcnt lgkmcnt(0)
	v_pk_fma_f32 v[162:163], v[146:147], v[44:45], v[166:167] op_sel_hi:[0,1,1]
	v_mov_b32_e32 v44, 0x2994
	ds_read2_b32 v[44:45], v44 offset1:1
	s_waitcnt lgkmcnt(0)
	v_pk_fma_f32 v[166:167], v[146:147], v[44:45], v[10:11] op_sel_hi:[0,1,1]
	v_mov_b32_e32 v10, 0x299c
	ds_read2_b32 v[10:11], v10 offset1:1
	v_mov_b32_e32 v44, 0x29fc
	ds_read2_b32 v[44:45], v44 offset1:1
	s_waitcnt lgkmcnt(1)
	v_pk_fma_f32 v[174:175], v[146:147], v[10:11], v[178:179] op_sel_hi:[0,1,1]
	v_mov_b32_e32 v10, 0x29a4
	ds_read2_b32 v[10:11], v10 offset1:1
	s_waitcnt lgkmcnt(1)
	v_fmac_f32_e32 v0, v146, v44
	v_mov_b32_e32 v44, 0x2a04
	v_mul_f32_e32 v45, v144, v45
	s_waitcnt lgkmcnt(0)
	v_pk_fma_f32 v[178:179], v[146:147], v[10:11], v[164:165] op_sel_hi:[0,1,1]
	v_mov_b32_e32 v10, 0x29ac
	ds_read2_b32 v[10:11], v10 offset1:1
	s_waitcnt lgkmcnt(0)
	v_pk_fma_f32 v[10:11], v[146:147], v[10:11], v[20:21] op_sel_hi:[0,1,1]
	v_mov_b32_e32 v20, 0x29b4
	ds_read2_b32 v[20:21], v20 offset1:1
	s_waitcnt lgkmcnt(0)
	v_pk_fma_f32 v[164:165], v[146:147], v[20:21], v[18:19] op_sel_hi:[0,1,1]
	v_mov_b32_e32 v18, 0x29bc
	ds_read2_b32 v[18:19], v18 offset1:1
	v_mov_b32_e32 v20, 0x29d4
	ds_read2_b32 v[20:21], v20 offset1:1
	s_waitcnt lgkmcnt(1)
	v_pk_fma_f32 v[158:159], v[146:147], v[18:19], v[158:159] op_sel_hi:[0,1,1]
	v_mov_b32_e32 v18, 0x29c4
	ds_read2_b32 v[18:19], v18 offset1:1
	s_waitcnt lgkmcnt(0)
	v_pk_fma_f32 v[182:183], v[146:147], v[18:19], v[30:31] op_sel_hi:[0,1,1]
	v_mov_b32_e32 v18, 0x29cc
	v_pk_fma_f32 v[30:31], v[146:147], v[20:21], v[152:153] op_sel_hi:[0,1,1]
	v_mov_b32_e32 v20, 0x29dc
	ds_read2_b32 v[18:19], v18 offset1:1
	ds_read2_b32 v[20:21], v20 offset1:1
	s_waitcnt lgkmcnt(1)
	v_pk_fma_f32 v[18:19], v[146:147], v[18:19], v[32:33] op_sel_hi:[0,1,1]
	s_waitcnt lgkmcnt(0)
	v_pk_fma_f32 v[32:33], v[146:147], v[20:21], v[38:39] op_sel_hi:[0,1,1]
	v_mov_b32_e32 v20, 0x29e4
	ds_read2_b32 v[20:21], v20 offset1:1
	s_waitcnt lgkmcnt(0)
	v_pk_fma_f32 v[38:39], v[146:147], v[20:21], v[22:23] op_sel_hi:[0,1,1]
	v_mov_b32_e32 v20, 0x29ec
	v_mov_b32_e32 v22, 0x29f4
	ds_read2_b32 v[20:21], v20 offset1:1
	ds_read2_b32 v[22:23], v22 offset1:1
	s_waitcnt lgkmcnt(1)
	v_pk_fma_f32 v[20:21], v[146:147], v[20:21], v[148:149] op_sel_hi:[0,1,1]
	s_waitcnt lgkmcnt(0)
	v_pk_fma_f32 v[22:23], v[146:147], v[22:23], v[168:169] op_sel_hi:[0,1,1]
	ds_read2_b32 v[146:147], v44 offset1:1
	v_mov_b32_e32 v44, 0x2a9c
	s_waitcnt lgkmcnt(0)
	v_pk_fma_f32 v[186:187], v[144:145], v[146:147], v[28:29] op_sel_hi:[0,1,1]
	v_mov_b32_e32 v28, 0x2a0c
	ds_read2_b32 v[28:29], v28 offset1:1
	s_waitcnt lgkmcnt(0)
	v_pk_fma_f32 v[152:153], v[144:145], v[28:29], v[26:27] op_sel_hi:[0,1,1]
	v_mov_b32_e32 v26, 0x2a14
	ds_read2_b32 v[26:27], v26 offset1:1
	v_mov_b32_e32 v28, 0x2a74
	ds_read2_b32 v[28:29], v28 offset1:1
	s_waitcnt lgkmcnt(1)
	v_pk_fma_f32 v[168:169], v[144:145], v[26:27], v[36:37] op_sel_hi:[0,1,1]
	v_mov_b32_e32 v26, 0x2a1c
	ds_read2_b32 v[26:27], v26 offset1:1
	s_waitcnt lgkmcnt(1)
	v_pk_fma_f32 v[28:29], v[144:145], v[28:29], v[170:171] op_sel_hi:[0,1,1]
	v_mov_b32_e32 v36, 0x2a84
	ds_read2_b32 v[36:37], v36 offset1:1
	s_waitcnt lgkmcnt(1)
	v_pk_fma_f32 v[184:185], v[144:145], v[26:27], v[34:35] op_sel_hi:[0,1,1]
	v_mov_b32_e32 v26, 0x2a24
	ds_read2_b32 v[26:27], v26 offset1:1
	v_mov_b32_e32 v34, 0x2a7c
	ds_read2_b32 v[34:35], v34 offset1:1
	s_waitcnt lgkmcnt(2)
	v_pk_fma_f32 v[36:37], v[144:145], v[36:37], v[176:177] op_sel_hi:[0,1,1]
	s_waitcnt lgkmcnt(1)
	v_pk_fma_f32 v[188:189], v[144:145], v[26:27], v[42:43] op_sel_hi:[0,1,1]
	v_mov_b32_e32 v26, 0x2a2c
	ds_read2_b32 v[26:27], v26 offset1:1
	v_mov_b32_e32 v42, 0x2a94
	ds_read2_b32 v[42:43], v42 offset1:1
	s_waitcnt lgkmcnt(2)
	v_pk_fma_f32 v[34:35], v[144:145], v[34:35], v[172:173] op_sel_hi:[0,1,1]
	s_waitcnt lgkmcnt(1)
	v_pk_fma_f32 v[190:191], v[144:145], v[26:27], v[40:41] op_sel_hi:[0,1,1]
	v_mov_b32_e32 v26, 0x2a34
	ds_read2_b32 v[26:27], v26 offset1:1
	s_waitcnt lgkmcnt(1)
	v_pk_fma_f32 v[42:43], v[144:145], v[42:43], v[166:167] op_sel_hi:[0,1,1]
	v_mov_b32_e32 v40, 0x2a8c
	ds_read2_b32 v[40:41], v40 offset1:1
	s_waitcnt lgkmcnt(1)
	v_pk_fma_f32 v[192:193], v[144:145], v[26:27], v[46:47] op_sel_hi:[0,1,1]
	ds_read2_b32 v[46:47], v44 offset1:1
	v_mov_b32_e32 v44, 0x2aa4
	v_mov_b32_e32 v26, 0x2a3c
	ds_read2_b32 v[26:27], v26 offset1:1
	s_waitcnt lgkmcnt(2)
	v_pk_fma_f32 v[40:41], v[144:145], v[40:41], v[162:163] op_sel_hi:[0,1,1]
	s_waitcnt lgkmcnt(1)
	v_pk_fma_f32 v[146:147], v[144:145], v[46:47], v[174:175] op_sel_hi:[0,1,1]
	ds_read2_b32 v[46:47], v44 offset1:1
	v_mov_b32_e32 v44, 0x2aac
	s_waitcnt lgkmcnt(1)
	v_pk_fma_f32 v[194:195], v[144:145], v[26:27], v[150:151] op_sel_hi:[0,1,1]
	v_mov_b32_e32 v26, 0x2a44
	ds_read2_b32 v[26:27], v26 offset1:1
	s_waitcnt lgkmcnt(1)
	v_pk_fma_f32 v[148:149], v[144:145], v[46:47], v[178:179] op_sel_hi:[0,1,1]
	ds_read2_b32 v[46:47], v44 offset1:1
	v_mov_b32_e32 v44, 0x2ab4
	s_waitcnt lgkmcnt(1)
	v_pk_fma_f32 v[196:197], v[144:145], v[26:27], v[154:155] op_sel_hi:[0,1,1]
	v_mov_b32_e32 v26, 0x2a4c
	s_waitcnt lgkmcnt(0)
	v_pk_fma_f32 v[10:11], v[144:145], v[46:47], v[10:11] op_sel_hi:[0,1,1]
	ds_read2_b32 v[46:47], v44 offset1:1
	ds_read2_b32 v[26:27], v26 offset1:1
	v_mov_b32_e32 v44, 0x2abc
	s_waitcnt lgkmcnt(1)
	v_pk_fma_f32 v[150:151], v[144:145], v[46:47], v[164:165] op_sel_hi:[0,1,1]
	ds_read2_b32 v[46:47], v44 offset1:1
	s_waitcnt lgkmcnt(1)
	v_pk_fma_f32 v[198:199], v[144:145], v[26:27], v[24:25] op_sel_hi:[0,1,1]
	v_mov_b32_e32 v24, 0x2a54
	v_mov_b32_e32 v44, 0x2ac4
	ds_read2_b32 v[24:25], v24 offset1:1
	s_waitcnt lgkmcnt(1)
	v_pk_fma_f32 v[154:155], v[144:145], v[46:47], v[158:159] op_sel_hi:[0,1,1]
	ds_read2_b32 v[46:47], v44 offset1:1
	v_mov_b32_e32 v44, 0x2acc
	v_mov_b32_e32 v26, 0x2a6c
	s_waitcnt lgkmcnt(1)
	v_pk_fma_f32 v[200:201], v[144:145], v[24:25], v[156:157] op_sel_hi:[0,1,1]
	ds_read2_b32 v[26:27], v26 offset1:1
	s_waitcnt lgkmcnt(1)
	v_pk_fma_f32 v[156:157], v[144:145], v[46:47], v[182:183] op_sel_hi:[0,1,1]
	ds_read2_b32 v[46:47], v44 offset1:1
	v_mov_b32_e32 v24, 0x2a64
	ds_read2_b32 v[24:25], v24 offset1:1
	s_waitcnt lgkmcnt(2)
	v_pk_fma_f32 v[26:27], v[144:145], v[26:27], v[160:161] op_sel_hi:[0,1,1]
	s_waitcnt lgkmcnt(1)
	v_pk_fma_f32 v[158:159], v[144:145], v[46:47], v[18:19] op_sel_hi:[0,1,1]
	v_mov_b32_e32 v18, 0x2ad4
	ds_read2_b32 v[18:19], v18 offset1:1
	s_waitcnt lgkmcnt(1)
	v_pk_fma_f32 v[24:25], v[144:145], v[24:25], v[180:181] op_sel_hi:[0,1,1]
	s_waitcnt lgkmcnt(0)
	v_pk_fma_f32 v[30:31], v[144:145], v[18:19], v[30:31] op_sel_hi:[0,1,1]
	v_mov_b32_e32 v18, 0x2adc
	ds_read2_b32 v[18:19], v18 offset1:1
	s_waitcnt lgkmcnt(0)
	v_pk_fma_f32 v[32:33], v[144:145], v[18:19], v[32:33] op_sel_hi:[0,1,1]
	v_mov_b32_e32 v18, 0x2ae4
	ds_read2_b32 v[18:19], v18 offset1:1
	s_waitcnt lgkmcnt(0)
	v_pk_fma_f32 v[38:39], v[144:145], v[18:19], v[38:39] op_sel_hi:[0,1,1]
	v_mov_b32_e32 v18, 0x2aec
	ds_read2_b32 v[18:19], v18 offset1:1
	s_waitcnt lgkmcnt(0)
	v_pk_fma_f32 v[20:21], v[144:145], v[18:19], v[20:21] op_sel_hi:[0,1,1]
	v_mov_b32_e32 v18, 0x2af4
	ds_read2_b32 v[18:19], v18 offset1:1
	s_waitcnt lgkmcnt(0)
	v_pk_fma_f32 v[166:167], v[144:145], v[18:19], v[22:23] op_sel_hi:[0,1,1]
	v_mov_b32_e32 v18, 0x2afc
	ds_read2_b32 v[46:47], v18 offset1:1
	v_mov_b32_e32 v18, 0x2b04
	ds_read2_b32 v[18:19], v18 offset1:1
	s_waitcnt lgkmcnt(1)
	v_mul_f32_e32 v44, v144, v46
	v_add_f32_e32 v46, v117, v2
	s_waitcnt lgkmcnt(0)
	v_pk_fma_f32 v[162:163], v[2:3], v[18:19], v[186:187] op_sel_hi:[0,1,1]
	v_mov_b32_e32 v18, 0x2b0c
	ds_read2_b32 v[18:19], v18 offset1:1
	v_mul_f32_e32 v117, 0x3fb8aa3b, v109
	v_fma_f32 v119, v109, s5, -v117
	v_rndne_f32_e32 v125, v117
	v_fmac_f32_e32 v119, 0x32a5705f, v109
	s_waitcnt lgkmcnt(0)
	v_pk_fma_f32 v[160:161], v[2:3], v[18:19], v[152:153] op_sel_hi:[0,1,1]
	v_mov_b32_e32 v18, 0x2b14
	ds_read2_b32 v[18:19], v18 offset1:1
	v_sub_f32_e32 v117, v117, v125
	v_add_f32_e32 v117, v117, v119
	v_exp_f32_e32 v117, v117
	v_cvt_i32_f32_e32 v119, v125
	s_waitcnt lgkmcnt(0)
	v_pk_fma_f32 v[170:171], v[2:3], v[18:19], v[168:169] op_sel_hi:[0,1,1]
	v_mov_b32_e32 v18, 0x2b1c
	ds_read2_b32 v[18:19], v18 offset1:1
	v_ldexp_f32 v117, v117, v119
	v_pk_add_f32 v[0:1], v[0:1], v[44:45]
	v_mov_b32_e32 v44, 0x2bfc
	ds_read2_b32 v[44:45], v44 offset1:1
	s_waitcnt lgkmcnt(1)
	v_pk_fma_f32 v[164:165], v[2:3], v[18:19], v[184:185] op_sel_hi:[0,1,1]
	v_mov_b32_e32 v18, 0x2b24
	ds_read2_b32 v[18:19], v18 offset1:1
	s_waitcnt lgkmcnt(0)
	v_pk_fma_f32 v[178:179], v[2:3], v[18:19], v[188:189] op_sel_hi:[0,1,1]
	v_mov_b32_e32 v18, 0x2b2c
	ds_read2_b32 v[18:19], v18 offset1:1
	s_waitcnt lgkmcnt(0)
	v_pk_fma_f32 v[174:175], v[2:3], v[18:19], v[190:191] op_sel_hi:[0,1,1]
	v_mov_b32_e32 v18, 0x2b34
	ds_read2_b32 v[18:19], v18 offset1:1
	s_waitcnt lgkmcnt(0)
	v_pk_fma_f32 v[186:187], v[2:3], v[18:19], v[192:193] op_sel_hi:[0,1,1]
	v_mov_b32_e32 v18, 0x2b3c
	ds_read2_b32 v[18:19], v18 offset1:1
	s_waitcnt lgkmcnt(0)
	v_pk_fma_f32 v[182:183], v[2:3], v[18:19], v[194:195] op_sel_hi:[0,1,1]
	v_mov_b32_e32 v18, 0x2b44
	ds_read2_b32 v[18:19], v18 offset1:1
	s_waitcnt lgkmcnt(0)
	v_pk_fma_f32 v[192:193], v[2:3], v[18:19], v[196:197] op_sel_hi:[0,1,1]
	v_mov_b32_e32 v18, 0x2b4c
	ds_read2_b32 v[18:19], v18 offset1:1
	s_waitcnt lgkmcnt(0)
	v_pk_fma_f32 v[188:189], v[2:3], v[18:19], v[198:199] op_sel_hi:[0,1,1]
	v_mov_b32_e32 v18, 0x2b54
	ds_read2_b32 v[18:19], v18 offset1:1
	s_waitcnt lgkmcnt(0)
	v_pk_fma_f32 v[200:201], v[2:3], v[18:19], v[200:201] op_sel_hi:[0,1,1]
	v_mov_b32_e32 v18, 0x2a5c
	ds_read2_b32 v[18:19], v18 offset1:1
	s_waitcnt lgkmcnt(0)
	v_pk_fma_f32 v[8:9], v[144:145], v[18:19], v[8:9] op_sel_hi:[0,1,1]
	v_mov_b32_e32 v18, 0x2b5c
	ds_read2_b32 v[18:19], v18 offset1:1
	s_waitcnt lgkmcnt(0)
	v_pk_fma_f32 v[204:205], v[2:3], v[18:19], v[8:9] op_sel_hi:[0,1,1]
	v_mov_b32_e32 v8, 0x2b64
	ds_read2_b32 v[8:9], v8 offset1:1
	s_waitcnt lgkmcnt(0)
	v_pk_fma_f32 v[222:223], v[2:3], v[8:9], v[24:25] op_sel_hi:[0,1,1]
	v_mov_b32_e32 v8, 0x2b6c
	ds_read2_b32 v[8:9], v8 offset1:1
	s_waitcnt lgkmcnt(0)
	v_pk_fma_f32 v[218:219], v[2:3], v[8:9], v[26:27] op_sel_hi:[0,1,1]
	v_mov_b32_e32 v8, 0x2b74
	ds_read2_b32 v[8:9], v8 offset1:1
	s_waitcnt lgkmcnt(0)
	v_pk_fma_f32 v[206:207], v[2:3], v[8:9], v[28:29] op_sel_hi:[0,1,1]
	v_mov_b32_e32 v8, 0x2b7c
	ds_read2_b32 v[8:9], v8 offset1:1
	v_mov_b32_e32 v28, 0x2cd4
	s_waitcnt lgkmcnt(0)
	v_pk_fma_f32 v[224:225], v[2:3], v[8:9], v[34:35] op_sel_hi:[0,1,1]
	v_mov_b32_e32 v8, 0x2b84
	ds_read2_b32 v[8:9], v8 offset1:1
	s_waitcnt lgkmcnt(0)
	v_pk_fma_f32 v[196:197], v[2:3], v[8:9], v[36:37] op_sel_hi:[0,1,1]
	v_mov_b32_e32 v8, 0x2b8c
	ds_read2_b32 v[8:9], v8 offset1:1
	v_mov_b32_e32 v36, 0x2ce4
	s_waitcnt lgkmcnt(0)
	v_pk_fma_f32 v[208:209], v[2:3], v[8:9], v[40:41] op_sel_hi:[0,1,1]
	v_mov_b32_e32 v8, 0x2b94
	ds_read2_b32 v[8:9], v8 offset1:1
	ds_read2_b32 v[40:41], v36 offset1:1
	v_mov_b32_e32 v36, 0x2cec
	ds_read2_b32 v[36:37], v36 offset1:1
	s_waitcnt lgkmcnt(2)
	v_pk_fma_f32 v[236:237], v[2:3], v[8:9], v[42:43] op_sel_hi:[0,1,1]
	v_mov_b32_e32 v8, 0x2b9c
	ds_read2_b32 v[8:9], v8 offset1:1
	v_mov_b32_e32 v42, 0x2cf4
	ds_read2_b32 v[42:43], v42 offset1:1
	s_waitcnt lgkmcnt(1)
	v_pk_fma_f32 v[232:233], v[2:3], v[8:9], v[146:147] op_sel_hi:[0,1,1]
	v_mov_b32_e32 v8, 0x2ba4
	ds_read2_b32 v[8:9], v8 offset1:1
	s_waitcnt lgkmcnt(0)
	v_pk_fma_f32 v[244:245], v[2:3], v[8:9], v[148:149] op_sel_hi:[0,1,1]
	v_mov_b32_e32 v8, 0x2bac
	ds_read2_b32 v[8:9], v8 offset1:1
	s_waitcnt lgkmcnt(0)
	v_pk_fma_f32 v[240:241], v[2:3], v[8:9], v[10:11] op_sel_hi:[0,1,1]
	v_mov_b32_e32 v8, 0x2bb4
	ds_read2_b32 v[8:9], v8 offset1:1
	s_waitcnt lgkmcnt(0)
	v_pk_fma_f32 v[252:253], v[2:3], v[8:9], v[150:151] op_sel_hi:[0,1,1]
	v_mov_b32_e32 v8, 0x2bbc
	ds_read2_b32 v[8:9], v8 offset1:1
	s_waitcnt lgkmcnt(0)
	v_pk_fma_f32 v[248:249], v[2:3], v[8:9], v[154:155] op_sel_hi:[0,1,1]
	v_mov_b32_e32 v8, 0x2bc4
	ds_read2_b32 v[8:9], v8 offset1:1
	s_waitcnt lgkmcnt(0)
	v_pk_fma_f32 v[18:19], v[2:3], v[8:9], v[156:157] op_sel_hi:[0,1,1]
	v_mov_b32_e32 v8, 0x2bcc
	ds_read2_b32 v[8:9], v8 offset1:1
	s_waitcnt lgkmcnt(0)
	v_pk_fma_f32 v[10:11], v[2:3], v[8:9], v[158:159] op_sel_hi:[0,1,1]
	v_mov_b32_e32 v8, 0x2bd4
	ds_read2_b32 v[8:9], v8 offset1:1
	s_waitcnt lgkmcnt(0)
	v_pk_fma_f32 v[26:27], v[2:3], v[8:9], v[30:31] op_sel_hi:[0,1,1]
	v_mov_b32_e32 v8, 0x2bdc
	ds_read2_b32 v[8:9], v8 offset1:1
	s_waitcnt lgkmcnt(0)
	v_pk_fma_f32 v[22:23], v[2:3], v[8:9], v[32:33] op_sel_hi:[0,1,1]
	v_mov_b32_e32 v8, 0x2be4
	ds_read2_b32 v[8:9], v8 offset1:1
	ds_read2_b32 v[32:33], v28 offset1:1
	v_mov_b32_e32 v28, 0x2cdc
	ds_read2_b32 v[28:29], v28 offset1:1
	s_waitcnt lgkmcnt(2)
	v_pk_fma_f32 v[34:35], v[2:3], v[8:9], v[38:39] op_sel_hi:[0,1,1]
	v_mov_b32_e32 v8, 0x2bec
	ds_read2_b32 v[8:9], v8 offset1:1
	s_waitcnt lgkmcnt(0)
	v_pk_fma_f32 v[30:31], v[2:3], v[8:9], v[20:21] op_sel_hi:[0,1,1]
	v_mov_b32_e32 v8, 0x2bf4
	ds_read2_b32 v[8:9], v8 offset1:1
	s_waitcnt lgkmcnt(0)
	v_pk_fma_f32 v[38:39], v[2:3], v[8:9], v[166:167] op_sel_hi:[0,1,1]
	v_fma_f32 v8, v229, s4, -v124
	v_mul_f32_e32 v9, 0x3fb8aa3b, v8
	v_fma_f32 v20, v8, s5, -v9
	v_rndne_f32_e32 v21, v9
	v_fmac_f32_e32 v20, 0x32a5705f, v8
	v_sub_f32_e32 v9, v9, v21
	v_add_f32_e32 v9, v9, v20
	v_exp_f32_e32 v9, v9
	v_cvt_i32_f32_e32 v20, v21
	v_cmp_ngt_f32_e32 vcc, s6, v8
	v_ldexp_f32 v9, v9, v20
	s_nop 0
	v_cndmask_b32_e32 v9, 0, v9, vcc
	v_cmp_nlt_f32_e32 vcc, s7, v8
	v_mov_b32_e32 v8, 0x2c04
	ds_read2_b32 v[172:173], v8 offset1:1
	v_mov_b32_e32 v8, 0x2c0c
	ds_read2_b32 v[168:169], v8 offset1:1
	v_mov_b32_e32 v8, 0x2c14
	ds_read2_b32 v[180:181], v8 offset1:1
	v_mov_b32_e32 v8, 0x2c1c
	ds_read2_b32 v[176:177], v8 offset1:1
	v_mov_b32_e32 v8, 0x2c24
	ds_read2_b32 v[190:191], v8 offset1:1
	v_mov_b32_e32 v8, 0x2c2c
	ds_read2_b32 v[184:185], v8 offset1:1
	v_mov_b32_e32 v8, 0x2c34
	ds_read2_b32 v[198:199], v8 offset1:1
	v_mov_b32_e32 v8, 0x2c3c
	ds_read2_b32 v[194:195], v8 offset1:1
	v_mov_b32_e32 v8, 0x2c44
	ds_read2_b32 v[210:211], v8 offset1:1
	v_mov_b32_e32 v8, 0x2c4c
	v_cndmask_b32_e32 v166, v103, v9, vcc
	ds_read2_b32 v[202:203], v8 offset1:1
	v_mov_b32_e32 v8, 0x2c54
	v_cmp_ngt_f32_e32 vcc, s6, v109
	ds_read2_b32 v[220:221], v8 offset1:1
	v_mov_b32_e32 v8, 0x2c5c
	v_cndmask_b32_e32 v117, 0, v117, vcc
	v_cmp_nlt_f32_e32 vcc, s7, v109
	v_fma_f32 v109, v111, s4, -v124
	ds_read2_b32 v[216:217], v8 offset1:1
	v_mov_b32_e32 v8, 0x2c64
	v_mul_f32_e32 v111, 0x3fb8aa3b, v109
	ds_read2_b32 v[226:227], v8 offset1:1
	v_mov_b32_e32 v8, 0x2c6c
	v_cndmask_b32_e32 v158, v103, v117, vcc
	v_fma_f32 v117, v109, s5, -v111
	v_rndne_f32_e32 v119, v111
	ds_read2_b32 v[228:229], v8 offset1:1
	v_mov_b32_e32 v8, 0x2c74
	v_fmac_f32_e32 v117, 0x32a5705f, v109
	v_sub_f32_e32 v111, v111, v119
	ds_read2_b32 v[212:213], v8 offset1:1
	v_mov_b32_e32 v8, 0x2c7c
	v_add_f32_e32 v111, v111, v117
	v_pk_fma_f32 v[26:27], v[166:167], v[32:33], v[26:27] op_sel_hi:[0,1,1]
	v_mov_b32_e32 v32, 0x2dd4
	ds_read2_b32 v[230:231], v8 offset1:1
	v_mov_b32_e32 v8, 0x2c84
	v_exp_f32_e32 v111, v111
	v_cvt_i32_f32_e32 v117, v119
	v_pk_fma_f32 v[38:39], v[166:167], v[42:43], v[38:39] op_sel_hi:[0,1,1]
	v_mov_b32_e32 v42, 0x2df4
	ds_read2_b32 v[32:33], v32 offset1:1
	ds_read2_b32 v[234:235], v8 offset1:1
	v_mov_b32_e32 v8, 0x2c8c
	ds_read2_b32 v[42:43], v42 offset1:1
	ds_read2_b32 v[214:215], v8 offset1:1
	v_mov_b32_e32 v8, 0x2c94
	ds_read2_b32 v[242:243], v8 offset1:1
	v_mov_b32_e32 v8, 0x2c9c
	ds_read2_b32 v[238:239], v8 offset1:1
	v_mov_b32_e32 v8, 0x2ca4
	v_ldexp_f32 v111, v111, v117
	v_cmp_ngt_f32_e32 vcc, s6, v109
	ds_read2_b32 v[250:251], v8 offset1:1
	v_mov_b32_e32 v8, 0x2cac
	v_mov_b32_e32 v20, 0x2cbc
	v_cndmask_b32_e32 v111, 0, v111, vcc
	v_cmp_nlt_f32_e32 vcc, s7, v109
	v_fma_f32 v109, v113, s4, -v124
	s_waitcnt lgkmcnt(6)
	v_pk_fma_f32 v[26:27], v[158:159], v[32:33], v[26:27] op_sel_hi:[0,1,1]
	v_mov_b32_e32 v32, 0x2ed4
	ds_read2_b32 v[246:247], v8 offset1:1
	ds_read2_b32 v[254:255], v20 offset1:1
	v_mov_b32_e32 v20, 0x2cc4
	v_cndmask_b32_e32 v156, v103, v111, vcc
	v_mul_f32_e32 v111, 0x3fb8aa3b, v109
	s_waitcnt lgkmcnt(6)
	v_pk_fma_f32 v[38:39], v[158:159], v[42:43], v[38:39] op_sel_hi:[0,1,1]
	v_mov_b32_e32 v42, 0x2ef4
	ds_read2_b32 v[32:33], v32 offset1:1
	ds_read2_b32 v[24:25], v20 offset1:1
	v_fma_f32 v113, v109, s5, -v111
	v_rndne_f32_e32 v117, v111
	ds_read2_b32 v[42:43], v42 offset1:1
	v_fmac_f32_e32 v113, 0x32a5705f, v109
	v_sub_f32_e32 v111, v111, v117
	v_add_f32_e32 v111, v111, v113
	v_exp_f32_e32 v111, v111
	v_cvt_i32_f32_e32 v113, v117
	v_pk_fma_f32 v[30:31], v[166:167], v[36:37], v[30:31] op_sel_hi:[0,1,1]
	v_mov_b32_e32 v36, 0x2dec
	ds_read2_b32 v[36:37], v36 offset1:1
	s_waitcnt lgkmcnt(3)
	v_pk_fma_f32 v[26:27], v[156:157], v[32:33], v[26:27] op_sel_hi:[0,1,1]
	v_mov_b32_e32 v32, 0x2fd4
	s_waitcnt lgkmcnt(1)
	v_pk_fma_f32 v[42:43], v[156:157], v[42:43], v[38:39] op_sel_hi:[0,1,1]
	v_mov_b32_e32 v38, 0x2de4
	ds_read2_b32 v[32:33], v32 offset1:1
	v_pk_fma_f32 v[18:19], v[166:167], v[24:25], v[18:19] op_sel_hi:[0,1,1]
	v_mov_b32_e32 v24, 0x2dc4
	ds_read2_b32 v[38:39], v38 offset1:1
	ds_read2_b32 v[24:25], v24 offset1:1
	v_ldexp_f32 v111, v111, v113
	v_cmp_ngt_f32_e32 vcc, s6, v109
	s_waitcnt lgkmcnt(3)
	v_pk_fma_f32 v[30:31], v[158:159], v[36:37], v[30:31] op_sel_hi:[0,1,1]
	v_mov_b32_e32 v36, 0x2eec
	v_cndmask_b32_e32 v111, 0, v111, vcc
	v_cmp_nlt_f32_e32 vcc, s7, v109
	v_pk_fma_f32 v[34:35], v[166:167], v[40:41], v[34:35] op_sel_hi:[0,1,1]
	ds_read2_b32 v[36:37], v36 offset1:1
	v_cndmask_b32_e32 v154, v103, v111, vcc
	s_waitcnt lgkmcnt(3)
	v_pk_fma_f32 v[40:41], v[154:155], v[32:33], v[26:27] op_sel_hi:[0,1,1]
	v_mov_b32_e32 v26, 0x2fec
	s_waitcnt lgkmcnt(2)
	v_pk_fma_f32 v[34:35], v[158:159], v[38:39], v[34:35] op_sel_hi:[0,1,1]
	v_mov_b32_e32 v38, 0x2ee4
	ds_read2_b32 v[26:27], v26 offset1:1
	s_waitcnt lgkmcnt(2)
	v_pk_fma_f32 v[18:19], v[158:159], v[24:25], v[18:19] op_sel_hi:[0,1,1]
	v_mov_b32_e32 v24, 0x2ec4
	ds_read2_b32 v[38:39], v38 offset1:1
	ds_read2_b32 v[24:25], v24 offset1:1
	s_waitcnt lgkmcnt(3)
	v_pk_fma_f32 v[30:31], v[156:157], v[36:37], v[30:31] op_sel_hi:[0,1,1]
	s_waitcnt lgkmcnt(2)
	v_pk_fma_f32 v[36:37], v[154:155], v[26:27], v[30:31] op_sel_hi:[0,1,1]
	v_mov_b32_e32 v26, 0x2ddc
	s_waitcnt lgkmcnt(1)
	v_pk_fma_f32 v[34:35], v[156:157], v[38:39], v[34:35] op_sel_hi:[0,1,1]
	v_mov_b32_e32 v38, 0x2fe4
	ds_read2_b32 v[26:27], v26 offset1:1
	s_waitcnt lgkmcnt(1)
	v_pk_fma_f32 v[18:19], v[156:157], v[24:25], v[18:19] op_sel_hi:[0,1,1]
	v_mov_b32_e32 v24, 0x2fc4
	ds_read2_b32 v[38:39], v38 offset1:1
	ds_read2_b32 v[24:25], v24 offset1:1
	v_pk_fma_f32 v[22:23], v[166:167], v[28:29], v[22:23] op_sel_hi:[0,1,1]
	s_waitcnt lgkmcnt(2)
	v_pk_fma_f32 v[22:23], v[158:159], v[26:27], v[22:23] op_sel_hi:[0,1,1]
	v_mov_b32_e32 v26, 0x2edc
	s_waitcnt lgkmcnt(1)
	v_pk_fma_f32 v[38:39], v[154:155], v[38:39], v[34:35] op_sel_hi:[0,1,1]
	v_mov_b32_e32 v34, 0x2ff4
	ds_read2_b32 v[26:27], v26 offset1:1
	s_waitcnt lgkmcnt(1)
	v_pk_fma_f32 v[24:25], v[154:155], v[24:25], v[18:19] op_sel_hi:[0,1,1]
	v_mov_b32_e32 v18, 0x2fdc
	ds_read2_b32 v[34:35], v34 offset1:1
	ds_read2_b32 v[18:19], v18 offset1:1
	v_mov_b32_e32 v20, 0x2ccc
	s_waitcnt lgkmcnt(2)
	v_pk_fma_f32 v[22:23], v[156:157], v[26:27], v[22:23] op_sel_hi:[0,1,1]
	ds_read2_b32 v[20:21], v20 offset1:1
	s_waitcnt lgkmcnt(2)
	v_pk_fma_f32 v[34:35], v[154:155], v[34:35], v[42:43] op_sel_hi:[0,1,1]
	s_waitcnt lgkmcnt(1)
	v_pk_fma_f32 v[42:43], v[154:155], v[18:19], v[22:23] op_sel_hi:[0,1,1]
	v_mov_b32_e32 v18, 0x2dcc
	ds_read2_b32 v[18:19], v18 offset1:1
	s_waitcnt lgkmcnt(1)
	v_pk_fma_f32 v[10:11], v[166:167], v[20:21], v[10:11] op_sel_hi:[0,1,1]
	v_mov_b32_e32 v8, 0x2cb4
	ds_read2_b32 v[8:9], v8 offset1:1
	v_mov_b32_e32 v26, 0x2d94
	s_waitcnt lgkmcnt(1)
	v_pk_fma_f32 v[10:11], v[158:159], v[18:19], v[10:11] op_sel_hi:[0,1,1]
	v_mov_b32_e32 v18, 0x2ecc
	ds_read2_b32 v[18:19], v18 offset1:1
	s_waitcnt lgkmcnt(1)
	v_pk_fma_f32 v[8:9], v[166:167], v[8:9], v[252:253] op_sel_hi:[0,1,1]
	ds_read2_b32 v[26:27], v26 offset1:1
	v_fma_f32 v109, v115, s4, -v124
	v_mul_f32_e32 v111, 0x3fb8aa3b, v109
	s_waitcnt lgkmcnt(1)
	v_pk_fma_f32 v[10:11], v[156:157], v[18:19], v[10:11] op_sel_hi:[0,1,1]
	v_mov_b32_e32 v18, 0x2db4
	ds_read2_b32 v[18:19], v18 offset1:1
	v_fma_f32 v113, v109, s5, -v111
	v_rndne_f32_e32 v115, v111
	v_fmac_f32_e32 v113, 0x32a5705f, v109
	v_sub_f32_e32 v111, v111, v115
	s_waitcnt lgkmcnt(0)
	v_pk_fma_f32 v[8:9], v[158:159], v[18:19], v[8:9] op_sel_hi:[0,1,1]
	v_mov_b32_e32 v18, 0x2eb4
	ds_read2_b32 v[18:19], v18 offset1:1
	v_add_f32_e32 v111, v111, v113
	v_exp_f32_e32 v111, v111
	v_cvt_i32_f32_e32 v113, v115
	v_cmp_ngt_f32_e32 vcc, s6, v109
	s_waitcnt lgkmcnt(0)
	v_pk_fma_f32 v[8:9], v[156:157], v[18:19], v[8:9] op_sel_hi:[0,1,1]
	v_mov_b32_e32 v18, 0x2fb4
	ds_read2_b32 v[18:19], v18 offset1:1
	v_ldexp_f32 v111, v111, v113
	v_cndmask_b32_e32 v111, 0, v111, vcc
	v_cmp_nlt_f32_e32 vcc, s7, v109
	v_fma_f32 v109, v116, s4, -v124
	s_waitcnt lgkmcnt(0)
	v_pk_fma_f32 v[20:21], v[154:155], v[18:19], v[8:9] op_sel_hi:[0,1,1]
	v_mov_b32_e32 v8, 0x2fcc
	ds_read2_b32 v[8:9], v8 offset1:1
	v_mov_b32_e32 v18, 0x2da4
	ds_read2_b32 v[18:19], v18 offset1:1
	v_cndmask_b32_e32 v152, v103, v111, vcc
	v_mul_f32_e32 v111, 0x3fb8aa3b, v109
	s_waitcnt lgkmcnt(1)
	v_pk_fma_f32 v[30:31], v[154:155], v[8:9], v[10:11] op_sel_hi:[0,1,1]
	v_mov_b32_e32 v10, 0x2dbc
	ds_read2_b32 v[10:11], v10 offset1:1
	v_pk_fma_f32 v[8:9], v[166:167], v[254:255], v[248:249] op_sel_hi:[0,1,1]
	v_fma_f32 v113, v109, s5, -v111
	v_rndne_f32_e32 v115, v111
	v_fmac_f32_e32 v113, 0x32a5705f, v109
	s_waitcnt lgkmcnt(0)
	v_pk_fma_f32 v[8:9], v[158:159], v[10:11], v[8:9] op_sel_hi:[0,1,1]
	v_mov_b32_e32 v10, 0x2ebc
	ds_read2_b32 v[10:11], v10 offset1:1
	v_sub_f32_e32 v111, v111, v115
	v_add_f32_e32 v111, v111, v113
	v_exp_f32_e32 v111, v111
	v_cvt_i32_f32_e32 v113, v115
	s_waitcnt lgkmcnt(0)
	v_pk_fma_f32 v[8:9], v[156:157], v[10:11], v[8:9] op_sel_hi:[0,1,1]
	v_pk_fma_f32 v[10:11], v[166:167], v[250:251], v[244:245] op_sel_hi:[0,1,1]
	v_pk_fma_f32 v[10:11], v[158:159], v[18:19], v[10:11] op_sel_hi:[0,1,1]
	v_mov_b32_e32 v18, 0x2ea4
	ds_read2_b32 v[18:19], v18 offset1:1
	v_mov_b32_e32 v28, 0x2d9c
	ds_read2_b32 v[28:29], v28 offset1:1
	v_ldexp_f32 v111, v111, v113
	v_cmp_ngt_f32_e32 vcc, s6, v109
	s_waitcnt lgkmcnt(1)
	v_pk_fma_f32 v[10:11], v[156:157], v[18:19], v[10:11] op_sel_hi:[0,1,1]
	v_mov_b32_e32 v18, 0x2fa4
	ds_read2_b32 v[18:19], v18 offset1:1
	v_cndmask_b32_e32 v111, 0, v111, vcc
	v_cmp_nlt_f32_e32 vcc, s7, v109
	v_fma_f32 v109, v118, s4, -v124
	v_mov_b32_e32 v32, 0x2d84
	s_waitcnt lgkmcnt(0)
	v_pk_fma_f32 v[10:11], v[154:155], v[18:19], v[10:11] op_sel_hi:[0,1,1]
	v_mov_b32_e32 v18, 0x2fbc
	ds_read2_b32 v[18:19], v18 offset1:1
	v_cndmask_b32_e32 v150, v103, v111, vcc
	v_mul_f32_e32 v111, 0x3fb8aa3b, v109
	v_fma_f32 v113, v109, s5, -v111
	v_rndne_f32_e32 v115, v111
	s_waitcnt lgkmcnt(0)
	v_pk_fma_f32 v[22:23], v[154:155], v[18:19], v[8:9] op_sel_hi:[0,1,1]
	v_mov_b32_e32 v18, 0x2dac
	ds_read2_b32 v[18:19], v18 offset1:1
	v_pk_fma_f32 v[8:9], v[166:167], v[246:247], v[240:241] op_sel_hi:[0,1,1]
	v_fmac_f32_e32 v113, 0x32a5705f, v109
	v_sub_f32_e32 v111, v111, v115
	v_add_f32_e32 v111, v111, v113
	s_waitcnt lgkmcnt(0)
	v_pk_fma_f32 v[8:9], v[158:159], v[18:19], v[8:9] op_sel_hi:[0,1,1]
	v_mov_b32_e32 v18, 0x2eac
	ds_read2_b32 v[18:19], v18 offset1:1
	v_exp_f32_e32 v111, v111
	v_cvt_i32_f32_e32 v113, v115
	v_cmp_ngt_f32_e32 vcc, s6, v109
	v_add_f32_e32 v46, v46, v166
	s_waitcnt lgkmcnt(0)
	v_pk_fma_f32 v[8:9], v[156:157], v[18:19], v[8:9] op_sel_hi:[0,1,1]
	v_pk_fma_f32 v[18:19], v[166:167], v[242:243], v[236:237] op_sel_hi:[0,1,1]
	v_pk_fma_f32 v[18:19], v[158:159], v[26:27], v[18:19] op_sel_hi:[0,1,1]
	v_mov_b32_e32 v26, 0x2e94
	ds_read2_b32 v[26:27], v26 offset1:1
	v_ldexp_f32 v111, v111, v113
	v_cndmask_b32_e32 v111, 0, v111, vcc
	v_cmp_nlt_f32_e32 vcc, s7, v109
	v_fma_f32 v109, v121, s4, -v124
	s_waitcnt lgkmcnt(0)
	v_pk_fma_f32 v[18:19], v[156:157], v[26:27], v[18:19] op_sel_hi:[0,1,1]
	v_mov_b32_e32 v26, 0x2f94
	ds_read2_b32 v[26:27], v26 offset1:1
	v_cndmask_b32_e32 v148, v103, v111, vcc
	v_mul_f32_e32 v111, 0x3fb8aa3b, v109
	v_fma_f32 v113, v109, s5, -v111
	v_rndne_f32_e32 v115, v111
	s_waitcnt lgkmcnt(0)
	v_pk_fma_f32 v[18:19], v[154:155], v[26:27], v[18:19] op_sel_hi:[0,1,1]
	v_mov_b32_e32 v26, 0x3094
	ds_read2_b32 v[26:27], v26 offset1:1
	v_fmac_f32_e32 v113, 0x32a5705f, v109
	v_sub_f32_e32 v111, v111, v115
	v_add_f32_e32 v111, v111, v113
	v_exp_f32_e32 v111, v111
	s_waitcnt lgkmcnt(0)
	v_pk_fma_f32 v[26:27], v[152:153], v[26:27], v[18:19] op_sel_hi:[0,1,1]
	v_mov_b32_e32 v18, 0x2fac
	ds_read2_b32 v[18:19], v18 offset1:1
	v_cvt_i32_f32_e32 v113, v115
	ds_read2_b32 v[32:33], v32 offset1:1
	v_add_f32_e32 v46, v46, v158
	v_add_f32_e32 v46, v46, v156
	s_waitcnt lgkmcnt(1)
	v_pk_fma_f32 v[8:9], v[154:155], v[18:19], v[8:9] op_sel_hi:[0,1,1]
	v_mov_b32_e32 v18, 0x30a4
	ds_read2_b32 v[18:19], v18 offset1:1
	v_add_f32_e32 v46, v46, v154
	v_add_f32_e32 v46, v46, v152
	v_ldexp_f32 v111, v111, v113
	v_cmp_ngt_f32_e32 vcc, s6, v109
	s_waitcnt lgkmcnt(0)
	v_pk_fma_f32 v[10:11], v[152:153], v[18:19], v[10:11] op_sel_hi:[0,1,1]
	v_mov_b32_e32 v18, 0x30ac
	ds_read2_b32 v[18:19], v18 offset1:1
	v_add_f32_e32 v46, v46, v150
	v_cndmask_b32_e32 v111, 0, v111, vcc
	v_cmp_nlt_f32_e32 vcc, s7, v109
	v_add_f32_e32 v46, v46, v148
	s_waitcnt lgkmcnt(0)
	v_pk_fma_f32 v[18:19], v[152:153], v[18:19], v[8:9] op_sel_hi:[0,1,1]
	v_pk_fma_f32 v[8:9], v[166:167], v[238:239], v[232:233] op_sel_hi:[0,1,1]
	v_pk_fma_f32 v[8:9], v[158:159], v[28:29], v[8:9] op_sel_hi:[0,1,1]
	v_mov_b32_e32 v28, 0x2e9c
	ds_read2_b32 v[28:29], v28 offset1:1
	v_cndmask_b32_e32 v146, v103, v111, vcc
	v_add_f32_e32 v109, v46, v146
	v_fma_f32 v46, v123, s4, -v124
	v_mul_f32_e32 v111, 0x3fb8aa3b, v46
	s_waitcnt lgkmcnt(0)
	v_pk_fma_f32 v[8:9], v[156:157], v[28:29], v[8:9] op_sel_hi:[0,1,1]
	v_mov_b32_e32 v28, 0x2f9c
	ds_read2_b32 v[28:29], v28 offset1:1
	v_fma_f32 v113, v46, s5, -v111
	v_rndne_f32_e32 v115, v111
	v_fmac_f32_e32 v113, 0x32a5705f, v46
	v_sub_f32_e32 v111, v111, v115
	s_waitcnt lgkmcnt(0)
	v_pk_fma_f32 v[8:9], v[154:155], v[28:29], v[8:9] op_sel_hi:[0,1,1]
	v_mov_b32_e32 v28, 0x309c
	ds_read2_b32 v[28:29], v28 offset1:1
	v_add_f32_e32 v111, v111, v113
	v_exp_f32_e32 v111, v111
	v_cvt_i32_f32_e32 v113, v115
	v_cmp_ngt_f32_e32 vcc, s6, v46
	s_waitcnt lgkmcnt(0)
	v_pk_fma_f32 v[8:9], v[152:153], v[28:29], v[8:9] op_sel_hi:[0,1,1]
	v_pk_fma_f32 v[28:29], v[166:167], v[234:235], v[196:197] op_sel_hi:[0,1,1]
	v_pk_fma_f32 v[28:29], v[158:159], v[32:33], v[28:29] op_sel_hi:[0,1,1]
	v_mov_b32_e32 v32, 0x2e84
	ds_read2_b32 v[32:33], v32 offset1:1
	v_ldexp_f32 v111, v111, v113
	v_cndmask_b32_e32 v111, 0, v111, vcc
	v_cmp_nlt_f32_e32 vcc, s7, v46
	v_mov_b32_e32 v46, v44
	s_waitcnt lgkmcnt(0)
	v_pk_fma_f32 v[28:29], v[156:157], v[32:33], v[28:29] op_sel_hi:[0,1,1]
	v_mov_b32_e32 v32, 0x2f84
	ds_read2_b32 v[32:33], v32 offset1:1
	v_pk_fma_f32 v[0:1], v[2:3], v[46:47], v[0:1] op_sel_hi:[0,1,1]
	v_mov_b32_e32 v2, 0x2cfc
	ds_read2_b32 v[46:47], v2 offset1:1
	v_mov_b32_e32 v2, 0x2dfc
	s_waitcnt lgkmcnt(1)
	v_pk_fma_f32 v[28:29], v[154:155], v[32:33], v[28:29] op_sel_hi:[0,1,1]
	v_mov_b32_e32 v32, 0x3084
	ds_read2_b32 v[32:33], v32 offset1:1
	s_waitcnt lgkmcnt(1)
	v_mov_b32_e32 v44, v46
	v_pk_fma_f32 v[0:1], v[166:167], v[44:45], v[0:1] op_sel_hi:[0,1,1]
	ds_read2_b32 v[44:45], v2 offset1:1
	v_mov_b32_e32 v2, 0x2efc
	s_waitcnt lgkmcnt(1)
	v_pk_fma_f32 v[28:29], v[152:153], v[32:33], v[28:29] op_sel_hi:[0,1,1]
	v_mov_b32_e32 v32, 0x30b4
	ds_read2_b32 v[32:33], v32 offset1:1
	s_waitcnt lgkmcnt(1)
	v_mov_b32_e32 v46, v44
	v_pk_fma_f32 v[0:1], v[158:159], v[46:47], v[0:1] op_sel_hi:[0,1,1]
	ds_read2_b32 v[46:47], v2 offset1:1
	v_mov_b32_e32 v2, 0x2ffc
	s_waitcnt lgkmcnt(1)
	v_pk_fma_f32 v[20:21], v[152:153], v[32:33], v[20:21] op_sel_hi:[0,1,1]
	v_mov_b32_e32 v32, 0x30bc
	ds_read2_b32 v[32:33], v32 offset1:1
	s_waitcnt lgkmcnt(1)
	v_mov_b32_e32 v44, v46
	v_pk_fma_f32 v[0:1], v[156:157], v[44:45], v[0:1] op_sel_hi:[0,1,1]
	ds_read2_b32 v[44:45], v2 offset1:1
	v_cndmask_b32_e32 v144, v103, v111, vcc
	s_waitcnt lgkmcnt(1)
	v_pk_fma_f32 v[22:23], v[152:153], v[32:33], v[22:23] op_sel_hi:[0,1,1]
	v_mov_b32_e32 v32, 0x30c4
	ds_read2_b32 v[32:33], v32 offset1:1
	s_waitcnt lgkmcnt(1)
	v_mov_b32_e32 v46, v44
	v_pk_fma_f32 v[46:47], v[154:155], v[46:47], v[0:1] op_sel_hi:[0,1,1]
	v_fma_f32 v1, v120, s4, -v124
	v_mul_f32_e32 v2, 0x3fb8aa3b, v1
	s_waitcnt lgkmcnt(0)
	v_pk_fma_f32 v[24:25], v[152:153], v[32:33], v[24:25] op_sel_hi:[0,1,1]
	v_mov_b32_e32 v32, 0x30cc
	ds_read2_b32 v[32:33], v32 offset1:1
	v_add_f32_e32 v0, v109, v144
	v_fma_f32 v44, v1, s5, -v2
	v_rndne_f32_e32 v109, v2
	v_fmac_f32_e32 v44, 0x32a5705f, v1
	v_sub_f32_e32 v2, v2, v109
	v_add_f32_e32 v2, v2, v44
	s_waitcnt lgkmcnt(0)
	v_pk_fma_f32 v[196:197], v[152:153], v[32:33], v[30:31] op_sel_hi:[0,1,1]
	v_mov_b32_e32 v32, 0x2d8c
	v_exp_f32_e32 v2, v2
	v_cvt_i32_f32_e32 v44, v109
	ds_read2_b32 v[32:33], v32 offset1:1
	v_cmp_ngt_f32_e32 vcc, s6, v1
	v_pk_fma_f32 v[30:31], v[166:167], v[214:215], v[208:209] op_sel_hi:[0,1,1]
	v_ldexp_f32 v2, v2, v44
	v_cndmask_b32_e32 v2, 0, v2, vcc
	v_cmp_nlt_f32_e32 vcc, s7, v1
	s_waitcnt lgkmcnt(0)
	v_pk_fma_f32 v[30:31], v[158:159], v[32:33], v[30:31] op_sel_hi:[0,1,1]
	v_mov_b32_e32 v32, 0x2e8c
	v_cndmask_b32_e32 v2, v103, v2, vcc
	ds_read2_b32 v[32:33], v32 offset1:1
	v_add_f32_e32 v1, v0, v2
	v_fma_f32 v0, v122, s4, -v124
	v_mul_f32_e32 v44, 0x3fb8aa3b, v0
	v_fma_f32 v109, v0, s5, -v44
	v_rndne_f32_e32 v111, v44
	v_fmac_f32_e32 v109, 0x32a5705f, v0
	v_sub_f32_e32 v44, v44, v111
	v_add_f32_e32 v44, v44, v109
	s_waitcnt lgkmcnt(0)
	v_pk_fma_f32 v[30:31], v[156:157], v[32:33], v[30:31] op_sel_hi:[0,1,1]
	v_mov_b32_e32 v32, 0x2f8c
	v_exp_f32_e32 v44, v44
	v_cvt_i32_f32_e32 v109, v111
	ds_read2_b32 v[32:33], v32 offset1:1
	v_cmp_ngt_f32_e32 vcc, s6, v0
	v_ldexp_f32 v44, v44, v109
	s_nop 0
	v_cndmask_b32_e32 v44, 0, v44, vcc
	v_cmp_nlt_f32_e32 vcc, s7, v0
	s_waitcnt lgkmcnt(0)
	v_pk_fma_f32 v[30:31], v[154:155], v[32:33], v[30:31] op_sel_hi:[0,1,1]
	v_mov_b32_e32 v32, 0x308c
	v_cndmask_b32_e32 v0, v103, v44, vcc
	ds_read2_b32 v[32:33], v32 offset1:1
	v_mov_b32_e32 v44, 0x2d74
	ds_read2_b32 v[116:117], v44 offset1:1
	v_mov_b32_e32 v44, 0x2e74
	v_mov_b32_e32 v109, 0x2d4c
	s_waitcnt lgkmcnt(1)
	v_pk_fma_f32 v[30:31], v[152:153], v[32:33], v[30:31] op_sel_hi:[0,1,1]
	v_pk_fma_f32 v[32:33], v[166:167], v[212:213], v[206:207] op_sel_hi:[0,1,1]
	s_waitcnt lgkmcnt(0)
	v_pk_fma_f32 v[32:33], v[158:159], v[116:117], v[32:33] op_sel_hi:[0,1,1]
	ds_read2_b32 v[116:117], v44 offset1:1
	v_mov_b32_e32 v44, 0x2f74
	s_waitcnt lgkmcnt(0)
	v_pk_fma_f32 v[32:33], v[156:157], v[116:117], v[32:33] op_sel_hi:[0,1,1]
	ds_read2_b32 v[116:117], v44 offset1:1
	v_mov_b32_e32 v44, 0x3074
	s_waitcnt lgkmcnt(0)
	v_pk_fma_f32 v[32:33], v[154:155], v[116:117], v[32:33] op_sel_hi:[0,1,1]
	ds_read2_b32 v[116:117], v44 offset1:1
	v_mov_b32_e32 v44, 0x30d4
	s_waitcnt lgkmcnt(0)
	v_pk_fma_f32 v[32:33], v[152:153], v[116:117], v[32:33] op_sel_hi:[0,1,1]
	ds_read2_b32 v[116:117], v44 offset1:1
	s_waitcnt lgkmcnt(0)
	v_pk_fma_f32 v[214:215], v[152:153], v[116:117], v[40:41] op_sel_hi:[0,1,1]
	v_mov_b32_e32 v40, 0x30dc
	ds_read2_b32 v[40:41], v40 offset1:1
	ds_read2_b32 v[116:117], v109 offset1:1
	v_mov_b32_e32 v109, 0x2e4c
	s_waitcnt lgkmcnt(1)
	v_pk_fma_f32 v[212:213], v[152:153], v[40:41], v[42:43] op_sel_hi:[0,1,1]
	v_mov_b32_e32 v40, 0x30e4
	ds_read2_b32 v[40:41], v40 offset1:1
	v_mov_b32_e32 v42, 0x2d54
	ds_read2_b32 v[42:43], v42 offset1:1
	s_waitcnt lgkmcnt(1)
	v_pk_fma_f32 v[206:207], v[152:153], v[40:41], v[38:39] op_sel_hi:[0,1,1]
	v_mov_b32_e32 v38, 0x30ec
	ds_read2_b32 v[38:39], v38 offset1:1
	v_mov_b32_e32 v40, 0x2d64
	ds_read2_b32 v[40:41], v40 offset1:1
	s_waitcnt lgkmcnt(1)
	v_pk_fma_f32 v[208:209], v[152:153], v[38:39], v[36:37] op_sel_hi:[0,1,1]
	v_mov_b32_e32 v38, 0x2d7c
	ds_read2_b32 v[38:39], v38 offset1:1
	v_pk_fma_f32 v[36:37], v[166:167], v[230:231], v[224:225] op_sel_hi:[0,1,1]
	s_waitcnt lgkmcnt(0)
	v_pk_fma_f32 v[36:37], v[158:159], v[38:39], v[36:37] op_sel_hi:[0,1,1]
	v_mov_b32_e32 v38, 0x2e7c
	ds_read2_b32 v[38:39], v38 offset1:1
	s_waitcnt lgkmcnt(0)
	v_pk_fma_f32 v[36:37], v[156:157], v[38:39], v[36:37] op_sel_hi:[0,1,1]
	v_mov_b32_e32 v38, 0x2f7c
	ds_read2_b32 v[38:39], v38 offset1:1
	s_waitcnt lgkmcnt(0)
	v_pk_fma_f32 v[36:37], v[154:155], v[38:39], v[36:37] op_sel_hi:[0,1,1]
	v_mov_b32_e32 v38, 0x307c
	ds_read2_b32 v[38:39], v38 offset1:1
	s_waitcnt lgkmcnt(0)
	v_pk_fma_f32 v[36:37], v[152:153], v[38:39], v[36:37] op_sel_hi:[0,1,1]
	v_pk_fma_f32 v[38:39], v[166:167], v[226:227], v[222:223] op_sel_hi:[0,1,1]
	v_pk_fma_f32 v[38:39], v[158:159], v[40:41], v[38:39] op_sel_hi:[0,1,1]
	v_mov_b32_e32 v40, 0x2e64
	ds_read2_b32 v[40:41], v40 offset1:1
	s_waitcnt lgkmcnt(0)
	v_pk_fma_f32 v[38:39], v[156:157], v[40:41], v[38:39] op_sel_hi:[0,1,1]
	v_mov_b32_e32 v40, 0x2f64
	ds_read2_b32 v[40:41], v40 offset1:1
	s_waitcnt lgkmcnt(0)
	v_pk_fma_f32 v[38:39], v[154:155], v[40:41], v[38:39] op_sel_hi:[0,1,1]
	v_mov_b32_e32 v40, 0x3064
	ds_read2_b32 v[40:41], v40 offset1:1
	s_waitcnt lgkmcnt(0)
	v_pk_fma_f32 v[38:39], v[152:153], v[40:41], v[38:39] op_sel_hi:[0,1,1]
	v_mov_b32_e32 v40, 0x30f4
	ds_read2_b32 v[40:41], v40 offset1:1
	s_waitcnt lgkmcnt(0)
	v_pk_fma_f32 v[226:227], v[152:153], v[40:41], v[34:35] op_sel_hi:[0,1,1]
	v_mov_b32_e32 v40, 0x2d6c
	ds_read2_b32 v[40:41], v40 offset1:1
	v_mov_b32_e32 v34, 0x30fc
	ds_read2_b32 v[222:223], v34 offset1:1
	v_pk_fma_f32 v[34:35], v[166:167], v[228:229], v[218:219] op_sel_hi:[0,1,1]
	s_waitcnt lgkmcnt(1)
	v_pk_fma_f32 v[34:35], v[158:159], v[40:41], v[34:35] op_sel_hi:[0,1,1]
	v_mov_b32_e32 v40, 0x2e6c
	ds_read2_b32 v[40:41], v40 offset1:1
	s_waitcnt lgkmcnt(1)
	v_mov_b32_e32 v44, v222
	v_pk_fma_f32 v[224:225], v[152:153], v[44:45], v[46:47] op_sel_hi:[0,1,1]
	v_mov_b32_e32 v44, 0x2d5c
	ds_read2_b32 v[44:45], v44 offset1:1
	s_waitcnt lgkmcnt(1)
	v_pk_fma_f32 v[34:35], v[156:157], v[40:41], v[34:35] op_sel_hi:[0,1,1]
	v_mov_b32_e32 v40, 0x2f6c
	ds_read2_b32 v[40:41], v40 offset1:1
	v_mov_b32_e32 v46, 0x2d44
	ds_read2_b32 v[46:47], v46 offset1:1
	s_waitcnt lgkmcnt(1)
	v_pk_fma_f32 v[34:35], v[154:155], v[40:41], v[34:35] op_sel_hi:[0,1,1]
	v_mov_b32_e32 v40, 0x306c
	ds_read2_b32 v[40:41], v40 offset1:1
	s_waitcnt lgkmcnt(0)
	v_pk_fma_f32 v[34:35], v[152:153], v[40:41], v[34:35] op_sel_hi:[0,1,1]
	v_pk_fma_f32 v[40:41], v[166:167], v[220:221], v[200:201] op_sel_hi:[0,1,1]
	v_pk_fma_f32 v[40:41], v[158:159], v[42:43], v[40:41] op_sel_hi:[0,1,1]
	v_mov_b32_e32 v42, 0x2e54
	ds_read2_b32 v[42:43], v42 offset1:1
	s_waitcnt lgkmcnt(0)
	v_pk_fma_f32 v[40:41], v[156:157], v[42:43], v[40:41] op_sel_hi:[0,1,1]
	v_mov_b32_e32 v42, 0x2f54
	ds_read2_b32 v[42:43], v42 offset1:1
	s_waitcnt lgkmcnt(0)
	v_pk_fma_f32 v[40:41], v[154:155], v[42:43], v[40:41] op_sel_hi:[0,1,1]
	v_mov_b32_e32 v42, 0x3054
	ds_read2_b32 v[42:43], v42 offset1:1
	s_waitcnt lgkmcnt(0)
	v_pk_fma_f32 v[40:41], v[152:153], v[42:43], v[40:41] op_sel_hi:[0,1,1]
	v_pk_fma_f32 v[42:43], v[166:167], v[216:217], v[204:205] op_sel_hi:[0,1,1]
	v_pk_fma_f32 v[42:43], v[158:159], v[44:45], v[42:43] op_sel_hi:[0,1,1]
	v_mov_b32_e32 v44, 0x2e5c
	ds_read2_b32 v[44:45], v44 offset1:1
	s_waitcnt lgkmcnt(0)
	v_pk_fma_f32 v[42:43], v[156:157], v[44:45], v[42:43] op_sel_hi:[0,1,1]
	v_mov_b32_e32 v44, 0x2f5c
	ds_read2_b32 v[44:45], v44 offset1:1
	s_waitcnt lgkmcnt(0)
	v_pk_fma_f32 v[42:43], v[154:155], v[44:45], v[42:43] op_sel_hi:[0,1,1]
	v_mov_b32_e32 v44, 0x305c
	ds_read2_b32 v[44:45], v44 offset1:1
	s_waitcnt lgkmcnt(0)
	v_pk_fma_f32 v[42:43], v[152:153], v[44:45], v[42:43] op_sel_hi:[0,1,1]
	v_pk_fma_f32 v[44:45], v[166:167], v[210:211], v[192:193] op_sel_hi:[0,1,1]
	v_pk_fma_f32 v[44:45], v[158:159], v[46:47], v[44:45] op_sel_hi:[0,1,1]
	v_mov_b32_e32 v46, 0x2e44
	ds_read2_b32 v[46:47], v46 offset1:1
	s_waitcnt lgkmcnt(0)
	v_pk_fma_f32 v[44:45], v[156:157], v[46:47], v[44:45] op_sel_hi:[0,1,1]
	v_mov_b32_e32 v46, 0x2f44
	ds_read2_b32 v[46:47], v46 offset1:1
	s_waitcnt lgkmcnt(0)
	v_pk_fma_f32 v[44:45], v[154:155], v[46:47], v[44:45] op_sel_hi:[0,1,1]
	v_mov_b32_e32 v46, 0x3044
	ds_read2_b32 v[46:47], v46 offset1:1
	s_waitcnt lgkmcnt(0)
	v_pk_fma_f32 v[44:45], v[152:153], v[46:47], v[44:45] op_sel_hi:[0,1,1]
	v_pk_fma_f32 v[46:47], v[166:167], v[202:203], v[188:189] op_sel_hi:[0,1,1]
	v_pk_fma_f32 v[46:47], v[158:159], v[116:117], v[46:47] op_sel_hi:[0,1,1]
	ds_read2_b32 v[116:117], v109 offset1:1
	v_mov_b32_e32 v109, 0x2f4c
	s_waitcnt lgkmcnt(0)
	v_pk_fma_f32 v[46:47], v[156:157], v[116:117], v[46:47] op_sel_hi:[0,1,1]
	ds_read2_b32 v[116:117], v109 offset1:1
	v_mov_b32_e32 v109, 0x304c
	s_waitcnt lgkmcnt(0)
	v_pk_fma_f32 v[46:47], v[154:155], v[116:117], v[46:47] op_sel_hi:[0,1,1]
	ds_read2_b32 v[116:117], v109 offset1:1
	v_mov_b32_e32 v109, 0x2d34
	ds_read2_b32 v[118:119], v109 offset1:1
	v_mov_b32_e32 v109, 0x2e34
	s_waitcnt lgkmcnt(1)
	v_pk_fma_f32 v[46:47], v[152:153], v[116:117], v[46:47] op_sel_hi:[0,1,1]
	v_pk_fma_f32 v[116:117], v[166:167], v[198:199], v[186:187] op_sel_hi:[0,1,1]
	s_waitcnt lgkmcnt(0)
	v_pk_fma_f32 v[116:117], v[158:159], v[118:119], v[116:117] op_sel_hi:[0,1,1]
	ds_read2_b32 v[118:119], v109 offset1:1
	v_mov_b32_e32 v109, 0x2f34
	s_waitcnt lgkmcnt(0)
	v_pk_fma_f32 v[116:117], v[156:157], v[118:119], v[116:117] op_sel_hi:[0,1,1]
	ds_read2_b32 v[118:119], v109 offset1:1
	v_mov_b32_e32 v109, 0x3034
	s_waitcnt lgkmcnt(0)
	v_pk_fma_f32 v[116:117], v[154:155], v[118:119], v[116:117] op_sel_hi:[0,1,1]
	ds_read2_b32 v[118:119], v109 offset1:1
	v_mov_b32_e32 v109, 0x3134
	s_waitcnt lgkmcnt(0)
	v_pk_fma_f32 v[116:117], v[152:153], v[118:119], v[116:117] op_sel_hi:[0,1,1]
	ds_read2_b32 v[118:119], v109 offset1:1
	v_mov_b32_e32 v109, 0x2d3c
	s_waitcnt lgkmcnt(0)
	v_pk_fma_f32 v[186:187], v[150:151], v[118:119], v[116:117] op_sel_hi:[0,1,1]
	ds_read2_b32 v[118:119], v109 offset1:1
	v_pk_fma_f32 v[116:117], v[166:167], v[194:195], v[182:183] op_sel_hi:[0,1,1]
	v_mov_b32_e32 v109, 0x2e3c
	s_waitcnt lgkmcnt(0)
	v_pk_fma_f32 v[116:117], v[158:159], v[118:119], v[116:117] op_sel_hi:[0,1,1]
	ds_read2_b32 v[118:119], v109 offset1:1
	v_mov_b32_e32 v109, 0x2f3c
	s_waitcnt lgkmcnt(0)
	v_pk_fma_f32 v[116:117], v[156:157], v[118:119], v[116:117] op_sel_hi:[0,1,1]
	ds_read2_b32 v[118:119], v109 offset1:1
	v_mov_b32_e32 v109, 0x303c
	s_waitcnt lgkmcnt(0)
	v_pk_fma_f32 v[116:117], v[154:155], v[118:119], v[116:117] op_sel_hi:[0,1,1]
	ds_read2_b32 v[118:119], v109 offset1:1
	v_mov_b32_e32 v109, 0x313c
	s_waitcnt lgkmcnt(0)
	v_pk_fma_f32 v[116:117], v[152:153], v[118:119], v[116:117] op_sel_hi:[0,1,1]
	ds_read2_b32 v[118:119], v109 offset1:1
	v_mov_b32_e32 v109, 0x2d24
	s_waitcnt lgkmcnt(0)
	v_pk_fma_f32 v[182:183], v[150:151], v[118:119], v[116:117] op_sel_hi:[0,1,1]
	ds_read2_b32 v[118:119], v109 offset1:1
	v_pk_fma_f32 v[116:117], v[166:167], v[190:191], v[178:179] op_sel_hi:[0,1,1]
	v_mov_b32_e32 v109, 0x2e24
	s_waitcnt lgkmcnt(0)
	v_pk_fma_f32 v[116:117], v[158:159], v[118:119], v[116:117] op_sel_hi:[0,1,1]
	ds_read2_b32 v[118:119], v109 offset1:1
	v_mov_b32_e32 v109, 0x2f24
	s_waitcnt lgkmcnt(0)
	v_pk_fma_f32 v[116:117], v[156:157], v[118:119], v[116:117] op_sel_hi:[0,1,1]
	ds_read2_b32 v[118:119], v109 offset1:1
	v_mov_b32_e32 v109, 0x3024
	s_waitcnt lgkmcnt(0)
	v_pk_fma_f32 v[116:117], v[154:155], v[118:119], v[116:117] op_sel_hi:[0,1,1]
	ds_read2_b32 v[118:119], v109 offset1:1
	v_mov_b32_e32 v109, 0x3124
	s_waitcnt lgkmcnt(0)
	v_pk_fma_f32 v[116:117], v[152:153], v[118:119], v[116:117] op_sel_hi:[0,1,1]
	ds_read2_b32 v[118:119], v109 offset1:1
	v_mov_b32_e32 v109, 0x3144
	s_waitcnt lgkmcnt(0)
	v_pk_fma_f32 v[198:199], v[150:151], v[118:119], v[116:117] op_sel_hi:[0,1,1]
	ds_read2_b32 v[116:117], v109 offset1:1
	v_mov_b32_e32 v109, 0x3564
	s_waitcnt lgkmcnt(0)
	v_pk_fma_f32 v[192:193], v[150:151], v[116:117], v[44:45] op_sel_hi:[0,1,1]
	v_mov_b32_e32 v44, 0x314c
	ds_read2_b32 v[44:45], v44 offset1:1
	s_waitcnt lgkmcnt(0)
	v_pk_fma_f32 v[194:195], v[150:151], v[44:45], v[46:47] op_sel_hi:[0,1,1]
	v_mov_b32_e32 v44, 0x3154
	ds_read2_b32 v[44:45], v44 offset1:1
	s_waitcnt lgkmcnt(0)
	v_pk_fma_f32 v[190:191], v[150:151], v[44:45], v[40:41] op_sel_hi:[0,1,1]
	v_mov_b32_e32 v40, 0x315c
	ds_read2_b32 v[40:41], v40 offset1:1
	s_waitcnt lgkmcnt(0)
	v_pk_fma_f32 v[188:189], v[150:151], v[40:41], v[42:43] op_sel_hi:[0,1,1]
	v_mov_b32_e32 v40, 0x3164
	ds_read2_b32 v[40:41], v40 offset1:1
	s_waitcnt lgkmcnt(0)
	v_pk_fma_f32 v[178:179], v[150:151], v[40:41], v[38:39] op_sel_hi:[0,1,1]
	v_mov_b32_e32 v40, 0x2d2c
	ds_read2_b32 v[40:41], v40 offset1:1
	v_pk_fma_f32 v[38:39], v[166:167], v[184:185], v[174:175] op_sel_hi:[0,1,1]
	s_waitcnt lgkmcnt(0)
	v_pk_fma_f32 v[38:39], v[158:159], v[40:41], v[38:39] op_sel_hi:[0,1,1]
	v_mov_b32_e32 v40, 0x2e2c
	ds_read2_b32 v[40:41], v40 offset1:1
	s_waitcnt lgkmcnt(0)
	v_pk_fma_f32 v[38:39], v[156:157], v[40:41], v[38:39] op_sel_hi:[0,1,1]
	v_mov_b32_e32 v40, 0x2f2c
	ds_read2_b32 v[40:41], v40 offset1:1
	s_waitcnt lgkmcnt(0)
	v_pk_fma_f32 v[38:39], v[154:155], v[40:41], v[38:39] op_sel_hi:[0,1,1]
	v_mov_b32_e32 v40, 0x302c
	ds_read2_b32 v[40:41], v40 offset1:1
	s_waitcnt lgkmcnt(0)
	v_pk_fma_f32 v[38:39], v[152:153], v[40:41], v[38:39] op_sel_hi:[0,1,1]
	v_mov_b32_e32 v40, 0x312c
	ds_read2_b32 v[40:41], v40 offset1:1
	s_waitcnt lgkmcnt(0)
	v_pk_fma_f32 v[200:201], v[150:151], v[40:41], v[38:39] op_sel_hi:[0,1,1]
	v_mov_b32_e32 v38, 0x316c
	ds_read2_b32 v[38:39], v38 offset1:1
	s_waitcnt lgkmcnt(0)
	v_pk_fma_f32 v[174:175], v[150:151], v[38:39], v[34:35] op_sel_hi:[0,1,1]
	v_mov_b32_e32 v38, 0x2d14
	ds_read2_b32 v[38:39], v38 offset1:1
	v_pk_fma_f32 v[34:35], v[166:167], v[180:181], v[170:171] op_sel_hi:[0,1,1]
	s_waitcnt lgkmcnt(0)
	v_pk_fma_f32 v[34:35], v[158:159], v[38:39], v[34:35] op_sel_hi:[0,1,1]
	v_mov_b32_e32 v38, 0x2e14
	ds_read2_b32 v[38:39], v38 offset1:1
	s_waitcnt lgkmcnt(0)
	v_pk_fma_f32 v[34:35], v[156:157], v[38:39], v[34:35] op_sel_hi:[0,1,1]
	v_mov_b32_e32 v38, 0x2f14
	ds_read2_b32 v[38:39], v38 offset1:1
	s_waitcnt lgkmcnt(0)
	v_pk_fma_f32 v[34:35], v[154:155], v[38:39], v[34:35] op_sel_hi:[0,1,1]
	v_mov_b32_e32 v38, 0x3014
	ds_read2_b32 v[38:39], v38 offset1:1
	s_waitcnt lgkmcnt(0)
	v_pk_fma_f32 v[34:35], v[152:153], v[38:39], v[34:35] op_sel_hi:[0,1,1]
	v_mov_b32_e32 v38, 0x3114
	ds_read2_b32 v[38:39], v38 offset1:1
	s_waitcnt lgkmcnt(0)
	v_pk_fma_f32 v[210:211], v[150:151], v[38:39], v[34:35] op_sel_hi:[0,1,1]
	v_mov_b32_e32 v34, 0x3174
	ds_read2_b32 v[34:35], v34 offset1:1
	s_waitcnt lgkmcnt(0)
	v_pk_fma_f32 v[204:205], v[150:151], v[34:35], v[32:33] op_sel_hi:[0,1,1]
	v_mov_b32_e32 v32, 0x317c
	ds_read2_b32 v[32:33], v32 offset1:1
	s_waitcnt lgkmcnt(0)
	v_pk_fma_f32 v[202:203], v[150:151], v[32:33], v[36:37] op_sel_hi:[0,1,1]
	v_mov_b32_e32 v32, 0x3184
	ds_read2_b32 v[32:33], v32 offset1:1
	s_waitcnt lgkmcnt(0)
	v_pk_fma_f32 v[180:181], v[150:151], v[32:33], v[28:29] op_sel_hi:[0,1,1]
	v_mov_b32_e32 v28, 0x318c
	ds_read2_b32 v[28:29], v28 offset1:1
	s_waitcnt lgkmcnt(0)
	v_pk_fma_f32 v[184:185], v[150:151], v[28:29], v[30:31] op_sel_hi:[0,1,1]
	v_mov_b32_e32 v28, 0x3194
	ds_read2_b32 v[28:29], v28 offset1:1
	s_waitcnt lgkmcnt(0)
	v_pk_fma_f32 v[170:171], v[150:151], v[28:29], v[26:27] op_sel_hi:[0,1,1]
	v_mov_b32_e32 v28, 0x2d1c
	ds_read2_b32 v[28:29], v28 offset1:1
	v_pk_fma_f32 v[26:27], v[166:167], v[176:177], v[164:165] op_sel_hi:[0,1,1]
	s_waitcnt lgkmcnt(0)
	v_pk_fma_f32 v[26:27], v[158:159], v[28:29], v[26:27] op_sel_hi:[0,1,1]
	v_mov_b32_e32 v28, 0x2e1c
	ds_read2_b32 v[28:29], v28 offset1:1
	s_waitcnt lgkmcnt(0)
	v_pk_fma_f32 v[26:27], v[156:157], v[28:29], v[26:27] op_sel_hi:[0,1,1]
	v_mov_b32_e32 v28, 0x2f1c
	ds_read2_b32 v[28:29], v28 offset1:1
	s_waitcnt lgkmcnt(0)
	v_pk_fma_f32 v[26:27], v[154:155], v[28:29], v[26:27] op_sel_hi:[0,1,1]
	v_mov_b32_e32 v28, 0x301c
	ds_read2_b32 v[28:29], v28 offset1:1
	s_waitcnt lgkmcnt(0)
	v_pk_fma_f32 v[26:27], v[152:153], v[28:29], v[26:27] op_sel_hi:[0,1,1]
	v_mov_b32_e32 v28, 0x311c
	ds_read2_b32 v[28:29], v28 offset1:1
	s_waitcnt lgkmcnt(0)
	v_pk_fma_f32 v[220:221], v[150:151], v[28:29], v[26:27] op_sel_hi:[0,1,1]
	v_mov_b32_e32 v26, 0x319c
	ds_read2_b32 v[26:27], v26 offset1:1
	s_waitcnt lgkmcnt(0)
	v_pk_fma_f32 v[164:165], v[150:151], v[26:27], v[8:9] op_sel_hi:[0,1,1]
	v_mov_b32_e32 v26, 0x2d04
	ds_read2_b32 v[26:27], v26 offset1:1
	v_pk_fma_f32 v[8:9], v[166:167], v[172:173], v[162:163] op_sel_hi:[0,1,1]
	s_waitcnt lgkmcnt(0)
	v_pk_fma_f32 v[8:9], v[158:159], v[26:27], v[8:9] op_sel_hi:[0,1,1]
	v_mov_b32_e32 v26, 0x2e04
	ds_read2_b32 v[26:27], v26 offset1:1
	s_waitcnt lgkmcnt(0)
	v_pk_fma_f32 v[8:9], v[156:157], v[26:27], v[8:9] op_sel_hi:[0,1,1]
	v_mov_b32_e32 v26, 0x2f04
	ds_read2_b32 v[26:27], v26 offset1:1
	s_waitcnt lgkmcnt(0)
	v_pk_fma_f32 v[8:9], v[154:155], v[26:27], v[8:9] op_sel_hi:[0,1,1]
	v_mov_b32_e32 v26, 0x3004
	ds_read2_b32 v[26:27], v26 offset1:1
	s_waitcnt lgkmcnt(0)
	v_pk_fma_f32 v[8:9], v[152:153], v[26:27], v[8:9] op_sel_hi:[0,1,1]
	v_mov_b32_e32 v26, 0x3104
	ds_read2_b32 v[26:27], v26 offset1:1
	s_waitcnt lgkmcnt(0)
	v_pk_fma_f32 v[8:9], v[150:151], v[26:27], v[8:9] op_sel_hi:[0,1,1]
	v_mov_b32_e32 v26, 0x31a4
	ds_read2_b32 v[26:27], v26 offset1:1
	s_waitcnt lgkmcnt(0)
	v_pk_fma_f32 v[216:217], v[150:151], v[26:27], v[10:11] op_sel_hi:[0,1,1]
	v_mov_b32_e32 v10, 0x31ac
	ds_read2_b32 v[10:11], v10 offset1:1
	s_waitcnt lgkmcnt(0)
	v_pk_fma_f32 v[218:219], v[150:151], v[10:11], v[18:19] op_sel_hi:[0,1,1]
	v_mov_b32_e32 v10, 0x31b4
	ds_read2_b32 v[10:11], v10 offset1:1
	v_mov_b32_e32 v18, 0x2d0c
	ds_read2_b32 v[18:19], v18 offset1:1
	s_waitcnt lgkmcnt(1)
	v_pk_fma_f32 v[176:177], v[150:151], v[10:11], v[20:21] op_sel_hi:[0,1,1]
	v_mov_b32_e32 v10, 0x31bc
	ds_read2_b32 v[10:11], v10 offset1:1
	s_waitcnt lgkmcnt(0)
	v_pk_fma_f32 v[172:173], v[150:151], v[10:11], v[22:23] op_sel_hi:[0,1,1]
	v_mov_b32_e32 v10, 0x31c4
	ds_read2_b32 v[10:11], v10 offset1:1
	s_waitcnt lgkmcnt(0)
	v_pk_fma_f32 v[162:163], v[150:151], v[10:11], v[24:25] op_sel_hi:[0,1,1]
	v_pk_fma_f32 v[10:11], v[166:167], v[168:169], v[160:161] op_sel_hi:[0,1,1]
	v_pk_fma_f32 v[10:11], v[158:159], v[18:19], v[10:11] op_sel_hi:[0,1,1]
	v_mov_b32_e32 v18, 0x2e0c
	ds_read2_b32 v[18:19], v18 offset1:1
	s_waitcnt lgkmcnt(0)
	v_pk_fma_f32 v[10:11], v[156:157], v[18:19], v[10:11] op_sel_hi:[0,1,1]
	v_mov_b32_e32 v18, 0x2f0c
	ds_read2_b32 v[18:19], v18 offset1:1
	s_waitcnt lgkmcnt(0)
	v_pk_fma_f32 v[10:11], v[154:155], v[18:19], v[10:11] op_sel_hi:[0,1,1]
	v_mov_b32_e32 v18, 0x300c
	ds_read2_b32 v[18:19], v18 offset1:1
	s_waitcnt lgkmcnt(0)
	v_pk_fma_f32 v[10:11], v[152:153], v[18:19], v[10:11] op_sel_hi:[0,1,1]
	v_mov_b32_e32 v18, 0x310c
	ds_read2_b32 v[18:19], v18 offset1:1
	s_waitcnt lgkmcnt(0)
	v_pk_fma_f32 v[32:33], v[150:151], v[18:19], v[10:11] op_sel_hi:[0,1,1]
	v_mov_b32_e32 v18, 0x31d4
	ds_read2_b32 v[18:19], v18 offset1:1
	v_mov_b32_e32 v10, 0x31cc
	ds_read2_b32 v[10:11], v10 offset1:1
	s_waitcnt lgkmcnt(1)
	v_pk_fma_f32 v[20:21], v[150:151], v[18:19], v[214:215] op_sel_hi:[0,1,1]
	v_mov_b32_e32 v18, 0x31dc
	ds_read2_b32 v[18:19], v18 offset1:1
	s_waitcnt lgkmcnt(1)
	v_pk_fma_f32 v[10:11], v[150:151], v[10:11], v[196:197] op_sel_hi:[0,1,1]
	s_waitcnt lgkmcnt(0)
	v_pk_fma_f32 v[22:23], v[150:151], v[18:19], v[212:213] op_sel_hi:[0,1,1]
	v_mov_b32_e32 v18, 0x31e4
	ds_read2_b32 v[18:19], v18 offset1:1
	s_waitcnt lgkmcnt(0)
	v_pk_fma_f32 v[24:25], v[150:151], v[18:19], v[206:207] op_sel_hi:[0,1,1]
	v_mov_b32_e32 v18, 0x31ec
	ds_read2_b32 v[18:19], v18 offset1:1
	s_waitcnt lgkmcnt(0)
	v_pk_fma_f32 v[26:27], v[150:151], v[18:19], v[208:209] op_sel_hi:[0,1,1]
	v_mov_b32_e32 v18, 0x31f4
	ds_read2_b32 v[18:19], v18 offset1:1
	s_waitcnt lgkmcnt(0)
	v_pk_fma_f32 v[28:29], v[150:151], v[18:19], v[226:227] op_sel_hi:[0,1,1]
	v_mov_b32_e32 v18, 0x31fc
	ds_read2_b32 v[18:19], v18 offset1:1
	s_waitcnt lgkmcnt(0)
	v_mov_b32_e32 v222, v18
	v_mov_b32_e32 v18, 0x3204
	ds_read2_b32 v[34:35], v18 offset1:1
	v_mov_b32_e32 v18, 0x320c
	v_pk_fma_f32 v[30:31], v[150:151], v[222:223], v[224:225] op_sel_hi:[0,1,1]
	s_waitcnt lgkmcnt(0)
	v_pk_fma_f32 v[8:9], v[148:149], v[34:35], v[8:9] op_sel_hi:[0,1,1]
	ds_read2_b32 v[34:35], v18 offset1:1
	v_mov_b32_e32 v18, 0x3214
	s_waitcnt lgkmcnt(0)
	v_pk_fma_f32 v[32:33], v[148:149], v[34:35], v[32:33] op_sel_hi:[0,1,1]
	ds_read2_b32 v[34:35], v18 offset1:1
	v_mov_b32_e32 v18, 0x321c
	ds_read2_b32 v[36:37], v18 offset1:1
	v_mov_b32_e32 v18, 0x3224
	ds_read2_b32 v[38:39], v18 offset1:1
	v_mov_b32_e32 v18, 0x322c
	ds_read2_b32 v[40:41], v18 offset1:1
	v_mov_b32_e32 v18, 0x3234
	ds_read2_b32 v[42:43], v18 offset1:1
	v_mov_b32_e32 v18, 0x323c
	ds_read2_b32 v[44:45], v18 offset1:1
	v_mov_b32_e32 v18, 0x3244
	ds_read2_b32 v[46:47], v18 offset1:1
	v_mov_b32_e32 v18, 0x324c
	ds_read2_b32 v[116:117], v18 offset1:1
	v_mov_b32_e32 v18, 0x3254
	s_waitcnt lgkmcnt(2)
	v_pk_fma_f32 v[44:45], v[148:149], v[44:45], v[182:183] op_sel_hi:[0,1,1]
	v_pk_fma_f32 v[34:35], v[148:149], v[34:35], v[210:211] op_sel_hi:[0,1,1]
	v_pk_fma_f32 v[36:37], v[148:149], v[36:37], v[220:221] op_sel_hi:[0,1,1]
	s_waitcnt lgkmcnt(0)
	v_pk_fma_f32 v[150:151], v[148:149], v[116:117], v[194:195] op_sel_hi:[0,1,1]
	ds_read2_b32 v[116:117], v18 offset1:1
	v_mov_b32_e32 v18, 0x325c
	v_pk_fma_f32 v[38:39], v[148:149], v[38:39], v[198:199] op_sel_hi:[0,1,1]
	v_pk_fma_f32 v[40:41], v[148:149], v[40:41], v[200:201] op_sel_hi:[0,1,1]
	v_pk_fma_f32 v[42:43], v[148:149], v[42:43], v[186:187] op_sel_hi:[0,1,1]
	s_waitcnt lgkmcnt(0)
	v_pk_fma_f32 v[152:153], v[148:149], v[116:117], v[190:191] op_sel_hi:[0,1,1]
	ds_read2_b32 v[116:117], v18 offset1:1
	v_mov_b32_e32 v18, 0x3264
	v_pk_fma_f32 v[46:47], v[148:149], v[46:47], v[192:193] op_sel_hi:[0,1,1]
	s_waitcnt lgkmcnt(0)
	v_pk_fma_f32 v[154:155], v[148:149], v[116:117], v[188:189] op_sel_hi:[0,1,1]
	ds_read2_b32 v[116:117], v18 offset1:1
	v_mov_b32_e32 v18, 0x326c
	s_waitcnt lgkmcnt(0)
	v_pk_fma_f32 v[156:157], v[148:149], v[116:117], v[178:179] op_sel_hi:[0,1,1]
	ds_read2_b32 v[116:117], v18 offset1:1
	v_mov_b32_e32 v18, 0x3274
	s_waitcnt lgkmcnt(0)
	v_pk_fma_f32 v[158:159], v[148:149], v[116:117], v[174:175] op_sel_hi:[0,1,1]
	ds_read2_b32 v[116:117], v18 offset1:1
	v_mov_b32_e32 v18, 0x327c
	s_waitcnt lgkmcnt(0)
	v_pk_fma_f32 v[160:161], v[148:149], v[116:117], v[204:205] op_sel_hi:[0,1,1]
	ds_read2_b32 v[116:117], v18 offset1:1
	v_mov_b32_e32 v18, 0x3284
	s_waitcnt lgkmcnt(0)
	v_pk_fma_f32 v[166:167], v[148:149], v[116:117], v[202:203] op_sel_hi:[0,1,1]
	ds_read2_b32 v[116:117], v18 offset1:1
	v_mov_b32_e32 v18, 0x328c
	s_waitcnt lgkmcnt(0)
	v_pk_fma_f32 v[168:169], v[148:149], v[116:117], v[180:181] op_sel_hi:[0,1,1]
	ds_read2_b32 v[116:117], v18 offset1:1
	v_mov_b32_e32 v18, 0x3294
	s_waitcnt lgkmcnt(0)
	v_pk_fma_f32 v[174:175], v[148:149], v[116:117], v[184:185] op_sel_hi:[0,1,1]
	ds_read2_b32 v[116:117], v18 offset1:1
	v_mov_b32_e32 v18, 0x329c
	s_waitcnt lgkmcnt(0)
	v_pk_fma_f32 v[170:171], v[148:149], v[116:117], v[170:171] op_sel_hi:[0,1,1]
	ds_read2_b32 v[116:117], v18 offset1:1
	v_mov_b32_e32 v18, 0x32a4
	s_waitcnt lgkmcnt(0)
	v_pk_fma_f32 v[164:165], v[148:149], v[116:117], v[164:165] op_sel_hi:[0,1,1]
	ds_read2_b32 v[116:117], v18 offset1:1
	v_mov_b32_e32 v18, 0x32ac
	s_waitcnt lgkmcnt(0)
	v_pk_fma_f32 v[178:179], v[148:149], v[116:117], v[216:217] op_sel_hi:[0,1,1]
	ds_read2_b32 v[116:117], v18 offset1:1
	v_mov_b32_e32 v18, 0x32b4
	s_waitcnt lgkmcnt(0)
	v_pk_fma_f32 v[180:181], v[148:149], v[116:117], v[218:219] op_sel_hi:[0,1,1]
	ds_read2_b32 v[116:117], v18 offset1:1
	v_mov_b32_e32 v18, 0x32bc
	s_waitcnt lgkmcnt(0)
	v_pk_fma_f32 v[176:177], v[148:149], v[116:117], v[176:177] op_sel_hi:[0,1,1]
	ds_read2_b32 v[116:117], v18 offset1:1
	v_mov_b32_e32 v18, 0x32c4
	s_waitcnt lgkmcnt(0)
	v_pk_fma_f32 v[172:173], v[148:149], v[116:117], v[172:173] op_sel_hi:[0,1,1]
	ds_read2_b32 v[116:117], v18 offset1:1
	v_mov_b32_e32 v18, 0x32cc
	s_waitcnt lgkmcnt(0)
	v_pk_fma_f32 v[162:163], v[148:149], v[116:117], v[162:163] op_sel_hi:[0,1,1]
	ds_read2_b32 v[116:117], v18 offset1:1
	s_waitcnt lgkmcnt(0)
	v_pk_fma_f32 v[182:183], v[148:149], v[116:117], v[10:11] op_sel_hi:[0,1,1]
	v_mov_b32_e32 v10, 0x32d4
	ds_read2_b32 v[10:11], v10 offset1:1
	s_waitcnt lgkmcnt(0)
	v_pk_fma_f32 v[20:21], v[148:149], v[10:11], v[20:21] op_sel_hi:[0,1,1]
	v_mov_b32_e32 v10, 0x32dc
	ds_read2_b32 v[10:11], v10 offset1:1
	s_waitcnt lgkmcnt(0)
	v_pk_fma_f32 v[22:23], v[148:149], v[10:11], v[22:23] op_sel_hi:[0,1,1]
	v_mov_b32_e32 v10, 0x32e4
	ds_read2_b32 v[10:11], v10 offset1:1
	s_waitcnt lgkmcnt(0)
	v_pk_fma_f32 v[24:25], v[148:149], v[10:11], v[24:25] op_sel_hi:[0,1,1]
	v_mov_b32_e32 v10, 0x32ec
	ds_read2_b32 v[10:11], v10 offset1:1
	s_waitcnt lgkmcnt(0)
	v_pk_fma_f32 v[26:27], v[148:149], v[10:11], v[26:27] op_sel_hi:[0,1,1]
	v_mov_b32_e32 v10, 0x32f4
	ds_read2_b32 v[10:11], v10 offset1:1
	s_waitcnt lgkmcnt(0)
	v_pk_fma_f32 v[28:29], v[148:149], v[10:11], v[28:29] op_sel_hi:[0,1,1]
	v_mov_b32_e32 v10, 0x32fc
	ds_read2_b32 v[10:11], v10 offset1:1
	s_waitcnt lgkmcnt(0)
	v_mov_b32_e32 v18, v10
	v_mov_b32_e32 v10, 0x3304
	v_pk_fma_f32 v[18:19], v[148:149], v[18:19], v[30:31] op_sel_hi:[0,1,1]
	ds_read2_b32 v[30:31], v10 offset1:1
	s_waitcnt lgkmcnt(0)
	v_pk_fma_f32 v[30:31], v[146:147], v[30:31], v[8:9] op_sel_hi:[0,1,1]
	v_mov_b32_e32 v8, 0x330c
	ds_read2_b32 v[8:9], v8 offset1:1
	s_waitcnt lgkmcnt(0)
	v_pk_fma_f32 v[32:33], v[146:147], v[8:9], v[32:33] op_sel_hi:[0,1,1]
	v_mov_b32_e32 v8, 0x3314
	ds_read2_b32 v[8:9], v8 offset1:1
	s_waitcnt lgkmcnt(0)
	v_pk_fma_f32 v[34:35], v[146:147], v[8:9], v[34:35] op_sel_hi:[0,1,1]
	v_mov_b32_e32 v8, 0x331c
	ds_read2_b32 v[8:9], v8 offset1:1
	s_waitcnt lgkmcnt(0)
	v_pk_fma_f32 v[36:37], v[146:147], v[8:9], v[36:37] op_sel_hi:[0,1,1]
	v_mov_b32_e32 v8, 0x3324
	ds_read2_b32 v[8:9], v8 offset1:1
	s_waitcnt lgkmcnt(0)
	v_pk_fma_f32 v[38:39], v[146:147], v[8:9], v[38:39] op_sel_hi:[0,1,1]
	v_mov_b32_e32 v8, 0x332c
	ds_read2_b32 v[8:9], v8 offset1:1
	s_waitcnt lgkmcnt(0)
	v_pk_fma_f32 v[40:41], v[146:147], v[8:9], v[40:41] op_sel_hi:[0,1,1]
	v_mov_b32_e32 v8, 0x3334
	ds_read2_b32 v[8:9], v8 offset1:1
	s_waitcnt lgkmcnt(0)
	v_pk_fma_f32 v[42:43], v[146:147], v[8:9], v[42:43] op_sel_hi:[0,1,1]
	v_mov_b32_e32 v8, 0x333c
	ds_read2_b32 v[8:9], v8 offset1:1
	s_waitcnt lgkmcnt(0)
	v_pk_fma_f32 v[44:45], v[146:147], v[8:9], v[44:45] op_sel_hi:[0,1,1]
	v_mov_b32_e32 v8, 0x3344
	ds_read2_b32 v[8:9], v8 offset1:1
	s_waitcnt lgkmcnt(0)
	v_pk_fma_f32 v[46:47], v[146:147], v[8:9], v[46:47] op_sel_hi:[0,1,1]
	v_mov_b32_e32 v8, 0x334c
	ds_read2_b32 v[8:9], v8 offset1:1
	s_waitcnt lgkmcnt(0)
	v_pk_fma_f32 v[148:149], v[146:147], v[8:9], v[150:151] op_sel_hi:[0,1,1]
	v_mov_b32_e32 v8, 0x3354
	ds_read2_b32 v[8:9], v8 offset1:1
	s_waitcnt lgkmcnt(0)
	v_pk_fma_f32 v[150:151], v[146:147], v[8:9], v[152:153] op_sel_hi:[0,1,1]
	v_mov_b32_e32 v8, 0x335c
	ds_read2_b32 v[8:9], v8 offset1:1
	s_waitcnt lgkmcnt(0)
	v_pk_fma_f32 v[152:153], v[146:147], v[8:9], v[154:155] op_sel_hi:[0,1,1]
	v_mov_b32_e32 v8, 0x3364
	ds_read2_b32 v[8:9], v8 offset1:1
	s_waitcnt lgkmcnt(0)
	v_pk_fma_f32 v[154:155], v[146:147], v[8:9], v[156:157] op_sel_hi:[0,1,1]
	v_mov_b32_e32 v8, 0x336c
	ds_read2_b32 v[8:9], v8 offset1:1
	s_waitcnt lgkmcnt(0)
	v_pk_fma_f32 v[156:157], v[146:147], v[8:9], v[158:159] op_sel_hi:[0,1,1]
	v_mov_b32_e32 v8, 0x3374
	ds_read2_b32 v[8:9], v8 offset1:1
	s_waitcnt lgkmcnt(0)
	v_pk_fma_f32 v[158:159], v[146:147], v[8:9], v[160:161] op_sel_hi:[0,1,1]
	v_mov_b32_e32 v8, 0x337c
	ds_read2_b32 v[8:9], v8 offset1:1
	s_waitcnt lgkmcnt(0)
	v_pk_fma_f32 v[160:161], v[146:147], v[8:9], v[166:167] op_sel_hi:[0,1,1]
	v_mov_b32_e32 v8, 0x3384
	ds_read2_b32 v[8:9], v8 offset1:1
	s_waitcnt lgkmcnt(0)
	v_pk_fma_f32 v[166:167], v[146:147], v[8:9], v[168:169] op_sel_hi:[0,1,1]
	v_mov_b32_e32 v8, 0x338c
	ds_read2_b32 v[8:9], v8 offset1:1
	s_waitcnt lgkmcnt(0)
	v_pk_fma_f32 v[168:169], v[146:147], v[8:9], v[174:175] op_sel_hi:[0,1,1]
	v_mov_b32_e32 v8, 0x3394
	ds_read2_b32 v[8:9], v8 offset1:1
	s_waitcnt lgkmcnt(0)
	v_pk_fma_f32 v[170:171], v[146:147], v[8:9], v[170:171] op_sel_hi:[0,1,1]
	v_mov_b32_e32 v8, 0x339c
	ds_read2_b32 v[8:9], v8 offset1:1
	s_waitcnt lgkmcnt(0)
	v_pk_fma_f32 v[164:165], v[146:147], v[8:9], v[164:165] op_sel_hi:[0,1,1]
	v_mov_b32_e32 v8, 0x33a4
	ds_read2_b32 v[8:9], v8 offset1:1
	s_waitcnt lgkmcnt(0)
	v_pk_fma_f32 v[174:175], v[146:147], v[8:9], v[178:179] op_sel_hi:[0,1,1]
	v_mov_b32_e32 v8, 0x33ac
	ds_read2_b32 v[8:9], v8 offset1:1
	s_waitcnt lgkmcnt(0)
	v_pk_fma_f32 v[178:179], v[146:147], v[8:9], v[180:181] op_sel_hi:[0,1,1]
	v_mov_b32_e32 v8, 0x33b4
	ds_read2_b32 v[8:9], v8 offset1:1
	s_waitcnt lgkmcnt(0)
	v_pk_fma_f32 v[176:177], v[146:147], v[8:9], v[176:177] op_sel_hi:[0,1,1]
	v_mov_b32_e32 v8, 0x33bc
	ds_read2_b32 v[8:9], v8 offset1:1
	s_waitcnt lgkmcnt(0)
	v_pk_fma_f32 v[172:173], v[146:147], v[8:9], v[172:173] op_sel_hi:[0,1,1]
	v_mov_b32_e32 v8, 0x33c4
	ds_read2_b32 v[8:9], v8 offset1:1
	s_waitcnt lgkmcnt(0)
	v_pk_fma_f32 v[162:163], v[146:147], v[8:9], v[162:163] op_sel_hi:[0,1,1]
	v_mov_b32_e32 v8, 0x33cc
	ds_read2_b32 v[8:9], v8 offset1:1
	s_waitcnt lgkmcnt(0)
	v_pk_fma_f32 v[180:181], v[146:147], v[8:9], v[182:183] op_sel_hi:[0,1,1]
	v_mov_b32_e32 v8, 0x33d4
	ds_read2_b32 v[8:9], v8 offset1:1
	s_waitcnt lgkmcnt(0)
	v_pk_fma_f32 v[20:21], v[146:147], v[8:9], v[20:21] op_sel_hi:[0,1,1]
	v_mov_b32_e32 v8, 0x33dc
	ds_read2_b32 v[8:9], v8 offset1:1
	s_waitcnt lgkmcnt(0)
	v_pk_fma_f32 v[22:23], v[146:147], v[8:9], v[22:23] op_sel_hi:[0,1,1]
	v_mov_b32_e32 v8, 0x33e4
	ds_read2_b32 v[8:9], v8 offset1:1
	s_waitcnt lgkmcnt(0)
	v_pk_fma_f32 v[24:25], v[146:147], v[8:9], v[24:25] op_sel_hi:[0,1,1]
	v_mov_b32_e32 v8, 0x33ec
	ds_read2_b32 v[8:9], v8 offset1:1
	s_waitcnt lgkmcnt(0)
	v_pk_fma_f32 v[26:27], v[146:147], v[8:9], v[26:27] op_sel_hi:[0,1,1]
	v_mov_b32_e32 v8, 0x33f4
	ds_read2_b32 v[8:9], v8 offset1:1
	s_waitcnt lgkmcnt(0)
	v_pk_fma_f32 v[28:29], v[146:147], v[8:9], v[28:29] op_sel_hi:[0,1,1]
	v_mov_b32_e32 v8, 0x33fc
	ds_read2_b32 v[8:9], v8 offset1:1
	s_waitcnt lgkmcnt(0)
	v_mov_b32_e32 v10, v8
	v_mov_b32_e32 v8, 0x3404
	v_pk_fma_f32 v[10:11], v[146:147], v[10:11], v[18:19] op_sel_hi:[0,1,1]
	ds_read2_b32 v[18:19], v8 offset1:1
	v_mov_b32_e32 v8, 0x340c
	s_waitcnt lgkmcnt(0)
	v_pk_fma_f32 v[18:19], v[144:145], v[18:19], v[30:31] op_sel_hi:[0,1,1]
	ds_read2_b32 v[30:31], v8 offset1:1
	v_mov_b32_e32 v8, 0x3414
	s_waitcnt lgkmcnt(0)
	v_pk_fma_f32 v[30:31], v[144:145], v[30:31], v[32:33] op_sel_hi:[0,1,1]
	ds_read2_b32 v[32:33], v8 offset1:1
	v_mov_b32_e32 v8, 0x341c
	s_waitcnt lgkmcnt(0)
	v_pk_fma_f32 v[32:33], v[144:145], v[32:33], v[34:35] op_sel_hi:[0,1,1]
	ds_read2_b32 v[34:35], v8 offset1:1
	v_mov_b32_e32 v8, 0x3424
	s_waitcnt lgkmcnt(0)
	v_pk_fma_f32 v[34:35], v[144:145], v[34:35], v[36:37] op_sel_hi:[0,1,1]
	ds_read2_b32 v[36:37], v8 offset1:1
	v_mov_b32_e32 v8, 0x342c
	s_waitcnt lgkmcnt(0)
	v_pk_fma_f32 v[36:37], v[144:145], v[36:37], v[38:39] op_sel_hi:[0,1,1]
	ds_read2_b32 v[38:39], v8 offset1:1
	v_mov_b32_e32 v8, 0x3434
	s_waitcnt lgkmcnt(0)
	v_pk_fma_f32 v[38:39], v[144:145], v[38:39], v[40:41] op_sel_hi:[0,1,1]
	ds_read2_b32 v[40:41], v8 offset1:1
	v_mov_b32_e32 v8, 0x343c
	s_waitcnt lgkmcnt(0)
	v_pk_fma_f32 v[40:41], v[144:145], v[40:41], v[42:43] op_sel_hi:[0,1,1]
	ds_read2_b32 v[42:43], v8 offset1:1
	v_mov_b32_e32 v8, 0x3444
	s_waitcnt lgkmcnt(0)
	v_pk_fma_f32 v[42:43], v[144:145], v[42:43], v[44:45] op_sel_hi:[0,1,1]
	ds_read2_b32 v[44:45], v8 offset1:1
	v_mov_b32_e32 v8, 0x344c
	s_waitcnt lgkmcnt(0)
	v_pk_fma_f32 v[44:45], v[144:145], v[44:45], v[46:47] op_sel_hi:[0,1,1]
	ds_read2_b32 v[46:47], v8 offset1:1
	v_mov_b32_e32 v8, 0x3454
	ds_read2_b32 v[116:117], v8 offset1:1
	v_mov_b32_e32 v8, 0x345c
	s_waitcnt lgkmcnt(1)
	v_pk_fma_f32 v[46:47], v[144:145], v[46:47], v[148:149] op_sel_hi:[0,1,1]
	s_waitcnt lgkmcnt(0)
	v_pk_fma_f32 v[146:147], v[144:145], v[116:117], v[150:151] op_sel_hi:[0,1,1]
	ds_read2_b32 v[116:117], v8 offset1:1
	v_mov_b32_e32 v8, 0x3464
	s_waitcnt lgkmcnt(0)
	v_pk_fma_f32 v[148:149], v[144:145], v[116:117], v[152:153] op_sel_hi:[0,1,1]
	ds_read2_b32 v[116:117], v8 offset1:1
	v_mov_b32_e32 v8, 0x346c
	s_waitcnt lgkmcnt(0)
	v_pk_fma_f32 v[150:151], v[144:145], v[116:117], v[154:155] op_sel_hi:[0,1,1]
	ds_read2_b32 v[116:117], v8 offset1:1
	v_mov_b32_e32 v8, 0x3474
	s_waitcnt lgkmcnt(0)
	v_pk_fma_f32 v[152:153], v[144:145], v[116:117], v[156:157] op_sel_hi:[0,1,1]
	ds_read2_b32 v[116:117], v8 offset1:1
	v_mov_b32_e32 v8, 0x347c
	s_waitcnt lgkmcnt(0)
	v_pk_fma_f32 v[154:155], v[144:145], v[116:117], v[158:159] op_sel_hi:[0,1,1]
	ds_read2_b32 v[116:117], v8 offset1:1
	v_mov_b32_e32 v8, 0x3484
	s_waitcnt lgkmcnt(0)
	v_pk_fma_f32 v[156:157], v[144:145], v[116:117], v[160:161] op_sel_hi:[0,1,1]
	ds_read2_b32 v[116:117], v8 offset1:1
	v_mov_b32_e32 v8, 0x348c
	s_waitcnt lgkmcnt(0)
	v_pk_fma_f32 v[158:159], v[144:145], v[116:117], v[166:167] op_sel_hi:[0,1,1]
	ds_read2_b32 v[116:117], v8 offset1:1
	v_mov_b32_e32 v8, 0x3494
	s_waitcnt lgkmcnt(0)
	v_pk_fma_f32 v[160:161], v[144:145], v[116:117], v[168:169] op_sel_hi:[0,1,1]
	ds_read2_b32 v[116:117], v8 offset1:1
	v_mov_b32_e32 v8, 0x349c
	s_waitcnt lgkmcnt(0)
	v_pk_fma_f32 v[166:167], v[144:145], v[116:117], v[170:171] op_sel_hi:[0,1,1]
	ds_read2_b32 v[116:117], v8 offset1:1
	v_mov_b32_e32 v8, 0x34a4
	s_waitcnt lgkmcnt(0)
	v_pk_fma_f32 v[164:165], v[144:145], v[116:117], v[164:165] op_sel_hi:[0,1,1]
	ds_read2_b32 v[116:117], v8 offset1:1
	v_mov_b32_e32 v8, 0x34ac
	s_waitcnt lgkmcnt(0)
	v_pk_fma_f32 v[168:169], v[144:145], v[116:117], v[174:175] op_sel_hi:[0,1,1]
	ds_read2_b32 v[116:117], v8 offset1:1
	v_mov_b32_e32 v8, 0x34b4
	s_waitcnt lgkmcnt(0)
	v_pk_fma_f32 v[170:171], v[144:145], v[116:117], v[178:179] op_sel_hi:[0,1,1]
	ds_read2_b32 v[116:117], v8 offset1:1
	v_mov_b32_e32 v8, 0x34bc
	s_waitcnt lgkmcnt(0)
	v_pk_fma_f32 v[174:175], v[144:145], v[116:117], v[176:177] op_sel_hi:[0,1,1]
	ds_read2_b32 v[116:117], v8 offset1:1
	v_mov_b32_e32 v8, 0x34c4
	s_waitcnt lgkmcnt(0)
	v_pk_fma_f32 v[172:173], v[144:145], v[116:117], v[172:173] op_sel_hi:[0,1,1]
	ds_read2_b32 v[116:117], v8 offset1:1
	v_mov_b32_e32 v8, 0x34cc
	s_waitcnt lgkmcnt(0)
	v_pk_fma_f32 v[162:163], v[144:145], v[116:117], v[162:163] op_sel_hi:[0,1,1]
	ds_read2_b32 v[116:117], v8 offset1:1
	v_mov_b32_e32 v8, 0x34d4
	s_waitcnt lgkmcnt(0)
	v_pk_fma_f32 v[176:177], v[144:145], v[116:117], v[180:181] op_sel_hi:[0,1,1]
	ds_read2_b32 v[116:117], v8 offset1:1
	v_mov_b32_e32 v8, 0x34dc
	s_waitcnt lgkmcnt(0)
	v_pk_fma_f32 v[20:21], v[144:145], v[116:117], v[20:21] op_sel_hi:[0,1,1]
	ds_read2_b32 v[116:117], v8 offset1:1
	v_mov_b32_e32 v8, 0x34e4
	s_waitcnt lgkmcnt(0)
	v_pk_fma_f32 v[22:23], v[144:145], v[116:117], v[22:23] op_sel_hi:[0,1,1]
	ds_read2_b32 v[116:117], v8 offset1:1
	v_mov_b32_e32 v8, 0x34ec
	s_waitcnt lgkmcnt(0)
	v_pk_fma_f32 v[24:25], v[144:145], v[116:117], v[24:25] op_sel_hi:[0,1,1]
	ds_read2_b32 v[116:117], v8 offset1:1
	v_mov_b32_e32 v8, 0x34f4
	s_waitcnt lgkmcnt(0)
	v_pk_fma_f32 v[26:27], v[144:145], v[116:117], v[26:27] op_sel_hi:[0,1,1]
	ds_read2_b32 v[116:117], v8 offset1:1
	v_mov_b32_e32 v8, 0x34fc
	ds_read2_b32 v[222:223], v8 offset1:1
	s_waitcnt lgkmcnt(1)
	v_pk_fma_f32 v[28:29], v[144:145], v[116:117], v[28:29] op_sel_hi:[0,1,1]
	ds_read2_b32 v[116:117], v109 offset1:1
	s_waitcnt lgkmcnt(1)
	v_mov_b32_e32 v8, v222
	v_pk_fma_f32 v[224:225], v[144:145], v[8:9], v[10:11] op_sel_hi:[0,1,1]
	v_mov_b32_e32 v8, 0x3504
	ds_read2_b32 v[8:9], v8 offset1:1
	v_mov_b32_e32 v10, 0x350c
	ds_read2_b32 v[10:11], v10 offset1:1
	v_mov_b32_e32 v109, 0x356c
	ds_read2_b32 v[118:119], v109 offset1:1
	s_waitcnt lgkmcnt(2)
	v_pk_fma_f32 v[8:9], v[2:3], v[8:9], v[18:19] op_sel_hi:[0,1,1]
	v_mov_b32_e32 v18, 0x3514
	s_waitcnt lgkmcnt(1)
	v_pk_fma_f32 v[10:11], v[2:3], v[10:11], v[30:31] op_sel_hi:[0,1,1]
	ds_read2_b32 v[18:19], v18 offset1:1
	v_mov_b32_e32 v30, 0x351c
	ds_read2_b32 v[30:31], v30 offset1:1
	v_mov_b32_e32 v109, 0x3574
	ds_read2_b32 v[120:121], v109 offset1:1
	s_waitcnt lgkmcnt(2)
	v_pk_fma_f32 v[18:19], v[2:3], v[18:19], v[32:33] op_sel_hi:[0,1,1]
	v_mov_b32_e32 v32, 0x3524
	s_waitcnt lgkmcnt(1)
	v_pk_fma_f32 v[30:31], v[2:3], v[30:31], v[34:35] op_sel_hi:[0,1,1]
	ds_read2_b32 v[32:33], v32 offset1:1
	v_mov_b32_e32 v34, 0x352c
	ds_read2_b32 v[34:35], v34 offset1:1
	v_mov_b32_e32 v109, 0x357c
	ds_read2_b32 v[122:123], v109 offset1:1
	s_waitcnt lgkmcnt(2)
	v_pk_fma_f32 v[32:33], v[2:3], v[32:33], v[36:37] op_sel_hi:[0,1,1]
	v_mov_b32_e32 v36, 0x3534
	s_waitcnt lgkmcnt(1)
	v_pk_fma_f32 v[34:35], v[2:3], v[34:35], v[38:39] op_sel_hi:[0,1,1]
	ds_read2_b32 v[36:37], v36 offset1:1
	v_mov_b32_e32 v38, 0x353c
	ds_read2_b32 v[38:39], v38 offset1:1
	v_mov_b32_e32 v109, 0x3584
	ds_read2_b32 v[144:145], v109 offset1:1
	s_waitcnt lgkmcnt(2)
	v_pk_fma_f32 v[36:37], v[2:3], v[36:37], v[40:41] op_sel_hi:[0,1,1]
	v_mov_b32_e32 v40, 0x3544
	s_waitcnt lgkmcnt(1)
	v_pk_fma_f32 v[38:39], v[2:3], v[38:39], v[42:43] op_sel_hi:[0,1,1]
	ds_read2_b32 v[40:41], v40 offset1:1
	v_mov_b32_e32 v42, 0x354c
	ds_read2_b32 v[42:43], v42 offset1:1
	v_mov_b32_e32 v109, 0x358c
	v_pk_fma_f32 v[116:117], v[2:3], v[116:117], v[150:151] op_sel_hi:[0,1,1]
	s_waitcnt lgkmcnt(1)
	v_pk_fma_f32 v[40:41], v[2:3], v[40:41], v[44:45] op_sel_hi:[0,1,1]
	v_mov_b32_e32 v44, 0x3554
	s_waitcnt lgkmcnt(0)
	v_pk_fma_f32 v[42:43], v[2:3], v[42:43], v[46:47] op_sel_hi:[0,1,1]
	ds_read2_b32 v[44:45], v44 offset1:1
	v_mov_b32_e32 v46, 0x355c
	ds_read2_b32 v[46:47], v46 offset1:1
	v_pk_fma_f32 v[118:119], v[2:3], v[118:119], v[152:153] op_sel_hi:[0,1,1]
	v_pk_fma_f32 v[120:121], v[2:3], v[120:121], v[154:155] op_sel_hi:[0,1,1]
	s_waitcnt lgkmcnt(1)
	v_pk_fma_f32 v[44:45], v[2:3], v[44:45], v[146:147] op_sel_hi:[0,1,1]
	ds_read2_b32 v[146:147], v109 offset1:1
	v_mov_b32_e32 v109, 0x3594
	s_waitcnt lgkmcnt(1)
	v_pk_fma_f32 v[46:47], v[2:3], v[46:47], v[148:149] op_sel_hi:[0,1,1]
	ds_read2_b32 v[148:149], v109 offset1:1
	v_mov_b32_e32 v109, 0x359c
	ds_read2_b32 v[150:151], v109 offset1:1
	v_mov_b32_e32 v109, 0x35a4
	ds_read2_b32 v[152:153], v109 offset1:1
	v_mov_b32_e32 v109, 0x35ac
	ds_read2_b32 v[154:155], v109 offset1:1
	v_mov_b32_e32 v109, 0x35b4
	v_pk_fma_f32 v[122:123], v[2:3], v[122:123], v[156:157] op_sel_hi:[0,1,1]
	ds_read2_b32 v[156:157], v109 offset1:1
	v_mov_b32_e32 v109, 0x35bc
	v_pk_fma_f32 v[144:145], v[2:3], v[144:145], v[158:159] op_sel_hi:[0,1,1]
	ds_read2_b32 v[158:159], v109 offset1:1
	v_mov_b32_e32 v109, 0x35c4
	s_waitcnt lgkmcnt(4)
	v_pk_fma_f32 v[150:151], v[2:3], v[150:151], v[164:165] op_sel_hi:[0,1,1]
	s_waitcnt lgkmcnt(1)
	v_pk_fma_f32 v[156:157], v[2:3], v[156:157], v[174:175] op_sel_hi:[0,1,1]
	v_pk_fma_f32 v[154:155], v[2:3], v[154:155], v[170:171] op_sel_hi:[0,1,1]
	s_waitcnt lgkmcnt(0)
	v_pk_fma_f32 v[164:165], v[2:3], v[158:159], v[172:173] op_sel_hi:[0,1,1]
	ds_read2_b32 v[158:159], v109 offset1:1
	v_mov_b32_e32 v109, 0x35cc
	v_pk_fma_f32 v[148:149], v[2:3], v[148:149], v[166:167] op_sel_hi:[0,1,1]
	v_pk_fma_f32 v[152:153], v[2:3], v[152:153], v[168:169] op_sel_hi:[0,1,1]
	v_pk_fma_f32 v[146:147], v[2:3], v[146:147], v[160:161] op_sel_hi:[0,1,1]
	s_waitcnt lgkmcnt(0)
	v_pk_fma_f32 v[162:163], v[2:3], v[158:159], v[162:163] op_sel_hi:[0,1,1]
	ds_read2_b32 v[158:159], v109 offset1:1
	v_mov_b32_e32 v109, 0x35d4
	s_waitcnt lgkmcnt(0)
	v_pk_fma_f32 v[182:183], v[2:3], v[158:159], v[176:177] op_sel_hi:[0,1,1]
	ds_read2_b32 v[158:159], v109 offset1:1
	v_mov_b32_e32 v109, 0x35dc
	s_waitcnt lgkmcnt(0)
	v_pk_fma_f32 v[20:21], v[2:3], v[158:159], v[20:21] op_sel_hi:[0,1,1]
	ds_read2_b32 v[158:159], v109 offset1:1
	v_mov_b32_e32 v109, 0x35e4
	s_waitcnt lgkmcnt(0)
	v_pk_fma_f32 v[22:23], v[2:3], v[158:159], v[22:23] op_sel_hi:[0,1,1]
	ds_read2_b32 v[158:159], v109 offset1:1
	s_waitcnt lgkmcnt(0)
	v_pk_fma_f32 v[184:185], v[2:3], v[158:159], v[24:25] op_sel_hi:[0,1,1]
	v_mov_b32_e32 v24, 0x35ec
	ds_read2_b32 v[24:25], v24 offset1:1
	s_waitcnt lgkmcnt(0)
	v_pk_fma_f32 v[186:187], v[2:3], v[24:25], v[26:27] op_sel_hi:[0,1,1]
	v_mov_b32_e32 v24, 0x35f4
	ds_read2_b32 v[24:25], v24 offset1:1
	s_waitcnt lgkmcnt(0)
	v_pk_fma_f32 v[28:29], v[2:3], v[24:25], v[28:29] op_sel_hi:[0,1,1]
	v_mov_b32_e32 v24, 0x35fc
	ds_read2_b32 v[228:229], v24 offset1:1
	v_mov_b32_e32 v24, 0x3604
	ds_read2_b32 v[24:25], v24 offset1:1
	s_waitcnt lgkmcnt(1)
	v_mov_b32_e32 v222, v228
	s_waitcnt lgkmcnt(0)
	v_pk_fma_f32 v[234:235], v[0:1], v[24:25], v[8:9] op_sel_hi:[0,1,1]
	v_mov_b32_e32 v8, 0x360c
	ds_read2_b32 v[8:9], v8 offset1:1
	s_waitcnt lgkmcnt(0)
	v_pk_fma_f32 v[236:237], v[0:1], v[8:9], v[10:11] op_sel_hi:[0,1,1]
	v_mov_b32_e32 v8, 0x3614
	ds_read2_b32 v[8:9], v8 offset1:1
	v_mov_b32_e32 v10, 0x36dc
	ds_read2_b32 v[10:11], v10 offset1:1
	s_waitcnt lgkmcnt(1)
	v_pk_fma_f32 v[202:203], v[0:1], v[8:9], v[18:19] op_sel_hi:[0,1,1]
	v_mov_b32_e32 v8, 0x361c
	ds_read2_b32 v[8:9], v8 offset1:1
	s_waitcnt lgkmcnt(1)
	v_pk_fma_f32 v[10:11], v[0:1], v[10:11], v[22:23] op_sel_hi:[0,1,1]
	v_mov_b32_e32 v22, 0x36f4
	ds_read2_b32 v[22:23], v22 offset1:1
	v_mov_b32_e32 v18, 0x36e4
	s_waitcnt lgkmcnt(1)
	v_pk_fma_f32 v[220:221], v[0:1], v[8:9], v[30:31] op_sel_hi:[0,1,1]
	v_mov_b32_e32 v8, 0x3624
	ds_read2_b32 v[8:9], v8 offset1:1
	s_waitcnt lgkmcnt(1)
	v_pk_fma_f32 v[22:23], v[0:1], v[22:23], v[28:29] op_sel_hi:[0,1,1]
	v_fma_f32 v28, v104, s4, -v124
	v_mul_f32_e32 v29, 0x3fb8aa3b, v28
	v_fma_f32 v30, v28, s5, -v29
	s_waitcnt lgkmcnt(0)
	v_pk_fma_f32 v[194:195], v[0:1], v[8:9], v[32:33] op_sel_hi:[0,1,1]
	v_mov_b32_e32 v8, 0x362c
	ds_read2_b32 v[8:9], v8 offset1:1
	v_rndne_f32_e32 v31, v29
	v_fma_f32 v104, v105, s4, -v124
	v_fmac_f32_e32 v30, 0x32a5705f, v28
	v_sub_f32_e32 v29, v29, v31
	s_waitcnt lgkmcnt(0)
	v_pk_fma_f32 v[196:197], v[0:1], v[8:9], v[34:35] op_sel_hi:[0,1,1]
	v_mov_b32_e32 v8, 0x3634
	ds_read2_b32 v[8:9], v8 offset1:1
	v_mul_f32_e32 v105, 0x3fb8aa3b, v104
	v_add_f32_e32 v29, v29, v30
	v_fma_f32 v109, v104, s5, -v105
	v_rndne_f32_e32 v111, v105
	s_waitcnt lgkmcnt(0)
	v_pk_fma_f32 v[190:191], v[0:1], v[8:9], v[36:37] op_sel_hi:[0,1,1]
	v_mov_b32_e32 v8, 0x363c
	ds_read2_b32 v[8:9], v8 offset1:1
	v_exp_f32_e32 v29, v29
	v_cvt_i32_f32_e32 v30, v31
	v_fmac_f32_e32 v109, 0x32a5705f, v104
	v_sub_f32_e32 v105, v105, v111
	s_waitcnt lgkmcnt(0)
	v_pk_fma_f32 v[192:193], v[0:1], v[8:9], v[38:39] op_sel_hi:[0,1,1]
	v_mov_b32_e32 v8, 0x3644
	ds_read2_b32 v[8:9], v8 offset1:1
	v_add_f32_e32 v105, v105, v109
	v_exp_f32_e32 v105, v105
	v_cvt_i32_f32_e32 v109, v111
	v_ldexp_f32 v29, v29, v30
	s_waitcnt lgkmcnt(0)
	v_pk_fma_f32 v[178:179], v[0:1], v[8:9], v[40:41] op_sel_hi:[0,1,1]
	v_mov_b32_e32 v8, 0x364c
	ds_read2_b32 v[8:9], v8 offset1:1
	v_cmp_ngt_f32_e32 vcc, s6, v28
	v_ldexp_f32 v105, v105, v109
	ds_read2_b32 v[18:19], v18 offset1:1
	v_cndmask_b32_e32 v29, 0, v29, vcc
	s_waitcnt lgkmcnt(1)
	v_pk_fma_f32 v[180:181], v[0:1], v[8:9], v[42:43] op_sel_hi:[0,1,1]
	v_mov_b32_e32 v8, 0x3654
	ds_read2_b32 v[8:9], v8 offset1:1
	v_cmp_nlt_f32_e32 vcc, s7, v28
	s_waitcnt lgkmcnt(1)
	v_pk_fma_f32 v[18:19], v[0:1], v[18:19], v[184:185] op_sel_hi:[0,1,1]
	v_mov_b32_e32 v28, 0x3704
	v_cndmask_b32_e32 v226, v103, v29, vcc
	s_waitcnt lgkmcnt(0)
	v_pk_fma_f32 v[174:175], v[0:1], v[8:9], v[44:45] op_sel_hi:[0,1,1]
	v_mov_b32_e32 v8, 0x365c
	ds_read2_b32 v[8:9], v8 offset1:1
	v_cmp_ngt_f32_e32 vcc, s6, v104
	v_mov_b32_e32 v30, 0x37dc
	v_mov_b32_e32 v32, 0x37e4
	v_cndmask_b32_e32 v105, 0, v105, vcc
	s_waitcnt lgkmcnt(0)
	v_pk_fma_f32 v[176:177], v[0:1], v[8:9], v[46:47] op_sel_hi:[0,1,1]
	v_mov_b32_e32 v8, 0x3664
	ds_read2_b32 v[8:9], v8 offset1:1
	v_cmp_nlt_f32_e32 vcc, s7, v104
	v_fma_f32 v104, v106, s4, -v124
	v_mov_b32_e32 v34, 0x37ec
	v_cndmask_b32_e32 v218, v103, v105, vcc
	s_waitcnt lgkmcnt(0)
	v_pk_fma_f32 v[170:171], v[0:1], v[8:9], v[116:117] op_sel_hi:[0,1,1]
	v_mov_b32_e32 v8, 0x366c
	ds_read2_b32 v[8:9], v8 offset1:1
	v_mul_f32_e32 v105, 0x3fb8aa3b, v104
	v_fma_f32 v106, v104, s5, -v105
	v_rndne_f32_e32 v109, v105
	v_fmac_f32_e32 v106, 0x32a5705f, v104
	s_waitcnt lgkmcnt(0)
	v_pk_fma_f32 v[172:173], v[0:1], v[8:9], v[118:119] op_sel_hi:[0,1,1]
	v_mov_b32_e32 v8, 0x3674
	ds_read2_b32 v[8:9], v8 offset1:1
	v_sub_f32_e32 v105, v105, v109
	v_add_f32_e32 v105, v105, v106
	v_exp_f32_e32 v105, v105
	v_cvt_i32_f32_e32 v106, v109
	s_waitcnt lgkmcnt(0)
	v_pk_fma_f32 v[166:167], v[0:1], v[8:9], v[120:121] op_sel_hi:[0,1,1]
	v_mov_b32_e32 v8, 0x367c
	ds_read2_b32 v[8:9], v8 offset1:1
	v_ldexp_f32 v105, v105, v106
	v_cmp_ngt_f32_e32 vcc, s6, v104
	ds_read2_b32 v[116:117], v28 offset1:1
	v_mov_b32_e32 v28, 0x370c
	s_waitcnt lgkmcnt(1)
	v_pk_fma_f32 v[168:169], v[0:1], v[8:9], v[122:123] op_sel_hi:[0,1,1]
	v_mov_b32_e32 v8, 0x3684
	ds_read2_b32 v[8:9], v8 offset1:1
	v_cndmask_b32_e32 v105, 0, v105, vcc
	v_cmp_nlt_f32_e32 vcc, s7, v104
	v_fma_f32 v104, v107, s4, -v124
	ds_read2_b32 v[118:119], v28 offset1:1
	s_waitcnt lgkmcnt(1)
	v_pk_fma_f32 v[158:159], v[0:1], v[8:9], v[144:145] op_sel_hi:[0,1,1]
	v_mov_b32_e32 v8, 0x368c
	ds_read2_b32 v[8:9], v8 offset1:1
	v_cndmask_b32_e32 v216, v103, v105, vcc
	v_mul_f32_e32 v105, 0x3fb8aa3b, v104
	v_fma_f32 v106, v104, s5, -v105
	v_rndne_f32_e32 v107, v105
	s_waitcnt lgkmcnt(0)
	v_pk_fma_f32 v[160:161], v[0:1], v[8:9], v[146:147] op_sel_hi:[0,1,1]
	v_mov_b32_e32 v8, 0x3694
	ds_read2_b32 v[8:9], v8 offset1:1
	v_fmac_f32_e32 v106, 0x32a5705f, v104
	v_sub_f32_e32 v105, v105, v107
	v_add_f32_e32 v105, v105, v106
	v_exp_f32_e32 v105, v105
	s_waitcnt lgkmcnt(0)
	v_pk_fma_f32 v[146:147], v[0:1], v[8:9], v[148:149] op_sel_hi:[0,1,1]
	v_mov_b32_e32 v8, 0x369c
	ds_read2_b32 v[8:9], v8 offset1:1
	v_cvt_i32_f32_e32 v106, v107
	v_cmp_ngt_f32_e32 vcc, s6, v104
	v_mov_b32_e32 v28, 0x3714
	ds_read2_b32 v[120:121], v28 offset1:1
	s_waitcnt lgkmcnt(1)
	v_pk_fma_f32 v[148:149], v[0:1], v[8:9], v[150:151] op_sel_hi:[0,1,1]
	v_mov_b32_e32 v8, 0x36a4
	ds_read2_b32 v[8:9], v8 offset1:1
	v_ldexp_f32 v105, v105, v106
	v_cndmask_b32_e32 v105, 0, v105, vcc
	v_cmp_nlt_f32_e32 vcc, s7, v104
	v_fma_f32 v104, v108, s4, -v124
	s_waitcnt lgkmcnt(0)
	v_pk_fma_f32 v[46:47], v[0:1], v[8:9], v[152:153] op_sel_hi:[0,1,1]
	v_mov_b32_e32 v8, 0x36ac
	ds_read2_b32 v[8:9], v8 offset1:1
	v_cndmask_b32_e32 v214, v103, v105, vcc
	v_mul_f32_e32 v105, 0x3fb8aa3b, v104
	v_fma_f32 v106, v104, s5, -v105
	v_rndne_f32_e32 v107, v105
	s_waitcnt lgkmcnt(0)
	v_pk_fma_f32 v[144:145], v[0:1], v[8:9], v[154:155] op_sel_hi:[0,1,1]
	v_mov_b32_e32 v8, 0x36b4
	ds_read2_b32 v[8:9], v8 offset1:1
	v_fmac_f32_e32 v106, 0x32a5705f, v104
	v_sub_f32_e32 v105, v105, v107
	v_add_f32_e32 v105, v105, v106
	v_exp_f32_e32 v105, v105
	s_waitcnt lgkmcnt(0)
	v_pk_fma_f32 v[38:39], v[0:1], v[8:9], v[156:157] op_sel_hi:[0,1,1]
	v_mov_b32_e32 v8, 0x36bc
	ds_read2_b32 v[8:9], v8 offset1:1
	v_cvt_i32_f32_e32 v106, v107
	v_cmp_ngt_f32_e32 vcc, s6, v104
	v_pk_fma_f32 v[108:109], v[226:227], v[118:119], v[236:237] op_sel_hi:[0,1,1]
	v_mov_b32_e32 v28, 0x371c
	v_ldexp_f32 v105, v105, v106
	s_waitcnt lgkmcnt(0)
	v_pk_fma_f32 v[40:41], v[0:1], v[8:9], v[164:165] op_sel_hi:[0,1,1]
	v_mov_b32_e32 v8, 0x36c4
	v_cndmask_b32_e32 v105, 0, v105, vcc
	v_cmp_nlt_f32_e32 vcc, s7, v104
	v_fma_f32 v104, v110, s4, -v124
	ds_read2_b32 v[8:9], v8 offset1:1
	v_cndmask_b32_e32 v212, v103, v105, vcc
	v_mul_f32_e32 v105, 0x3fb8aa3b, v104
	v_fma_f32 v106, v104, s5, -v105
	v_rndne_f32_e32 v107, v105
	v_fmac_f32_e32 v106, 0x32a5705f, v104
	v_sub_f32_e32 v105, v105, v107
	v_add_f32_e32 v105, v105, v106
	v_exp_f32_e32 v105, v105
	v_cvt_i32_f32_e32 v106, v107
	s_waitcnt lgkmcnt(0)
	v_pk_fma_f32 v[24:25], v[0:1], v[8:9], v[162:163] op_sel_hi:[0,1,1]
	v_mov_b32_e32 v8, 0x36cc
	ds_read2_b32 v[8:9], v8 offset1:1
	v_ldexp_f32 v105, v105, v106
	v_cmp_ngt_f32_e32 vcc, s6, v104
	ds_read2_b32 v[122:123], v28 offset1:1
	v_mov_b32_e32 v28, 0x3724
	v_cndmask_b32_e32 v105, 0, v105, vcc
	v_cmp_nlt_f32_e32 vcc, s7, v104
	v_fma_f32 v104, v112, s4, -v124
	s_waitcnt lgkmcnt(1)
	v_pk_fma_f32 v[26:27], v[0:1], v[8:9], v[182:183] op_sel_hi:[0,1,1]
	v_cndmask_b32_e32 v210, v103, v105, vcc
	v_mul_f32_e32 v105, 0x3fb8aa3b, v104
	v_mov_b32_e32 v8, 0x36d4
	v_fma_f32 v106, v104, s5, -v105
	v_rndne_f32_e32 v107, v105
	ds_read2_b32 v[8:9], v8 offset1:1
	v_fmac_f32_e32 v106, 0x32a5705f, v104
	v_sub_f32_e32 v105, v105, v107
	v_add_f32_e32 v105, v105, v106
	v_exp_f32_e32 v105, v105
	v_cvt_i32_f32_e32 v106, v107
	s_waitcnt lgkmcnt(0)
	v_pk_fma_f32 v[8:9], v[0:1], v[8:9], v[20:21] op_sel_hi:[0,1,1]
	v_mov_b32_e32 v20, 0x36ec
	ds_read2_b32 v[20:21], v20 offset1:1
	v_ldexp_f32 v105, v105, v106
	v_cmp_ngt_f32_e32 vcc, s6, v104
	ds_read2_b32 v[242:243], v28 offset1:1
	v_mov_b32_e32 v28, 0x372c
	v_cndmask_b32_e32 v105, 0, v105, vcc
	v_cmp_nlt_f32_e32 vcc, s7, v104
	v_fma_f32 v104, v114, s4, -v124
	s_waitcnt lgkmcnt(1)
	v_pk_fma_f32 v[20:21], v[0:1], v[20:21], v[186:187] op_sel_hi:[0,1,1]
	v_cndmask_b32_e32 v206, v103, v105, vcc
	v_mul_f32_e32 v105, 0x3fb8aa3b, v104
	v_fma_f32 v106, v104, s5, -v105
	v_rndne_f32_e32 v107, v105
	v_fmac_f32_e32 v106, 0x32a5705f, v104
	v_sub_f32_e32 v105, v105, v107
	v_add_f32_e32 v1, v1, v0
	v_add_f32_e32 v105, v105, v106
	v_add_f32_e32 v1, v1, v226
	v_exp_f32_e32 v105, v105
	v_cvt_i32_f32_e32 v106, v107
	v_add_f32_e32 v1, v1, v218
	v_add_f32_e32 v1, v1, v216
	v_add_f32_e32 v1, v1, v214
	v_add_f32_e32 v1, v1, v212
	v_ldexp_f32 v105, v105, v106
	v_cmp_ngt_f32_e32 vcc, s6, v104
	v_add_f32_e32 v1, v1, v210
	v_add_f32_e32 v1, v1, v206
	v_cndmask_b32_e32 v105, 0, v105, vcc
	v_cmp_nlt_f32_e32 vcc, s7, v104
	ds_read2_b32 v[244:245], v28 offset1:1
	v_mov_b32_e32 v28, 0x3734
	v_cndmask_b32_e32 v204, v103, v105, vcc
	v_add_f32_e32 v104, v1, v204
	v_fma_f32 v1, v3, s4, -v124
	v_mul_f32_e32 v3, 0x3fb8aa3b, v1
	v_fma_f32 v105, v1, s5, -v3
	v_rndne_f32_e32 v106, v3
	v_fmac_f32_e32 v105, 0x32a5705f, v1
	v_sub_f32_e32 v3, v3, v106
	v_add_f32_e32 v3, v3, v105
	v_exp_f32_e32 v3, v3
	v_cvt_i32_f32_e32 v105, v106
	v_cmp_ngt_f32_e32 vcc, s6, v1
	v_pk_fma_f32 v[106:107], v[226:227], v[116:117], v[234:235] op_sel_hi:[0,1,1]
	ds_read2_b32 v[246:247], v28 offset1:1
	v_ldexp_f32 v3, v3, v105
	v_cndmask_b32_e32 v3, 0, v3, vcc
	v_cmp_nlt_f32_e32 vcc, s7, v1
	v_mov_b32_e32 v1, 0x3804
	ds_read2_b32 v[110:111], v1 offset1:1
	v_mov_b32_e32 v1, 0x380c
	ds_read2_b32 v[112:113], v1 offset1:1
	v_mov_b32_e32 v1, 0x390c
	v_mov_b32_e32 v28, 0x373c
	s_waitcnt lgkmcnt(1)
	v_pk_fma_f32 v[106:107], v[218:219], v[110:111], v[106:107] op_sel_hi:[0,1,1]
	ds_read2_b32 v[110:111], v1 offset1:1
	v_mov_b32_e32 v1, 0x3904
	s_waitcnt lgkmcnt(1)
	v_pk_fma_f32 v[108:109], v[218:219], v[112:113], v[108:109] op_sel_hi:[0,1,1]
	ds_read2_b32 v[112:113], v1 offset1:1
	v_mov_b32_e32 v1, 0x3a04
	s_waitcnt lgkmcnt(1)
	v_pk_fma_f32 v[108:109], v[216:217], v[110:111], v[108:109] op_sel_hi:[0,1,1]
	ds_read2_b32 v[110:111], v1 offset1:1
	v_mov_b32_e32 v1, 0x3a0c
	s_waitcnt lgkmcnt(1)
	v_pk_fma_f32 v[106:107], v[216:217], v[112:113], v[106:107] op_sel_hi:[0,1,1]
	ds_read2_b32 v[112:113], v1 offset1:1
	v_mov_b32_e32 v1, 0x3814
	ds_read2_b32 v[114:115], v1 offset1:1
	v_mov_b32_e32 v1, 0x381c
	ds_read2_b32 v[116:117], v1 offset1:1
	s_waitcnt lgkmcnt(3)
	v_pk_fma_f32 v[106:107], v[214:215], v[110:111], v[106:107] op_sel_hi:[0,1,1]
	v_pk_fma_f32 v[110:111], v[226:227], v[120:121], v[202:203] op_sel_hi:[0,1,1]
	v_mov_b32_e32 v1, 0x391c
	s_waitcnt lgkmcnt(2)
	v_pk_fma_f32 v[108:109], v[214:215], v[112:113], v[108:109] op_sel_hi:[0,1,1]
	v_pk_fma_f32 v[112:113], v[226:227], v[122:123], v[220:221] op_sel_hi:[0,1,1]
	s_waitcnt lgkmcnt(1)
	v_pk_fma_f32 v[110:111], v[218:219], v[114:115], v[110:111] op_sel_hi:[0,1,1]
	ds_read2_b32 v[114:115], v1 offset1:1
	v_mov_b32_e32 v1, 0x3914
	s_waitcnt lgkmcnt(1)
	v_pk_fma_f32 v[112:113], v[218:219], v[116:117], v[112:113] op_sel_hi:[0,1,1]
	ds_read2_b32 v[116:117], v1 offset1:1
	v_mov_b32_e32 v1, 0x3a14
	s_waitcnt lgkmcnt(1)
	v_pk_fma_f32 v[112:113], v[216:217], v[114:115], v[112:113] op_sel_hi:[0,1,1]
	ds_read2_b32 v[114:115], v1 offset1:1
	v_mov_b32_e32 v1, 0x3a1c
	s_waitcnt lgkmcnt(1)
	v_pk_fma_f32 v[110:111], v[216:217], v[116:117], v[110:111] op_sel_hi:[0,1,1]
	ds_read2_b32 v[116:117], v1 offset1:1
	v_mov_b32_e32 v1, 0x3824
	ds_read2_b32 v[118:119], v1 offset1:1
	v_mov_b32_e32 v1, 0x382c
	ds_read2_b32 v[120:121], v1 offset1:1
	s_waitcnt lgkmcnt(3)
	v_pk_fma_f32 v[110:111], v[214:215], v[114:115], v[110:111] op_sel_hi:[0,1,1]
	v_pk_fma_f32 v[114:115], v[226:227], v[242:243], v[194:195] op_sel_hi:[0,1,1]
	v_mov_b32_e32 v1, 0x392c
	s_waitcnt lgkmcnt(2)
	v_pk_fma_f32 v[112:113], v[214:215], v[116:117], v[112:113] op_sel_hi:[0,1,1]
	v_pk_fma_f32 v[116:117], v[226:227], v[244:245], v[196:197] op_sel_hi:[0,1,1]
	s_waitcnt lgkmcnt(1)
	v_pk_fma_f32 v[114:115], v[218:219], v[118:119], v[114:115] op_sel_hi:[0,1,1]
	ds_read2_b32 v[118:119], v1 offset1:1
	v_mov_b32_e32 v1, 0x3924
	s_waitcnt lgkmcnt(1)
	v_pk_fma_f32 v[116:117], v[218:219], v[120:121], v[116:117] op_sel_hi:[0,1,1]
	ds_read2_b32 v[120:121], v1 offset1:1
	v_mov_b32_e32 v1, 0x3a24
	s_waitcnt lgkmcnt(1)
	v_pk_fma_f32 v[116:117], v[216:217], v[118:119], v[116:117] op_sel_hi:[0,1,1]
	ds_read2_b32 v[118:119], v1 offset1:1
	v_mov_b32_e32 v1, 0x3a2c
	s_waitcnt lgkmcnt(1)
	v_pk_fma_f32 v[114:115], v[216:217], v[120:121], v[114:115] op_sel_hi:[0,1,1]
	ds_read2_b32 v[120:121], v1 offset1:1
	v_mov_b32_e32 v1, 0x3834
	ds_read2_b32 v[122:123], v1 offset1:1
	ds_read2_b32 v[248:249], v28 offset1:1
	v_mov_b32_e32 v28, 0x3744
	ds_read2_b32 v[238:239], v28 offset1:1
	v_mov_b32_e32 v28, 0x374c
	v_mov_b32_e32 v1, 0x383c
	ds_read2_b32 v[240:241], v28 offset1:1
	s_waitcnt lgkmcnt(5)
	v_pk_fma_f32 v[114:115], v[214:215], v[118:119], v[114:115] op_sel_hi:[0,1,1]
	v_pk_fma_f32 v[118:119], v[226:227], v[246:247], v[190:191] op_sel_hi:[0,1,1]
	ds_read2_b32 v[190:191], v1 offset1:1
	v_mov_b32_e32 v1, 0x393c
	s_waitcnt lgkmcnt(4)
	v_pk_fma_f32 v[118:119], v[218:219], v[122:123], v[118:119] op_sel_hi:[0,1,1]
	ds_read2_b32 v[122:123], v1 offset1:1
	v_pk_fma_f32 v[116:117], v[214:215], v[120:121], v[116:117] op_sel_hi:[0,1,1]
	s_waitcnt lgkmcnt(4)
	v_pk_fma_f32 v[120:121], v[226:227], v[248:249], v[192:193] op_sel_hi:[0,1,1]
	v_mov_b32_e32 v1, 0x3934
	s_waitcnt lgkmcnt(1)
	v_pk_fma_f32 v[120:121], v[218:219], v[190:191], v[120:121] op_sel_hi:[0,1,1]
	ds_read2_b32 v[190:191], v1 offset1:1
	v_mov_b32_e32 v1, 0x3a34
	s_waitcnt lgkmcnt(1)
	v_pk_fma_f32 v[120:121], v[216:217], v[122:123], v[120:121] op_sel_hi:[0,1,1]
	ds_read2_b32 v[122:123], v1 offset1:1
	v_mov_b32_e32 v1, 0x3a3c
	s_waitcnt lgkmcnt(1)
	v_pk_fma_f32 v[118:119], v[216:217], v[190:191], v[118:119] op_sel_hi:[0,1,1]
	ds_read2_b32 v[190:191], v1 offset1:1
	v_mov_b32_e32 v1, 0x3b0c
	s_waitcnt lgkmcnt(1)
	v_pk_fma_f32 v[118:119], v[214:215], v[122:123], v[118:119] op_sel_hi:[0,1,1]
	ds_read2_b32 v[122:123], v1 offset1:1
	v_mov_b32_e32 v1, 0x3b04
	s_waitcnt lgkmcnt(1)
	v_pk_fma_f32 v[120:121], v[214:215], v[190:191], v[120:121] op_sel_hi:[0,1,1]
	ds_read2_b32 v[190:191], v1 offset1:1
	v_mov_b32_e32 v1, 0x3b1c
	s_waitcnt lgkmcnt(1)
	v_pk_fma_f32 v[108:109], v[212:213], v[122:123], v[108:109] op_sel_hi:[0,1,1]
	ds_read2_b32 v[122:123], v1 offset1:1
	v_mov_b32_e32 v1, 0x3b14
	s_waitcnt lgkmcnt(1)
	v_pk_fma_f32 v[106:107], v[212:213], v[190:191], v[106:107] op_sel_hi:[0,1,1]
	ds_read2_b32 v[190:191], v1 offset1:1
	v_mov_b32_e32 v1, 0x3b2c
	s_waitcnt lgkmcnt(1)
	v_pk_fma_f32 v[112:113], v[212:213], v[122:123], v[112:113] op_sel_hi:[0,1,1]
	ds_read2_b32 v[122:123], v1 offset1:1
	v_mov_b32_e32 v1, 0x3b24
	s_waitcnt lgkmcnt(1)
	v_pk_fma_f32 v[110:111], v[212:213], v[190:191], v[110:111] op_sel_hi:[0,1,1]
	ds_read2_b32 v[190:191], v1 offset1:1
	v_mov_b32_e32 v1, 0x3b3c
	s_waitcnt lgkmcnt(1)
	v_pk_fma_f32 v[116:117], v[212:213], v[122:123], v[116:117] op_sel_hi:[0,1,1]
	ds_read2_b32 v[122:123], v1 offset1:1
	v_mov_b32_e32 v28, 0x3754
	v_mov_b32_e32 v1, 0x3b34
	ds_read2_b32 v[230:231], v28 offset1:1
	v_mov_b32_e32 v28, 0x375c
	s_waitcnt lgkmcnt(2)
	v_pk_fma_f32 v[114:115], v[212:213], v[190:191], v[114:115] op_sel_hi:[0,1,1]
	ds_read2_b32 v[190:191], v1 offset1:1
	v_mov_b32_e32 v1, 0x3844
	ds_read2_b32 v[232:233], v28 offset1:1
	s_waitcnt lgkmcnt(3)
	v_pk_fma_f32 v[120:121], v[212:213], v[122:123], v[120:121] op_sel_hi:[0,1,1]
	v_pk_fma_f32 v[122:123], v[226:227], v[238:239], v[178:179] op_sel_hi:[0,1,1]
	v_pk_fma_f32 v[178:179], v[226:227], v[240:241], v[180:181] op_sel_hi:[0,1,1]
	ds_read2_b32 v[180:181], v1 offset1:1
	v_mov_b32_e32 v1, 0x384c
	s_waitcnt lgkmcnt(2)
	v_pk_fma_f32 v[118:119], v[212:213], v[190:191], v[118:119] op_sel_hi:[0,1,1]
	ds_read2_b32 v[190:191], v1 offset1:1
	v_mov_b32_e32 v1, 0x394c
	s_waitcnt lgkmcnt(1)
	v_pk_fma_f32 v[122:123], v[218:219], v[180:181], v[122:123] op_sel_hi:[0,1,1]
	ds_read2_b32 v[180:181], v1 offset1:1
	v_mov_b32_e32 v1, 0x3944
	s_waitcnt lgkmcnt(1)
	v_pk_fma_f32 v[178:179], v[218:219], v[190:191], v[178:179] op_sel_hi:[0,1,1]
	ds_read2_b32 v[190:191], v1 offset1:1
	v_mov_b32_e32 v1, 0x3a44
	s_waitcnt lgkmcnt(1)
	v_pk_fma_f32 v[178:179], v[216:217], v[180:181], v[178:179] op_sel_hi:[0,1,1]
	ds_read2_b32 v[180:181], v1 offset1:1
	v_mov_b32_e32 v1, 0x3a4c
	s_waitcnt lgkmcnt(1)
	v_pk_fma_f32 v[122:123], v[216:217], v[190:191], v[122:123] op_sel_hi:[0,1,1]
	ds_read2_b32 v[190:191], v1 offset1:1
	v_mov_b32_e32 v1, 0x3b4c
	s_waitcnt lgkmcnt(1)
	v_pk_fma_f32 v[122:123], v[214:215], v[180:181], v[122:123] op_sel_hi:[0,1,1]
	ds_read2_b32 v[180:181], v1 offset1:1
	v_mov_b32_e32 v1, 0x3b44
	s_waitcnt lgkmcnt(1)
	v_pk_fma_f32 v[178:179], v[214:215], v[190:191], v[178:179] op_sel_hi:[0,1,1]
	ds_read2_b32 v[190:191], v1 offset1:1
	v_mov_b32_e32 v1, 0x3854
	s_waitcnt lgkmcnt(1)
	v_pk_fma_f32 v[178:179], v[212:213], v[180:181], v[178:179] op_sel_hi:[0,1,1]
	ds_read2_b32 v[180:181], v1 offset1:1
	v_mov_b32_e32 v1, 0x385c
	s_waitcnt lgkmcnt(1)
	v_pk_fma_f32 v[122:123], v[212:213], v[190:191], v[122:123] op_sel_hi:[0,1,1]
	v_pk_fma_f32 v[174:175], v[226:227], v[230:231], v[174:175] op_sel_hi:[0,1,1]
	ds_read2_b32 v[190:191], v1 offset1:1
	v_mov_b32_e32 v1, 0x395c
	s_waitcnt lgkmcnt(1)
	v_pk_fma_f32 v[174:175], v[218:219], v[180:181], v[174:175] op_sel_hi:[0,1,1]
	ds_read2_b32 v[180:181], v1 offset1:1
	v_pk_fma_f32 v[176:177], v[226:227], v[232:233], v[176:177] op_sel_hi:[0,1,1]
	v_mov_b32_e32 v1, 0x3954
	s_waitcnt lgkmcnt(1)
	v_pk_fma_f32 v[176:177], v[218:219], v[190:191], v[176:177] op_sel_hi:[0,1,1]
	ds_read2_b32 v[190:191], v1 offset1:1
	v_mov_b32_e32 v1, 0x3a54
	s_waitcnt lgkmcnt(1)
	v_pk_fma_f32 v[176:177], v[216:217], v[180:181], v[176:177] op_sel_hi:[0,1,1]
	ds_read2_b32 v[180:181], v1 offset1:1
	v_mov_b32_e32 v1, 0x3a5c
	s_waitcnt lgkmcnt(1)
	v_pk_fma_f32 v[174:175], v[216:217], v[190:191], v[174:175] op_sel_hi:[0,1,1]
	ds_read2_b32 v[190:191], v1 offset1:1
	v_mov_b32_e32 v1, 0x3b5c
	s_waitcnt lgkmcnt(1)
	v_pk_fma_f32 v[174:175], v[214:215], v[180:181], v[174:175] op_sel_hi:[0,1,1]
	ds_read2_b32 v[180:181], v1 offset1:1
	v_mov_b32_e32 v28, 0x3764
	v_mov_b32_e32 v1, 0x3b54
	ds_read2_b32 v[198:199], v28 offset1:1
	s_waitcnt lgkmcnt(2)
	v_pk_fma_f32 v[176:177], v[214:215], v[190:191], v[176:177] op_sel_hi:[0,1,1]
	ds_read2_b32 v[190:191], v1 offset1:1
	v_mov_b32_e32 v1, 0x3864
	s_waitcnt lgkmcnt(2)
	v_pk_fma_f32 v[176:177], v[212:213], v[180:181], v[176:177] op_sel_hi:[0,1,1]
	ds_read2_b32 v[180:181], v1 offset1:1
	v_mov_b32_e32 v28, 0x376c
	ds_read2_b32 v[200:201], v28 offset1:1
	v_mov_b32_e32 v1, 0x386c
	s_waitcnt lgkmcnt(2)
	v_pk_fma_f32 v[174:175], v[212:213], v[190:191], v[174:175] op_sel_hi:[0,1,1]
	v_pk_fma_f32 v[170:171], v[226:227], v[198:199], v[170:171] op_sel_hi:[0,1,1]
	ds_read2_b32 v[190:191], v1 offset1:1
	v_mov_b32_e32 v1, 0x396c
	s_waitcnt lgkmcnt(2)
	v_pk_fma_f32 v[170:171], v[218:219], v[180:181], v[170:171] op_sel_hi:[0,1,1]
	ds_read2_b32 v[180:181], v1 offset1:1
	s_waitcnt lgkmcnt(2)
	v_pk_fma_f32 v[172:173], v[226:227], v[200:201], v[172:173] op_sel_hi:[0,1,1]
	v_mov_b32_e32 v1, 0x3964
	s_waitcnt lgkmcnt(1)
	v_pk_fma_f32 v[172:173], v[218:219], v[190:191], v[172:173] op_sel_hi:[0,1,1]
	ds_read2_b32 v[190:191], v1 offset1:1
	v_mov_b32_e32 v1, 0x3a64
	s_waitcnt lgkmcnt(1)
	v_pk_fma_f32 v[172:173], v[216:217], v[180:181], v[172:173] op_sel_hi:[0,1,1]
	ds_read2_b32 v[180:181], v1 offset1:1
	v_mov_b32_e32 v1, 0x3a6c
	s_waitcnt lgkmcnt(1)
	v_pk_fma_f32 v[170:171], v[216:217], v[190:191], v[170:171] op_sel_hi:[0,1,1]
	ds_read2_b32 v[190:191], v1 offset1:1
	v_mov_b32_e32 v1, 0x3b6c
	s_waitcnt lgkmcnt(1)
	v_pk_fma_f32 v[170:171], v[214:215], v[180:181], v[170:171] op_sel_hi:[0,1,1]
	ds_read2_b32 v[180:181], v1 offset1:1
	v_mov_b32_e32 v28, 0x3774
	v_mov_b32_e32 v1, 0x3b64
	ds_read2_b32 v[186:187], v28 offset1:1
	s_waitcnt lgkmcnt(2)
	v_pk_fma_f32 v[172:173], v[214:215], v[190:191], v[172:173] op_sel_hi:[0,1,1]
	ds_read2_b32 v[190:191], v1 offset1:1
	v_mov_b32_e32 v1, 0x3874
	s_waitcnt lgkmcnt(2)
	v_pk_fma_f32 v[172:173], v[212:213], v[180:181], v[172:173] op_sel_hi:[0,1,1]
	ds_read2_b32 v[180:181], v1 offset1:1
	v_mov_b32_e32 v28, 0x377c
	ds_read2_b32 v[188:189], v28 offset1:1
	v_mov_b32_e32 v1, 0x387c
	s_waitcnt lgkmcnt(3)
	v_pk_fma_f32 v[166:167], v[226:227], v[186:187], v[166:167] op_sel_hi:[0,1,1]
	ds_read2_b32 v[186:187], v1 offset1:1
	v_mov_b32_e32 v1, 0x397c
	s_waitcnt lgkmcnt(2)
	v_pk_fma_f32 v[166:167], v[218:219], v[180:181], v[166:167] op_sel_hi:[0,1,1]
	ds_read2_b32 v[180:181], v1 offset1:1
	s_waitcnt lgkmcnt(2)
	v_pk_fma_f32 v[168:169], v[226:227], v[188:189], v[168:169] op_sel_hi:[0,1,1]
	v_mov_b32_e32 v1, 0x3974
	s_waitcnt lgkmcnt(1)
	v_pk_fma_f32 v[168:169], v[218:219], v[186:187], v[168:169] op_sel_hi:[0,1,1]
	ds_read2_b32 v[186:187], v1 offset1:1
	v_mov_b32_e32 v1, 0x3a74
	s_waitcnt lgkmcnt(1)
	v_pk_fma_f32 v[168:169], v[216:217], v[180:181], v[168:169] op_sel_hi:[0,1,1]
	ds_read2_b32 v[180:181], v1 offset1:1
	v_mov_b32_e32 v1, 0x3a7c
	s_waitcnt lgkmcnt(1)
	v_pk_fma_f32 v[166:167], v[216:217], v[186:187], v[166:167] op_sel_hi:[0,1,1]
	ds_read2_b32 v[186:187], v1 offset1:1
	v_mov_b32_e32 v1, 0x3b7c
	v_mov_b32_e32 v28, 0x3784
	s_waitcnt lgkmcnt(1)
	v_pk_fma_f32 v[166:167], v[214:215], v[180:181], v[166:167] op_sel_hi:[0,1,1]
	ds_read2_b32 v[180:181], v1 offset1:1
	ds_read2_b32 v[182:183], v28 offset1:1
	v_mov_b32_e32 v1, 0x3b74
	v_mov_b32_e32 v28, 0x378c
	s_waitcnt lgkmcnt(2)
	v_pk_fma_f32 v[168:169], v[214:215], v[186:187], v[168:169] op_sel_hi:[0,1,1]
	ds_read2_b32 v[186:187], v1 offset1:1
	v_mov_b32_e32 v1, 0x3884
	ds_read2_b32 v[184:185], v28 offset1:1
	s_waitcnt lgkmcnt(3)
	v_pk_fma_f32 v[168:169], v[212:213], v[180:181], v[168:169] op_sel_hi:[0,1,1]
	ds_read2_b32 v[180:181], v1 offset1:1
	v_mov_b32_e32 v1, 0x388c
	s_waitcnt lgkmcnt(3)
	v_pk_fma_f32 v[158:159], v[226:227], v[182:183], v[158:159] op_sel_hi:[0,1,1]
	ds_read2_b32 v[182:183], v1 offset1:1
	v_mov_b32_e32 v1, 0x3984
	s_waitcnt lgkmcnt(2)
	v_pk_fma_f32 v[160:161], v[226:227], v[184:185], v[160:161] op_sel_hi:[0,1,1]
	s_waitcnt lgkmcnt(1)
	v_pk_fma_f32 v[158:159], v[218:219], v[180:181], v[158:159] op_sel_hi:[0,1,1]
	ds_read2_b32 v[180:181], v1 offset1:1
	v_mov_b32_e32 v1, 0x398c
	s_waitcnt lgkmcnt(1)
	v_pk_fma_f32 v[160:161], v[218:219], v[182:183], v[160:161] op_sel_hi:[0,1,1]
	ds_read2_b32 v[182:183], v1 offset1:1
	v_mov_b32_e32 v1, 0x3a84
	s_waitcnt lgkmcnt(1)
	v_pk_fma_f32 v[158:159], v[216:217], v[180:181], v[158:159] op_sel_hi:[0,1,1]
	ds_read2_b32 v[180:181], v1 offset1:1
	v_mov_b32_e32 v1, 0x3a8c
	s_waitcnt lgkmcnt(1)
	v_pk_fma_f32 v[160:161], v[216:217], v[182:183], v[160:161] op_sel_hi:[0,1,1]
	ds_read2_b32 v[182:183], v1 offset1:1
	v_mov_b32_e32 v1, 0x3b84
	s_waitcnt lgkmcnt(1)
	v_pk_fma_f32 v[158:159], v[214:215], v[180:181], v[158:159] op_sel_hi:[0,1,1]
	ds_read2_b32 v[180:181], v1 offset1:1
	v_mov_b32_e32 v1, 0x3b8c
	s_waitcnt lgkmcnt(1)
	v_pk_fma_f32 v[160:161], v[214:215], v[182:183], v[160:161] op_sel_hi:[0,1,1]
	ds_read2_b32 v[182:183], v1 offset1:1
	v_mov_b32_e32 v1, 0x3c04
	s_waitcnt lgkmcnt(1)
	v_pk_fma_f32 v[158:159], v[212:213], v[180:181], v[158:159] op_sel_hi:[0,1,1]
	ds_read2_b32 v[180:181], v1 offset1:1
	v_mov_b32_e32 v1, 0x3c0c
	s_waitcnt lgkmcnt(1)
	v_pk_fma_f32 v[160:161], v[212:213], v[182:183], v[160:161] op_sel_hi:[0,1,1]
	ds_read2_b32 v[182:183], v1 offset1:1
	v_mov_b32_e32 v1, 0x3c14
	s_waitcnt lgkmcnt(1)
	v_pk_fma_f32 v[106:107], v[210:211], v[180:181], v[106:107] op_sel_hi:[0,1,1]
	ds_read2_b32 v[180:181], v1 offset1:1
	v_mov_b32_e32 v1, 0x3c1c
	s_waitcnt lgkmcnt(1)
	v_pk_fma_f32 v[108:109], v[210:211], v[182:183], v[108:109] op_sel_hi:[0,1,1]
	ds_read2_b32 v[182:183], v1 offset1:1
	v_mov_b32_e32 v1, 0x3c24
	s_waitcnt lgkmcnt(1)
	v_pk_fma_f32 v[110:111], v[210:211], v[180:181], v[110:111] op_sel_hi:[0,1,1]
	ds_read2_b32 v[180:181], v1 offset1:1
	v_mov_b32_e32 v1, 0x3c2c
	s_waitcnt lgkmcnt(1)
	v_pk_fma_f32 v[112:113], v[210:211], v[182:183], v[112:113] op_sel_hi:[0,1,1]
	ds_read2_b32 v[182:183], v1 offset1:1
	v_mov_b32_e32 v1, 0x3c34
	s_waitcnt lgkmcnt(1)
	v_pk_fma_f32 v[114:115], v[210:211], v[180:181], v[114:115] op_sel_hi:[0,1,1]
	ds_read2_b32 v[180:181], v1 offset1:1
	v_mov_b32_e32 v1, 0x3c3c
	s_waitcnt lgkmcnt(1)
	v_pk_fma_f32 v[116:117], v[210:211], v[182:183], v[116:117] op_sel_hi:[0,1,1]
	ds_read2_b32 v[182:183], v1 offset1:1
	v_mov_b32_e32 v1, 0x3c44
	s_waitcnt lgkmcnt(1)
	v_pk_fma_f32 v[118:119], v[210:211], v[180:181], v[118:119] op_sel_hi:[0,1,1]
	ds_read2_b32 v[180:181], v1 offset1:1
	v_mov_b32_e32 v1, 0x3c4c
	s_waitcnt lgkmcnt(1)
	v_pk_fma_f32 v[120:121], v[210:211], v[182:183], v[120:121] op_sel_hi:[0,1,1]
	ds_read2_b32 v[182:183], v1 offset1:1
	v_mov_b32_e32 v1, 0x3c54
	s_waitcnt lgkmcnt(1)
	v_pk_fma_f32 v[122:123], v[210:211], v[180:181], v[122:123] op_sel_hi:[0,1,1]
	ds_read2_b32 v[180:181], v1 offset1:1
	v_mov_b32_e32 v1, 0x3c5c
	s_waitcnt lgkmcnt(1)
	v_pk_fma_f32 v[178:179], v[210:211], v[182:183], v[178:179] op_sel_hi:[0,1,1]
	ds_read2_b32 v[182:183], v1 offset1:1
	v_mov_b32_e32 v1, 0x3c64
	s_waitcnt lgkmcnt(1)
	v_pk_fma_f32 v[174:175], v[210:211], v[180:181], v[174:175] op_sel_hi:[0,1,1]
	v_pk_fma_f32 v[170:171], v[212:213], v[190:191], v[170:171] op_sel_hi:[0,1,1]
	v_mov_b32_e32 v28, 0x3794
	s_waitcnt lgkmcnt(0)
	v_pk_fma_f32 v[182:183], v[210:211], v[182:183], v[176:177] op_sel_hi:[0,1,1]
	ds_read2_b32 v[176:177], v1 offset1:1
	v_mov_b32_e32 v1, 0x3c6c
	ds_read2_b32 v[180:181], v1 offset1:1
	v_mov_b32_e32 v1, 0x3c74
	ds_read2_b32 v[162:163], v28 offset1:1
	s_waitcnt lgkmcnt(2)
	v_pk_fma_f32 v[170:171], v[210:211], v[176:177], v[170:171] op_sel_hi:[0,1,1]
	ds_read2_b32 v[176:177], v1 offset1:1
	v_mov_b32_e32 v1, 0x3c7c
	s_waitcnt lgkmcnt(2)
	v_pk_fma_f32 v[172:173], v[210:211], v[180:181], v[172:173] op_sel_hi:[0,1,1]
	ds_read2_b32 v[180:181], v1 offset1:1
	v_mov_b32_e32 v28, 0x379c
	ds_read2_b32 v[164:165], v28 offset1:1
	v_pk_fma_f32 v[166:167], v[212:213], v[186:187], v[166:167] op_sel_hi:[0,1,1]
	v_mov_b32_e32 v1, 0x3c84
	s_waitcnt lgkmcnt(2)
	v_pk_fma_f32 v[166:167], v[210:211], v[176:177], v[166:167] op_sel_hi:[0,1,1]
	ds_read2_b32 v[176:177], v1 offset1:1
	v_mov_b32_e32 v1, 0x3c8c
	s_waitcnt lgkmcnt(2)
	v_pk_fma_f32 v[168:169], v[210:211], v[180:181], v[168:169] op_sel_hi:[0,1,1]
	ds_read2_b32 v[180:181], v1 offset1:1
	v_mov_b32_e32 v1, 0x3894
	v_pk_fma_f32 v[146:147], v[226:227], v[162:163], v[146:147] op_sel_hi:[0,1,1]
	ds_read2_b32 v[162:163], v1 offset1:1
	v_mov_b32_e32 v1, 0x389c
	s_waitcnt lgkmcnt(3)
	v_pk_fma_f32 v[148:149], v[226:227], v[164:165], v[148:149] op_sel_hi:[0,1,1]
	ds_read2_b32 v[164:165], v1 offset1:1
	v_mov_b32_e32 v1, 0x399c
	s_waitcnt lgkmcnt(1)
	v_pk_fma_f32 v[146:147], v[218:219], v[162:163], v[146:147] op_sel_hi:[0,1,1]
	ds_read2_b32 v[162:163], v1 offset1:1
	v_mov_b32_e32 v1, 0x3994
	s_waitcnt lgkmcnt(1)
	v_pk_fma_f32 v[148:149], v[218:219], v[164:165], v[148:149] op_sel_hi:[0,1,1]
	ds_read2_b32 v[164:165], v1 offset1:1
	v_mov_b32_e32 v1, 0x3a94
	s_waitcnt lgkmcnt(1)
	v_pk_fma_f32 v[148:149], v[216:217], v[162:163], v[148:149] op_sel_hi:[0,1,1]
	ds_read2_b32 v[162:163], v1 offset1:1
	v_mov_b32_e32 v1, 0x3a9c
	s_waitcnt lgkmcnt(1)
	v_pk_fma_f32 v[146:147], v[216:217], v[164:165], v[146:147] op_sel_hi:[0,1,1]
	ds_read2_b32 v[164:165], v1 offset1:1
	v_mov_b32_e32 v1, 0x3b9c
	s_waitcnt lgkmcnt(1)
	v_pk_fma_f32 v[146:147], v[214:215], v[162:163], v[146:147] op_sel_hi:[0,1,1]
	ds_read2_b32 v[162:163], v1 offset1:1
	v_mov_b32_e32 v1, 0x3b94
	v_mov_b32_e32 v28, 0x37a4
	s_waitcnt lgkmcnt(1)
	v_pk_fma_f32 v[148:149], v[214:215], v[164:165], v[148:149] op_sel_hi:[0,1,1]
	ds_read2_b32 v[164:165], v1 offset1:1
	ds_read2_b32 v[154:155], v28 offset1:1
	v_mov_b32_e32 v28, 0x37ac
	ds_read2_b32 v[156:157], v28 offset1:1
	v_mov_b32_e32 v1, 0x3c94
	s_waitcnt lgkmcnt(3)
	v_pk_fma_f32 v[148:149], v[212:213], v[162:163], v[148:149] op_sel_hi:[0,1,1]
	ds_read2_b32 v[162:163], v1 offset1:1
	v_mov_b32_e32 v1, 0x3c9c
	s_waitcnt lgkmcnt(3)
	v_pk_fma_f32 v[146:147], v[212:213], v[164:165], v[146:147] op_sel_hi:[0,1,1]
	ds_read2_b32 v[164:165], v1 offset1:1
	v_mov_b32_e32 v1, 0x38ac
	s_waitcnt lgkmcnt(3)
	v_pk_fma_f32 v[46:47], v[226:227], v[154:155], v[46:47] op_sel_hi:[0,1,1]
	ds_read2_b32 v[154:155], v1 offset1:1
	v_mov_b32_e32 v1, 0x38a4
	s_waitcnt lgkmcnt(3)
	v_pk_fma_f32 v[144:145], v[226:227], v[156:157], v[144:145] op_sel_hi:[0,1,1]
	ds_read2_b32 v[156:157], v1 offset1:1
	v_mov_b32_e32 v1, 0x39ac
	s_waitcnt lgkmcnt(1)
	v_pk_fma_f32 v[144:145], v[218:219], v[154:155], v[144:145] op_sel_hi:[0,1,1]
	ds_read2_b32 v[154:155], v1 offset1:1
	v_mov_b32_e32 v1, 0x39a4
	s_waitcnt lgkmcnt(1)
	v_pk_fma_f32 v[46:47], v[218:219], v[156:157], v[46:47] op_sel_hi:[0,1,1]
	ds_read2_b32 v[156:157], v1 offset1:1
	v_mov_b32_e32 v1, 0x3aac
	s_waitcnt lgkmcnt(1)
	v_pk_fma_f32 v[144:145], v[216:217], v[154:155], v[144:145] op_sel_hi:[0,1,1]
	ds_read2_b32 v[154:155], v1 offset1:1
	v_mov_b32_e32 v1, 0x3aa4
	s_waitcnt lgkmcnt(1)
	v_pk_fma_f32 v[46:47], v[216:217], v[156:157], v[46:47] op_sel_hi:[0,1,1]
	ds_read2_b32 v[156:157], v1 offset1:1
	v_mov_b32_e32 v1, 0x3bac
	s_waitcnt lgkmcnt(1)
	v_pk_fma_f32 v[144:145], v[214:215], v[154:155], v[144:145] op_sel_hi:[0,1,1]
	ds_read2_b32 v[154:155], v1 offset1:1
	v_mov_b32_e32 v1, 0x3ba4
	s_waitcnt lgkmcnt(1)
	v_pk_fma_f32 v[46:47], v[214:215], v[156:157], v[46:47] op_sel_hi:[0,1,1]
	ds_read2_b32 v[156:157], v1 offset1:1
	v_mov_b32_e32 v1, 0x3cac
	s_waitcnt lgkmcnt(1)
	v_pk_fma_f32 v[144:145], v[212:213], v[154:155], v[144:145] op_sel_hi:[0,1,1]
	ds_read2_b32 v[154:155], v1 offset1:1
	v_mov_b32_e32 v1, 0x3ca4
	s_waitcnt lgkmcnt(1)
	v_pk_fma_f32 v[46:47], v[212:213], v[156:157], v[46:47] op_sel_hi:[0,1,1]
	ds_read2_b32 v[156:157], v1 offset1:1
	v_mov_b32_e32 v1, 0x3d0c
	s_waitcnt lgkmcnt(1)
	v_pk_fma_f32 v[144:145], v[210:211], v[154:155], v[144:145] op_sel_hi:[0,1,1]
	ds_read2_b32 v[154:155], v1 offset1:1
	v_mov_b32_e32 v1, 0x3d04
	s_waitcnt lgkmcnt(1)
	v_pk_fma_f32 v[46:47], v[210:211], v[156:157], v[46:47] op_sel_hi:[0,1,1]
	ds_read2_b32 v[156:157], v1 offset1:1
	v_mov_b32_e32 v1, 0x3d1c
	s_waitcnt lgkmcnt(1)
	v_pk_fma_f32 v[108:109], v[206:207], v[154:155], v[108:109] op_sel_hi:[0,1,1]
	ds_read2_b32 v[154:155], v1 offset1:1
	v_mov_b32_e32 v1, 0x3d14
	s_waitcnt lgkmcnt(1)
	v_pk_fma_f32 v[106:107], v[206:207], v[156:157], v[106:107] op_sel_hi:[0,1,1]
	ds_read2_b32 v[156:157], v1 offset1:1
	v_mov_b32_e32 v1, 0x3d2c
	s_waitcnt lgkmcnt(1)
	v_pk_fma_f32 v[112:113], v[206:207], v[154:155], v[112:113] op_sel_hi:[0,1,1]
	ds_read2_b32 v[154:155], v1 offset1:1
	v_mov_b32_e32 v1, 0x3d24
	s_waitcnt lgkmcnt(1)
	v_pk_fma_f32 v[110:111], v[206:207], v[156:157], v[110:111] op_sel_hi:[0,1,1]
	ds_read2_b32 v[156:157], v1 offset1:1
	v_mov_b32_e32 v1, 0x3d3c
	s_waitcnt lgkmcnt(1)
	v_pk_fma_f32 v[116:117], v[206:207], v[154:155], v[116:117] op_sel_hi:[0,1,1]
	ds_read2_b32 v[154:155], v1 offset1:1
	v_mov_b32_e32 v1, 0x3d34
	s_waitcnt lgkmcnt(1)
	v_pk_fma_f32 v[114:115], v[206:207], v[156:157], v[114:115] op_sel_hi:[0,1,1]
	ds_read2_b32 v[156:157], v1 offset1:1
	v_mov_b32_e32 v1, 0x3d4c
	s_waitcnt lgkmcnt(1)
	v_pk_fma_f32 v[120:121], v[206:207], v[154:155], v[120:121] op_sel_hi:[0,1,1]
	ds_read2_b32 v[154:155], v1 offset1:1
	v_mov_b32_e32 v1, 0x3d44
	v_mov_b32_e32 v28, 0x37b4
	s_waitcnt lgkmcnt(1)
	v_pk_fma_f32 v[118:119], v[206:207], v[156:157], v[118:119] op_sel_hi:[0,1,1]
	ds_read2_b32 v[156:157], v1 offset1:1
	ds_read2_b32 v[150:151], v28 offset1:1
	v_mov_b32_e32 v28, 0x37bc
	v_mov_b32_e32 v1, 0x38b4
	ds_read2_b32 v[152:153], v28 offset1:1
	v_pk_fma_f32 v[158:159], v[210:211], v[176:177], v[158:159] op_sel_hi:[0,1,1]
	s_waitcnt lgkmcnt(2)
	v_pk_fma_f32 v[176:177], v[206:207], v[156:157], v[122:123] op_sel_hi:[0,1,1]
	ds_read2_b32 v[122:123], v1 offset1:1
	v_mov_b32_e32 v1, 0x38bc
	s_waitcnt lgkmcnt(2)
	v_pk_fma_f32 v[38:39], v[226:227], v[150:151], v[38:39] op_sel_hi:[0,1,1]
	ds_read2_b32 v[150:151], v1 offset1:1
	v_mov_b32_e32 v1, 0x39b4
	s_waitcnt lgkmcnt(2)
	v_pk_fma_f32 v[40:41], v[226:227], v[152:153], v[40:41] op_sel_hi:[0,1,1]
	s_waitcnt lgkmcnt(1)
	v_pk_fma_f32 v[38:39], v[218:219], v[122:123], v[38:39] op_sel_hi:[0,1,1]
	ds_read2_b32 v[122:123], v1 offset1:1
	v_mov_b32_e32 v1, 0x39bc
	s_waitcnt lgkmcnt(1)
	v_pk_fma_f32 v[40:41], v[218:219], v[150:151], v[40:41] op_sel_hi:[0,1,1]
	ds_read2_b32 v[150:151], v1 offset1:1
	v_mov_b32_e32 v1, 0x3ab4
	s_waitcnt lgkmcnt(1)
	v_pk_fma_f32 v[38:39], v[216:217], v[122:123], v[38:39] op_sel_hi:[0,1,1]
	ds_read2_b32 v[122:123], v1 offset1:1
	v_mov_b32_e32 v1, 0x3abc
	s_waitcnt lgkmcnt(1)
	v_pk_fma_f32 v[40:41], v[216:217], v[150:151], v[40:41] op_sel_hi:[0,1,1]
	ds_read2_b32 v[150:151], v1 offset1:1
	v_mov_b32_e32 v1, 0x3bb4
	s_waitcnt lgkmcnt(1)
	v_pk_fma_f32 v[38:39], v[214:215], v[122:123], v[38:39] op_sel_hi:[0,1,1]
	ds_read2_b32 v[122:123], v1 offset1:1
	v_mov_b32_e32 v1, 0x3bbc
	s_waitcnt lgkmcnt(1)
	v_pk_fma_f32 v[40:41], v[214:215], v[150:151], v[40:41] op_sel_hi:[0,1,1]
	ds_read2_b32 v[150:151], v1 offset1:1
	v_mov_b32_e32 v1, 0x3cb4
	s_waitcnt lgkmcnt(1)
	v_pk_fma_f32 v[38:39], v[212:213], v[122:123], v[38:39] op_sel_hi:[0,1,1]
	ds_read2_b32 v[122:123], v1 offset1:1
	v_mov_b32_e32 v1, 0x3cbc
	s_waitcnt lgkmcnt(1)
	v_pk_fma_f32 v[40:41], v[212:213], v[150:151], v[40:41] op_sel_hi:[0,1,1]
	ds_read2_b32 v[150:151], v1 offset1:1
	v_mov_b32_e32 v1, 0x3d5c
	s_waitcnt lgkmcnt(1)
	v_pk_fma_f32 v[38:39], v[210:211], v[122:123], v[38:39] op_sel_hi:[0,1,1]
	ds_read2_b32 v[122:123], v1 offset1:1
	v_mov_b32_e32 v1, 0x3d54
	s_waitcnt lgkmcnt(1)
	v_pk_fma_f32 v[40:41], v[210:211], v[150:151], v[40:41] op_sel_hi:[0,1,1]
	ds_read2_b32 v[150:151], v1 offset1:1
	v_mov_b32_e32 v1, 0x3d6c
	s_waitcnt lgkmcnt(1)
	v_pk_fma_f32 v[192:193], v[206:207], v[122:123], v[182:183] op_sel_hi:[0,1,1]
	ds_read2_b32 v[122:123], v1 offset1:1
	v_mov_b32_e32 v1, 0x3d64
	v_pk_fma_f32 v[160:161], v[210:211], v[180:181], v[160:161] op_sel_hi:[0,1,1]
	s_waitcnt lgkmcnt(1)
	v_pk_fma_f32 v[180:181], v[206:207], v[150:151], v[174:175] op_sel_hi:[0,1,1]
	ds_read2_b32 v[150:151], v1 offset1:1
	v_mov_b32_e32 v1, 0x3d7c
	s_waitcnt lgkmcnt(1)
	v_pk_fma_f32 v[194:195], v[206:207], v[122:123], v[172:173] op_sel_hi:[0,1,1]
	ds_read2_b32 v[122:123], v1 offset1:1
	v_mov_b32_e32 v1, 0x3d74
	s_waitcnt lgkmcnt(1)
	v_pk_fma_f32 v[182:183], v[206:207], v[150:151], v[170:171] op_sel_hi:[0,1,1]
	ds_read2_b32 v[150:151], v1 offset1:1
	v_mov_b32_e32 v1, 0x3d84
	s_waitcnt lgkmcnt(1)
	v_pk_fma_f32 v[196:197], v[206:207], v[122:123], v[168:169] op_sel_hi:[0,1,1]
	ds_read2_b32 v[122:123], v1 offset1:1
	v_mov_b32_e32 v1, 0x3d8c
	s_waitcnt lgkmcnt(1)
	v_pk_fma_f32 v[184:185], v[206:207], v[150:151], v[166:167] op_sel_hi:[0,1,1]
	ds_read2_b32 v[150:151], v1 offset1:1
	v_mov_b32_e32 v1, 0x3d9c
	s_waitcnt lgkmcnt(1)
	v_pk_fma_f32 v[190:191], v[206:207], v[122:123], v[158:159] op_sel_hi:[0,1,1]
	ds_read2_b32 v[122:123], v1 offset1:1
	v_mov_b32_e32 v1, 0x3d94
	s_waitcnt lgkmcnt(1)
	v_pk_fma_f32 v[188:189], v[206:207], v[150:151], v[160:161] op_sel_hi:[0,1,1]
	ds_read2_b32 v[150:151], v1 offset1:1
	v_pk_fma_f32 v[148:149], v[210:211], v[164:165], v[148:149] op_sel_hi:[0,1,1]
	v_mov_b32_e32 v1, 0x3dac
	v_pk_fma_f32 v[146:147], v[210:211], v[162:163], v[146:147] op_sel_hi:[0,1,1]
	s_waitcnt lgkmcnt(1)
	v_pk_fma_f32 v[198:199], v[206:207], v[122:123], v[148:149] op_sel_hi:[0,1,1]
	ds_read2_b32 v[122:123], v1 offset1:1
	v_mov_b32_e32 v1, 0x3da4
	s_waitcnt lgkmcnt(1)
	v_pk_fma_f32 v[186:187], v[206:207], v[150:151], v[146:147] op_sel_hi:[0,1,1]
	ds_read2_b32 v[146:147], v1 offset1:1
	v_mov_b32_e32 v1, 0x3db4
	s_waitcnt lgkmcnt(1)
	v_pk_fma_f32 v[150:151], v[206:207], v[122:123], v[144:145] op_sel_hi:[0,1,1]
	v_mov_b32_e32 v28, 0x37c4
	ds_read2_b32 v[42:43], v28 offset1:1
	s_waitcnt lgkmcnt(1)
	v_pk_fma_f32 v[148:149], v[206:207], v[146:147], v[46:47] op_sel_hi:[0,1,1]
	ds_read2_b32 v[46:47], v1 offset1:1
	v_mov_b32_e32 v1, 0x3dbc
	ds_read2_b32 v[122:123], v1 offset1:1
	v_mov_b32_e32 v28, 0x37cc
	v_mov_b32_e32 v1, 0x38c4
	ds_read2_b32 v[44:45], v28 offset1:1
	v_pk_fma_f32 v[178:179], v[206:207], v[154:155], v[178:179] op_sel_hi:[0,1,1]
	s_waitcnt lgkmcnt(2)
	v_pk_fma_f32 v[154:155], v[206:207], v[46:47], v[38:39] op_sel_hi:[0,1,1]
	ds_read2_b32 v[38:39], v1 offset1:1
	v_mov_b32_e32 v1, 0x38cc
	s_waitcnt lgkmcnt(2)
	v_pk_fma_f32 v[152:153], v[206:207], v[122:123], v[40:41] op_sel_hi:[0,1,1]
	ds_read2_b32 v[40:41], v1 offset1:1
	v_pk_fma_f32 v[24:25], v[226:227], v[42:43], v[24:25] op_sel_hi:[0,1,1]
	v_mov_b32_e32 v1, 0x39cc
	s_waitcnt lgkmcnt(2)
	v_pk_fma_f32 v[26:27], v[226:227], v[44:45], v[26:27] op_sel_hi:[0,1,1]
	s_waitcnt lgkmcnt(1)
	v_pk_fma_f32 v[24:25], v[218:219], v[38:39], v[24:25] op_sel_hi:[0,1,1]
	ds_read2_b32 v[38:39], v1 offset1:1
	v_mov_b32_e32 v1, 0x39c4
	s_waitcnt lgkmcnt(1)
	v_pk_fma_f32 v[26:27], v[218:219], v[40:41], v[26:27] op_sel_hi:[0,1,1]
	ds_read2_b32 v[40:41], v1 offset1:1
	v_mov_b32_e32 v1, 0x3ac4
	s_waitcnt lgkmcnt(1)
	v_pk_fma_f32 v[26:27], v[216:217], v[38:39], v[26:27] op_sel_hi:[0,1,1]
	ds_read2_b32 v[38:39], v1 offset1:1
	v_mov_b32_e32 v1, 0x3acc
	s_waitcnt lgkmcnt(1)
	v_pk_fma_f32 v[24:25], v[216:217], v[40:41], v[24:25] op_sel_hi:[0,1,1]
	ds_read2_b32 v[40:41], v1 offset1:1
	v_mov_b32_e32 v1, 0x3bcc
	s_waitcnt lgkmcnt(1)
	v_pk_fma_f32 v[24:25], v[214:215], v[38:39], v[24:25] op_sel_hi:[0,1,1]
	ds_read2_b32 v[38:39], v1 offset1:1
	v_mov_b32_e32 v1, 0x3bc4
	s_waitcnt lgkmcnt(1)
	v_pk_fma_f32 v[26:27], v[214:215], v[40:41], v[26:27] op_sel_hi:[0,1,1]
	ds_read2_b32 v[40:41], v1 offset1:1
	v_mov_b32_e32 v1, 0x3cc4
	s_waitcnt lgkmcnt(1)
	v_pk_fma_f32 v[26:27], v[212:213], v[38:39], v[26:27] op_sel_hi:[0,1,1]
	ds_read2_b32 v[38:39], v1 offset1:1
	v_mov_b32_e32 v1, 0x3ccc
	s_waitcnt lgkmcnt(1)
	v_pk_fma_f32 v[24:25], v[212:213], v[40:41], v[24:25] op_sel_hi:[0,1,1]
	ds_read2_b32 v[40:41], v1 offset1:1
	v_mov_b32_e32 v1, 0x3dcc
	s_waitcnt lgkmcnt(1)
	v_pk_fma_f32 v[24:25], v[210:211], v[38:39], v[24:25] op_sel_hi:[0,1,1]
	ds_read2_b32 v[38:39], v1 offset1:1
	v_mov_b32_e32 v1, 0x3dc4
	s_waitcnt lgkmcnt(1)
	v_pk_fma_f32 v[26:27], v[210:211], v[40:41], v[26:27] op_sel_hi:[0,1,1]
	ds_read2_b32 v[40:41], v1 offset1:1
	v_mov_b32_e32 v1, 0x3e04
	s_waitcnt lgkmcnt(1)
	v_pk_fma_f32 v[174:175], v[206:207], v[38:39], v[26:27] op_sel_hi:[0,1,1]
	v_mov_b32_e32 v28, 0x37d4
	ds_read2_b32 v[28:29], v28 offset1:1
	s_waitcnt lgkmcnt(1)
	v_pk_fma_f32 v[172:173], v[206:207], v[40:41], v[24:25] op_sel_hi:[0,1,1]
	ds_read2_b32 v[24:25], v1 offset1:1
	v_mov_b32_e32 v1, 0x3e0c
	ds_read2_b32 v[26:27], v1 offset1:1
	v_mov_b32_e32 v1, 0x3e14
	s_waitcnt lgkmcnt(2)
	v_pk_fma_f32 v[200:201], v[226:227], v[28:29], v[8:9] op_sel_hi:[0,1,1]
	s_waitcnt lgkmcnt(1)
	v_pk_fma_f32 v[164:165], v[204:205], v[24:25], v[106:107] op_sel_hi:[0,1,1]
	ds_read2_b32 v[24:25], v1 offset1:1
	v_mov_b32_e32 v1, 0x3e1c
	s_waitcnt lgkmcnt(1)
	v_pk_fma_f32 v[156:157], v[204:205], v[26:27], v[108:109] op_sel_hi:[0,1,1]
	ds_read2_b32 v[26:27], v1 offset1:1
	v_mov_b32_e32 v1, 0x3e24
	s_waitcnt lgkmcnt(1)
	v_pk_fma_f32 v[166:167], v[204:205], v[24:25], v[110:111] op_sel_hi:[0,1,1]
	ds_read2_b32 v[24:25], v1 offset1:1
	v_mov_b32_e32 v1, 0x3e2c
	s_waitcnt lgkmcnt(1)
	v_pk_fma_f32 v[158:159], v[204:205], v[26:27], v[112:113] op_sel_hi:[0,1,1]
	ds_read2_b32 v[26:27], v1 offset1:1
	v_mov_b32_e32 v1, 0x3e34
	s_waitcnt lgkmcnt(1)
	v_pk_fma_f32 v[168:169], v[204:205], v[24:25], v[114:115] op_sel_hi:[0,1,1]
	ds_read2_b32 v[24:25], v1 offset1:1
	v_mov_b32_e32 v1, 0x3e3c
	s_waitcnt lgkmcnt(1)
	v_pk_fma_f32 v[160:161], v[204:205], v[26:27], v[116:117] op_sel_hi:[0,1,1]
	ds_read2_b32 v[26:27], v1 offset1:1
	v_mov_b32_e32 v1, 0x36fc
	ds_read2_b32 v[8:9], v1 offset1:1
	v_cndmask_b32_e32 v208, v103, v3, vcc
	v_pk_fma_f32 v[2:3], v[2:3], v[222:223], v[224:225] op_sel_hi:[0,1,1]
	v_mov_b32_e32 v36, 0x37f4
	ds_read2_b32 v[30:31], v30 offset1:1
	s_waitcnt lgkmcnt(1)
	v_mov_b32_e32 v228, v8
	v_pk_fma_f32 v[2:3], v[0:1], v[228:229], v[2:3] op_sel_hi:[0,1,1]
	v_mov_b32_e32 v0, 0x37fc
	ds_read2_b32 v[0:1], v0 offset1:1
	ds_read2_b32 v[32:33], v32 offset1:1
	ds_read2_b32 v[34:35], v34 offset1:1
	ds_read2_b32 v[36:37], v36 offset1:1
	s_waitcnt lgkmcnt(4)
	v_pk_fma_f32 v[202:203], v[226:227], v[30:31], v[10:11] op_sel_hi:[0,1,1]
	s_waitcnt lgkmcnt(3)
	v_mov_b32_e32 v8, v0
	v_mov_b32_e32 v0, 0x38fc
	v_pk_fma_f32 v[2:3], v[226:227], v[8:9], v[2:3] op_sel_hi:[0,1,1]
	ds_read2_b32 v[8:9], v0 offset1:1
	s_waitcnt lgkmcnt(2)
	v_pk_fma_f32 v[146:147], v[226:227], v[34:35], v[20:21] op_sel_hi:[0,1,1]
	v_pk_fma_f32 v[144:145], v[226:227], v[32:33], v[18:19] op_sel_hi:[0,1,1]
	s_waitcnt lgkmcnt(1)
	v_pk_fma_f32 v[220:221], v[226:227], v[36:37], v[22:23] op_sel_hi:[0,1,1]
	v_pk_fma_f32 v[170:171], v[204:205], v[24:25], v[118:119] op_sel_hi:[0,1,1]
	s_waitcnt lgkmcnt(0)
	v_mov_b32_e32 v0, v8
	v_pk_fma_f32 v[0:1], v[218:219], v[0:1], v[2:3] op_sel_hi:[0,1,1]
	v_mov_b32_e32 v2, 0x39fc
	ds_read2_b32 v[2:3], v2 offset1:1
	v_pk_fma_f32 v[162:163], v[204:205], v[26:27], v[120:121] op_sel_hi:[0,1,1]
	v_mov_b32_e32 v105, 0x3f0c
	s_waitcnt lgkmcnt(0)
	v_mov_b32_e32 v8, v2
	v_mov_b32_e32 v2, 0x3afc
	v_pk_fma_f32 v[0:1], v[216:217], v[8:9], v[0:1] op_sel_hi:[0,1,1]
	ds_read2_b32 v[8:9], v2 offset1:1
	s_waitcnt lgkmcnt(0)
	v_mov_b32_e32 v2, v8
	v_pk_fma_f32 v[0:1], v[214:215], v[2:3], v[0:1] op_sel_hi:[0,1,1]
	v_mov_b32_e32 v2, 0x3bfc
	ds_read2_b32 v[2:3], v2 offset1:1
	s_waitcnt lgkmcnt(0)
	v_mov_b32_e32 v8, v2
	v_mov_b32_e32 v2, 0x3cfc
	v_pk_fma_f32 v[0:1], v[212:213], v[8:9], v[0:1] op_sel_hi:[0,1,1]
	ds_read2_b32 v[8:9], v2 offset1:1
	s_waitcnt lgkmcnt(0)
	v_mov_b32_e32 v2, v8
	v_pk_fma_f32 v[0:1], v[210:211], v[2:3], v[0:1] op_sel_hi:[0,1,1]
	v_mov_b32_e32 v2, 0x3dfc
	ds_read2_b32 v[2:3], v2 offset1:1
	s_waitcnt lgkmcnt(0)
	v_mov_b32_e32 v8, v2
	v_pk_fma_f32 v[226:227], v[206:207], v[8:9], v[0:1] op_sel_hi:[0,1,1]
	v_mov_b32_e32 v0, 0x3e44
	ds_read2_b32 v[0:1], v0 offset1:1
	v_mov_b32_e32 v2, 0x3e4c
	ds_read2_b32 v[8:9], v2 offset1:1
	v_mov_b32_e32 v2, 0x3e5c
	s_waitcnt lgkmcnt(1)
	v_pk_fma_f32 v[176:177], v[204:205], v[0:1], v[176:177] op_sel_hi:[0,1,1]
	v_mov_b32_e32 v0, 0x3e54
	ds_read2_b32 v[0:1], v0 offset1:1
	s_waitcnt lgkmcnt(1)
	v_pk_fma_f32 v[46:47], v[204:205], v[8:9], v[178:179] op_sel_hi:[0,1,1]
	ds_read2_b32 v[8:9], v2 offset1:1
	v_mov_b32_e32 v2, 0x3e6c
	s_waitcnt lgkmcnt(1)
	v_pk_fma_f32 v[224:225], v[204:205], v[0:1], v[180:181] op_sel_hi:[0,1,1]
	v_mov_b32_e32 v0, 0x3e64
	ds_read2_b32 v[0:1], v0 offset1:1
	s_waitcnt lgkmcnt(1)
	v_pk_fma_f32 v[222:223], v[204:205], v[8:9], v[192:193] op_sel_hi:[0,1,1]
	ds_read2_b32 v[8:9], v2 offset1:1
	v_mov_b32_e32 v2, 0x3e7c
	ds_read2_b32 v[10:11], v2 offset1:1
	s_waitcnt lgkmcnt(2)
	v_pk_fma_f32 v[24:25], v[204:205], v[0:1], v[182:183] op_sel_hi:[0,1,1]
	v_mov_b32_e32 v0, 0x3e74
	ds_read2_b32 v[0:1], v0 offset1:1
	v_mov_b32_e32 v2, 0x3e8c
	ds_read2_b32 v[18:19], v2 offset1:1
	v_mov_b32_e32 v2, 0x3e9c
	s_waitcnt lgkmcnt(3)
	v_pk_fma_f32 v[8:9], v[204:205], v[8:9], v[194:195] op_sel_hi:[0,1,1]
	s_waitcnt lgkmcnt(1)
	v_pk_fma_f32 v[26:27], v[204:205], v[0:1], v[184:185] op_sel_hi:[0,1,1]
	v_mov_b32_e32 v0, 0x3e84
	ds_read2_b32 v[0:1], v0 offset1:1
	s_waitcnt lgkmcnt(1)
	v_pk_fma_f32 v[20:21], v[204:205], v[18:19], v[188:189] op_sel_hi:[0,1,1]
	ds_read2_b32 v[18:19], v2 offset1:1
	v_mov_b32_e32 v2, 0x38d4
	ds_read2_b32 v[30:31], v2 offset1:1
	s_waitcnt lgkmcnt(2)
	v_pk_fma_f32 v[22:23], v[204:205], v[0:1], v[190:191] op_sel_hi:[0,1,1]
	v_mov_b32_e32 v0, 0x3e94
	ds_read2_b32 v[0:1], v0 offset1:1
	v_mov_b32_e32 v2, 0x39dc
	ds_read2_b32 v[32:33], v2 offset1:1
	v_mov_b32_e32 v2, 0x39d4
	ds_read2_b32 v[34:35], v2 offset1:1
	s_waitcnt lgkmcnt(2)
	v_pk_fma_f32 v[28:29], v[204:205], v[0:1], v[186:187] op_sel_hi:[0,1,1]
	v_mov_b32_e32 v0, 0x38dc
	ds_read2_b32 v[0:1], v0 offset1:1
	v_mov_b32_e32 v2, 0x3adc
	v_pk_fma_f32 v[30:31], v[218:219], v[30:31], v[200:201] op_sel_hi:[0,1,1]
	s_waitcnt lgkmcnt(1)
	v_pk_fma_f32 v[30:31], v[216:217], v[34:35], v[30:31] op_sel_hi:[0,1,1]
	v_pk_fma_f32 v[10:11], v[204:205], v[10:11], v[196:197] op_sel_hi:[0,1,1]
	s_waitcnt lgkmcnt(0)
	v_pk_fma_f32 v[0:1], v[218:219], v[0:1], v[202:203] op_sel_hi:[0,1,1]
	v_pk_fma_f32 v[0:1], v[216:217], v[32:33], v[0:1] op_sel_hi:[0,1,1]
	ds_read2_b32 v[32:33], v2 offset1:1
	v_mov_b32_e32 v2, 0x3ad4
	ds_read2_b32 v[34:35], v2 offset1:1
	v_mov_b32_e32 v2, 0x3bdc
	v_pk_fma_f32 v[18:19], v[204:205], v[18:19], v[198:199] op_sel_hi:[0,1,1]
	s_waitcnt lgkmcnt(1)
	v_pk_fma_f32 v[0:1], v[214:215], v[32:33], v[0:1] op_sel_hi:[0,1,1]
	ds_read2_b32 v[32:33], v2 offset1:1
	v_mov_b32_e32 v2, 0x3bd4
	s_waitcnt lgkmcnt(1)
	v_pk_fma_f32 v[30:31], v[214:215], v[34:35], v[30:31] op_sel_hi:[0,1,1]
	ds_read2_b32 v[34:35], v2 offset1:1
	v_mov_b32_e32 v2, 0x3cdc
	s_waitcnt lgkmcnt(1)
	v_pk_fma_f32 v[0:1], v[212:213], v[32:33], v[0:1] op_sel_hi:[0,1,1]
	ds_read2_b32 v[32:33], v2 offset1:1
	v_mov_b32_e32 v2, 0x3cd4
	s_waitcnt lgkmcnt(1)
	v_pk_fma_f32 v[30:31], v[212:213], v[34:35], v[30:31] op_sel_hi:[0,1,1]
	ds_read2_b32 v[34:35], v2 offset1:1
	v_mov_b32_e32 v2, 0x3ddc
	s_waitcnt lgkmcnt(1)
	v_pk_fma_f32 v[0:1], v[210:211], v[32:33], v[0:1] op_sel_hi:[0,1,1]
	ds_read2_b32 v[32:33], v2 offset1:1
	v_mov_b32_e32 v2, 0x3dd4
	s_waitcnt lgkmcnt(1)
	v_pk_fma_f32 v[30:31], v[210:211], v[34:35], v[30:31] op_sel_hi:[0,1,1]
	ds_read2_b32 v[34:35], v2 offset1:1
	v_mov_b32_e32 v2, 0x3eac
	s_waitcnt lgkmcnt(1)
	v_pk_fma_f32 v[0:1], v[206:207], v[32:33], v[0:1] op_sel_hi:[0,1,1]
	s_waitcnt lgkmcnt(0)
	v_pk_fma_f32 v[40:41], v[206:207], v[34:35], v[30:31] op_sel_hi:[0,1,1]
	ds_read2_b32 v[30:31], v2 offset1:1
	v_mov_b32_e32 v2, 0x3ea4
	ds_read2_b32 v[32:33], v2 offset1:1
	v_mov_b32_e32 v2, 0x3eb4
	s_waitcnt lgkmcnt(1)
	v_pk_fma_f32 v[34:35], v[204:205], v[30:31], v[150:151] op_sel_hi:[0,1,1]
	ds_read2_b32 v[30:31], v2 offset1:1
	v_mov_b32_e32 v2, 0x3ebc
	ds_read2_b32 v[36:37], v2 offset1:1
	v_mov_b32_e32 v2, 0x3ec4
	ds_read2_b32 v[42:43], v2 offset1:1
	v_mov_b32_e32 v2, 0x3ecc
	s_waitcnt lgkmcnt(2)
	v_pk_fma_f32 v[38:39], v[204:205], v[30:31], v[154:155] op_sel_hi:[0,1,1]
	ds_read2_b32 v[30:31], v2 offset1:1
	v_mov_b32_e32 v2, 0x3edc
	s_waitcnt lgkmcnt(1)
	v_pk_fma_f32 v[44:45], v[204:205], v[42:43], v[172:173] op_sel_hi:[0,1,1]
	ds_read2_b32 v[42:43], v2 offset1:1
	v_mov_b32_e32 v2, 0x3ed4
	ds_read2_b32 v[106:107], v2 offset1:1
	s_waitcnt lgkmcnt(2)
	v_pk_fma_f32 v[30:31], v[204:205], v[30:31], v[174:175] op_sel_hi:[0,1,1]
	v_pk_fma_f32 v[32:33], v[204:205], v[32:33], v[148:149] op_sel_hi:[0,1,1]
	v_pk_fma_f32 v[36:37], v[204:205], v[36:37], v[152:153] op_sel_hi:[0,1,1]
	s_waitcnt lgkmcnt(1)
	v_pk_fma_f32 v[42:43], v[204:205], v[42:43], v[0:1] op_sel_hi:[0,1,1]
	s_waitcnt lgkmcnt(0)
	v_pk_fma_f32 v[40:41], v[204:205], v[106:107], v[40:41] op_sel_hi:[0,1,1]
	ds_read2_b32 v[106:107], v105 offset1:1
	v_mov_b32_e32 v105, 0x3f04
	ds_read2_b32 v[108:109], v105 offset1:1
	v_mov_b32_e32 v105, 0x3f1c
	v_mov_b32_e32 v0, 0x3efc
	s_waitcnt lgkmcnt(1)
	v_pk_fma_f32 v[190:191], v[208:209], v[106:107], v[156:157] op_sel_hi:[0,1,1]
	ds_read2_b32 v[106:107], v105 offset1:1
	v_mov_b32_e32 v105, 0x3f14
	s_waitcnt lgkmcnt(1)
	v_pk_fma_f32 v[192:193], v[208:209], v[108:109], v[164:165] op_sel_hi:[0,1,1]
	ds_read2_b32 v[108:109], v105 offset1:1
	v_mov_b32_e32 v105, 0x3f2c
	s_waitcnt lgkmcnt(1)
	v_pk_fma_f32 v[186:187], v[208:209], v[106:107], v[158:159] op_sel_hi:[0,1,1]
	ds_read2_b32 v[106:107], v105 offset1:1
	v_mov_b32_e32 v105, 0x3f24
	s_waitcnt lgkmcnt(1)
	v_pk_fma_f32 v[188:189], v[208:209], v[108:109], v[166:167] op_sel_hi:[0,1,1]
	ds_read2_b32 v[108:109], v105 offset1:1
	v_mov_b32_e32 v105, 0x3f3c
	s_waitcnt lgkmcnt(1)
	v_pk_fma_f32 v[182:183], v[208:209], v[106:107], v[160:161] op_sel_hi:[0,1,1]
	ds_read2_b32 v[106:107], v105 offset1:1
	v_mov_b32_e32 v105, 0x3f34
	s_waitcnt lgkmcnt(1)
	v_pk_fma_f32 v[184:185], v[208:209], v[108:109], v[168:169] op_sel_hi:[0,1,1]
	ds_read2_b32 v[108:109], v105 offset1:1
	v_mov_b32_e32 v105, 0x3f4c
	s_waitcnt lgkmcnt(1)
	v_pk_fma_f32 v[178:179], v[208:209], v[106:107], v[162:163] op_sel_hi:[0,1,1]
	ds_read2_b32 v[106:107], v105 offset1:1
	v_mov_b32_e32 v105, 0x3f44
	s_waitcnt lgkmcnt(1)
	v_pk_fma_f32 v[180:181], v[208:209], v[108:109], v[170:171] op_sel_hi:[0,1,1]
	ds_read2_b32 v[108:109], v105 offset1:1
	v_mov_b32_e32 v105, 0x3f54
	s_waitcnt lgkmcnt(1)
	v_pk_fma_f32 v[168:169], v[208:209], v[106:107], v[46:47] op_sel_hi:[0,1,1]
	v_mov_b32_e32 v46, 0x3f5c
	ds_read2_b32 v[46:47], v46 offset1:1
	ds_read2_b32 v[106:107], v105 offset1:1
	v_mov_b32_e32 v105, 0x38ec
	s_waitcnt lgkmcnt(2)
	v_pk_fma_f32 v[170:171], v[208:209], v[108:109], v[176:177] op_sel_hi:[0,1,1]
	ds_read2_b32 v[0:1], v0 offset1:1
	s_waitcnt lgkmcnt(2)
	v_pk_fma_f32 v[166:167], v[208:209], v[46:47], v[222:223] op_sel_hi:[0,1,1]
	v_mov_b32_e32 v46, 0x38e4
	s_waitcnt lgkmcnt(1)
	v_pk_fma_f32 v[176:177], v[208:209], v[106:107], v[224:225] op_sel_hi:[0,1,1]
	ds_read2_b32 v[46:47], v46 offset1:1
	ds_read2_b32 v[106:107], v105 offset1:1
	v_mov_b32_e32 v105, 0x39e4
	ds_read2_b32 v[108:109], v105 offset1:1
	v_mov_b32_e32 v105, 0x39ec
	s_waitcnt lgkmcnt(2)
	v_pk_fma_f32 v[46:47], v[218:219], v[46:47], v[144:145] op_sel_hi:[0,1,1]
	ds_read2_b32 v[110:111], v105 offset1:1
	v_mov_b32_e32 v105, 0x3ae4
	s_waitcnt lgkmcnt(1)
	v_pk_fma_f32 v[46:47], v[216:217], v[108:109], v[46:47] op_sel_hi:[0,1,1]
	ds_read2_b32 v[108:109], v105 offset1:1
	v_pk_fma_f32 v[106:107], v[218:219], v[106:107], v[146:147] op_sel_hi:[0,1,1]
	v_mov_b32_e32 v105, 0x3aec
	s_waitcnt lgkmcnt(1)
	v_pk_fma_f32 v[106:107], v[216:217], v[110:111], v[106:107] op_sel_hi:[0,1,1]
	ds_read2_b32 v[110:111], v105 offset1:1
	v_mov_b32_e32 v105, 0x3be4
	s_waitcnt lgkmcnt(1)
	v_pk_fma_f32 v[46:47], v[214:215], v[108:109], v[46:47] op_sel_hi:[0,1,1]
	ds_read2_b32 v[108:109], v105 offset1:1
	v_mov_b32_e32 v105, 0x3bec
	s_waitcnt lgkmcnt(1)
	v_pk_fma_f32 v[106:107], v[214:215], v[110:111], v[106:107] op_sel_hi:[0,1,1]
	ds_read2_b32 v[110:111], v105 offset1:1
	v_mov_b32_e32 v105, 0x3ce4
	s_waitcnt lgkmcnt(1)
	v_pk_fma_f32 v[46:47], v[212:213], v[108:109], v[46:47] op_sel_hi:[0,1,1]
	ds_read2_b32 v[108:109], v105 offset1:1
	v_mov_b32_e32 v105, 0x3cec
	s_waitcnt lgkmcnt(1)
	v_pk_fma_f32 v[106:107], v[212:213], v[110:111], v[106:107] op_sel_hi:[0,1,1]
	ds_read2_b32 v[110:111], v105 offset1:1
	v_mov_b32_e32 v105, 0x3de4
	s_waitcnt lgkmcnt(1)
	v_pk_fma_f32 v[46:47], v[210:211], v[108:109], v[46:47] op_sel_hi:[0,1,1]
	ds_read2_b32 v[108:109], v105 offset1:1
	v_mov_b32_e32 v105, 0x3dec
	s_waitcnt lgkmcnt(1)
	v_pk_fma_f32 v[106:107], v[210:211], v[110:111], v[106:107] op_sel_hi:[0,1,1]
	ds_read2_b32 v[110:111], v105 offset1:1
	v_mov_b32_e32 v105, 0x3ee4
	s_waitcnt lgkmcnt(1)
	v_pk_fma_f32 v[46:47], v[206:207], v[108:109], v[46:47] op_sel_hi:[0,1,1]
	ds_read2_b32 v[108:109], v105 offset1:1
	v_mov_b32_e32 v105, 0x3eec
	s_waitcnt lgkmcnt(1)
	v_pk_fma_f32 v[106:107], v[206:207], v[110:111], v[106:107] op_sel_hi:[0,1,1]
	ds_read2_b32 v[110:111], v105 offset1:1
	v_mov_b32_e32 v105, 0x3f6c
	s_waitcnt lgkmcnt(1)
	v_pk_fma_f32 v[46:47], v[204:205], v[108:109], v[46:47] op_sel_hi:[0,1,1]
	ds_read2_b32 v[108:109], v105 offset1:1
	v_mov_b32_e32 v105, 0x3f64
	s_waitcnt lgkmcnt(1)
	v_pk_fma_f32 v[106:107], v[204:205], v[110:111], v[106:107] op_sel_hi:[0,1,1]
	ds_read2_b32 v[110:111], v105 offset1:1
	v_mov_b32_e32 v2, v0
	s_waitcnt lgkmcnt(1)
	v_pk_fma_f32 v[200:201], v[208:209], v[108:109], v[8:9] op_sel_hi:[0,1,1]
	v_mov_b32_e32 v8, 0x3f7c
	ds_read2_b32 v[8:9], v8 offset1:1
	s_waitcnt lgkmcnt(1)
	v_pk_fma_f32 v[202:203], v[208:209], v[110:111], v[24:25] op_sel_hi:[0,1,1]
	v_mov_b32_e32 v24, 0x3f74
	ds_read_b32 v0, v102 offset:16380
	ds_read2_b32 v[24:25], v24 offset1:1
	s_waitcnt lgkmcnt(2)
	v_pk_fma_f32 v[196:197], v[208:209], v[8:9], v[10:11] op_sel_hi:[0,1,1]
	v_mov_b32_e32 v8, 0x3f84
	ds_read2_b32 v[8:9], v8 offset1:1
	v_mov_b32_e32 v10, 0x3f8c
	ds_read2_b32 v[10:11], v10 offset1:1
	v_pk_fma_f32 v[2:3], v[204:205], v[2:3], v[226:227] op_sel_hi:[0,1,1]
	s_waitcnt lgkmcnt(2)
	v_pk_fma_f32 v[198:199], v[208:209], v[24:25], v[26:27] op_sel_hi:[0,1,1]
	s_waitcnt lgkmcnt(1)
	v_pk_fma_f32 v[194:195], v[208:209], v[8:9], v[22:23] op_sel_hi:[0,1,1]
	v_mov_b32_e32 v8, 0x3f9c
	s_waitcnt lgkmcnt(0)
	v_pk_fma_f32 v[164:165], v[208:209], v[10:11], v[20:21] op_sel_hi:[0,1,1]
	ds_read2_b32 v[8:9], v8 offset1:1
	v_mov_b32_e32 v10, 0x3f94
	ds_read2_b32 v[10:11], v10 offset1:1
	s_waitcnt lgkmcnt(1)
	v_pk_fma_f32 v[172:173], v[208:209], v[8:9], v[18:19] op_sel_hi:[0,1,1]
	v_mov_b32_e32 v8, 0x3fac
	s_waitcnt lgkmcnt(0)
	v_pk_fma_f32 v[174:175], v[208:209], v[10:11], v[28:29] op_sel_hi:[0,1,1]
	ds_read2_b32 v[8:9], v8 offset1:1
	v_mov_b32_e32 v10, 0x3fa4
	ds_read2_b32 v[10:11], v10 offset1:1
	s_waitcnt lgkmcnt(1)
	v_pk_fma_f32 v[162:163], v[208:209], v[8:9], v[34:35] op_sel_hi:[0,1,1]
	v_mov_b32_e32 v8, 0x3fb4
	s_waitcnt lgkmcnt(0)
	v_pk_fma_f32 v[160:161], v[208:209], v[10:11], v[32:33] op_sel_hi:[0,1,1]
	ds_read2_b32 v[8:9], v8 offset1:1
	v_mov_b32_e32 v10, 0x3fbc
	ds_read2_b32 v[10:11], v10 offset1:1
	s_waitcnt lgkmcnt(1)
	v_pk_fma_f32 v[158:159], v[208:209], v[8:9], v[38:39] op_sel_hi:[0,1,1]
	v_mov_b32_e32 v8, 0x3fcc
	s_waitcnt lgkmcnt(0)
	v_pk_fma_f32 v[152:153], v[208:209], v[10:11], v[36:37] op_sel_hi:[0,1,1]
	ds_read2_b32 v[8:9], v8 offset1:1
	v_mov_b32_e32 v10, 0x3fc4
	ds_read2_b32 v[10:11], v10 offset1:1
	s_waitcnt lgkmcnt(1)
	v_pk_fma_f32 v[154:155], v[208:209], v[8:9], v[30:31] op_sel_hi:[0,1,1]
	v_mov_b32_e32 v8, 0x3fdc
	s_waitcnt lgkmcnt(0)
	v_pk_fma_f32 v[156:157], v[208:209], v[10:11], v[44:45] op_sel_hi:[0,1,1]
	ds_read2_b32 v[8:9], v8 offset1:1
	v_mov_b32_e32 v10, 0x3fd4
	ds_read2_b32 v[10:11], v10 offset1:1
	s_waitcnt lgkmcnt(1)
	v_pk_fma_f32 v[150:151], v[208:209], v[8:9], v[42:43] op_sel_hi:[0,1,1]
	v_mov_b32_e32 v8, 0x3fe4
	s_waitcnt lgkmcnt(0)
	v_pk_fma_f32 v[148:149], v[208:209], v[10:11], v[40:41] op_sel_hi:[0,1,1]
	ds_read2_b32 v[8:9], v8 offset1:1
	v_mov_b32_e32 v10, 0x3fec
	ds_read2_b32 v[10:11], v10 offset1:1
	s_waitcnt lgkmcnt(1)
	v_pk_fma_f32 v[146:147], v[208:209], v[8:9], v[46:47] op_sel_hi:[0,1,1]
	v_mov_b32_e32 v8, 0x38f4
	s_waitcnt lgkmcnt(0)
	v_pk_fma_f32 v[144:145], v[208:209], v[10:11], v[106:107] op_sel_hi:[0,1,1]
	ds_read2_b32 v[8:9], v8 offset1:1
	v_mov_b32_e32 v10, 0x39f4
	ds_read2_b32 v[10:11], v10 offset1:1
	v_add_f32_e32 v47, v104, v208
	s_waitcnt lgkmcnt(1)
	v_pk_fma_f32 v[8:9], v[218:219], v[8:9], v[220:221] op_sel_hi:[0,1,1]
	s_waitcnt lgkmcnt(0)
	v_pk_fma_f32 v[8:9], v[216:217], v[10:11], v[8:9] op_sel_hi:[0,1,1]
	v_mov_b32_e32 v10, 0x3af4
	ds_read2_b32 v[10:11], v10 offset1:1
	s_waitcnt lgkmcnt(0)
	v_pk_fma_f32 v[8:9], v[214:215], v[10:11], v[8:9] op_sel_hi:[0,1,1]
	v_mov_b32_e32 v10, 0x3bf4
	ds_read2_b32 v[10:11], v10 offset1:1
	s_waitcnt lgkmcnt(0)
	v_pk_fma_f32 v[8:9], v[212:213], v[10:11], v[8:9] op_sel_hi:[0,1,1]
	v_mov_b32_e32 v10, 0x3cf4
	ds_read2_b32 v[10:11], v10 offset1:1
	s_waitcnt lgkmcnt(0)
	v_pk_fma_f32 v[8:9], v[210:211], v[10:11], v[8:9] op_sel_hi:[0,1,1]
	v_mov_b32_e32 v10, 0x3df4
	ds_read2_b32 v[10:11], v10 offset1:1
	s_waitcnt lgkmcnt(0)
	v_pk_fma_f32 v[8:9], v[206:207], v[10:11], v[8:9] op_sel_hi:[0,1,1]
	v_mov_b32_e32 v10, 0x3ef4
	ds_read2_b32 v[10:11], v10 offset1:1
	s_waitcnt lgkmcnt(0)
	v_pk_fma_f32 v[8:9], v[204:205], v[10:11], v[8:9] op_sel_hi:[0,1,1]
	v_mov_b32_e32 v10, 0x3ff4
	ds_read2_b32 v[10:11], v10 offset1:1
	v_pk_fma_f32 v[204:205], v[208:209], v[0:1], v[2:3] op_sel_hi:[0,1,1]
	s_waitcnt lgkmcnt(0)
	v_pk_fma_f32 v[206:207], v[208:209], v[10:11], v[8:9] op_sel_hi:[0,1,1]
	v_mov_b32_e32 v8, v124
	s_cbranch_scc0 .LBB1_1
	v_mul_f32_e32 v0, 0x42800000, v47
	s_mov_b32 s2, 0x43800000
	v_div_scale_f32 v1, s[0:1], v0, v0, s2
	v_rcp_f32_e32 v2, v1
	s_ashr_i32 s0, s20, 3
	s_ashr_i32 s1, s0, 31
	s_lshl_b64 s[0:1], s[0:1], 19
	v_fma_f32 v3, -v1, v2, 1.0
	v_fmac_f32_e32 v2, v3, v2
	v_div_scale_f32 v3, vcc, s2, v0, s2
	v_mul_f32_e32 v4, v3, v2
	v_fma_f32 v5, -v1, v4, v3
	v_fmac_f32_e32 v4, v5, v2
	v_fma_f32 v1, -v1, v4, v3
	v_div_fmas_f32 v1, v1, v2, v4
	v_div_fixup_f32 v0, v1, v0, s2
	v_accvgpr_read_b32 v3, a1
	v_fma_mixlo_f16 v1, v0, v205, 0
	v_accvgpr_read_b32 v2, a0
	v_pk_mul_f32 v[6:7], v[0:1], v[190:191] op_sel_hi:[0,1]
	v_pk_mul_f32 v[8:9], v[0:1], v[192:193] op_sel_hi:[0,1]
	v_lshlrev_b64 v[2:3], 9, v[2:3]
	v_cvt_pk_f16_f32 v9, v8, v9
	v_cvt_pk_f16_f32 v10, v6, v7
	v_lshl_add_u64 v[2:3], v[2:3], 0, s[0:1]
	s_lshl_b32 s0, s20, 6
	v_fma_mixlo_f16 v12, v0, v205, -v1 op_sel_hi:[0,0,1]
	v_pack_b32_f16 v6, v1, v9
	v_lshrrev_b32_e32 v1, 16, v10
	s_and_b32 s0, s0, 0x1c0
	v_alignbit_b32 v7, v10, v9, 16
	v_cvt_f32_f16_e64 v8, -v9
	v_cvt_f32_f16_sdwa v9, -v9 dst_sel:DWORD dst_unused:UNUSED_PAD src0_sel:WORD_1
	v_cvt_f32_f16_e64 v10, -v10
	v_cvt_f32_f16_e64 v11, -v1
	v_or_b32_e32 v2, s0, v2
	v_lshlrev_b64 v[2:3], 1, v[2:3]
	v_lshl_add_u64 v[4:5], s[8:9], 0, v[2:3]
	global_store_short v[4:5], v1, off offset:8
	global_store_dwordx2 v[4:5], v[6:7], off
	v_pk_fma_f32 v[6:7], v[0:1], v[192:193], v[8:9] op_sel_hi:[0,1,1]
	v_pk_fma_f32 v[8:9], v[0:1], v[190:191], v[10:11] op_sel_hi:[0,1,1]
	v_cvt_pk_f16_f32 v1, v8, v9
	v_cvt_pk_f16_f32 v6, v6, v7
	v_alignbit_b32 v9, v1, v6, 16
	v_pack_b32_f16 v8, v12, v6
	v_pk_mul_f32 v[10:11], v[0:1], v[186:187] op_sel_hi:[0,1]
	v_pk_mul_f32 v[6:7], v[0:1], v[188:189] op_sel_hi:[0,1]
	v_cvt_pk_f16_f32 v6, v6, v7
	v_cvt_pk_f16_f32 v7, v10, v11
	v_cvt_f32_f16_e64 v12, -v7
	v_cvt_f32_f16_sdwa v13, -v7 dst_sel:DWORD dst_unused:UNUSED_PAD src0_sel:WORD_1
	v_cvt_f32_f16_e64 v10, -v6
	v_cvt_f32_f16_sdwa v11, -v6 dst_sel:DWORD dst_unused:UNUSED_PAD src0_sel:WORD_1
	v_lshl_add_u64 v[2:3], s[10:11], 0, v[2:3]
	global_store_short_d16_hi v[2:3], v1, off offset:8
	global_store_dwordx2 v[2:3], v[8:9], off
	v_pk_fma_f32 v[8:9], v[0:1], v[186:187], v[12:13] op_sel_hi:[0,1,1]
	v_pk_fma_f32 v[14:15], v[0:1], v[188:189], v[10:11] op_sel_hi:[0,1,1]
	v_cvt_pk_f16_f32 v11, v8, v9
	v_pk_mul_f32 v[8:9], v[0:1], v[182:183] op_sel_hi:[0,1]
	v_pk_mul_f32 v[12:13], v[0:1], v[184:185] op_sel_hi:[0,1]
	v_cvt_pk_f16_f32 v9, v8, v9
	v_cvt_pk_f16_f32 v8, v12, v13
	v_cvt_f32_f16_e64 v16, -v9
	v_cvt_f32_f16_sdwa v17, -v9 dst_sel:DWORD dst_unused:UNUSED_PAD src0_sel:WORD_1
	v_cvt_f32_f16_e64 v12, -v8
	v_cvt_f32_f16_sdwa v13, -v8 dst_sel:DWORD dst_unused:UNUSED_PAD src0_sel:WORD_1
	global_store_dwordx4 v[4:5], v[6:9], off offset:10 sc1
	v_cvt_pk_f16_f32 v10, v14, v15
	v_pk_mul_f32 v[14:15], v[0:1], v[178:179] op_sel_hi:[0,1]
	v_pk_fma_f32 v[6:7], v[0:1], v[182:183], v[16:17] op_sel_hi:[0,1,1]
	v_pk_fma_f32 v[8:9], v[0:1], v[184:185], v[12:13] op_sel_hi:[0,1,1]
	v_cvt_pk_f16_f32 v13, v6, v7
	v_pk_mul_f32 v[6:7], v[0:1], v[180:181] op_sel_hi:[0,1]
	v_cvt_pk_f16_f32 v6, v6, v7
	v_cvt_pk_f16_f32 v7, v14, v15
	v_cvt_f32_f16_e64 v16, -v7
	v_cvt_f32_f16_sdwa v17, -v7 dst_sel:DWORD dst_unused:UNUSED_PAD src0_sel:WORD_1
	v_cvt_f32_f16_e64 v14, -v6
	v_cvt_f32_f16_sdwa v15, -v6 dst_sel:DWORD dst_unused:UNUSED_PAD src0_sel:WORD_1
	v_cvt_pk_f16_f32 v12, v8, v9
	v_pk_fma_f32 v[8:9], v[0:1], v[178:179], v[16:17] op_sel_hi:[0,1,1]
	global_store_dwordx4 v[2:3], v[10:13], off offset:10 sc1
	s_nop 1
	v_cvt_pk_f16_f32 v11, v8, v9
	v_pk_mul_f32 v[8:9], v[0:1], v[168:169] op_sel_hi:[0,1]
	v_pk_fma_f32 v[12:13], v[0:1], v[180:181], v[14:15] op_sel_hi:[0,1,1]
	v_pk_mul_f32 v[14:15], v[0:1], v[170:171] op_sel_hi:[0,1]
	v_cvt_pk_f16_f32 v9, v8, v9
	v_cvt_pk_f16_f32 v8, v14, v15
	v_cvt_f32_f16_e64 v16, -v9
	v_cvt_f32_f16_sdwa v17, -v9 dst_sel:DWORD dst_unused:UNUSED_PAD src0_sel:WORD_1
	v_cvt_f32_f16_e64 v14, -v8
	v_cvt_f32_f16_sdwa v15, -v8 dst_sel:DWORD dst_unused:UNUSED_PAD src0_sel:WORD_1
	global_store_dwordx4 v[4:5], v[6:9], off offset:26 sc1
	v_cvt_pk_f16_f32 v10, v12, v13
	s_nop 0
	v_pk_fma_f32 v[6:7], v[0:1], v[168:169], v[16:17] op_sel_hi:[0,1,1]
	v_pk_fma_f32 v[8:9], v[0:1], v[170:171], v[14:15] op_sel_hi:[0,1,1]
	v_cvt_pk_f16_f32 v13, v6, v7
	v_pk_mul_f32 v[14:15], v[0:1], v[166:167] op_sel_hi:[0,1]
	v_pk_mul_f32 v[6:7], v[0:1], v[176:177] op_sel_hi:[0,1]
	v_cvt_pk_f16_f32 v6, v6, v7
	v_cvt_pk_f16_f32 v7, v14, v15
	v_cvt_f32_f16_e64 v16, -v7
	v_cvt_f32_f16_sdwa v17, -v7 dst_sel:DWORD dst_unused:UNUSED_PAD src0_sel:WORD_1
	v_cvt_f32_f16_e64 v14, -v6
	v_cvt_f32_f16_sdwa v15, -v6 dst_sel:DWORD dst_unused:UNUSED_PAD src0_sel:WORD_1
	v_cvt_pk_f16_f32 v12, v8, v9
	v_pk_fma_f32 v[8:9], v[0:1], v[166:167], v[16:17] op_sel_hi:[0,1,1]
	global_store_dwordx4 v[2:3], v[10:13], off offset:26 sc1
	s_nop 1
	v_cvt_pk_f16_f32 v11, v8, v9
	v_pk_mul_f32 v[8:9], v[0:1], v[200:201] op_sel_hi:[0,1]
	v_pk_fma_f32 v[12:13], v[0:1], v[176:177], v[14:15] op_sel_hi:[0,1,1]
	v_pk_mul_f32 v[14:15], v[0:1], v[202:203] op_sel_hi:[0,1]
	v_cvt_pk_f16_f32 v9, v8, v9
	v_cvt_pk_f16_f32 v8, v14, v15
	v_cvt_f32_f16_e64 v16, -v9
	v_cvt_f32_f16_sdwa v17, -v9 dst_sel:DWORD dst_unused:UNUSED_PAD src0_sel:WORD_1
	v_cvt_f32_f16_e64 v14, -v8
	v_cvt_f32_f16_sdwa v15, -v8 dst_sel:DWORD dst_unused:UNUSED_PAD src0_sel:WORD_1
	global_store_dwordx4 v[4:5], v[6:9], off offset:42 sc1
	v_cvt_pk_f16_f32 v10, v12, v13
	s_nop 0
	v_pk_fma_f32 v[6:7], v[0:1], v[200:201], v[16:17] op_sel_hi:[0,1,1]
	v_pk_fma_f32 v[8:9], v[0:1], v[202:203], v[14:15] op_sel_hi:[0,1,1]
	v_cvt_pk_f16_f32 v13, v6, v7
	v_pk_mul_f32 v[14:15], v[0:1], v[196:197] op_sel_hi:[0,1]
	v_pk_mul_f32 v[6:7], v[0:1], v[198:199] op_sel_hi:[0,1]
	v_cvt_pk_f16_f32 v6, v6, v7
	v_cvt_pk_f16_f32 v7, v14, v15
	v_cvt_f32_f16_e64 v16, -v7
	v_cvt_f32_f16_sdwa v17, -v7 dst_sel:DWORD dst_unused:UNUSED_PAD src0_sel:WORD_1
	v_cvt_f32_f16_e64 v14, -v6
	v_cvt_f32_f16_sdwa v15, -v6 dst_sel:DWORD dst_unused:UNUSED_PAD src0_sel:WORD_1
	v_cvt_pk_f16_f32 v12, v8, v9
	v_pk_fma_f32 v[8:9], v[0:1], v[196:197], v[16:17] op_sel_hi:[0,1,1]
	global_store_dwordx4 v[2:3], v[10:13], off offset:42 sc1
	s_nop 1
	v_cvt_pk_f16_f32 v11, v8, v9
	v_pk_mul_f32 v[8:9], v[0:1], v[164:165] op_sel_hi:[0,1]
	v_pk_fma_f32 v[12:13], v[0:1], v[198:199], v[14:15] op_sel_hi:[0,1,1]
	v_pk_mul_f32 v[14:15], v[0:1], v[194:195] op_sel_hi:[0,1]
	v_cvt_pk_f16_f32 v9, v8, v9
	v_cvt_pk_f16_f32 v8, v14, v15
	v_cvt_f32_f16_e64 v16, -v9
	v_cvt_f32_f16_sdwa v17, -v9 dst_sel:DWORD dst_unused:UNUSED_PAD src0_sel:WORD_1
	v_cvt_f32_f16_e64 v14, -v8
	v_cvt_f32_f16_sdwa v15, -v8 dst_sel:DWORD dst_unused:UNUSED_PAD src0_sel:WORD_1
	global_store_dwordx4 v[4:5], v[6:9], off offset:58 sc1
	v_cvt_pk_f16_f32 v10, v12, v13
	s_nop 0
	v_pk_fma_f32 v[6:7], v[0:1], v[164:165], v[16:17] op_sel_hi:[0,1,1]
	v_pk_fma_f32 v[8:9], v[0:1], v[194:195], v[14:15] op_sel_hi:[0,1,1]
	v_cvt_pk_f16_f32 v13, v6, v7
	v_pk_mul_f32 v[14:15], v[0:1], v[172:173] op_sel_hi:[0,1]
	v_pk_mul_f32 v[6:7], v[0:1], v[174:175] op_sel_hi:[0,1]
	v_cvt_pk_f16_f32 v6, v6, v7
	v_cvt_pk_f16_f32 v7, v14, v15
	v_cvt_f32_f16_e64 v16, -v7
	v_cvt_f32_f16_sdwa v17, -v7 dst_sel:DWORD dst_unused:UNUSED_PAD src0_sel:WORD_1
	v_cvt_f32_f16_e64 v14, -v6
	v_cvt_f32_f16_sdwa v15, -v6 dst_sel:DWORD dst_unused:UNUSED_PAD src0_sel:WORD_1
	v_cvt_pk_f16_f32 v12, v8, v9
	v_pk_fma_f32 v[8:9], v[0:1], v[172:173], v[16:17] op_sel_hi:[0,1,1]
	global_store_dwordx4 v[2:3], v[10:13], off offset:58 sc1
	s_nop 1
	v_cvt_pk_f16_f32 v11, v8, v9
	v_pk_mul_f32 v[8:9], v[0:1], v[162:163] op_sel_hi:[0,1]
	v_pk_fma_f32 v[12:13], v[0:1], v[174:175], v[14:15] op_sel_hi:[0,1,1]
	v_pk_mul_f32 v[14:15], v[0:1], v[160:161] op_sel_hi:[0,1]
	v_cvt_pk_f16_f32 v9, v8, v9
	v_cvt_pk_f16_f32 v8, v14, v15
	v_cvt_f32_f16_e64 v16, -v9
	v_cvt_f32_f16_sdwa v17, -v9 dst_sel:DWORD dst_unused:UNUSED_PAD src0_sel:WORD_1
	v_cvt_f32_f16_e64 v14, -v8
	v_cvt_f32_f16_sdwa v15, -v8 dst_sel:DWORD dst_unused:UNUSED_PAD src0_sel:WORD_1
	global_store_dwordx4 v[4:5], v[6:9], off offset:74 sc1
	v_cvt_pk_f16_f32 v10, v12, v13
	s_nop 0
	v_pk_fma_f32 v[6:7], v[0:1], v[162:163], v[16:17] op_sel_hi:[0,1,1]
	v_pk_fma_f32 v[8:9], v[0:1], v[160:161], v[14:15] op_sel_hi:[0,1,1]
	v_cvt_pk_f16_f32 v13, v6, v7
	v_pk_mul_f32 v[14:15], v[0:1], v[152:153] op_sel_hi:[0,1]
	v_pk_mul_f32 v[6:7], v[0:1], v[158:159] op_sel_hi:[0,1]
	v_cvt_pk_f16_f32 v6, v6, v7
	v_cvt_pk_f16_f32 v7, v14, v15
	v_cvt_f32_f16_e64 v16, -v7
	v_cvt_f32_f16_sdwa v17, -v7 dst_sel:DWORD dst_unused:UNUSED_PAD src0_sel:WORD_1
	v_cvt_f32_f16_e64 v14, -v6
	v_cvt_f32_f16_sdwa v15, -v6 dst_sel:DWORD dst_unused:UNUSED_PAD src0_sel:WORD_1
	v_cvt_pk_f16_f32 v12, v8, v9
	v_pk_fma_f32 v[8:9], v[0:1], v[152:153], v[16:17] op_sel_hi:[0,1,1]
	global_store_dwordx4 v[2:3], v[10:13], off offset:74 sc1
	s_nop 1
	v_cvt_pk_f16_f32 v11, v8, v9
	v_pk_mul_f32 v[8:9], v[0:1], v[154:155] op_sel_hi:[0,1]
	v_pk_fma_f32 v[12:13], v[0:1], v[158:159], v[14:15] op_sel_hi:[0,1,1]
	v_pk_mul_f32 v[14:15], v[0:1], v[156:157] op_sel_hi:[0,1]
	v_cvt_pk_f16_f32 v9, v8, v9
	v_cvt_pk_f16_f32 v8, v14, v15
	v_cvt_f32_f16_e64 v16, -v9
	v_cvt_f32_f16_sdwa v17, -v9 dst_sel:DWORD dst_unused:UNUSED_PAD src0_sel:WORD_1
	v_cvt_f32_f16_e64 v14, -v8
	v_cvt_f32_f16_sdwa v15, -v8 dst_sel:DWORD dst_unused:UNUSED_PAD src0_sel:WORD_1
	global_store_dwordx4 v[4:5], v[6:9], off offset:90 sc1
	v_cvt_pk_f16_f32 v10, v12, v13
	s_nop 0
	v_pk_fma_f32 v[6:7], v[0:1], v[154:155], v[16:17] op_sel_hi:[0,1,1]
	v_pk_fma_f32 v[8:9], v[0:1], v[156:157], v[14:15] op_sel_hi:[0,1,1]
	v_cvt_pk_f16_f32 v13, v6, v7
	v_pk_mul_f32 v[14:15], v[0:1], v[150:151] op_sel_hi:[0,1]
	v_pk_mul_f32 v[6:7], v[0:1], v[148:149] op_sel_hi:[0,1]
	v_cvt_pk_f16_f32 v6, v6, v7
	v_cvt_pk_f16_f32 v7, v14, v15
	v_cvt_f32_f16_e64 v16, -v7
	v_cvt_f32_f16_sdwa v17, -v7 dst_sel:DWORD dst_unused:UNUSED_PAD src0_sel:WORD_1
	v_cvt_f32_f16_e64 v14, -v6
	v_cvt_f32_f16_sdwa v15, -v6 dst_sel:DWORD dst_unused:UNUSED_PAD src0_sel:WORD_1
	v_cvt_pk_f16_f32 v12, v8, v9
	v_pk_fma_f32 v[8:9], v[0:1], v[150:151], v[16:17] op_sel_hi:[0,1,1]
	global_store_dwordx4 v[2:3], v[10:13], off offset:90 sc1
	s_nop 1
	v_pk_fma_f32 v[12:13], v[0:1], v[148:149], v[14:15] op_sel_hi:[0,1,1]
	v_cvt_pk_f16_f32 v11, v8, v9
	v_pk_mul_f32 v[14:15], v[0:1], v[146:147] op_sel_hi:[0,1]
	v_pk_mul_f32 v[8:9], v[0:1], v[144:145] op_sel_hi:[0,1]
	v_cvt_pk_f16_f32 v9, v8, v9
	v_cvt_pk_f16_f32 v8, v14, v15
	v_cvt_f32_f16_e64 v14, -v8
	v_cvt_f32_f16_sdwa v15, -v8 dst_sel:DWORD dst_unused:UNUSED_PAD src0_sel:WORD_1
	v_cvt_f32_f16_e64 v16, -v9
	v_cvt_f32_f16_sdwa v17, -v9 dst_sel:DWORD dst_unused:UNUSED_PAD src0_sel:WORD_1
	v_cvt_pk_f16_f32 v10, v12, v13
	v_pk_mul_f32 v[12:13], v[0:1], v[206:207] op_sel_hi:[0,1]
	global_store_dwordx4 v[4:5], v[6:9], off offset:106 sc1
	s_nop 1
	v_pk_fma_f32 v[6:7], v[0:1], v[146:147], v[14:15] op_sel_hi:[0,1,1]
	v_pk_fma_f32 v[8:9], v[0:1], v[144:145], v[16:17] op_sel_hi:[0,1,1]
	v_cvt_pk_f16_f32 v1, v12, v13
	v_cvt_f32_f16_e32 v14, v1
	v_cvt_f32_f16_sdwa v15, v1 dst_sel:DWORD dst_unused:UNUSED_PAD src0_sel:WORD_1
	v_cvt_pk_f16_f32 v12, v6, v7
	v_cvt_pk_f16_f32 v13, v8, v9
	global_store_dwordx4 v[2:3], v[10:13], off offset:106 sc1
	v_pk_fma_f32 v[6:7], v[0:1], v[206:207], v[14:15] op_sel_hi:[0,1,1] neg_lo:[0,0,1] neg_hi:[0,0,1]
	v_cvt_pk_f16_f32 v6, v6, v7
	v_fma_mixlo_f16 v7, v0, v204, 0
	v_fma_mixlo_f16 v0, v0, v204, -v7 op_sel_hi:[0,0,1]
	global_store_short v[4:5], v7, off offset:126
	global_store_dword v[4:5], v1, off offset:122
	global_store_short v[2:3], v0, off offset:126
	global_store_dword v[2:3], v6, off offset:122
	s_endpgm
	.p2alignl 8, 3212836864

_Z14fused_ln_wprepILb0EEvPKfPfS1_S1_PKiS4_S1_S1_PDF16_S5_S1_S5_S5_S1_S5_S5_:
	s_cmpk_gt_i32 s2, 0xff
	s_mov_b64 s[4:5], -1
	s_cbranch_scc0 .LBB3_10
	s_load_dwordx2 s[4:5], s[0:1], 0x0
	s_lshl_b32 s3, s2, 2
	s_addk_i32 s3, 0xfc00
	v_lshrrev_b32_e32 v1, 6, v0
	v_or_b32_e32 v28, s3, v1
	v_ashrrev_i32_e32 v29, 31, v28
	v_lshlrev_b32_e32 v1, 3, v0
	v_lshlrev_b64 v[2:3], 11, v[28:29]
	v_and_b32_e32 v1, 0x1f8, v1
	s_waitcnt lgkmcnt(0)
	v_lshl_add_u64 v[4:5], s[4:5], 0, v[2:3]
	v_lshlrev_b32_e32 v2, 2, v1
	v_mov_b32_e32 v3, 0
	v_lshl_add_u64 v[12:13], v[4:5], 0, v[2:3]
	global_load_dwordx4 v[4:7], v[12:13], off
	global_load_dwordx4 v[8:11], v[12:13], off offset:16
	v_mbcnt_lo_u32_b32 v12, -1, 0
	v_mbcnt_hi_u32_b32 v12, -1, v12
	v_and_b32_e32 v13, 64, v12
	v_xor_b32_e32 v14, 32, v12
	v_add_u32_e32 v13, 64, v13
	v_cmp_lt_i32_e32 vcc, v14, v13
	v_xor_b32_e32 v16, 16, v12
	s_load_dwordx8 s[4:11], s[0:1], 0x30
	v_cndmask_b32_e32 v14, v12, v14, vcc
	v_lshlrev_b32_e32 v38, 2, v14
	v_cmp_lt_i32_e32 vcc, v16, v13
	s_mov_b32 s3, 0xf800000
	v_lshlrev_b64 v[28:29], 10, v[28:29]
	v_cndmask_b32_e32 v16, v12, v16, vcc
	v_lshlrev_b32_e32 v39, 2, v16
	v_xor_b32_e32 v16, 8, v12
	v_cmp_lt_i32_e32 vcc, v16, v13
	s_mov_b32 s12, 0x43800000
	s_cmpk_lg_i32 s2, 0x100
	v_cndmask_b32_e32 v16, v12, v16, vcc
	v_lshlrev_b32_e32 v40, 2, v16
	v_xor_b32_e32 v16, 4, v12
	v_cmp_lt_i32_e32 vcc, v16, v13
	s_waitcnt vmcnt(1)
	v_add_f32_e32 v14, 0, v4
	v_add_f32_e32 v14, v14, v5
	v_add_f32_e32 v14, v14, v6
	v_add_f32_e32 v14, v14, v7
	s_waitcnt vmcnt(0)
	v_add_f32_e32 v14, v14, v8
	v_add_f32_e32 v14, v14, v9
	v_add_f32_e32 v14, v14, v10
	v_add_f32_e32 v14, v14, v11
	ds_bpermute_b32 v15, v38, v14
	v_cndmask_b32_e32 v16, v12, v16, vcc
	v_lshlrev_b32_e32 v41, 2, v16
	v_xor_b32_e32 v16, 2, v12
	v_cmp_lt_i32_e32 vcc, v16, v13
	s_waitcnt lgkmcnt(0)
	v_add_f32_e32 v14, v14, v15
	ds_bpermute_b32 v15, v39, v14
	v_cndmask_b32_e32 v16, v12, v16, vcc
	v_lshlrev_b32_e32 v42, 2, v16
	v_xor_b32_e32 v16, 1, v12
	v_cmp_lt_i32_e32 vcc, v16, v13
	s_waitcnt lgkmcnt(0)
	v_add_f32_e32 v14, v14, v15
	ds_bpermute_b32 v15, v40, v14
	v_cndmask_b32_e32 v12, v12, v16, vcc
	v_lshlrev_b32_e32 v43, 2, v12
	s_waitcnt lgkmcnt(0)
	v_add_f32_e32 v14, v14, v15
	ds_bpermute_b32 v15, v41, v14
	s_waitcnt lgkmcnt(0)
	v_add_f32_e32 v14, v14, v15
	ds_bpermute_b32 v15, v42, v14
	s_waitcnt lgkmcnt(0)
	v_add_f32_e32 v30, v14, v15
	ds_bpermute_b32 v31, v43, v30
	global_load_dwordx4 v[12:15], v2, s[4:5] offset:16
	global_load_dwordx4 v[16:19], v2, s[6:7] offset:16
	global_load_dwordx4 v[20:23], v2, s[4:5]
	global_load_dwordx4 v[24:27], v2, s[6:7]
	s_mov_b32 s6, 0
	s_mov_b32 s7, 1
	s_waitcnt lgkmcnt(0)
	v_add_f32_e32 v2, v30, v31
	v_mul_f32_e32 v2, 0x3b000000, v2
	v_pk_add_f32 v[4:5], v[4:5], v[2:3] op_sel_hi:[1,0] neg_lo:[0,1] neg_hi:[0,1]
	v_pk_add_f32 v[6:7], v[6:7], v[2:3] op_sel_hi:[1,0] neg_lo:[0,1] neg_hi:[0,1]
	v_pk_mul_f32 v[30:31], v[4:5], v[4:5]
	v_pk_add_f32 v[8:9], v[8:9], v[2:3] op_sel_hi:[1,0] neg_lo:[0,1] neg_hi:[0,1]
	v_pk_add_f32 v[10:11], v[10:11], v[2:3] op_sel_hi:[1,0] neg_lo:[0,1] neg_hi:[0,1]
	v_pk_mul_f32 v[32:33], v[6:7], v[6:7]
	v_add_f32_e32 v2, v30, v31
	v_add_f32_e32 v2, v32, v2
	v_pk_mul_f32 v[34:35], v[8:9], v[8:9]
	v_add_f32_e32 v2, v33, v2
	v_add_f32_e32 v2, v34, v2
	v_pk_mul_f32 v[36:37], v[10:11], v[10:11]
	v_add_f32_e32 v2, v35, v2
	v_add_f32_e32 v2, v36, v2
	v_add_f32_e32 v2, v37, v2
	ds_bpermute_b32 v30, v38, v2
	v_mov_b32_e32 v32, 0x3727c5ac
	v_mov_b32_e32 v34, 0x260
	s_waitcnt lgkmcnt(0)
	v_add_f32_e32 v2, v2, v30
	ds_bpermute_b32 v30, v39, v2
	s_waitcnt lgkmcnt(0)
	v_add_f32_e32 v2, v2, v30
	ds_bpermute_b32 v30, v40, v2
	s_waitcnt lgkmcnt(0)
	v_add_f32_e32 v2, v2, v30
	ds_bpermute_b32 v30, v41, v2
	s_waitcnt lgkmcnt(0)
	v_add_f32_e32 v2, v2, v30
	ds_bpermute_b32 v30, v42, v2
	s_waitcnt lgkmcnt(0)
	v_add_f32_e32 v2, v2, v30
	ds_bpermute_b32 v33, v43, v2
	v_lshl_add_u64 v[30:31], s[8:9], 0, v[28:29]
	v_lshl_add_u64 v[28:29], s[10:11], 0, v[28:29]
	s_waitcnt lgkmcnt(0)
	v_add_f32_e32 v2, v2, v33
	v_fmac_f32_e32 v32, 0x3b000000, v2
	v_mul_f32_e32 v2, 0x4f800000, v32
	v_cmp_gt_f32_e32 vcc, s3, v32
	s_nop 1
	v_cndmask_b32_e32 v32, v32, v2, vcc
	v_sqrt_f32_e32 v33, v32
	v_lshlrev_b32_e32 v2, 1, v1
	v_lshl_add_u64 v[30:31], v[30:31], 0, v[2:3]
	v_lshl_add_u64 v[28:29], v[28:29], 0, v[2:3]
	v_add_u32_e32 v1, -1, v33
	v_add_u32_e32 v35, 1, v33
	v_fma_f32 v36, -v1, v33, v32
	v_fma_f32 v37, -v35, v33, v32
	v_cmp_ge_f32_e64 s[4:5], 0, v36
	s_nop 1
	v_cndmask_b32_e64 v1, v33, v1, s[4:5]
	v_cmp_lt_f32_e64 s[4:5], 0, v37
	s_nop 1
	v_cndmask_b32_e64 v1, v1, v35, s[4:5]
	v_mul_f32_e32 v33, 0x37800000, v1
	v_cndmask_b32_e32 v1, v1, v33, vcc
	v_cmp_class_f32_e32 vcc, v32, v34
	s_nop 1
	v_cndmask_b32_e32 v1, v1, v32, vcc
	v_div_scale_f32 v32, s[4:5], v1, v1, 1.0
	v_rcp_f32_e32 v33, v32
	v_div_scale_f32 v2, vcc, 1.0, v1, 1.0
	v_fma_f32 v34, -v32, v33, 1.0
	v_fmac_f32_e32 v33, v34, v33
	v_mul_f32_e32 v34, v2, v33
	v_fma_f32 v35, -v32, v34, v2
	v_fmac_f32_e32 v34, v35, v33
	v_fma_f32 v2, -v32, v34, v2
	v_div_fmas_f32 v2, v2, v33, v34
	v_div_fixup_f32 v2, v2, v1, 1.0
	v_pk_mul_f32 v[4:5], v[4:5], v[2:3] op_sel_hi:[1,0]
	v_pk_mul_f32 v[6:7], v[6:7], v[2:3] op_sel_hi:[1,0]
	v_pk_mul_f32 v[8:9], v[8:9], v[2:3] op_sel_hi:[1,0]
	v_pk_mul_f32 v[10:11], v[10:11], v[2:3] op_sel_hi:[1,0]
	s_waitcnt vmcnt(0)
	v_pk_fma_f32 v[20:21], v[20:21], v[4:5], v[24:25]
	v_pk_fma_f32 v[22:23], v[22:23], v[6:7], v[26:27]
	v_pk_fma_f32 v[8:9], v[12:13], v[8:9], v[16:17]
	v_pk_fma_f32 v[10:11], v[14:15], v[10:11], v[18:19]
	v_pk_mul_f32 v[4:5], v[20:21], s[12:13] op_sel_hi:[1,0]
	v_pk_mul_f32 v[6:7], v[22:23], s[12:13] op_sel_hi:[1,0]
	v_pk_mul_f32 v[12:13], v[8:9], s[12:13] op_sel_hi:[1,0]
	v_pk_mul_f32 v[14:15], v[10:11], s[12:13] op_sel_hi:[1,0]
	v_cvt_pk_f16_f32 v4, v4, v5
	v_cvt_pk_f16_f32 v5, v6, v7
	v_cvt_pk_f16_f32 v6, v12, v13
	v_cvt_pk_f16_f32 v7, v14, v15
	v_cvt_f32_f16_e32 v12, v4
	v_cvt_f32_f16_sdwa v13, v4 dst_sel:DWORD dst_unused:UNUSED_PAD src0_sel:WORD_1
	v_cvt_f32_f16_e32 v14, v5
	v_cvt_f32_f16_sdwa v15, v5 dst_sel:DWORD dst_unused:UNUSED_PAD src0_sel:WORD_1
	v_cvt_f32_f16_e32 v16, v6
	v_cvt_f32_f16_sdwa v17, v6 dst_sel:DWORD dst_unused:UNUSED_PAD src0_sel:WORD_1
	v_cvt_f32_f16_e32 v18, v7
	v_cvt_f32_f16_sdwa v19, v7 dst_sel:DWORD dst_unused:UNUSED_PAD src0_sel:WORD_1
	global_store_dwordx4 v[30:31], v[4:7], off sc1
	v_pk_fma_f32 v[8:9], v[8:9], s[12:13], v[16:17] op_sel_hi:[1,0,1] neg_lo:[0,0,1] neg_hi:[0,0,1]
	v_pk_fma_f32 v[10:11], v[10:11], s[12:13], v[18:19] op_sel_hi:[1,0,1] neg_lo:[0,0,1] neg_hi:[0,0,1]
	v_pk_fma_f32 v[4:5], v[20:21], s[12:13], v[12:13] op_sel_hi:[1,0,1] neg_lo:[0,0,1] neg_hi:[0,0,1]
	v_pk_fma_f32 v[6:7], v[22:23], s[12:13], v[14:15] op_sel_hi:[1,0,1] neg_lo:[0,0,1] neg_hi:[0,0,1]
	v_cvt_pk_f16_f32 v4, v4, v5
	v_cvt_pk_f16_f32 v5, v6, v7
	v_cvt_pk_f16_f32 v6, v8, v9
	v_cvt_pk_f16_f32 v7, v10, v11
	global_store_dwordx4 v[28:29], v[4:7], off sc1
	s_cbranch_scc1 .LBB3_9
	s_load_dwordx2 s[4:5], s[0:1], 0x8
	v_or_b32_e32 v1, 0x100, v0
	s_mov_b64 s[8:9], 0
	s_mov_b32 s10, s6
	v_mov_b64_e32 v[4:5], v[0:1]
	s_branch .LBB3_4

.LBB3_10:
	s_andn2_b64 vcc, exec, s[4:5]
	s_cbranch_vccnz .LBB3_15
	s_mov_b64 s[4:5], -1
	s_cmpk_gt_i32 s2, 0xbf
	v_lshrrev_b32_e32 v2, 4, v0
	v_lshlrev_b32_e32 v3, 4, v0
	v_lshrrev_b32_e32 v1, 3, v0
	v_and_b32_e32 v0, 7, v0
	s_cbranch_scc0 .LBB3_13
	s_load_dwordx4 s[4:7], s[0:1], 0x68
	s_load_dwordx2 s[8:9], s[0:1], 0x78
	s_lshl_b32 s3, s2, 3
	s_lshl_b32 s10, s2, 6
	s_and_b32 s3, s3, 0x7fffffc0
	s_and_b32 s10, s10, 0x1c0
	s_addk_i32 s3, 0xfa00
	s_lshl_b32 s11, s10, 2
	s_waitcnt lgkmcnt(0)
	s_add_u32 s4, s4, s11
	s_addc_u32 s5, s5, 0
	v_and_b32_e32 v20, 0xf0, v3
	v_mov_b32_e32 v21, 0
	v_lshl_add_u64 v[16:17], s[4:5], 0, v[20:21]
	v_or_b32_e32 v18, s3, v2
	v_mov_b32_e32 v19, v21
	s_movk_i32 s4, 0x104
	v_lshlrev_b64 v[4:5], 11, v[18:19]
	v_mad_u32_u24 v26, v2, s4, v20
	v_or_b32_e32 v20, 16, v18
	v_lshl_add_u64 v[12:13], v[16:17], 0, v[4:5]
	v_lshlrev_b64 v[4:5], 11, v[20:21]
	v_lshl_add_u64 v[14:15], v[16:17], 0, v[4:5]
	global_load_dwordx4 v[4:7], v[12:13], off nt
	global_load_dwordx4 v[8:11], v[14:15], off nt
	v_or_b32_e32 v20, 32, v18
	v_lshlrev_b64 v[12:13], 11, v[20:21]
	v_lshl_add_u64 v[12:13], v[16:17], 0, v[12:13]
	v_or_b32_e32 v20, 48, v18
	global_load_dwordx4 v[12:15], v[12:13], off nt
	v_lshlrev_b64 v[18:19], 11, v[20:21]
	v_lshl_add_u64 v[16:17], v[16:17], 0, v[18:19]
	global_load_dwordx4 v[16:19], v[16:17], off nt
	v_lshlrev_b32_e32 v20, 2, v1
	s_movk_i32 s5, 0x820
	v_mad_u32_u24 v27, v0, s5, v20
	v_add_u32_e32 v32, 0x30c0, v26
	v_add_u32_e32 v33, 0x30c8, v26
	v_add_u32_e32 v28, 0x1040, v26
	v_add_u32_e32 v29, 0x1048, v26
	v_add_u32_e32 v30, 0x2080, v26
	v_add_u32_e32 v31, 0x2088, v26
	v_add_u32_e32 v34, 0x400, v27
	s_mov_b32 s4, 0x45800000
	v_or_b32_e32 v20, s10, v1
	v_lshl_or_b32 v22, v0, 3, s3
	v_lshl_add_u32 v20, v20, 9, v22
	v_lshlrev_b64 v[22:23], 1, v[20:21]
	v_lshl_add_u64 v[24:25], s[6:7], 0, v[22:23]
	v_lshl_add_u64 v[22:23], s[8:9], 0, v[22:23]
	v_add_u32_e32 v20, 0x4000, v20
	s_waitcnt vmcnt(3)
	ds_write2_b32 v26, v4, v5 offset1:1
	ds_write2_b32 v26, v6, v7 offset0:2 offset1:3
	s_waitcnt vmcnt(2)
	ds_write2_b32 v28, v8, v9 offset1:1
	ds_write2_b32 v29, v10, v11 offset1:1
	s_waitcnt vmcnt(1)
	ds_write2_b32 v30, v12, v13 offset1:1
	ds_write2_b32 v31, v14, v15 offset1:1
	s_waitcnt vmcnt(0)
	ds_write2_b32 v32, v16, v17 offset1:1
	ds_write2_b32 v33, v18, v19 offset1:1
	s_waitcnt lgkmcnt(0)
	s_barrier
	ds_read2_b32 v[4:5], v27 offset1:32
	ds_read2_b32 v[12:13], v27 offset0:65 offset1:97
	ds_read2_b32 v[32:33], v27 offset0:130 offset1:162
	ds_read2_b32 v[14:15], v27 offset0:195 offset1:227
	ds_read2_b32 v[40:41], v34 offset0:4 offset1:36
	ds_read2_b32 v[16:17], v34 offset0:69 offset1:101
	ds_read2_b32 v[42:43], v34 offset0:134 offset1:166
	ds_read2_b32 v[18:19], v34 offset0:199 offset1:231
	s_waitcnt lgkmcnt(7)
	v_fma_mixlo_f16 v8, v4, s4, 0
	s_waitcnt lgkmcnt(5)
	v_mov_b32_e32 v26, v32
	s_waitcnt lgkmcnt(4)
	v_mov_b32_e32 v27, v14
	s_waitcnt lgkmcnt(3)
	v_mov_b32_e32 v28, v40
	s_waitcnt lgkmcnt(2)
	v_mov_b32_e32 v29, v16
	s_waitcnt lgkmcnt(1)
	v_mov_b32_e32 v30, v42
	s_waitcnt lgkmcnt(0)
	v_mov_b32_e32 v31, v18
	v_mul_f32_e32 v6, 0x45800000, v4
	v_mul_f32_e32 v7, 0x45800000, v12
	v_mov_b32_e32 v14, v33
	v_fma_mixlo_f16 v4, v4, s4, -v8 op_sel_hi:[0,0,1]
	v_pk_mul_f32 v[8:9], v[26:27], s[4:5] op_sel_hi:[1,0]
	v_pk_mul_f32 v[32:33], v[28:29], s[4:5] op_sel_hi:[1,0]
	v_pk_mul_f32 v[34:35], v[30:31], s[4:5] op_sel_hi:[1,0]
	v_cvt_pk_f16_f32 v6, v6, v7
	v_cvt_pk_f16_f32 v7, v8, v9
	v_cvt_pk_f16_f32 v8, v32, v33
	v_cvt_pk_f16_f32 v9, v34, v35
	v_cvt_f32_f16_e32 v32, v7
	v_cvt_f32_f16_sdwa v33, v7 dst_sel:DWORD dst_unused:UNUSED_PAD src0_sel:WORD_1
	v_cvt_f32_f16_e32 v34, v8
	v_cvt_f32_f16_sdwa v35, v8 dst_sel:DWORD dst_unused:UNUSED_PAD src0_sel:WORD_1
	v_cvt_f32_f16_e32 v38, v9
	v_cvt_f32_f16_sdwa v39, v9 dst_sel:DWORD dst_unused:UNUSED_PAD src0_sel:WORD_1
	v_fma_mixlo_f16 v11, v12, s4, 0
	v_fma_mixlo_f16 v10, v5, s4, 0
	global_store_dwordx4 v[24:25], v[6:9], off sc1
	v_pk_fma_f32 v[24:25], v[30:31], s[4:5], v[38:39] op_sel_hi:[1,0,1] neg_lo:[0,0,1] neg_hi:[0,0,1]
	v_mul_f32_e32 v16, 0x45800000, v5
	v_pk_fma_f32 v[6:7], v[26:27], s[4:5], v[32:33] op_sel_hi:[1,0,1] neg_lo:[0,0,1] neg_hi:[0,0,1]
	v_pk_fma_f32 v[8:9], v[28:29], s[4:5], v[34:35] op_sel_hi:[1,0,1] neg_lo:[0,0,1] neg_hi:[0,0,1]
	v_fma_mixlo_f16 v10, v5, s4, -v10 op_sel_hi:[0,0,1]
	v_pk_mul_f32 v[36:37], v[14:15], s[4:5] op_sel_hi:[1,0]
	v_fma_mixhi_f16 v4, v12, s4, -v11 op_sel_hi:[0,0,1]
	v_cvt_pk_f16_f32 v5, v6, v7
	v_cvt_pk_f16_f32 v6, v8, v9
	v_cvt_pk_f16_f32 v7, v24, v25
	global_store_dwordx4 v[22:23], v[4:7], off sc1
	v_mul_f32_e32 v18, 0x45800000, v13
	v_fma_mixlo_f16 v8, v13, s4, 0
	v_cvt_pk_f16_f32 v5, v36, v37
	v_cvt_f32_f16_e32 v6, v5
	v_cvt_f32_f16_sdwa v7, v5 dst_sel:DWORD dst_unused:UNUSED_PAD src0_sel:WORD_1
	v_cvt_pk_f16_f32 v4, v16, v18
	v_mov_b32_e32 v16, v41
	v_fma_mixhi_f16 v10, v13, s4, -v8 op_sel_hi:[0,0,1]
	v_pk_fma_f32 v[8:9], v[14:15], s[4:5], v[6:7] op_sel_hi:[1,0,1] neg_lo:[0,0,1] neg_hi:[0,0,1]
	v_pk_mul_f32 v[6:7], v[16:17], s[4:5] op_sel_hi:[1,0]
	v_mov_b32_e32 v18, v43
	v_cvt_pk_f16_f32 v6, v6, v7
	v_pk_mul_f32 v[14:15], v[18:19], s[4:5] op_sel_hi:[1,0]
	v_cvt_f32_f16_e32 v12, v6
	v_cvt_f32_f16_sdwa v13, v6 dst_sel:DWORD dst_unused:UNUSED_PAD src0_sel:WORD_1
	v_cvt_pk_f16_f32 v7, v14, v15
	v_cvt_f32_f16_e32 v14, v7
	v_cvt_f32_f16_sdwa v15, v7 dst_sel:DWORD dst_unused:UNUSED_PAD src0_sel:WORD_1
	v_cvt_pk_f16_f32 v11, v8, v9
	v_pk_fma_f32 v[8:9], v[16:17], s[4:5], v[12:13] op_sel_hi:[1,0,1] neg_lo:[0,0,1] neg_hi:[0,0,1]
	s_nop 0
	v_cvt_pk_f16_f32 v12, v8, v9
	v_pk_fma_f32 v[8:9], v[18:19], s[4:5], v[14:15] op_sel_hi:[1,0,1] neg_lo:[0,0,1] neg_hi:[0,0,1]
	s_mov_b64 s[4:5], 0
	v_cvt_pk_f16_f32 v13, v8, v9
	v_lshlrev_b64 v[8:9], 1, v[20:21]
	v_lshl_add_u64 v[14:15], s[6:7], 0, v[8:9]
	global_store_dwordx4 v[14:15], v[4:7], off sc1
	s_nop 1
	v_lshl_add_u64 v[4:5], s[8:9], 0, v[8:9]
	global_store_dwordx4 v[4:5], v[10:13], off sc1
.LBB3_13:
	s_andn2_b64 vcc, exec, s[4:5]
	s_cbranch_vccnz .LBB3_15
	s_load_dwordx4 s[4:7], s[0:1], 0x50
	s_load_dwordx2 s[8:9], s[0:1], 0x60
	s_mul_hi_i32 s0, s2, 0x2aaaaaab
	s_lshr_b32 s1, s0, 31
	s_ashr_i32 s0, s0, 2
	s_add_i32 s0, s0, s1
	s_mul_i32 s1, s0, 24
	s_sub_i32 s1, s2, s1
	s_lshl_b32 s2, s1, 6
	s_ashr_i32 s3, s2, 31
	s_lshl_b32 s10, s0, 6
	s_lshl_b64 s[0:1], s[2:3], 2
	s_waitcnt lgkmcnt(0)
	s_add_u32 s0, s4, s0
	s_addc_u32 s1, s5, s1
	v_and_b32_e32 v20, 0xf0, v3
	v_mov_b32_e32 v21, 0
	v_lshl_add_u64 v[16:17], s[0:1], 0, v[20:21]
	v_or_b32_e32 v3, s10, v2
	s_movk_i32 s4, 0x1800
	v_mad_i64_i32 v[12:13], s[0:1], v3, s4, v[16:17]
	v_or_b32_e32 v4, 16, v3
	v_mad_i64_i32 v[14:15], s[0:1], v4, s4, v[16:17]
	global_load_dwordx4 v[4:7], v[12:13], off nt
	global_load_dwordx4 v[8:11], v[14:15], off nt
	v_or_b32_e32 v12, 32, v3
	v_mad_i64_i32 v[12:13], s[0:1], v12, s4, v[16:17]
	global_load_dwordx4 v[12:15], v[12:13], off nt
	v_or_b32_e32 v3, 48, v3
	v_mad_i64_i32 v[16:17], s[0:1], v3, s4, v[16:17]
	global_load_dwordx4 v[16:19], v[16:17], off nt
	s_movk_i32 s1, 0x104
	v_lshlrev_b32_e32 v3, 2, v1
	s_movk_i32 s4, 0x820
	v_mad_u32_u24 v2, v2, s1, v20
	v_mad_u32_u24 v3, v0, s4, v3
	v_add_u32_e32 v28, 0x1040, v2
	v_add_u32_e32 v29, 0x1048, v2
	v_add_u32_e32 v30, 0x2080, v2
	v_add_u32_e32 v31, 0x2088, v2
	v_add_u32_e32 v32, 0x30c0, v2
	v_add_u32_e32 v33, 0x30c8, v2
	v_add_u32_e32 v34, 0x400, v3
	s_mov_b32 s0, 0x45800000
	s_ashr_i32 s1, s10, 31
	v_or_b32_e32 v22, s2, v1
	v_mov_b32_e32 v23, s3
	v_lshl_or_b32 v20, v0, 3, s10
	v_lshlrev_b64 v[0:1], 9, v[22:23]
	v_mov_b32_e32 v21, s1
	v_lshl_add_u64 v[0:1], v[0:1], 0, v[20:21]
	v_lshlrev_b64 v[24:25], 1, v[0:1]
	v_lshl_add_u64 v[26:27], s[6:7], 0, v[24:25]
	v_or_b32_e32 v22, 32, v22
	s_waitcnt vmcnt(3)
	ds_write2_b32 v2, v4, v5 offset1:1
	ds_write2_b32 v2, v6, v7 offset0:2 offset1:3
	s_waitcnt vmcnt(2)
	ds_write2_b32 v28, v8, v9 offset1:1
	ds_write2_b32 v29, v10, v11 offset1:1
	s_waitcnt vmcnt(1)
	ds_write2_b32 v30, v12, v13 offset1:1
	ds_write2_b32 v31, v14, v15 offset1:1
	s_waitcnt vmcnt(0)
	ds_write2_b32 v32, v16, v17 offset1:1
	ds_write2_b32 v33, v18, v19 offset1:1
	s_waitcnt lgkmcnt(0)
	s_barrier
	ds_read2_b32 v[8:9], v3 offset1:32
	ds_read2_b32 v[10:11], v3 offset0:65 offset1:97
	ds_read2_b32 v[38:39], v3 offset0:130 offset1:162
	ds_read2_b32 v[12:13], v3 offset0:195 offset1:227
	ds_read2_b32 v[40:41], v34 offset0:4 offset1:36
	ds_read2_b32 v[14:15], v34 offset0:69 offset1:101
	ds_read2_b32 v[42:43], v34 offset0:134 offset1:166
	ds_read2_b32 v[16:17], v34 offset0:199 offset1:231
	s_waitcnt lgkmcnt(5)
	v_mov_b32_e32 v2, v38
	s_waitcnt lgkmcnt(4)
	v_mov_b32_e32 v3, v12
	s_waitcnt lgkmcnt(3)
	v_mov_b32_e32 v18, v40
	s_waitcnt lgkmcnt(2)
	v_mov_b32_e32 v19, v14
	s_waitcnt lgkmcnt(1)
	v_mov_b32_e32 v28, v42
	s_waitcnt lgkmcnt(0)
	v_mov_b32_e32 v29, v16
	v_pk_mul_f32 v[6:7], v[2:3], s[0:1] op_sel_hi:[1,0]
	v_pk_mul_f32 v[30:31], v[18:19], s[0:1] op_sel_hi:[1,0]
	v_pk_mul_f32 v[32:33], v[28:29], s[0:1] op_sel_hi:[1,0]
	v_cvt_pk_f16_f32 v5, v6, v7
	v_cvt_pk_f16_f32 v6, v30, v31
	v_cvt_pk_f16_f32 v7, v32, v33
	v_cvt_f32_f16_e32 v30, v5
	v_cvt_f32_f16_sdwa v31, v5 dst_sel:DWORD dst_unused:UNUSED_PAD src0_sel:WORD_1
	v_cvt_f32_f16_e32 v32, v6
	v_cvt_f32_f16_sdwa v33, v6 dst_sel:DWORD dst_unused:UNUSED_PAD src0_sel:WORD_1
	v_cvt_f32_f16_e32 v34, v7
	v_cvt_f32_f16_sdwa v35, v7 dst_sel:DWORD dst_unused:UNUSED_PAD src0_sel:WORD_1
	v_mul_f32_e32 v1, 0x45800000, v8
	v_mul_f32_e32 v4, 0x45800000, v10
	v_fma_mixlo_f16 v0, v8, s0, 0
	v_fma_mixlo_f16 v36, v10, s0, 0
	v_fma_mixlo_f16 v0, v8, s0, -v0 op_sel_hi:[0,0,1]
	v_cvt_pk_f16_f32 v4, v1, v4
	v_pk_fma_f32 v[2:3], v[2:3], s[0:1], v[30:31] op_sel_hi:[1,0,1] neg_lo:[0,0,1] neg_hi:[0,0,1]
	v_pk_fma_f32 v[18:19], v[18:19], s[0:1], v[32:33] op_sel_hi:[1,0,1] neg_lo:[0,0,1] neg_hi:[0,0,1]
	v_pk_fma_f32 v[28:29], v[28:29], s[0:1], v[34:35] op_sel_hi:[1,0,1] neg_lo:[0,0,1] neg_hi:[0,0,1]
	v_fma_mixhi_f16 v0, v10, s0, -v36 op_sel_hi:[0,0,1]
	v_cvt_pk_f16_f32 v1, v2, v3
	v_cvt_pk_f16_f32 v2, v18, v19
	v_cvt_pk_f16_f32 v3, v28, v29
	global_store_dwordx4 v[26:27], v[4:7], off sc1
	v_mov_b32_e32 v12, v39
	v_mov_b32_e32 v14, v41
	v_lshl_add_u64 v[4:5], s[8:9], 0, v[24:25]
	global_store_dwordx4 v[4:5], v[0:3], off sc1
	v_fma_mixlo_f16 v6, v11, s0, 0
	v_mov_b32_e32 v16, v43
	v_fma_mixlo_f16 v0, v9, s0, 0
	v_fma_mixlo_f16 v0, v9, s0, -v0 op_sel_hi:[0,0,1]
	v_pk_mul_f32 v[2:3], v[12:13], s[0:1] op_sel_hi:[1,0]
	v_mul_f32_e32 v4, 0x45800000, v11
	v_cvt_pk_f16_f32 v5, v2, v3
	v_fma_mixhi_f16 v0, v11, s0, -v6 op_sel_hi:[0,0,1]
	v_pk_mul_f32 v[6:7], v[14:15], s[0:1] op_sel_hi:[1,0]
	v_pk_mul_f32 v[10:11], v[16:17], s[0:1] op_sel_hi:[1,0]
	v_cvt_f32_f16_e32 v2, v5
	v_cvt_f32_f16_sdwa v3, v5 dst_sel:DWORD dst_unused:UNUSED_PAD src0_sel:WORD_1
	v_cvt_pk_f16_f32 v6, v6, v7
	v_cvt_pk_f16_f32 v7, v10, v11
	v_mul_f32_e32 v1, 0x45800000, v9
	v_cvt_f32_f16_e32 v8, v6
	v_cvt_f32_f16_sdwa v9, v6 dst_sel:DWORD dst_unused:UNUSED_PAD src0_sel:WORD_1
	v_cvt_f32_f16_e32 v10, v7
	v_cvt_f32_f16_sdwa v11, v7 dst_sel:DWORD dst_unused:UNUSED_PAD src0_sel:WORD_1
	v_pk_fma_f32 v[2:3], v[12:13], s[0:1], v[2:3] op_sel_hi:[1,0,1] neg_lo:[0,0,1] neg_hi:[0,0,1]
	v_cvt_pk_f16_f32 v4, v1, v4
	v_cvt_pk_f16_f32 v1, v2, v3
	v_pk_fma_f32 v[2:3], v[14:15], s[0:1], v[8:9] op_sel_hi:[1,0,1] neg_lo:[0,0,1] neg_hi:[0,0,1]
	v_pk_fma_f32 v[8:9], v[16:17], s[0:1], v[10:11] op_sel_hi:[1,0,1] neg_lo:[0,0,1] neg_hi:[0,0,1]
	v_cvt_pk_f16_f32 v2, v2, v3
	v_cvt_pk_f16_f32 v3, v8, v9
	v_lshlrev_b64 v[8:9], 9, v[22:23]
	v_lshl_add_u64 v[8:9], v[8:9], 0, v[20:21]
	v_lshlrev_b64 v[8:9], 1, v[8:9]
	v_lshl_add_u64 v[10:11], s[6:7], 0, v[8:9]
	global_store_dwordx4 v[10:11], v[4:7], off sc1
	s_nop 1
	v_lshl_add_u64 v[4:5], s[8:9], 0, v[8:9]
	global_store_dwordx4 v[4:5], v[0:3], off sc1

.LBB4_10:
	s_or_b64 exec, exec, s[12:13]
	s_waitcnt vmcnt(0)
	v_add_f32_e32 v11, 0, v6
	v_add_f32_e32 v11, v7, v11
	v_mbcnt_lo_u32_b32 v14, -1, 0
	v_add_f32_e32 v11, v8, v11
	v_mbcnt_hi_u32_b32 v14, -1, v14
	v_add_f32_e32 v11, v9, v11
	v_and_b32_e32 v15, 64, v14
	v_add_f32_e32 v11, v2, v11
	v_add_u32_e32 v15, 64, v15
	v_xor_b32_e32 v16, 32, v14
	v_add_f32_e32 v11, v3, v11
	v_cmp_lt_i32_e32 vcc, v16, v15
	v_add_f32_e32 v11, v4, v11
	v_add_f32_e32 v11, v5, v11
	v_cndmask_b32_e32 v16, v14, v16, vcc
	v_lshlrev_b32_e32 v38, 2, v16
	ds_bpermute_b32 v16, v38, v11
	s_mov_b32 s3, 0xf800000
	v_lshlrev_b64 v[12:13], 9, v[12:13]
	s_load_dwordx4 s[12:15], s[0:1], 0x40
	s_waitcnt lgkmcnt(0)
	v_add_f32_e32 v11, v11, v16
	v_xor_b32_e32 v16, 16, v14
	v_cmp_lt_i32_e32 vcc, v16, v15
	s_nop 1
	v_cndmask_b32_e32 v16, v14, v16, vcc
	v_lshlrev_b32_e32 v39, 2, v16
	ds_bpermute_b32 v16, v39, v11
	s_waitcnt lgkmcnt(0)
	v_add_f32_e32 v11, v11, v16
	v_xor_b32_e32 v16, 8, v14
	v_cmp_lt_i32_e32 vcc, v16, v15
	s_nop 1
	v_cndmask_b32_e32 v16, v14, v16, vcc
	v_lshlrev_b32_e32 v40, 2, v16
	ds_bpermute_b32 v16, v40, v11
	s_waitcnt lgkmcnt(0)
	v_add_f32_e32 v11, v11, v16
	v_xor_b32_e32 v16, 4, v14
	v_cmp_lt_i32_e32 vcc, v16, v15
	s_nop 1
	v_cndmask_b32_e32 v16, v14, v16, vcc
	v_lshlrev_b32_e32 v41, 2, v16
	ds_bpermute_b32 v16, v41, v11
	s_waitcnt lgkmcnt(0)
	v_add_f32_e32 v11, v11, v16
	v_xor_b32_e32 v16, 2, v14
	v_cmp_lt_i32_e32 vcc, v16, v15
	s_nop 1
	v_cndmask_b32_e32 v16, v14, v16, vcc
	v_lshlrev_b32_e32 v42, 2, v16
	ds_bpermute_b32 v16, v42, v11
	s_waitcnt lgkmcnt(0)
	v_add_f32_e32 v11, v11, v16
	v_xor_b32_e32 v16, 1, v14
	v_cmp_lt_i32_e32 vcc, v16, v15
	s_nop 1
	v_cndmask_b32_e32 v14, v14, v16, vcc
	v_lshlrev_b32_e32 v43, 2, v14
	ds_bpermute_b32 v14, v43, v11
	s_waitcnt lgkmcnt(0)
	v_add_f32_e32 v11, v11, v14
	v_mul_f32_e32 v22, 0x3b000000, v11
	v_pk_add_f32 v[30:31], v[6:7], v[22:23] op_sel_hi:[1,0] neg_lo:[0,1] neg_hi:[0,1]
	v_pk_add_f32 v[32:33], v[8:9], v[22:23] op_sel_hi:[1,0] neg_lo:[0,1] neg_hi:[0,1]
	v_pk_mul_f32 v[24:25], v[30:31], v[30:31]
	v_pk_mul_f32 v[26:27], v[32:33], v[32:33]
	v_add_f32_e32 v11, v24, v25
	v_pk_add_f32 v[34:35], v[2:3], v[22:23] op_sel_hi:[1,0] neg_lo:[0,1] neg_hi:[0,1]
	v_add_f32_e32 v11, v26, v11
	v_pk_mul_f32 v[28:29], v[34:35], v[34:35]
	v_add_f32_e32 v11, v27, v11
	v_pk_add_f32 v[36:37], v[4:5], v[22:23] op_sel_hi:[1,0] neg_lo:[0,1] neg_hi:[0,1]
	v_add_f32_e32 v11, v28, v11
	global_load_dwordx4 v[14:17], v10, s[8:9]
	global_load_dwordx4 v[18:21], v10, s[10:11]
	v_pk_mul_f32 v[22:23], v[36:37], v[36:37]
	v_add_f32_e32 v11, v29, v11
	v_add_f32_e32 v11, v22, v11
	v_add_f32_e32 v11, v23, v11
	global_load_dwordx4 v[22:25], v10, s[8:9] offset:16
	global_load_dwordx4 v[26:29], v10, s[10:11] offset:16
	ds_bpermute_b32 v38, v38, v11
	s_waitcnt lgkmcnt(0)
	v_add_f32_e32 v11, v11, v38
	ds_bpermute_b32 v38, v39, v11
	v_mov_b32_e32 v39, 0x3727c5ac
	s_waitcnt lgkmcnt(0)
	v_add_f32_e32 v11, v11, v38
	ds_bpermute_b32 v38, v40, v11
	s_waitcnt lgkmcnt(0)
	v_add_f32_e32 v11, v11, v38
	ds_bpermute_b32 v38, v41, v11
	s_waitcnt lgkmcnt(0)
	v_add_f32_e32 v11, v11, v38
	ds_bpermute_b32 v38, v42, v11
	v_mov_b32_e32 v42, 0x260
	s_waitcnt lgkmcnt(0)
	v_add_f32_e32 v11, v11, v38
	ds_bpermute_b32 v38, v43, v11
	s_waitcnt lgkmcnt(0)
	v_add_f32_e32 v11, v11, v38
	v_fmac_f32_e32 v39, 0x3b000000, v11
	v_mul_f32_e32 v11, 0x4f800000, v39
	v_cmp_gt_f32_e32 vcc, s3, v39
	s_nop 1
	v_cndmask_b32_e32 v40, v39, v11, vcc
	v_sqrt_f32_e32 v41, v40
	v_lshl_add_u64 v[38:39], v[12:13], 2, s[6:7]
	v_mov_b32_e32 v11, 0
	v_lshl_add_u64 v[38:39], v[38:39], 0, v[10:11]
	v_add_u32_e32 v43, -1, v41
	v_add_u32_e32 v44, 1, v41
	v_fma_f32 v45, -v43, v41, v40
	v_fma_f32 v46, -v44, v41, v40
	v_cmp_ge_f32_e64 s[4:5], 0, v45
	global_store_dwordx4 v[38:39], v[6:9], off sc1
	global_store_dwordx4 v[38:39], v[2:5], off offset:16 sc1
	v_cndmask_b32_e64 v41, v41, v43, s[4:5]
	v_cmp_lt_f32_e64 s[4:5], 0, v46
	v_lshlrev_b64 v[12:13], 1, v[12:13]
	v_lshlrev_b32_e32 v10, 1, v1
	v_cndmask_b32_e64 v41, v41, v44, s[4:5]
	v_mul_f32_e32 v43, 0x37800000, v41
	v_cndmask_b32_e32 v41, v41, v43, vcc
	v_cmp_class_f32_e32 vcc, v40, v42
	s_nop 1
	v_cndmask_b32_e32 v40, v41, v40, vcc
	v_div_scale_f32 v41, s[4:5], v40, v40, 1.0
	v_rcp_f32_e32 v42, v41
	s_mov_b32 s4, 0x43800000
	v_fma_f32 v2, -v41, v42, 1.0
	v_fmac_f32_e32 v42, v2, v42
	v_div_scale_f32 v2, vcc, 1.0, v40, 1.0
	v_mul_f32_e32 v3, v2, v42
	v_fma_f32 v4, -v41, v3, v2
	v_fmac_f32_e32 v3, v4, v42
	v_fma_f32 v2, -v41, v3, v2
	v_div_fmas_f32 v2, v2, v42, v3
	v_div_fixup_f32 v2, v2, v40, 1.0
	v_pk_mul_f32 v[4:5], v[30:31], v[2:3] op_sel_hi:[1,0]
	v_pk_mul_f32 v[8:9], v[32:33], v[2:3] op_sel_hi:[1,0]
	s_waitcnt vmcnt(4)
	v_pk_fma_f32 v[4:5], v[14:15], v[4:5], v[18:19]
	v_pk_fma_f32 v[8:9], v[16:17], v[8:9], v[20:21]
	v_pk_mul_f32 v[6:7], v[4:5], s[4:5] op_sel_hi:[1,0]
	v_pk_mul_f32 v[16:17], v[34:35], v[2:3] op_sel_hi:[1,0]
	v_pk_mul_f32 v[2:3], v[36:37], v[2:3] op_sel_hi:[1,0]
	v_pk_mul_f32 v[14:15], v[8:9], s[4:5] op_sel_hi:[1,0]
	s_waitcnt vmcnt(2)
	v_pk_fma_f32 v[20:21], v[24:25], v[2:3], v[28:29]
	v_cvt_pk_f16_f32 v2, v6, v7
	v_cvt_f32_f16_e32 v6, v2
	v_cvt_f32_f16_sdwa v7, v2 dst_sel:DWORD dst_unused:UNUSED_PAD src0_sel:WORD_1
	v_cvt_pk_f16_f32 v3, v14, v15
	v_cvt_f32_f16_e32 v14, v3
	v_cvt_f32_f16_sdwa v15, v3 dst_sel:DWORD dst_unused:UNUSED_PAD src0_sel:WORD_1
	v_pk_fma_f32 v[16:17], v[22:23], v[16:17], v[26:27]
	v_pk_mul_f32 v[22:23], v[20:21], s[4:5] op_sel_hi:[1,0]
	v_pk_mul_f32 v[18:19], v[16:17], s[4:5] op_sel_hi:[1,0]
	v_pk_fma_f32 v[4:5], v[4:5], s[4:5], v[6:7] op_sel_hi:[1,0,1] neg_lo:[0,0,1] neg_hi:[0,0,1]
	v_pk_fma_f32 v[8:9], v[8:9], s[4:5], v[14:15] op_sel_hi:[1,0,1] neg_lo:[0,0,1] neg_hi:[0,0,1]
	v_cvt_pk_f16_f32 v6, v4, v5
	v_cvt_pk_f16_f32 v4, v18, v19
	v_cvt_pk_f16_f32 v5, v22, v23
	v_cvt_f32_f16_e32 v14, v4
	v_cvt_f32_f16_sdwa v15, v4 dst_sel:DWORD dst_unused:UNUSED_PAD src0_sel:WORD_1
	v_cvt_f32_f16_e32 v18, v5
	v_cvt_f32_f16_sdwa v19, v5 dst_sel:DWORD dst_unused:UNUSED_PAD src0_sel:WORD_1
	v_cvt_pk_f16_f32 v7, v8, v9
	v_pk_fma_f32 v[8:9], v[16:17], s[4:5], v[14:15] op_sel_hi:[1,0,1] neg_lo:[0,0,1] neg_hi:[0,0,1]
	v_pk_fma_f32 v[14:15], v[20:21], s[4:5], v[18:19] op_sel_hi:[1,0,1] neg_lo:[0,0,1] neg_hi:[0,0,1]
	v_cvt_pk_f16_f32 v8, v8, v9
	v_cvt_pk_f16_f32 v9, v14, v15
	v_lshl_add_u64 v[14:15], s[12:13], 0, v[12:13]
	v_lshl_add_u64 v[14:15], v[14:15], 0, v[10:11]
	global_store_dwordx4 v[14:15], v[2:5], off sc1
	s_mov_b64 s[4:5], 0
	s_nop 0
	v_lshl_add_u64 v[2:3], s[14:15], 0, v[12:13]
	v_lshl_add_u64 v[2:3], v[2:3], 0, v[10:11]
	global_store_dwordx4 v[2:3], v[6:9], off sc1
.LBB4_11:
	s_and_b64 vcc, exec, s[4:5]
	s_cbranch_vccz .LBB4_16
	s_mov_b64 s[4:5], -1
	s_cmpk_gt_i32 s2, 0xbf
	v_lshrrev_b32_e32 v2, 4, v0
	v_lshlrev_b32_e32 v3, 4, v0
	v_lshrrev_b32_e32 v1, 3, v0
	v_and_b32_e32 v0, 7, v0
	s_cbranch_scc0 .LBB4_14
	s_load_dwordx4 s[4:7], s[0:1], 0x68
	s_load_dwordx2 s[8:9], s[0:1], 0x78
	s_lshl_b32 s3, s2, 3
	s_lshl_b32 s10, s2, 6
	s_and_b32 s3, s3, 0x7fffffc0
	s_and_b32 s10, s10, 0x1c0
	s_addk_i32 s3, 0xfa00
	s_lshl_b32 s11, s10, 2
	s_waitcnt lgkmcnt(0)
	s_add_u32 s4, s4, s11
	s_addc_u32 s5, s5, 0
	v_and_b32_e32 v20, 0xf0, v3
	v_mov_b32_e32 v21, 0
	v_lshl_add_u64 v[16:17], s[4:5], 0, v[20:21]
	v_or_b32_e32 v18, s3, v2
	v_mov_b32_e32 v19, v21
	s_movk_i32 s4, 0x104
	v_lshlrev_b64 v[4:5], 11, v[18:19]
	v_mad_u32_u24 v26, v2, s4, v20
	v_or_b32_e32 v20, 16, v18
	v_lshl_add_u64 v[12:13], v[16:17], 0, v[4:5]
	v_lshlrev_b64 v[4:5], 11, v[20:21]
	v_lshl_add_u64 v[14:15], v[16:17], 0, v[4:5]
	global_load_dwordx4 v[4:7], v[12:13], off nt
	global_load_dwordx4 v[8:11], v[14:15], off nt
	v_or_b32_e32 v20, 32, v18
	v_lshlrev_b64 v[12:13], 11, v[20:21]
	v_lshl_add_u64 v[12:13], v[16:17], 0, v[12:13]
	v_or_b32_e32 v20, 48, v18
	global_load_dwordx4 v[12:15], v[12:13], off nt
	v_lshlrev_b64 v[18:19], 11, v[20:21]
	v_lshl_add_u64 v[16:17], v[16:17], 0, v[18:19]
	global_load_dwordx4 v[16:19], v[16:17], off nt
	v_lshlrev_b32_e32 v20, 2, v1
	s_movk_i32 s5, 0x820
	v_mad_u32_u24 v27, v0, s5, v20
	v_add_u32_e32 v32, 0x30c0, v26
	v_add_u32_e32 v33, 0x30c8, v26
	v_add_u32_e32 v28, 0x1040, v26
	v_add_u32_e32 v29, 0x1048, v26
	v_add_u32_e32 v30, 0x2080, v26
	v_add_u32_e32 v31, 0x2088, v26
	v_add_u32_e32 v34, 0x400, v27
	s_mov_b32 s4, 0x45800000
	v_or_b32_e32 v20, s10, v1
	v_lshl_or_b32 v22, v0, 3, s3
	v_lshl_add_u32 v20, v20, 9, v22
	v_lshlrev_b64 v[22:23], 1, v[20:21]
	v_lshl_add_u64 v[24:25], s[6:7], 0, v[22:23]
	v_lshl_add_u64 v[22:23], s[8:9], 0, v[22:23]
	v_add_u32_e32 v20, 0x4000, v20
	s_waitcnt vmcnt(3)
	ds_write2_b32 v26, v4, v5 offset1:1
	ds_write2_b32 v26, v6, v7 offset0:2 offset1:3
	s_waitcnt vmcnt(2)
	ds_write2_b32 v28, v8, v9 offset1:1
	ds_write2_b32 v29, v10, v11 offset1:1
	s_waitcnt vmcnt(1)
	ds_write2_b32 v30, v12, v13 offset1:1
	ds_write2_b32 v31, v14, v15 offset1:1
	s_waitcnt vmcnt(0)
	ds_write2_b32 v32, v16, v17 offset1:1
	ds_write2_b32 v33, v18, v19 offset1:1
	s_waitcnt lgkmcnt(0)
	s_barrier
	ds_read2_b32 v[4:5], v27 offset1:32
	ds_read2_b32 v[12:13], v27 offset0:65 offset1:97
	ds_read2_b32 v[32:33], v27 offset0:130 offset1:162
	ds_read2_b32 v[14:15], v27 offset0:195 offset1:227
	ds_read2_b32 v[40:41], v34 offset0:4 offset1:36
	ds_read2_b32 v[16:17], v34 offset0:69 offset1:101
	ds_read2_b32 v[42:43], v34 offset0:134 offset1:166
	ds_read2_b32 v[18:19], v34 offset0:199 offset1:231
	s_waitcnt lgkmcnt(7)
	v_fma_mixlo_f16 v8, v4, s4, 0
	s_waitcnt lgkmcnt(5)
	v_mov_b32_e32 v26, v32
	s_waitcnt lgkmcnt(4)
	v_mov_b32_e32 v27, v14
	s_waitcnt lgkmcnt(3)
	v_mov_b32_e32 v28, v40
	s_waitcnt lgkmcnt(2)
	v_mov_b32_e32 v29, v16
	s_waitcnt lgkmcnt(1)
	v_mov_b32_e32 v30, v42
	s_waitcnt lgkmcnt(0)
	v_mov_b32_e32 v31, v18
	v_mul_f32_e32 v6, 0x45800000, v4
	v_mul_f32_e32 v7, 0x45800000, v12
	v_mov_b32_e32 v14, v33
	v_fma_mixlo_f16 v4, v4, s4, -v8 op_sel_hi:[0,0,1]
	v_pk_mul_f32 v[8:9], v[26:27], s[4:5] op_sel_hi:[1,0]
	v_pk_mul_f32 v[32:33], v[28:29], s[4:5] op_sel_hi:[1,0]
	v_pk_mul_f32 v[34:35], v[30:31], s[4:5] op_sel_hi:[1,0]
	v_cvt_pk_f16_f32 v6, v6, v7
	v_cvt_pk_f16_f32 v7, v8, v9
	v_cvt_pk_f16_f32 v8, v32, v33
	v_cvt_pk_f16_f32 v9, v34, v35
	v_cvt_f32_f16_e32 v32, v7
	v_cvt_f32_f16_sdwa v33, v7 dst_sel:DWORD dst_unused:UNUSED_PAD src0_sel:WORD_1
	v_cvt_f32_f16_e32 v34, v8
	v_cvt_f32_f16_sdwa v35, v8 dst_sel:DWORD dst_unused:UNUSED_PAD src0_sel:WORD_1
	v_cvt_f32_f16_e32 v38, v9
	v_cvt_f32_f16_sdwa v39, v9 dst_sel:DWORD dst_unused:UNUSED_PAD src0_sel:WORD_1
	v_fma_mixlo_f16 v11, v12, s4, 0
	v_fma_mixlo_f16 v10, v5, s4, 0
	global_store_dwordx4 v[24:25], v[6:9], off sc1
	v_pk_fma_f32 v[24:25], v[30:31], s[4:5], v[38:39] op_sel_hi:[1,0,1] neg_lo:[0,0,1] neg_hi:[0,0,1]
	v_mul_f32_e32 v16, 0x45800000, v5
	v_pk_fma_f32 v[6:7], v[26:27], s[4:5], v[32:33] op_sel_hi:[1,0,1] neg_lo:[0,0,1] neg_hi:[0,0,1]
	v_pk_fma_f32 v[8:9], v[28:29], s[4:5], v[34:35] op_sel_hi:[1,0,1] neg_lo:[0,0,1] neg_hi:[0,0,1]
	v_fma_mixlo_f16 v10, v5, s4, -v10 op_sel_hi:[0,0,1]
	v_pk_mul_f32 v[36:37], v[14:15], s[4:5] op_sel_hi:[1,0]
	v_fma_mixhi_f16 v4, v12, s4, -v11 op_sel_hi:[0,0,1]
	v_cvt_pk_f16_f32 v5, v6, v7
	v_cvt_pk_f16_f32 v6, v8, v9
	v_cvt_pk_f16_f32 v7, v24, v25
	global_store_dwordx4 v[22:23], v[4:7], off sc1
	v_mul_f32_e32 v18, 0x45800000, v13
	v_fma_mixlo_f16 v8, v13, s4, 0
	v_cvt_pk_f16_f32 v5, v36, v37
	v_cvt_f32_f16_e32 v6, v5
	v_cvt_f32_f16_sdwa v7, v5 dst_sel:DWORD dst_unused:UNUSED_PAD src0_sel:WORD_1
	v_cvt_pk_f16_f32 v4, v16, v18
	v_mov_b32_e32 v16, v41
	v_fma_mixhi_f16 v10, v13, s4, -v8 op_sel_hi:[0,0,1]
	v_pk_fma_f32 v[8:9], v[14:15], s[4:5], v[6:7] op_sel_hi:[1,0,1] neg_lo:[0,0,1] neg_hi:[0,0,1]
	v_pk_mul_f32 v[6:7], v[16:17], s[4:5] op_sel_hi:[1,0]
	v_mov_b32_e32 v18, v43
	v_cvt_pk_f16_f32 v6, v6, v7
	v_pk_mul_f32 v[14:15], v[18:19], s[4:5] op_sel_hi:[1,0]
	v_cvt_f32_f16_e32 v12, v6
	v_cvt_f32_f16_sdwa v13, v6 dst_sel:DWORD dst_unused:UNUSED_PAD src0_sel:WORD_1
	v_cvt_pk_f16_f32 v7, v14, v15
	v_cvt_f32_f16_e32 v14, v7
	v_cvt_f32_f16_sdwa v15, v7 dst_sel:DWORD dst_unused:UNUSED_PAD src0_sel:WORD_1
	v_cvt_pk_f16_f32 v11, v8, v9
	v_pk_fma_f32 v[8:9], v[16:17], s[4:5], v[12:13] op_sel_hi:[1,0,1] neg_lo:[0,0,1] neg_hi:[0,0,1]
	s_nop 0
	v_cvt_pk_f16_f32 v12, v8, v9
	v_pk_fma_f32 v[8:9], v[18:19], s[4:5], v[14:15] op_sel_hi:[1,0,1] neg_lo:[0,0,1] neg_hi:[0,0,1]
	s_mov_b64 s[4:5], 0
	v_cvt_pk_f16_f32 v13, v8, v9
	v_lshlrev_b64 v[8:9], 1, v[20:21]
	v_lshl_add_u64 v[14:15], s[6:7], 0, v[8:9]
	global_store_dwordx4 v[14:15], v[4:7], off sc1
	s_nop 1
	v_lshl_add_u64 v[4:5], s[8:9], 0, v[8:9]
	global_store_dwordx4 v[4:5], v[10:13], off sc1

.LBB5_8:
	s_mov_b32 s0, 0x38800000
	v_pk_mul_f32 v[116:117], v[64:65], s[0:1] op_sel_hi:[1,0]
	v_lshlrev_b32_e32 v0, 1, v73
	v_cvt_pk_f16_f32 v81, v116, v117
	v_lshrrev_b32_e32 v1, 5, v68
	v_lshlrev_b32_e32 v70, 4, v76
	v_mul_u32_u24_e32 v69, 0x90, v72
	v_cvt_f32_f16_e32 v116, v81
	v_cvt_f32_f16_sdwa v117, v81 dst_sel:DWORD dst_unused:UNUSED_PAD src0_sel:WORD_1
	v_and_or_b32 v0, v0, 2, v1
	v_add3_u32 v77, v74, v70, v69
	v_mul_f32_e32 v69, 0x38800000, v62
	v_mul_f32_e32 v71, 0x38800000, v63
	v_lshlrev_b32_e32 v68, 3, v0
	v_cvt_pk_f16_f32 v80, v69, v71
	v_mul_u32_u24_e32 v69, 0x90, v82
	v_add3_u32 v78, v74, v68, v69
	ds_write_b64 v78, v[80:81]
	v_pk_fma_f32 v[80:81], v[64:65], s[0:1], v[116:117] op_sel_hi:[1,0,1] neg_lo:[0,0,1] neg_hi:[0,0,1]
	v_fma_mixlo_f16 v87, v58, s0, 0
	v_cvt_pk_f16_f32 v119, v80, v81
	v_pk_mul_f32 v[80:81], v[60:61], s[0:1] op_sel_hi:[1,0]
	v_fma_mixlo_f16 v116, v58, s0, -v87 op_sel_hi:[0,0,1]
	v_cvt_pk_f16_f32 v85, v80, v81
	v_cvt_f32_f16_e32 v80, v85
	v_cvt_f32_f16_sdwa v81, v85 dst_sel:DWORD dst_unused:UNUSED_PAD src0_sel:WORD_1
	v_fma_mixlo_f16 v89, v59, s0, 0
	v_fma_mixhi_f16 v116, v59, s0, -v89 op_sel_hi:[0,0,1]
	v_fma_mixlo_f16 v91, v46, s0, 0
	v_pk_fma_f32 v[80:81], v[60:61], s[0:1], v[80:81] op_sel_hi:[1,0,1] neg_lo:[0,0,1] neg_hi:[0,0,1]
	v_fma_mixlo_f16 v120, v46, s0, -v91 op_sel_hi:[0,0,1]
	v_cvt_pk_f16_f32 v117, v80, v81
	v_pk_mul_f32 v[80:81], v[48:49], s[0:1] op_sel_hi:[1,0]
	v_mul_f32_e32 v68, 0x38800000, v58
	v_cvt_pk_f16_f32 v87, v80, v81
	v_cvt_f32_f16_e32 v80, v87
	v_cvt_f32_f16_sdwa v81, v87 dst_sel:DWORD dst_unused:UNUSED_PAD src0_sel:WORD_1
	v_mul_f32_e32 v69, 0x38800000, v59
	v_cvt_pk_f16_f32 v84, v68, v69
	v_mul_f32_e32 v68, 0x38800000, v46
	v_pk_fma_f32 v[80:81], v[48:49], s[0:1], v[80:81] op_sel_hi:[1,0,1] neg_lo:[0,0,1] neg_hi:[0,0,1]
	v_mul_f32_e32 v69, 0x38800000, v47
	v_cvt_pk_f16_f32 v121, v80, v81
	v_pk_mul_f32 v[80:81], v[44:45], s[0:1] op_sel_hi:[1,0]
	v_cvt_pk_f16_f32 v86, v68, v69
	v_cvt_pk_f16_f32 v89, v80, v81
	v_cvt_f32_f16_e32 v80, v89
	v_cvt_f32_f16_sdwa v81, v89 dst_sel:DWORD dst_unused:UNUSED_PAD src0_sel:WORD_1
	v_mul_f32_e32 v68, 0x38800000, v42
	v_mul_f32_e32 v69, 0x38800000, v43
	v_cvt_pk_f16_f32 v88, v68, v69
	v_pk_fma_f32 v[80:81], v[44:45], s[0:1], v[80:81] op_sel_hi:[1,0,1] neg_lo:[0,0,1] neg_hi:[0,0,1]
	v_mul_f32_e32 v68, 0x38800000, v30
	v_cvt_pk_f16_f32 v123, v80, v81
	v_pk_mul_f32 v[80:81], v[32:33], s[0:1] op_sel_hi:[1,0]
	v_fma_mixlo_f16 v124, v30, s0, 0
	v_cvt_pk_f16_f32 v91, v80, v81
	v_cvt_f32_f16_e32 v80, v91
	v_cvt_f32_f16_sdwa v81, v91 dst_sel:DWORD dst_unused:UNUSED_PAD src0_sel:WORD_1
	v_mul_f32_e32 v69, 0x38800000, v31
	v_fma_mixlo_f16 v125, v31, s0, 0
	v_cvt_pk_f16_f32 v90, v68, v69
	v_mul_f32_e32 v68, 0x38800000, v26
	v_mul_f32_e32 v69, 0x38800000, v27
	v_fma_mixlo_f16 v124, v30, s0, -v124 op_sel_hi:[0,0,1]
	v_pk_fma_f32 v[80:81], v[32:33], s[0:1], v[80:81] op_sel_hi:[1,0,1] neg_lo:[0,0,1] neg_hi:[0,0,1]
	v_fma_mixlo_f16 v93, v47, s0, 0
	v_fma_mixlo_f16 v95, v42, s0, 0
	v_cvt_pk_f16_f32 v92, v68, v69
	v_mul_f32_e32 v68, 0x38800000, v14
	v_mul_f32_e32 v69, 0x38800000, v15
	ds_write_b64 v78, v[84:85] offset:2304
	v_fma_mixhi_f16 v124, v31, s0, -v125 op_sel_hi:[0,0,1]
	v_cvt_pk_f16_f32 v125, v80, v81
	v_pk_mul_f32 v[80:81], v[28:29], s[0:1] op_sel_hi:[1,0]
	v_pk_mul_f32 v[84:85], v[16:17], s[0:1] op_sel_hi:[1,0]
	v_cvt_pk_f16_f32 v94, v68, v69
	v_fma_mixhi_f16 v120, v47, s0, -v93 op_sel_hi:[0,0,1]
	v_fma_mixlo_f16 v122, v42, s0, -v95 op_sel_hi:[0,0,1]
	v_cvt_pk_f16_f32 v93, v80, v81
	v_cvt_pk_f16_f32 v95, v84, v85
	ds_write_b64 v78, v[86:87] offset:32
	ds_write_b64 v78, v[88:89] offset:2336
	ds_write_b64 v78, v[90:91] offset:64
	ds_write_b64 v78, v[92:93] offset:2368
	ds_write_b64 v78, v[94:95] offset:96
	ds_read_b128 v[84:87], v77
	v_lshlrev_b64 v[0:1], 6, v[66:67]
	v_mul_f32_e32 v68, 0x38800000, v10
	v_mul_f32_e32 v69, 0x38800000, v11
	v_lshlrev_b32_e32 v98, 1, v75
	v_mov_b32_e32 v99, 0
	v_cvt_pk_f16_f32 v96, v68, v69
	v_lshl_add_u64 v[68:69], s[12:13], 0, v[98:99]
	v_mov_b32_e32 v71, v99
	v_or_b32_e32 v100, v0, v72
	v_mov_b32_e32 v101, v1
	v_lshl_add_u64 v[68:69], v[68:69], 0, v[70:71]
	v_lshlrev_b64 v[100:101], 11, v[100:101]
	v_lshl_add_u64 v[102:103], v[68:69], 0, v[100:101]
	v_cvt_f32_f16_e32 v80, v93
	v_cvt_f32_f16_sdwa v81, v93 dst_sel:DWORD dst_unused:UNUSED_PAD src0_sel:WORD_1
	s_waitcnt lgkmcnt(0)
	global_store_dwordx4 v[102:103], v[84:87], off sc1
	v_fma_mixlo_f16 v126, v26, s0, 0
	v_fma_mixlo_f16 v79, v62, s0, 0
	v_cvt_f32_f16_e32 v84, v95
	v_cvt_f32_f16_sdwa v85, v95 dst_sel:DWORD dst_unused:UNUSED_PAD src0_sel:WORD_1
	v_fma_mixlo_f16 v127, v27, s0, 0
	v_fma_mixlo_f16 v128, v14, s0, 0
	v_fma_mixlo_f16 v126, v26, s0, -v126 op_sel_hi:[0,0,1]
	v_pk_fma_f32 v[80:81], v[28:29], s[0:1], v[80:81] op_sel_hi:[1,0,1] neg_lo:[0,0,1] neg_hi:[0,0,1]
	v_fma_mixlo_f16 v83, v63, s0, 0
	v_fma_mixlo_f16 v129, v15, s0, 0
	v_fma_mixlo_f16 v118, v62, s0, -v79 op_sel_hi:[0,0,1]
	v_fma_mixhi_f16 v126, v27, s0, -v127 op_sel_hi:[0,0,1]
	v_cvt_pk_f16_f32 v127, v80, v81
	v_fma_mixlo_f16 v80, v14, s0, -v128 op_sel_hi:[0,0,1]
	v_pk_fma_f32 v[84:85], v[16:17], s[0:1], v[84:85] op_sel_hi:[1,0,1] neg_lo:[0,0,1] neg_hi:[0,0,1]
	v_fma_mixhi_f16 v118, v63, s0, -v83 op_sel_hi:[0,0,1]
	v_fma_mixhi_f16 v80, v15, s0, -v129 op_sel_hi:[0,0,1]
	v_cvt_pk_f16_f32 v81, v84, v85
	v_fma_mixlo_f16 v97, v43, s0, 0
	ds_read_b128 v[88:91], v77 offset:1152
	ds_write_b64 v78, v[118:119]
	ds_write_b64 v78, v[120:121] offset:32
	ds_write_b64 v78, v[124:125] offset:64
	ds_write_b64 v78, v[80:81] offset:96
	v_pk_mul_f32 v[80:81], v[12:13], s[0:1] op_sel_hi:[1,0]
	v_fma_mixhi_f16 v122, v43, s0, -v97 op_sel_hi:[0,0,1]
	v_cvt_pk_f16_f32 v97, v80, v81
	ds_write_b64 v78, v[96:97] offset:2400
	ds_read_b128 v[84:87], v77 offset:2304
	ds_read_b128 v[92:95], v77 offset:3456
	v_or_b32_e32 v132, 8, v72
	v_or_b32_e32 v133, 16, v72
	v_or_b32_e32 v104, v0, v132
	v_mov_b32_e32 v105, v1
	v_or_b32_e32 v108, v0, v133
	v_mov_b32_e32 v109, v1
	v_or_b32_e32 v134, 24, v72
	v_lshlrev_b64 v[104:105], 11, v[104:105]
	v_lshlrev_b64 v[108:109], 11, v[108:109]
	v_or_b32_e32 v112, v0, v134
	v_mov_b32_e32 v113, v1
	v_lshl_add_u64 v[106:107], v[68:69], 0, v[104:105]
	v_lshl_add_u64 v[110:111], v[68:69], 0, v[108:109]
	v_lshlrev_b64 v[112:113], 11, v[112:113]
	v_lshl_add_u64 v[114:115], v[68:69], 0, v[112:113]
	s_waitcnt lgkmcnt(7)
	global_store_dwordx4 v[106:107], v[88:91], off sc1
	s_waitcnt lgkmcnt(1)
	global_store_dwordx4 v[110:111], v[84:87], off sc1
	s_waitcnt lgkmcnt(0)
	global_store_dwordx4 v[114:115], v[92:95], off sc1
	v_fma_mixlo_f16 v130, v10, s0, 0
	v_cvt_f32_f16_e32 v84, v97
	v_cvt_f32_f16_sdwa v85, v97 dst_sel:DWORD dst_unused:UNUSED_PAD src0_sel:WORD_1
	v_fma_mixlo_f16 v131, v11, s0, 0
	v_fma_mixlo_f16 v80, v10, s0, -v130 op_sel_hi:[0,0,1]
	v_fma_mixhi_f16 v80, v11, s0, -v131 op_sel_hi:[0,0,1]
	v_pk_fma_f32 v[84:85], v[12:13], s[0:1], v[84:85] op_sel_hi:[1,0,1] neg_lo:[0,0,1] neg_hi:[0,0,1]
	ds_write_b64 v78, v[116:117] offset:2304
	ds_write_b64 v78, v[122:123] offset:2336
	ds_write_b64 v78, v[126:127] offset:2368
	v_cvt_pk_f16_f32 v81, v84, v85
	ds_write_b64 v78, v[80:81] offset:2400
	ds_read_b128 v[84:87], v77
	v_lshl_add_u64 v[80:81], s[14:15], 0, v[98:99]
	v_lshl_add_u64 v[70:71], v[80:81], 0, v[70:71]
	v_lshl_add_u64 v[80:81], v[70:71], 0, v[100:101]
	ds_read_b128 v[88:91], v77 offset:1152
	s_waitcnt lgkmcnt(1)
	global_store_dwordx4 v[80:81], v[84:87], off sc1
	ds_read_b128 v[84:87], v77 offset:2304
	ds_read_b128 v[92:95], v77 offset:3456
	v_lshl_add_u64 v[80:81], v[70:71], 0, v[104:105]
	s_waitcnt lgkmcnt(2)
	global_store_dwordx4 v[80:81], v[88:91], off sc1
	v_lshl_add_u64 v[80:81], v[70:71], 0, v[108:109]
	s_waitcnt lgkmcnt(1)
	global_store_dwordx4 v[80:81], v[84:87], off sc1
	v_lshl_add_u64 v[80:81], v[70:71], 0, v[112:113]
	s_waitcnt lgkmcnt(0)
	global_store_dwordx4 v[80:81], v[92:95], off sc1
	v_or_b32_e32 v79, 32, v0
	v_mul_f32_e32 v0, 0x38800000, v54
	v_mul_f32_e32 v80, 0x38800000, v55
	v_cvt_pk_f16_f32 v80, v0, v80
	v_mul_f32_e32 v0, 0x38800000, v50
	v_mul_f32_e32 v81, 0x38800000, v51
	v_cvt_pk_f16_f32 v84, v0, v81
	v_mul_f32_e32 v0, 0x38800000, v38
	v_mul_f32_e32 v81, 0x38800000, v39
	v_cvt_pk_f16_f32 v86, v0, v81
	v_mul_f32_e32 v0, 0x38800000, v34
	v_mul_f32_e32 v81, 0x38800000, v35
	v_cvt_pk_f16_f32 v88, v0, v81
	v_mul_f32_e32 v0, 0x38800000, v22
	v_mul_f32_e32 v81, 0x38800000, v23
	v_cvt_pk_f16_f32 v90, v0, v81
	v_mul_f32_e32 v0, 0x38800000, v18
	v_mul_f32_e32 v81, 0x38800000, v19
	v_cvt_pk_f16_f32 v92, v0, v81
	v_mul_f32_e32 v0, 0x38800000, v6
	v_mul_f32_e32 v81, 0x38800000, v7
	v_cvt_pk_f16_f32 v94, v0, v81
	v_mul_f32_e32 v0, 0x38800000, v2
	v_mul_f32_e32 v81, 0x38800000, v3
	v_pk_mul_f32 v[110:111], v[56:57], s[0:1] op_sel_hi:[1,0]
	v_cvt_pk_f16_f32 v96, v0, v81
	v_cvt_pk_f16_f32 v81, v110, v111
	v_cvt_f32_f16_e32 v110, v81
	v_cvt_f32_f16_sdwa v111, v81 dst_sel:DWORD dst_unused:UNUSED_PAD src0_sel:WORD_1
	v_fma_mixlo_f16 v83, v54, s0, 0
	ds_write_b64 v78, v[80:81]
	v_fma_mixlo_f16 v85, v55, s0, 0
	v_pk_fma_f32 v[80:81], v[56:57], s[0:1], v[110:111] op_sel_hi:[1,0,1] neg_lo:[0,0,1] neg_hi:[0,0,1]
	v_fma_mixlo_f16 v112, v54, s0, -v83 op_sel_hi:[0,0,1]
	v_cvt_pk_f16_f32 v113, v80, v81
	v_pk_mul_f32 v[80:81], v[52:53], s[0:1] op_sel_hi:[1,0]
	v_fma_mixhi_f16 v112, v55, s0, -v85 op_sel_hi:[0,0,1]
	v_cvt_pk_f16_f32 v85, v80, v81
	v_cvt_f32_f16_e32 v80, v85
	v_cvt_f32_f16_sdwa v81, v85 dst_sel:DWORD dst_unused:UNUSED_PAD src0_sel:WORD_1
	v_fma_mixlo_f16 v87, v50, s0, 0
	v_fma_mixlo_f16 v110, v50, s0, -v87 op_sel_hi:[0,0,1]
	v_fma_mixlo_f16 v89, v51, s0, 0
	v_pk_fma_f32 v[80:81], v[52:53], s[0:1], v[80:81] op_sel_hi:[1,0,1] neg_lo:[0,0,1] neg_hi:[0,0,1]
	v_fma_mixhi_f16 v110, v51, s0, -v89 op_sel_hi:[0,0,1]
	v_cvt_pk_f16_f32 v111, v80, v81
	v_pk_mul_f32 v[80:81], v[40:41], s[0:1] op_sel_hi:[1,0]
	v_fma_mixlo_f16 v91, v38, s0, 0
	v_cvt_pk_f16_f32 v87, v80, v81
	v_cvt_f32_f16_e32 v80, v87
	v_cvt_f32_f16_sdwa v81, v87 dst_sel:DWORD dst_unused:UNUSED_PAD src0_sel:WORD_1
	v_fma_mixlo_f16 v114, v38, s0, -v91 op_sel_hi:[0,0,1]
	v_fma_mixlo_f16 v118, v22, s0, 0
	v_fma_mixlo_f16 v119, v23, s0, 0
	v_pk_fma_f32 v[80:81], v[40:41], s[0:1], v[80:81] op_sel_hi:[1,0,1] neg_lo:[0,0,1] neg_hi:[0,0,1]
	v_fma_mixlo_f16 v118, v22, s0, -v118 op_sel_hi:[0,0,1]
	v_cvt_pk_f16_f32 v115, v80, v81
	v_pk_mul_f32 v[80:81], v[36:37], s[0:1] op_sel_hi:[1,0]
	v_fma_mixlo_f16 v93, v39, s0, 0
	v_cvt_pk_f16_f32 v89, v80, v81
	v_cvt_f32_f16_e32 v80, v89
	v_cvt_f32_f16_sdwa v81, v89 dst_sel:DWORD dst_unused:UNUSED_PAD src0_sel:WORD_1
	v_fma_mixlo_f16 v95, v34, s0, 0
	ds_write_b64 v78, v[84:85] offset:2304
	v_fma_mixhi_f16 v118, v23, s0, -v119 op_sel_hi:[0,0,1]
	v_pk_fma_f32 v[80:81], v[36:37], s[0:1], v[80:81] op_sel_hi:[1,0,1] neg_lo:[0,0,1] neg_hi:[0,0,1]
	v_pk_mul_f32 v[84:85], v[8:9], s[0:1] op_sel_hi:[1,0]
	v_cvt_pk_f16_f32 v117, v80, v81
	v_pk_mul_f32 v[80:81], v[24:25], s[0:1] op_sel_hi:[1,0]
	v_fma_mixhi_f16 v114, v39, s0, -v93 op_sel_hi:[0,0,1]
	v_cvt_pk_f16_f32 v91, v80, v81
	v_cvt_f32_f16_e32 v80, v91
	v_cvt_f32_f16_sdwa v81, v91 dst_sel:DWORD dst_unused:UNUSED_PAD src0_sel:WORD_1
	v_fma_mixlo_f16 v116, v34, s0, -v95 op_sel_hi:[0,0,1]
	v_cvt_pk_f16_f32 v95, v84, v85
	ds_write_b64 v78, v[86:87] offset:32
	v_pk_fma_f32 v[80:81], v[24:25], s[0:1], v[80:81] op_sel_hi:[1,0,1] neg_lo:[0,0,1] neg_hi:[0,0,1]
	ds_write_b64 v78, v[88:89] offset:2336
	v_cvt_pk_f16_f32 v119, v80, v81
	v_pk_mul_f32 v[80:81], v[20:21], s[0:1] op_sel_hi:[1,0]
	ds_write_b64 v78, v[90:91] offset:64
	v_cvt_pk_f16_f32 v93, v80, v81
	ds_write_b64 v78, v[92:93] offset:2368
	ds_write_b64 v78, v[94:95] offset:96
	ds_read_b128 v[84:87], v77
	ds_read_b128 v[88:91], v77 offset:1152
	v_or_b32_e32 v0, v79, v72
	v_lshlrev_b64 v[98:99], 11, v[0:1]
	v_or_b32_e32 v0, v79, v132
	v_lshl_add_u64 v[100:101], v[68:69], 0, v[98:99]
	v_lshlrev_b64 v[102:103], 11, v[0:1]
	v_lshl_add_u64 v[104:105], v[68:69], 0, v[102:103]
	v_cvt_f32_f16_e32 v80, v93
	v_cvt_f32_f16_sdwa v81, v93 dst_sel:DWORD dst_unused:UNUSED_PAD src0_sel:WORD_1
	s_waitcnt lgkmcnt(1)
	global_store_dwordx4 v[100:101], v[84:87], off sc1
	s_waitcnt lgkmcnt(0)
	global_store_dwordx4 v[104:105], v[88:91], off sc1
	v_fma_mixlo_f16 v120, v18, s0, 0
	v_cvt_f32_f16_e32 v84, v95
	v_cvt_f32_f16_sdwa v85, v95 dst_sel:DWORD dst_unused:UNUSED_PAD src0_sel:WORD_1
	v_fma_mixlo_f16 v121, v19, s0, 0
	v_fma_mixlo_f16 v120, v18, s0, -v120 op_sel_hi:[0,0,1]
	v_pk_fma_f32 v[80:81], v[20:21], s[0:1], v[80:81] op_sel_hi:[1,0,1] neg_lo:[0,0,1] neg_hi:[0,0,1]
	v_pk_fma_f32 v[84:85], v[8:9], s[0:1], v[84:85] op_sel_hi:[1,0,1] neg_lo:[0,0,1] neg_hi:[0,0,1]
	v_fma_mixlo_f16 v97, v35, s0, 0
	v_fma_mixhi_f16 v120, v19, s0, -v121 op_sel_hi:[0,0,1]
	v_cvt_pk_f16_f32 v121, v80, v81
	v_cvt_pk_f16_f32 v81, v84, v85
	v_pk_mul_f32 v[84:85], v[4:5], s[0:1] op_sel_hi:[1,0]
	v_fma_mixhi_f16 v116, v35, s0, -v97 op_sel_hi:[0,0,1]
	v_cvt_pk_f16_f32 v97, v84, v85
	v_cvt_f32_f16_e32 v92, v97
	v_cvt_f32_f16_sdwa v93, v97 dst_sel:DWORD dst_unused:UNUSED_PAD src0_sel:WORD_1
	v_fma_mixlo_f16 v122, v6, s0, 0
	v_fma_mixlo_f16 v123, v7, s0, 0
	v_fma_mixlo_f16 v80, v6, s0, -v122 op_sel_hi:[0,0,1]
	v_fma_mixlo_f16 v124, v2, s0, 0
	v_fma_mixhi_f16 v80, v7, s0, -v123 op_sel_hi:[0,0,1]
	v_fma_mixlo_f16 v125, v3, s0, 0
	ds_write_b64 v78, v[112:113]
	ds_write_b64 v78, v[114:115] offset:32
	ds_write_b64 v78, v[118:119] offset:64
	ds_write_b64 v78, v[80:81] offset:96
	v_fma_mixlo_f16 v80, v2, s0, -v124 op_sel_hi:[0,0,1]
	ds_write_b64 v78, v[96:97] offset:2400
	v_pk_fma_f32 v[92:93], v[4:5], s[0:1], v[92:93] op_sel_hi:[1,0,1] neg_lo:[0,0,1] neg_hi:[0,0,1]
	v_fma_mixhi_f16 v80, v3, s0, -v125 op_sel_hi:[0,0,1]
	ds_read_b128 v[84:87], v77 offset:2304
	ds_read_b128 v[88:91], v77 offset:3456
	v_cvt_pk_f16_f32 v81, v92, v93
	v_or_b32_e32 v0, v79, v133
	ds_write_b64 v78, v[110:111] offset:2304
	ds_write_b64 v78, v[116:117] offset:2336
	ds_write_b64 v78, v[120:121] offset:2368
	ds_write_b64 v78, v[80:81] offset:2400
	v_lshlrev_b64 v[106:107], 11, v[0:1]
	v_or_b32_e32 v0, v79, v134
	ds_read_b128 v[78:81], v77
	v_lshl_add_u64 v[108:109], v[68:69], 0, v[106:107]
	v_lshlrev_b64 v[0:1], 11, v[0:1]
	v_lshl_add_u64 v[68:69], v[68:69], 0, v[0:1]
	s_waitcnt lgkmcnt(6)
	global_store_dwordx4 v[108:109], v[84:87], off sc1
	s_waitcnt lgkmcnt(5)
	global_store_dwordx4 v[68:69], v[88:91], off sc1
	v_lshl_add_u64 v[68:69], v[70:71], 0, v[98:99]
	ds_read_b128 v[84:87], v77 offset:1152
	s_waitcnt lgkmcnt(1)
	global_store_dwordx4 v[68:69], v[78:81], off sc1
	ds_read_b128 v[78:81], v77 offset:2304
	ds_read_b128 v[88:91], v77 offset:3456
	v_lshl_add_u64 v[68:69], v[70:71], 0, v[102:103]
	s_waitcnt lgkmcnt(2)
	global_store_dwordx4 v[68:69], v[84:87], off sc1
	v_lshl_add_u64 v[68:69], v[70:71], 0, v[106:107]
	v_lshl_add_u64 v[0:1], v[70:71], 0, v[0:1]
	s_waitcnt lgkmcnt(1)
	global_store_dwordx4 v[68:69], v[78:81], off sc1
	s_waitcnt lgkmcnt(0)
	global_store_dwordx4 v[0:1], v[88:91], off sc1
	s_cbranch_execnz .LBB5_7
.LBB5_9:
	s_cmp_lt_u32 s2, 4
	v_mov_b32_e32 v0, 0x38800000
	v_mov_b32_e32 v1, 0x37000000
	s_cselect_b64 vcc, -1, 0
	v_cndmask_b32_e32 v88, v0, v1, vcc
	v_lshlrev_b64 v[0:1], 10, v[66:67]
	v_lshlrev_b32_e32 v68, 1, v82
	v_lshlrev_b32_e32 v78, 4, v76
	v_or_b32_e32 v89, v0, v75
	v_mul_u32_u24_e32 v0, 0x240, v73
	v_add_u32_e32 v76, v74, v78
	s_movk_i32 s2, 0x90
	v_fma_mixlo_f16 v91, v88, v62, 0
	v_add3_u32 v73, v74, v68, v0
	v_fma_mixlo_f16 v92, v88, v63, 0
	v_fma_mixlo_f16 v93, v88, v64, 0
	v_fma_mixlo_f16 v94, v88, v65, 0
	v_fma_mixlo_f16 v95, v88, v58, 0
	v_fma_mixlo_f16 v96, v88, v59, 0
	v_fma_mixlo_f16 v97, v88, v60, 0
	v_fma_mixlo_f16 v98, v88, v61, 0
	v_fma_mixlo_f16 v99, v88, v54, 0
	v_fma_mixlo_f16 v100, v88, v55, 0
	v_fma_mixlo_f16 v101, v88, v56, 0
	v_fma_mixlo_f16 v102, v88, v57, 0
	v_fma_mixlo_f16 v103, v88, v50, 0
	v_fma_mixlo_f16 v104, v88, v51, 0
	v_fma_mixlo_f16 v105, v88, v52, 0
	v_fma_mixlo_f16 v106, v88, v53, 0
	v_fma_mixlo_f16 v107, v88, v46, 0
	v_fma_mixlo_f16 v108, v88, v47, 0
	v_fma_mixlo_f16 v109, v88, v48, 0
	v_fma_mixlo_f16 v110, v88, v49, 0
	v_fma_mixlo_f16 v111, v88, v42, 0
	v_fma_mixlo_f16 v112, v88, v43, 0
	v_fma_mixlo_f16 v113, v88, v44, 0
	v_fma_mixlo_f16 v114, v88, v45, 0
	v_fma_mixlo_f16 v115, v88, v38, 0
	v_fma_mixlo_f16 v116, v88, v39, 0
	v_fma_mixlo_f16 v117, v88, v40, 0
	v_fma_mixlo_f16 v118, v88, v41, 0
	v_fma_mixlo_f16 v119, v88, v34, 0
	v_fma_mixlo_f16 v120, v88, v35, 0
	v_fma_mixlo_f16 v121, v88, v36, 0
	v_fma_mixlo_f16 v122, v88, v37, 0
	v_mad_u32_u24 v90, v72, s2, v76
	ds_write_b16 v73, v91
	ds_write_b16 v73, v92 offset:144
	ds_write_b16 v73, v93 offset:288
	ds_write_b16 v73, v94 offset:432
	ds_write_b16 v73, v95 offset:32
	ds_write_b16 v73, v96 offset:176
	ds_write_b16 v73, v97 offset:320
	ds_write_b16 v73, v98 offset:464
	ds_write_b16 v73, v99 offset:64
	ds_write_b16 v73, v100 offset:208
	ds_write_b16 v73, v101 offset:352
	ds_write_b16 v73, v102 offset:496
	ds_write_b16 v73, v103 offset:96
	ds_write_b16 v73, v104 offset:240
	ds_write_b16 v73, v105 offset:384
	ds_write_b16 v73, v106 offset:528
	ds_write_b16 v73, v107 offset:2304
	ds_write_b16 v73, v108 offset:2448
	ds_write_b16 v73, v109 offset:2592
	ds_write_b16 v73, v110 offset:2736
	ds_write_b16 v73, v111 offset:2336
	ds_write_b16 v73, v112 offset:2480
	ds_write_b16 v73, v113 offset:2624
	ds_write_b16 v73, v114 offset:2768
	ds_write_b16 v73, v115 offset:2368
	ds_write_b16 v73, v116 offset:2512
	ds_write_b16 v73, v117 offset:2656
	ds_write_b16 v73, v118 offset:2800
	ds_write_b16 v73, v119 offset:2400
	ds_write_b16 v73, v120 offset:2544
	ds_write_b16 v73, v121 offset:2688
	ds_write_b16 v73, v122 offset:2832
	ds_read_b128 v[68:71], v90
	v_or_b32_e32 v123, 8, v72
	s_and_b64 s[0:1], vcc, exec
	v_mad_u32_u24 v124, v123, s2, v76
	s_cselect_b32 s1, s5, s9
	s_cselect_b32 s0, s4, s8
	v_mov_b32_e32 v79, 0
	v_or_b32_e32 v0, v89, v72
	ds_read_b128 v[74:77], v124
	v_lshl_add_u64 v[66:67], s[0:1], 0, v[78:79]
	v_lshlrev_b64 v[80:81], 7, v[0:1]
	v_lshl_add_u64 v[82:83], v[66:67], 0, v[80:81]
	v_or_b32_e32 v0, v89, v123
	s_waitcnt lgkmcnt(1)
	global_store_dwordx4 v[82:83], v[68:71], off sc1
	v_lshlrev_b64 v[82:83], 7, v[0:1]
	v_or_b32_e32 v125, 16, v72
	v_lshl_add_u64 v[68:69], v[66:67], 0, v[82:83]
	s_waitcnt lgkmcnt(0)
	global_store_dwordx4 v[68:69], v[74:77], off sc1
	ds_read_b128 v[68:71], v124 offset:1152
	v_or_b32_e32 v0, v89, v125
	v_lshlrev_b64 v[84:85], 7, v[0:1]
	v_lshl_add_u64 v[86:87], v[66:67], 0, v[84:85]
	ds_read_b128 v[74:77], v124 offset:2304
	s_waitcnt lgkmcnt(1)
	global_store_dwordx4 v[86:87], v[68:71], off sc1
	v_or_b32_e32 v86, 24, v72
	v_or_b32_e32 v0, v89, v86
	v_lshlrev_b64 v[68:69], 7, v[0:1]
	v_fma_mixlo_f16 v0, v88, v62, -v91 op_sel_hi:[0,0,1]
	ds_write_b16 v73, v0
	v_fma_mixlo_f16 v0, v88, v63, -v92 op_sel_hi:[0,0,1]
	ds_write_b16 v73, v0 offset:144
	v_fma_mixlo_f16 v0, v88, v64, -v93 op_sel_hi:[0,0,1]
	ds_write_b16 v73, v0 offset:288
	v_fma_mixlo_f16 v0, v88, v65, -v94 op_sel_hi:[0,0,1]
	ds_write_b16 v73, v0 offset:432
	v_fma_mixlo_f16 v0, v88, v58, -v95 op_sel_hi:[0,0,1]
	ds_write_b16 v73, v0 offset:32
	v_fma_mixlo_f16 v0, v88, v59, -v96 op_sel_hi:[0,0,1]
	ds_write_b16 v73, v0 offset:176
	v_fma_mixlo_f16 v0, v88, v60, -v97 op_sel_hi:[0,0,1]
	ds_write_b16 v73, v0 offset:320
	v_fma_mixlo_f16 v0, v88, v61, -v98 op_sel_hi:[0,0,1]
	ds_write_b16 v73, v0 offset:464
	v_fma_mixlo_f16 v0, v88, v54, -v99 op_sel_hi:[0,0,1]
	ds_write_b16 v73, v0 offset:64
	v_fma_mixlo_f16 v0, v88, v55, -v100 op_sel_hi:[0,0,1]
	ds_write_b16 v73, v0 offset:208
	v_fma_mixlo_f16 v0, v88, v56, -v101 op_sel_hi:[0,0,1]
	ds_write_b16 v73, v0 offset:352
	v_fma_mixlo_f16 v0, v88, v57, -v102 op_sel_hi:[0,0,1]
	ds_write_b16 v73, v0 offset:496
	v_fma_mixlo_f16 v0, v88, v50, -v103 op_sel_hi:[0,0,1]
	ds_write_b16 v73, v0 offset:96
	v_fma_mixlo_f16 v0, v88, v51, -v104 op_sel_hi:[0,0,1]
	ds_write_b16 v73, v0 offset:240
	v_fma_mixlo_f16 v0, v88, v52, -v105 op_sel_hi:[0,0,1]
	ds_write_b16 v73, v0 offset:384
	v_fma_mixlo_f16 v0, v88, v53, -v106 op_sel_hi:[0,0,1]
	ds_write_b16 v73, v0 offset:528
	v_fma_mixlo_f16 v0, v88, v46, -v107 op_sel_hi:[0,0,1]
	ds_write_b16 v73, v0 offset:2304
	v_fma_mixlo_f16 v0, v88, v47, -v108 op_sel_hi:[0,0,1]
	ds_write_b16 v73, v0 offset:2448
	v_fma_mixlo_f16 v0, v88, v48, -v109 op_sel_hi:[0,0,1]
	ds_write_b16 v73, v0 offset:2592
	v_fma_mixlo_f16 v0, v88, v49, -v110 op_sel_hi:[0,0,1]
	ds_write_b16 v73, v0 offset:2736
	v_fma_mixlo_f16 v0, v88, v42, -v111 op_sel_hi:[0,0,1]
	ds_write_b16 v73, v0 offset:2336
	v_fma_mixlo_f16 v0, v88, v43, -v112 op_sel_hi:[0,0,1]
	ds_write_b16 v73, v0 offset:2480
	v_fma_mixlo_f16 v0, v88, v44, -v113 op_sel_hi:[0,0,1]
	ds_write_b16 v73, v0 offset:2624
	v_fma_mixlo_f16 v0, v88, v45, -v114 op_sel_hi:[0,0,1]
	ds_write_b16 v73, v0 offset:2768
	v_fma_mixlo_f16 v0, v88, v38, -v115 op_sel_hi:[0,0,1]
	ds_write_b16 v73, v0 offset:2368
	v_fma_mixlo_f16 v0, v88, v39, -v116 op_sel_hi:[0,0,1]
	ds_write_b16 v73, v0 offset:2512
	v_fma_mixlo_f16 v0, v88, v40, -v117 op_sel_hi:[0,0,1]
	ds_write_b16 v73, v0 offset:2656
	v_fma_mixlo_f16 v0, v88, v41, -v118 op_sel_hi:[0,0,1]
	ds_write_b16 v73, v0 offset:2800
	v_fma_mixlo_f16 v0, v88, v34, -v119 op_sel_hi:[0,0,1]
	ds_write_b16 v73, v0 offset:2400
	v_fma_mixlo_f16 v0, v88, v35, -v120 op_sel_hi:[0,0,1]
	ds_write_b16 v73, v0 offset:2544
	v_fma_mixlo_f16 v0, v88, v36, -v121 op_sel_hi:[0,0,1]
	ds_write_b16 v73, v0 offset:2688
	v_fma_mixlo_f16 v0, v88, v37, -v122 op_sel_hi:[0,0,1]
	ds_write_b16 v73, v0 offset:2832
	ds_read_b128 v[34:37], v90
	s_cselect_b32 s1, s7, s11
	s_cselect_b32 s0, s6, s10
	v_lshl_add_u64 v[46:47], s[0:1], 0, v[78:79]
	v_lshl_add_u64 v[70:71], v[66:67], 0, v[68:69]
	v_lshl_add_u64 v[42:43], v[46:47], 0, v[80:81]
	ds_read_b128 v[38:41], v124
	s_waitcnt lgkmcnt(14)
	global_store_dwordx4 v[70:71], v[74:77], off sc1
	s_waitcnt lgkmcnt(1)
	global_store_dwordx4 v[42:43], v[34:37], off sc1
	ds_read_b128 v[34:37], v124 offset:1152
	ds_read_b128 v[42:45], v124 offset:2304
	v_lshl_add_u64 v[48:49], v[46:47], 0, v[82:83]
	s_waitcnt lgkmcnt(2)
	global_store_dwordx4 v[48:49], v[38:41], off sc1
	v_or_b32_e32 v52, 32, v89
	v_fma_mixlo_f16 v53, v88, v30, 0
	v_lshl_add_u64 v[38:39], v[46:47], 0, v[84:85]
	s_waitcnt lgkmcnt(1)
	global_store_dwordx4 v[38:39], v[34:37], off sc1
	v_fma_mixlo_f16 v54, v88, v31, 0
	v_fma_mixlo_f16 v55, v88, v32, 0
	v_lshl_add_u64 v[34:35], v[46:47], 0, v[68:69]
	v_fma_mixlo_f16 v56, v88, v33, 0
	v_fma_mixlo_f16 v57, v88, v26, 0
	v_fma_mixlo_f16 v58, v88, v27, 0
	v_fma_mixlo_f16 v59, v88, v28, 0
	v_fma_mixlo_f16 v60, v88, v29, 0
	v_fma_mixlo_f16 v61, v88, v22, 0
	v_fma_mixlo_f16 v62, v88, v23, 0
	v_fma_mixlo_f16 v63, v88, v24, 0
	v_fma_mixlo_f16 v64, v88, v25, 0
	v_fma_mixlo_f16 v65, v88, v18, 0
	v_fma_mixlo_f16 v68, v88, v19, 0
	v_fma_mixlo_f16 v69, v88, v20, 0
	v_fma_mixlo_f16 v70, v88, v21, 0
	v_fma_mixlo_f16 v71, v88, v14, 0
	v_fma_mixlo_f16 v74, v88, v15, 0
	v_fma_mixlo_f16 v75, v88, v16, 0
	v_fma_mixlo_f16 v76, v88, v17, 0
	v_fma_mixlo_f16 v77, v88, v10, 0
	v_fma_mixlo_f16 v78, v88, v11, 0
	v_fma_mixlo_f16 v79, v88, v12, 0
	v_fma_mixlo_f16 v80, v88, v13, 0
	v_fma_mixlo_f16 v81, v88, v6, 0
	v_fma_mixlo_f16 v82, v88, v7, 0
	v_fma_mixlo_f16 v83, v88, v8, 0
	v_fma_mixlo_f16 v84, v88, v9, 0
	v_fma_mixlo_f16 v85, v88, v2, 0
	v_fma_mixlo_f16 v87, v88, v3, 0
	v_fma_mixlo_f16 v89, v88, v4, 0
	v_fma_mixlo_f16 v91, v88, v5, 0
	ds_write_b16 v73, v53
	ds_write_b16 v73, v54 offset:144
	ds_write_b16 v73, v55 offset:288
	ds_write_b16 v73, v56 offset:432
	ds_write_b16 v73, v57 offset:32
	ds_write_b16 v73, v58 offset:176
	ds_write_b16 v73, v59 offset:320
	ds_write_b16 v73, v60 offset:464
	ds_write_b16 v73, v61 offset:64
	ds_write_b16 v73, v62 offset:208
	ds_write_b16 v73, v63 offset:352
	ds_write_b16 v73, v64 offset:496
	ds_write_b16 v73, v65 offset:96
	ds_write_b16 v73, v68 offset:240
	ds_write_b16 v73, v69 offset:384
	ds_write_b16 v73, v70 offset:528
	ds_write_b16 v73, v71 offset:2304
	ds_write_b16 v73, v74 offset:2448
	ds_write_b16 v73, v75 offset:2592
	ds_write_b16 v73, v76 offset:2736
	ds_write_b16 v73, v77 offset:2336
	ds_write_b16 v73, v78 offset:2480
	ds_write_b16 v73, v79 offset:2624
	ds_write_b16 v73, v80 offset:2768
	ds_write_b16 v73, v81 offset:2368
	ds_write_b16 v73, v82 offset:2512
	ds_write_b16 v73, v83 offset:2656
	ds_write_b16 v73, v84 offset:2800
	ds_write_b16 v73, v85 offset:2400
	ds_write_b16 v73, v87 offset:2544
	ds_write_b16 v73, v89 offset:2688
	ds_write_b16 v73, v91 offset:2832
	s_waitcnt lgkmcnt(14)
	global_store_dwordx4 v[34:35], v[42:45], off sc1
	ds_read_b128 v[34:37], v90
	v_or_b32_e32 v0, v52, v72
	ds_read_b128 v[38:41], v124
	v_lshlrev_b64 v[42:43], 7, v[0:1]
	v_lshl_add_u64 v[44:45], v[66:67], 0, v[42:43]
	v_or_b32_e32 v0, v52, v123
	s_waitcnt lgkmcnt(1)
	global_store_dwordx4 v[44:45], v[34:37], off sc1
	v_lshlrev_b64 v[44:45], 7, v[0:1]
	v_or_b32_e32 v0, v52, v125
	v_lshl_add_u64 v[34:35], v[66:67], 0, v[44:45]
	s_waitcnt lgkmcnt(0)
	global_store_dwordx4 v[34:35], v[38:41], off sc1
	ds_read_b128 v[34:37], v124 offset:1152
	v_lshlrev_b64 v[48:49], 7, v[0:1]
	v_lshl_add_u64 v[50:51], v[66:67], 0, v[48:49]
	v_or_b32_e32 v0, v52, v86
	ds_read_b128 v[38:41], v124 offset:2304
	s_waitcnt lgkmcnt(1)
	global_store_dwordx4 v[50:51], v[34:37], off sc1
	s_nop 1
	v_lshlrev_b64 v[34:35], 7, v[0:1]
	v_fma_mixlo_f16 v0, v88, v30, -v53 op_sel_hi:[0,0,1]
	ds_write_b16 v73, v0
	v_fma_mixlo_f16 v0, v88, v31, -v54 op_sel_hi:[0,0,1]
	ds_write_b16 v73, v0 offset:144
	v_fma_mixlo_f16 v0, v88, v32, -v55 op_sel_hi:[0,0,1]
	ds_write_b16 v73, v0 offset:288
	v_fma_mixlo_f16 v0, v88, v33, -v56 op_sel_hi:[0,0,1]
	ds_write_b16 v73, v0 offset:432
	v_fma_mixlo_f16 v0, v88, v26, -v57 op_sel_hi:[0,0,1]
	ds_write_b16 v73, v0 offset:32
	v_fma_mixlo_f16 v0, v88, v27, -v58 op_sel_hi:[0,0,1]
	ds_write_b16 v73, v0 offset:176
	v_fma_mixlo_f16 v0, v88, v28, -v59 op_sel_hi:[0,0,1]
	ds_write_b16 v73, v0 offset:320
	v_fma_mixlo_f16 v0, v88, v29, -v60 op_sel_hi:[0,0,1]
	ds_write_b16 v73, v0 offset:464
	v_fma_mixlo_f16 v0, v88, v22, -v61 op_sel_hi:[0,0,1]
	ds_write_b16 v73, v0 offset:64
	v_fma_mixlo_f16 v0, v88, v23, -v62 op_sel_hi:[0,0,1]
	ds_write_b16 v73, v0 offset:208
	v_fma_mixlo_f16 v0, v88, v24, -v63 op_sel_hi:[0,0,1]
	ds_write_b16 v73, v0 offset:352
	v_fma_mixlo_f16 v0, v88, v25, -v64 op_sel_hi:[0,0,1]
	ds_write_b16 v73, v0 offset:496
	v_fma_mixlo_f16 v0, v88, v18, -v65 op_sel_hi:[0,0,1]
	ds_write_b16 v73, v0 offset:96
	v_fma_mixlo_f16 v0, v88, v19, -v68 op_sel_hi:[0,0,1]
	ds_write_b16 v73, v0 offset:240
	v_fma_mixlo_f16 v0, v88, v20, -v69 op_sel_hi:[0,0,1]
	ds_write_b16 v73, v0 offset:384
	v_fma_mixlo_f16 v0, v88, v21, -v70 op_sel_hi:[0,0,1]
	ds_write_b16 v73, v0 offset:528
	v_fma_mixlo_f16 v0, v88, v14, -v71 op_sel_hi:[0,0,1]
	ds_write_b16 v73, v0 offset:2304
	v_fma_mixlo_f16 v0, v88, v15, -v74 op_sel_hi:[0,0,1]
	ds_write_b16 v73, v0 offset:2448
	v_fma_mixlo_f16 v0, v88, v16, -v75 op_sel_hi:[0,0,1]
	ds_write_b16 v73, v0 offset:2592
	v_fma_mixlo_f16 v0, v88, v17, -v76 op_sel_hi:[0,0,1]
	ds_write_b16 v73, v0 offset:2736
	v_fma_mixlo_f16 v0, v88, v10, -v77 op_sel_hi:[0,0,1]
	ds_write_b16 v73, v0 offset:2336
	v_fma_mixlo_f16 v0, v88, v11, -v78 op_sel_hi:[0,0,1]
	ds_write_b16 v73, v0 offset:2480
	v_fma_mixlo_f16 v0, v88, v12, -v79 op_sel_hi:[0,0,1]
	ds_write_b16 v73, v0 offset:2624
	v_fma_mixlo_f16 v0, v88, v13, -v80 op_sel_hi:[0,0,1]
	ds_write_b16 v73, v0 offset:2768
	v_fma_mixlo_f16 v0, v88, v6, -v81 op_sel_hi:[0,0,1]
	ds_write_b16 v73, v0 offset:2368
	v_fma_mixlo_f16 v0, v88, v7, -v82 op_sel_hi:[0,0,1]
	ds_write_b16 v73, v0 offset:2512
	v_fma_mixlo_f16 v0, v88, v8, -v83 op_sel_hi:[0,0,1]
	ds_write_b16 v73, v0 offset:2656
	v_fma_mixlo_f16 v0, v88, v9, -v84 op_sel_hi:[0,0,1]
	ds_write_b16 v73, v0 offset:2800
	v_fma_mixlo_f16 v0, v88, v2, -v85 op_sel_hi:[0,0,1]
	ds_write_b16 v73, v0 offset:2400
	v_fma_mixlo_f16 v0, v88, v3, -v87 op_sel_hi:[0,0,1]
	ds_write_b16 v73, v0 offset:2544
	v_fma_mixlo_f16 v0, v88, v4, -v89 op_sel_hi:[0,0,1]
	ds_write_b16 v73, v0 offset:2688
	v_fma_mixlo_f16 v0, v88, v5, -v91 op_sel_hi:[0,0,1]
	ds_write_b16 v73, v0 offset:2832
	ds_read_b128 v[0:3], v90
	v_lshl_add_u64 v[4:5], v[66:67], 0, v[34:35]
	s_waitcnt lgkmcnt(14)
	global_store_dwordx4 v[4:5], v[38:41], off sc1
	v_lshl_add_u64 v[8:9], v[46:47], 0, v[42:43]
	ds_read_b128 v[4:7], v124
	s_waitcnt lgkmcnt(1)
	global_store_dwordx4 v[8:9], v[0:3], off sc1
	ds_read_b128 v[0:3], v124 offset:1152
	ds_read_b128 v[8:11], v124 offset:2304
	v_lshl_add_u64 v[12:13], v[46:47], 0, v[44:45]
	s_waitcnt lgkmcnt(2)
	global_store_dwordx4 v[12:13], v[4:7], off sc1
	s_nop 1
	v_lshl_add_u64 v[4:5], v[46:47], 0, v[48:49]
	s_waitcnt lgkmcnt(1)
	global_store_dwordx4 v[4:5], v[0:3], off sc1
	s_nop 1
	v_lshl_add_u64 v[0:1], v[46:47], 0, v[34:35]
	s_waitcnt lgkmcnt(0)
	global_store_dwordx4 v[0:1], v[8:11], off sc1
	s_endpgm
	.p2alignl 8, 3212836864

.LBB6_9:
	s_mov_b32 s60, s14
	s_mov_b32 s61, s15
	s_mov_b32 s24, s60
	s_mov_b32 s25, s61
	s_load_dwordx2 s[28:29], s[0:1], 0x58
	s_load_dwordx2 s[30:31], s[0:1], 0x68
	s_load_dwordx2 s[32:33], s[0:1], 0x78
	v_and_b32_e32 v66, 63, v0
	v_lshrrev_b32_e32 v67, 6, v0
	v_and_b32_e32 v68, 15, v0
	v_bfe_u32 v69, v0, 4, 2
	v_mul_u32_u24_e32 v70, 0x2000, v67
	s_movk_i32 s2, 0x440
	v_mad_u32_u24 v71, v69, s2, v70
	v_lshl_add_u32 v71, v68, 2, v71
	v_lshrrev_b32_e32 v72, 4, v66
	s_movk_i32 s3, 0x110
	v_mad_u32_u24 v78, v72, s3, v70
	v_lshl_add_u32 v78, v68, 4, v78
	v_lshrrev_b32_e32 v73, 1, v67
	v_lshl_add_u32 v79, v73, 6, v72
	v_and_b32_e32 v73, 1, v67
	v_lshlrev_b32_e32 v73, 8, v73
	v_lshl_add_u32 v73, v79, 11, v73
	v_lshl_add_u32 v73, v68, 4, v73
	v_and_b32_e32 v72, 0x4f, v0
	v_lshlrev_b32_e32 v72, 2, v72
	s_waitcnt lgkmcnt(0)
	s_lshl_b32 s2, s25, 2
	s_add_u32 s28, s28, s2
	s_addc_u32 s29, s29, 0
	global_load_dword v74, v72, s[28:29]
	global_load_dword v75, v72, s[28:29] offset:64
	global_load_dword v76, v72, s[28:29] offset:128
	global_load_dword v77, v72, s[28:29] offset:192
	s_lshl_b32 s2, s24, 11
	s_lshl_b32 s3, s25, 2
	s_add_u32 s2, s2, s3
	s_add_u32 s34, s30, s2
	s_addc_u32 s35, s31, 0
	s_add_u32 s36, s32, s2
	s_addc_u32 s37, s33, 0
	s_mov_b32 s38, s34
	s_addc_u32 s39, s35, 0
	global_load_dwordx4 v[100:103], v73, s[38:39]
	s_add_u32 s38, s34, 0x2000
	s_addc_u32 s39, s35, 0
	global_load_dwordx4 v[104:107], v73, s[38:39]
	s_add_u32 s38, s34, 0x4000
	s_addc_u32 s39, s35, 0
	global_load_dwordx4 v[108:111], v73, s[38:39]
	s_add_u32 s38, s34, 0x6000
	s_addc_u32 s39, s35, 0
	global_load_dwordx4 v[112:115], v73, s[38:39]
	s_add_u32 s38, s34, 0x8000
	s_addc_u32 s39, s35, 0
	global_load_dwordx4 v[116:119], v73, s[38:39]
	s_add_u32 s38, s34, 0xa000
	s_addc_u32 s39, s35, 0
	global_load_dwordx4 v[120:123], v73, s[38:39]
	s_add_u32 s38, s34, 0xc000
	s_addc_u32 s39, s35, 0
	global_load_dwordx4 v[124:127], v73, s[38:39]
	s_add_u32 s38, s34, 0xe000
	s_addc_u32 s39, s35, 0
	global_load_dwordx4 v[128:131], v73, s[38:39]
	s_add_u32 s38, s34, 0x10000
	s_addc_u32 s39, s35, 0
	global_load_dwordx4 v[132:135], v73, s[38:39]
	s_add_u32 s38, s34, 0x12000
	s_addc_u32 s39, s35, 0
	global_load_dwordx4 v[136:139], v73, s[38:39]
	s_add_u32 s38, s34, 0x14000
	s_addc_u32 s39, s35, 0
	global_load_dwordx4 v[140:143], v73, s[38:39]
	s_add_u32 s38, s34, 0x16000
	s_addc_u32 s39, s35, 0
	global_load_dwordx4 v[144:147], v73, s[38:39]
	s_add_u32 s38, s34, 0x18000
	s_addc_u32 s39, s35, 0
	global_load_dwordx4 v[148:151], v73, s[38:39]
	s_add_u32 s38, s34, 0x1a000
	s_addc_u32 s39, s35, 0
	global_load_dwordx4 v[152:155], v73, s[38:39]
	s_add_u32 s38, s34, 0x1c000
	s_addc_u32 s39, s35, 0
	global_load_dwordx4 v[156:159], v73, s[38:39]
	s_add_u32 s38, s34, 0x1e000
	s_addc_u32 s39, s35, 0
	global_load_dwordx4 v[160:163], v73, s[38:39]
	s_waitcnt vmcnt(16)
	v_fmamk_f32 v62, v62, 0x35800000, v74
	v_fmamk_f32 v63, v63, 0x35800000, v74
	v_fmamk_f32 v64, v64, 0x35800000, v74
	v_fmamk_f32 v65, v65, 0x35800000, v74
	v_fmamk_f32 v58, v58, 0x35800000, v75
	v_fmamk_f32 v59, v59, 0x35800000, v75
	v_fmamk_f32 v60, v60, 0x35800000, v75
	v_fmamk_f32 v61, v61, 0x35800000, v75
	v_fmamk_f32 v54, v54, 0x35800000, v76
	v_fmamk_f32 v55, v55, 0x35800000, v76
	v_fmamk_f32 v56, v56, 0x35800000, v76
	v_fmamk_f32 v57, v57, 0x35800000, v76
	v_fmamk_f32 v50, v50, 0x35800000, v77
	v_fmamk_f32 v51, v51, 0x35800000, v77
	v_fmamk_f32 v52, v52, 0x35800000, v77
	v_fmamk_f32 v53, v53, 0x35800000, v77
	ds_write_b32 v71, v62
	ds_write_b32 v71, v63 offset:272
	ds_write_b32 v71, v64 offset:544
	ds_write_b32 v71, v65 offset:816
	ds_write_b32 v71, v58 offset:64
	ds_write_b32 v71, v59 offset:336
	ds_write_b32 v71, v60 offset:608
	ds_write_b32 v71, v61 offset:880
	ds_write_b32 v71, v54 offset:128
	ds_write_b32 v71, v55 offset:400
	ds_write_b32 v71, v56 offset:672
	ds_write_b32 v71, v57 offset:944
	ds_write_b32 v71, v50 offset:192
	ds_write_b32 v71, v51 offset:464
	ds_write_b32 v71, v52 offset:736
	ds_write_b32 v71, v53 offset:1008
	ds_read_b128 v[164:167], v78
	ds_read_b128 v[168:171], v78 offset:1088
	ds_read_b128 v[172:175], v78 offset:2176
	ds_read_b128 v[176:179], v78 offset:3264
	s_waitcnt lgkmcnt(0)
	s_waitcnt vmcnt(15)
	v_add_f32_e32 v164, v100, v164
	v_add_f32_e32 v165, v101, v165
	v_add_f32_e32 v166, v102, v166
	v_add_f32_e32 v167, v103, v167
	s_mov_b32 s38, s36
	s_addc_u32 s39, s37, 0
	global_store_dwordx4 v73, v[164:167], s[38:39] sc1
	s_waitcnt vmcnt(15)
	v_add_f32_e32 v168, v104, v168
	v_add_f32_e32 v169, v105, v169
	v_add_f32_e32 v170, v106, v170
	v_add_f32_e32 v171, v107, v171
	s_add_u32 s38, s36, 0x2000
	s_addc_u32 s39, s37, 0
	global_store_dwordx4 v73, v[168:171], s[38:39] sc1
	s_waitcnt vmcnt(15)
	v_add_f32_e32 v172, v108, v172
	v_add_f32_e32 v173, v109, v173
	v_add_f32_e32 v174, v110, v174
	v_add_f32_e32 v175, v111, v175
	s_add_u32 s38, s36, 0x4000
	s_addc_u32 s39, s37, 0
	global_store_dwordx4 v73, v[172:175], s[38:39] sc1
	s_waitcnt vmcnt(15)
	v_add_f32_e32 v176, v112, v176
	v_add_f32_e32 v177, v113, v177
	v_add_f32_e32 v178, v114, v178
	v_add_f32_e32 v179, v115, v179
	s_add_u32 s38, s36, 0x6000
	s_addc_u32 s39, s37, 0
	global_store_dwordx4 v73, v[176:179], s[38:39] sc1
	v_fmamk_f32 v46, v46, 0x35800000, v74
	v_fmamk_f32 v47, v47, 0x35800000, v74
	v_fmamk_f32 v48, v48, 0x35800000, v74
	v_fmamk_f32 v49, v49, 0x35800000, v74
	v_fmamk_f32 v42, v42, 0x35800000, v75
	v_fmamk_f32 v43, v43, 0x35800000, v75
	v_fmamk_f32 v44, v44, 0x35800000, v75
	v_fmamk_f32 v45, v45, 0x35800000, v75
	v_fmamk_f32 v38, v38, 0x35800000, v76
	v_fmamk_f32 v39, v39, 0x35800000, v76
	v_fmamk_f32 v40, v40, 0x35800000, v76
	v_fmamk_f32 v41, v41, 0x35800000, v76
	v_fmamk_f32 v34, v34, 0x35800000, v77
	v_fmamk_f32 v35, v35, 0x35800000, v77
	v_fmamk_f32 v36, v36, 0x35800000, v77
	v_fmamk_f32 v37, v37, 0x35800000, v77
	ds_write_b32 v71, v46
	ds_write_b32 v71, v47 offset:272
	ds_write_b32 v71, v48 offset:544
	ds_write_b32 v71, v49 offset:816
	ds_write_b32 v71, v42 offset:64
	ds_write_b32 v71, v43 offset:336
	ds_write_b32 v71, v44 offset:608
	ds_write_b32 v71, v45 offset:880
	ds_write_b32 v71, v38 offset:128
	ds_write_b32 v71, v39 offset:400
	ds_write_b32 v71, v40 offset:672
	ds_write_b32 v71, v41 offset:944
	ds_write_b32 v71, v34 offset:192
	ds_write_b32 v71, v35 offset:464
	ds_write_b32 v71, v36 offset:736
	ds_write_b32 v71, v37 offset:1008
	ds_read_b128 v[180:183], v78
	ds_read_b128 v[184:187], v78 offset:1088
	ds_read_b128 v[188:191], v78 offset:2176
	ds_read_b128 v[192:195], v78 offset:3264
	s_waitcnt lgkmcnt(0)
	s_waitcnt vmcnt(15)
	v_add_f32_e32 v180, v116, v180
	v_add_f32_e32 v181, v117, v181
	v_add_f32_e32 v182, v118, v182
	v_add_f32_e32 v183, v119, v183
	s_add_u32 s38, s36, 0x8000
	s_addc_u32 s39, s37, 0
	global_store_dwordx4 v73, v[180:183], s[38:39] sc1
	s_waitcnt vmcnt(15)
	v_add_f32_e32 v184, v120, v184
	v_add_f32_e32 v185, v121, v185
	v_add_f32_e32 v186, v122, v186
	v_add_f32_e32 v187, v123, v187
	s_add_u32 s38, s36, 0xa000
	s_addc_u32 s39, s37, 0
	global_store_dwordx4 v73, v[184:187], s[38:39] sc1
	s_waitcnt vmcnt(15)
	v_add_f32_e32 v188, v124, v188
	v_add_f32_e32 v189, v125, v189
	v_add_f32_e32 v190, v126, v190
	v_add_f32_e32 v191, v127, v191
	s_add_u32 s38, s36, 0xc000
	s_addc_u32 s39, s37, 0
	global_store_dwordx4 v73, v[188:191], s[38:39] sc1
	s_waitcnt vmcnt(15)
	v_add_f32_e32 v192, v128, v192
	v_add_f32_e32 v193, v129, v193
	v_add_f32_e32 v194, v130, v194
	v_add_f32_e32 v195, v131, v195
	s_add_u32 s38, s36, 0xe000
	s_addc_u32 s39, s37, 0
	global_store_dwordx4 v73, v[192:195], s[38:39] sc1
	v_fmamk_f32 v30, v30, 0x35800000, v74
	v_fmamk_f32 v31, v31, 0x35800000, v74
	v_fmamk_f32 v32, v32, 0x35800000, v74
	v_fmamk_f32 v33, v33, 0x35800000, v74
	v_fmamk_f32 v26, v26, 0x35800000, v75
	v_fmamk_f32 v27, v27, 0x35800000, v75
	v_fmamk_f32 v28, v28, 0x35800000, v75
	v_fmamk_f32 v29, v29, 0x35800000, v75
	v_fmamk_f32 v22, v22, 0x35800000, v76
	v_fmamk_f32 v23, v23, 0x35800000, v76
	v_fmamk_f32 v24, v24, 0x35800000, v76
	v_fmamk_f32 v25, v25, 0x35800000, v76
	v_fmamk_f32 v18, v18, 0x35800000, v77
	v_fmamk_f32 v19, v19, 0x35800000, v77
	v_fmamk_f32 v20, v20, 0x35800000, v77
	v_fmamk_f32 v21, v21, 0x35800000, v77
	ds_write_b32 v71, v30
	ds_write_b32 v71, v31 offset:272
	ds_write_b32 v71, v32 offset:544
	ds_write_b32 v71, v33 offset:816
	ds_write_b32 v71, v26 offset:64
	ds_write_b32 v71, v27 offset:336
	ds_write_b32 v71, v28 offset:608
	ds_write_b32 v71, v29 offset:880
	ds_write_b32 v71, v22 offset:128
	ds_write_b32 v71, v23 offset:400
	ds_write_b32 v71, v24 offset:672
	ds_write_b32 v71, v25 offset:944
	ds_write_b32 v71, v18 offset:192
	ds_write_b32 v71, v19 offset:464
	ds_write_b32 v71, v20 offset:736
	ds_write_b32 v71, v21 offset:1008
	ds_read_b128 v[164:167], v78
	ds_read_b128 v[168:171], v78 offset:1088
	ds_read_b128 v[172:175], v78 offset:2176
	ds_read_b128 v[176:179], v78 offset:3264
	s_waitcnt lgkmcnt(0)
	s_waitcnt vmcnt(15)
	v_add_f32_e32 v164, v132, v164
	v_add_f32_e32 v165, v133, v165
	v_add_f32_e32 v166, v134, v166
	v_add_f32_e32 v167, v135, v167
	s_add_u32 s38, s36, 0x10000
	s_addc_u32 s39, s37, 0
	global_store_dwordx4 v73, v[164:167], s[38:39] sc1
	s_waitcnt vmcnt(15)
	v_add_f32_e32 v168, v136, v168
	v_add_f32_e32 v169, v137, v169
	v_add_f32_e32 v170, v138, v170
	v_add_f32_e32 v171, v139, v171
	s_add_u32 s38, s36, 0x12000
	s_addc_u32 s39, s37, 0
	global_store_dwordx4 v73, v[168:171], s[38:39] sc1
	s_waitcnt vmcnt(15)
	v_add_f32_e32 v172, v140, v172
	v_add_f32_e32 v173, v141, v173
	v_add_f32_e32 v174, v142, v174
	v_add_f32_e32 v175, v143, v175
	s_add_u32 s38, s36, 0x14000
	s_addc_u32 s39, s37, 0
	global_store_dwordx4 v73, v[172:175], s[38:39] sc1
	s_waitcnt vmcnt(15)
	v_add_f32_e32 v176, v144, v176
	v_add_f32_e32 v177, v145, v177
	v_add_f32_e32 v178, v146, v178
	v_add_f32_e32 v179, v147, v179
	s_add_u32 s38, s36, 0x16000
	s_addc_u32 s39, s37, 0
	global_store_dwordx4 v73, v[176:179], s[38:39] sc1
	v_fmamk_f32 v14, v14, 0x35800000, v74
	v_fmamk_f32 v15, v15, 0x35800000, v74
	v_fmamk_f32 v16, v16, 0x35800000, v74
	v_fmamk_f32 v17, v17, 0x35800000, v74
	v_fmamk_f32 v10, v10, 0x35800000, v75
	v_fmamk_f32 v11, v11, 0x35800000, v75
	v_fmamk_f32 v12, v12, 0x35800000, v75
	v_fmamk_f32 v13, v13, 0x35800000, v75
	v_fmamk_f32 v6, v6, 0x35800000, v76
	v_fmamk_f32 v7, v7, 0x35800000, v76
	v_fmamk_f32 v8, v8, 0x35800000, v76
	v_fmamk_f32 v9, v9, 0x35800000, v76
	v_fmamk_f32 v2, v2, 0x35800000, v77
	v_fmamk_f32 v3, v3, 0x35800000, v77
	v_fmamk_f32 v4, v4, 0x35800000, v77
	v_fmamk_f32 v5, v5, 0x35800000, v77
	ds_write_b32 v71, v14
	ds_write_b32 v71, v15 offset:272
	ds_write_b32 v71, v16 offset:544
	ds_write_b32 v71, v17 offset:816
	ds_write_b32 v71, v10 offset:64
	ds_write_b32 v71, v11 offset:336
	ds_write_b32 v71, v12 offset:608
	ds_write_b32 v71, v13 offset:880
	ds_write_b32 v71, v6 offset:128
	ds_write_b32 v71, v7 offset:400
	ds_write_b32 v71, v8 offset:672
	ds_write_b32 v71, v9 offset:944
	ds_write_b32 v71, v2 offset:192
	ds_write_b32 v71, v3 offset:464
	ds_write_b32 v71, v4 offset:736
	ds_write_b32 v71, v5 offset:1008
	ds_read_b128 v[180:183], v78
	ds_read_b128 v[184:187], v78 offset:1088
	ds_read_b128 v[188:191], v78 offset:2176
	ds_read_b128 v[192:195], v78 offset:3264
	s_waitcnt lgkmcnt(0)
	s_waitcnt vmcnt(15)
	v_add_f32_e32 v180, v148, v180
	v_add_f32_e32 v181, v149, v181
	v_add_f32_e32 v182, v150, v182
	v_add_f32_e32 v183, v151, v183
	s_add_u32 s38, s36, 0x18000
	s_addc_u32 s39, s37, 0
	global_store_dwordx4 v73, v[180:183], s[38:39] sc1
	s_waitcnt vmcnt(15)
	v_add_f32_e32 v184, v152, v184
	v_add_f32_e32 v185, v153, v185
	v_add_f32_e32 v186, v154, v186
	v_add_f32_e32 v187, v155, v187
	s_add_u32 s38, s36, 0x1a000
	s_addc_u32 s39, s37, 0
	global_store_dwordx4 v73, v[184:187], s[38:39] sc1
	s_waitcnt vmcnt(15)
	v_add_f32_e32 v188, v156, v188
	v_add_f32_e32 v189, v157, v189
	v_add_f32_e32 v190, v158, v190
	v_add_f32_e32 v191, v159, v191
	s_add_u32 s38, s36, 0x1c000
	s_addc_u32 s39, s37, 0
	global_store_dwordx4 v73, v[188:191], s[38:39] sc1
	s_waitcnt vmcnt(15)
	v_add_f32_e32 v192, v160, v192
	v_add_f32_e32 v193, v161, v193
	v_add_f32_e32 v194, v162, v194
	v_add_f32_e32 v195, v163, v195
	s_add_u32 s38, s36, 0x1e000
	s_addc_u32 s39, s37, 0
	global_store_dwordx4 v73, v[192:195], s[38:39] sc1
	s_endpgm
	.p2alignl 8, 3212836864

_Z18fused_router_wprepILb1EEvPKfS1_S1_PKiPfS4_PiS5_S5_S5_S4_S1_PDF16_S6_S1_S6_:
	s_cmpk_gt_i32 s2, 0xff
	s_mov_b64 s[4:5], -1
	s_cbranch_scc0 .LBB7_6
	s_cmpk_gt_u32 s2, 0x8ff
	v_lshrrev_b32_e32 v1, 4, v0
	v_lshlrev_b32_e32 v2, 4, v0
	s_cbranch_scc0 .LBB7_3
	s_load_dwordx4 s[4:7], s[0:1], 0x70
	s_add_i32 s3, s2, 0xfffff700
	s_lshr_b32 s10, s3, 8
	s_lshl_b32 s3, s2, 3
	s_lshl_b32 s8, s2, 6
	s_mov_b32 s11, 0
	s_and_b32 s3, s3, 0x7c0
	s_and_b32 s12, s8, 0x1c0
	s_lshl_b64 s[8:9], s[10:11], 9
	s_lshl_b64 s[10:11], s[10:11], 22
	s_waitcnt lgkmcnt(0)
	s_add_u32 s4, s4, s10
	s_addc_u32 s5, s5, s11
	s_lshl_b32 s10, s12, 2
	s_add_u32 s4, s4, s10
	s_addc_u32 s5, s5, 0
	v_and_b32_e32 v20, 0xf0, v2
	v_mov_b32_e32 v21, 0
	v_or_b32_e32 v3, s3, v1
	v_lshl_add_u64 v[16:17], s[4:5], 0, v[20:21]
	v_lshlrev_b32_e32 v18, 11, v3
	v_mov_b32_e32 v19, v21
	s_movk_i32 s4, 0x104
	v_lshl_add_u64 v[12:13], v[16:17], 0, v[18:19]
	v_mad_u32_u24 v3, v1, s4, v20
	v_or_b32_e32 v20, 0x8000, v18
	v_lshl_add_u64 v[14:15], v[16:17], 0, v[20:21]
	global_load_dwordx4 v[4:7], v[12:13], off nt
	global_load_dwordx4 v[8:11], v[14:15], off nt
	v_or_b32_e32 v20, 0x10000, v18
	v_lshl_add_u64 v[12:13], v[16:17], 0, v[20:21]
	global_load_dwordx4 v[12:15], v[12:13], off nt
	v_or_b32_e32 v20, 0x18000, v18
	v_lshl_add_u64 v[16:17], v[16:17], 0, v[20:21]
	global_load_dwordx4 v[16:19], v[16:17], off nt
	v_lshrrev_b32_e32 v20, 3, v0
	v_and_b32_e32 v26, 7, v0
	s_movk_i32 s5, 0x820
	v_lshlrev_b32_e32 v22, 2, v20
	v_add_u32_e32 v27, 0x1040, v3
	v_add_u32_e32 v28, 0x1048, v3
	v_add_u32_e32 v29, 0x2080, v3
	v_add_u32_e32 v30, 0x2088, v3
	v_add_u32_e32 v31, 0x30c0, v3
	v_mad_u32_u24 v33, v26, s5, v22
	s_or_b32 s5, s8, s12
	v_add_u32_e32 v32, 0x30c8, v3
	v_add_u32_e32 v34, 0x400, v33
	v_or_b32_e32 v22, s5, v20
	v_lshlrev_b32_e32 v20, 4, v26
	s_mov_b32 s4, 0x45800000
	s_lshl_b32 s3, s3, 1
	s_add_u32 s6, s6, s3
	v_mov_b32_e32 v23, s9
	s_addc_u32 s7, s7, 0
	v_lshlrev_b64 v[24:25], 12, v[22:23]
	v_lshl_add_u64 v[20:21], s[6:7], 0, v[20:21]
	v_lshl_add_u64 v[24:25], v[20:21], 0, v[24:25]
	v_or_b32_e32 v22, 32, v22
	s_waitcnt vmcnt(3)
	ds_write2_b32 v3, v4, v5 offset1:1
	ds_write2_b32 v3, v6, v7 offset0:2 offset1:3
	s_waitcnt vmcnt(2)
	ds_write2_b32 v27, v8, v9 offset1:1
	ds_write2_b32 v28, v10, v11 offset1:1
	s_waitcnt vmcnt(1)
	ds_write2_b32 v29, v12, v13 offset1:1
	ds_write2_b32 v30, v14, v15 offset1:1
	s_waitcnt vmcnt(0)
	ds_write2_b32 v31, v16, v17 offset1:1
	ds_write2_b32 v32, v18, v19 offset1:1
	s_waitcnt lgkmcnt(0)
	s_barrier
	ds_read2_b32 v[4:5], v33 offset1:32
	ds_read2_b32 v[26:27], v33 offset0:65 offset1:97
	ds_read2_b32 v[6:7], v33 offset0:130 offset1:162
	ds_read2_b32 v[28:29], v33 offset0:195 offset1:227
	ds_read2_b32 v[8:9], v34 offset0:4 offset1:36
	ds_read2_b32 v[30:31], v34 offset0:69 offset1:101
	ds_read2_b32 v[10:11], v34 offset0:134 offset1:166
	ds_read2_b32 v[12:13], v34 offset0:199 offset1:231
	s_waitcnt lgkmcnt(6)
	v_mov_b32_e32 v14, v26
	s_waitcnt lgkmcnt(5)
	v_mov_b32_e32 v15, v6
	s_waitcnt lgkmcnt(4)
	v_mov_b32_e32 v16, v28
	s_waitcnt lgkmcnt(3)
	v_mov_b32_e32 v17, v8
	s_waitcnt lgkmcnt(2)
	v_mov_b32_e32 v18, v30
	s_waitcnt lgkmcnt(1)
	v_mov_b32_e32 v19, v10
	v_fma_mixlo_f16 v3, v4, s4, 0
	v_fma_mixlo_f16 v10, v5, s4, 0
	v_mov_b32_e32 v6, v27
	v_pk_mul_f32 v[4:5], v[14:15], s[4:5] op_sel_hi:[1,0]
	v_pk_mul_f32 v[14:15], v[16:17], s[4:5] op_sel_hi:[1,0]
	v_pk_mul_f32 v[16:17], v[18:19], s[4:5] op_sel_hi:[1,0]
	v_mov_b32_e32 v8, v29
	v_pk_mul_f32 v[6:7], v[6:7], s[4:5] op_sel_hi:[1,0]
	v_cvt_pk_f16_f32 v14, v14, v15
	v_cvt_pk_f16_f32 v15, v16, v17
	v_pk_mul_f32 v[8:9], v[8:9], s[4:5] op_sel_hi:[1,0]
	v_cvt_pk_f16_f32 v5, v4, v5
	v_cvt_pk_f16_f32 v16, v6, v7
	v_lshrrev_b32_e32 v7, 16, v15
	v_cvt_pk_f16_f32 v17, v8, v9
	v_pack_b32_f16 v4, v3, v5
	v_alignbit_b32 v5, v14, v5, 16
	v_alignbit_b32 v6, v15, v14, 16
	v_pack_b32_f16 v8, v10, v16
	s_waitcnt lgkmcnt(0)
	v_fma_mixhi_f16 v7, v12, s4, 0
	v_mov_b32_e32 v10, v31
	global_store_dwordx4 v[24:25], v[4:7], off sc1
	v_alignbit_b32 v9, v17, v16, 16
	s_nop 0
	v_pk_mul_f32 v[4:5], v[10:11], s[4:5] op_sel_hi:[1,0]
	s_nop 0
	v_cvt_pk_f16_f32 v3, v4, v5
	v_lshrrev_b32_e32 v11, 16, v3
	v_lshlrev_b64 v[4:5], 12, v[22:23]
	v_alignbit_b32 v10, v3, v17, 16
	v_fma_mixhi_f16 v11, v13, s4, 0
	v_lshl_add_u64 v[4:5], v[20:21], 0, v[4:5]
	global_store_dwordx4 v[4:5], v[8:11], off sc1
	s_mov_b64 s[4:5], 0
.LBB7_3:
	s_andn2_b64 vcc, exec, s[4:5]
	s_cbranch_vccnz .LBB7_5
	s_load_dwordx4 s[4:7], s[0:1], 0x58
	s_load_dwordx2 s[8:9], s[0:1], 0x68
	s_add_i32 s3, s2, 0xffffff00
	s_lshr_b32 s12, s3, 8
	s_lshl_b32 s3, s2, 1
	s_lshl_b32 s10, s2, 6
	s_mov_b32 s13, 0
	s_and_b32 s3, s3, 0x1c0
	s_and_b32 s14, s10, 0x7c0
	s_lshl_b64 s[10:11], s[12:13], 11
	s_lshl_b64 s[12:13], s[12:13], 22
	s_waitcnt lgkmcnt(0)
	s_add_u32 s4, s4, s12
	s_addc_u32 s5, s5, s13
	s_lshl_b32 s12, s14, 2
	s_add_u32 s4, s4, s12
	s_addc_u32 s5, s5, 0
	v_and_b32_e32 v14, 0xf0, v2
	v_mov_b32_e32 v15, 0
	v_or_b32_e32 v2, s3, v1
	v_lshl_add_u64 v[16:17], s[4:5], 0, v[14:15]
	v_lshlrev_b32_e32 v18, 13, v2
	v_mov_b32_e32 v19, v15
	s_movk_i32 s4, 0x104
	v_lshl_add_u64 v[10:11], v[16:17], 0, v[18:19]
	v_mad_u32_u24 v1, v1, s4, v14
	v_or_b32_e32 v14, 0x20000, v18
	v_lshl_add_u64 v[12:13], v[16:17], 0, v[14:15]
	global_load_dwordx4 v[2:5], v[10:11], off nt
	global_load_dwordx4 v[6:9], v[12:13], off nt
	v_or_b32_e32 v14, 0x40000, v18
	v_lshl_add_u64 v[10:11], v[16:17], 0, v[14:15]
	global_load_dwordx4 v[10:13], v[10:11], off nt
	v_or_b32_e32 v14, 0x60000, v18
	v_lshl_add_u64 v[14:15], v[16:17], 0, v[14:15]
	global_load_dwordx4 v[14:17], v[14:15], off nt
	v_lshrrev_b32_e32 v18, 3, v0
	v_and_b32_e32 v34, 7, v0
	s_movk_i32 s5, 0x820
	v_lshlrev_b32_e32 v19, 2, v18
	v_mad_u32_u24 v19, v34, s5, v19
	v_add_u32_e32 v22, 0x4100, v1
	v_add_u32_e32 v23, 0x4108, v1
	v_add_u32_e32 v29, 0x4000, v19
	v_add_u32_e32 v24, 0x5140, v1
	v_add_u32_e32 v25, 0x5148, v1
	v_add_u32_e32 v26, 0x6180, v1
	v_add_u32_e32 v27, 0x6188, v1
	v_add_u32_e32 v28, 0x71c0, v1
	v_add_u32_e32 v1, 0x71c8, v1
	v_add_u32_e32 v30, 0x4400, v19
	v_add_u32_e32 v31, 0x4800, v19
	s_mov_b32 s4, 0x45800000
	s_or_b32 s5, s10, s14
	v_mov_b32_e32 v19, s11
	s_lshl_b32 s3, s3, 1
	v_or_b32_e32 v18, s5, v18
	v_lshlrev_b64 v[20:21], 10, v[18:19]
	v_or_b32_e32 v18, 32, v18
	s_waitcnt vmcnt(3)
	ds_write2_b32 v22, v2, v3 offset1:1
	ds_write2_b32 v23, v4, v5 offset1:1
	s_waitcnt vmcnt(2)
	ds_write2_b32 v24, v6, v7 offset1:1
	ds_write2_b32 v25, v8, v9 offset1:1
	s_waitcnt vmcnt(1)
	ds_write2_b32 v26, v10, v11 offset1:1
	ds_write2_b32 v27, v12, v13 offset1:1
	s_waitcnt vmcnt(0)
	ds_write2_b32 v28, v14, v15 offset1:1
	ds_write2_b32 v1, v16, v17 offset1:1
	s_waitcnt lgkmcnt(0)
	s_barrier
	ds_read2_b32 v[10:11], v29 offset0:64 offset1:96
	ds_read2_b32 v[12:13], v29 offset0:129 offset1:161
	ds_read2_b32 v[36:37], v29 offset0:194 offset1:226
	ds_read2_b32 v[14:15], v30 offset0:3 offset1:35
	ds_read2_b32 v[38:39], v30 offset0:68 offset1:100
	ds_read2_b32 v[16:17], v30 offset0:133 offset1:165
	ds_read2_b32 v[40:41], v30 offset0:198 offset1:230
	ds_read2_b32 v[22:23], v31 offset0:7 offset1:39
	s_waitcnt lgkmcnt(5)
	v_mov_b32_e32 v4, v36
	s_waitcnt lgkmcnt(4)
	v_mov_b32_e32 v5, v14
	s_waitcnt lgkmcnt(3)
	v_mov_b32_e32 v24, v38
	s_waitcnt lgkmcnt(2)
	v_mov_b32_e32 v25, v16
	s_waitcnt lgkmcnt(1)
	v_mov_b32_e32 v26, v40
	s_waitcnt lgkmcnt(0)
	v_mov_b32_e32 v27, v22
	v_pk_mul_f32 v[8:9], v[4:5], s[4:5] op_sel_hi:[1,0]
	v_pk_mul_f32 v[28:29], v[24:25], s[4:5] op_sel_hi:[1,0]
	v_pk_mul_f32 v[30:31], v[26:27], s[4:5] op_sel_hi:[1,0]
	v_cvt_pk_f16_f32 v7, v8, v9
	v_cvt_pk_f16_f32 v8, v28, v29
	v_cvt_pk_f16_f32 v9, v30, v31
	v_cvt_f32_f16_e32 v28, v7
	v_cvt_f32_f16_sdwa v29, v7 dst_sel:DWORD dst_unused:UNUSED_PAD src0_sel:WORD_1
	v_cvt_f32_f16_e32 v30, v8
	v_cvt_f32_f16_sdwa v31, v8 dst_sel:DWORD dst_unused:UNUSED_PAD src0_sel:WORD_1
	v_cvt_f32_f16_e32 v32, v9
	v_cvt_f32_f16_sdwa v33, v9 dst_sel:DWORD dst_unused:UNUSED_PAD src0_sel:WORD_1
	v_mul_f32_e32 v1, 0x45800000, v10
	v_mul_f32_e32 v3, 0x45800000, v12
	v_cvt_pk_f16_f32 v6, v1, v3
	v_lshl_or_b32 v1, v34, 4, s3
	v_fma_mixlo_f16 v2, v10, s4, 0
	v_pk_fma_f32 v[4:5], v[4:5], s[4:5], v[28:29] op_sel_hi:[1,0,1] neg_lo:[0,0,1] neg_hi:[0,0,1]
	v_pk_fma_f32 v[24:25], v[24:25], s[4:5], v[30:31] op_sel_hi:[1,0,1] neg_lo:[0,0,1] neg_hi:[0,0,1]
	v_or_b32_e32 v20, v20, v1
	v_fma_mixlo_f16 v35, v12, s4, 0
	v_fma_mixlo_f16 v2, v10, s4, -v2 op_sel_hi:[0,0,1]
	v_pk_fma_f32 v[26:27], v[26:27], s[4:5], v[32:33] op_sel_hi:[1,0,1] neg_lo:[0,0,1] neg_hi:[0,0,1]
	v_cvt_pk_f16_f32 v3, v4, v5
	v_cvt_pk_f16_f32 v4, v24, v25
	v_lshl_add_u64 v[24:25], s[6:7], 0, v[20:21]
	v_fma_mixhi_f16 v2, v12, s4, -v35 op_sel_hi:[0,0,1]
	v_cvt_pk_f16_f32 v5, v26, v27
	global_store_dwordx4 v[24:25], v[6:9], off sc1
	v_mov_b32_e32 v14, v37
	v_mov_b32_e32 v16, v39
	v_lshl_add_u64 v[6:7], s[8:9], 0, v[20:21]
	global_store_dwordx4 v[6:7], v[2:5], off sc1
	v_fma_mixlo_f16 v8, v13, s4, 0
	v_mov_b32_e32 v22, v41
	v_fma_mixlo_f16 v2, v11, s4, 0
	v_fma_mixlo_f16 v2, v11, s4, -v2 op_sel_hi:[0,0,1]
	v_pk_mul_f32 v[4:5], v[14:15], s[4:5] op_sel_hi:[1,0]
	v_mul_f32_e32 v6, 0x45800000, v13
	v_cvt_pk_f16_f32 v7, v4, v5
	v_fma_mixhi_f16 v2, v13, s4, -v8 op_sel_hi:[0,0,1]
	v_pk_mul_f32 v[8:9], v[16:17], s[4:5] op_sel_hi:[1,0]
	v_pk_mul_f32 v[12:13], v[22:23], s[4:5] op_sel_hi:[1,0]
	v_cvt_f32_f16_e32 v4, v7
	v_cvt_f32_f16_sdwa v5, v7 dst_sel:DWORD dst_unused:UNUSED_PAD src0_sel:WORD_1
	v_cvt_pk_f16_f32 v8, v8, v9
	v_cvt_pk_f16_f32 v9, v12, v13
	v_mul_f32_e32 v3, 0x45800000, v11
	v_cvt_f32_f16_e32 v10, v8
	v_cvt_f32_f16_sdwa v11, v8 dst_sel:DWORD dst_unused:UNUSED_PAD src0_sel:WORD_1
	v_cvt_f32_f16_e32 v12, v9
	v_cvt_f32_f16_sdwa v13, v9 dst_sel:DWORD dst_unused:UNUSED_PAD src0_sel:WORD_1
	v_pk_fma_f32 v[4:5], v[14:15], s[4:5], v[4:5] op_sel_hi:[1,0,1] neg_lo:[0,0,1] neg_hi:[0,0,1]
	v_cvt_pk_f16_f32 v6, v3, v6
	v_cvt_pk_f16_f32 v3, v4, v5
	v_pk_fma_f32 v[4:5], v[16:17], s[4:5], v[10:11] op_sel_hi:[1,0,1] neg_lo:[0,0,1] neg_hi:[0,0,1]
	v_pk_fma_f32 v[10:11], v[22:23], s[4:5], v[12:13] op_sel_hi:[1,0,1] neg_lo:[0,0,1] neg_hi:[0,0,1]
	v_cvt_pk_f16_f32 v4, v4, v5
	v_cvt_pk_f16_f32 v5, v10, v11
	v_lshlrev_b64 v[10:11], 10, v[18:19]
	v_or_b32_e32 v10, v10, v1
	v_lshl_add_u64 v[12:13], s[6:7], 0, v[10:11]
	global_store_dwordx4 v[12:13], v[6:9], off sc1
	s_nop 1
	v_lshl_add_u64 v[6:7], s[8:9], 0, v[10:11]
	global_store_dwordx4 v[6:7], v[2:5], off sc1

.LBB7_39:
	s_or_b64 exec, exec, s[4:5]
	v_cmp_gt_u32_e32 vcc, 32, v0
	s_waitcnt lgkmcnt(0)
	s_barrier
	s_and_saveexec_b64 s[2:3], vcc
	s_cbranch_execz .LBB7_70
	s_load_dwordx4 s[16:19], s[0:1], 0x18
	s_load_dwordx2 s[20:21], s[0:1], 0x50
	s_load_dwordx2 s[22:23], s[0:1], 0x40
	v_mov_b32_e32 v3, 0x8208
	v_mad_u32_u24 v4, v0, 36, v3
	s_waitcnt lgkmcnt(0)
	s_load_dword s2, s[16:17], 0x0
	v_mov_b32_e32 v3, 0x8210
	v_mov_b32_e32 v2, 0x8200
	v_mad_u32_u24 v5, v0, 36, v3
	v_mov_b32_e32 v3, 0x8218
	v_mad_u32_u24 v2, v0, 36, v2
	v_mad_u32_u24 v6, v0, 36, v3
	s_waitcnt lgkmcnt(0)
	v_med3_i32 v3, s2, 1, 8
	v_add_u32_e32 v12, -1, v3
	ds_read2_b32 v[2:3], v2 offset1:1
	ds_read2_b32 v[8:9], v4 offset1:1
	ds_read2_b32 v[4:5], v5 offset1:1
	ds_read2_b32 v[6:7], v6 offset1:1
	s_mov_b32 s2, 0x3fb8aa3b
	s_mov_b32 s3, 0xc2ce8ed0
	s_mov_b32 s6, 0x42b17218
	s_waitcnt lgkmcnt(3)
	v_cmp_ge_f32_e32 vcc, v2, v3
	v_max_f32_e32 v14, v3, v3
	v_max_f32_e32 v15, v2, v2
	v_cndmask_b32_e64 v13, 0, 1, vcc
	s_waitcnt lgkmcnt(2)
	v_cmp_gt_f32_e32 vcc, v8, v3
	v_max_f32_e32 v14, v15, v14
	v_max3_f32 v14, v14, v8, v9
	v_cndmask_b32_e64 v15, 0, 1, vcc
	v_cmp_gt_f32_e32 vcc, v9, v3
	s_waitcnt lgkmcnt(1)
	v_max3_f32 v14, v14, v4, v5
	s_waitcnt lgkmcnt(0)
	v_max3_f32 v14, v14, v6, v7
	v_addc_co_u32_e32 v13, vcc, v15, v13, vcc
	v_cmp_ge_f32_e32 vcc, v2, v8
	v_or_b32_e32 v10, s24, v0
	v_ashrrev_i32_e32 v11, 31, v10
	v_cndmask_b32_e64 v15, 0, 1, vcc
	v_cmp_ge_f32_e32 vcc, v3, v8
	s_nop 1
	v_cndmask_b32_e64 v16, 0, 1, vcc
	v_cmp_gt_f32_e32 vcc, v9, v8
	s_nop 1
	v_addc_co_u32_e32 v15, vcc, v15, v16, vcc
	v_cmp_ge_f32_e32 vcc, v2, v9
	s_nop 1
	v_cndmask_b32_e64 v16, 0, 1, vcc
	v_cmp_ge_f32_e32 vcc, v3, v9
	s_nop 1
	v_cndmask_b32_e64 v17, 0, 1, vcc
	v_cmp_ge_f32_e32 vcc, v8, v9
	s_nop 1
	v_addc_co_u32_e32 v16, vcc, v16, v17, vcc
	v_cmp_gt_f32_e32 vcc, v4, v3
	s_nop 1
	v_cndmask_b32_e64 v17, 0, 1, vcc
	v_cmp_ge_f32_e32 vcc, v2, v4
	s_nop 1
	v_cndmask_b32_e64 v18, 0, 1, vcc
	v_cmp_ge_f32_e32 vcc, v3, v4
	s_nop 1
	v_cndmask_b32_e64 v19, 0, 1, vcc
	v_cmp_ge_f32_e32 vcc, v2, v5
	s_nop 1
	v_cndmask_b32_e64 v20, 0, 1, vcc
	v_cmp_ge_f32_e32 vcc, v3, v5
	s_nop 1
	v_cndmask_b32_e64 v21, 0, 1, vcc
	v_cmp_gt_f32_e32 vcc, v4, v8
	s_nop 1
	v_cndmask_b32_e64 v22, 0, 1, vcc
	v_cmp_gt_f32_e32 vcc, v4, v9
	s_nop 1
	v_cndmask_b32_e64 v23, 0, 1, vcc
	v_cmp_ge_f32_e32 vcc, v9, v4
	s_nop 1
	v_cndmask_b32_e64 v24, 0, 1, vcc
	v_cmp_ge_f32_e32 vcc, v9, v5
	s_nop 1
	v_cndmask_b32_e64 v25, 0, 1, vcc
	v_cmp_gt_f32_e32 vcc, v5, v3
	s_nop 1
	v_addc_co_u32_e32 v13, vcc, v13, v17, vcc
	v_cmp_gt_f32_e32 vcc, v5, v8
	s_nop 1
	v_addc_co_u32_e32 v15, vcc, v15, v22, vcc
	v_cmp_gt_f32_e32 vcc, v5, v9
	s_nop 1
	v_addc_co_u32_e32 v16, vcc, v16, v23, vcc
	v_cmp_ge_f32_e32 vcc, v8, v4
	s_nop 1
	v_addc_co_u32_e32 v17, vcc, v18, v19, vcc
	v_cmp_gt_f32_e32 vcc, v5, v4
	s_nop 1
	v_addc_co_u32_e32 v17, vcc, v17, v24, vcc
	v_cmp_ge_f32_e32 vcc, v8, v5
	s_nop 1
	v_addc_co_u32_e32 v18, vcc, v20, v21, vcc
	v_cmp_ge_f32_e32 vcc, v4, v5
	s_nop 1
	v_addc_co_u32_e32 v18, vcc, v18, v25, vcc
	v_cmp_gt_f32_e32 vcc, v6, v3
	s_nop 1
	v_cndmask_b32_e64 v19, 0, 1, vcc
	v_cmp_ge_f32_e32 vcc, v2, v6
	s_nop 1
	v_cndmask_b32_e64 v20, 0, 1, vcc
	v_cmp_ge_f32_e32 vcc, v3, v6
	s_nop 1
	v_cndmask_b32_e64 v21, 0, 1, vcc
	v_cmp_ge_f32_e32 vcc, v2, v7
	s_nop 1
	v_cndmask_b32_e64 v22, 0, 1, vcc
	v_cmp_ge_f32_e32 vcc, v3, v7
	s_nop 1
	v_cndmask_b32_e64 v23, 0, 1, vcc
	v_cmp_gt_f32_e32 vcc, v6, v8
	s_nop 1
	v_cndmask_b32_e64 v24, 0, 1, vcc
	v_cmp_gt_f32_e32 vcc, v6, v9
	s_nop 1
	v_cndmask_b32_e64 v25, 0, 1, vcc
	v_cmp_ge_f32_e32 vcc, v9, v6
	s_nop 1
	v_cndmask_b32_e64 v26, 0, 1, vcc
	v_cmp_ge_f32_e32 vcc, v9, v7
	s_nop 1
	v_cndmask_b32_e64 v27, 0, 1, vcc
	v_cmp_ge_f32_e32 vcc, v8, v6
	s_nop 1
	v_addc_co_u32_e32 v20, vcc, v20, v21, vcc
	v_cmp_ge_f32_e32 vcc, v8, v7
	s_nop 1
	v_addc_co_u32_e32 v21, vcc, v22, v23, vcc
	v_cmp_gt_f32_e32 vcc, v6, v4
	s_nop 1
	v_cndmask_b32_e64 v22, 0, 1, vcc
	v_cmp_gt_f32_e32 vcc, v6, v5
	s_nop 1
	v_cndmask_b32_e64 v23, 0, 1, vcc
	v_cmp_ge_f32_e32 vcc, v5, v6
	s_nop 1
	v_cndmask_b32_e64 v28, 0, 1, vcc
	v_cmp_ge_f32_e32 vcc, v5, v7
	s_nop 1
	v_cndmask_b32_e64 v29, 0, 1, vcc
	v_cmp_gt_f32_e32 vcc, v7, v3
	s_nop 1
	v_addc_co_u32_e32 v13, vcc, v13, v19, vcc
	v_cmp_eq_u32_e32 vcc, v13, v12
	s_nop 1
	v_cndmask_b32_e32 v13, v2, v3, vcc
	v_cmp_gt_f32_e32 vcc, v7, v8
	s_nop 1
	v_addc_co_u32_e32 v15, vcc, v15, v24, vcc
	v_cmp_eq_u32_e32 vcc, v15, v12
	s_nop 1
	v_cndmask_b32_e32 v13, v13, v8, vcc
	v_cmp_gt_f32_e32 vcc, v7, v9
	s_nop 1
	v_addc_co_u32_e32 v15, vcc, v16, v25, vcc
	v_cmp_eq_u32_e32 vcc, v15, v12
	v_sub_f32_e32 v16, v2, v14
	s_nop 0
	v_cndmask_b32_e32 v13, v13, v9, vcc
	v_cmp_gt_f32_e32 vcc, v7, v4
	s_nop 1
	v_addc_co_u32_e32 v15, vcc, v17, v22, vcc
	v_cmp_eq_u32_e32 vcc, v15, v12
	v_mul_f32_e32 v17, 0x3fb8aa3b, v16
	v_rndne_f32_e32 v19, v17
	v_cndmask_b32_e32 v13, v13, v4, vcc
	v_cmp_gt_f32_e32 vcc, v7, v5
	s_nop 1
	v_addc_co_u32_e32 v15, vcc, v18, v23, vcc
	v_cmp_eq_u32_e32 vcc, v15, v12
	v_fma_f32 v18, v16, s2, -v17
	v_fmac_f32_e32 v18, 0x32a5705f, v16
	v_cndmask_b32_e32 v13, v13, v5, vcc
	v_cmp_ge_f32_e32 vcc, v4, v6
	v_sub_f32_e32 v17, v17, v19
	v_add_f32_e32 v17, v17, v18
	v_addc_co_u32_e32 v15, vcc, v20, v26, vcc
	v_cmp_gt_f32_e32 vcc, v7, v6
	v_exp_f32_e32 v17, v17
	v_cvt_i32_f32_e32 v18, v19
	v_addc_co_u32_e32 v15, vcc, v15, v28, vcc
	v_cmp_eq_u32_e32 vcc, v15, v12
	s_nop 1
	v_cndmask_b32_e32 v13, v13, v6, vcc
	v_cmp_ge_f32_e32 vcc, v4, v7
	s_nop 1
	v_addc_co_u32_e32 v15, vcc, v21, v27, vcc
	v_cmp_ge_f32_e32 vcc, v6, v7
	s_nop 1
	v_addc_co_u32_e32 v15, vcc, v15, v29, vcc
	v_cmp_eq_u32_e32 vcc, v15, v12
	v_ldexp_f32 v12, v17, v18
	s_nop 0
	v_cndmask_b32_e32 v19, v13, v7, vcc
	v_sub_f32_e32 v13, v3, v14
	v_mul_f32_e32 v15, 0x3fb8aa3b, v13
	v_fma_f32 v17, v13, s2, -v15
	v_rndne_f32_e32 v18, v15
	v_fmac_f32_e32 v17, 0x32a5705f, v13
	v_sub_f32_e32 v15, v15, v18
	v_add_f32_e32 v15, v15, v17
	v_exp_f32_e32 v15, v15
	v_cvt_i32_f32_e32 v17, v18
	v_cmp_ngt_f32_e32 vcc, s3, v16
	v_mov_b32_e32 v18, 0x7f800000
	v_cmp_lt_f32_e64 s[10:11], v3, v19
	v_cndmask_b32_e32 v12, 0, v12, vcc
	v_cmp_nlt_f32_e32 vcc, s6, v16
	v_ldexp_f32 v15, v15, v17
	v_cmp_lt_f32_e64 s[8:9], v9, v19
	v_cndmask_b32_e32 v12, v18, v12, vcc
	v_cmp_ngt_f32_e32 vcc, s3, v13
	v_cmp_lt_f32_e64 s[14:15], v8, v19
	v_cmp_lt_f32_e64 s[4:5], v5, v19
	v_cndmask_b32_e32 v15, 0, v15, vcc
	v_cmp_nlt_f32_e32 vcc, s6, v13
	v_cmp_lt_f32_e64 s[12:13], v4, v19
	s_nop 0
	v_cndmask_b32_e32 v13, v18, v15, vcc
	v_sub_f32_e32 v15, v8, v14
	v_mul_f32_e32 v16, 0x3fb8aa3b, v15
	v_fma_f32 v17, v15, s2, -v16
	v_rndne_f32_e32 v20, v16
	v_fmac_f32_e32 v17, 0x32a5705f, v15
	v_sub_f32_e32 v16, v16, v20
	v_add_f32_e32 v16, v16, v17
	v_exp_f32_e32 v16, v16
	v_cvt_i32_f32_e32 v17, v20
	v_cmp_lt_f32_e32 vcc, v2, v19
	v_cndmask_b32_e64 v13, v13, 0, s[10:11]
	v_ldexp_f32 v3, v16, v17
	v_sub_f32_e32 v16, v9, v14
	v_mul_f32_e32 v17, 0x3fb8aa3b, v16
	v_fma_f32 v20, v16, s2, -v17
	v_rndne_f32_e32 v21, v17
	v_fmac_f32_e32 v20, 0x32a5705f, v16
	v_sub_f32_e32 v17, v17, v21
	v_add_f32_e32 v17, v17, v20
	v_exp_f32_e32 v17, v17
	v_cvt_i32_f32_e32 v20, v21
	v_cndmask_b32_e64 v12, v12, 0, vcc
	v_cmp_ngt_f32_e32 vcc, s3, v15
	s_nop 1
	v_cndmask_b32_e32 v3, 0, v3, vcc
	v_cmp_nlt_f32_e32 vcc, s6, v15
	v_ldexp_f32 v15, v17, v20
	s_nop 0
	v_cndmask_b32_e32 v3, v18, v3, vcc
	v_cmp_ngt_f32_e32 vcc, s3, v16
	v_cndmask_b32_e64 v8, v3, 0, s[14:15]
	s_nop 0
	v_cndmask_b32_e32 v15, 0, v15, vcc
	v_cmp_nlt_f32_e32 vcc, s6, v16
	v_sub_f32_e32 v16, v4, v14
	v_mul_f32_e32 v17, 0x3fb8aa3b, v16
	v_fma_f32 v20, v16, s2, -v17
	v_rndne_f32_e32 v21, v17
	v_fmac_f32_e32 v20, 0x32a5705f, v16
	v_sub_f32_e32 v17, v17, v21
	v_add_f32_e32 v17, v17, v20
	v_exp_f32_e32 v17, v17
	v_cvt_i32_f32_e32 v20, v21
	v_cndmask_b32_e32 v15, v18, v15, vcc
	v_cndmask_b32_e64 v9, v15, 0, s[8:9]
	v_sub_f32_e32 v15, v5, v14
	v_ldexp_f32 v3, v17, v20
	v_mul_f32_e32 v17, 0x3fb8aa3b, v15
	v_fma_f32 v20, v15, s2, -v17
	v_rndne_f32_e32 v21, v17
	v_fmac_f32_e32 v20, 0x32a5705f, v15
	v_sub_f32_e32 v17, v17, v21
	v_add_f32_e32 v17, v17, v20
	v_exp_f32_e32 v17, v17
	v_cvt_i32_f32_e32 v20, v21
	v_cmp_ngt_f32_e32 vcc, s3, v16
	s_nop 1
	v_cndmask_b32_e32 v3, 0, v3, vcc
	v_cmp_nlt_f32_e32 vcc, s6, v16
	v_ldexp_f32 v16, v17, v20
	s_nop 0
	v_cndmask_b32_e32 v3, v18, v3, vcc
	v_cmp_ngt_f32_e32 vcc, s3, v15
	v_cndmask_b32_e64 v4, v3, 0, s[12:13]
	s_nop 0
	v_cndmask_b32_e32 v16, 0, v16, vcc
	v_cmp_nlt_f32_e32 vcc, s6, v15
	s_nop 1
	v_cndmask_b32_e32 v15, v18, v16, vcc
	v_sub_f32_e32 v16, v6, v14
	v_mul_f32_e32 v17, 0x3fb8aa3b, v16
	v_fma_f32 v20, v16, s2, -v17
	v_rndne_f32_e32 v21, v17
	v_fmac_f32_e32 v20, 0x32a5705f, v16
	v_sub_f32_e32 v17, v17, v21
	v_add_f32_e32 v17, v17, v20
	v_exp_f32_e32 v17, v17
	v_cvt_i32_f32_e32 v20, v21
	v_sub_f32_e32 v14, v7, v14
	v_cndmask_b32_e64 v5, v15, 0, s[4:5]
	v_mul_f32_e32 v15, 0x3fb8aa3b, v14
	v_ldexp_f32 v3, v17, v20
	v_fma_f32 v17, v14, s2, -v15
	v_rndne_f32_e32 v20, v15
	v_fmac_f32_e32 v17, 0x32a5705f, v14
	v_sub_f32_e32 v15, v15, v20
	v_add_f32_e32 v15, v15, v17
	v_exp_f32_e32 v15, v15
	v_cvt_i32_f32_e32 v17, v20
	v_cmp_ngt_f32_e32 vcc, s3, v16
	v_ldexp_f32 v15, v15, v17
	s_nop 0
	v_cndmask_b32_e32 v3, 0, v3, vcc
	v_cmp_nlt_f32_e32 vcc, s6, v16
	s_nop 1
	v_cndmask_b32_e32 v3, v18, v3, vcc
	v_cmp_ngt_f32_e32 vcc, s3, v14
	v_cmp_lt_f32_e64 s[2:3], v7, v19
	s_nop 0
	v_cndmask_b32_e32 v15, 0, v15, vcc
	v_cmp_nlt_f32_e32 vcc, s6, v14
	v_cmp_lt_f32_e64 s[6:7], v6, v19
	v_lshlrev_b64 v[6:7], 5, v[10:11]
	v_cndmask_b32_e32 v14, v18, v15, vcc
	v_cndmask_b32_e64 v15, v14, 0, s[2:3]
	v_cndmask_b32_e64 v14, v3, 0, s[6:7]
	v_add_f32_e32 v3, v12, v13
	v_add_f32_e32 v3, v8, v3
	v_add_f32_e32 v3, v9, v3
	v_add_f32_e32 v3, v4, v3
	v_add_f32_e32 v3, v5, v3
	v_add_f32_e32 v3, v14, v3
	v_add_f32_e32 v3, v15, v3
	v_div_scale_f32 v18, s[16:17], v3, v3, 1.0
	v_rcp_f32_e32 v20, v18
	v_cmp_nlt_f32_e64 s[16:17], v2, v19
	v_lshl_add_u64 v[16:17], s[18:19], 0, v[6:7]
	v_fma_f32 v2, -v18, v20, 1.0
	v_fmac_f32_e32 v20, v2, v20
	v_div_scale_f32 v2, vcc, 1.0, v3, 1.0
	v_mul_f32_e32 v6, v2, v20
	v_fma_f32 v7, -v18, v6, v2
	v_fmac_f32_e32 v6, v7, v20
	v_fma_f32 v2, -v18, v6, v2
	v_div_fmas_f32 v2, v2, v20, v6
	v_div_fixup_f32 v18, v2, v3, 1.0
	v_pk_mul_f32 v[6:7], v[12:13], v[18:19] op_sel_hi:[1,0]
	v_lshlrev_b32_e32 v12, 3, v10
	v_pk_mul_f32 v[8:9], v[8:9], v[18:19] op_sel_hi:[1,0]
	v_pk_mul_f32 v[2:3], v[4:5], v[18:19] op_sel_hi:[1,0]
	v_pk_mul_f32 v[4:5], v[14:15], v[18:19] op_sel_hi:[1,0]
	v_mov_b32_e32 v14, 0
	v_ashrrev_i32_e32 v13, 31, v12
	global_store_dwordx4 v[16:17], v[6:9], off sc1
	global_store_dwordx4 v[16:17], v[2:5], off offset:16 sc1
	s_and_saveexec_b64 s[18:19], s[16:17]
	s_cbranch_execz .LBB7_42
	v_lshlrev_b64 v[14:15], 2, v[12:13]
	v_lshl_add_u64 v[16:17], s[20:21], 0, v[14:15]
	v_lshl_add_u64 v[14:15], s[22:23], 0, v[14:15]
	v_mov_b32_e32 v18, 0
	global_store_dword v[14:15], v18, off
	global_store_dword v[16:17], v6, off
	v_mov_b32_e32 v14, 1

_Z18fused_router_wprepILb0EEvPKfS1_S1_PKiPfS4_PiS5_S5_S5_S4_S1_PDF16_S6_S1_S6_:
	s_cmpk_gt_i32 s2, 0xff
	s_mov_b64 s[4:5], -1
	s_cbranch_scc0 .LBB8_6
	v_lshlrev_b32_e32 v2, 2, v0
	s_lshl_b32 s3, s2, 6
	v_and_b32_e32 v2, 60, v2
	s_cmpk_gt_u32 s2, 0x8ff
	v_lshrrev_b32_e32 v1, 4, v0
	v_mov_b32_e32 v3, 0
	v_lshlrev_b32_e32 v2, 2, v2
	s_cbranch_scc0 .LBB8_3
	s_load_dwordx4 s[4:7], s[0:1], 0x70
	s_add_i32 s8, s2, 0xfffff700
	s_lshr_b32 s10, s8, 8
	s_lshl_b32 s8, s2, 3
	s_mov_b32 s11, 0
	s_and_b32 s12, s8, 0x7c0
	s_and_b32 s13, s3, 0x1c0
	s_lshl_b64 s[8:9], s[10:11], 9
	s_lshl_b64 s[10:11], s[10:11], 22
	s_waitcnt lgkmcnt(0)
	s_add_u32 s4, s4, s10
	s_addc_u32 s5, s5, s11
	s_lshl_b32 s10, s13, 2
	s_add_u32 s4, s4, s10
	s_addc_u32 s5, s5, 0
	v_or_b32_e32 v4, s12, v1
	v_lshl_add_u64 v[16:17], s[4:5], 0, v[2:3]
	v_lshlrev_b32_e32 v18, 11, v4
	v_mov_b32_e32 v19, v3
	v_lshl_add_u64 v[12:13], v[16:17], 0, v[18:19]
	v_or_b32_e32 v4, 0x8000, v18
	v_mov_b32_e32 v5, v3
	v_lshl_add_u64 v[14:15], v[16:17], 0, v[4:5]
	global_load_dwordx4 v[4:7], v[12:13], off nt
	global_load_dwordx4 v[8:11], v[14:15], off nt
	v_or_b32_e32 v12, 0x10000, v18
	v_mov_b32_e32 v13, v3
	v_lshl_add_u64 v[12:13], v[16:17], 0, v[12:13]
	global_load_dwordx4 v[12:15], v[12:13], off nt
	v_or_b32_e32 v18, 0x18000, v18
	v_lshl_add_u64 v[16:17], v[16:17], 0, v[18:19]
	global_load_dwordx4 v[16:19], v[16:17], off nt
	s_movk_i32 s5, 0x104
	v_lshrrev_b32_e32 v22, 3, v0
	v_and_b32_e32 v23, 7, v0
	v_mov_b32_e32 v21, v3
	s_movk_i32 s10, 0x820
	v_mad_u32_u24 v3, v1, s5, v2
	v_lshlrev_b32_e32 v24, 2, v22
	v_add_u32_e32 v26, 0x1040, v3
	v_add_u32_e32 v27, 0x1048, v3
	v_add_u32_e32 v28, 0x2080, v3
	v_add_u32_e32 v29, 0x2088, v3
	v_add_u32_e32 v30, 0x30c0, v3
	v_add_u32_e32 v31, 0x30c8, v3
	v_mad_u32_u24 v32, v23, s10, v24
	v_add_u32_e32 v33, 0x400, v32
	s_mov_b32 s4, 0x45800000
	s_or_b32 s5, s8, s13
	s_lshl_b32 s8, s12, 1
	s_add_u32 s6, s6, s8
	v_lshlrev_b32_e32 v20, 4, v23
	v_mov_b32_e32 v23, s9
	v_or_b32_e32 v22, s5, v22
	s_addc_u32 s7, s7, 0
	v_lshlrev_b64 v[24:25], 12, v[22:23]
	v_lshl_add_u64 v[20:21], s[6:7], 0, v[20:21]
	v_lshl_add_u64 v[24:25], v[20:21], 0, v[24:25]
	v_or_b32_e32 v22, 32, v22
	s_waitcnt vmcnt(3)
	ds_write2_b32 v3, v4, v5 offset1:1
	ds_write2_b32 v3, v6, v7 offset0:2 offset1:3
	s_waitcnt vmcnt(2)
	ds_write2_b32 v26, v8, v9 offset1:1
	ds_write2_b32 v27, v10, v11 offset1:1
	s_waitcnt vmcnt(1)
	ds_write2_b32 v28, v12, v13 offset1:1
	ds_write2_b32 v29, v14, v15 offset1:1
	s_waitcnt vmcnt(0)
	ds_write2_b32 v30, v16, v17 offset1:1
	ds_write2_b32 v31, v18, v19 offset1:1
	s_waitcnt lgkmcnt(0)
	s_barrier
	ds_read2_b32 v[4:5], v32 offset1:32
	ds_read2_b32 v[26:27], v32 offset0:65 offset1:97
	ds_read2_b32 v[6:7], v32 offset0:130 offset1:162
	ds_read2_b32 v[28:29], v32 offset0:195 offset1:227
	ds_read2_b32 v[10:11], v33 offset0:4 offset1:36
	ds_read2_b32 v[30:31], v33 offset0:69 offset1:101
	ds_read2_b32 v[12:13], v33 offset0:134 offset1:166
	ds_read2_b32 v[14:15], v33 offset0:199 offset1:231
	s_waitcnt lgkmcnt(6)
	v_mov_b32_e32 v8, v26
	s_waitcnt lgkmcnt(5)
	v_mov_b32_e32 v9, v6
	s_waitcnt lgkmcnt(4)
	v_mov_b32_e32 v16, v28
	s_waitcnt lgkmcnt(3)
	v_mov_b32_e32 v17, v10
	s_waitcnt lgkmcnt(2)
	v_mov_b32_e32 v18, v30
	s_waitcnt lgkmcnt(1)
	v_mov_b32_e32 v19, v12
	v_fma_mixlo_f16 v3, v4, s4, 0
	v_fma_mixlo_f16 v12, v5, s4, 0
	v_mov_b32_e32 v6, v27
	v_pk_mul_f32 v[4:5], v[8:9], s[4:5] op_sel_hi:[1,0]
	v_pk_mul_f32 v[8:9], v[16:17], s[4:5] op_sel_hi:[1,0]
	v_pk_mul_f32 v[16:17], v[18:19], s[4:5] op_sel_hi:[1,0]
	v_pk_mul_f32 v[6:7], v[6:7], s[4:5] op_sel_hi:[1,0]
	v_cvt_pk_f16_f32 v8, v8, v9
	v_cvt_pk_f16_f32 v9, v16, v17
	v_cvt_pk_f16_f32 v5, v4, v5
	v_cvt_pk_f16_f32 v16, v6, v7
	v_lshrrev_b32_e32 v7, 16, v9
	v_mov_b32_e32 v10, v29
	v_pack_b32_f16 v4, v3, v5
	v_alignbit_b32 v5, v8, v5, 16
	v_alignbit_b32 v6, v9, v8, 16
	s_waitcnt lgkmcnt(0)
	v_fma_mixhi_f16 v7, v14, s4, 0
	v_pack_b32_f16 v8, v12, v16
	global_store_dwordx4 v[24:25], v[4:7], off sc1
	v_mov_b32_e32 v12, v31
	s_nop 0
	v_pk_mul_f32 v[4:5], v[10:11], s[4:5] op_sel_hi:[1,0]
	s_nop 0
	v_cvt_pk_f16_f32 v3, v4, v5
	v_pk_mul_f32 v[4:5], v[12:13], s[4:5] op_sel_hi:[1,0]
	v_alignbit_b32 v9, v3, v16, 16
	v_cvt_pk_f16_f32 v4, v4, v5
	v_alignbit_b32 v10, v4, v3, 16
	v_lshrrev_b32_e32 v11, 16, v4
	v_lshlrev_b64 v[4:5], 12, v[22:23]
	v_fma_mixhi_f16 v11, v15, s4, 0
	v_lshl_add_u64 v[4:5], v[20:21], 0, v[4:5]
	global_store_dwordx4 v[4:5], v[8:11], off sc1
	s_mov_b64 s[4:5], 0
.LBB8_3:
	s_andn2_b64 vcc, exec, s[4:5]
	s_cbranch_vccnz .LBB8_5
	s_load_dwordx4 s[4:7], s[0:1], 0x58
	s_add_i32 s8, s2, 0xffffff00
	s_lshr_b32 s10, s8, 8
	s_lshl_b32 s8, s2, 1
	s_mov_b32 s11, 0
	s_and_b32 s12, s8, 0x1c0
	s_and_b32 s3, s3, 0x7c0
	s_lshl_b64 s[8:9], s[10:11], 11
	s_lshl_b64 s[10:11], s[10:11], 22
	s_waitcnt lgkmcnt(0)
	s_add_u32 s4, s4, s10
	s_addc_u32 s5, s5, s11
	s_lshl_b32 s10, s3, 2
	s_add_u32 s4, s4, s10
	s_addc_u32 s5, s5, 0
	v_mov_b32_e32 v3, 0
	v_or_b32_e32 v4, s12, v1
	v_lshl_add_u64 v[16:17], s[4:5], 0, v[2:3]
	v_lshlrev_b32_e32 v18, 13, v4
	v_mov_b32_e32 v19, v3
	s_movk_i32 s4, 0x104
	v_lshl_add_u64 v[12:13], v[16:17], 0, v[18:19]
	v_mad_u32_u24 v1, v1, s4, v2
	v_or_b32_e32 v2, 0x20000, v18
	v_lshl_add_u64 v[14:15], v[16:17], 0, v[2:3]
	global_load_dwordx4 v[4:7], v[12:13], off nt
	global_load_dwordx4 v[8:11], v[14:15], off nt
	v_or_b32_e32 v2, 0x40000, v18
	v_lshl_add_u64 v[12:13], v[16:17], 0, v[2:3]
	global_load_dwordx4 v[12:15], v[12:13], off nt
	v_or_b32_e32 v2, 0x60000, v18
	v_lshl_add_u64 v[16:17], v[16:17], 0, v[2:3]
	global_load_dwordx4 v[16:19], v[16:17], off nt
	v_lshrrev_b32_e32 v2, 3, v0
	v_and_b32_e32 v24, 7, v0
	s_movk_i32 s5, 0x820
	v_lshlrev_b32_e32 v20, 2, v2
	v_mad_u32_u24 v32, v24, s5, v20
	s_or_b32 s3, s8, s3
	s_lshl_b32 s5, s12, 1
	s_add_u32 s6, s6, s5
	v_add_u32_e32 v26, 0x1040, v1
	v_add_u32_e32 v27, 0x1048, v1
	v_add_u32_e32 v28, 0x2080, v1
	v_add_u32_e32 v29, 0x2088, v1
	v_or_b32_e32 v20, s3, v2
	s_addc_u32 s7, s7, 0
	v_lshlrev_b32_e32 v2, 4, v24
	v_add_u32_e32 v30, 0x30c0, v1
	v_add_u32_e32 v31, 0x30c8, v1
	v_add_u32_e32 v33, 0x400, v32
	v_lshl_add_u64 v[24:25], s[6:7], 0, v[2:3]
	s_mov_b32 s4, 0x45800000
	v_mov_b32_e32 v21, s9
	v_lshlrev_b64 v[22:23], 10, v[20:21]
	v_lshl_add_u64 v[22:23], v[24:25], 0, v[22:23]
	v_or_b32_e32 v20, 32, v20
	s_waitcnt vmcnt(3)
	ds_write2_b32 v1, v4, v5 offset1:1
	ds_write2_b32 v1, v6, v7 offset0:2 offset1:3
	s_waitcnt vmcnt(2)
	ds_write2_b32 v26, v8, v9 offset1:1
	ds_write2_b32 v27, v10, v11 offset1:1
	s_waitcnt vmcnt(1)
	ds_write2_b32 v28, v12, v13 offset1:1
	ds_write2_b32 v29, v14, v15 offset1:1
	s_waitcnt vmcnt(0)
	ds_write2_b32 v30, v16, v17 offset1:1
	ds_write2_b32 v31, v18, v19 offset1:1
	s_waitcnt lgkmcnt(0)
	s_barrier
	ds_read2_b32 v[2:3], v32 offset1:32
	ds_read2_b32 v[18:19], v32 offset0:65 offset1:97
	ds_read2_b32 v[4:5], v32 offset0:130 offset1:162
	ds_read2_b32 v[26:27], v32 offset0:195 offset1:227
	ds_read2_b32 v[6:7], v33 offset0:4 offset1:36
	ds_read2_b32 v[28:29], v33 offset0:69 offset1:101
	ds_read2_b32 v[8:9], v33 offset0:134 offset1:166
	ds_read2_b32 v[10:11], v33 offset0:199 offset1:231
	s_waitcnt lgkmcnt(6)
	v_mov_b32_e32 v12, v18
	s_waitcnt lgkmcnt(5)
	v_mov_b32_e32 v13, v4
	s_waitcnt lgkmcnt(4)
	v_mov_b32_e32 v14, v26
	s_waitcnt lgkmcnt(3)
	v_mov_b32_e32 v15, v6
	s_waitcnt lgkmcnt(2)
	v_mov_b32_e32 v16, v28
	s_waitcnt lgkmcnt(1)
	v_mov_b32_e32 v17, v8
	v_fma_mixlo_f16 v1, v2, s4, 0
	v_fma_mixlo_f16 v18, v3, s4, 0
	v_mov_b32_e32 v4, v19
	v_pk_mul_f32 v[2:3], v[12:13], s[4:5] op_sel_hi:[1,0]
	v_pk_mul_f32 v[12:13], v[14:15], s[4:5] op_sel_hi:[1,0]
	v_pk_mul_f32 v[14:15], v[16:17], s[4:5] op_sel_hi:[1,0]
	v_mov_b32_e32 v8, v29
	v_pk_mul_f32 v[4:5], v[4:5], s[4:5] op_sel_hi:[1,0]
	v_cvt_pk_f16_f32 v12, v12, v13
	v_cvt_pk_f16_f32 v13, v14, v15
	v_mov_b32_e32 v6, v27
	v_pk_mul_f32 v[8:9], v[8:9], s[4:5] op_sel_hi:[1,0]
	v_cvt_pk_f16_f32 v3, v2, v3
	v_cvt_pk_f16_f32 v14, v4, v5
	v_lshrrev_b32_e32 v5, 16, v13
	v_pk_mul_f32 v[6:7], v[6:7], s[4:5] op_sel_hi:[1,0]
	v_pack_b32_f16 v2, v1, v3
	v_alignbit_b32 v3, v12, v3, 16
	v_alignbit_b32 v4, v13, v12, 16
	s_waitcnt lgkmcnt(0)
	v_fma_mixhi_f16 v5, v10, s4, 0
	v_cvt_pk_f16_f32 v1, v8, v9
	v_cvt_pk_f16_f32 v15, v6, v7
	global_store_dwordx4 v[22:23], v[2:5], off sc1
	v_lshrrev_b32_e32 v9, 16, v1
	v_pack_b32_f16 v6, v18, v14
	v_lshlrev_b64 v[2:3], 10, v[20:21]
	v_alignbit_b32 v7, v15, v14, 16
	v_alignbit_b32 v8, v1, v15, 16
	v_fma_mixhi_f16 v9, v11, s4, 0
	v_lshl_add_u64 v[2:3], v[24:25], 0, v[2:3]
	global_store_dwordx4 v[2:3], v[6:9], off sc1

.LBB8_39:
	s_or_b64 exec, exec, s[4:5]
	v_cmp_gt_u32_e32 vcc, 32, v0
	s_waitcnt lgkmcnt(0)
	s_barrier
	s_and_saveexec_b64 s[2:3], vcc
	s_cbranch_execz .LBB8_70
	s_load_dwordx4 s[16:19], s[0:1], 0x18
	s_load_dwordx2 s[20:21], s[0:1], 0x50
	s_load_dwordx2 s[22:23], s[0:1], 0x40
	v_mov_b32_e32 v3, 0x4108
	v_mad_u32_u24 v4, v0, 36, v3
	s_waitcnt lgkmcnt(0)
	s_load_dword s2, s[16:17], 0x0
	v_mov_b32_e32 v3, 0x4110
	v_mov_b32_e32 v2, 0x4100
	v_mad_u32_u24 v5, v0, 36, v3
	v_mov_b32_e32 v3, 0x4118
	v_mad_u32_u24 v2, v0, 36, v2
	v_mad_u32_u24 v6, v0, 36, v3
	s_waitcnt lgkmcnt(0)
	v_med3_i32 v3, s2, 1, 8
	v_add_u32_e32 v12, -1, v3
	ds_read2_b32 v[2:3], v2 offset1:1
	ds_read2_b32 v[8:9], v4 offset1:1
	ds_read2_b32 v[4:5], v5 offset1:1
	ds_read2_b32 v[6:7], v6 offset1:1
	s_mov_b32 s2, 0x3fb8aa3b
	s_mov_b32 s3, 0xc2ce8ed0
	s_mov_b32 s6, 0x42b17218
	s_waitcnt lgkmcnt(3)
	v_cmp_ge_f32_e32 vcc, v2, v3
	v_max_f32_e32 v14, v3, v3
	v_max_f32_e32 v15, v2, v2
	v_cndmask_b32_e64 v13, 0, 1, vcc
	s_waitcnt lgkmcnt(2)
	v_cmp_gt_f32_e32 vcc, v8, v3
	v_max_f32_e32 v14, v15, v14
	v_max3_f32 v14, v14, v8, v9
	v_cndmask_b32_e64 v15, 0, 1, vcc
	v_cmp_gt_f32_e32 vcc, v9, v3
	s_waitcnt lgkmcnt(1)
	v_max3_f32 v14, v14, v4, v5
	s_waitcnt lgkmcnt(0)
	v_max3_f32 v14, v14, v6, v7
	v_addc_co_u32_e32 v13, vcc, v15, v13, vcc
	v_cmp_ge_f32_e32 vcc, v2, v8
	v_or_b32_e32 v10, s24, v0
	v_ashrrev_i32_e32 v11, 31, v10
	v_cndmask_b32_e64 v15, 0, 1, vcc
	v_cmp_ge_f32_e32 vcc, v3, v8
	s_nop 1
	v_cndmask_b32_e64 v16, 0, 1, vcc
	v_cmp_gt_f32_e32 vcc, v9, v8
	s_nop 1
	v_addc_co_u32_e32 v15, vcc, v15, v16, vcc
	v_cmp_ge_f32_e32 vcc, v2, v9
	s_nop 1
	v_cndmask_b32_e64 v16, 0, 1, vcc
	v_cmp_ge_f32_e32 vcc, v3, v9
	s_nop 1
	v_cndmask_b32_e64 v17, 0, 1, vcc
	v_cmp_ge_f32_e32 vcc, v8, v9
	s_nop 1
	v_addc_co_u32_e32 v16, vcc, v16, v17, vcc
	v_cmp_gt_f32_e32 vcc, v4, v3
	s_nop 1
	v_cndmask_b32_e64 v17, 0, 1, vcc
	v_cmp_ge_f32_e32 vcc, v2, v4
	s_nop 1
	v_cndmask_b32_e64 v18, 0, 1, vcc
	v_cmp_ge_f32_e32 vcc, v3, v4
	s_nop 1
	v_cndmask_b32_e64 v19, 0, 1, vcc
	v_cmp_ge_f32_e32 vcc, v2, v5
	s_nop 1
	v_cndmask_b32_e64 v20, 0, 1, vcc
	v_cmp_ge_f32_e32 vcc, v3, v5
	s_nop 1
	v_cndmask_b32_e64 v21, 0, 1, vcc
	v_cmp_gt_f32_e32 vcc, v4, v8
	s_nop 1
	v_cndmask_b32_e64 v22, 0, 1, vcc
	v_cmp_gt_f32_e32 vcc, v4, v9
	s_nop 1
	v_cndmask_b32_e64 v23, 0, 1, vcc
	v_cmp_ge_f32_e32 vcc, v9, v4
	s_nop 1
	v_cndmask_b32_e64 v24, 0, 1, vcc
	v_cmp_ge_f32_e32 vcc, v9, v5
	s_nop 1
	v_cndmask_b32_e64 v25, 0, 1, vcc
	v_cmp_gt_f32_e32 vcc, v5, v3
	s_nop 1
	v_addc_co_u32_e32 v13, vcc, v13, v17, vcc
	v_cmp_gt_f32_e32 vcc, v5, v8
	s_nop 1
	v_addc_co_u32_e32 v15, vcc, v15, v22, vcc
	v_cmp_gt_f32_e32 vcc, v5, v9
	s_nop 1
	v_addc_co_u32_e32 v16, vcc, v16, v23, vcc
	v_cmp_ge_f32_e32 vcc, v8, v4
	s_nop 1
	v_addc_co_u32_e32 v17, vcc, v18, v19, vcc
	v_cmp_gt_f32_e32 vcc, v5, v4
	s_nop 1
	v_addc_co_u32_e32 v17, vcc, v17, v24, vcc
	v_cmp_ge_f32_e32 vcc, v8, v5
	s_nop 1
	v_addc_co_u32_e32 v18, vcc, v20, v21, vcc
	v_cmp_ge_f32_e32 vcc, v4, v5
	s_nop 1
	v_addc_co_u32_e32 v18, vcc, v18, v25, vcc
	v_cmp_gt_f32_e32 vcc, v6, v3
	s_nop 1
	v_cndmask_b32_e64 v19, 0, 1, vcc
	v_cmp_ge_f32_e32 vcc, v2, v6
	s_nop 1
	v_cndmask_b32_e64 v20, 0, 1, vcc
	v_cmp_ge_f32_e32 vcc, v3, v6
	s_nop 1
	v_cndmask_b32_e64 v21, 0, 1, vcc
	v_cmp_ge_f32_e32 vcc, v2, v7
	s_nop 1
	v_cndmask_b32_e64 v22, 0, 1, vcc
	v_cmp_ge_f32_e32 vcc, v3, v7
	s_nop 1
	v_cndmask_b32_e64 v23, 0, 1, vcc
	v_cmp_gt_f32_e32 vcc, v6, v8
	s_nop 1
	v_cndmask_b32_e64 v24, 0, 1, vcc
	v_cmp_gt_f32_e32 vcc, v6, v9
	s_nop 1
	v_cndmask_b32_e64 v25, 0, 1, vcc
	v_cmp_ge_f32_e32 vcc, v9, v6
	s_nop 1
	v_cndmask_b32_e64 v26, 0, 1, vcc
	v_cmp_ge_f32_e32 vcc, v9, v7
	s_nop 1
	v_cndmask_b32_e64 v27, 0, 1, vcc
	v_cmp_ge_f32_e32 vcc, v8, v6
	s_nop 1
	v_addc_co_u32_e32 v20, vcc, v20, v21, vcc
	v_cmp_ge_f32_e32 vcc, v8, v7
	s_nop 1
	v_addc_co_u32_e32 v21, vcc, v22, v23, vcc
	v_cmp_gt_f32_e32 vcc, v6, v4
	s_nop 1
	v_cndmask_b32_e64 v22, 0, 1, vcc
	v_cmp_gt_f32_e32 vcc, v6, v5
	s_nop 1
	v_cndmask_b32_e64 v23, 0, 1, vcc
	v_cmp_ge_f32_e32 vcc, v5, v6
	s_nop 1
	v_cndmask_b32_e64 v28, 0, 1, vcc
	v_cmp_ge_f32_e32 vcc, v5, v7
	s_nop 1
	v_cndmask_b32_e64 v29, 0, 1, vcc
	v_cmp_gt_f32_e32 vcc, v7, v3
	s_nop 1
	v_addc_co_u32_e32 v13, vcc, v13, v19, vcc
	v_cmp_eq_u32_e32 vcc, v13, v12
	s_nop 1
	v_cndmask_b32_e32 v13, v2, v3, vcc
	v_cmp_gt_f32_e32 vcc, v7, v8
	s_nop 1
	v_addc_co_u32_e32 v15, vcc, v15, v24, vcc
	v_cmp_eq_u32_e32 vcc, v15, v12
	s_nop 1
	v_cndmask_b32_e32 v13, v13, v8, vcc
	v_cmp_gt_f32_e32 vcc, v7, v9
	s_nop 1
	v_addc_co_u32_e32 v15, vcc, v16, v25, vcc
	v_cmp_eq_u32_e32 vcc, v15, v12
	v_sub_f32_e32 v16, v2, v14
	s_nop 0
	v_cndmask_b32_e32 v13, v13, v9, vcc
	v_cmp_gt_f32_e32 vcc, v7, v4
	s_nop 1
	v_addc_co_u32_e32 v15, vcc, v17, v22, vcc
	v_cmp_eq_u32_e32 vcc, v15, v12
	v_mul_f32_e32 v17, 0x3fb8aa3b, v16
	v_rndne_f32_e32 v19, v17
	v_cndmask_b32_e32 v13, v13, v4, vcc
	v_cmp_gt_f32_e32 vcc, v7, v5
	s_nop 1
	v_addc_co_u32_e32 v15, vcc, v18, v23, vcc
	v_cmp_eq_u32_e32 vcc, v15, v12
	v_fma_f32 v18, v16, s2, -v17
	v_fmac_f32_e32 v18, 0x32a5705f, v16
	v_cndmask_b32_e32 v13, v13, v5, vcc
	v_cmp_ge_f32_e32 vcc, v4, v6
	v_sub_f32_e32 v17, v17, v19
	v_add_f32_e32 v17, v17, v18
	v_addc_co_u32_e32 v15, vcc, v20, v26, vcc
	v_cmp_gt_f32_e32 vcc, v7, v6
	v_exp_f32_e32 v17, v17
	v_cvt_i32_f32_e32 v18, v19
	v_addc_co_u32_e32 v15, vcc, v15, v28, vcc
	v_cmp_eq_u32_e32 vcc, v15, v12
	s_nop 1
	v_cndmask_b32_e32 v13, v13, v6, vcc
	v_cmp_ge_f32_e32 vcc, v4, v7
	s_nop 1
	v_addc_co_u32_e32 v15, vcc, v21, v27, vcc
	v_cmp_ge_f32_e32 vcc, v6, v7
	s_nop 1
	v_addc_co_u32_e32 v15, vcc, v15, v29, vcc
	v_cmp_eq_u32_e32 vcc, v15, v12
	v_ldexp_f32 v12, v17, v18
	s_nop 0
	v_cndmask_b32_e32 v19, v13, v7, vcc
	v_sub_f32_e32 v13, v3, v14
	v_mul_f32_e32 v15, 0x3fb8aa3b, v13
	v_fma_f32 v17, v13, s2, -v15
	v_rndne_f32_e32 v18, v15
	v_fmac_f32_e32 v17, 0x32a5705f, v13
	v_sub_f32_e32 v15, v15, v18
	v_add_f32_e32 v15, v15, v17
	v_exp_f32_e32 v15, v15
	v_cvt_i32_f32_e32 v17, v18
	v_cmp_ngt_f32_e32 vcc, s3, v16
	v_mov_b32_e32 v18, 0x7f800000
	v_cmp_lt_f32_e64 s[10:11], v3, v19
	v_cndmask_b32_e32 v12, 0, v12, vcc
	v_cmp_nlt_f32_e32 vcc, s6, v16
	v_ldexp_f32 v15, v15, v17
	v_cmp_lt_f32_e64 s[8:9], v9, v19
	v_cndmask_b32_e32 v12, v18, v12, vcc
	v_cmp_ngt_f32_e32 vcc, s3, v13
	v_cmp_lt_f32_e64 s[14:15], v8, v19
	v_cmp_lt_f32_e64 s[4:5], v5, v19
	v_cndmask_b32_e32 v15, 0, v15, vcc
	v_cmp_nlt_f32_e32 vcc, s6, v13
	v_cmp_lt_f32_e64 s[12:13], v4, v19
	s_nop 0
	v_cndmask_b32_e32 v13, v18, v15, vcc
	v_sub_f32_e32 v15, v8, v14
	v_mul_f32_e32 v16, 0x3fb8aa3b, v15
	v_fma_f32 v17, v15, s2, -v16
	v_rndne_f32_e32 v20, v16
	v_fmac_f32_e32 v17, 0x32a5705f, v15
	v_sub_f32_e32 v16, v16, v20
	v_add_f32_e32 v16, v16, v17
	v_exp_f32_e32 v16, v16
	v_cvt_i32_f32_e32 v17, v20
	v_cmp_lt_f32_e32 vcc, v2, v19
	v_cndmask_b32_e64 v13, v13, 0, s[10:11]
	v_ldexp_f32 v3, v16, v17
	v_sub_f32_e32 v16, v9, v14
	v_mul_f32_e32 v17, 0x3fb8aa3b, v16
	v_fma_f32 v20, v16, s2, -v17
	v_rndne_f32_e32 v21, v17
	v_fmac_f32_e32 v20, 0x32a5705f, v16
	v_sub_f32_e32 v17, v17, v21
	v_add_f32_e32 v17, v17, v20
	v_exp_f32_e32 v17, v17
	v_cvt_i32_f32_e32 v20, v21
	v_cndmask_b32_e64 v12, v12, 0, vcc
	v_cmp_ngt_f32_e32 vcc, s3, v15
	s_nop 1
	v_cndmask_b32_e32 v3, 0, v3, vcc
	v_cmp_nlt_f32_e32 vcc, s6, v15
	v_ldexp_f32 v15, v17, v20
	s_nop 0
	v_cndmask_b32_e32 v3, v18, v3, vcc
	v_cmp_ngt_f32_e32 vcc, s3, v16
	v_cndmask_b32_e64 v8, v3, 0, s[14:15]
	s_nop 0
	v_cndmask_b32_e32 v15, 0, v15, vcc
	v_cmp_nlt_f32_e32 vcc, s6, v16
	v_sub_f32_e32 v16, v4, v14
	v_mul_f32_e32 v17, 0x3fb8aa3b, v16
	v_fma_f32 v20, v16, s2, -v17
	v_rndne_f32_e32 v21, v17
	v_fmac_f32_e32 v20, 0x32a5705f, v16
	v_sub_f32_e32 v17, v17, v21
	v_add_f32_e32 v17, v17, v20
	v_exp_f32_e32 v17, v17
	v_cvt_i32_f32_e32 v20, v21
	v_cndmask_b32_e32 v15, v18, v15, vcc
	v_cndmask_b32_e64 v9, v15, 0, s[8:9]
	v_sub_f32_e32 v15, v5, v14
	v_ldexp_f32 v3, v17, v20
	v_mul_f32_e32 v17, 0x3fb8aa3b, v15
	v_fma_f32 v20, v15, s2, -v17
	v_rndne_f32_e32 v21, v17
	v_fmac_f32_e32 v20, 0x32a5705f, v15
	v_sub_f32_e32 v17, v17, v21
	v_add_f32_e32 v17, v17, v20
	v_exp_f32_e32 v17, v17
	v_cvt_i32_f32_e32 v20, v21
	v_cmp_ngt_f32_e32 vcc, s3, v16
	s_nop 1
	v_cndmask_b32_e32 v3, 0, v3, vcc
	v_cmp_nlt_f32_e32 vcc, s6, v16
	v_ldexp_f32 v16, v17, v20
	s_nop 0
	v_cndmask_b32_e32 v3, v18, v3, vcc
	v_cmp_ngt_f32_e32 vcc, s3, v15
	v_cndmask_b32_e64 v4, v3, 0, s[12:13]
	s_nop 0
	v_cndmask_b32_e32 v16, 0, v16, vcc
	v_cmp_nlt_f32_e32 vcc, s6, v15
	s_nop 1
	v_cndmask_b32_e32 v15, v18, v16, vcc
	v_sub_f32_e32 v16, v6, v14
	v_mul_f32_e32 v17, 0x3fb8aa3b, v16
	v_fma_f32 v20, v16, s2, -v17
	v_rndne_f32_e32 v21, v17
	v_fmac_f32_e32 v20, 0x32a5705f, v16
	v_sub_f32_e32 v17, v17, v21
	v_add_f32_e32 v17, v17, v20
	v_exp_f32_e32 v17, v17
	v_cvt_i32_f32_e32 v20, v21
	v_sub_f32_e32 v14, v7, v14
	v_cndmask_b32_e64 v5, v15, 0, s[4:5]
	v_mul_f32_e32 v15, 0x3fb8aa3b, v14
	v_ldexp_f32 v3, v17, v20
	v_fma_f32 v17, v14, s2, -v15
	v_rndne_f32_e32 v20, v15
	v_fmac_f32_e32 v17, 0x32a5705f, v14
	v_sub_f32_e32 v15, v15, v20
	v_add_f32_e32 v15, v15, v17
	v_exp_f32_e32 v15, v15
	v_cvt_i32_f32_e32 v17, v20
	v_cmp_ngt_f32_e32 vcc, s3, v16
	v_ldexp_f32 v15, v15, v17
	s_nop 0
	v_cndmask_b32_e32 v3, 0, v3, vcc
	v_cmp_nlt_f32_e32 vcc, s6, v16
	s_nop 1
	v_cndmask_b32_e32 v3, v18, v3, vcc
	v_cmp_ngt_f32_e32 vcc, s3, v14
	v_cmp_lt_f32_e64 s[2:3], v7, v19
	s_nop 0
	v_cndmask_b32_e32 v15, 0, v15, vcc
	v_cmp_nlt_f32_e32 vcc, s6, v14
	v_cmp_lt_f32_e64 s[6:7], v6, v19
	v_lshlrev_b64 v[6:7], 5, v[10:11]
	v_cndmask_b32_e32 v14, v18, v15, vcc
	v_cndmask_b32_e64 v15, v14, 0, s[2:3]
	v_cndmask_b32_e64 v14, v3, 0, s[6:7]
	v_add_f32_e32 v3, v12, v13
	v_add_f32_e32 v3, v8, v3
	v_add_f32_e32 v3, v9, v3
	v_add_f32_e32 v3, v4, v3
	v_add_f32_e32 v3, v5, v3
	v_add_f32_e32 v3, v14, v3
	v_add_f32_e32 v3, v15, v3
	v_div_scale_f32 v18, s[16:17], v3, v3, 1.0
	v_rcp_f32_e32 v20, v18
	v_cmp_nlt_f32_e64 s[16:17], v2, v19
	v_lshl_add_u64 v[16:17], s[18:19], 0, v[6:7]
	v_fma_f32 v2, -v18, v20, 1.0
	v_fmac_f32_e32 v20, v2, v20
	v_div_scale_f32 v2, vcc, 1.0, v3, 1.0
	v_mul_f32_e32 v6, v2, v20
	v_fma_f32 v7, -v18, v6, v2
	v_fmac_f32_e32 v6, v7, v20
	v_fma_f32 v2, -v18, v6, v2
	v_div_fmas_f32 v2, v2, v20, v6
	v_div_fixup_f32 v18, v2, v3, 1.0
	v_pk_mul_f32 v[6:7], v[12:13], v[18:19] op_sel_hi:[1,0]
	v_lshlrev_b32_e32 v12, 3, v10
	v_pk_mul_f32 v[8:9], v[8:9], v[18:19] op_sel_hi:[1,0]
	v_pk_mul_f32 v[2:3], v[4:5], v[18:19] op_sel_hi:[1,0]
	v_pk_mul_f32 v[4:5], v[14:15], v[18:19] op_sel_hi:[1,0]
	v_mov_b32_e32 v14, 0
	v_ashrrev_i32_e32 v13, 31, v12
	global_store_dwordx4 v[16:17], v[6:9], off sc1
	global_store_dwordx4 v[16:17], v[2:5], off offset:16 sc1
	s_and_saveexec_b64 s[18:19], s[16:17]
	s_cbranch_execz .LBB8_42
	v_lshlrev_b64 v[14:15], 2, v[12:13]
	v_lshl_add_u64 v[16:17], s[20:21], 0, v[14:15]
	v_lshl_add_u64 v[14:15], s[22:23], 0, v[14:15]
	v_mov_b32_e32 v18, 0
	global_store_dword v[14:15], v18, off
	global_store_dword v[16:17], v6, off
	v_mov_b32_e32 v14, 1

.Lgsk_g3_8:
	v_fma_f32 v83, |v83|, v86, v83
	v_fma_f32 v88, |v88|, v91, v88
	v_fma_f32 v93, |v93|, v96, v93
	v_fma_f32 v98, |v98|, v101, v98
	v_cvt_f16_f32_e32 v82, v83
	v_cvt_f16_f32_e32 v87, v88
	v_cvt_f16_f32_e32 v92, v93
	v_cvt_f16_f32_e32 v97, v98
	v_fma_mixlo_f16 v84, v83, 1.0, -v82 op_sel_hi:[0,0,1]
	v_fma_mixlo_f16 v89, v88, 1.0, -v87 op_sel_hi:[0,0,1]
	v_fma_mixlo_f16 v94, v93, 1.0, -v92 op_sel_hi:[0,0,1]
	v_fma_mixlo_f16 v99, v98, 1.0, -v97 op_sel_hi:[0,0,1]
	s_waitcnt lgkmcnt(0)
	s_sub_i32 s2, s42, 0
	v_cmp_gt_i32_e32 vcc, s2, v75
	s_and_saveexec_b64 s[44:45], vcc
	s_add_u32 s2, s38, 0x0
	s_addc_u32 s3, s39, 0
	global_store_dwordx4 v76, v[104:107], s[2:3] sc1
	s_add_u32 s2, s40, 0x0
	s_addc_u32 s3, s41, 0
	global_store_dwordx4 v76, v[120:123], s[2:3] sc1
	s_mov_b64 exec, s[44:45]
	s_sub_i32 s2, s42, 8
	v_cmp_gt_i32_e32 vcc, s2, v75
	s_and_saveexec_b64 s[44:45], vcc
	s_add_u32 s2, s38, 0x8000
	s_addc_u32 s3, s39, 0
	global_store_dwordx4 v76, v[108:111], s[2:3] sc1
	s_add_u32 s2, s40, 0x8000
	s_addc_u32 s3, s41, 0
	global_store_dwordx4 v76, v[124:127], s[2:3] sc1
	s_mov_b64 exec, s[44:45]
	s_sub_i32 s2, s42, 16
	v_cmp_gt_i32_e32 vcc, s2, v75
	s_and_saveexec_b64 s[44:45], vcc
	s_add_u32 s2, s38, 0x10000
	s_addc_u32 s3, s39, 0
	global_store_dwordx4 v76, v[112:115], s[2:3] sc1
	s_add_u32 s2, s40, 0x10000
	s_addc_u32 s3, s41, 0
	global_store_dwordx4 v76, v[128:131], s[2:3] sc1
	s_mov_b64 exec, s[44:45]
	s_sub_i32 s2, s42, 24
	v_cmp_gt_i32_e32 vcc, s2, v75
	s_and_saveexec_b64 s[44:45], vcc
	s_add_u32 s2, s38, 0x18000
	s_addc_u32 s3, s39, 0
	global_store_dwordx4 v76, v[116:119], s[2:3] sc1
	s_add_u32 s2, s40, 0x18000
	s_addc_u32 s3, s41, 0
	global_store_dwordx4 v76, v[132:135], s[2:3] sc1
	s_mov_b64 exec, s[44:45]
	ds_write_b16 v71, v82
	ds_write_b16 v71, v87 offset:144
	ds_write_b16 v71, v92 offset:288
	ds_write_b16 v71, v97 offset:432
	ds_write_b16 v71, v84 offset:4608
	ds_write_b16 v71, v89 offset:4752
	ds_write_b16 v71, v94 offset:4896
	ds_write_b16 v71, v99 offset:5040
	v_fma_f32 v82, v26, s61, v141
	v_fma_f32 v87, v27, s61, v141
	v_fma_f32 v92, v28, s61, v141
	v_fma_f32 v97, v29, s61, v141
	v_fma_f32 v83, v26, s62, v145
	v_fma_f32 v88, v27, s62, v145
	v_fma_f32 v93, v28, s62, v145
	v_fma_f32 v98, v29, s62, v145
	v_mul_f32_e32 v84, v82, v82
	v_mul_f32_e32 v89, v87, v87
	v_mul_f32_e32 v94, v92, v92
	v_mul_f32_e32 v99, v97, v97
	v_cmp_lt_f32_e64 s[64:65], |v82|, 1.0
	v_cmp_lt_f32_e64 s[66:67], |v87|, 1.0
	v_cmp_lt_f32_e64 s[68:69], |v92|, 1.0
	v_cmp_lt_f32_e64 s[70:71], |v97|, 1.0
	v_fma_f32 v86, v84, v103, s56
	v_fma_f32 v91, v89, v103, s56
	v_fma_f32 v96, v94, v103, s56
	v_fma_f32 v101, v99, v103, s56
	s_and_b64 s[72:73], s[64:65], s[66:67]
	s_and_b64 s[74:75], s[68:69], s[70:71]
	s_and_b64 s[72:73], s[72:73], s[74:75]
	v_fma_f32 v86, v84, v86, s57
	v_fma_f32 v91, v89, v91, s57
	v_fma_f32 v96, v94, v96, s57
	v_fma_f32 v101, v99, v101, s57
	v_fma_f32 v86, v84, v86, s58
	v_fma_f32 v91, v89, v91, s58
	v_fma_f32 v96, v94, v96, s58
	v_fma_f32 v101, v99, v101, s58
	v_fma_f32 v86, v84, v86, s59
	v_fma_f32 v91, v89, v91, s59
	v_fma_f32 v96, v94, v96, s59
	v_fma_f32 v101, v99, v101, s59
	v_fma_f32 v86, v84, v86, s60
	v_fma_f32 v91, v89, v91, s60
	v_fma_f32 v96, v94, v96, s60
	v_fma_f32 v101, v99, v101, s60
	v_fma_f32 v86, |v82|, v86, |v82|
	v_fma_f32 v91, |v87|, v91, |v87|
	v_fma_f32 v96, |v92|, v96, |v92|
	v_fma_f32 v101, |v97|, v101, |v97|
	s_cmp_eq_u64 s[72:73], exec
	s_cbranch_scc1 .Lgsk_g3_9
	v_fma_f32 v85, |v82|, v102, s50
	v_fma_f32 v90, |v87|, v102, s50
	v_fma_f32 v95, |v92|, v102, s50
	v_fma_f32 v100, |v97|, v102, s50
	v_fma_f32 v85, |v82|, v85, s51
	v_fma_f32 v90, |v87|, v90, s51
	v_fma_f32 v95, |v92|, v95, s51
	v_fma_f32 v100, |v97|, v100, s51
	v_fma_f32 v85, |v82|, v85, s52
	v_fma_f32 v90, |v87|, v90, s52
	v_fma_f32 v95, |v92|, v95, s52
	v_fma_f32 v100, |v97|, v100, s52
	v_fma_f32 v85, |v82|, v85, s53
	v_fma_f32 v90, |v87|, v90, s53
	v_fma_f32 v95, |v92|, v95, s53
	v_fma_f32 v100, |v97|, v100, s53
	v_fma_f32 v85, |v82|, v85, s54
	v_fma_f32 v90, |v87|, v90, s54
	v_fma_f32 v95, |v92|, v95, s54
	v_fma_f32 v100, |v97|, v100, s54
	v_fma_f32 v85, |v82|, v85, s55
	v_fma_f32 v90, |v87|, v90, s55
	v_fma_f32 v95, |v92|, v95, s55
	v_fma_f32 v100, |v97|, v100, s55
	v_fma_f32 v85, |v82|, v85, |v82|
	v_fma_f32 v90, |v87|, v90, |v87|
	v_fma_f32 v95, |v92|, v95, |v92|
	v_fma_f32 v100, |v97|, v100, |v97|
	v_mul_f32_e32 v85, 0xbfb8aa3b, v85
	v_mul_f32_e32 v90, 0xbfb8aa3b, v90
	v_mul_f32_e32 v95, 0xbfb8aa3b, v95
	v_mul_f32_e32 v100, 0xbfb8aa3b, v100
	v_exp_f32_e32 v85, v85
	v_exp_f32_e32 v90, v90
	v_exp_f32_e32 v95, v95
	v_exp_f32_e32 v100, v100
	s_nop 0
	v_sub_f32_e32 v85, 1.0, v85
	v_sub_f32_e32 v90, 1.0, v90
	v_sub_f32_e32 v95, 1.0, v95
	v_sub_f32_e32 v100, 1.0, v100
	v_cndmask_b32_e64 v86, v85, v86, s[64:65]
	v_cndmask_b32_e64 v91, v90, v91, s[66:67]
	v_cndmask_b32_e64 v96, v95, v96, s[68:69]
	v_cndmask_b32_e64 v101, v100, v101, s[70:71]

.Lgsk_g3_15:
	v_fma_f32 v83, |v83|, v86, v83
	v_fma_f32 v88, |v88|, v91, v88
	v_fma_f32 v93, |v93|, v96, v93
	v_fma_f32 v98, |v98|, v101, v98
	v_cvt_f16_f32_e32 v82, v83
	v_cvt_f16_f32_e32 v87, v88
	v_cvt_f16_f32_e32 v92, v93
	v_cvt_f16_f32_e32 v97, v98
	v_fma_mixlo_f16 v84, v83, 1.0, -v82 op_sel_hi:[0,0,1]
	v_fma_mixlo_f16 v89, v88, 1.0, -v87 op_sel_hi:[0,0,1]
	v_fma_mixlo_f16 v94, v93, 1.0, -v92 op_sel_hi:[0,0,1]
	v_fma_mixlo_f16 v99, v98, 1.0, -v97 op_sel_hi:[0,0,1]
	ds_write_b16 v71, v82 offset:2400
	ds_write_b16 v71, v87 offset:2544
	ds_write_b16 v71, v92 offset:2688
	ds_write_b16 v71, v97 offset:2832
	ds_write_b16 v71, v84 offset:7008
	ds_write_b16 v71, v89 offset:7152
	ds_write_b16 v71, v94 offset:7296
	ds_write_b16 v71, v99 offset:7440
	ds_read_b128 v[104:107], v74
	ds_read_b128 v[108:111], v74 offset:1152
	ds_read_b128 v[112:115], v74 offset:2304
	ds_read_b128 v[116:119], v74 offset:3456
	ds_read_b128 v[120:123], v74 offset:4608
	ds_read_b128 v[124:127], v74 offset:5760
	ds_read_b128 v[128:131], v74 offset:6912
	ds_read_b128 v[132:135], v74 offset:8064
	s_waitcnt lgkmcnt(0)
	s_sub_i32 s2, s42, 32
	v_cmp_gt_i32_e32 vcc, s2, v75
	s_and_saveexec_b64 s[44:45], vcc
	s_add_u32 s2, s38, 0x20000
	s_addc_u32 s3, s39, 0
	global_store_dwordx4 v76, v[104:107], s[2:3] sc1
	s_add_u32 s2, s40, 0x20000
	s_addc_u32 s3, s41, 0
	global_store_dwordx4 v76, v[120:123], s[2:3] sc1
	s_mov_b64 exec, s[44:45]
	s_sub_i32 s2, s42, 40
	v_cmp_gt_i32_e32 vcc, s2, v75
	s_and_saveexec_b64 s[44:45], vcc
	s_add_u32 s2, s38, 0x28000
	s_addc_u32 s3, s39, 0
	global_store_dwordx4 v76, v[108:111], s[2:3] sc1
	s_add_u32 s2, s40, 0x28000
	s_addc_u32 s3, s41, 0
	global_store_dwordx4 v76, v[124:127], s[2:3] sc1
	s_mov_b64 exec, s[44:45]
	s_sub_i32 s2, s42, 48
	v_cmp_gt_i32_e32 vcc, s2, v75
	s_and_saveexec_b64 s[44:45], vcc
	s_add_u32 s2, s38, 0x30000
	s_addc_u32 s3, s39, 0
	global_store_dwordx4 v76, v[112:115], s[2:3] sc1
	s_add_u32 s2, s40, 0x30000
	s_addc_u32 s3, s41, 0
	global_store_dwordx4 v76, v[128:131], s[2:3] sc1
	s_mov_b64 exec, s[44:45]
	s_sub_i32 s2, s42, 56
	v_cmp_gt_i32_e32 vcc, s2, v75
	s_and_saveexec_b64 s[44:45], vcc
	s_add_u32 s2, s38, 0x38000
	s_addc_u32 s3, s39, 0
	global_store_dwordx4 v76, v[116:119], s[2:3] sc1
	s_add_u32 s2, s40, 0x38000
	s_addc_u32 s3, s41, 0
	global_store_dwordx4 v76, v[132:135], s[2:3] sc1
	s_mov_b64 exec, s[44:45]
	s_endpgm

.Lgsk_g1_8:
	v_fma_f32 v83, |v83|, v86, v83
	v_fma_f32 v88, |v88|, v91, v88
	v_fma_f32 v93, |v93|, v96, v93
	v_fma_f32 v98, |v98|, v101, v98
	v_cvt_f16_f32_e32 v82, v83
	v_cvt_f16_f32_e32 v87, v88
	v_cvt_f16_f32_e32 v92, v93
	v_cvt_f16_f32_e32 v97, v98
	s_waitcnt lgkmcnt(0)
	s_sub_i32 s2, s42, 0
	v_cmp_gt_i32_e32 vcc, s2, v75
	s_and_saveexec_b64 s[44:45], vcc
	s_add_u32 s2, s38, 0x0
	s_addc_u32 s3, s39, 0
	global_store_dwordx4 v76, v[104:107], s[2:3] sc1
	s_mov_b64 exec, s[44:45]
	s_sub_i32 s2, s42, 8
	v_cmp_gt_i32_e32 vcc, s2, v75
	s_and_saveexec_b64 s[44:45], vcc
	s_add_u32 s2, s38, 0x8000
	s_addc_u32 s3, s39, 0
	global_store_dwordx4 v76, v[108:111], s[2:3] sc1
	s_mov_b64 exec, s[44:45]
	s_sub_i32 s2, s42, 16
	v_cmp_gt_i32_e32 vcc, s2, v75
	s_and_saveexec_b64 s[44:45], vcc
	s_add_u32 s2, s38, 0x10000
	s_addc_u32 s3, s39, 0
	global_store_dwordx4 v76, v[112:115], s[2:3] sc1
	s_mov_b64 exec, s[44:45]
	s_sub_i32 s2, s42, 24
	v_cmp_gt_i32_e32 vcc, s2, v75
	s_and_saveexec_b64 s[44:45], vcc
	s_add_u32 s2, s38, 0x18000
	s_addc_u32 s3, s39, 0
	global_store_dwordx4 v76, v[116:119], s[2:3] sc1
	s_mov_b64 exec, s[44:45]
	ds_write_b16 v71, v82
	ds_write_b16 v71, v87 offset:144
	ds_write_b16 v71, v92 offset:288
	ds_write_b16 v71, v97 offset:432
	v_fma_f32 v82, v26, s61, v137
	v_fma_f32 v87, v27, s61, v137
	v_fma_f32 v92, v28, s61, v137
	v_fma_f32 v97, v29, s61, v137
	v_fma_f32 v83, v26, s62, v141
	v_fma_f32 v88, v27, s62, v141
	v_fma_f32 v93, v28, s62, v141
	v_fma_f32 v98, v29, s62, v141
	v_mul_f32_e32 v84, v82, v82
	v_mul_f32_e32 v89, v87, v87
	v_mul_f32_e32 v94, v92, v92
	v_mul_f32_e32 v99, v97, v97
	v_cmp_lt_f32_e64 s[64:65], |v82|, 1.0
	v_cmp_lt_f32_e64 s[66:67], |v87|, 1.0
	v_cmp_lt_f32_e64 s[68:69], |v92|, 1.0
	v_cmp_lt_f32_e64 s[70:71], |v97|, 1.0
	v_fma_f32 v86, v84, v103, s56
	v_fma_f32 v91, v89, v103, s56
	v_fma_f32 v96, v94, v103, s56
	v_fma_f32 v101, v99, v103, s56
	s_and_b64 s[72:73], s[64:65], s[66:67]
	s_and_b64 s[74:75], s[68:69], s[70:71]
	s_and_b64 s[72:73], s[72:73], s[74:75]
	v_fma_f32 v86, v84, v86, s57
	v_fma_f32 v91, v89, v91, s57
	v_fma_f32 v96, v94, v96, s57
	v_fma_f32 v101, v99, v101, s57
	v_fma_f32 v86, v84, v86, s58
	v_fma_f32 v91, v89, v91, s58
	v_fma_f32 v96, v94, v96, s58
	v_fma_f32 v101, v99, v101, s58
	v_fma_f32 v86, v84, v86, s59
	v_fma_f32 v91, v89, v91, s59
	v_fma_f32 v96, v94, v96, s59
	v_fma_f32 v101, v99, v101, s59
	v_fma_f32 v86, v84, v86, s60
	v_fma_f32 v91, v89, v91, s60
	v_fma_f32 v96, v94, v96, s60
	v_fma_f32 v101, v99, v101, s60
	v_fma_f32 v86, |v82|, v86, |v82|
	v_fma_f32 v91, |v87|, v91, |v87|
	v_fma_f32 v96, |v92|, v96, |v92|
	v_fma_f32 v101, |v97|, v101, |v97|
	s_cmp_eq_u64 s[72:73], exec
	s_cbranch_scc1 .Lgsk_g1_9
	v_fma_f32 v85, |v82|, v102, s50
	v_fma_f32 v90, |v87|, v102, s50
	v_fma_f32 v95, |v92|, v102, s50
	v_fma_f32 v100, |v97|, v102, s50
	v_fma_f32 v85, |v82|, v85, s51
	v_fma_f32 v90, |v87|, v90, s51
	v_fma_f32 v95, |v92|, v95, s51
	v_fma_f32 v100, |v97|, v100, s51
	v_fma_f32 v85, |v82|, v85, s52
	v_fma_f32 v90, |v87|, v90, s52
	v_fma_f32 v95, |v92|, v95, s52
	v_fma_f32 v100, |v97|, v100, s52
	v_fma_f32 v85, |v82|, v85, s53
	v_fma_f32 v90, |v87|, v90, s53
	v_fma_f32 v95, |v92|, v95, s53
	v_fma_f32 v100, |v97|, v100, s53
	v_fma_f32 v85, |v82|, v85, s54
	v_fma_f32 v90, |v87|, v90, s54
	v_fma_f32 v95, |v92|, v95, s54
	v_fma_f32 v100, |v97|, v100, s54
	v_fma_f32 v85, |v82|, v85, s55
	v_fma_f32 v90, |v87|, v90, s55
	v_fma_f32 v95, |v92|, v95, s55
	v_fma_f32 v100, |v97|, v100, s55
	v_fma_f32 v85, |v82|, v85, |v82|
	v_fma_f32 v90, |v87|, v90, |v87|
	v_fma_f32 v95, |v92|, v95, |v92|
	v_fma_f32 v100, |v97|, v100, |v97|
	v_mul_f32_e32 v85, 0xbfb8aa3b, v85
	v_mul_f32_e32 v90, 0xbfb8aa3b, v90
	v_mul_f32_e32 v95, 0xbfb8aa3b, v95
	v_mul_f32_e32 v100, 0xbfb8aa3b, v100
	v_exp_f32_e32 v85, v85
	v_exp_f32_e32 v90, v90
	v_exp_f32_e32 v95, v95
	v_exp_f32_e32 v100, v100
	s_nop 0
	v_sub_f32_e32 v85, 1.0, v85
	v_sub_f32_e32 v90, 1.0, v90
	v_sub_f32_e32 v95, 1.0, v95
	v_sub_f32_e32 v100, 1.0, v100
	v_cndmask_b32_e64 v86, v85, v86, s[64:65]
	v_cndmask_b32_e64 v91, v90, v91, s[66:67]
	v_cndmask_b32_e64 v96, v95, v96, s[68:69]
	v_cndmask_b32_e64 v101, v100, v101, s[70:71]

.Lgsk_g1_15:
	v_fma_f32 v83, |v83|, v86, v83
	v_fma_f32 v88, |v88|, v91, v88
	v_fma_f32 v93, |v93|, v96, v93
	v_fma_f32 v98, |v98|, v101, v98
	v_cvt_f16_f32_e32 v82, v83
	v_cvt_f16_f32_e32 v87, v88
	v_cvt_f16_f32_e32 v92, v93
	v_cvt_f16_f32_e32 v97, v98
	ds_write_b16 v71, v82 offset:2400
	ds_write_b16 v71, v87 offset:2544
	ds_write_b16 v71, v92 offset:2688
	ds_write_b16 v71, v97 offset:2832
	ds_read_b128 v[104:107], v74
	ds_read_b128 v[108:111], v74 offset:1152
	ds_read_b128 v[112:115], v74 offset:2304
	ds_read_b128 v[116:119], v74 offset:3456
	s_waitcnt lgkmcnt(0)
	s_sub_i32 s2, s42, 32
	v_cmp_gt_i32_e32 vcc, s2, v75
	s_and_saveexec_b64 s[44:45], vcc
	s_add_u32 s2, s38, 0x20000
	s_addc_u32 s3, s39, 0
	global_store_dwordx4 v76, v[104:107], s[2:3] sc1
	s_mov_b64 exec, s[44:45]
	s_sub_i32 s2, s42, 40
	v_cmp_gt_i32_e32 vcc, s2, v75
	s_and_saveexec_b64 s[44:45], vcc
	s_add_u32 s2, s38, 0x28000
	s_addc_u32 s3, s39, 0
	global_store_dwordx4 v76, v[108:111], s[2:3] sc1
	s_mov_b64 exec, s[44:45]
	s_sub_i32 s2, s42, 48
	v_cmp_gt_i32_e32 vcc, s2, v75
	s_and_saveexec_b64 s[44:45], vcc
	s_add_u32 s2, s38, 0x30000
	s_addc_u32 s3, s39, 0
	global_store_dwordx4 v76, v[112:115], s[2:3] sc1
	s_mov_b64 exec, s[44:45]
	s_sub_i32 s2, s42, 56
	v_cmp_gt_i32_e32 vcc, s2, v75
	s_and_saveexec_b64 s[44:45], vcc
	s_add_u32 s2, s38, 0x38000
	s_addc_u32 s3, s39, 0
	global_store_dwordx4 v76, v[116:119], s[2:3] sc1
	s_mov_b64 exec, s[44:45]
	s_endpgm

_Z12wprep_kernelILb1EEvPKfPDF16_S2_ii:
	s_load_dwordx8 s[8:15], s[0:1], 0x0
	s_lshl_b32 s6, s3, 6
	s_lshl_b32 s0, s2, 6
	v_lshrrev_b32_e32 v1, 4, v0
	v_lshlrev_b32_e32 v2, 4, v0
	s_waitcnt lgkmcnt(0)
	s_ashr_i32 s3, s14, 31
	s_mul_i32 s16, s15, s4
	s_mul_hi_i32 s7, s15, s4
	s_mul_i32 s1, s16, s3
	s_mul_hi_u32 s2, s16, s14
	s_add_i32 s1, s2, s1
	s_mul_i32 s2, s7, s14
	s_add_i32 s5, s1, s2
	s_mul_i32 s4, s16, s14
	s_lshl_b64 s[4:5], s[4:5], 2
	s_add_u32 s2, s8, s4
	s_addc_u32 s8, s9, s5
	s_ashr_i32 s1, s0, 31
	s_lshl_b64 s[4:5], s[0:1], 2
	s_add_u32 s4, s2, s4
	s_addc_u32 s5, s8, s5
	v_and_b32_e32 v18, 0xf0, v2
	v_mov_b32_e32 v19, 0
	v_or_b32_e32 v16, s6, v1
	v_lshl_add_u64 v[14:15], s[4:5], 0, v[18:19]
	v_mad_i64_i32 v[2:3], s[4:5], s15, v16, 0
	v_lshl_add_u64 v[10:11], v[2:3], 2, v[14:15]
	v_or_b32_e32 v2, 16, v16
	v_mad_i64_i32 v[2:3], s[4:5], s15, v2, 0
	v_lshl_add_u64 v[12:13], v[2:3], 2, v[14:15]
	global_load_dwordx4 v[2:5], v[10:11], off nt
	global_load_dwordx4 v[6:9], v[12:13], off nt
	v_or_b32_e32 v10, 32, v16
	v_mad_i64_i32 v[10:11], s[4:5], s15, v10, 0
	v_lshl_add_u64 v[10:11], v[10:11], 2, v[14:15]
	v_or_b32_e32 v16, 48, v16
	global_load_dwordx4 v[10:13], v[10:11], off nt
	v_mad_i64_i32 v[16:17], s[4:5], s15, v16, 0
	v_lshl_add_u64 v[14:15], v[16:17], 2, v[14:15]
	global_load_dwordx4 v[14:17], v[14:15], off nt
	s_movk_i32 s4, 0x104
	v_mad_u32_u24 v1, v1, s4, v18
	v_lshrrev_b32_e32 v18, 3, v0
	s_movk_i32 s5, 0x820
	v_and_b32_e32 v22, 7, v0
	v_lshlrev_b32_e32 v0, 2, v18
	v_mad_u32_u24 v0, v22, s5, v0
	v_lshl_or_b32 v20, v22, 3, s6
	v_add_u32_e32 v23, 0x1040, v1
	v_add_u32_e32 v24, 0x1048, v1
	v_add_u32_e32 v25, 0x2080, v1
	v_add_u32_e32 v26, 0x2088, v1
	v_add_u32_e32 v27, 0x30c0, v1
	v_add_u32_e32 v28, 0x30c8, v1
	v_add_u32_e32 v22, 0x400, v0
	s_mov_b32 s2, 0x45800000
	s_add_u32 s0, s16, s0
	s_addc_u32 s1, s7, s1
	s_ashr_i32 s4, s6, 31
	v_mov_b32_e32 v21, s4
	s_waitcnt vmcnt(3)
	ds_write2_b32 v1, v2, v3 offset1:1
	ds_write2_b32 v1, v4, v5 offset0:2 offset1:3
	s_waitcnt vmcnt(2)
	ds_write2_b32 v23, v6, v7 offset1:1
	ds_write2_b32 v24, v8, v9 offset1:1
	s_waitcnt vmcnt(1)
	ds_write2_b32 v25, v10, v11 offset1:1
	ds_write2_b32 v26, v12, v13 offset1:1
	s_waitcnt vmcnt(0)
	ds_write2_b32 v27, v14, v15 offset1:1
	ds_write2_b32 v28, v16, v17 offset1:1
	s_waitcnt lgkmcnt(0)
	s_barrier
	ds_read2_b32 v[8:9], v0 offset1:32
	ds_read2_b32 v[10:11], v0 offset0:65 offset1:97
	ds_read2_b32 v[32:33], v0 offset0:130 offset1:162
	ds_read2_b32 v[12:13], v0 offset0:195 offset1:227
	ds_read2_b32 v[34:35], v22 offset0:4 offset1:36
	ds_read2_b32 v[14:15], v22 offset0:69 offset1:101
	ds_read2_b32 v[36:37], v22 offset0:134 offset1:166
	ds_read2_b32 v[16:17], v22 offset0:199 offset1:231
	s_waitcnt lgkmcnt(7)
	v_fma_mixlo_f16 v0, v8, s2, 0
	s_waitcnt lgkmcnt(5)
	v_mov_b32_e32 v2, v32
	s_waitcnt lgkmcnt(4)
	v_mov_b32_e32 v3, v12
	v_fma_mixlo_f16 v5, v10, s2, 0
	s_waitcnt lgkmcnt(3)
	v_mov_b32_e32 v22, v34
	s_waitcnt lgkmcnt(2)
	v_mov_b32_e32 v23, v14
	s_waitcnt lgkmcnt(1)
	v_mov_b32_e32 v24, v36
	s_waitcnt lgkmcnt(0)
	v_mov_b32_e32 v25, v16
	v_fma_mixlo_f16 v0, v8, s2, -v0 op_sel_hi:[0,0,1]
	v_pk_mul_f32 v[6:7], v[2:3], s[2:3] op_sel_hi:[1,0]
	v_pk_mul_f32 v[26:27], v[22:23], s[2:3] op_sel_hi:[1,0]
	v_pk_mul_f32 v[28:29], v[24:25], s[2:3] op_sel_hi:[1,0]
	v_fma_mixhi_f16 v0, v10, s2, -v5 op_sel_hi:[0,0,1]
	v_cvt_pk_f16_f32 v5, v6, v7
	v_cvt_f32_f16_e32 v30, v5
	v_cvt_f32_f16_sdwa v31, v5 dst_sel:DWORD dst_unused:UNUSED_PAD src0_sel:WORD_1
	v_cvt_pk_f16_f32 v6, v26, v27
	v_cvt_pk_f16_f32 v7, v28, v29
	v_cvt_f32_f16_e32 v26, v6
	v_cvt_f32_f16_sdwa v27, v6 dst_sel:DWORD dst_unused:UNUSED_PAD src0_sel:WORD_1
	v_cvt_f32_f16_e32 v28, v7
	v_cvt_f32_f16_sdwa v29, v7 dst_sel:DWORD dst_unused:UNUSED_PAD src0_sel:WORD_1
	v_mul_f32_e32 v1, 0x45800000, v8
	v_mul_f32_e32 v4, 0x45800000, v10
	v_pk_fma_f32 v[2:3], v[2:3], s[2:3], v[30:31] op_sel_hi:[1,0,1] neg_lo:[0,0,1] neg_hi:[0,0,1]
	v_cvt_pk_f16_f32 v4, v1, v4
	v_cvt_pk_f16_f32 v1, v2, v3
	v_pk_fma_f32 v[2:3], v[22:23], s[2:3], v[26:27] op_sel_hi:[1,0,1] neg_lo:[0,0,1] neg_hi:[0,0,1]
	v_pk_fma_f32 v[22:23], v[24:25], s[2:3], v[28:29] op_sel_hi:[1,0,1] neg_lo:[0,0,1] neg_hi:[0,0,1]
	v_cvt_pk_f16_f32 v2, v2, v3
	v_cvt_pk_f16_f32 v3, v22, v23
	v_lshl_add_u64 v[22:23], s[0:1], 0, v[18:19]
	v_mad_u64_u32 v[24:25], s[4:5], v22, s14, v[20:21]
	v_mul_lo_u32 v8, v22, s3
	v_mul_lo_u32 v10, v23, s14
	v_add3_u32 v25, v10, v25, v8
	v_lshlrev_b64 v[22:23], 1, v[24:25]
	v_lshl_add_u64 v[24:25], s[10:11], 0, v[22:23]
	global_store_dwordx4 v[24:25], v[4:7], off sc1
	v_mov_b32_e32 v12, v33
	v_mov_b32_e32 v14, v35
	v_lshl_add_u64 v[4:5], s[12:13], 0, v[22:23]
	global_store_dwordx4 v[4:5], v[0:3], off sc1
	v_fma_mixlo_f16 v6, v11, s2, 0
	v_mov_b32_e32 v16, v37
	v_fma_mixlo_f16 v0, v9, s2, 0
	v_fma_mixlo_f16 v0, v9, s2, -v0 op_sel_hi:[0,0,1]
	v_pk_mul_f32 v[2:3], v[12:13], s[2:3] op_sel_hi:[1,0]
	v_mul_f32_e32 v4, 0x45800000, v11
	v_cvt_pk_f16_f32 v5, v2, v3
	v_fma_mixhi_f16 v0, v11, s2, -v6 op_sel_hi:[0,0,1]
	v_pk_mul_f32 v[6:7], v[14:15], s[2:3] op_sel_hi:[1,0]
	v_pk_mul_f32 v[10:11], v[16:17], s[2:3] op_sel_hi:[1,0]
	v_cvt_f32_f16_e32 v2, v5
	v_cvt_f32_f16_sdwa v3, v5 dst_sel:DWORD dst_unused:UNUSED_PAD src0_sel:WORD_1
	v_cvt_pk_f16_f32 v6, v6, v7
	v_cvt_pk_f16_f32 v7, v10, v11
	v_mul_f32_e32 v1, 0x45800000, v9
	v_cvt_f32_f16_e32 v8, v6
	v_cvt_f32_f16_sdwa v9, v6 dst_sel:DWORD dst_unused:UNUSED_PAD src0_sel:WORD_1
	v_cvt_f32_f16_e32 v10, v7
	v_cvt_f32_f16_sdwa v11, v7 dst_sel:DWORD dst_unused:UNUSED_PAD src0_sel:WORD_1
	v_pk_fma_f32 v[2:3], v[12:13], s[2:3], v[2:3] op_sel_hi:[1,0,1] neg_lo:[0,0,1] neg_hi:[0,0,1]
	v_or_b32_e32 v18, 32, v18
	v_cvt_pk_f16_f32 v4, v1, v4
	v_cvt_pk_f16_f32 v1, v2, v3
	v_pk_fma_f32 v[2:3], v[14:15], s[2:3], v[8:9] op_sel_hi:[1,0,1] neg_lo:[0,0,1] neg_hi:[0,0,1]
	v_pk_fma_f32 v[8:9], v[16:17], s[2:3], v[10:11] op_sel_hi:[1,0,1] neg_lo:[0,0,1] neg_hi:[0,0,1]
	v_cvt_pk_f16_f32 v2, v2, v3
	v_cvt_pk_f16_f32 v3, v8, v9
	v_lshl_add_u64 v[8:9], s[0:1], 0, v[18:19]
	v_mad_u64_u32 v[10:11], s[0:1], v8, s14, v[20:21]
	v_mul_lo_u32 v8, v8, s3
	v_mul_lo_u32 v9, v9, s14
	v_add3_u32 v11, v9, v11, v8
	v_lshlrev_b64 v[8:9], 1, v[10:11]
	v_lshl_add_u64 v[10:11], s[10:11], 0, v[8:9]
	global_store_dwordx4 v[10:11], v[4:7], off sc1
	s_nop 1
	v_lshl_add_u64 v[4:5], s[12:13], 0, v[8:9]
	global_store_dwordx4 v[4:5], v[0:3], off sc1
	s_endpgm
	.p2alignl 8, 3212836864

.LBB12_55:
	s_or_b64 exec, exec, s[0:1]
	s_cmp_eq_u32 s22, 1
	s_cselect_b64 s[0:1], -1, 0
	v_cndmask_b32_e64 v84, 1.0, 0, s[0:1]
	s_and_b64 s[0:1], s[0:1], exec
	v_and_b32_e32 v85, 0x6000, v76
	s_waitcnt vmcnt(3)
	v_mul_f32_e32 v76, v84, v68
	s_cselect_b32 s0, s3, s7
	s_cselect_b32 s1, s2, s6
	s_waitcnt vmcnt(2)
	v_mul_f32_e32 v72, v84, v70
	s_waitcnt vmcnt(1)
	v_mul_f32_e32 v71, v84, v71
	s_waitcnt vmcnt(0)
	v_mul_f32_e32 v70, v84, v78
	v_fmamk_f32 v62, v62, 0x35800000, v76
	v_mov_b32_e32 v82, s1
	v_mov_b32_e32 v83, s0
	v_lshl_or_b32 v78, v75, 2, v85
	v_lshlrev_b32_e32 v84, 4, v75
	v_mul_f32_e32 v75, v79, v62
	v_mul_u32_u24_e32 v62, 0x440, v74
	v_fmamk_f32 v54, v54, 0x35800000, v71
	v_fmamk_f32 v50, v50, 0x35800000, v70
	v_lshl_add_u64 v[0:1], v[0:1], 2, v[82:83]
	v_or_b32_e32 v82, v78, v62
	v_mul_f32_e32 v54, v79, v54
	v_mul_f32_e32 v50, v79, v50
	v_fmamk_f32 v58, v58, 0x35800000, v72
	v_fmamk_f32 v55, v55, 0x35800000, v71
	ds_write2_b32 v82, v54, v50 offset0:32 offset1:48
	v_fmamk_f32 v50, v51, 0x35800000, v70
	v_mul_f32_e32 v58, v79, v58
	v_mul_f32_e32 v55, v69, v55
	v_mul_f32_e32 v50, v69, v50
	v_fmamk_f32 v63, v63, 0x35800000, v76
	ds_write2_b32 v82, v75, v58 offset1:16
	v_fmamk_f32 v58, v59, 0x35800000, v72
	v_fmamk_f32 v56, v56, 0x35800000, v71
	ds_write2_b32 v82, v55, v50 offset0:100 offset1:116
	v_fmamk_f32 v50, v52, 0x35800000, v70
	v_mul_f32_e32 v63, v69, v63
	v_mul_f32_e32 v58, v69, v58
	v_mul_f32_e32 v56, v81, v56
	v_mul_f32_e32 v50, v81, v50
	v_fmamk_f32 v64, v64, 0x35800000, v76
	ds_write2_b32 v82, v63, v58 offset0:68 offset1:84
	v_fmamk_f32 v58, v60, 0x35800000, v72
	v_fmamk_f32 v57, v57, 0x35800000, v71
	ds_write2_b32 v82, v56, v50 offset0:168 offset1:184
	v_fmamk_f32 v50, v53, 0x35800000, v70
	v_mul_f32_e32 v64, v81, v64
	v_mul_f32_e32 v58, v81, v58
	v_mul_f32_e32 v57, v80, v57
	v_mul_f32_e32 v50, v80, v50
	v_or_b32_e32 v68, v85, v84
	v_mov_b32_e32 v85, 0
	v_fmamk_f32 v65, v65, 0x35800000, v76
	ds_write2_b32 v82, v64, v58 offset0:136 offset1:152
	v_fmamk_f32 v58, v61, 0x35800000, v72
	ds_write2_b32 v82, v57, v50 offset0:236 offset1:252
	v_add_u32_e32 v50, v74, v73
	v_lshl_add_u64 v[0:1], v[0:1], 0, v[84:85]
	v_mul_f32_e32 v65, v80, v65
	v_mul_f32_e32 v58, v80, v58
	v_cmp_gt_i32_e32 vcc, s8, v50
	ds_write2_b32 v82, v65, v58 offset0:204 offset1:220
	s_and_saveexec_b64 s[0:1], vcc
	s_cbranch_execz .LBB12_57
	s_movk_i32 s2, 0x110
	v_mad_u32_u24 v51, v74, s2, v68
	ds_read_b128 v[52:55], v51
	v_ashrrev_i32_e32 v51, 31, v50
	v_lshlrev_b64 v[50:51], 11, v[50:51]
	v_lshl_add_u64 v[50:51], v[0:1], 0, v[50:51]
	s_waitcnt lgkmcnt(0)
	global_store_dwordx4 v[50:51], v[52:55], off sc1
.LBB12_57:
	s_or_b64 exec, exec, s[0:1]
	s_nop 0
	v_or_b32_e32 v52, 4, v74
	v_add_u32_e32 v50, v52, v73
	v_cmp_gt_i32_e32 vcc, s8, v50
	s_and_saveexec_b64 s[0:1], vcc
	s_cbranch_execz .LBB12_59
	s_movk_i32 s2, 0x110
	v_mad_u32_u24 v51, v52, s2, v68
	ds_read_b128 v[54:57], v51
	v_ashrrev_i32_e32 v51, 31, v50
	v_lshlrev_b64 v[50:51], 11, v[50:51]
	v_lshl_add_u64 v[50:51], v[0:1], 0, v[50:51]
	s_waitcnt lgkmcnt(0)
	global_store_dwordx4 v[50:51], v[54:57], off sc1
.LBB12_59:
	s_or_b64 exec, exec, s[0:1]
	v_or_b32_e32 v53, 8, v74
	v_add_u32_e32 v50, v53, v73
	v_cmp_gt_i32_e32 vcc, s8, v50
	s_and_saveexec_b64 s[0:1], vcc
	s_cbranch_execz .LBB12_61
	s_movk_i32 s2, 0x110
	v_mad_u32_u24 v51, v53, s2, v68
	ds_read_b128 v[54:57], v51
	v_ashrrev_i32_e32 v51, 31, v50
	v_lshlrev_b64 v[50:51], 11, v[50:51]
	v_lshl_add_u64 v[50:51], v[0:1], 0, v[50:51]
	s_waitcnt lgkmcnt(0)
	global_store_dwordx4 v[50:51], v[54:57], off sc1
.LBB12_61:
	s_or_b64 exec, exec, s[0:1]
	s_nop 0
	v_or_b32_e32 v54, 12, v74
	v_add_u32_e32 v50, v54, v73
	v_cmp_gt_i32_e32 vcc, s8, v50
	s_and_saveexec_b64 s[0:1], vcc
	s_cbranch_execz .LBB12_63
	s_movk_i32 s2, 0x110
	v_mad_u32_u24 v51, v54, s2, v68
	ds_read_b128 v[56:59], v51
	v_ashrrev_i32_e32 v51, 31, v50
	v_lshlrev_b64 v[50:51], 11, v[50:51]
	v_lshl_add_u64 v[50:51], v[0:1], 0, v[50:51]
	s_waitcnt lgkmcnt(0)
	global_store_dwordx4 v[50:51], v[56:59], off sc1

.LBB12_71:
	s_or_b64 exec, exec, s[0:1]
	v_fmamk_f32 v46, v46, 0x35800000, v76
	v_fmamk_f32 v38, v38, 0x35800000, v71
	v_fmamk_f32 v34, v34, 0x35800000, v70
	s_waitcnt vmcnt(0)
	v_mul_f32_e32 v58, v55, v46
	v_add_u32_e32 v46, v78, v62
	v_mul_f32_e32 v38, v55, v38
	v_mul_f32_e32 v34, v55, v34
	v_fmamk_f32 v42, v42, 0x35800000, v72
	v_fmamk_f32 v39, v39, 0x35800000, v71
	ds_write2_b32 v46, v38, v34 offset0:32 offset1:48
	v_fmamk_f32 v34, v35, 0x35800000, v70
	v_mul_f32_e32 v42, v55, v42
	v_mul_f32_e32 v39, v51, v39
	v_mul_f32_e32 v34, v51, v34
	v_fmamk_f32 v47, v47, 0x35800000, v76
	ds_write2_b32 v46, v58, v42 offset1:16
	v_fmamk_f32 v42, v43, 0x35800000, v72
	v_fmamk_f32 v40, v40, 0x35800000, v71
	ds_write2_b32 v46, v39, v34 offset0:100 offset1:116
	v_fmamk_f32 v34, v36, 0x35800000, v70
	v_mul_f32_e32 v47, v51, v47
	v_mul_f32_e32 v42, v51, v42
	v_mul_f32_e32 v40, v57, v40
	v_mul_f32_e32 v34, v57, v34
	v_fmamk_f32 v48, v48, 0x35800000, v76
	ds_write2_b32 v46, v47, v42 offset0:68 offset1:84
	v_fmamk_f32 v42, v44, 0x35800000, v72
	v_fmamk_f32 v41, v41, 0x35800000, v71
	ds_write2_b32 v46, v40, v34 offset0:168 offset1:184
	v_fmamk_f32 v34, v37, 0x35800000, v70
	v_mul_f32_e32 v48, v57, v48
	v_mul_f32_e32 v42, v57, v42
	v_mul_f32_e32 v41, v56, v41
	v_mul_f32_e32 v34, v56, v34
	v_fmamk_f32 v49, v49, 0x35800000, v76
	ds_write2_b32 v46, v48, v42 offset0:136 offset1:152
	v_fmamk_f32 v42, v45, 0x35800000, v72
	ds_write2_b32 v46, v41, v34 offset0:236 offset1:252
	v_add_u32_e32 v34, v74, v50
	v_mul_f32_e32 v49, v56, v49
	v_mul_f32_e32 v42, v56, v42
	v_cmp_gt_i32_e32 vcc, s8, v34
	ds_write2_b32 v46, v49, v42 offset0:204 offset1:220
	s_and_saveexec_b64 s[0:1], vcc
	s_cbranch_execz .LBB12_73
	s_movk_i32 s2, 0x110
	v_mad_u32_u24 v35, v74, s2, v68
	ds_read_b128 v[36:39], v35
	v_ashrrev_i32_e32 v35, 31, v34
	v_lshlrev_b64 v[34:35], 11, v[34:35]
	v_lshl_add_u64 v[34:35], v[0:1], 0, v[34:35]
	s_waitcnt lgkmcnt(0)
	global_store_dwordx4 v[34:35], v[36:39], off sc1
.LBB12_73:
	s_or_b64 exec, exec, s[0:1]
	v_add_u32_e32 v34, v52, v50
	v_cmp_gt_i32_e32 vcc, s8, v34
	s_and_saveexec_b64 s[0:1], vcc
	s_cbranch_execz .LBB12_75
	s_movk_i32 s2, 0x110
	v_mad_u32_u24 v35, v52, s2, v68
	ds_read_b128 v[36:39], v35
	v_ashrrev_i32_e32 v35, 31, v34
	v_lshlrev_b64 v[34:35], 11, v[34:35]
	v_lshl_add_u64 v[34:35], v[0:1], 0, v[34:35]
	s_waitcnt lgkmcnt(0)
	global_store_dwordx4 v[34:35], v[36:39], off sc1
.LBB12_75:
	s_or_b64 exec, exec, s[0:1]
	v_add_u32_e32 v34, v53, v50
	v_cmp_gt_i32_e32 vcc, s8, v34
	s_and_saveexec_b64 s[0:1], vcc
	s_cbranch_execz .LBB12_77
	s_movk_i32 s2, 0x110
	v_mad_u32_u24 v35, v53, s2, v68
	ds_read_b128 v[36:39], v35
	v_ashrrev_i32_e32 v35, 31, v34
	v_lshlrev_b64 v[34:35], 11, v[34:35]
	v_lshl_add_u64 v[34:35], v[0:1], 0, v[34:35]
	s_waitcnt lgkmcnt(0)
	global_store_dwordx4 v[34:35], v[36:39], off sc1
.LBB12_77:
	s_or_b64 exec, exec, s[0:1]
	v_add_u32_e32 v34, v54, v50
	v_cmp_gt_i32_e32 vcc, s8, v34
	s_and_saveexec_b64 s[0:1], vcc
	s_cbranch_execz .LBB12_79
	s_movk_i32 s2, 0x110
	v_mad_u32_u24 v35, v54, s2, v68
	ds_read_b128 v[36:39], v35
	v_ashrrev_i32_e32 v35, 31, v34
	v_lshlrev_b64 v[34:35], 11, v[34:35]
	v_lshl_add_u64 v[34:35], v[0:1], 0, v[34:35]
	s_waitcnt lgkmcnt(0)
	global_store_dwordx4 v[34:35], v[36:39], off sc1

.LBB12_87:
	s_or_b64 exec, exec, s[0:1]
	v_fmamk_f32 v22, v22, 0x35800000, v71
	v_fmamk_f32 v18, v18, 0x35800000, v70
	s_waitcnt vmcnt(0)
	v_mul_f32_e32 v22, v36, v22
	v_mul_f32_e32 v18, v36, v18
	v_fmamk_f32 v30, v30, 0x35800000, v76
	v_fmamk_f32 v26, v26, 0x35800000, v72
	v_fmamk_f32 v23, v23, 0x35800000, v71
	ds_write2_b32 v46, v22, v18 offset0:32 offset1:48
	v_fmamk_f32 v18, v19, 0x35800000, v70
	v_mul_f32_e32 v30, v36, v30
	v_mul_f32_e32 v26, v36, v26
	v_mul_f32_e32 v23, v35, v23
	v_mul_f32_e32 v18, v35, v18
	v_fmamk_f32 v31, v31, 0x35800000, v76
	ds_write2_b32 v46, v30, v26 offset1:16
	v_fmamk_f32 v26, v27, 0x35800000, v72
	v_fmamk_f32 v24, v24, 0x35800000, v71
	ds_write2_b32 v46, v23, v18 offset0:100 offset1:116
	v_fmamk_f32 v18, v20, 0x35800000, v70
	v_mul_f32_e32 v31, v35, v31
	v_mul_f32_e32 v26, v35, v26
	v_mul_f32_e32 v24, v38, v24
	v_mul_f32_e32 v18, v38, v18
	v_fmamk_f32 v32, v32, 0x35800000, v76
	ds_write2_b32 v46, v31, v26 offset0:68 offset1:84
	v_fmamk_f32 v26, v28, 0x35800000, v72
	v_fmamk_f32 v25, v25, 0x35800000, v71
	ds_write2_b32 v46, v24, v18 offset0:168 offset1:184
	v_fmamk_f32 v18, v21, 0x35800000, v70
	v_mul_f32_e32 v32, v38, v32
	v_mul_f32_e32 v26, v38, v26
	v_mul_f32_e32 v25, v37, v25
	v_mul_f32_e32 v18, v37, v18
	v_fmamk_f32 v33, v33, 0x35800000, v76
	ds_write2_b32 v46, v32, v26 offset0:136 offset1:152
	v_fmamk_f32 v26, v29, 0x35800000, v72
	ds_write2_b32 v46, v25, v18 offset0:236 offset1:252
	v_add_u32_e32 v18, v74, v34
	v_mul_f32_e32 v33, v37, v33
	v_mul_f32_e32 v26, v37, v26
	v_cmp_gt_i32_e32 vcc, s8, v18
	ds_write2_b32 v46, v33, v26 offset0:204 offset1:220
	s_and_saveexec_b64 s[0:1], vcc
	s_cbranch_execz .LBB12_89
	s_movk_i32 s2, 0x110
	v_mad_u32_u24 v19, v74, s2, v68
	ds_read_b128 v[20:23], v19
	v_ashrrev_i32_e32 v19, 31, v18
	v_lshlrev_b64 v[18:19], 11, v[18:19]
	v_lshl_add_u64 v[18:19], v[0:1], 0, v[18:19]
	s_waitcnt lgkmcnt(0)
	global_store_dwordx4 v[18:19], v[20:23], off sc1
.LBB12_89:
	s_or_b64 exec, exec, s[0:1]
	v_add_u32_e32 v18, v52, v34
	v_cmp_gt_i32_e32 vcc, s8, v18
	s_and_saveexec_b64 s[0:1], vcc
	s_cbranch_execz .LBB12_91
	s_movk_i32 s2, 0x110
	v_mad_u32_u24 v19, v52, s2, v68
	ds_read_b128 v[20:23], v19
	v_ashrrev_i32_e32 v19, 31, v18
	v_lshlrev_b64 v[18:19], 11, v[18:19]
	v_lshl_add_u64 v[18:19], v[0:1], 0, v[18:19]
	s_waitcnt lgkmcnt(0)
	global_store_dwordx4 v[18:19], v[20:23], off sc1
.LBB12_91:
	s_or_b64 exec, exec, s[0:1]
	v_add_u32_e32 v18, v53, v34
	v_cmp_gt_i32_e32 vcc, s8, v18
	s_and_saveexec_b64 s[0:1], vcc
	s_cbranch_execz .LBB12_93
	s_movk_i32 s2, 0x110
	v_mad_u32_u24 v19, v53, s2, v68
	ds_read_b128 v[20:23], v19
	v_ashrrev_i32_e32 v19, 31, v18
	v_lshlrev_b64 v[18:19], 11, v[18:19]
	v_lshl_add_u64 v[18:19], v[0:1], 0, v[18:19]
	s_waitcnt lgkmcnt(0)
	global_store_dwordx4 v[18:19], v[20:23], off sc1
.LBB12_93:
	s_or_b64 exec, exec, s[0:1]
	v_add_u32_e32 v18, v54, v34
	v_cmp_gt_i32_e32 vcc, s8, v18
	s_and_saveexec_b64 s[0:1], vcc
	s_cbranch_execz .LBB12_95
	s_movk_i32 s2, 0x110
	v_mad_u32_u24 v19, v54, s2, v68
	ds_read_b128 v[20:23], v19
	v_ashrrev_i32_e32 v19, 31, v18
	v_lshlrev_b64 v[18:19], 11, v[18:19]
	v_lshl_add_u64 v[18:19], v[0:1], 0, v[18:19]
	s_waitcnt lgkmcnt(0)
	global_store_dwordx4 v[18:19], v[20:23], off sc1

.LBB12_103:
	s_or_b64 exec, exec, s[0:1]
	v_fmamk_f32 v6, v6, 0x35800000, v71
	v_fmamk_f32 v2, v2, 0x35800000, v70
	s_waitcnt vmcnt(0)
	v_mul_f32_e32 v6, v20, v6
	v_mul_f32_e32 v2, v20, v2
	v_fmamk_f32 v14, v14, 0x35800000, v76
	v_fmamk_f32 v10, v10, 0x35800000, v72
	v_fmamk_f32 v7, v7, 0x35800000, v71
	ds_write2_b32 v46, v6, v2 offset0:32 offset1:48
	v_fmamk_f32 v2, v3, 0x35800000, v70
	v_mul_f32_e32 v14, v20, v14
	v_mul_f32_e32 v10, v20, v10
	v_mul_f32_e32 v7, v19, v7
	v_mul_f32_e32 v2, v19, v2
	v_fmamk_f32 v15, v15, 0x35800000, v76
	ds_write2_b32 v46, v14, v10 offset1:16
	v_fmamk_f32 v10, v11, 0x35800000, v72
	v_fmamk_f32 v8, v8, 0x35800000, v71
	ds_write2_b32 v46, v7, v2 offset0:100 offset1:116
	v_fmamk_f32 v2, v4, 0x35800000, v70
	v_mul_f32_e32 v15, v19, v15
	v_mul_f32_e32 v10, v19, v10
	v_mul_f32_e32 v8, v22, v8
	v_fmac_f32_e32 v71, 0x35800000, v9
	v_mul_f32_e32 v2, v22, v2
	v_fmac_f32_e32 v70, 0x35800000, v5
	v_fmamk_f32 v16, v16, 0x35800000, v76
	ds_write2_b32 v46, v15, v10 offset0:68 offset1:84
	v_fmamk_f32 v10, v12, 0x35800000, v72
	v_mul_f32_e32 v9, v21, v71
	ds_write2_b32 v46, v8, v2 offset0:168 offset1:184
	v_mul_f32_e32 v2, v21, v70
	v_mul_f32_e32 v16, v22, v16
	v_fmac_f32_e32 v76, 0x35800000, v17
	v_mul_f32_e32 v10, v22, v10
	v_fmac_f32_e32 v72, 0x35800000, v13
	ds_write2_b32 v46, v9, v2 offset0:236 offset1:252
	v_add_u32_e32 v2, v74, v18
	v_mul_f32_e32 v17, v21, v76
	ds_write2_b32 v46, v16, v10 offset0:136 offset1:152
	v_mul_f32_e32 v10, v21, v72
	v_cmp_gt_i32_e32 vcc, s8, v2
	ds_write2_b32 v46, v17, v10 offset0:204 offset1:220
	s_and_saveexec_b64 s[0:1], vcc
	s_cbranch_execz .LBB12_105
	s_movk_i32 s2, 0x110
	v_mad_u32_u24 v3, v74, s2, v68
	ds_read_b128 v[4:7], v3
	v_ashrrev_i32_e32 v3, 31, v2
	v_lshlrev_b64 v[2:3], 11, v[2:3]
	v_lshl_add_u64 v[2:3], v[0:1], 0, v[2:3]
	s_waitcnt lgkmcnt(0)
	global_store_dwordx4 v[2:3], v[4:7], off sc1
.LBB12_105:
	s_or_b64 exec, exec, s[0:1]
	v_add_u32_e32 v2, v52, v18
	v_cmp_gt_i32_e32 vcc, s8, v2
	s_and_saveexec_b64 s[0:1], vcc
	s_cbranch_execz .LBB12_107
	s_movk_i32 s2, 0x110
	v_mad_u32_u24 v3, v52, s2, v68
	ds_read_b128 v[4:7], v3
	v_ashrrev_i32_e32 v3, 31, v2
	v_lshlrev_b64 v[2:3], 11, v[2:3]
	v_lshl_add_u64 v[2:3], v[0:1], 0, v[2:3]
	s_waitcnt lgkmcnt(0)
	global_store_dwordx4 v[2:3], v[4:7], off sc1
.LBB12_107:
	s_or_b64 exec, exec, s[0:1]
	v_add_u32_e32 v2, v53, v18
	v_cmp_gt_i32_e32 vcc, s8, v2
	s_and_saveexec_b64 s[0:1], vcc
	s_cbranch_execz .LBB12_109
	s_movk_i32 s2, 0x110
	v_mad_u32_u24 v3, v53, s2, v68
	ds_read_b128 v[4:7], v3
	v_ashrrev_i32_e32 v3, 31, v2
	v_lshlrev_b64 v[2:3], 11, v[2:3]
	v_lshl_add_u64 v[2:3], v[0:1], 0, v[2:3]
	s_waitcnt lgkmcnt(0)
	global_store_dwordx4 v[2:3], v[4:7], off sc1
.LBB12_109:
	s_or_b64 exec, exec, s[0:1]
	v_add_u32_e32 v2, v54, v18
	v_cmp_gt_i32_e32 vcc, s8, v2
	s_and_saveexec_b64 s[0:1], vcc
	s_cbranch_execz .LBB12_111
	s_movk_i32 s0, 0x110
	v_mad_u32_u24 v3, v54, s0, v68
	ds_read_b128 v[4:7], v3
	v_ashrrev_i32_e32 v3, 31, v2
	v_lshlrev_b64 v[2:3], 11, v[2:3]
	v_lshl_add_u64 v[0:1], v[0:1], 0, v[2:3]
	s_waitcnt lgkmcnt(0)
	global_store_dwordx4 v[0:1], v[4:7], off sc1

.LBB13_55:
	s_or_b64 exec, exec, s[0:1]
	v_and_b32_e32 v81, 0x6000, v72
	v_lshlrev_b32_e32 v84, 4, v71
	s_waitcnt vmcnt(3)
	v_fmamk_f32 v62, v62, 0x35800000, v76
	s_waitcnt lgkmcnt(0)
	v_mov_b32_e32 v82, s10
	v_mov_b32_e32 v83, s11
	v_lshl_or_b32 v72, v71, 2, v81
	v_or_b32_e32 v71, v81, v84
	s_waitcnt vmcnt(0)
	v_mul_f32_e32 v81, v78, v62
	v_mul_u32_u24_e32 v62, 0x440, v70
	v_fmamk_f32 v54, v54, 0x35800000, v74
	v_fmamk_f32 v50, v50, 0x35800000, v68
	v_lshl_add_u64 v[0:1], v[0:1], 2, v[82:83]
	v_or_b32_e32 v82, v72, v62
	v_mul_f32_e32 v54, v78, v54
	v_mul_f32_e32 v50, v78, v50
	v_fmamk_f32 v58, v58, 0x35800000, v75
	v_fmamk_f32 v55, v55, 0x35800000, v74
	ds_write2_b32 v82, v54, v50 offset0:32 offset1:48
	v_fmamk_f32 v50, v51, 0x35800000, v68
	v_mul_f32_e32 v58, v78, v58
	v_mul_f32_e32 v55, v69, v55
	v_mul_f32_e32 v50, v69, v50
	v_fmamk_f32 v63, v63, 0x35800000, v76
	ds_write2_b32 v82, v81, v58 offset1:16
	v_fmamk_f32 v58, v59, 0x35800000, v75
	v_fmamk_f32 v56, v56, 0x35800000, v74
	ds_write2_b32 v82, v55, v50 offset0:100 offset1:116
	v_fmamk_f32 v50, v52, 0x35800000, v68
	v_mul_f32_e32 v63, v69, v63
	v_mul_f32_e32 v58, v69, v58
	v_mul_f32_e32 v56, v80, v56
	v_mul_f32_e32 v50, v80, v50
	v_fmamk_f32 v64, v64, 0x35800000, v76
	ds_write2_b32 v82, v63, v58 offset0:68 offset1:84
	v_fmamk_f32 v58, v60, 0x35800000, v75
	v_fmamk_f32 v57, v57, 0x35800000, v74
	ds_write2_b32 v82, v56, v50 offset0:168 offset1:184
	v_fmamk_f32 v50, v53, 0x35800000, v68
	v_mul_f32_e32 v64, v80, v64
	v_mul_f32_e32 v58, v80, v58
	v_mul_f32_e32 v57, v79, v57
	v_mul_f32_e32 v50, v79, v50
	v_mov_b32_e32 v85, 0
	v_fmamk_f32 v65, v65, 0x35800000, v76
	ds_write2_b32 v82, v64, v58 offset0:136 offset1:152
	v_fmamk_f32 v58, v61, 0x35800000, v75
	ds_write2_b32 v82, v57, v50 offset0:236 offset1:252
	v_add_u32_e32 v50, v70, v73
	v_lshl_add_u64 v[0:1], v[0:1], 0, v[84:85]
	v_mul_f32_e32 v65, v79, v65
	v_mul_f32_e32 v58, v79, v58
	v_cmp_gt_i32_e32 vcc, s2, v50
	ds_write2_b32 v82, v65, v58 offset0:204 offset1:220
	s_and_saveexec_b64 s[0:1], vcc
	s_cbranch_execz .LBB13_57
	s_movk_i32 s3, 0x110
	v_mad_u32_u24 v51, v70, s3, v71
	ds_read_b128 v[52:55], v51
	v_ashrrev_i32_e32 v51, 31, v50
	v_lshlrev_b64 v[50:51], 11, v[50:51]
	v_lshl_add_u64 v[50:51], v[0:1], 0, v[50:51]
	s_waitcnt lgkmcnt(0)
	global_store_dwordx4 v[50:51], v[52:55], off sc1
.LBB13_57:
	s_or_b64 exec, exec, s[0:1]
	s_nop 0
	v_or_b32_e32 v52, 4, v70
	v_add_u32_e32 v50, v52, v73
	v_cmp_gt_i32_e32 vcc, s2, v50
	s_and_saveexec_b64 s[0:1], vcc
	s_cbranch_execz .LBB13_59
	s_movk_i32 s3, 0x110
	v_mad_u32_u24 v51, v52, s3, v71
	ds_read_b128 v[54:57], v51
	v_ashrrev_i32_e32 v51, 31, v50
	v_lshlrev_b64 v[50:51], 11, v[50:51]
	v_lshl_add_u64 v[50:51], v[0:1], 0, v[50:51]
	s_waitcnt lgkmcnt(0)
	global_store_dwordx4 v[50:51], v[54:57], off sc1
.LBB13_59:
	s_or_b64 exec, exec, s[0:1]
	v_or_b32_e32 v53, 8, v70
	v_add_u32_e32 v50, v53, v73
	v_cmp_gt_i32_e32 vcc, s2, v50
	s_and_saveexec_b64 s[0:1], vcc
	s_cbranch_execz .LBB13_61
	s_movk_i32 s3, 0x110
	v_mad_u32_u24 v51, v53, s3, v71
	ds_read_b128 v[54:57], v51
	v_ashrrev_i32_e32 v51, 31, v50
	v_lshlrev_b64 v[50:51], 11, v[50:51]
	v_lshl_add_u64 v[50:51], v[0:1], 0, v[50:51]
	s_waitcnt lgkmcnt(0)
	global_store_dwordx4 v[50:51], v[54:57], off sc1
.LBB13_61:
	s_or_b64 exec, exec, s[0:1]
	s_nop 0
	v_or_b32_e32 v54, 12, v70
	v_add_u32_e32 v50, v54, v73
	v_cmp_gt_i32_e32 vcc, s2, v50
	s_and_saveexec_b64 s[0:1], vcc
	s_cbranch_execz .LBB13_63
	s_movk_i32 s3, 0x110
	v_mad_u32_u24 v51, v54, s3, v71
	ds_read_b128 v[56:59], v51
	v_ashrrev_i32_e32 v51, 31, v50
	v_lshlrev_b64 v[50:51], 11, v[50:51]
	v_lshl_add_u64 v[50:51], v[0:1], 0, v[50:51]
	s_waitcnt lgkmcnt(0)
	global_store_dwordx4 v[50:51], v[56:59], off sc1

.LBB13_71:
	s_or_b64 exec, exec, s[0:1]
	v_fmamk_f32 v46, v46, 0x35800000, v76
	v_fmamk_f32 v38, v38, 0x35800000, v74
	v_fmamk_f32 v34, v34, 0x35800000, v68
	s_waitcnt vmcnt(0)
	v_mul_f32_e32 v58, v55, v46
	v_add_u32_e32 v46, v72, v62
	v_mul_f32_e32 v38, v55, v38
	v_mul_f32_e32 v34, v55, v34
	v_fmamk_f32 v42, v42, 0x35800000, v75
	v_fmamk_f32 v39, v39, 0x35800000, v74
	ds_write2_b32 v46, v38, v34 offset0:32 offset1:48
	v_fmamk_f32 v34, v35, 0x35800000, v68
	v_mul_f32_e32 v42, v55, v42
	v_mul_f32_e32 v39, v51, v39
	v_mul_f32_e32 v34, v51, v34
	v_fmamk_f32 v47, v47, 0x35800000, v76
	ds_write2_b32 v46, v58, v42 offset1:16
	v_fmamk_f32 v42, v43, 0x35800000, v75
	v_fmamk_f32 v40, v40, 0x35800000, v74
	ds_write2_b32 v46, v39, v34 offset0:100 offset1:116
	v_fmamk_f32 v34, v36, 0x35800000, v68
	v_mul_f32_e32 v47, v51, v47
	v_mul_f32_e32 v42, v51, v42
	v_mul_f32_e32 v40, v57, v40
	v_mul_f32_e32 v34, v57, v34
	v_fmamk_f32 v48, v48, 0x35800000, v76
	ds_write2_b32 v46, v47, v42 offset0:68 offset1:84
	v_fmamk_f32 v42, v44, 0x35800000, v75
	v_fmamk_f32 v41, v41, 0x35800000, v74
	ds_write2_b32 v46, v40, v34 offset0:168 offset1:184
	v_fmamk_f32 v34, v37, 0x35800000, v68
	v_mul_f32_e32 v48, v57, v48
	v_mul_f32_e32 v42, v57, v42
	v_mul_f32_e32 v41, v56, v41
	v_mul_f32_e32 v34, v56, v34
	v_fmamk_f32 v49, v49, 0x35800000, v76
	ds_write2_b32 v46, v48, v42 offset0:136 offset1:152
	v_fmamk_f32 v42, v45, 0x35800000, v75
	ds_write2_b32 v46, v41, v34 offset0:236 offset1:252
	v_add_u32_e32 v34, v70, v50
	v_mul_f32_e32 v49, v56, v49
	v_mul_f32_e32 v42, v56, v42
	v_cmp_gt_i32_e32 vcc, s2, v34
	ds_write2_b32 v46, v49, v42 offset0:204 offset1:220
	s_and_saveexec_b64 s[0:1], vcc
	s_cbranch_execz .LBB13_73
	s_movk_i32 s3, 0x110
	v_mad_u32_u24 v35, v70, s3, v71
	ds_read_b128 v[36:39], v35
	v_ashrrev_i32_e32 v35, 31, v34
	v_lshlrev_b64 v[34:35], 11, v[34:35]
	v_lshl_add_u64 v[34:35], v[0:1], 0, v[34:35]
	s_waitcnt lgkmcnt(0)
	global_store_dwordx4 v[34:35], v[36:39], off sc1
.LBB13_73:
	s_or_b64 exec, exec, s[0:1]
	v_add_u32_e32 v34, v52, v50
	v_cmp_gt_i32_e32 vcc, s2, v34
	s_and_saveexec_b64 s[0:1], vcc
	s_cbranch_execz .LBB13_75
	s_movk_i32 s3, 0x110
	v_mad_u32_u24 v35, v52, s3, v71
	ds_read_b128 v[36:39], v35
	v_ashrrev_i32_e32 v35, 31, v34
	v_lshlrev_b64 v[34:35], 11, v[34:35]
	v_lshl_add_u64 v[34:35], v[0:1], 0, v[34:35]
	s_waitcnt lgkmcnt(0)
	global_store_dwordx4 v[34:35], v[36:39], off sc1
.LBB13_75:
	s_or_b64 exec, exec, s[0:1]
	v_add_u32_e32 v34, v53, v50
	v_cmp_gt_i32_e32 vcc, s2, v34
	s_and_saveexec_b64 s[0:1], vcc
	s_cbranch_execz .LBB13_77
	s_movk_i32 s3, 0x110
	v_mad_u32_u24 v35, v53, s3, v71
	ds_read_b128 v[36:39], v35
	v_ashrrev_i32_e32 v35, 31, v34
	v_lshlrev_b64 v[34:35], 11, v[34:35]
	v_lshl_add_u64 v[34:35], v[0:1], 0, v[34:35]
	s_waitcnt lgkmcnt(0)
	global_store_dwordx4 v[34:35], v[36:39], off sc1
.LBB13_77:
	s_or_b64 exec, exec, s[0:1]
	v_add_u32_e32 v34, v54, v50
	v_cmp_gt_i32_e32 vcc, s2, v34
	s_and_saveexec_b64 s[0:1], vcc
	s_cbranch_execz .LBB13_79
	s_movk_i32 s3, 0x110
	v_mad_u32_u24 v35, v54, s3, v71
	ds_read_b128 v[36:39], v35
	v_ashrrev_i32_e32 v35, 31, v34
	v_lshlrev_b64 v[34:35], 11, v[34:35]
	v_lshl_add_u64 v[34:35], v[0:1], 0, v[34:35]
	s_waitcnt lgkmcnt(0)
	global_store_dwordx4 v[34:35], v[36:39], off sc1

.LBB13_87:
	s_or_b64 exec, exec, s[0:1]
	v_fmamk_f32 v22, v22, 0x35800000, v74
	v_fmamk_f32 v18, v18, 0x35800000, v68
	s_waitcnt vmcnt(0)
	v_mul_f32_e32 v22, v36, v22
	v_mul_f32_e32 v18, v36, v18
	v_fmamk_f32 v30, v30, 0x35800000, v76
	v_fmamk_f32 v26, v26, 0x35800000, v75
	v_fmamk_f32 v23, v23, 0x35800000, v74
	ds_write2_b32 v46, v22, v18 offset0:32 offset1:48
	v_fmamk_f32 v18, v19, 0x35800000, v68
	v_mul_f32_e32 v30, v36, v30
	v_mul_f32_e32 v26, v36, v26
	v_mul_f32_e32 v23, v35, v23
	v_mul_f32_e32 v18, v35, v18
	v_fmamk_f32 v31, v31, 0x35800000, v76
	ds_write2_b32 v46, v30, v26 offset1:16
	v_fmamk_f32 v26, v27, 0x35800000, v75
	v_fmamk_f32 v24, v24, 0x35800000, v74
	ds_write2_b32 v46, v23, v18 offset0:100 offset1:116
	v_fmamk_f32 v18, v20, 0x35800000, v68
	v_mul_f32_e32 v31, v35, v31
	v_mul_f32_e32 v26, v35, v26
	v_mul_f32_e32 v24, v38, v24
	v_mul_f32_e32 v18, v38, v18
	v_fmamk_f32 v32, v32, 0x35800000, v76
	ds_write2_b32 v46, v31, v26 offset0:68 offset1:84
	v_fmamk_f32 v26, v28, 0x35800000, v75
	v_fmamk_f32 v25, v25, 0x35800000, v74
	ds_write2_b32 v46, v24, v18 offset0:168 offset1:184
	v_fmamk_f32 v18, v21, 0x35800000, v68
	v_mul_f32_e32 v32, v38, v32
	v_mul_f32_e32 v26, v38, v26
	v_mul_f32_e32 v25, v37, v25
	v_mul_f32_e32 v18, v37, v18
	v_fmamk_f32 v33, v33, 0x35800000, v76
	ds_write2_b32 v46, v32, v26 offset0:136 offset1:152
	v_fmamk_f32 v26, v29, 0x35800000, v75
	ds_write2_b32 v46, v25, v18 offset0:236 offset1:252
	v_add_u32_e32 v18, v70, v34
	v_mul_f32_e32 v33, v37, v33
	v_mul_f32_e32 v26, v37, v26
	v_cmp_gt_i32_e32 vcc, s2, v18
	ds_write2_b32 v46, v33, v26 offset0:204 offset1:220
	s_and_saveexec_b64 s[0:1], vcc
	s_cbranch_execz .LBB13_89
	s_movk_i32 s3, 0x110
	v_mad_u32_u24 v19, v70, s3, v71
	ds_read_b128 v[20:23], v19
	v_ashrrev_i32_e32 v19, 31, v18
	v_lshlrev_b64 v[18:19], 11, v[18:19]
	v_lshl_add_u64 v[18:19], v[0:1], 0, v[18:19]
	s_waitcnt lgkmcnt(0)
	global_store_dwordx4 v[18:19], v[20:23], off sc1
.LBB13_89:
	s_or_b64 exec, exec, s[0:1]
	v_add_u32_e32 v18, v52, v34
	v_cmp_gt_i32_e32 vcc, s2, v18
	s_and_saveexec_b64 s[0:1], vcc
	s_cbranch_execz .LBB13_91
	s_movk_i32 s3, 0x110
	v_mad_u32_u24 v19, v52, s3, v71
	ds_read_b128 v[20:23], v19
	v_ashrrev_i32_e32 v19, 31, v18
	v_lshlrev_b64 v[18:19], 11, v[18:19]
	v_lshl_add_u64 v[18:19], v[0:1], 0, v[18:19]
	s_waitcnt lgkmcnt(0)
	global_store_dwordx4 v[18:19], v[20:23], off sc1
.LBB13_91:
	s_or_b64 exec, exec, s[0:1]
	v_add_u32_e32 v18, v53, v34
	v_cmp_gt_i32_e32 vcc, s2, v18
	s_and_saveexec_b64 s[0:1], vcc
	s_cbranch_execz .LBB13_93
	s_movk_i32 s3, 0x110
	v_mad_u32_u24 v19, v53, s3, v71
	ds_read_b128 v[20:23], v19
	v_ashrrev_i32_e32 v19, 31, v18
	v_lshlrev_b64 v[18:19], 11, v[18:19]
	v_lshl_add_u64 v[18:19], v[0:1], 0, v[18:19]
	s_waitcnt lgkmcnt(0)
	global_store_dwordx4 v[18:19], v[20:23], off sc1
.LBB13_93:
	s_or_b64 exec, exec, s[0:1]
	v_add_u32_e32 v18, v54, v34
	v_cmp_gt_i32_e32 vcc, s2, v18
	s_and_saveexec_b64 s[0:1], vcc
	s_cbranch_execz .LBB13_95
	s_movk_i32 s3, 0x110
	v_mad_u32_u24 v19, v54, s3, v71
	ds_read_b128 v[20:23], v19
	v_ashrrev_i32_e32 v19, 31, v18
	v_lshlrev_b64 v[18:19], 11, v[18:19]
	v_lshl_add_u64 v[18:19], v[0:1], 0, v[18:19]
	s_waitcnt lgkmcnt(0)
	global_store_dwordx4 v[18:19], v[20:23], off sc1

.LBB13_103:
	s_or_b64 exec, exec, s[0:1]
	v_fmamk_f32 v6, v6, 0x35800000, v74
	v_fmamk_f32 v2, v2, 0x35800000, v68
	s_waitcnt vmcnt(0)
	v_mul_f32_e32 v6, v20, v6
	v_mul_f32_e32 v2, v20, v2
	v_fmamk_f32 v14, v14, 0x35800000, v76
	v_fmamk_f32 v10, v10, 0x35800000, v75
	v_fmamk_f32 v7, v7, 0x35800000, v74
	ds_write2_b32 v46, v6, v2 offset0:32 offset1:48
	v_fmamk_f32 v2, v3, 0x35800000, v68
	v_mul_f32_e32 v14, v20, v14
	v_mul_f32_e32 v10, v20, v10
	v_mul_f32_e32 v7, v19, v7
	v_mul_f32_e32 v2, v19, v2
	v_fmamk_f32 v15, v15, 0x35800000, v76
	ds_write2_b32 v46, v14, v10 offset1:16
	v_fmamk_f32 v10, v11, 0x35800000, v75
	v_fmamk_f32 v8, v8, 0x35800000, v74
	ds_write2_b32 v46, v7, v2 offset0:100 offset1:116
	v_fmamk_f32 v2, v4, 0x35800000, v68
	v_mul_f32_e32 v15, v19, v15
	v_mul_f32_e32 v10, v19, v10
	v_mul_f32_e32 v8, v22, v8
	v_fmac_f32_e32 v74, 0x35800000, v9
	v_mul_f32_e32 v2, v22, v2
	v_fmac_f32_e32 v68, 0x35800000, v5
	v_fmamk_f32 v16, v16, 0x35800000, v76
	ds_write2_b32 v46, v15, v10 offset0:68 offset1:84
	v_fmamk_f32 v10, v12, 0x35800000, v75
	v_mul_f32_e32 v9, v21, v74
	ds_write2_b32 v46, v8, v2 offset0:168 offset1:184
	v_mul_f32_e32 v2, v21, v68
	v_mul_f32_e32 v16, v22, v16
	v_fmac_f32_e32 v76, 0x35800000, v17
	v_mul_f32_e32 v10, v22, v10
	v_fmac_f32_e32 v75, 0x35800000, v13
	ds_write2_b32 v46, v9, v2 offset0:236 offset1:252
	v_add_u32_e32 v2, v70, v18
	v_mul_f32_e32 v17, v21, v76
	ds_write2_b32 v46, v16, v10 offset0:136 offset1:152
	v_mul_f32_e32 v10, v21, v75
	v_cmp_gt_i32_e32 vcc, s2, v2
	ds_write2_b32 v46, v17, v10 offset0:204 offset1:220
	s_and_saveexec_b64 s[0:1], vcc
	s_cbranch_execz .LBB13_105
	s_movk_i32 s3, 0x110
	v_mad_u32_u24 v3, v70, s3, v71
	ds_read_b128 v[4:7], v3
	v_ashrrev_i32_e32 v3, 31, v2
	v_lshlrev_b64 v[2:3], 11, v[2:3]
	v_lshl_add_u64 v[2:3], v[0:1], 0, v[2:3]
	s_waitcnt lgkmcnt(0)
	global_store_dwordx4 v[2:3], v[4:7], off sc1
.LBB13_105:
	s_or_b64 exec, exec, s[0:1]
	v_add_u32_e32 v2, v52, v18
	v_cmp_gt_i32_e32 vcc, s2, v2
	s_and_saveexec_b64 s[0:1], vcc
	s_cbranch_execz .LBB13_107
	s_movk_i32 s3, 0x110
	v_mad_u32_u24 v3, v52, s3, v71
	ds_read_b128 v[4:7], v3
	v_ashrrev_i32_e32 v3, 31, v2
	v_lshlrev_b64 v[2:3], 11, v[2:3]
	v_lshl_add_u64 v[2:3], v[0:1], 0, v[2:3]
	s_waitcnt lgkmcnt(0)
	global_store_dwordx4 v[2:3], v[4:7], off sc1
.LBB13_107:
	s_or_b64 exec, exec, s[0:1]
	v_add_u32_e32 v2, v53, v18
	v_cmp_gt_i32_e32 vcc, s2, v2
	s_and_saveexec_b64 s[0:1], vcc
	s_cbranch_execz .LBB13_109
	s_movk_i32 s3, 0x110
	v_mad_u32_u24 v3, v53, s3, v71
	ds_read_b128 v[4:7], v3
	v_ashrrev_i32_e32 v3, 31, v2
	v_lshlrev_b64 v[2:3], 11, v[2:3]
	v_lshl_add_u64 v[2:3], v[0:1], 0, v[2:3]
	s_waitcnt lgkmcnt(0)
	global_store_dwordx4 v[2:3], v[4:7], off sc1
.LBB13_109:
	s_or_b64 exec, exec, s[0:1]
	v_add_u32_e32 v2, v54, v18
	v_cmp_gt_i32_e32 vcc, s2, v2
	s_and_saveexec_b64 s[0:1], vcc
	s_cbranch_execz .LBB13_111
	s_movk_i32 s0, 0x110
	v_mad_u32_u24 v3, v54, s0, v71
	ds_read_b128 v[4:7], v3
	v_ashrrev_i32_e32 v3, 31, v2
	v_lshlrev_b64 v[2:3], 11, v[2:3]
	v_lshl_add_u64 v[0:1], v[0:1], 0, v[2:3]
	s_waitcnt lgkmcnt(0)
	global_store_dwordx4 v[0:1], v[4:7], off sc1

.LBB14_7:
	s_or_b64 exec, exec, s[2:3]
	v_lshlrev_b64 v[8:9], 9, v[8:9]
	v_lshl_add_u64 v[8:9], v[8:9], 2, s[6:7]
	v_mov_b32_e32 v11, 0
	v_lshl_add_u64 v[8:9], v[8:9], 0, v[10:11]
	s_waitcnt vmcnt(0)
	global_store_dwordx4 v[8:9], v[4:7], off sc1
	global_store_dwordx4 v[8:9], v[0:3], off offset:16 sc1
	s_endpgm
	.p2alignl 8, 3212836864
